# MoE up/down and router loops: buffer-rotation SALU moved in front of the interval barrier (off the post-release path); on top of the P3 changes
# speedup vs baseline: 1.0064x; 1.0018x over previous
; __device__ __forceinline__ void rt_step(const RtLoad& L, const bf16_t* bh, const bf16_t* bl, f32x4 (&acc)[2][5], float (&ss)[2], int ko) {
;     RtW W;
; #pragma unroll
;     for (int n = 0; n < 5; ++n) { W.wh[n] = *(const bf16x8*)(bh + (size_t)n * 16 * D + ko); W.wl[n] = *(const bf16x8*)(bl + (size_t)n * 16 * D + ko); }
;     bf16x8 ahi[2], alo[2];
; #pragma unroll
;     for (int mi = 0; mi < 2; ++mi) { const u32x4 xw = L.x[mi]; const f32x4 xa = (f32x4){bflo(xw.x), bfhi(xw.x), bflo(xw.y), bfhi(xw.y)}, xb = (f32x4){bflo(xw.z), bfhi(xw.z), bflo(xw.w), bfhi(xw.w)};
;         ss[mi] += (xa.x * xa.x + xa.y * xa.y) + (xa.z * xa.z + xa.w * xa.w) + (xb.x * xb.x + xb.y * xb.y) + (xb.z * xb.z + xb.w * xb.w);
;         const float u[8] = {xa.x * L.g[0].x, xa.y * L.g[0].y, xa.z * L.g[0].z, xa.w * L.g[0].w, xb.x * L.g[1].x, xb.y * L.g[1].y, xb.z * L.g[1].z, xb.w * L.g[1].w};
;         unsigned hb[8]; float lo[8];
; #pragma unroll
;         for (int j = 0; j < 8; ++j) { hb[j] = f2bf(u[j]); lo[j] = u[j] - __builtin_bit_cast(float, hb[j] << 16); }
;         const u32x4 hw = (u32x4){hb[0] | (hb[1] << 16), hb[2] | (hb[3] << 16), hb[4] | (hb[5] << 16), hb[6] | (hb[7] << 16)};
;         const u32x4 lw = (u32x4){pk2(lo[0], lo[1]), pk2(lo[2], lo[3]), pk2(lo[4], lo[5]), pk2(lo[6], lo[7])};
;         ahi[mi] = __builtin_bit_cast(bf16x8, hw); alo[mi] = __builtin_bit_cast(bf16x8, lw); }
; #pragma unroll
;     for (int n = 0; n < 5; ++n)
; #pragma unroll
;         for (int mi = 0; mi < 2; ++mi) { acc[mi][n] = __builtin_amdgcn_mfma_f32_16x16x32_bf16(ahi[mi], W.wh[n], acc[mi][n], 0, 0, 0);
;             acc[mi][n] = __builtin_amdgcn_mfma_f32_16x16x32_bf16(alo[mi], W.wh[n], acc[mi][n], 0, 0, 0);
;             acc[mi][n] = __builtin_amdgcn_mfma_f32_16x16x32_bf16(ahi[mi], W.wl[n], acc[mi][n], 0, 0, 0); }
; }
; __device__ __forceinline__ void p5_router(Frame& F) {
;     const bf16_t* H = (const bf16_t*)(F.ws + WS_HB);
;     const bf16_t* RBH = (const bf16_t*)(F.ws + WS_RB); const bf16_t* RBL = RBH + 80 * D;
;     unsigned* ctl = (unsigned*)(F.ws + WS_CTL);
;     LAS float* part = (LAS float*)F.lds;
;     LAS float* lg = part + 4 * 64 * 80;
;     LAS float* ssp = lg + 64 * 80;
;     LAS float* rs = ssp + 256;
;     const int lane = F.lane, wave = F.wave;
;     for (int tile = F.bid; tile < M / 64; tile += F.G) {
;         const int m0 = tile * 64;
.Lrt_prodone:
	v_mov_b32_e32 v18, 0
	v_mov_b32_e32 v19, 0
	v_mov_b32_e32 v20, 0
	v_mov_b32_e32 v21, 0
	v_mov_b32_e32 v22, 0
	v_mov_b32_e32 v23, 0
	v_mov_b32_e32 v24, 0
	v_mov_b32_e32 v25, 0
	v_mov_b32_e32 v26, 0
	v_mov_b32_e32 v27, 0
	v_mov_b32_e32 v28, 0
	v_mov_b32_e32 v29, 0
	v_mov_b32_e32 v30, 0
	v_mov_b32_e32 v31, 0
	v_mov_b32_e32 v32, 0
	v_mov_b32_e32 v33, 0
	v_mov_b32_e32 v34, 0
	v_mov_b32_e32 v35, 0
	v_mov_b32_e32 v36, 0
	v_mov_b32_e32 v37, 0
	v_mov_b32_e32 v42, 0
	v_mov_b32_e32 v43, 0
	v_mov_b32_e32 v44, 0
	v_mov_b32_e32 v45, 0
	s_mov_b32 s94, 86016
	s_mov_b32 s95, 0
	s_mov_b32 s91, 28672
	s_mov_b32 s25, 57344
	s_barrier
	s_cmp_gt_u32 s84, 3
	s_cbranch_scc1 .Lrt_path3
	s_add_i32 s39, s39, 0x80
	s_and_b32 s39, s39, 0x1fff
	s_add_u32 s40, s86, s39
	s_addc_u32 s41, s87, 0
	s_add_i32 m0, s94, s98
	s_nop 0
	global_load_lds_dwordx4 v208, s[40:41]
	s_add_i32 m0, s94, s99
	s_nop 0
	global_load_lds_dwordx4 v209, s[40:41]
	s_add_i32 m0, s94, s100
	s_nop 0
	global_load_lds_dwordx4 v210, s[40:41]
	s_add_i32 m0, s94, s101
	s_nop 0
	global_load_lds_dwordx4 v211, s[40:41]
	v_add_u32_e32 v214, s95, v212
	v_add_u32_e32 v215, s95, v213
	ds_read_b128 v[38:41], v215
	ds_read_b128 v[58:61], v214 offset:0
	ds_read_b128 v[62:65], v214 offset:2048
	ds_read_b128 v[66:69], v214 offset:4096
	ds_read_b128 v[70:73], v214 offset:6144
	ds_read_b128 v[74:77], v214 offset:8192
	ds_read_b128 v[100:103], v214 offset:10240
	ds_read_b128 v[104:107], v214 offset:12288
	ds_read_b128 v[108:111], v214 offset:14336
	ds_read_b128 v[112:115], v214 offset:16384
	ds_read_b128 v[116:119], v214 offset:18432
	s_waitcnt vmcnt(8)
	s_mov_b32 s33, s94
	s_mov_b32 s94, s95
	s_mov_b32 s95, s91
	s_mov_b32 s91, s25
	s_mov_b32 s25, s33
	s_waitcnt lgkmcnt(0)
	s_barrier
	s_add_i32 s39, s39, 0x80
	s_and_b32 s39, s39, 0x1fff
	s_add_u32 s40, s86, s39
	s_addc_u32 s41, s87, 0
	s_add_i32 m0, s94, s98
	s_nop 0
	global_load_lds_dwordx4 v208, s[40:41]
	s_add_i32 m0, s94, s99
	s_nop 0
	global_load_lds_dwordx4 v209, s[40:41]
	s_add_i32 m0, s94, s100
	s_nop 0
	global_load_lds_dwordx4 v210, s[40:41]
	s_add_i32 m0, s94, s101
	s_nop 0
	global_load_lds_dwordx4 v211, s[40:41]
	v_add_u32_e32 v214, s95, v212
	v_add_u32_e32 v215, s95, v213
	ds_read_b128 v[226:229], v215
	ds_read_b128 v[230:233], v214 offset:0
	ds_read_b128 v[234:237], v214 offset:2048
	ds_read_b128 v[238:241], v214 offset:4096
	ds_read_b128 v[242:245], v214 offset:6144
	ds_read_b128 v[246:249], v214 offset:8192
	ds_read_b128 v[120:123], v214 offset:10240
	ds_read_b128 v[124:127], v214 offset:12288
	ds_read_b128 v[132:135], v214 offset:14336
	ds_read_b128 v[136:139], v214 offset:16384
	ds_read_b128 v[140:143], v214 offset:18432
	v_mfma_f32_16x16x32_bf16 v[18:21], v[38:41], v[58:61], v[18:21]
	v_mfma_f32_16x16x32_bf16 v[22:25], v[38:41], v[62:65], v[22:25]
	v_mfma_f32_16x16x32_bf16 v[26:29], v[38:41], v[66:69], v[26:29]
	v_mfma_f32_16x16x32_bf16 v[30:33], v[38:41], v[70:73], v[30:33]
	v_mfma_f32_16x16x32_bf16 v[34:37], v[38:41], v[74:77], v[34:37]
	v_mfma_f32_16x16x32_bf16 v[42:45], v[38:41], v[38:41], v[42:45]
	v_mfma_f32_16x16x32_bf16 v[18:21], v[38:41], v[100:103], v[18:21]
	v_mfma_f32_16x16x32_bf16 v[22:25], v[38:41], v[104:107], v[22:25]
	v_mfma_f32_16x16x32_bf16 v[26:29], v[38:41], v[108:111], v[26:29]
	v_mfma_f32_16x16x32_bf16 v[30:33], v[38:41], v[112:115], v[30:33]
	v_mfma_f32_16x16x32_bf16 v[34:37], v[38:41], v[116:119], v[34:37]
	s_waitcnt vmcnt(8)
	s_mov_b32 s33, s94
	s_mov_b32 s94, s95
	s_mov_b32 s95, s91
	s_mov_b32 s91, s25
	s_mov_b32 s25, s33
	s_waitcnt lgkmcnt(0)
	s_barrier
	s_add_i32 s39, s39, 0x80
	s_and_b32 s39, s39, 0x1fff
	s_add_u32 s40, s86, s39
	s_addc_u32 s41, s87, 0
	s_add_i32 m0, s94, s98
	s_nop 0
	global_load_lds_dwordx4 v208, s[40:41]
	s_add_i32 m0, s94, s99
	s_nop 0
	global_load_lds_dwordx4 v209, s[40:41]
	s_add_i32 m0, s94, s100
	s_nop 0
	global_load_lds_dwordx4 v210, s[40:41]
	s_add_i32 m0, s94, s101
	s_nop 0
	global_load_lds_dwordx4 v211, s[40:41]
	v_add_u32_e32 v214, s95, v212
	v_add_u32_e32 v215, s95, v213
	ds_read_b128 v[38:41], v215
	ds_read_b128 v[58:61], v214 offset:0
	ds_read_b128 v[62:65], v214 offset:2048
	ds_read_b128 v[66:69], v214 offset:4096
	ds_read_b128 v[70:73], v214 offset:6144
	ds_read_b128 v[74:77], v214 offset:8192
	ds_read_b128 v[100:103], v214 offset:10240
	ds_read_b128 v[104:107], v214 offset:12288
	ds_read_b128 v[108:111], v214 offset:14336
	ds_read_b128 v[112:115], v214 offset:16384
	ds_read_b128 v[116:119], v214 offset:18432
	v_mfma_f32_16x16x32_bf16 v[18:21], v[226:229], v[230:233], v[18:21]
	v_mfma_f32_16x16x32_bf16 v[22:25], v[226:229], v[234:237], v[22:25]
	v_mfma_f32_16x16x32_bf16 v[26:29], v[226:229], v[238:241], v[26:29]
	v_mfma_f32_16x16x32_bf16 v[30:33], v[226:229], v[242:245], v[30:33]
	v_mfma_f32_16x16x32_bf16 v[34:37], v[226:229], v[246:249], v[34:37]
	v_mfma_f32_16x16x32_bf16 v[42:45], v[226:229], v[226:229], v[42:45]
	v_mfma_f32_16x16x32_bf16 v[18:21], v[226:229], v[120:123], v[18:21]
	v_mfma_f32_16x16x32_bf16 v[22:25], v[226:229], v[124:127], v[22:25]
	v_mfma_f32_16x16x32_bf16 v[26:29], v[226:229], v[132:135], v[26:29]
	v_mfma_f32_16x16x32_bf16 v[30:33], v[226:229], v[136:139], v[30:33]
	v_mfma_f32_16x16x32_bf16 v[34:37], v[226:229], v[140:143], v[34:37]
	s_waitcnt vmcnt(8)
	s_mov_b32 s33, s94
	s_mov_b32 s94, s95
	s_mov_b32 s95, s91
	s_mov_b32 s91, s25
	s_mov_b32 s25, s33
	s_waitcnt lgkmcnt(0)
	s_barrier
; __device__ __forceinline__ void rt_step(const RtLoad& L, const bf16_t* bh, const bf16_t* bl, f32x4 (&acc)[2][5], float (&ss)[2], int ko) {
;     RtW W;
; #pragma unroll
;     for (int n = 0; n < 5; ++n) { W.wh[n] = *(const bf16x8*)(bh + (size_t)n * 16 * D + ko); W.wl[n] = *(const bf16x8*)(bl + (size_t)n * 16 * D + ko); }
;     bf16x8 ahi[2], alo[2];
; #pragma unroll
;     for (int mi = 0; mi < 2; ++mi) { const u32x4 xw = L.x[mi]; const f32x4 xa = (f32x4){bflo(xw.x), bfhi(xw.x), bflo(xw.y), bfhi(xw.y)}, xb = (f32x4){bflo(xw.z), bfhi(xw.z), bflo(xw.w), bfhi(xw.w)};
;         ss[mi] += (xa.x * xa.x + xa.y * xa.y) + (xa.z * xa.z + xa.w * xa.w) + (xb.x * xb.x + xb.y * xb.y) + (xb.z * xb.z + xb.w * xb.w);
;         const float u[8] = {xa.x * L.g[0].x, xa.y * L.g[0].y, xa.z * L.g[0].z, xa.w * L.g[0].w, xb.x * L.g[1].x, xb.y * L.g[1].y, xb.z * L.g[1].z, xb.w * L.g[1].w};
;         unsigned hb[8]; float lo[8];
; #pragma unroll
;         for (int j = 0; j < 8; ++j) { hb[j] = f2bf(u[j]); lo[j] = u[j] - __builtin_bit_cast(float, hb[j] << 16); }
;         const u32x4 hw = (u32x4){hb[0] | (hb[1] << 16), hb[2] | (hb[3] << 16), hb[4] | (hb[5] << 16), hb[6] | (hb[7] << 16)};
;         const u32x4 lw = (u32x4){pk2(lo[0], lo[1]), pk2(lo[2], lo[3]), pk2(lo[4], lo[5]), pk2(lo[6], lo[7])};
;         ahi[mi] = __builtin_bit_cast(bf16x8, hw); alo[mi] = __builtin_bit_cast(bf16x8, lw); }
; #pragma unroll
;     for (int n = 0; n < 5; ++n)
; #pragma unroll
;         for (int mi = 0; mi < 2; ++mi) { acc[mi][n] = __builtin_amdgcn_mfma_f32_16x16x32_bf16(ahi[mi], W.wh[n], acc[mi][n], 0, 0, 0);
;             acc[mi][n] = __builtin_amdgcn_mfma_f32_16x16x32_bf16(alo[mi], W.wh[n], acc[mi][n], 0, 0, 0);
;             acc[mi][n] = __builtin_amdgcn_mfma_f32_16x16x32_bf16(ahi[mi], W.wl[n], acc[mi][n], 0, 0, 0); }
; }
; __device__ __forceinline__ void p5_router(Frame& F) {
;     const bf16_t* H = (const bf16_t*)(F.ws + WS_HB);
;     const bf16_t* RBH = (const bf16_t*)(F.ws + WS_RB); const bf16_t* RBL = RBH + 80 * D;
;     unsigned* ctl = (unsigned*)(F.ws + WS_CTL);
;     LAS float* part = (LAS float*)F.lds;
;     LAS float* lg = part + 4 * 64 * 80;
;     LAS float* ssp = lg + 64 * 80;
;     LAS float* rs = ssp + 256;
;     const int lane = F.lane, wave = F.wave;
;     for (int tile = F.bid; tile < M / 64; tile += F.G) {
;         const int m0 = tile * 64;
	s_add_i32 s39, s39, 0x80
	s_and_b32 s39, s39, 0x1fff
	s_add_u32 s40, s86, s39
	s_addc_u32 s41, s87, 0
	s_add_i32 m0, s94, s98
	s_nop 0
	global_load_lds_dwordx4 v208, s[40:41]
	s_add_i32 m0, s94, s99
	s_nop 0
	global_load_lds_dwordx4 v209, s[40:41]
	s_add_i32 m0, s94, s100
	s_nop 0
	global_load_lds_dwordx4 v210, s[40:41]
	s_add_i32 m0, s94, s101
	s_nop 0
	global_load_lds_dwordx4 v211, s[40:41]
	v_add_u32_e32 v214, s95, v212
	v_add_u32_e32 v215, s95, v213
	ds_read_b128 v[226:229], v215
	ds_read_b128 v[230:233], v214 offset:0
	ds_read_b128 v[234:237], v214 offset:2048
	ds_read_b128 v[238:241], v214 offset:4096
	ds_read_b128 v[242:245], v214 offset:6144
	ds_read_b128 v[246:249], v214 offset:8192
	ds_read_b128 v[120:123], v214 offset:10240
	ds_read_b128 v[124:127], v214 offset:12288
	ds_read_b128 v[132:135], v214 offset:14336
	ds_read_b128 v[136:139], v214 offset:16384
	ds_read_b128 v[140:143], v214 offset:18432
	v_mfma_f32_16x16x32_bf16 v[18:21], v[38:41], v[58:61], v[18:21]
	v_mfma_f32_16x16x32_bf16 v[22:25], v[38:41], v[62:65], v[22:25]
	v_mfma_f32_16x16x32_bf16 v[26:29], v[38:41], v[66:69], v[26:29]
	v_mfma_f32_16x16x32_bf16 v[30:33], v[38:41], v[70:73], v[30:33]
	v_mfma_f32_16x16x32_bf16 v[34:37], v[38:41], v[74:77], v[34:37]
	v_mfma_f32_16x16x32_bf16 v[42:45], v[38:41], v[38:41], v[42:45]
	v_mfma_f32_16x16x32_bf16 v[18:21], v[38:41], v[100:103], v[18:21]
	v_mfma_f32_16x16x32_bf16 v[22:25], v[38:41], v[104:107], v[22:25]
	v_mfma_f32_16x16x32_bf16 v[26:29], v[38:41], v[108:111], v[26:29]
	v_mfma_f32_16x16x32_bf16 v[30:33], v[38:41], v[112:115], v[30:33]
	v_mfma_f32_16x16x32_bf16 v[34:37], v[38:41], v[116:119], v[34:37]
	s_waitcnt vmcnt(8)
	s_mov_b32 s33, s94
	s_mov_b32 s94, s95
	s_mov_b32 s95, s91
	s_mov_b32 s91, s25
	s_mov_b32 s25, s33
	s_waitcnt lgkmcnt(0)
	s_barrier
	s_add_i32 s39, s39, 0x80
	s_and_b32 s39, s39, 0x1fff
	s_add_u32 s40, s86, s39
	s_addc_u32 s41, s87, 0
	s_add_i32 m0, s94, s98
	s_nop 0
	global_load_lds_dwordx4 v208, s[40:41]
	s_add_i32 m0, s94, s99
	s_nop 0
	global_load_lds_dwordx4 v209, s[40:41]
	s_add_i32 m0, s94, s100
	s_nop 0
	global_load_lds_dwordx4 v210, s[40:41]
	s_add_i32 m0, s94, s101
	s_nop 0
	global_load_lds_dwordx4 v211, s[40:41]
	v_add_u32_e32 v214, s95, v212
	v_add_u32_e32 v215, s95, v213
	ds_read_b128 v[38:41], v215
	ds_read_b128 v[58:61], v214 offset:0
	ds_read_b128 v[62:65], v214 offset:2048
	ds_read_b128 v[66:69], v214 offset:4096
	ds_read_b128 v[70:73], v214 offset:6144
	ds_read_b128 v[74:77], v214 offset:8192
	ds_read_b128 v[100:103], v214 offset:10240
	ds_read_b128 v[104:107], v214 offset:12288
	ds_read_b128 v[108:111], v214 offset:14336
	ds_read_b128 v[112:115], v214 offset:16384
	ds_read_b128 v[116:119], v214 offset:18432
	v_mfma_f32_16x16x32_bf16 v[18:21], v[226:229], v[230:233], v[18:21]
	v_mfma_f32_16x16x32_bf16 v[22:25], v[226:229], v[234:237], v[22:25]
	v_mfma_f32_16x16x32_bf16 v[26:29], v[226:229], v[238:241], v[26:29]
	v_mfma_f32_16x16x32_bf16 v[30:33], v[226:229], v[242:245], v[30:33]
	v_mfma_f32_16x16x32_bf16 v[34:37], v[226:229], v[246:249], v[34:37]
	v_mfma_f32_16x16x32_bf16 v[42:45], v[226:229], v[226:229], v[42:45]
	v_mfma_f32_16x16x32_bf16 v[18:21], v[226:229], v[120:123], v[18:21]
	v_mfma_f32_16x16x32_bf16 v[22:25], v[226:229], v[124:127], v[22:25]
	v_mfma_f32_16x16x32_bf16 v[26:29], v[226:229], v[132:135], v[26:29]
	v_mfma_f32_16x16x32_bf16 v[30:33], v[226:229], v[136:139], v[30:33]
	v_mfma_f32_16x16x32_bf16 v[34:37], v[226:229], v[140:143], v[34:37]
	s_waitcnt vmcnt(8)
	s_mov_b32 s33, s94
	s_mov_b32 s94, s95
	s_mov_b32 s95, s91
	s_mov_b32 s91, s25
	s_mov_b32 s25, s33
	s_waitcnt lgkmcnt(0)
	s_barrier
	s_mov_b32 s85, 13
.Lrt_loop_p4:
	s_add_i32 s39, s39, 0x80
	s_and_b32 s39, s39, 0x1fff
	s_add_u32 s40, s86, s39
	s_addc_u32 s41, s87, 0
	s_add_i32 m0, s94, s98
	s_nop 0
	global_load_lds_dwordx4 v208, s[40:41]
	s_add_i32 m0, s94, s99
	s_nop 0
	global_load_lds_dwordx4 v209, s[40:41]
	s_add_i32 m0, s94, s100
	s_nop 0
	global_load_lds_dwordx4 v210, s[40:41]
	s_add_i32 m0, s94, s101
	s_nop 0
	global_load_lds_dwordx4 v211, s[40:41]
	v_add_u32_e32 v214, s95, v212
	v_add_u32_e32 v215, s95, v213
	ds_read_b128 v[226:229], v215
	ds_read_b128 v[230:233], v214 offset:0
	ds_read_b128 v[234:237], v214 offset:2048
	ds_read_b128 v[238:241], v214 offset:4096
	ds_read_b128 v[242:245], v214 offset:6144
	ds_read_b128 v[246:249], v214 offset:8192
	ds_read_b128 v[120:123], v214 offset:10240
	ds_read_b128 v[124:127], v214 offset:12288
	ds_read_b128 v[132:135], v214 offset:14336
	ds_read_b128 v[136:139], v214 offset:16384
	ds_read_b128 v[140:143], v214 offset:18432
	v_mfma_f32_16x16x32_bf16 v[18:21], v[38:41], v[58:61], v[18:21]
	v_mfma_f32_16x16x32_bf16 v[22:25], v[38:41], v[62:65], v[22:25]
	v_mfma_f32_16x16x32_bf16 v[26:29], v[38:41], v[66:69], v[26:29]
	v_mfma_f32_16x16x32_bf16 v[30:33], v[38:41], v[70:73], v[30:33]
	v_mfma_f32_16x16x32_bf16 v[34:37], v[38:41], v[74:77], v[34:37]
	v_mfma_f32_16x16x32_bf16 v[42:45], v[38:41], v[38:41], v[42:45]
	v_mfma_f32_16x16x32_bf16 v[18:21], v[38:41], v[100:103], v[18:21]
	v_mfma_f32_16x16x32_bf16 v[22:25], v[38:41], v[104:107], v[22:25]
	v_mfma_f32_16x16x32_bf16 v[26:29], v[38:41], v[108:111], v[26:29]
	v_mfma_f32_16x16x32_bf16 v[30:33], v[38:41], v[112:115], v[30:33]
	v_mfma_f32_16x16x32_bf16 v[34:37], v[38:41], v[116:119], v[34:37]
	s_waitcnt vmcnt(8)
	s_mov_b32 s33, s94
	s_mov_b32 s94, s95
	s_mov_b32 s95, s91
	s_mov_b32 s91, s25
	s_mov_b32 s25, s33
	s_waitcnt lgkmcnt(0)
	s_barrier
; __device__ __forceinline__ void rt_step(const RtLoad& L, const bf16_t* bh, const bf16_t* bl, f32x4 (&acc)[2][5], float (&ss)[2], int ko) {
;     RtW W;
; #pragma unroll
;     for (int n = 0; n < 5; ++n) { W.wh[n] = *(const bf16x8*)(bh + (size_t)n * 16 * D + ko); W.wl[n] = *(const bf16x8*)(bl + (size_t)n * 16 * D + ko); }
;     bf16x8 ahi[2], alo[2];
; #pragma unroll
;     for (int mi = 0; mi < 2; ++mi) { const u32x4 xw = L.x[mi]; const f32x4 xa = (f32x4){bflo(xw.x), bfhi(xw.x), bflo(xw.y), bfhi(xw.y)}, xb = (f32x4){bflo(xw.z), bfhi(xw.z), bflo(xw.w), bfhi(xw.w)};
;         ss[mi] += (xa.x * xa.x + xa.y * xa.y) + (xa.z * xa.z + xa.w * xa.w) + (xb.x * xb.x + xb.y * xb.y) + (xb.z * xb.z + xb.w * xb.w);
;         const float u[8] = {xa.x * L.g[0].x, xa.y * L.g[0].y, xa.z * L.g[0].z, xa.w * L.g[0].w, xb.x * L.g[1].x, xb.y * L.g[1].y, xb.z * L.g[1].z, xb.w * L.g[1].w};
;         unsigned hb[8]; float lo[8];
; #pragma unroll
;         for (int j = 0; j < 8; ++j) { hb[j] = f2bf(u[j]); lo[j] = u[j] - __builtin_bit_cast(float, hb[j] << 16); }
;         const u32x4 hw = (u32x4){hb[0] | (hb[1] << 16), hb[2] | (hb[3] << 16), hb[4] | (hb[5] << 16), hb[6] | (hb[7] << 16)};
;         const u32x4 lw = (u32x4){pk2(lo[0], lo[1]), pk2(lo[2], lo[3]), pk2(lo[4], lo[5]), pk2(lo[6], lo[7])};
;         ahi[mi] = __builtin_bit_cast(bf16x8, hw); alo[mi] = __builtin_bit_cast(bf16x8, lw); }
; #pragma unroll
;     for (int n = 0; n < 5; ++n)
; #pragma unroll
;         for (int mi = 0; mi < 2; ++mi) { acc[mi][n] = __builtin_amdgcn_mfma_f32_16x16x32_bf16(ahi[mi], W.wh[n], acc[mi][n], 0, 0, 0);
;             acc[mi][n] = __builtin_amdgcn_mfma_f32_16x16x32_bf16(alo[mi], W.wh[n], acc[mi][n], 0, 0, 0);
;             acc[mi][n] = __builtin_amdgcn_mfma_f32_16x16x32_bf16(ahi[mi], W.wl[n], acc[mi][n], 0, 0, 0); }
; }
; __device__ __forceinline__ void p5_router(Frame& F) {
;     const bf16_t* H = (const bf16_t*)(F.ws + WS_HB);
;     const bf16_t* RBH = (const bf16_t*)(F.ws + WS_RB); const bf16_t* RBL = RBH + 80 * D;
;     unsigned* ctl = (unsigned*)(F.ws + WS_CTL);
;     LAS float* part = (LAS float*)F.lds;
;     LAS float* lg = part + 4 * 64 * 80;
;     LAS float* ssp = lg + 64 * 80;
;     LAS float* rs = ssp + 256;
;     const int lane = F.lane, wave = F.wave;
;     for (int tile = F.bid; tile < M / 64; tile += F.G) {
;         const int m0 = tile * 64;
	s_add_i32 s39, s39, 0x80
	s_and_b32 s39, s39, 0x1fff
	s_add_u32 s40, s86, s39
	s_addc_u32 s41, s87, 0
	s_add_i32 m0, s94, s98
	s_nop 0
	global_load_lds_dwordx4 v208, s[40:41]
	s_add_i32 m0, s94, s99
	s_nop 0
	global_load_lds_dwordx4 v209, s[40:41]
	s_add_i32 m0, s94, s100
	s_nop 0
	global_load_lds_dwordx4 v210, s[40:41]
	s_add_i32 m0, s94, s101
	s_nop 0
	global_load_lds_dwordx4 v211, s[40:41]
	v_add_u32_e32 v214, s95, v212
	v_add_u32_e32 v215, s95, v213
	ds_read_b128 v[38:41], v215
	ds_read_b128 v[58:61], v214 offset:0
	ds_read_b128 v[62:65], v214 offset:2048
	ds_read_b128 v[66:69], v214 offset:4096
	ds_read_b128 v[70:73], v214 offset:6144
	ds_read_b128 v[74:77], v214 offset:8192
	ds_read_b128 v[100:103], v214 offset:10240
	ds_read_b128 v[104:107], v214 offset:12288
	ds_read_b128 v[108:111], v214 offset:14336
	ds_read_b128 v[112:115], v214 offset:16384
	ds_read_b128 v[116:119], v214 offset:18432
	v_mfma_f32_16x16x32_bf16 v[18:21], v[226:229], v[230:233], v[18:21]
	v_mfma_f32_16x16x32_bf16 v[22:25], v[226:229], v[234:237], v[22:25]
	v_mfma_f32_16x16x32_bf16 v[26:29], v[226:229], v[238:241], v[26:29]
	v_mfma_f32_16x16x32_bf16 v[30:33], v[226:229], v[242:245], v[30:33]
	v_mfma_f32_16x16x32_bf16 v[34:37], v[226:229], v[246:249], v[34:37]
	v_mfma_f32_16x16x32_bf16 v[42:45], v[226:229], v[226:229], v[42:45]
	v_mfma_f32_16x16x32_bf16 v[18:21], v[226:229], v[120:123], v[18:21]
	v_mfma_f32_16x16x32_bf16 v[22:25], v[226:229], v[124:127], v[22:25]
	v_mfma_f32_16x16x32_bf16 v[26:29], v[226:229], v[132:135], v[26:29]
	v_mfma_f32_16x16x32_bf16 v[30:33], v[226:229], v[136:139], v[30:33]
	v_mfma_f32_16x16x32_bf16 v[34:37], v[226:229], v[140:143], v[34:37]
	s_waitcnt vmcnt(8)
	s_mov_b32 s33, s94
	s_mov_b32 s94, s95
	s_mov_b32 s95, s91
	s_mov_b32 s91, s25
	s_mov_b32 s25, s33
	s_waitcnt lgkmcnt(0)
	s_barrier
	s_add_i32 s39, s39, 0x80
	s_and_b32 s39, s39, 0x1fff
	s_add_u32 s40, s86, s39
	s_addc_u32 s41, s87, 0
	s_add_i32 m0, s94, s98
	s_nop 0
	global_load_lds_dwordx4 v208, s[40:41]
	s_add_i32 m0, s94, s99
	s_nop 0
	global_load_lds_dwordx4 v209, s[40:41]
	s_add_i32 m0, s94, s100
	s_nop 0
	global_load_lds_dwordx4 v210, s[40:41]
	s_add_i32 m0, s94, s101
	s_nop 0
	global_load_lds_dwordx4 v211, s[40:41]
	v_add_u32_e32 v214, s95, v212
	v_add_u32_e32 v215, s95, v213
	ds_read_b128 v[226:229], v215
	ds_read_b128 v[230:233], v214 offset:0
	ds_read_b128 v[234:237], v214 offset:2048
	ds_read_b128 v[238:241], v214 offset:4096
	ds_read_b128 v[242:245], v214 offset:6144
	ds_read_b128 v[246:249], v214 offset:8192
	ds_read_b128 v[120:123], v214 offset:10240
	ds_read_b128 v[124:127], v214 offset:12288
	ds_read_b128 v[132:135], v214 offset:14336
	ds_read_b128 v[136:139], v214 offset:16384
	ds_read_b128 v[140:143], v214 offset:18432
	v_mfma_f32_16x16x32_bf16 v[18:21], v[38:41], v[58:61], v[18:21]
	v_mfma_f32_16x16x32_bf16 v[22:25], v[38:41], v[62:65], v[22:25]
	v_mfma_f32_16x16x32_bf16 v[26:29], v[38:41], v[66:69], v[26:29]
	v_mfma_f32_16x16x32_bf16 v[30:33], v[38:41], v[70:73], v[30:33]
	v_mfma_f32_16x16x32_bf16 v[34:37], v[38:41], v[74:77], v[34:37]
	v_mfma_f32_16x16x32_bf16 v[42:45], v[38:41], v[38:41], v[42:45]
	v_mfma_f32_16x16x32_bf16 v[18:21], v[38:41], v[100:103], v[18:21]
	v_mfma_f32_16x16x32_bf16 v[22:25], v[38:41], v[104:107], v[22:25]
	v_mfma_f32_16x16x32_bf16 v[26:29], v[38:41], v[108:111], v[26:29]
	v_mfma_f32_16x16x32_bf16 v[30:33], v[38:41], v[112:115], v[30:33]
	v_mfma_f32_16x16x32_bf16 v[34:37], v[38:41], v[116:119], v[34:37]
	s_waitcnt vmcnt(8)
	s_mov_b32 s33, s94
	s_mov_b32 s94, s95
	s_mov_b32 s95, s91
	s_mov_b32 s91, s25
	s_mov_b32 s25, s33
	s_waitcnt lgkmcnt(0)
	s_barrier
	s_add_i32 s39, s39, 0x80
	s_and_b32 s39, s39, 0x1fff
	s_add_u32 s40, s86, s39
	s_addc_u32 s41, s87, 0
	s_add_i32 m0, s94, s98
	s_nop 0
	global_load_lds_dwordx4 v208, s[40:41]
	s_add_i32 m0, s94, s99
	s_nop 0
	global_load_lds_dwordx4 v209, s[40:41]
	s_add_i32 m0, s94, s100
	s_nop 0
	global_load_lds_dwordx4 v210, s[40:41]
	s_add_i32 m0, s94, s101
	s_nop 0
	global_load_lds_dwordx4 v211, s[40:41]
	v_add_u32_e32 v214, s95, v212
	v_add_u32_e32 v215, s95, v213
	ds_read_b128 v[38:41], v215
	ds_read_b128 v[58:61], v214 offset:0
	ds_read_b128 v[62:65], v214 offset:2048
	ds_read_b128 v[66:69], v214 offset:4096
	ds_read_b128 v[70:73], v214 offset:6144
	ds_read_b128 v[74:77], v214 offset:8192
	ds_read_b128 v[100:103], v214 offset:10240
	ds_read_b128 v[104:107], v214 offset:12288
	ds_read_b128 v[108:111], v214 offset:14336
	ds_read_b128 v[112:115], v214 offset:16384
	ds_read_b128 v[116:119], v214 offset:18432
	v_mfma_f32_16x16x32_bf16 v[18:21], v[226:229], v[230:233], v[18:21]
	v_mfma_f32_16x16x32_bf16 v[22:25], v[226:229], v[234:237], v[22:25]
	v_mfma_f32_16x16x32_bf16 v[26:29], v[226:229], v[238:241], v[26:29]
	v_mfma_f32_16x16x32_bf16 v[30:33], v[226:229], v[242:245], v[30:33]
	v_mfma_f32_16x16x32_bf16 v[34:37], v[226:229], v[246:249], v[34:37]
	v_mfma_f32_16x16x32_bf16 v[42:45], v[226:229], v[226:229], v[42:45]
	v_mfma_f32_16x16x32_bf16 v[18:21], v[226:229], v[120:123], v[18:21]
	v_mfma_f32_16x16x32_bf16 v[22:25], v[226:229], v[124:127], v[22:25]
	v_mfma_f32_16x16x32_bf16 v[26:29], v[226:229], v[132:135], v[26:29]
	v_mfma_f32_16x16x32_bf16 v[30:33], v[226:229], v[136:139], v[30:33]
	v_mfma_f32_16x16x32_bf16 v[34:37], v[226:229], v[140:143], v[34:37]
	s_waitcnt vmcnt(8)
	s_mov_b32 s33, s94
	s_mov_b32 s94, s95
	s_mov_b32 s95, s91
	s_mov_b32 s91, s25
	s_mov_b32 s25, s33
	s_waitcnt lgkmcnt(0)
	s_barrier
	s_sub_u32 s85, s85, 1
	s_cmp_lg_u32 s85, 0
	s_cbranch_scc1 .Lrt_loop_p4
; __device__ __forceinline__ void rt_step(const RtLoad& L, const bf16_t* bh, const bf16_t* bl, f32x4 (&acc)[2][5], float (&ss)[2], int ko) {
;     RtW W;
; #pragma unroll
;     for (int n = 0; n < 5; ++n) { W.wh[n] = *(const bf16x8*)(bh + (size_t)n * 16 * D + ko); W.wl[n] = *(const bf16x8*)(bl + (size_t)n * 16 * D + ko); }
;     bf16x8 ahi[2], alo[2];
; #pragma unroll
;     for (int mi = 0; mi < 2; ++mi) { const u32x4 xw = L.x[mi]; const f32x4 xa = (f32x4){bflo(xw.x), bfhi(xw.x), bflo(xw.y), bfhi(xw.y)}, xb = (f32x4){bflo(xw.z), bfhi(xw.z), bflo(xw.w), bfhi(xw.w)};
;         ss[mi] += (xa.x * xa.x + xa.y * xa.y) + (xa.z * xa.z + xa.w * xa.w) + (xb.x * xb.x + xb.y * xb.y) + (xb.z * xb.z + xb.w * xb.w);
;         const float u[8] = {xa.x * L.g[0].x, xa.y * L.g[0].y, xa.z * L.g[0].z, xa.w * L.g[0].w, xb.x * L.g[1].x, xb.y * L.g[1].y, xb.z * L.g[1].z, xb.w * L.g[1].w};
;         unsigned hb[8]; float lo[8];
; #pragma unroll
;         for (int j = 0; j < 8; ++j) { hb[j] = f2bf(u[j]); lo[j] = u[j] - __builtin_bit_cast(float, hb[j] << 16); }
;         const u32x4 hw = (u32x4){hb[0] | (hb[1] << 16), hb[2] | (hb[3] << 16), hb[4] | (hb[5] << 16), hb[6] | (hb[7] << 16)};
;         const u32x4 lw = (u32x4){pk2(lo[0], lo[1]), pk2(lo[2], lo[3]), pk2(lo[4], lo[5]), pk2(lo[6], lo[7])};
;         ahi[mi] = __builtin_bit_cast(bf16x8, hw); alo[mi] = __builtin_bit_cast(bf16x8, lw); }
; #pragma unroll
;     for (int n = 0; n < 5; ++n)
; #pragma unroll
;         for (int mi = 0; mi < 2; ++mi) { acc[mi][n] = __builtin_amdgcn_mfma_f32_16x16x32_bf16(ahi[mi], W.wh[n], acc[mi][n], 0, 0, 0);
;             acc[mi][n] = __builtin_amdgcn_mfma_f32_16x16x32_bf16(alo[mi], W.wh[n], acc[mi][n], 0, 0, 0);
;             acc[mi][n] = __builtin_amdgcn_mfma_f32_16x16x32_bf16(ahi[mi], W.wl[n], acc[mi][n], 0, 0, 0); }
; }
; __device__ __forceinline__ void p5_router(Frame& F) {
;     const bf16_t* H = (const bf16_t*)(F.ws + WS_HB);
;     const bf16_t* RBH = (const bf16_t*)(F.ws + WS_RB); const bf16_t* RBL = RBH + 80 * D;
;     unsigned* ctl = (unsigned*)(F.ws + WS_CTL);
;     LAS float* part = (LAS float*)F.lds;
;     LAS float* lg = part + 4 * 64 * 80;
;     LAS float* ssp = lg + 64 * 80;
;     LAS float* rs = ssp + 256;
;     const int lane = F.lane, wave = F.wave;
;     for (int tile = F.bid; tile < M / 64; tile += F.G) {
;         const int m0 = tile * 64;
	s_add_i32 s39, s39, 0x80
	s_and_b32 s39, s39, 0x1fff
	s_add_u32 s40, s86, s39
	s_addc_u32 s41, s87, 0
	s_add_i32 m0, s94, s98
	s_nop 0
	global_load_lds_dwordx4 v208, s[40:41]
	s_add_i32 m0, s94, s99
	s_nop 0
	global_load_lds_dwordx4 v209, s[40:41]
	s_add_i32 m0, s94, s100
	s_nop 0
	global_load_lds_dwordx4 v210, s[40:41]
	s_add_i32 m0, s94, s101
	s_nop 0
	global_load_lds_dwordx4 v211, s[40:41]
	v_add_u32_e32 v214, s95, v212
	v_add_u32_e32 v215, s95, v213
	ds_read_b128 v[226:229], v215
	ds_read_b128 v[230:233], v214 offset:0
	ds_read_b128 v[234:237], v214 offset:2048
	ds_read_b128 v[238:241], v214 offset:4096
	ds_read_b128 v[242:245], v214 offset:6144
	ds_read_b128 v[246:249], v214 offset:8192
	ds_read_b128 v[120:123], v214 offset:10240
	ds_read_b128 v[124:127], v214 offset:12288
	ds_read_b128 v[132:135], v214 offset:14336
	ds_read_b128 v[136:139], v214 offset:16384
	ds_read_b128 v[140:143], v214 offset:18432
	v_mfma_f32_16x16x32_bf16 v[18:21], v[38:41], v[58:61], v[18:21]
	v_mfma_f32_16x16x32_bf16 v[22:25], v[38:41], v[62:65], v[22:25]
	v_mfma_f32_16x16x32_bf16 v[26:29], v[38:41], v[66:69], v[26:29]
	v_mfma_f32_16x16x32_bf16 v[30:33], v[38:41], v[70:73], v[30:33]
	v_mfma_f32_16x16x32_bf16 v[34:37], v[38:41], v[74:77], v[34:37]
	v_mfma_f32_16x16x32_bf16 v[42:45], v[38:41], v[38:41], v[42:45]
	v_mfma_f32_16x16x32_bf16 v[18:21], v[38:41], v[100:103], v[18:21]
	v_mfma_f32_16x16x32_bf16 v[22:25], v[38:41], v[104:107], v[22:25]
	v_mfma_f32_16x16x32_bf16 v[26:29], v[38:41], v[108:111], v[26:29]
	v_mfma_f32_16x16x32_bf16 v[30:33], v[38:41], v[112:115], v[30:33]
	v_mfma_f32_16x16x32_bf16 v[34:37], v[38:41], v[116:119], v[34:37]
	s_waitcnt vmcnt(8)
	s_mov_b32 s33, s94
	s_mov_b32 s94, s95
	s_mov_b32 s95, s91
	s_mov_b32 s91, s25
	s_mov_b32 s25, s33
	s_waitcnt lgkmcnt(0)
	s_barrier
	s_add_i32 s39, s39, 0x80
	s_and_b32 s39, s39, 0x1fff
	s_add_u32 s40, s86, s39
	s_addc_u32 s41, s87, 0
	s_add_i32 m0, s94, s98
	s_nop 0
	global_load_lds_dwordx4 v208, s[40:41]
	s_add_i32 m0, s94, s99
	s_nop 0
	global_load_lds_dwordx4 v209, s[40:41]
	s_add_i32 m0, s94, s100
	s_nop 0
	global_load_lds_dwordx4 v210, s[40:41]
	s_add_i32 m0, s94, s101
	s_nop 0
	global_load_lds_dwordx4 v211, s[40:41]
	v_add_u32_e32 v214, s95, v212
	v_add_u32_e32 v215, s95, v213
	ds_read_b128 v[38:41], v215
	ds_read_b128 v[58:61], v214 offset:0
	ds_read_b128 v[62:65], v214 offset:2048
	ds_read_b128 v[66:69], v214 offset:4096
	ds_read_b128 v[70:73], v214 offset:6144
	ds_read_b128 v[74:77], v214 offset:8192
	ds_read_b128 v[100:103], v214 offset:10240
	ds_read_b128 v[104:107], v214 offset:12288
	ds_read_b128 v[108:111], v214 offset:14336
	ds_read_b128 v[112:115], v214 offset:16384
	ds_read_b128 v[116:119], v214 offset:18432
	v_mfma_f32_16x16x32_bf16 v[18:21], v[226:229], v[230:233], v[18:21]
	v_mfma_f32_16x16x32_bf16 v[22:25], v[226:229], v[234:237], v[22:25]
	v_mfma_f32_16x16x32_bf16 v[26:29], v[226:229], v[238:241], v[26:29]
	v_mfma_f32_16x16x32_bf16 v[30:33], v[226:229], v[242:245], v[30:33]
	v_mfma_f32_16x16x32_bf16 v[34:37], v[226:229], v[246:249], v[34:37]
	v_mfma_f32_16x16x32_bf16 v[42:45], v[226:229], v[226:229], v[42:45]
	v_mfma_f32_16x16x32_bf16 v[18:21], v[226:229], v[120:123], v[18:21]
	v_mfma_f32_16x16x32_bf16 v[22:25], v[226:229], v[124:127], v[22:25]
	v_mfma_f32_16x16x32_bf16 v[26:29], v[226:229], v[132:135], v[26:29]
	v_mfma_f32_16x16x32_bf16 v[30:33], v[226:229], v[136:139], v[30:33]
	v_mfma_f32_16x16x32_bf16 v[34:37], v[226:229], v[140:143], v[34:37]
	s_waitcnt vmcnt(8)
	s_mov_b32 s33, s94
	s_mov_b32 s94, s95
	s_mov_b32 s95, s91
	s_mov_b32 s91, s25
	s_mov_b32 s25, s33
	s_waitcnt lgkmcnt(0)
	s_barrier
	s_add_i32 s39, s39, 0x80
	s_and_b32 s39, s39, 0x1fff
	s_add_u32 s40, s86, s39
	s_addc_u32 s41, s87, 0
	s_add_i32 m0, s94, s98
	s_nop 0
	global_load_lds_dwordx4 v208, s[40:41]
	s_add_i32 m0, s94, s99
	s_nop 0
	global_load_lds_dwordx4 v209, s[40:41]
	s_add_i32 m0, s94, s100
	s_nop 0
	global_load_lds_dwordx4 v210, s[40:41]
	s_add_i32 m0, s94, s101
	s_nop 0
	global_load_lds_dwordx4 v211, s[40:41]
	v_add_u32_e32 v214, s95, v212
	v_add_u32_e32 v215, s95, v213
	ds_read_b128 v[226:229], v215
	ds_read_b128 v[230:233], v214 offset:0
	ds_read_b128 v[234:237], v214 offset:2048
	ds_read_b128 v[238:241], v214 offset:4096
	ds_read_b128 v[242:245], v214 offset:6144
	ds_read_b128 v[246:249], v214 offset:8192
	ds_read_b128 v[120:123], v214 offset:10240
	ds_read_b128 v[124:127], v214 offset:12288
	ds_read_b128 v[132:135], v214 offset:14336
	ds_read_b128 v[136:139], v214 offset:16384
	ds_read_b128 v[140:143], v214 offset:18432
	v_mfma_f32_16x16x32_bf16 v[18:21], v[38:41], v[58:61], v[18:21]
	v_mfma_f32_16x16x32_bf16 v[22:25], v[38:41], v[62:65], v[22:25]
	v_mfma_f32_16x16x32_bf16 v[26:29], v[38:41], v[66:69], v[26:29]
	v_mfma_f32_16x16x32_bf16 v[30:33], v[38:41], v[70:73], v[30:33]
	v_mfma_f32_16x16x32_bf16 v[34:37], v[38:41], v[74:77], v[34:37]
	v_mfma_f32_16x16x32_bf16 v[42:45], v[38:41], v[38:41], v[42:45]
	v_mfma_f32_16x16x32_bf16 v[18:21], v[38:41], v[100:103], v[18:21]
	v_mfma_f32_16x16x32_bf16 v[22:25], v[38:41], v[104:107], v[22:25]
	v_mfma_f32_16x16x32_bf16 v[26:29], v[38:41], v[108:111], v[26:29]
	v_mfma_f32_16x16x32_bf16 v[30:33], v[38:41], v[112:115], v[30:33]
	v_mfma_f32_16x16x32_bf16 v[34:37], v[38:41], v[116:119], v[34:37]
	s_waitcnt vmcnt(8)
	s_mov_b32 s33, s94
	s_mov_b32 s94, s95
	s_mov_b32 s95, s91
	s_mov_b32 s91, s25
	s_mov_b32 s25, s33
	s_waitcnt lgkmcnt(0)
	s_barrier
; __device__ __forceinline__ void rt_step(const RtLoad& L, const bf16_t* bh, const bf16_t* bl, f32x4 (&acc)[2][5], float (&ss)[2], int ko) {
;     RtW W;
; #pragma unroll
;     for (int n = 0; n < 5; ++n) { W.wh[n] = *(const bf16x8*)(bh + (size_t)n * 16 * D + ko); W.wl[n] = *(const bf16x8*)(bl + (size_t)n * 16 * D + ko); }
;     bf16x8 ahi[2], alo[2];
; #pragma unroll
;     for (int mi = 0; mi < 2; ++mi) { const u32x4 xw = L.x[mi]; const f32x4 xa = (f32x4){bflo(xw.x), bfhi(xw.x), bflo(xw.y), bfhi(xw.y)}, xb = (f32x4){bflo(xw.z), bfhi(xw.z), bflo(xw.w), bfhi(xw.w)};
;         ss[mi] += (xa.x * xa.x + xa.y * xa.y) + (xa.z * xa.z + xa.w * xa.w) + (xb.x * xb.x + xb.y * xb.y) + (xb.z * xb.z + xb.w * xb.w);
;         const float u[8] = {xa.x * L.g[0].x, xa.y * L.g[0].y, xa.z * L.g[0].z, xa.w * L.g[0].w, xb.x * L.g[1].x, xb.y * L.g[1].y, xb.z * L.g[1].z, xb.w * L.g[1].w};
;         unsigned hb[8]; float lo[8];
; #pragma unroll
;         for (int j = 0; j < 8; ++j) { hb[j] = f2bf(u[j]); lo[j] = u[j] - __builtin_bit_cast(float, hb[j] << 16); }
;         const u32x4 hw = (u32x4){hb[0] | (hb[1] << 16), hb[2] | (hb[3] << 16), hb[4] | (hb[5] << 16), hb[6] | (hb[7] << 16)};
;         const u32x4 lw = (u32x4){pk2(lo[0], lo[1]), pk2(lo[2], lo[3]), pk2(lo[4], lo[5]), pk2(lo[6], lo[7])};
;         ahi[mi] = __builtin_bit_cast(bf16x8, hw); alo[mi] = __builtin_bit_cast(bf16x8, lw); }
; #pragma unroll
;     for (int n = 0; n < 5; ++n)
; #pragma unroll
;         for (int mi = 0; mi < 2; ++mi) { acc[mi][n] = __builtin_amdgcn_mfma_f32_16x16x32_bf16(ahi[mi], W.wh[n], acc[mi][n], 0, 0, 0);
;             acc[mi][n] = __builtin_amdgcn_mfma_f32_16x16x32_bf16(alo[mi], W.wh[n], acc[mi][n], 0, 0, 0);
;             acc[mi][n] = __builtin_amdgcn_mfma_f32_16x16x32_bf16(ahi[mi], W.wl[n], acc[mi][n], 0, 0, 0); }
; }
; __device__ __forceinline__ void p5_router(Frame& F) {
;     const bf16_t* H = (const bf16_t*)(F.ws + WS_HB);
;     const bf16_t* RBH = (const bf16_t*)(F.ws + WS_RB); const bf16_t* RBL = RBH + 80 * D;
;     unsigned* ctl = (unsigned*)(F.ws + WS_CTL);
;     LAS float* part = (LAS float*)F.lds;
;     LAS float* lg = part + 4 * 64 * 80;
;     LAS float* ssp = lg + 64 * 80;
;     LAS float* rs = ssp + 256;
;     const int lane = F.lane, wave = F.wave;
;     for (int tile = F.bid; tile < M / 64; tile += F.G) {
;         const int m0 = tile * 64;
	s_add_i32 s39, s39, 0x80
	s_and_b32 s39, s39, 0x1fff
	s_add_u32 s40, s86, s39
	s_addc_u32 s41, s87, 0
	s_add_i32 m0, s94, s98
	s_nop 0
	global_load_lds_dwordx4 v208, s[40:41]
	s_add_i32 m0, s94, s99
	s_nop 0
	global_load_lds_dwordx4 v209, s[40:41]
	s_add_i32 m0, s94, s100
	s_nop 0
	global_load_lds_dwordx4 v210, s[40:41]
	s_add_i32 m0, s94, s101
	s_nop 0
	global_load_lds_dwordx4 v211, s[40:41]
	v_add_u32_e32 v214, s95, v212
	v_add_u32_e32 v215, s95, v213
	ds_read_b128 v[38:41], v215
	ds_read_b128 v[58:61], v214 offset:0
	ds_read_b128 v[62:65], v214 offset:2048
	ds_read_b128 v[66:69], v214 offset:4096
	ds_read_b128 v[70:73], v214 offset:6144
	ds_read_b128 v[74:77], v214 offset:8192
	ds_read_b128 v[100:103], v214 offset:10240
	ds_read_b128 v[104:107], v214 offset:12288
	ds_read_b128 v[108:111], v214 offset:14336
	ds_read_b128 v[112:115], v214 offset:16384
	ds_read_b128 v[116:119], v214 offset:18432
	v_mfma_f32_16x16x32_bf16 v[18:21], v[226:229], v[230:233], v[18:21]
	v_mfma_f32_16x16x32_bf16 v[22:25], v[226:229], v[234:237], v[22:25]
	v_mfma_f32_16x16x32_bf16 v[26:29], v[226:229], v[238:241], v[26:29]
	v_mfma_f32_16x16x32_bf16 v[30:33], v[226:229], v[242:245], v[30:33]
	v_mfma_f32_16x16x32_bf16 v[34:37], v[226:229], v[246:249], v[34:37]
	v_mfma_f32_16x16x32_bf16 v[42:45], v[226:229], v[226:229], v[42:45]
	v_mfma_f32_16x16x32_bf16 v[18:21], v[226:229], v[120:123], v[18:21]
	v_mfma_f32_16x16x32_bf16 v[22:25], v[226:229], v[124:127], v[22:25]
	v_mfma_f32_16x16x32_bf16 v[26:29], v[226:229], v[132:135], v[26:29]
	v_mfma_f32_16x16x32_bf16 v[30:33], v[226:229], v[136:139], v[30:33]
	v_mfma_f32_16x16x32_bf16 v[34:37], v[226:229], v[140:143], v[34:37]
	s_waitcnt vmcnt(8)
	s_mov_b32 s33, s94
	s_mov_b32 s94, s95
	s_mov_b32 s95, s91
	s_mov_b32 s91, s25
	s_mov_b32 s25, s33
	s_waitcnt lgkmcnt(0)
	s_barrier
	v_add_u32_e32 v214, s95, v212
	v_add_u32_e32 v215, s95, v213
	ds_read_b128 v[226:229], v215
	ds_read_b128 v[230:233], v214 offset:0
	ds_read_b128 v[234:237], v214 offset:2048
	ds_read_b128 v[238:241], v214 offset:4096
	ds_read_b128 v[242:245], v214 offset:6144
	ds_read_b128 v[246:249], v214 offset:8192
	ds_read_b128 v[120:123], v214 offset:10240
	ds_read_b128 v[124:127], v214 offset:12288
	ds_read_b128 v[132:135], v214 offset:14336
	ds_read_b128 v[136:139], v214 offset:16384
	ds_read_b128 v[140:143], v214 offset:18432
	v_mfma_f32_16x16x32_bf16 v[18:21], v[38:41], v[58:61], v[18:21]
	v_mfma_f32_16x16x32_bf16 v[22:25], v[38:41], v[62:65], v[22:25]
	v_mfma_f32_16x16x32_bf16 v[26:29], v[38:41], v[66:69], v[26:29]
	v_mfma_f32_16x16x32_bf16 v[30:33], v[38:41], v[70:73], v[30:33]
	v_mfma_f32_16x16x32_bf16 v[34:37], v[38:41], v[74:77], v[34:37]
	v_mfma_f32_16x16x32_bf16 v[42:45], v[38:41], v[38:41], v[42:45]
	v_mfma_f32_16x16x32_bf16 v[18:21], v[38:41], v[100:103], v[18:21]
	v_mfma_f32_16x16x32_bf16 v[22:25], v[38:41], v[104:107], v[22:25]
	v_mfma_f32_16x16x32_bf16 v[26:29], v[38:41], v[108:111], v[26:29]
	v_mfma_f32_16x16x32_bf16 v[30:33], v[38:41], v[112:115], v[30:33]
	v_mfma_f32_16x16x32_bf16 v[34:37], v[38:41], v[116:119], v[34:37]
	s_waitcnt vmcnt(4)
	s_mov_b32 s33, s94
	s_mov_b32 s94, s95
	s_mov_b32 s95, s91
	s_mov_b32 s91, s25
	s_mov_b32 s25, s33
	s_waitcnt lgkmcnt(0)
	s_barrier
	v_add_u32_e32 v214, s95, v212
	v_add_u32_e32 v215, s95, v213
	ds_read_b128 v[38:41], v215
	ds_read_b128 v[58:61], v214 offset:0
	ds_read_b128 v[62:65], v214 offset:2048
	ds_read_b128 v[66:69], v214 offset:4096
	ds_read_b128 v[70:73], v214 offset:6144
	ds_read_b128 v[74:77], v214 offset:8192
	ds_read_b128 v[100:103], v214 offset:10240
	ds_read_b128 v[104:107], v214 offset:12288
	ds_read_b128 v[108:111], v214 offset:14336
	ds_read_b128 v[112:115], v214 offset:16384
	ds_read_b128 v[116:119], v214 offset:18432
	v_mfma_f32_16x16x32_bf16 v[18:21], v[226:229], v[230:233], v[18:21]
	v_mfma_f32_16x16x32_bf16 v[22:25], v[226:229], v[234:237], v[22:25]
	v_mfma_f32_16x16x32_bf16 v[26:29], v[226:229], v[238:241], v[26:29]
	v_mfma_f32_16x16x32_bf16 v[30:33], v[226:229], v[242:245], v[30:33]
	v_mfma_f32_16x16x32_bf16 v[34:37], v[226:229], v[246:249], v[34:37]
	v_mfma_f32_16x16x32_bf16 v[42:45], v[226:229], v[226:229], v[42:45]
	v_mfma_f32_16x16x32_bf16 v[18:21], v[226:229], v[120:123], v[18:21]
	v_mfma_f32_16x16x32_bf16 v[22:25], v[226:229], v[124:127], v[22:25]
	v_mfma_f32_16x16x32_bf16 v[26:29], v[226:229], v[132:135], v[26:29]
	v_mfma_f32_16x16x32_bf16 v[30:33], v[226:229], v[136:139], v[30:33]
	v_mfma_f32_16x16x32_bf16 v[34:37], v[226:229], v[140:143], v[34:37]
	s_waitcnt vmcnt(0)
	s_mov_b32 s33, s94
	s_mov_b32 s94, s95
	s_mov_b32 s95, s91
	s_mov_b32 s91, s25
	s_mov_b32 s25, s33
	s_waitcnt lgkmcnt(0)
	s_barrier
	v_add_u32_e32 v214, s95, v212
	v_add_u32_e32 v215, s95, v213
	ds_read_b128 v[226:229], v215
	ds_read_b128 v[230:233], v214 offset:0
	ds_read_b128 v[234:237], v214 offset:2048
	ds_read_b128 v[238:241], v214 offset:4096
	ds_read_b128 v[242:245], v214 offset:6144
	ds_read_b128 v[246:249], v214 offset:8192
	ds_read_b128 v[120:123], v214 offset:10240
	ds_read_b128 v[124:127], v214 offset:12288
	ds_read_b128 v[132:135], v214 offset:14336
	ds_read_b128 v[136:139], v214 offset:16384
	ds_read_b128 v[140:143], v214 offset:18432
	v_mfma_f32_16x16x32_bf16 v[18:21], v[38:41], v[58:61], v[18:21]
	v_mfma_f32_16x16x32_bf16 v[22:25], v[38:41], v[62:65], v[22:25]
	v_mfma_f32_16x16x32_bf16 v[26:29], v[38:41], v[66:69], v[26:29]
	v_mfma_f32_16x16x32_bf16 v[30:33], v[38:41], v[70:73], v[30:33]
	v_mfma_f32_16x16x32_bf16 v[34:37], v[38:41], v[74:77], v[34:37]
	v_mfma_f32_16x16x32_bf16 v[42:45], v[38:41], v[38:41], v[42:45]
	v_mfma_f32_16x16x32_bf16 v[18:21], v[38:41], v[100:103], v[18:21]
	v_mfma_f32_16x16x32_bf16 v[22:25], v[38:41], v[104:107], v[22:25]
	v_mfma_f32_16x16x32_bf16 v[26:29], v[38:41], v[108:111], v[26:29]
	v_mfma_f32_16x16x32_bf16 v[30:33], v[38:41], v[112:115], v[30:33]
	v_mfma_f32_16x16x32_bf16 v[34:37], v[38:41], v[116:119], v[34:37]
	s_mov_b32 s33, s94
	s_mov_b32 s94, s95
	s_mov_b32 s95, s91
	s_mov_b32 s91, s25
	s_mov_b32 s25, s33
	s_waitcnt lgkmcnt(0)
	s_barrier
	v_mfma_f32_16x16x32_bf16 v[18:21], v[226:229], v[230:233], v[18:21]
	v_mfma_f32_16x16x32_bf16 v[22:25], v[226:229], v[234:237], v[22:25]
	v_mfma_f32_16x16x32_bf16 v[26:29], v[226:229], v[238:241], v[26:29]
	v_mfma_f32_16x16x32_bf16 v[30:33], v[226:229], v[242:245], v[30:33]
	v_mfma_f32_16x16x32_bf16 v[34:37], v[226:229], v[246:249], v[34:37]
	v_mfma_f32_16x16x32_bf16 v[42:45], v[226:229], v[226:229], v[42:45]
	v_mfma_f32_16x16x32_bf16 v[18:21], v[226:229], v[120:123], v[18:21]
	v_mfma_f32_16x16x32_bf16 v[22:25], v[226:229], v[124:127], v[22:25]
	v_mfma_f32_16x16x32_bf16 v[26:29], v[226:229], v[132:135], v[26:29]
	v_mfma_f32_16x16x32_bf16 v[30:33], v[226:229], v[136:139], v[30:33]
	v_mfma_f32_16x16x32_bf16 v[34:37], v[226:229], v[140:143], v[34:37]
	s_branch .Lrt_out
; __device__ __forceinline__ void rt_step(const RtLoad& L, const bf16_t* bh, const bf16_t* bl, f32x4 (&acc)[2][5], float (&ss)[2], int ko) {
;     RtW W;
; #pragma unroll
;     for (int n = 0; n < 5; ++n) { W.wh[n] = *(const bf16x8*)(bh + (size_t)n * 16 * D + ko); W.wl[n] = *(const bf16x8*)(bl + (size_t)n * 16 * D + ko); }
;     bf16x8 ahi[2], alo[2];
; #pragma unroll
;     for (int mi = 0; mi < 2; ++mi) { const u32x4 xw = L.x[mi]; const f32x4 xa = (f32x4){bflo(xw.x), bfhi(xw.x), bflo(xw.y), bfhi(xw.y)}, xb = (f32x4){bflo(xw.z), bfhi(xw.z), bflo(xw.w), bfhi(xw.w)};
;         ss[mi] += (xa.x * xa.x + xa.y * xa.y) + (xa.z * xa.z + xa.w * xa.w) + (xb.x * xb.x + xb.y * xb.y) + (xb.z * xb.z + xb.w * xb.w);
;         const float u[8] = {xa.x * L.g[0].x, xa.y * L.g[0].y, xa.z * L.g[0].z, xa.w * L.g[0].w, xb.x * L.g[1].x, xb.y * L.g[1].y, xb.z * L.g[1].z, xb.w * L.g[1].w};
;         unsigned hb[8]; float lo[8];
; #pragma unroll
;         for (int j = 0; j < 8; ++j) { hb[j] = f2bf(u[j]); lo[j] = u[j] - __builtin_bit_cast(float, hb[j] << 16); }
;         const u32x4 hw = (u32x4){hb[0] | (hb[1] << 16), hb[2] | (hb[3] << 16), hb[4] | (hb[5] << 16), hb[6] | (hb[7] << 16)};
;         const u32x4 lw = (u32x4){pk2(lo[0], lo[1]), pk2(lo[2], lo[3]), pk2(lo[4], lo[5]), pk2(lo[6], lo[7])};
;         ahi[mi] = __builtin_bit_cast(bf16x8, hw); alo[mi] = __builtin_bit_cast(bf16x8, lw); }
; #pragma unroll
;     for (int n = 0; n < 5; ++n)
; #pragma unroll
;         for (int mi = 0; mi < 2; ++mi) { acc[mi][n] = __builtin_amdgcn_mfma_f32_16x16x32_bf16(ahi[mi], W.wh[n], acc[mi][n], 0, 0, 0);
;             acc[mi][n] = __builtin_amdgcn_mfma_f32_16x16x32_bf16(alo[mi], W.wh[n], acc[mi][n], 0, 0, 0);
;             acc[mi][n] = __builtin_amdgcn_mfma_f32_16x16x32_bf16(ahi[mi], W.wl[n], acc[mi][n], 0, 0, 0); }
; }
; __device__ __forceinline__ void p5_router(Frame& F) {
;     const bf16_t* H = (const bf16_t*)(F.ws + WS_HB);
;     const bf16_t* RBH = (const bf16_t*)(F.ws + WS_RB); const bf16_t* RBL = RBH + 80 * D;
;     unsigned* ctl = (unsigned*)(F.ws + WS_CTL);
;     LAS float* part = (LAS float*)F.lds;
;     LAS float* lg = part + 4 * 64 * 80;
;     LAS float* ssp = lg + 64 * 80;
;     LAS float* rs = ssp + 256;
;     const int lane = F.lane, wave = F.wave;
;     for (int tile = F.bid; tile < M / 64; tile += F.G) {
;         const int m0 = tile * 64;
.Lrt_path3:
	s_add_i32 s39, s39, 0x80
	s_and_b32 s39, s39, 0x1fff
	s_add_u32 s40, s86, s39
	s_addc_u32 s41, s87, 0
	s_add_i32 m0, s94, s98
	s_nop 0
	global_load_lds_dwordx4 v208, s[40:41]
	s_add_i32 m0, s94, s99
	s_nop 0
	global_load_lds_dwordx4 v209, s[40:41]
	s_add_i32 m0, s94, s100
	s_nop 0
	global_load_lds_dwordx4 v210, s[40:41]
	v_add_u32_e32 v214, s95, v212
	v_add_u32_e32 v215, s95, v213
	ds_read_b128 v[38:41], v215
	ds_read_b128 v[58:61], v214 offset:0
	ds_read_b128 v[62:65], v214 offset:2048
	ds_read_b128 v[66:69], v214 offset:4096
	ds_read_b128 v[70:73], v214 offset:6144
	ds_read_b128 v[74:77], v214 offset:8192
	ds_read_b128 v[100:103], v214 offset:10240
	ds_read_b128 v[104:107], v214 offset:12288
	ds_read_b128 v[108:111], v214 offset:14336
	ds_read_b128 v[112:115], v214 offset:16384
	ds_read_b128 v[116:119], v214 offset:18432
	s_waitcnt vmcnt(6)
	s_mov_b32 s33, s94
	s_mov_b32 s94, s95
	s_mov_b32 s95, s91
	s_mov_b32 s91, s25
	s_mov_b32 s25, s33
	s_waitcnt lgkmcnt(0)
	s_barrier
	s_add_i32 s39, s39, 0x80
	s_and_b32 s39, s39, 0x1fff
	s_add_u32 s40, s86, s39
	s_addc_u32 s41, s87, 0
	s_add_i32 m0, s94, s98
	s_nop 0
	global_load_lds_dwordx4 v208, s[40:41]
	s_add_i32 m0, s94, s99
	s_nop 0
	global_load_lds_dwordx4 v209, s[40:41]
	s_add_i32 m0, s94, s100
	s_nop 0
	global_load_lds_dwordx4 v210, s[40:41]
	v_add_u32_e32 v214, s95, v212
	v_add_u32_e32 v215, s95, v213
	ds_read_b128 v[226:229], v215
	ds_read_b128 v[230:233], v214 offset:0
	ds_read_b128 v[234:237], v214 offset:2048
	ds_read_b128 v[238:241], v214 offset:4096
	ds_read_b128 v[242:245], v214 offset:6144
	ds_read_b128 v[246:249], v214 offset:8192
	ds_read_b128 v[120:123], v214 offset:10240
	ds_read_b128 v[124:127], v214 offset:12288
	ds_read_b128 v[132:135], v214 offset:14336
	ds_read_b128 v[136:139], v214 offset:16384
	ds_read_b128 v[140:143], v214 offset:18432
	v_mfma_f32_16x16x32_bf16 v[18:21], v[38:41], v[58:61], v[18:21]
	v_mfma_f32_16x16x32_bf16 v[22:25], v[38:41], v[62:65], v[22:25]
	v_mfma_f32_16x16x32_bf16 v[26:29], v[38:41], v[66:69], v[26:29]
	v_mfma_f32_16x16x32_bf16 v[30:33], v[38:41], v[70:73], v[30:33]
	v_mfma_f32_16x16x32_bf16 v[34:37], v[38:41], v[74:77], v[34:37]
	v_mfma_f32_16x16x32_bf16 v[42:45], v[38:41], v[38:41], v[42:45]
	v_mfma_f32_16x16x32_bf16 v[18:21], v[38:41], v[100:103], v[18:21]
	v_mfma_f32_16x16x32_bf16 v[22:25], v[38:41], v[104:107], v[22:25]
	v_mfma_f32_16x16x32_bf16 v[26:29], v[38:41], v[108:111], v[26:29]
	v_mfma_f32_16x16x32_bf16 v[30:33], v[38:41], v[112:115], v[30:33]
	v_mfma_f32_16x16x32_bf16 v[34:37], v[38:41], v[116:119], v[34:37]
	s_waitcnt vmcnt(6)
	s_mov_b32 s33, s94
	s_mov_b32 s94, s95
	s_mov_b32 s95, s91
	s_mov_b32 s91, s25
	s_mov_b32 s25, s33
	s_waitcnt lgkmcnt(0)
	s_barrier
	s_add_i32 s39, s39, 0x80
	s_and_b32 s39, s39, 0x1fff
	s_add_u32 s40, s86, s39
	s_addc_u32 s41, s87, 0
	s_add_i32 m0, s94, s98
	s_nop 0
	global_load_lds_dwordx4 v208, s[40:41]
	s_add_i32 m0, s94, s99
	s_nop 0
	global_load_lds_dwordx4 v209, s[40:41]
	s_add_i32 m0, s94, s100
	s_nop 0
	global_load_lds_dwordx4 v210, s[40:41]
	v_add_u32_e32 v214, s95, v212
	v_add_u32_e32 v215, s95, v213
	ds_read_b128 v[38:41], v215
	ds_read_b128 v[58:61], v214 offset:0
	ds_read_b128 v[62:65], v214 offset:2048
	ds_read_b128 v[66:69], v214 offset:4096
	ds_read_b128 v[70:73], v214 offset:6144
	ds_read_b128 v[74:77], v214 offset:8192
	ds_read_b128 v[100:103], v214 offset:10240
	ds_read_b128 v[104:107], v214 offset:12288
	ds_read_b128 v[108:111], v214 offset:14336
	ds_read_b128 v[112:115], v214 offset:16384
	ds_read_b128 v[116:119], v214 offset:18432
	v_mfma_f32_16x16x32_bf16 v[18:21], v[226:229], v[230:233], v[18:21]
	v_mfma_f32_16x16x32_bf16 v[22:25], v[226:229], v[234:237], v[22:25]
	v_mfma_f32_16x16x32_bf16 v[26:29], v[226:229], v[238:241], v[26:29]
	v_mfma_f32_16x16x32_bf16 v[30:33], v[226:229], v[242:245], v[30:33]
	v_mfma_f32_16x16x32_bf16 v[34:37], v[226:229], v[246:249], v[34:37]
	v_mfma_f32_16x16x32_bf16 v[42:45], v[226:229], v[226:229], v[42:45]
	v_mfma_f32_16x16x32_bf16 v[18:21], v[226:229], v[120:123], v[18:21]
	v_mfma_f32_16x16x32_bf16 v[22:25], v[226:229], v[124:127], v[22:25]
	v_mfma_f32_16x16x32_bf16 v[26:29], v[226:229], v[132:135], v[26:29]
	v_mfma_f32_16x16x32_bf16 v[30:33], v[226:229], v[136:139], v[30:33]
	v_mfma_f32_16x16x32_bf16 v[34:37], v[226:229], v[140:143], v[34:37]
	s_waitcnt vmcnt(6)
	s_mov_b32 s33, s94
	s_mov_b32 s94, s95
	s_mov_b32 s95, s91
	s_mov_b32 s91, s25
	s_mov_b32 s25, s33
	s_waitcnt lgkmcnt(0)
	s_barrier
	s_add_i32 s39, s39, 0x80
	s_and_b32 s39, s39, 0x1fff
	s_add_u32 s40, s86, s39
	s_addc_u32 s41, s87, 0
	s_add_i32 m0, s94, s98
	s_nop 0
	global_load_lds_dwordx4 v208, s[40:41]
	s_add_i32 m0, s94, s99
	s_nop 0
	global_load_lds_dwordx4 v209, s[40:41]
	s_add_i32 m0, s94, s100
	s_nop 0
	global_load_lds_dwordx4 v210, s[40:41]
	v_add_u32_e32 v214, s95, v212
	v_add_u32_e32 v215, s95, v213
	ds_read_b128 v[226:229], v215
	ds_read_b128 v[230:233], v214 offset:0
	ds_read_b128 v[234:237], v214 offset:2048
	ds_read_b128 v[238:241], v214 offset:4096
	ds_read_b128 v[242:245], v214 offset:6144
	ds_read_b128 v[246:249], v214 offset:8192
	ds_read_b128 v[120:123], v214 offset:10240
	ds_read_b128 v[124:127], v214 offset:12288
	ds_read_b128 v[132:135], v214 offset:14336
	ds_read_b128 v[136:139], v214 offset:16384
	ds_read_b128 v[140:143], v214 offset:18432
	v_mfma_f32_16x16x32_bf16 v[18:21], v[38:41], v[58:61], v[18:21]
	v_mfma_f32_16x16x32_bf16 v[22:25], v[38:41], v[62:65], v[22:25]
	v_mfma_f32_16x16x32_bf16 v[26:29], v[38:41], v[66:69], v[26:29]
	v_mfma_f32_16x16x32_bf16 v[30:33], v[38:41], v[70:73], v[30:33]
	v_mfma_f32_16x16x32_bf16 v[34:37], v[38:41], v[74:77], v[34:37]
	v_mfma_f32_16x16x32_bf16 v[42:45], v[38:41], v[38:41], v[42:45]
	v_mfma_f32_16x16x32_bf16 v[18:21], v[38:41], v[100:103], v[18:21]
	v_mfma_f32_16x16x32_bf16 v[22:25], v[38:41], v[104:107], v[22:25]
	v_mfma_f32_16x16x32_bf16 v[26:29], v[38:41], v[108:111], v[26:29]
	v_mfma_f32_16x16x32_bf16 v[30:33], v[38:41], v[112:115], v[30:33]
	v_mfma_f32_16x16x32_bf16 v[34:37], v[38:41], v[116:119], v[34:37]
	s_waitcnt vmcnt(6)
	s_mov_b32 s33, s94
	s_mov_b32 s94, s95
	s_mov_b32 s95, s91
	s_mov_b32 s91, s25
	s_mov_b32 s25, s33
	s_waitcnt lgkmcnt(0)
	s_barrier
; __device__ __forceinline__ void rt_step(const RtLoad& L, const bf16_t* bh, const bf16_t* bl, f32x4 (&acc)[2][5], float (&ss)[2], int ko) {
;     RtW W;
; #pragma unroll
;     for (int n = 0; n < 5; ++n) { W.wh[n] = *(const bf16x8*)(bh + (size_t)n * 16 * D + ko); W.wl[n] = *(const bf16x8*)(bl + (size_t)n * 16 * D + ko); }
;     bf16x8 ahi[2], alo[2];
; #pragma unroll
;     for (int mi = 0; mi < 2; ++mi) { const u32x4 xw = L.x[mi]; const f32x4 xa = (f32x4){bflo(xw.x), bfhi(xw.x), bflo(xw.y), bfhi(xw.y)}, xb = (f32x4){bflo(xw.z), bfhi(xw.z), bflo(xw.w), bfhi(xw.w)};
;         ss[mi] += (xa.x * xa.x + xa.y * xa.y) + (xa.z * xa.z + xa.w * xa.w) + (xb.x * xb.x + xb.y * xb.y) + (xb.z * xb.z + xb.w * xb.w);
;         const float u[8] = {xa.x * L.g[0].x, xa.y * L.g[0].y, xa.z * L.g[0].z, xa.w * L.g[0].w, xb.x * L.g[1].x, xb.y * L.g[1].y, xb.z * L.g[1].z, xb.w * L.g[1].w};
;         unsigned hb[8]; float lo[8];
; #pragma unroll
;         for (int j = 0; j < 8; ++j) { hb[j] = f2bf(u[j]); lo[j] = u[j] - __builtin_bit_cast(float, hb[j] << 16); }
;         const u32x4 hw = (u32x4){hb[0] | (hb[1] << 16), hb[2] | (hb[3] << 16), hb[4] | (hb[5] << 16), hb[6] | (hb[7] << 16)};
;         const u32x4 lw = (u32x4){pk2(lo[0], lo[1]), pk2(lo[2], lo[3]), pk2(lo[4], lo[5]), pk2(lo[6], lo[7])};
;         ahi[mi] = __builtin_bit_cast(bf16x8, hw); alo[mi] = __builtin_bit_cast(bf16x8, lw); }
; #pragma unroll
;     for (int n = 0; n < 5; ++n)
; #pragma unroll
;         for (int mi = 0; mi < 2; ++mi) { acc[mi][n] = __builtin_amdgcn_mfma_f32_16x16x32_bf16(ahi[mi], W.wh[n], acc[mi][n], 0, 0, 0);
;             acc[mi][n] = __builtin_amdgcn_mfma_f32_16x16x32_bf16(alo[mi], W.wh[n], acc[mi][n], 0, 0, 0);
;             acc[mi][n] = __builtin_amdgcn_mfma_f32_16x16x32_bf16(ahi[mi], W.wl[n], acc[mi][n], 0, 0, 0); }
; }
; __device__ __forceinline__ void p5_router(Frame& F) {
;     const bf16_t* H = (const bf16_t*)(F.ws + WS_HB);
;     const bf16_t* RBH = (const bf16_t*)(F.ws + WS_RB); const bf16_t* RBL = RBH + 80 * D;
;     unsigned* ctl = (unsigned*)(F.ws + WS_CTL);
;     LAS float* part = (LAS float*)F.lds;
;     LAS float* lg = part + 4 * 64 * 80;
;     LAS float* ssp = lg + 64 * 80;
;     LAS float* rs = ssp + 256;
;     const int lane = F.lane, wave = F.wave;
;     for (int tile = F.bid; tile < M / 64; tile += F.G) {
;         const int m0 = tile * 64;
	s_add_i32 s39, s39, 0x80
	s_and_b32 s39, s39, 0x1fff
	s_add_u32 s40, s86, s39
	s_addc_u32 s41, s87, 0
	s_add_i32 m0, s94, s98
	s_nop 0
	global_load_lds_dwordx4 v208, s[40:41]
	s_add_i32 m0, s94, s99
	s_nop 0
	global_load_lds_dwordx4 v209, s[40:41]
	s_add_i32 m0, s94, s100
	s_nop 0
	global_load_lds_dwordx4 v210, s[40:41]
	v_add_u32_e32 v214, s95, v212
	v_add_u32_e32 v215, s95, v213
	ds_read_b128 v[38:41], v215
	ds_read_b128 v[58:61], v214 offset:0
	ds_read_b128 v[62:65], v214 offset:2048
	ds_read_b128 v[66:69], v214 offset:4096
	ds_read_b128 v[70:73], v214 offset:6144
	ds_read_b128 v[74:77], v214 offset:8192
	ds_read_b128 v[100:103], v214 offset:10240
	ds_read_b128 v[104:107], v214 offset:12288
	ds_read_b128 v[108:111], v214 offset:14336
	ds_read_b128 v[112:115], v214 offset:16384
	ds_read_b128 v[116:119], v214 offset:18432
	v_mfma_f32_16x16x32_bf16 v[18:21], v[226:229], v[230:233], v[18:21]
	v_mfma_f32_16x16x32_bf16 v[22:25], v[226:229], v[234:237], v[22:25]
	v_mfma_f32_16x16x32_bf16 v[26:29], v[226:229], v[238:241], v[26:29]
	v_mfma_f32_16x16x32_bf16 v[30:33], v[226:229], v[242:245], v[30:33]
	v_mfma_f32_16x16x32_bf16 v[34:37], v[226:229], v[246:249], v[34:37]
	v_mfma_f32_16x16x32_bf16 v[42:45], v[226:229], v[226:229], v[42:45]
	v_mfma_f32_16x16x32_bf16 v[18:21], v[226:229], v[120:123], v[18:21]
	v_mfma_f32_16x16x32_bf16 v[22:25], v[226:229], v[124:127], v[22:25]
	v_mfma_f32_16x16x32_bf16 v[26:29], v[226:229], v[132:135], v[26:29]
	v_mfma_f32_16x16x32_bf16 v[30:33], v[226:229], v[136:139], v[30:33]
	v_mfma_f32_16x16x32_bf16 v[34:37], v[226:229], v[140:143], v[34:37]
	s_waitcnt vmcnt(6)
	s_mov_b32 s33, s94
	s_mov_b32 s94, s95
	s_mov_b32 s95, s91
	s_mov_b32 s91, s25
	s_mov_b32 s25, s33
	s_waitcnt lgkmcnt(0)
	s_barrier
	s_mov_b32 s85, 13
.Lrt_loop_p3:
	s_add_i32 s39, s39, 0x80
	s_and_b32 s39, s39, 0x1fff
	s_add_u32 s40, s86, s39
	s_addc_u32 s41, s87, 0
	s_add_i32 m0, s94, s98
	s_nop 0
	global_load_lds_dwordx4 v208, s[40:41]
	s_add_i32 m0, s94, s99
	s_nop 0
	global_load_lds_dwordx4 v209, s[40:41]
	s_add_i32 m0, s94, s100
	s_nop 0
	global_load_lds_dwordx4 v210, s[40:41]
	v_add_u32_e32 v214, s95, v212
	v_add_u32_e32 v215, s95, v213
	ds_read_b128 v[226:229], v215
	ds_read_b128 v[230:233], v214 offset:0
	ds_read_b128 v[234:237], v214 offset:2048
	ds_read_b128 v[238:241], v214 offset:4096
	ds_read_b128 v[242:245], v214 offset:6144
	ds_read_b128 v[246:249], v214 offset:8192
	ds_read_b128 v[120:123], v214 offset:10240
	ds_read_b128 v[124:127], v214 offset:12288
	ds_read_b128 v[132:135], v214 offset:14336
	ds_read_b128 v[136:139], v214 offset:16384
	ds_read_b128 v[140:143], v214 offset:18432
	v_mfma_f32_16x16x32_bf16 v[18:21], v[38:41], v[58:61], v[18:21]
	v_mfma_f32_16x16x32_bf16 v[22:25], v[38:41], v[62:65], v[22:25]
	v_mfma_f32_16x16x32_bf16 v[26:29], v[38:41], v[66:69], v[26:29]
	v_mfma_f32_16x16x32_bf16 v[30:33], v[38:41], v[70:73], v[30:33]
	v_mfma_f32_16x16x32_bf16 v[34:37], v[38:41], v[74:77], v[34:37]
	v_mfma_f32_16x16x32_bf16 v[42:45], v[38:41], v[38:41], v[42:45]
	v_mfma_f32_16x16x32_bf16 v[18:21], v[38:41], v[100:103], v[18:21]
	v_mfma_f32_16x16x32_bf16 v[22:25], v[38:41], v[104:107], v[22:25]
	v_mfma_f32_16x16x32_bf16 v[26:29], v[38:41], v[108:111], v[26:29]
	v_mfma_f32_16x16x32_bf16 v[30:33], v[38:41], v[112:115], v[30:33]
	v_mfma_f32_16x16x32_bf16 v[34:37], v[38:41], v[116:119], v[34:37]
	s_waitcnt vmcnt(6)
	s_mov_b32 s33, s94
	s_mov_b32 s94, s95
	s_mov_b32 s95, s91
	s_mov_b32 s91, s25
	s_mov_b32 s25, s33
	s_waitcnt lgkmcnt(0)
	s_barrier
	s_add_i32 s39, s39, 0x80
	s_and_b32 s39, s39, 0x1fff
	s_add_u32 s40, s86, s39
	s_addc_u32 s41, s87, 0
	s_add_i32 m0, s94, s98
	s_nop 0
	global_load_lds_dwordx4 v208, s[40:41]
	s_add_i32 m0, s94, s99
	s_nop 0
	global_load_lds_dwordx4 v209, s[40:41]
	s_add_i32 m0, s94, s100
	s_nop 0
	global_load_lds_dwordx4 v210, s[40:41]
	v_add_u32_e32 v214, s95, v212
	v_add_u32_e32 v215, s95, v213
	ds_read_b128 v[38:41], v215
	ds_read_b128 v[58:61], v214 offset:0
	ds_read_b128 v[62:65], v214 offset:2048
	ds_read_b128 v[66:69], v214 offset:4096
	ds_read_b128 v[70:73], v214 offset:6144
	ds_read_b128 v[74:77], v214 offset:8192
	ds_read_b128 v[100:103], v214 offset:10240
	ds_read_b128 v[104:107], v214 offset:12288
	ds_read_b128 v[108:111], v214 offset:14336
	ds_read_b128 v[112:115], v214 offset:16384
	ds_read_b128 v[116:119], v214 offset:18432
	v_mfma_f32_16x16x32_bf16 v[18:21], v[226:229], v[230:233], v[18:21]
	v_mfma_f32_16x16x32_bf16 v[22:25], v[226:229], v[234:237], v[22:25]
	v_mfma_f32_16x16x32_bf16 v[26:29], v[226:229], v[238:241], v[26:29]
	v_mfma_f32_16x16x32_bf16 v[30:33], v[226:229], v[242:245], v[30:33]
	v_mfma_f32_16x16x32_bf16 v[34:37], v[226:229], v[246:249], v[34:37]
	v_mfma_f32_16x16x32_bf16 v[42:45], v[226:229], v[226:229], v[42:45]
	v_mfma_f32_16x16x32_bf16 v[18:21], v[226:229], v[120:123], v[18:21]
	v_mfma_f32_16x16x32_bf16 v[22:25], v[226:229], v[124:127], v[22:25]
	v_mfma_f32_16x16x32_bf16 v[26:29], v[226:229], v[132:135], v[26:29]
	v_mfma_f32_16x16x32_bf16 v[30:33], v[226:229], v[136:139], v[30:33]
	v_mfma_f32_16x16x32_bf16 v[34:37], v[226:229], v[140:143], v[34:37]
	s_waitcnt vmcnt(6)
	s_mov_b32 s33, s94
	s_mov_b32 s94, s95
	s_mov_b32 s95, s91
	s_mov_b32 s91, s25
	s_mov_b32 s25, s33
	s_waitcnt lgkmcnt(0)
	s_barrier
; __device__ __forceinline__ void rt_step(const RtLoad& L, const bf16_t* bh, const bf16_t* bl, f32x4 (&acc)[2][5], float (&ss)[2], int ko) {
;     RtW W;
; #pragma unroll
;     for (int n = 0; n < 5; ++n) { W.wh[n] = *(const bf16x8*)(bh + (size_t)n * 16 * D + ko); W.wl[n] = *(const bf16x8*)(bl + (size_t)n * 16 * D + ko); }
;     bf16x8 ahi[2], alo[2];
; #pragma unroll
;     for (int mi = 0; mi < 2; ++mi) { const u32x4 xw = L.x[mi]; const f32x4 xa = (f32x4){bflo(xw.x), bfhi(xw.x), bflo(xw.y), bfhi(xw.y)}, xb = (f32x4){bflo(xw.z), bfhi(xw.z), bflo(xw.w), bfhi(xw.w)};
;         ss[mi] += (xa.x * xa.x + xa.y * xa.y) + (xa.z * xa.z + xa.w * xa.w) + (xb.x * xb.x + xb.y * xb.y) + (xb.z * xb.z + xb.w * xb.w);
;         const float u[8] = {xa.x * L.g[0].x, xa.y * L.g[0].y, xa.z * L.g[0].z, xa.w * L.g[0].w, xb.x * L.g[1].x, xb.y * L.g[1].y, xb.z * L.g[1].z, xb.w * L.g[1].w};
;         unsigned hb[8]; float lo[8];
; #pragma unroll
;         for (int j = 0; j < 8; ++j) { hb[j] = f2bf(u[j]); lo[j] = u[j] - __builtin_bit_cast(float, hb[j] << 16); }
;         const u32x4 hw = (u32x4){hb[0] | (hb[1] << 16), hb[2] | (hb[3] << 16), hb[4] | (hb[5] << 16), hb[6] | (hb[7] << 16)};
;         const u32x4 lw = (u32x4){pk2(lo[0], lo[1]), pk2(lo[2], lo[3]), pk2(lo[4], lo[5]), pk2(lo[6], lo[7])};
;         ahi[mi] = __builtin_bit_cast(bf16x8, hw); alo[mi] = __builtin_bit_cast(bf16x8, lw); }
; #pragma unroll
;     for (int n = 0; n < 5; ++n)
; #pragma unroll
;         for (int mi = 0; mi < 2; ++mi) { acc[mi][n] = __builtin_amdgcn_mfma_f32_16x16x32_bf16(ahi[mi], W.wh[n], acc[mi][n], 0, 0, 0);
;             acc[mi][n] = __builtin_amdgcn_mfma_f32_16x16x32_bf16(alo[mi], W.wh[n], acc[mi][n], 0, 0, 0);
;             acc[mi][n] = __builtin_amdgcn_mfma_f32_16x16x32_bf16(ahi[mi], W.wl[n], acc[mi][n], 0, 0, 0); }
; }
; __device__ __forceinline__ void p5_router(Frame& F) {
;     const bf16_t* H = (const bf16_t*)(F.ws + WS_HB);
;     const bf16_t* RBH = (const bf16_t*)(F.ws + WS_RB); const bf16_t* RBL = RBH + 80 * D;
;     unsigned* ctl = (unsigned*)(F.ws + WS_CTL);
;     LAS float* part = (LAS float*)F.lds;
;     LAS float* lg = part + 4 * 64 * 80;
;     LAS float* ssp = lg + 64 * 80;
;     LAS float* rs = ssp + 256;
;     const int lane = F.lane, wave = F.wave;
;     for (int tile = F.bid; tile < M / 64; tile += F.G) {
;         const int m0 = tile * 64;
	s_add_i32 s39, s39, 0x80
	s_and_b32 s39, s39, 0x1fff
	s_add_u32 s40, s86, s39
	s_addc_u32 s41, s87, 0
	s_add_i32 m0, s94, s98
	s_nop 0
	global_load_lds_dwordx4 v208, s[40:41]
	s_add_i32 m0, s94, s99
	s_nop 0
	global_load_lds_dwordx4 v209, s[40:41]
	s_add_i32 m0, s94, s100
	s_nop 0
	global_load_lds_dwordx4 v210, s[40:41]
	v_add_u32_e32 v214, s95, v212
	v_add_u32_e32 v215, s95, v213
	ds_read_b128 v[226:229], v215
	ds_read_b128 v[230:233], v214 offset:0
	ds_read_b128 v[234:237], v214 offset:2048
	ds_read_b128 v[238:241], v214 offset:4096
	ds_read_b128 v[242:245], v214 offset:6144
	ds_read_b128 v[246:249], v214 offset:8192
	ds_read_b128 v[120:123], v214 offset:10240
	ds_read_b128 v[124:127], v214 offset:12288
	ds_read_b128 v[132:135], v214 offset:14336
	ds_read_b128 v[136:139], v214 offset:16384
	ds_read_b128 v[140:143], v214 offset:18432
	v_mfma_f32_16x16x32_bf16 v[18:21], v[38:41], v[58:61], v[18:21]
	v_mfma_f32_16x16x32_bf16 v[22:25], v[38:41], v[62:65], v[22:25]
	v_mfma_f32_16x16x32_bf16 v[26:29], v[38:41], v[66:69], v[26:29]
	v_mfma_f32_16x16x32_bf16 v[30:33], v[38:41], v[70:73], v[30:33]
	v_mfma_f32_16x16x32_bf16 v[34:37], v[38:41], v[74:77], v[34:37]
	v_mfma_f32_16x16x32_bf16 v[42:45], v[38:41], v[38:41], v[42:45]
	v_mfma_f32_16x16x32_bf16 v[18:21], v[38:41], v[100:103], v[18:21]
	v_mfma_f32_16x16x32_bf16 v[22:25], v[38:41], v[104:107], v[22:25]
	v_mfma_f32_16x16x32_bf16 v[26:29], v[38:41], v[108:111], v[26:29]
	v_mfma_f32_16x16x32_bf16 v[30:33], v[38:41], v[112:115], v[30:33]
	v_mfma_f32_16x16x32_bf16 v[34:37], v[38:41], v[116:119], v[34:37]
	s_waitcnt vmcnt(6)
	s_mov_b32 s33, s94
	s_mov_b32 s94, s95
	s_mov_b32 s95, s91
	s_mov_b32 s91, s25
	s_mov_b32 s25, s33
	s_waitcnt lgkmcnt(0)
	s_barrier
	s_add_i32 s39, s39, 0x80
	s_and_b32 s39, s39, 0x1fff
	s_add_u32 s40, s86, s39
	s_addc_u32 s41, s87, 0
	s_add_i32 m0, s94, s98
	s_nop 0
	global_load_lds_dwordx4 v208, s[40:41]
	s_add_i32 m0, s94, s99
	s_nop 0
	global_load_lds_dwordx4 v209, s[40:41]
	s_add_i32 m0, s94, s100
	s_nop 0
	global_load_lds_dwordx4 v210, s[40:41]
	v_add_u32_e32 v214, s95, v212
	v_add_u32_e32 v215, s95, v213
	ds_read_b128 v[38:41], v215
	ds_read_b128 v[58:61], v214 offset:0
	ds_read_b128 v[62:65], v214 offset:2048
	ds_read_b128 v[66:69], v214 offset:4096
	ds_read_b128 v[70:73], v214 offset:6144
	ds_read_b128 v[74:77], v214 offset:8192
	ds_read_b128 v[100:103], v214 offset:10240
	ds_read_b128 v[104:107], v214 offset:12288
	ds_read_b128 v[108:111], v214 offset:14336
	ds_read_b128 v[112:115], v214 offset:16384
	ds_read_b128 v[116:119], v214 offset:18432
	v_mfma_f32_16x16x32_bf16 v[18:21], v[226:229], v[230:233], v[18:21]
	v_mfma_f32_16x16x32_bf16 v[22:25], v[226:229], v[234:237], v[22:25]
	v_mfma_f32_16x16x32_bf16 v[26:29], v[226:229], v[238:241], v[26:29]
	v_mfma_f32_16x16x32_bf16 v[30:33], v[226:229], v[242:245], v[30:33]
	v_mfma_f32_16x16x32_bf16 v[34:37], v[226:229], v[246:249], v[34:37]
	v_mfma_f32_16x16x32_bf16 v[42:45], v[226:229], v[226:229], v[42:45]
	v_mfma_f32_16x16x32_bf16 v[18:21], v[226:229], v[120:123], v[18:21]
	v_mfma_f32_16x16x32_bf16 v[22:25], v[226:229], v[124:127], v[22:25]
	v_mfma_f32_16x16x32_bf16 v[26:29], v[226:229], v[132:135], v[26:29]
	v_mfma_f32_16x16x32_bf16 v[30:33], v[226:229], v[136:139], v[30:33]
	v_mfma_f32_16x16x32_bf16 v[34:37], v[226:229], v[140:143], v[34:37]
	s_waitcnt vmcnt(6)
	s_mov_b32 s33, s94
	s_mov_b32 s94, s95
	s_mov_b32 s95, s91
	s_mov_b32 s91, s25
	s_mov_b32 s25, s33
	s_waitcnt lgkmcnt(0)
	s_barrier
	s_sub_u32 s85, s85, 1
	s_cmp_lg_u32 s85, 0
	s_cbranch_scc1 .Lrt_loop_p3
	s_add_i32 s39, s39, 0x80
	s_and_b32 s39, s39, 0x1fff
	s_add_u32 s40, s86, s39
	s_addc_u32 s41, s87, 0
	s_add_i32 m0, s94, s98
	s_nop 0
	global_load_lds_dwordx4 v208, s[40:41]
	s_add_i32 m0, s94, s99
	s_nop 0
	global_load_lds_dwordx4 v209, s[40:41]
	s_add_i32 m0, s94, s100
	s_nop 0
	global_load_lds_dwordx4 v210, s[40:41]
	v_add_u32_e32 v214, s95, v212
	v_add_u32_e32 v215, s95, v213
	ds_read_b128 v[226:229], v215
	ds_read_b128 v[230:233], v214 offset:0
	ds_read_b128 v[234:237], v214 offset:2048
	ds_read_b128 v[238:241], v214 offset:4096
	ds_read_b128 v[242:245], v214 offset:6144
	ds_read_b128 v[246:249], v214 offset:8192
	ds_read_b128 v[120:123], v214 offset:10240
	ds_read_b128 v[124:127], v214 offset:12288
	ds_read_b128 v[132:135], v214 offset:14336
	ds_read_b128 v[136:139], v214 offset:16384
	ds_read_b128 v[140:143], v214 offset:18432
	v_mfma_f32_16x16x32_bf16 v[18:21], v[38:41], v[58:61], v[18:21]
	v_mfma_f32_16x16x32_bf16 v[22:25], v[38:41], v[62:65], v[22:25]
	v_mfma_f32_16x16x32_bf16 v[26:29], v[38:41], v[66:69], v[26:29]
	v_mfma_f32_16x16x32_bf16 v[30:33], v[38:41], v[70:73], v[30:33]
	v_mfma_f32_16x16x32_bf16 v[34:37], v[38:41], v[74:77], v[34:37]
	v_mfma_f32_16x16x32_bf16 v[42:45], v[38:41], v[38:41], v[42:45]
	v_mfma_f32_16x16x32_bf16 v[18:21], v[38:41], v[100:103], v[18:21]
	v_mfma_f32_16x16x32_bf16 v[22:25], v[38:41], v[104:107], v[22:25]
	v_mfma_f32_16x16x32_bf16 v[26:29], v[38:41], v[108:111], v[26:29]
	v_mfma_f32_16x16x32_bf16 v[30:33], v[38:41], v[112:115], v[30:33]
	v_mfma_f32_16x16x32_bf16 v[34:37], v[38:41], v[116:119], v[34:37]
	s_waitcnt vmcnt(6)
	s_mov_b32 s33, s94
	s_mov_b32 s94, s95
	s_mov_b32 s95, s91
	s_mov_b32 s91, s25
	s_mov_b32 s25, s33
	s_waitcnt lgkmcnt(0)
	s_barrier
; __device__ __forceinline__ void rt_step(const RtLoad& L, const bf16_t* bh, const bf16_t* bl, f32x4 (&acc)[2][5], float (&ss)[2], int ko) {
;     RtW W;
; #pragma unroll
;     for (int n = 0; n < 5; ++n) { W.wh[n] = *(const bf16x8*)(bh + (size_t)n * 16 * D + ko); W.wl[n] = *(const bf16x8*)(bl + (size_t)n * 16 * D + ko); }
;     bf16x8 ahi[2], alo[2];
; #pragma unroll
;     for (int mi = 0; mi < 2; ++mi) { const u32x4 xw = L.x[mi]; const f32x4 xa = (f32x4){bflo(xw.x), bfhi(xw.x), bflo(xw.y), bfhi(xw.y)}, xb = (f32x4){bflo(xw.z), bfhi(xw.z), bflo(xw.w), bfhi(xw.w)};
;         ss[mi] += (xa.x * xa.x + xa.y * xa.y) + (xa.z * xa.z + xa.w * xa.w) + (xb.x * xb.x + xb.y * xb.y) + (xb.z * xb.z + xb.w * xb.w);
;         const float u[8] = {xa.x * L.g[0].x, xa.y * L.g[0].y, xa.z * L.g[0].z, xa.w * L.g[0].w, xb.x * L.g[1].x, xb.y * L.g[1].y, xb.z * L.g[1].z, xb.w * L.g[1].w};
;         unsigned hb[8]; float lo[8];
; #pragma unroll
;         for (int j = 0; j < 8; ++j) { hb[j] = f2bf(u[j]); lo[j] = u[j] - __builtin_bit_cast(float, hb[j] << 16); }
;         const u32x4 hw = (u32x4){hb[0] | (hb[1] << 16), hb[2] | (hb[3] << 16), hb[4] | (hb[5] << 16), hb[6] | (hb[7] << 16)};
;         const u32x4 lw = (u32x4){pk2(lo[0], lo[1]), pk2(lo[2], lo[3]), pk2(lo[4], lo[5]), pk2(lo[6], lo[7])};
;         ahi[mi] = __builtin_bit_cast(bf16x8, hw); alo[mi] = __builtin_bit_cast(bf16x8, lw); }
; #pragma unroll
;     for (int n = 0; n < 5; ++n)
; #pragma unroll
;         for (int mi = 0; mi < 2; ++mi) { acc[mi][n] = __builtin_amdgcn_mfma_f32_16x16x32_bf16(ahi[mi], W.wh[n], acc[mi][n], 0, 0, 0);
;             acc[mi][n] = __builtin_amdgcn_mfma_f32_16x16x32_bf16(alo[mi], W.wh[n], acc[mi][n], 0, 0, 0);
;             acc[mi][n] = __builtin_amdgcn_mfma_f32_16x16x32_bf16(ahi[mi], W.wl[n], acc[mi][n], 0, 0, 0); }
; }
; __device__ __forceinline__ void p5_router(Frame& F) {
;     const bf16_t* H = (const bf16_t*)(F.ws + WS_HB);
;     const bf16_t* RBH = (const bf16_t*)(F.ws + WS_RB); const bf16_t* RBL = RBH + 80 * D;
;     unsigned* ctl = (unsigned*)(F.ws + WS_CTL);
;     LAS float* part = (LAS float*)F.lds;
;     LAS float* lg = part + 4 * 64 * 80;
;     LAS float* ssp = lg + 64 * 80;
;     LAS float* rs = ssp + 256;
;     const int lane = F.lane, wave = F.wave;
;     for (int tile = F.bid; tile < M / 64; tile += F.G) {
;         const int m0 = tile * 64;
	s_add_i32 s39, s39, 0x80
	s_and_b32 s39, s39, 0x1fff
	s_add_u32 s40, s86, s39
	s_addc_u32 s41, s87, 0
	s_add_i32 m0, s94, s98
	s_nop 0
	global_load_lds_dwordx4 v208, s[40:41]
	s_add_i32 m0, s94, s99
	s_nop 0
	global_load_lds_dwordx4 v209, s[40:41]
	s_add_i32 m0, s94, s100
	s_nop 0
	global_load_lds_dwordx4 v210, s[40:41]
	v_add_u32_e32 v214, s95, v212
	v_add_u32_e32 v215, s95, v213
	ds_read_b128 v[38:41], v215
	ds_read_b128 v[58:61], v214 offset:0
	ds_read_b128 v[62:65], v214 offset:2048
	ds_read_b128 v[66:69], v214 offset:4096
	ds_read_b128 v[70:73], v214 offset:6144
	ds_read_b128 v[74:77], v214 offset:8192
	ds_read_b128 v[100:103], v214 offset:10240
	ds_read_b128 v[104:107], v214 offset:12288
	ds_read_b128 v[108:111], v214 offset:14336
	ds_read_b128 v[112:115], v214 offset:16384
	ds_read_b128 v[116:119], v214 offset:18432
	v_mfma_f32_16x16x32_bf16 v[18:21], v[226:229], v[230:233], v[18:21]
	v_mfma_f32_16x16x32_bf16 v[22:25], v[226:229], v[234:237], v[22:25]
	v_mfma_f32_16x16x32_bf16 v[26:29], v[226:229], v[238:241], v[26:29]
	v_mfma_f32_16x16x32_bf16 v[30:33], v[226:229], v[242:245], v[30:33]
	v_mfma_f32_16x16x32_bf16 v[34:37], v[226:229], v[246:249], v[34:37]
	v_mfma_f32_16x16x32_bf16 v[42:45], v[226:229], v[226:229], v[42:45]
	v_mfma_f32_16x16x32_bf16 v[18:21], v[226:229], v[120:123], v[18:21]
	v_mfma_f32_16x16x32_bf16 v[22:25], v[226:229], v[124:127], v[22:25]
	v_mfma_f32_16x16x32_bf16 v[26:29], v[226:229], v[132:135], v[26:29]
	v_mfma_f32_16x16x32_bf16 v[30:33], v[226:229], v[136:139], v[30:33]
	v_mfma_f32_16x16x32_bf16 v[34:37], v[226:229], v[140:143], v[34:37]
	s_waitcnt vmcnt(6)
	s_mov_b32 s33, s94
	s_mov_b32 s94, s95
	s_mov_b32 s95, s91
	s_mov_b32 s91, s25
	s_mov_b32 s25, s33
	s_waitcnt lgkmcnt(0)
	s_barrier
	s_add_i32 s39, s39, 0x80
	s_and_b32 s39, s39, 0x1fff
	s_add_u32 s40, s86, s39
	s_addc_u32 s41, s87, 0
	s_add_i32 m0, s94, s98
	s_nop 0
	global_load_lds_dwordx4 v208, s[40:41]
	s_add_i32 m0, s94, s99
	s_nop 0
	global_load_lds_dwordx4 v209, s[40:41]
	s_add_i32 m0, s94, s100
	s_nop 0
	global_load_lds_dwordx4 v210, s[40:41]
	v_add_u32_e32 v214, s95, v212
	v_add_u32_e32 v215, s95, v213
	ds_read_b128 v[226:229], v215
	ds_read_b128 v[230:233], v214 offset:0
	ds_read_b128 v[234:237], v214 offset:2048
	ds_read_b128 v[238:241], v214 offset:4096
	ds_read_b128 v[242:245], v214 offset:6144
	ds_read_b128 v[246:249], v214 offset:8192
	ds_read_b128 v[120:123], v214 offset:10240
	ds_read_b128 v[124:127], v214 offset:12288
	ds_read_b128 v[132:135], v214 offset:14336
	ds_read_b128 v[136:139], v214 offset:16384
	ds_read_b128 v[140:143], v214 offset:18432
	v_mfma_f32_16x16x32_bf16 v[18:21], v[38:41], v[58:61], v[18:21]
	v_mfma_f32_16x16x32_bf16 v[22:25], v[38:41], v[62:65], v[22:25]
	v_mfma_f32_16x16x32_bf16 v[26:29], v[38:41], v[66:69], v[26:29]
	v_mfma_f32_16x16x32_bf16 v[30:33], v[38:41], v[70:73], v[30:33]
	v_mfma_f32_16x16x32_bf16 v[34:37], v[38:41], v[74:77], v[34:37]
	v_mfma_f32_16x16x32_bf16 v[42:45], v[38:41], v[38:41], v[42:45]
	v_mfma_f32_16x16x32_bf16 v[18:21], v[38:41], v[100:103], v[18:21]
	v_mfma_f32_16x16x32_bf16 v[22:25], v[38:41], v[104:107], v[22:25]
	v_mfma_f32_16x16x32_bf16 v[26:29], v[38:41], v[108:111], v[26:29]
	v_mfma_f32_16x16x32_bf16 v[30:33], v[38:41], v[112:115], v[30:33]
	v_mfma_f32_16x16x32_bf16 v[34:37], v[38:41], v[116:119], v[34:37]
	s_waitcnt vmcnt(6)
	s_mov_b32 s33, s94
	s_mov_b32 s94, s95
	s_mov_b32 s95, s91
	s_mov_b32 s91, s25
	s_mov_b32 s25, s33
	s_waitcnt lgkmcnt(0)
	s_barrier
	s_add_i32 s39, s39, 0x80
	s_and_b32 s39, s39, 0x1fff
	s_add_u32 s40, s86, s39
	s_addc_u32 s41, s87, 0
	s_add_i32 m0, s94, s98
	s_nop 0
	global_load_lds_dwordx4 v208, s[40:41]
	s_add_i32 m0, s94, s99
	s_nop 0
	global_load_lds_dwordx4 v209, s[40:41]
	s_add_i32 m0, s94, s100
	s_nop 0
	global_load_lds_dwordx4 v210, s[40:41]
	v_add_u32_e32 v214, s95, v212
	v_add_u32_e32 v215, s95, v213
	ds_read_b128 v[38:41], v215
	ds_read_b128 v[58:61], v214 offset:0
	ds_read_b128 v[62:65], v214 offset:2048
	ds_read_b128 v[66:69], v214 offset:4096
	ds_read_b128 v[70:73], v214 offset:6144
	ds_read_b128 v[74:77], v214 offset:8192
	ds_read_b128 v[100:103], v214 offset:10240
	ds_read_b128 v[104:107], v214 offset:12288
	ds_read_b128 v[108:111], v214 offset:14336
	ds_read_b128 v[112:115], v214 offset:16384
	ds_read_b128 v[116:119], v214 offset:18432
	v_mfma_f32_16x16x32_bf16 v[18:21], v[226:229], v[230:233], v[18:21]
	v_mfma_f32_16x16x32_bf16 v[22:25], v[226:229], v[234:237], v[22:25]
	v_mfma_f32_16x16x32_bf16 v[26:29], v[226:229], v[238:241], v[26:29]
	v_mfma_f32_16x16x32_bf16 v[30:33], v[226:229], v[242:245], v[30:33]
	v_mfma_f32_16x16x32_bf16 v[34:37], v[226:229], v[246:249], v[34:37]
	v_mfma_f32_16x16x32_bf16 v[42:45], v[226:229], v[226:229], v[42:45]
	v_mfma_f32_16x16x32_bf16 v[18:21], v[226:229], v[120:123], v[18:21]
	v_mfma_f32_16x16x32_bf16 v[22:25], v[226:229], v[124:127], v[22:25]
	v_mfma_f32_16x16x32_bf16 v[26:29], v[226:229], v[132:135], v[26:29]
	v_mfma_f32_16x16x32_bf16 v[30:33], v[226:229], v[136:139], v[30:33]
	v_mfma_f32_16x16x32_bf16 v[34:37], v[226:229], v[140:143], v[34:37]
	s_waitcnt vmcnt(6)
	s_mov_b32 s33, s94
	s_mov_b32 s94, s95
	s_mov_b32 s95, s91
	s_mov_b32 s91, s25
	s_mov_b32 s25, s33
	s_waitcnt lgkmcnt(0)
	s_barrier
; __device__ __forceinline__ void rt_step(const RtLoad& L, const bf16_t* bh, const bf16_t* bl, f32x4 (&acc)[2][5], float (&ss)[2], int ko) {
;     RtW W;
; #pragma unroll
;     for (int n = 0; n < 5; ++n) { W.wh[n] = *(const bf16x8*)(bh + (size_t)n * 16 * D + ko); W.wl[n] = *(const bf16x8*)(bl + (size_t)n * 16 * D + ko); }
;     bf16x8 ahi[2], alo[2];
; #pragma unroll
;     for (int mi = 0; mi < 2; ++mi) { const u32x4 xw = L.x[mi]; const f32x4 xa = (f32x4){bflo(xw.x), bfhi(xw.x), bflo(xw.y), bfhi(xw.y)}, xb = (f32x4){bflo(xw.z), bfhi(xw.z), bflo(xw.w), bfhi(xw.w)};
;         ss[mi] += (xa.x * xa.x + xa.y * xa.y) + (xa.z * xa.z + xa.w * xa.w) + (xb.x * xb.x + xb.y * xb.y) + (xb.z * xb.z + xb.w * xb.w);
;         const float u[8] = {xa.x * L.g[0].x, xa.y * L.g[0].y, xa.z * L.g[0].z, xa.w * L.g[0].w, xb.x * L.g[1].x, xb.y * L.g[1].y, xb.z * L.g[1].z, xb.w * L.g[1].w};
;         unsigned hb[8]; float lo[8];
; #pragma unroll
;         for (int j = 0; j < 8; ++j) { hb[j] = f2bf(u[j]); lo[j] = u[j] - __builtin_bit_cast(float, hb[j] << 16); }
;         const u32x4 hw = (u32x4){hb[0] | (hb[1] << 16), hb[2] | (hb[3] << 16), hb[4] | (hb[5] << 16), hb[6] | (hb[7] << 16)};
;         const u32x4 lw = (u32x4){pk2(lo[0], lo[1]), pk2(lo[2], lo[3]), pk2(lo[4], lo[5]), pk2(lo[6], lo[7])};
;         ahi[mi] = __builtin_bit_cast(bf16x8, hw); alo[mi] = __builtin_bit_cast(bf16x8, lw); }
; #pragma unroll
;     for (int n = 0; n < 5; ++n)
; #pragma unroll
;         for (int mi = 0; mi < 2; ++mi) { acc[mi][n] = __builtin_amdgcn_mfma_f32_16x16x32_bf16(ahi[mi], W.wh[n], acc[mi][n], 0, 0, 0);
;             acc[mi][n] = __builtin_amdgcn_mfma_f32_16x16x32_bf16(alo[mi], W.wh[n], acc[mi][n], 0, 0, 0);
;             acc[mi][n] = __builtin_amdgcn_mfma_f32_16x16x32_bf16(ahi[mi], W.wl[n], acc[mi][n], 0, 0, 0); }
; }
; __device__ __forceinline__ void p5_router(Frame& F) {
;     const bf16_t* H = (const bf16_t*)(F.ws + WS_HB);
;     const bf16_t* RBH = (const bf16_t*)(F.ws + WS_RB); const bf16_t* RBL = RBH + 80 * D;
;     unsigned* ctl = (unsigned*)(F.ws + WS_CTL);
;     LAS float* part = (LAS float*)F.lds;
;     LAS float* lg = part + 4 * 64 * 80;
;     LAS float* ssp = lg + 64 * 80;
;     LAS float* rs = ssp + 256;
;     const int lane = F.lane, wave = F.wave;
;     for (int tile = F.bid; tile < M / 64; tile += F.G) {
;         const int m0 = tile * 64;
	v_add_u32_e32 v214, s95, v212
	v_add_u32_e32 v215, s95, v213
	ds_read_b128 v[226:229], v215
	ds_read_b128 v[230:233], v214 offset:0
	ds_read_b128 v[234:237], v214 offset:2048
	ds_read_b128 v[238:241], v214 offset:4096
	ds_read_b128 v[242:245], v214 offset:6144
	ds_read_b128 v[246:249], v214 offset:8192
	ds_read_b128 v[120:123], v214 offset:10240
	ds_read_b128 v[124:127], v214 offset:12288
	ds_read_b128 v[132:135], v214 offset:14336
	ds_read_b128 v[136:139], v214 offset:16384
	ds_read_b128 v[140:143], v214 offset:18432
	v_mfma_f32_16x16x32_bf16 v[18:21], v[38:41], v[58:61], v[18:21]
	v_mfma_f32_16x16x32_bf16 v[22:25], v[38:41], v[62:65], v[22:25]
	v_mfma_f32_16x16x32_bf16 v[26:29], v[38:41], v[66:69], v[26:29]
	v_mfma_f32_16x16x32_bf16 v[30:33], v[38:41], v[70:73], v[30:33]
	v_mfma_f32_16x16x32_bf16 v[34:37], v[38:41], v[74:77], v[34:37]
	v_mfma_f32_16x16x32_bf16 v[42:45], v[38:41], v[38:41], v[42:45]
	v_mfma_f32_16x16x32_bf16 v[18:21], v[38:41], v[100:103], v[18:21]
	v_mfma_f32_16x16x32_bf16 v[22:25], v[38:41], v[104:107], v[22:25]
	v_mfma_f32_16x16x32_bf16 v[26:29], v[38:41], v[108:111], v[26:29]
	v_mfma_f32_16x16x32_bf16 v[30:33], v[38:41], v[112:115], v[30:33]
	v_mfma_f32_16x16x32_bf16 v[34:37], v[38:41], v[116:119], v[34:37]
	s_waitcnt vmcnt(3)
	s_mov_b32 s33, s94
	s_mov_b32 s94, s95
	s_mov_b32 s95, s91
	s_mov_b32 s91, s25
	s_mov_b32 s25, s33
	s_waitcnt lgkmcnt(0)
	s_barrier
	v_add_u32_e32 v214, s95, v212
	v_add_u32_e32 v215, s95, v213
	ds_read_b128 v[38:41], v215
	ds_read_b128 v[58:61], v214 offset:0
	ds_read_b128 v[62:65], v214 offset:2048
	ds_read_b128 v[66:69], v214 offset:4096
	ds_read_b128 v[70:73], v214 offset:6144
	ds_read_b128 v[74:77], v214 offset:8192
	ds_read_b128 v[100:103], v214 offset:10240
	ds_read_b128 v[104:107], v214 offset:12288
	ds_read_b128 v[108:111], v214 offset:14336
	ds_read_b128 v[112:115], v214 offset:16384
	ds_read_b128 v[116:119], v214 offset:18432
	v_mfma_f32_16x16x32_bf16 v[18:21], v[226:229], v[230:233], v[18:21]
	v_mfma_f32_16x16x32_bf16 v[22:25], v[226:229], v[234:237], v[22:25]
	v_mfma_f32_16x16x32_bf16 v[26:29], v[226:229], v[238:241], v[26:29]
	v_mfma_f32_16x16x32_bf16 v[30:33], v[226:229], v[242:245], v[30:33]
	v_mfma_f32_16x16x32_bf16 v[34:37], v[226:229], v[246:249], v[34:37]
	v_mfma_f32_16x16x32_bf16 v[42:45], v[226:229], v[226:229], v[42:45]
	v_mfma_f32_16x16x32_bf16 v[18:21], v[226:229], v[120:123], v[18:21]
	v_mfma_f32_16x16x32_bf16 v[22:25], v[226:229], v[124:127], v[22:25]
	v_mfma_f32_16x16x32_bf16 v[26:29], v[226:229], v[132:135], v[26:29]
	v_mfma_f32_16x16x32_bf16 v[30:33], v[226:229], v[136:139], v[30:33]
	v_mfma_f32_16x16x32_bf16 v[34:37], v[226:229], v[140:143], v[34:37]
	s_waitcnt vmcnt(0)
	s_mov_b32 s33, s94
	s_mov_b32 s94, s95
	s_mov_b32 s95, s91
	s_mov_b32 s91, s25
	s_mov_b32 s25, s33
	s_waitcnt lgkmcnt(0)
	s_barrier
	v_add_u32_e32 v214, s95, v212
	v_add_u32_e32 v215, s95, v213
	ds_read_b128 v[226:229], v215
	ds_read_b128 v[230:233], v214 offset:0
	ds_read_b128 v[234:237], v214 offset:2048
	ds_read_b128 v[238:241], v214 offset:4096
	ds_read_b128 v[242:245], v214 offset:6144
	ds_read_b128 v[246:249], v214 offset:8192
	ds_read_b128 v[120:123], v214 offset:10240
	ds_read_b128 v[124:127], v214 offset:12288
	ds_read_b128 v[132:135], v214 offset:14336
	ds_read_b128 v[136:139], v214 offset:16384
	ds_read_b128 v[140:143], v214 offset:18432
	v_mfma_f32_16x16x32_bf16 v[18:21], v[38:41], v[58:61], v[18:21]
	v_mfma_f32_16x16x32_bf16 v[22:25], v[38:41], v[62:65], v[22:25]
	v_mfma_f32_16x16x32_bf16 v[26:29], v[38:41], v[66:69], v[26:29]
	v_mfma_f32_16x16x32_bf16 v[30:33], v[38:41], v[70:73], v[30:33]
	v_mfma_f32_16x16x32_bf16 v[34:37], v[38:41], v[74:77], v[34:37]
	v_mfma_f32_16x16x32_bf16 v[42:45], v[38:41], v[38:41], v[42:45]
	v_mfma_f32_16x16x32_bf16 v[18:21], v[38:41], v[100:103], v[18:21]
	v_mfma_f32_16x16x32_bf16 v[22:25], v[38:41], v[104:107], v[22:25]
	v_mfma_f32_16x16x32_bf16 v[26:29], v[38:41], v[108:111], v[26:29]
	v_mfma_f32_16x16x32_bf16 v[30:33], v[38:41], v[112:115], v[30:33]
	v_mfma_f32_16x16x32_bf16 v[34:37], v[38:41], v[116:119], v[34:37]
	s_mov_b32 s33, s94
	s_mov_b32 s94, s95
	s_mov_b32 s95, s91
	s_mov_b32 s91, s25
	s_mov_b32 s25, s33
	s_waitcnt lgkmcnt(0)
	s_barrier
	v_mfma_f32_16x16x32_bf16 v[18:21], v[226:229], v[230:233], v[18:21]
	v_mfma_f32_16x16x32_bf16 v[22:25], v[226:229], v[234:237], v[22:25]
	v_mfma_f32_16x16x32_bf16 v[26:29], v[226:229], v[238:241], v[26:29]
	v_mfma_f32_16x16x32_bf16 v[30:33], v[226:229], v[242:245], v[30:33]
	v_mfma_f32_16x16x32_bf16 v[34:37], v[226:229], v[246:249], v[34:37]
	v_mfma_f32_16x16x32_bf16 v[42:45], v[226:229], v[226:229], v[42:45]
	v_mfma_f32_16x16x32_bf16 v[18:21], v[226:229], v[120:123], v[18:21]
	v_mfma_f32_16x16x32_bf16 v[22:25], v[226:229], v[124:127], v[22:25]
	v_mfma_f32_16x16x32_bf16 v[26:29], v[226:229], v[132:135], v[26:29]
	v_mfma_f32_16x16x32_bf16 v[30:33], v[226:229], v[136:139], v[30:33]
	v_mfma_f32_16x16x32_bf16 v[34:37], v[226:229], v[140:143], v[34:37]

;     __device__ __forceinline__ unsigned row(const Unit& u, int r) const { return (unsigned)slot_tok[u.pm * 256 + r]; }
; template <int MODE>
; __device__ __forceinline__ void moe_unit(PG8_LAS unsigned char* lds, int e, int cb, int slot0  , int nv  , const bf16_t* A, const int* slot_tok,
;                                          const float* W0, const float* W1, bf16_t* OUT, const float* slot_rs  , const int* slot_dst) {
;     ...
;     const int tid = threadIdx.x, wid = __builtin_amdgcn_readfirstlane(tid >> 6), lane = tid & 63, wr = wid >> 1, wc = wid & 1, fr = lane & 15, fq = lane >> 4;
;     unsigned aoff[NMU];
; #pragma unroll
;     for (int i = 0; i < NMU; ++i) { const int R = 8 * (wid + 8 * i) + (lane >> 3), C = 8 * ((lane & 7) ^ ((R >> 1) & 7)); const int w4 = R / RWU, r = 4 * (R - RWU * w4) + w4;
;         const unsigned row = r < nv ? (MODE == 0 ? (unsigned)slot_tok[slot0 + r] : (unsigned)(slot0 + r)) : (MODE == 0 ? 0u : (unsigned)slot0); aoff[i] = (row * (unsigned)K + (unsigned)C) * 2u; }
;     const int jj0 = 2 * (lane & 31), typ = lane >> 5;
;     const int R0 = MODE == 0 ? 64 * (jj0 >> 5) + 32 * typ + 16 * ((jj0 >> 2) & 1) + 4 * ((jj0 >> 3) & 3) + (jj0 & 3) : 2 * lane;
;     const char* Bb = MODE == 0 ? (const char*)((typ ? W1 : W0) + (size_t)e * K * LDB + 64 * cb + jj0) + (size_t)(8 * wid) * RB
;                                : (const char*)(W0 + (size_t)e * K * LDB + 128 * cb + 2 * lane) + (size_t)(8 * wid) * RB;
;     const unsigned bw0 = (unsigned)(R0 * 128 + ((wid ^ ((R0 >> 1) & 7)) * 16)), bw1 = bw0 + 128u;
;     const int nvw = (nv - wr + 3) >> 2, mcnt = nvw <= 0 ? 0 : (((nvw + 15) >> 4) > NMU ? NMU : ((nvw + 15) >> 4));
;     ...
;     f32x4 acc[NMU][4];
; #pragma unroll
;     for (int m = 0; m < NMU; ++m)
; #pragma unroll
;         for (int n = 0; n < 4; ++n) acc[m][n] = (f32x4){0.f, 0.f, 0.f, 0.f};
;     f32x2 s0[8], s1[8];
;     float g0[8];
;     MU_GLDS_A(0, 0); MU_B_ISSUE(s0, 0); MU_G_LOAD(g0, 0); MU_B_ISSUE(s1, 1);
;     MU_B_WAIT(s0, 8); MU_B_WRITE(s0, 0, g0); __builtin_amdgcn_sched_barrier(0); MU_B_ISSUE(s0, 2);
;     asm volatile("s_waitcnt vmcnt(16)" ::: "memory");
;     asm volatile("s_waitcnt lgkmcnt(0)" ::: "memory"); __builtin_amdgcn_s_barrier(); asm volatile("" ::: "memory");
.LBB0_699:
	s_or_b64 exec, exec, s[56:57]
	s_waitcnt vmcnt(0)
	v_lshlrev_b32_e32 v5, 13, v5
	v_lshlrev_b32_e32 v6, 13, v6
	v_lshlrev_b32_e32 v4, 13, v4
	v_lshlrev_b32_e32 v8, 13, v8
	v_lshlrev_b32_e32 v7, 13, v7
	s_lshr_b32 s33, s58, 7
	s_bfe_u32 s70, s58, 0x10006
	v_add_u32_e32 v166, s33, v176
	v_add_u32_e32 v166, v166, v94
	v_ashrrev_i32_e32 v167, 31, v166
	v_lshl_add_u64 v[166:167], v[166:167], 2, v[96:97]
	v_lshl_add_u64 v[166:167], v[166:167], 0, s[10:11]
	global_load_dword v178, v[166:167], off
	global_load_dword v179, v[166:167], off offset:256
	global_load_dword v180, v[166:167], off offset:512
	global_load_dword v181, v[166:167], off offset:768
	global_load_dword v182, v[166:167], off offset:1024
	v_bfe_u32 v166, v131, 1, 3
	v_xor_b32_e32 v166, v171, v166
	v_lshlrev_b32_e32 v166, 4, v166
	v_lshl_add_u32 v166, v170, 7, v166
	s_mul_i32 s56, s33, 0x2800
	v_add_u32_e32 v135, s56, v166
	v_xor_b32_e32 v137, 64, v135
	s_lshl_b32 s56, s70, 13
	s_add_i32 s56, s56, 0x1e000
	v_add_u32_e32 v139, s56, v166
	v_xor_b32_e32 v141, 64, v139
	v_xor_b32_e32 v1, s62, v177
	v_lshl_add_u32 v1, v1, 4, v172
	v_add_u32_e32 v1, 0x1e000, v1
	s_lshl_b32 s56, s62, 2
	v_add_u32_e32 v166, s56, v171
	v_xor_b32_e32 v166, v166, v131
	v_and_b32_e32 v166, 7, v166
	v_lshlrev_b32_e32 v166, 4, v166
	v_or_b32_e32 v86, v5, v166
	v_or_b32_e32 v134, v6, v166
	v_or_b32_e32 v136, v4, v166
	v_or_b32_e32 v138, v8, v166
	v_or_b32_e32 v140, v7, v166
	s_lshl_b64 s[56:57], s[54:55], 23
	s_lshl_b32 s59, s60, 8
	s_add_u32 s56, s56, s59
	s_addc_u32 s57, s57, 0
	s_lshl_b32 s59, s62, 14
	s_add_u32 s56, s56, s59
	s_addc_u32 s57, s57, 0
	v_mov_b32_e32 v91, 0
	v_lshl_add_u64 v[132:133], v[82:83], 0, s[56:57]
	v_lshl_add_u64 v[132:133], v[132:133], 0, v[90:91]
	s_lshl_b32 s54, s60, 6
	s_ashr_i32 s55, s54, 31
	v_readlane_b32 s28, v254, 9
	v_readlane_b32 s29, v254, 10
	s_lshl_b32 s56, s62, 5
	s_mov_b64 s[30:31], s[4:5]
	s_mov_b64 s[34:35], 0x1000
	s_mov_b64 s[36:37], 0x2000
	s_mov_b64 s[38:39], 0x3000
	s_mov_b64 s[40:41], 0x20000
	s_add_u32 s28, s28, s56
	s_addc_u32 s29, s29, 0
	s_mov_b32 s42, 0
	s_mov_b32 s43, 0xa000
	s_mov_b32 s44, 0x14000
	s_lshl_b32 s6, s62, 10
	s_load_dwordx8 s[12:19], s[28:29], 0x0
	s_load_dwordx8 s[20:27], s[28:29], 0x100
	s_add_u32 s28, s28, 0x200
	s_addc_u32 s29, s29, 0
	s_add_i32 m0, s6, 0x0
	s_nop 0
	global_load_lds_dwordx4 v86, s[30:31]
	s_add_i32 m0, s6, 0x2000
	s_nop 0
	global_load_lds_dwordx4 v134, s[30:31]
	s_add_i32 m0, s6, 0x4000
	s_nop 0
	global_load_lds_dwordx4 v136, s[30:31]
	s_add_i32 m0, s6, 0x6000
	s_nop 0
	global_load_lds_dwordx4 v138, s[30:31]
	s_add_i32 m0, s6, 0x8000
	s_nop 0
	global_load_lds_dwordx4 v140, s[30:31]
	s_add_u32 s30, s30, 0x80
	s_addc_u32 s31, s31, 0
	s_add_i32 m0, s6, 0xa000
	s_nop 0
	global_load_lds_dwordx4 v86, s[30:31]
	s_add_i32 m0, s6, 0xc000
	s_nop 0
	global_load_lds_dwordx4 v134, s[30:31]
	s_add_i32 m0, s6, 0xe000
	s_nop 0
	global_load_lds_dwordx4 v136, s[30:31]
	s_add_i32 m0, s6, 0x10000
	s_nop 0
	global_load_lds_dwordx4 v138, s[30:31]
	s_add_i32 m0, s6, 0x12000
	s_nop 0
	global_load_lds_dwordx4 v140, s[30:31]
	global_load_dwordx2 v[98:99], v[132:133], off
	global_load_dwordx2 v[100:101], v[132:133], off offset:2048
	v_lshl_add_u64 v[166:167], v[132:133], 0, s[34:35]
	global_load_dwordx2 v[102:103], v[166:167], off
	global_load_dwordx2 v[104:105], v[166:167], off offset:2048
	v_lshl_add_u64 v[166:167], v[132:133], 0, s[36:37]
	global_load_dwordx2 v[106:107], v[166:167], off
	global_load_dwordx2 v[108:109], v[166:167], off offset:2048
	v_lshl_add_u64 v[166:167], v[132:133], 0, s[38:39]
	global_load_dwordx2 v[110:111], v[166:167], off
	global_load_dwordx2 v[112:113], v[166:167], off offset:2048
	v_lshl_add_u64 v[132:133], v[132:133], 0, s[40:41]
	global_load_dwordx2 v[114:115], v[132:133], off
	global_load_dwordx2 v[116:117], v[132:133], off offset:2048
	v_lshl_add_u64 v[166:167], v[132:133], 0, s[34:35]
	global_load_dwordx2 v[118:119], v[166:167], off
	global_load_dwordx2 v[120:121], v[166:167], off offset:2048
	v_lshl_add_u64 v[166:167], v[132:133], 0, s[36:37]
	global_load_dwordx2 v[122:123], v[166:167], off
	global_load_dwordx2 v[124:125], v[166:167], off offset:2048
	v_lshl_add_u64 v[166:167], v[132:133], 0, s[38:39]
	global_load_dwordx2 v[126:127], v[166:167], off
	global_load_dwordx2 v[128:129], v[166:167], off offset:2048
	v_lshl_add_u64 v[132:133], v[132:133], 0, s[40:41]
	global_load_dwordx2 v[186:187], v[132:133], off
	global_load_dwordx2 v[188:189], v[132:133], off offset:2048
	v_lshl_add_u64 v[166:167], v[132:133], 0, s[34:35]
	global_load_dwordx2 v[190:191], v[166:167], off
	global_load_dwordx2 v[192:193], v[166:167], off offset:2048
	v_lshl_add_u64 v[166:167], v[132:133], 0, s[36:37]
	global_load_dwordx2 v[194:195], v[166:167], off
	global_load_dwordx2 v[196:197], v[166:167], off offset:2048
	v_lshl_add_u64 v[166:167], v[132:133], 0, s[38:39]
	global_load_dwordx2 v[198:199], v[166:167], off
	global_load_dwordx2 v[200:201], v[166:167], off offset:2048
	v_lshl_add_u64 v[132:133], v[132:133], 0, s[40:41]
	global_load_dwordx2 v[202:203], v[132:133], off
	global_load_dwordx2 v[204:205], v[132:133], off offset:2048
	v_lshl_add_u64 v[166:167], v[132:133], 0, s[34:35]
	global_load_dwordx2 v[206:207], v[166:167], off
	global_load_dwordx2 v[208:209], v[166:167], off offset:2048
	v_lshl_add_u64 v[166:167], v[132:133], 0, s[36:37]
	global_load_dwordx2 v[210:211], v[166:167], off
	global_load_dwordx2 v[212:213], v[166:167], off offset:2048
	v_lshl_add_u64 v[166:167], v[132:133], 0, s[38:39]
	global_load_dwordx2 v[214:215], v[166:167], off
	global_load_dwordx2 v[216:217], v[166:167], off offset:2048
	v_mov_b32_e32 v78, 0
; #define MU_GLDS_A(buf, kt) do { _Pragma("unroll") for (int i = 0; i < NMU; ++i) \
;         __builtin_amdgcn_global_load_lds((const unsigned*)((const char*)A + aoff[i] + (size_t)(kt) * 128), (PG8_LAS unsigned*)(MU_SA(buf) + wid * 1024 + i * 8192), 16, 0, 0); } while (0)
; #define MU_B_ISSUE(sb, kt) do { const char* kb_ = Bb + (size_t)(kt) * (64 * (size_t)RB); _Pragma("unroll") for (int j = 0; j < 8; ++j) { const char* p_ = kb_ + (size_t)j * RB; \
;         asm volatile("global_load_dwordx2 %0, %1, off" : "=&v"(sb[j]) : "v"(p_) : "memory"); } } while (0)
; #define MU_B_WAIT(sb, N) asm volatile("s_waitcnt vmcnt(%8)" : "+v"(sb[0]), "+v"(sb[1]), "+v"(sb[2]), "+v"(sb[3]), "+v"(sb[4]), "+v"(sb[5]), "+v"(sb[6]), "+v"(sb[7]) : "n"(N) : "memory")
; #define MU_COMPUTE(buf) MU_COMPUTE_N(buf, NMU)
; template <int MODE>
; __device__ __forceinline__ void moe_unit(PG8_LAS unsigned char* lds, int e, int cb, int slot0  , int nv  , const bf16_t* A, const int* slot_tok,
;                                          const float* W0, const float* W1, bf16_t* OUT, const float* slot_rs  , const int* slot_dst) {
;     ...
;     f32x4 acc[NMU][4];
; #pragma unroll
;     for (int m = 0; m < NMU; ++m)
; #pragma unroll
;         for (int n = 0; n < 4; ++n) acc[m][n] = (f32x4){0.f, 0.f, 0.f, 0.f};
;     f32x2 s0[8], s1[8];
;     float g0[8];
;     MU_GLDS_A(0, 0); MU_B_ISSUE(s0, 0); MU_G_LOAD(g0, 0); MU_B_ISSUE(s1, 1);
;     MU_B_WAIT(s0, 8); MU_B_WRITE(s0, 0, g0); __builtin_amdgcn_sched_barrier(0); MU_B_ISSUE(s0, 2);
;     asm volatile("s_waitcnt vmcnt(16)" ::: "memory");
;     asm volatile("s_waitcnt lgkmcnt(0)" ::: "memory"); __builtin_amdgcn_s_barrier(); asm volatile("" ::: "memory");
; #pragma unroll 1
;     for (int t = 0; t < nt; t += 2) {
;         if (t + 2 < nt) MU_B_WAIT(s1, 8); else MU_B_WAIT(s1, 0);
;         MU_G_LOAD(g0, t + 1); MU_B_WRITE(s1, 1, g0); __builtin_amdgcn_sched_barrier(0); MU_GLDS_A(1, t + 1); __builtin_amdgcn_sched_barrier(0);
;         if (t + 3 < nt) { MU_B_ISSUE(s1, t + 3); }
;         MU_COMPUTE(0);
;         MU_END(t + 3 >= nt);
;         if (t + 2 < nt) { MU_B_WAIT(s0, 8); MU_G_LOAD(g0, t + 2); MU_B_WRITE(s0, 0, g0); __builtin_amdgcn_sched_barrier(0); MU_GLDS_A(0, t + 2); __builtin_amdgcn_sched_barrier(0); }
	v_mov_b32_e32 v79, 0
	v_mov_b32_e32 v80, 0
	v_mov_b32_e32 v81, 0
	v_mov_b32_e32 v74, 0
	v_mov_b32_e32 v75, 0
	v_mov_b32_e32 v76, 0
	v_mov_b32_e32 v77, 0
	v_mov_b32_e32 v70, 0
	v_mov_b32_e32 v71, 0
	v_mov_b32_e32 v72, 0
	v_mov_b32_e32 v73, 0
	v_mov_b32_e32 v66, 0
	v_mov_b32_e32 v67, 0
	v_mov_b32_e32 v68, 0
	v_mov_b32_e32 v69, 0
	v_mov_b32_e32 v62, 0
	v_mov_b32_e32 v63, 0
	v_mov_b32_e32 v64, 0
	v_mov_b32_e32 v65, 0
	v_mov_b32_e32 v58, 0
	v_mov_b32_e32 v59, 0
	v_mov_b32_e32 v60, 0
	v_mov_b32_e32 v61, 0
	v_mov_b32_e32 v54, 0
	v_mov_b32_e32 v55, 0
	v_mov_b32_e32 v56, 0
	v_mov_b32_e32 v57, 0
	v_mov_b32_e32 v50, 0
	v_mov_b32_e32 v51, 0
	v_mov_b32_e32 v52, 0
	v_mov_b32_e32 v53, 0
	v_mov_b32_e32 v46, 0
	v_mov_b32_e32 v47, 0
	v_mov_b32_e32 v48, 0
	v_mov_b32_e32 v49, 0
	v_mov_b32_e32 v42, 0
	v_mov_b32_e32 v43, 0
	v_mov_b32_e32 v44, 0
	v_mov_b32_e32 v45, 0
	v_mov_b32_e32 v38, 0
	v_mov_b32_e32 v39, 0
	v_mov_b32_e32 v40, 0
	v_mov_b32_e32 v41, 0
	v_mov_b32_e32 v34, 0
	v_mov_b32_e32 v35, 0
	v_mov_b32_e32 v36, 0
	v_mov_b32_e32 v37, 0
	v_mov_b32_e32 v18, 0
	v_mov_b32_e32 v19, 0
	v_mov_b32_e32 v20, 0
	v_mov_b32_e32 v21, 0
	v_mov_b32_e32 v22, 0
	v_mov_b32_e32 v23, 0
	v_mov_b32_e32 v24, 0
	v_mov_b32_e32 v25, 0
	v_mov_b32_e32 v26, 0
	v_mov_b32_e32 v27, 0
	v_mov_b32_e32 v28, 0
	v_mov_b32_e32 v29, 0
	v_mov_b32_e32 v30, 0
	v_mov_b32_e32 v31, 0
	v_mov_b32_e32 v32, 0
	v_mov_b32_e32 v33, 0
	v_mov_b32_e32 v2, 0
	v_mov_b32_e32 v3, 0
	v_mov_b32_e32 v4, 0
	v_mov_b32_e32 v5, 0
	v_mov_b32_e32 v6, 0
	v_mov_b32_e32 v7, 0
	v_mov_b32_e32 v8, 0
	v_mov_b32_e32 v9, 0
	v_mov_b32_e32 v10, 0
	v_mov_b32_e32 v11, 0
	v_mov_b32_e32 v12, 0
	v_mov_b32_e32 v13, 0
	v_mov_b32_e32 v14, 0
	v_mov_b32_e32 v15, 0
	v_mov_b32_e32 v16, 0
	v_mov_b32_e32 v17, 0
	s_waitcnt vmcnt(24)
	s_waitcnt lgkmcnt(0)
	v_mul_f32_e32 v98, s12, v98
	v_mul_f32_e32 v99, s12, v99
	v_mul_f32_e32 v100, s13, v100
	v_mul_f32_e32 v101, s13, v101
	v_mul_f32_e32 v102, s14, v102
	v_mul_f32_e32 v103, s14, v103
	v_mul_f32_e32 v104, s15, v104
	v_mul_f32_e32 v105, s15, v105
	v_mul_f32_e32 v106, s16, v106
	v_mul_f32_e32 v107, s16, v107
	v_mul_f32_e32 v108, s17, v108
	v_mul_f32_e32 v109, s17, v109
	v_mul_f32_e32 v110, s18, v110
	v_mul_f32_e32 v111, s18, v111
	v_mul_f32_e32 v112, s19, v112
	v_mul_f32_e32 v113, s19, v113
	v_cvt_pk_bf16_f32 v158, v98, v100
	v_cvt_pk_bf16_f32 v159, v102, v104
	v_cvt_pk_bf16_f32 v160, v106, v108
	v_cvt_pk_bf16_f32 v161, v110, v112
	v_cvt_pk_bf16_f32 v162, v99, v101
	v_cvt_pk_bf16_f32 v163, v103, v105
	v_cvt_pk_bf16_f32 v164, v107, v109
	v_cvt_pk_bf16_f32 v165, v111, v113
	ds_write_b128 v1, v[158:161] offset:0
	ds_write_b128 v1, v[162:165] offset:128
	v_lshl_add_u64 v[132:133], v[132:133], 0, s[40:41]
	global_load_dwordx2 v[98:99], v[132:133], off
	global_load_dwordx2 v[100:101], v[132:133], off offset:2048
	v_lshl_add_u64 v[166:167], v[132:133], 0, s[34:35]
	global_load_dwordx2 v[102:103], v[166:167], off
	global_load_dwordx2 v[104:105], v[166:167], off offset:2048
	v_lshl_add_u64 v[166:167], v[132:133], 0, s[36:37]
	global_load_dwordx2 v[106:107], v[166:167], off
	global_load_dwordx2 v[108:109], v[166:167], off offset:2048
	v_lshl_add_u64 v[166:167], v[132:133], 0, s[38:39]
	global_load_dwordx2 v[110:111], v[166:167], off
	global_load_dwordx2 v[112:113], v[166:167], off offset:2048
	s_waitcnt lgkmcnt(0)
	s_barrier
	s_sub_i32 s56, s69, s33
	s_add_i32 s56, s56, 3
	s_ashr_i32 s56, s56, 2
	s_cmp_gt_i32 s56, 64
	s_cbranch_scc1 .Lmu_frag5
	s_cmp_gt_u32 s62, 3
	s_cbranch_scc1 .Lmu_grpY4
	s_waitcnt vmcnt(24)
	v_mul_f32_e32 v114, s20, v114
	v_mul_f32_e32 v115, s20, v115
	v_mul_f32_e32 v116, s21, v116
	v_mul_f32_e32 v117, s21, v117
	v_mul_f32_e32 v118, s22, v118
	v_mul_f32_e32 v119, s22, v119
	v_mul_f32_e32 v120, s23, v120
	v_mul_f32_e32 v121, s23, v121
	v_mul_f32_e32 v122, s24, v122
	v_mul_f32_e32 v123, s24, v123
	v_mul_f32_e32 v124, s25, v124
	v_mul_f32_e32 v125, s25, v125
	v_mul_f32_e32 v126, s26, v126
	v_mul_f32_e32 v127, s26, v127
	v_mul_f32_e32 v128, s27, v128
	v_mul_f32_e32 v129, s27, v129
	v_cvt_pk_bf16_f32 v158, v114, v116
	v_cvt_pk_bf16_f32 v159, v118, v120
	v_cvt_pk_bf16_f32 v160, v122, v124
	v_cvt_pk_bf16_f32 v161, v126, v128
	v_cvt_pk_bf16_f32 v162, v115, v117
	v_cvt_pk_bf16_f32 v163, v119, v121
	v_cvt_pk_bf16_f32 v164, v123, v125
	v_cvt_pk_bf16_f32 v165, v127, v129
	ds_write_b128 v1, v[158:161] offset:19456
	ds_write_b128 v1, v[162:165] offset:19584
	v_add_u32_e32 v91, s42, v135
	v_add_u32_e32 v93, s42, v137
	ds_read_b128 v[238:241], v139 offset:0
	ds_read_b128 v[242:245], v139 offset:2048
	ds_read_b128 v[246:249], v139 offset:4096
	ds_read_b128 v[250:253], v139 offset:6144
	ds_read_b128 v[218:221], v91 offset:0
	ds_read_b128 v[222:225], v91 offset:2048
	ds_read_b128 v[226:229], v91 offset:4096
	ds_read_b128 v[230:233], v91 offset:6144
	s_add_i32 s47, s44, s6
	s_add_u32 s30, s30, 0x80
	s_addc_u32 s31, s31, 0
	s_waitcnt lgkmcnt(0)
; #define MU_GLDS_A(buf, kt) do { _Pragma("unroll") for (int i = 0; i < NMU; ++i) \
;         __builtin_amdgcn_global_load_lds((const unsigned*)((const char*)A + aoff[i] + (size_t)(kt) * 128), (PG8_LAS unsigned*)(MU_SA(buf) + wid * 1024 + i * 8192), 16, 0, 0); } while (0)
; #define MU_B_ISSUE(sb, kt) do { const char* kb_ = Bb + (size_t)(kt) * (64 * (size_t)RB); _Pragma("unroll") for (int j = 0; j < 8; ++j) { const char* p_ = kb_ + (size_t)j * RB; \
;         asm volatile("global_load_dwordx2 %0, %1, off" : "=&v"(sb[j]) : "v"(p_) : "memory"); } } while (0)
; #define MU_B_WAIT(sb, N) asm volatile("s_waitcnt vmcnt(%8)" : "+v"(sb[0]), "+v"(sb[1]), "+v"(sb[2]), "+v"(sb[3]), "+v"(sb[4]), "+v"(sb[5]), "+v"(sb[6]), "+v"(sb[7]) : "n"(N) : "memory")
; #define MU_COMPUTE(buf) MU_COMPUTE_N(buf, NMU)
; template <int MODE>
; __device__ __forceinline__ void moe_unit(PG8_LAS unsigned char* lds, int e, int cb, int slot0  , int nv  , const bf16_t* A, const int* slot_tok,
;                                          const float* W0, const float* W1, bf16_t* OUT, const float* slot_rs  , const int* slot_dst) {
;     ...
;     f32x4 acc[NMU][4];
; #pragma unroll
;     for (int m = 0; m < NMU; ++m)
; #pragma unroll
;         for (int n = 0; n < 4; ++n) acc[m][n] = (f32x4){0.f, 0.f, 0.f, 0.f};
;     f32x2 s0[8], s1[8];
;     float g0[8];
;     MU_GLDS_A(0, 0); MU_B_ISSUE(s0, 0); MU_G_LOAD(g0, 0); MU_B_ISSUE(s1, 1);
;     MU_B_WAIT(s0, 8); MU_B_WRITE(s0, 0, g0); __builtin_amdgcn_sched_barrier(0); MU_B_ISSUE(s0, 2);
;     asm volatile("s_waitcnt vmcnt(16)" ::: "memory");
;     asm volatile("s_waitcnt lgkmcnt(0)" ::: "memory"); __builtin_amdgcn_s_barrier(); asm volatile("" ::: "memory");
; #pragma unroll 1
;     for (int t = 0; t < nt; t += 2) {
;         if (t + 2 < nt) MU_B_WAIT(s1, 8); else MU_B_WAIT(s1, 0);
;         MU_G_LOAD(g0, t + 1); MU_B_WRITE(s1, 1, g0); __builtin_amdgcn_sched_barrier(0); MU_GLDS_A(1, t + 1); __builtin_amdgcn_sched_barrier(0);
;         if (t + 3 < nt) { MU_B_ISSUE(s1, t + 3); }
;         MU_COMPUTE(0);
;         MU_END(t + 3 >= nt);
;         if (t + 2 < nt) { MU_B_WAIT(s0, 8); MU_G_LOAD(g0, t + 2); MU_B_WRITE(s0, 0, g0); __builtin_amdgcn_sched_barrier(0); MU_GLDS_A(0, t + 2); __builtin_amdgcn_sched_barrier(0); }
;         if (t + 4 < nt) { MU_B_ISSUE(s0, t + 4); }
;         MU_COMPUTE(1);
;         MU_END(t + 4 >= nt);
	v_mfma_f32_16x16x32_bf16 v[78:81], v[238:241], v[218:221], v[78:81]
	v_mfma_f32_16x16x32_bf16 v[74:77], v[242:245], v[218:221], v[74:77]
	v_mfma_f32_16x16x32_bf16 v[70:73], v[246:249], v[218:221], v[70:73]
	v_mfma_f32_16x16x32_bf16 v[66:69], v[250:253], v[218:221], v[66:69]
	ds_read_b128 v[218:221], v93 offset:0
	ds_read_b128 v[142:145], v141 offset:0
	s_mov_b32 m0, s47
	s_nop 0
	global_load_lds_dwordx4 v86, s[30:31]
	v_mfma_f32_16x16x32_bf16 v[62:65], v[238:241], v[222:225], v[62:65]
	v_mfma_f32_16x16x32_bf16 v[58:61], v[242:245], v[222:225], v[58:61]
	v_mfma_f32_16x16x32_bf16 v[54:57], v[246:249], v[222:225], v[54:57]
	v_mfma_f32_16x16x32_bf16 v[50:53], v[250:253], v[222:225], v[50:53]
	ds_read_b128 v[222:225], v93 offset:2048
	ds_read_b128 v[146:149], v141 offset:2048
	s_add_i32 m0, s47, 0x2000
	s_nop 0
	global_load_lds_dwordx4 v134, s[30:31]
	v_mfma_f32_16x16x32_bf16 v[46:49], v[238:241], v[226:229], v[46:49]
	v_mfma_f32_16x16x32_bf16 v[42:45], v[242:245], v[226:229], v[42:45]
	v_mfma_f32_16x16x32_bf16 v[38:41], v[246:249], v[226:229], v[38:41]
	v_mfma_f32_16x16x32_bf16 v[34:37], v[250:253], v[226:229], v[34:37]
	ds_read_b128 v[226:229], v93 offset:4096
	ds_read_b128 v[150:153], v141 offset:4096
	s_add_i32 m0, s47, 0x4000
	s_nop 0
	global_load_lds_dwordx4 v136, s[30:31]
	v_mfma_f32_16x16x32_bf16 v[18:21], v[238:241], v[230:233], v[18:21]
	v_mfma_f32_16x16x32_bf16 v[22:25], v[242:245], v[230:233], v[22:25]
	v_mfma_f32_16x16x32_bf16 v[26:29], v[246:249], v[230:233], v[26:29]
	v_mfma_f32_16x16x32_bf16 v[30:33], v[250:253], v[230:233], v[30:33]
	ds_read_b128 v[230:233], v93 offset:6144
	ds_read_b128 v[154:157], v141 offset:6144
	s_add_i32 m0, s47, 0x6000
	s_nop 0
	global_load_lds_dwordx4 v138, s[30:31]
	s_add_i32 m0, s47, 0x8000
	s_nop 0
	global_load_lds_dwordx4 v140, s[30:31]
	s_waitcnt lgkmcnt(0)
	s_load_dwordx8 s[12:19], s[28:29], 0x0
	s_add_u32 s28, s28, 0x100
	s_addc_u32 s29, s29, 0
	v_mfma_f32_16x16x32_bf16 v[78:81], v[142:145], v[218:221], v[78:81]
	v_mfma_f32_16x16x32_bf16 v[74:77], v[146:149], v[218:221], v[74:77]
	v_mfma_f32_16x16x32_bf16 v[70:73], v[150:153], v[218:221], v[70:73]
	v_mfma_f32_16x16x32_bf16 v[66:69], v[154:157], v[218:221], v[66:69]
	v_lshl_add_u64 v[132:133], v[132:133], 0, s[40:41]
	global_load_dwordx2 v[114:115], v[132:133], off
	global_load_dwordx2 v[116:117], v[132:133], off offset:2048
	v_mfma_f32_16x16x32_bf16 v[62:65], v[142:145], v[222:225], v[62:65]
	v_mfma_f32_16x16x32_bf16 v[58:61], v[146:149], v[222:225], v[58:61]
	v_mfma_f32_16x16x32_bf16 v[54:57], v[150:153], v[222:225], v[54:57]
	v_mfma_f32_16x16x32_bf16 v[50:53], v[154:157], v[222:225], v[50:53]
	v_lshl_add_u64 v[166:167], v[132:133], 0, s[34:35]
	global_load_dwordx2 v[118:119], v[166:167], off
	global_load_dwordx2 v[120:121], v[166:167], off offset:2048
	v_mfma_f32_16x16x32_bf16 v[46:49], v[142:145], v[226:229], v[46:49]
	v_mfma_f32_16x16x32_bf16 v[42:45], v[146:149], v[226:229], v[42:45]
	v_mfma_f32_16x16x32_bf16 v[38:41], v[150:153], v[226:229], v[38:41]
	v_mfma_f32_16x16x32_bf16 v[34:37], v[154:157], v[226:229], v[34:37]
	v_lshl_add_u64 v[166:167], v[132:133], 0, s[36:37]
	global_load_dwordx2 v[122:123], v[166:167], off
	global_load_dwordx2 v[124:125], v[166:167], off offset:2048
	v_mfma_f32_16x16x32_bf16 v[18:21], v[142:145], v[230:233], v[18:21]
	v_mfma_f32_16x16x32_bf16 v[22:25], v[146:149], v[230:233], v[22:25]
	v_mfma_f32_16x16x32_bf16 v[26:29], v[150:153], v[230:233], v[26:29]
	v_mfma_f32_16x16x32_bf16 v[30:33], v[154:157], v[230:233], v[30:33]
	v_lshl_add_u64 v[166:167], v[132:133], 0, s[38:39]
	global_load_dwordx2 v[126:127], v[166:167], off
	global_load_dwordx2 v[128:129], v[166:167], off offset:2048
	s_mov_b32 s47, s42
	s_mov_b32 s42, s43
	s_mov_b32 s43, s44
	s_mov_b32 s44, s47
	s_waitcnt lgkmcnt(0)
	s_barrier
	s_waitcnt vmcnt(29)
	v_mul_f32_e32 v186, s12, v186
	v_mul_f32_e32 v187, s12, v187
	v_mul_f32_e32 v188, s13, v188
	v_mul_f32_e32 v189, s13, v189
	v_mul_f32_e32 v190, s14, v190
	v_mul_f32_e32 v191, s14, v191
	v_mul_f32_e32 v192, s15, v192
	v_mul_f32_e32 v193, s15, v193
	v_mul_f32_e32 v194, s16, v194
	v_mul_f32_e32 v195, s16, v195
	v_mul_f32_e32 v196, s17, v196
	v_mul_f32_e32 v197, s17, v197
	v_mul_f32_e32 v198, s18, v198
	v_mul_f32_e32 v199, s18, v199
	v_mul_f32_e32 v200, s19, v200
	v_mul_f32_e32 v201, s19, v201
	v_cvt_pk_bf16_f32 v158, v186, v188
	v_cvt_pk_bf16_f32 v159, v190, v192
	v_cvt_pk_bf16_f32 v160, v194, v196
	v_cvt_pk_bf16_f32 v161, v198, v200
	v_cvt_pk_bf16_f32 v162, v187, v189
	v_cvt_pk_bf16_f32 v163, v191, v193
	v_cvt_pk_bf16_f32 v164, v195, v197
	v_cvt_pk_bf16_f32 v165, v199, v201
	ds_write_b128 v1, v[158:161] offset:0
	ds_write_b128 v1, v[162:165] offset:128
	v_add_u32_e32 v91, s42, v135
	v_add_u32_e32 v93, s42, v137
	ds_read_b128 v[238:241], v139 offset:19456
	ds_read_b128 v[242:245], v139 offset:21504
	ds_read_b128 v[246:249], v139 offset:23552
	ds_read_b128 v[250:253], v139 offset:25600
	ds_read_b128 v[218:221], v91 offset:0
	ds_read_b128 v[222:225], v91 offset:2048
	ds_read_b128 v[226:229], v91 offset:4096
	ds_read_b128 v[230:233], v91 offset:6144
	s_add_i32 s47, s44, s6
	s_add_u32 s30, s30, 0x80
	s_addc_u32 s31, s31, 0
	s_waitcnt lgkmcnt(0)
; #define MU_GLDS_A(buf, kt) do { _Pragma("unroll") for (int i = 0; i < NMU; ++i) \
;         __builtin_amdgcn_global_load_lds((const unsigned*)((const char*)A + aoff[i] + (size_t)(kt) * 128), (PG8_LAS unsigned*)(MU_SA(buf) + wid * 1024 + i * 8192), 16, 0, 0); } while (0)
; #define MU_B_ISSUE(sb, kt) do { const char* kb_ = Bb + (size_t)(kt) * (64 * (size_t)RB); _Pragma("unroll") for (int j = 0; j < 8; ++j) { const char* p_ = kb_ + (size_t)j * RB; \
;         asm volatile("global_load_dwordx2 %0, %1, off" : "=&v"(sb[j]) : "v"(p_) : "memory"); } } while (0)
; #define MU_B_WAIT(sb, N) asm volatile("s_waitcnt vmcnt(%8)" : "+v"(sb[0]), "+v"(sb[1]), "+v"(sb[2]), "+v"(sb[3]), "+v"(sb[4]), "+v"(sb[5]), "+v"(sb[6]), "+v"(sb[7]) : "n"(N) : "memory")
; #define MU_COMPUTE(buf) MU_COMPUTE_N(buf, NMU)
; template <int MODE>
; __device__ __forceinline__ void moe_unit(PG8_LAS unsigned char* lds, int e, int cb, int slot0  , int nv  , const bf16_t* A, const int* slot_tok,
;                                          const float* W0, const float* W1, bf16_t* OUT, const float* slot_rs  , const int* slot_dst) {
;     ...
;     f32x4 acc[NMU][4];
; #pragma unroll
;     for (int m = 0; m < NMU; ++m)
; #pragma unroll
;         for (int n = 0; n < 4; ++n) acc[m][n] = (f32x4){0.f, 0.f, 0.f, 0.f};
;     f32x2 s0[8], s1[8];
;     float g0[8];
;     MU_GLDS_A(0, 0); MU_B_ISSUE(s0, 0); MU_G_LOAD(g0, 0); MU_B_ISSUE(s1, 1);
;     MU_B_WAIT(s0, 8); MU_B_WRITE(s0, 0, g0); __builtin_amdgcn_sched_barrier(0); MU_B_ISSUE(s0, 2);
;     asm volatile("s_waitcnt vmcnt(16)" ::: "memory");
;     asm volatile("s_waitcnt lgkmcnt(0)" ::: "memory"); __builtin_amdgcn_s_barrier(); asm volatile("" ::: "memory");
; #pragma unroll 1
;     for (int t = 0; t < nt; t += 2) {
;         if (t + 2 < nt) MU_B_WAIT(s1, 8); else MU_B_WAIT(s1, 0);
;         MU_G_LOAD(g0, t + 1); MU_B_WRITE(s1, 1, g0); __builtin_amdgcn_sched_barrier(0); MU_GLDS_A(1, t + 1); __builtin_amdgcn_sched_barrier(0);
;         if (t + 3 < nt) { MU_B_ISSUE(s1, t + 3); }
;         MU_COMPUTE(0);
;         MU_END(t + 3 >= nt);
;         if (t + 2 < nt) { MU_B_WAIT(s0, 8); MU_G_LOAD(g0, t + 2); MU_B_WRITE(s0, 0, g0); __builtin_amdgcn_sched_barrier(0); MU_GLDS_A(0, t + 2); __builtin_amdgcn_sched_barrier(0); }
;         if (t + 4 < nt) { MU_B_ISSUE(s0, t + 4); }
;         MU_COMPUTE(1);
;         MU_END(t + 4 >= nt);
	v_mfma_f32_16x16x32_bf16 v[78:81], v[238:241], v[218:221], v[78:81]
	v_mfma_f32_16x16x32_bf16 v[74:77], v[242:245], v[218:221], v[74:77]
	v_mfma_f32_16x16x32_bf16 v[70:73], v[246:249], v[218:221], v[70:73]
	v_mfma_f32_16x16x32_bf16 v[66:69], v[250:253], v[218:221], v[66:69]
	ds_read_b128 v[218:221], v93 offset:0
	ds_read_b128 v[142:145], v141 offset:19456
	s_mov_b32 m0, s47
	s_nop 0
	global_load_lds_dwordx4 v86, s[30:31]
	v_mfma_f32_16x16x32_bf16 v[62:65], v[238:241], v[222:225], v[62:65]
	v_mfma_f32_16x16x32_bf16 v[58:61], v[242:245], v[222:225], v[58:61]
	v_mfma_f32_16x16x32_bf16 v[54:57], v[246:249], v[222:225], v[54:57]
	v_mfma_f32_16x16x32_bf16 v[50:53], v[250:253], v[222:225], v[50:53]
	ds_read_b128 v[222:225], v93 offset:2048
	ds_read_b128 v[146:149], v141 offset:21504
	s_add_i32 m0, s47, 0x2000
	s_nop 0
	global_load_lds_dwordx4 v134, s[30:31]
	v_mfma_f32_16x16x32_bf16 v[46:49], v[238:241], v[226:229], v[46:49]
	v_mfma_f32_16x16x32_bf16 v[42:45], v[242:245], v[226:229], v[42:45]
	v_mfma_f32_16x16x32_bf16 v[38:41], v[246:249], v[226:229], v[38:41]
	v_mfma_f32_16x16x32_bf16 v[34:37], v[250:253], v[226:229], v[34:37]
	ds_read_b128 v[226:229], v93 offset:4096
	ds_read_b128 v[150:153], v141 offset:23552
	s_add_i32 m0, s47, 0x4000
	s_nop 0
	global_load_lds_dwordx4 v136, s[30:31]
	v_mfma_f32_16x16x32_bf16 v[18:21], v[238:241], v[230:233], v[18:21]
	v_mfma_f32_16x16x32_bf16 v[22:25], v[242:245], v[230:233], v[22:25]
	v_mfma_f32_16x16x32_bf16 v[26:29], v[246:249], v[230:233], v[26:29]
	v_mfma_f32_16x16x32_bf16 v[30:33], v[250:253], v[230:233], v[30:33]
	ds_read_b128 v[230:233], v93 offset:6144
	ds_read_b128 v[154:157], v141 offset:25600
	s_add_i32 m0, s47, 0x6000
	s_nop 0
	global_load_lds_dwordx4 v138, s[30:31]
	s_add_i32 m0, s47, 0x8000
	s_nop 0
	global_load_lds_dwordx4 v140, s[30:31]
	s_waitcnt lgkmcnt(0)
	s_load_dwordx8 s[20:27], s[28:29], 0x0
	s_add_u32 s28, s28, 0x100
	s_addc_u32 s29, s29, 0
	v_mfma_f32_16x16x32_bf16 v[78:81], v[142:145], v[218:221], v[78:81]
	v_mfma_f32_16x16x32_bf16 v[74:77], v[146:149], v[218:221], v[74:77]
	v_mfma_f32_16x16x32_bf16 v[70:73], v[150:153], v[218:221], v[70:73]
	v_mfma_f32_16x16x32_bf16 v[66:69], v[154:157], v[218:221], v[66:69]
	v_lshl_add_u64 v[132:133], v[132:133], 0, s[40:41]
	global_load_dwordx2 v[186:187], v[132:133], off
	global_load_dwordx2 v[188:189], v[132:133], off offset:2048
	v_mfma_f32_16x16x32_bf16 v[62:65], v[142:145], v[222:225], v[62:65]
	v_mfma_f32_16x16x32_bf16 v[58:61], v[146:149], v[222:225], v[58:61]
	v_mfma_f32_16x16x32_bf16 v[54:57], v[150:153], v[222:225], v[54:57]
	v_mfma_f32_16x16x32_bf16 v[50:53], v[154:157], v[222:225], v[50:53]
	v_lshl_add_u64 v[166:167], v[132:133], 0, s[34:35]
	global_load_dwordx2 v[190:191], v[166:167], off
	global_load_dwordx2 v[192:193], v[166:167], off offset:2048
	v_mfma_f32_16x16x32_bf16 v[46:49], v[142:145], v[226:229], v[46:49]
	v_mfma_f32_16x16x32_bf16 v[42:45], v[146:149], v[226:229], v[42:45]
	v_mfma_f32_16x16x32_bf16 v[38:41], v[150:153], v[226:229], v[38:41]
	v_mfma_f32_16x16x32_bf16 v[34:37], v[154:157], v[226:229], v[34:37]
	v_lshl_add_u64 v[166:167], v[132:133], 0, s[36:37]
	global_load_dwordx2 v[194:195], v[166:167], off
	global_load_dwordx2 v[196:197], v[166:167], off offset:2048
	v_mfma_f32_16x16x32_bf16 v[18:21], v[142:145], v[230:233], v[18:21]
	v_mfma_f32_16x16x32_bf16 v[22:25], v[146:149], v[230:233], v[22:25]
	v_mfma_f32_16x16x32_bf16 v[26:29], v[150:153], v[230:233], v[26:29]
	v_mfma_f32_16x16x32_bf16 v[30:33], v[154:157], v[230:233], v[30:33]
	v_lshl_add_u64 v[166:167], v[132:133], 0, s[38:39]
	global_load_dwordx2 v[198:199], v[166:167], off
	global_load_dwordx2 v[200:201], v[166:167], off offset:2048
	s_waitcnt vmcnt(21)
	s_mov_b32 s47, s42
	s_mov_b32 s42, s43
	s_mov_b32 s43, s44
	s_mov_b32 s44, s47
	s_waitcnt lgkmcnt(0)
	s_barrier
	v_mul_f32_e32 v202, s20, v202
	v_mul_f32_e32 v203, s20, v203
	v_mul_f32_e32 v204, s21, v204
	v_mul_f32_e32 v205, s21, v205
	v_mul_f32_e32 v206, s22, v206
	v_mul_f32_e32 v207, s22, v207
	v_mul_f32_e32 v208, s23, v208
	v_mul_f32_e32 v209, s23, v209
	v_mul_f32_e32 v210, s24, v210
	v_mul_f32_e32 v211, s24, v211
	v_mul_f32_e32 v212, s25, v212
	v_mul_f32_e32 v213, s25, v213
	v_mul_f32_e32 v214, s26, v214
	v_mul_f32_e32 v215, s26, v215
	v_mul_f32_e32 v216, s27, v216
	v_mul_f32_e32 v217, s27, v217
	v_cvt_pk_bf16_f32 v158, v202, v204
	v_cvt_pk_bf16_f32 v159, v206, v208
	v_cvt_pk_bf16_f32 v160, v210, v212
	v_cvt_pk_bf16_f32 v161, v214, v216
	v_cvt_pk_bf16_f32 v162, v203, v205
	v_cvt_pk_bf16_f32 v163, v207, v209
	v_cvt_pk_bf16_f32 v164, v211, v213
	v_cvt_pk_bf16_f32 v165, v215, v217
	ds_write_b128 v1, v[158:161] offset:19456
	ds_write_b128 v1, v[162:165] offset:19584
	v_add_u32_e32 v91, s42, v135
	v_add_u32_e32 v93, s42, v137
	ds_read_b128 v[238:241], v139 offset:0
	ds_read_b128 v[242:245], v139 offset:2048
	ds_read_b128 v[246:249], v139 offset:4096
	ds_read_b128 v[250:253], v139 offset:6144
	ds_read_b128 v[218:221], v91 offset:0
	ds_read_b128 v[222:225], v91 offset:2048
	ds_read_b128 v[226:229], v91 offset:4096
	ds_read_b128 v[230:233], v91 offset:6144
	s_add_i32 s47, s44, s6
	s_add_u32 s30, s30, 0x80
	s_addc_u32 s31, s31, 0
	s_waitcnt lgkmcnt(0)
; #define MU_GLDS_A(buf, kt) do { _Pragma("unroll") for (int i = 0; i < NMU; ++i) \
;         __builtin_amdgcn_global_load_lds((const unsigned*)((const char*)A + aoff[i] + (size_t)(kt) * 128), (PG8_LAS unsigned*)(MU_SA(buf) + wid * 1024 + i * 8192), 16, 0, 0); } while (0)
; #define MU_B_ISSUE(sb, kt) do { const char* kb_ = Bb + (size_t)(kt) * (64 * (size_t)RB); _Pragma("unroll") for (int j = 0; j < 8; ++j) { const char* p_ = kb_ + (size_t)j * RB; \
;         asm volatile("global_load_dwordx2 %0, %1, off" : "=&v"(sb[j]) : "v"(p_) : "memory"); } } while (0)
; #define MU_B_WAIT(sb, N) asm volatile("s_waitcnt vmcnt(%8)" : "+v"(sb[0]), "+v"(sb[1]), "+v"(sb[2]), "+v"(sb[3]), "+v"(sb[4]), "+v"(sb[5]), "+v"(sb[6]), "+v"(sb[7]) : "n"(N) : "memory")
; #define MU_COMPUTE(buf) MU_COMPUTE_N(buf, NMU)
; template <int MODE>
; __device__ __forceinline__ void moe_unit(PG8_LAS unsigned char* lds, int e, int cb, int slot0  , int nv  , const bf16_t* A, const int* slot_tok,
;                                          const float* W0, const float* W1, bf16_t* OUT, const float* slot_rs  , const int* slot_dst) {
;     ...
;     f32x4 acc[NMU][4];
; #pragma unroll
;     for (int m = 0; m < NMU; ++m)
; #pragma unroll
;         for (int n = 0; n < 4; ++n) acc[m][n] = (f32x4){0.f, 0.f, 0.f, 0.f};
;     f32x2 s0[8], s1[8];
;     float g0[8];
;     MU_GLDS_A(0, 0); MU_B_ISSUE(s0, 0); MU_G_LOAD(g0, 0); MU_B_ISSUE(s1, 1);
;     MU_B_WAIT(s0, 8); MU_B_WRITE(s0, 0, g0); __builtin_amdgcn_sched_barrier(0); MU_B_ISSUE(s0, 2);
;     asm volatile("s_waitcnt vmcnt(16)" ::: "memory");
;     asm volatile("s_waitcnt lgkmcnt(0)" ::: "memory"); __builtin_amdgcn_s_barrier(); asm volatile("" ::: "memory");
; #pragma unroll 1
;     for (int t = 0; t < nt; t += 2) {
;         if (t + 2 < nt) MU_B_WAIT(s1, 8); else MU_B_WAIT(s1, 0);
;         MU_G_LOAD(g0, t + 1); MU_B_WRITE(s1, 1, g0); __builtin_amdgcn_sched_barrier(0); MU_GLDS_A(1, t + 1); __builtin_amdgcn_sched_barrier(0);
;         if (t + 3 < nt) { MU_B_ISSUE(s1, t + 3); }
;         MU_COMPUTE(0);
;         MU_END(t + 3 >= nt);
;         if (t + 2 < nt) { MU_B_WAIT(s0, 8); MU_G_LOAD(g0, t + 2); MU_B_WRITE(s0, 0, g0); __builtin_amdgcn_sched_barrier(0); MU_GLDS_A(0, t + 2); __builtin_amdgcn_sched_barrier(0); }
;         if (t + 4 < nt) { MU_B_ISSUE(s0, t + 4); }
;         MU_COMPUTE(1);
;         MU_END(t + 4 >= nt);
	v_mfma_f32_16x16x32_bf16 v[78:81], v[238:241], v[218:221], v[78:81]
	v_mfma_f32_16x16x32_bf16 v[74:77], v[242:245], v[218:221], v[74:77]
	v_mfma_f32_16x16x32_bf16 v[70:73], v[246:249], v[218:221], v[70:73]
	v_mfma_f32_16x16x32_bf16 v[66:69], v[250:253], v[218:221], v[66:69]
	ds_read_b128 v[218:221], v93 offset:0
	ds_read_b128 v[142:145], v141 offset:0
	s_mov_b32 m0, s47
	s_nop 0
	global_load_lds_dwordx4 v86, s[30:31]
	v_mfma_f32_16x16x32_bf16 v[62:65], v[238:241], v[222:225], v[62:65]
	v_mfma_f32_16x16x32_bf16 v[58:61], v[242:245], v[222:225], v[58:61]
	v_mfma_f32_16x16x32_bf16 v[54:57], v[246:249], v[222:225], v[54:57]
	v_mfma_f32_16x16x32_bf16 v[50:53], v[250:253], v[222:225], v[50:53]
	ds_read_b128 v[222:225], v93 offset:2048
	ds_read_b128 v[146:149], v141 offset:2048
	s_add_i32 m0, s47, 0x2000
	s_nop 0
	global_load_lds_dwordx4 v134, s[30:31]
	v_mfma_f32_16x16x32_bf16 v[46:49], v[238:241], v[226:229], v[46:49]
	v_mfma_f32_16x16x32_bf16 v[42:45], v[242:245], v[226:229], v[42:45]
	v_mfma_f32_16x16x32_bf16 v[38:41], v[246:249], v[226:229], v[38:41]
	v_mfma_f32_16x16x32_bf16 v[34:37], v[250:253], v[226:229], v[34:37]
	ds_read_b128 v[226:229], v93 offset:4096
	ds_read_b128 v[150:153], v141 offset:4096
	s_add_i32 m0, s47, 0x4000
	s_nop 0
	global_load_lds_dwordx4 v136, s[30:31]
	v_mfma_f32_16x16x32_bf16 v[18:21], v[238:241], v[230:233], v[18:21]
	v_mfma_f32_16x16x32_bf16 v[22:25], v[242:245], v[230:233], v[22:25]
	v_mfma_f32_16x16x32_bf16 v[26:29], v[246:249], v[230:233], v[26:29]
	v_mfma_f32_16x16x32_bf16 v[30:33], v[250:253], v[230:233], v[30:33]
	ds_read_b128 v[230:233], v93 offset:6144
	ds_read_b128 v[154:157], v141 offset:6144
	s_add_i32 m0, s47, 0x6000
	s_nop 0
	global_load_lds_dwordx4 v138, s[30:31]
	s_add_i32 m0, s47, 0x8000
	s_nop 0
	global_load_lds_dwordx4 v140, s[30:31]
	s_waitcnt lgkmcnt(0)
	s_load_dwordx8 s[12:19], s[28:29], 0x0
	s_add_u32 s28, s28, 0x100
	s_addc_u32 s29, s29, 0
	v_mfma_f32_16x16x32_bf16 v[78:81], v[142:145], v[218:221], v[78:81]
	v_mfma_f32_16x16x32_bf16 v[74:77], v[146:149], v[218:221], v[74:77]
	v_mfma_f32_16x16x32_bf16 v[70:73], v[150:153], v[218:221], v[70:73]
	v_mfma_f32_16x16x32_bf16 v[66:69], v[154:157], v[218:221], v[66:69]
	v_lshl_add_u64 v[132:133], v[132:133], 0, s[40:41]
	global_load_dwordx2 v[202:203], v[132:133], off
	global_load_dwordx2 v[204:205], v[132:133], off offset:2048
	v_mfma_f32_16x16x32_bf16 v[62:65], v[142:145], v[222:225], v[62:65]
	v_mfma_f32_16x16x32_bf16 v[58:61], v[146:149], v[222:225], v[58:61]
	v_mfma_f32_16x16x32_bf16 v[54:57], v[150:153], v[222:225], v[54:57]
	v_mfma_f32_16x16x32_bf16 v[50:53], v[154:157], v[222:225], v[50:53]
	v_lshl_add_u64 v[166:167], v[132:133], 0, s[34:35]
	global_load_dwordx2 v[206:207], v[166:167], off
	global_load_dwordx2 v[208:209], v[166:167], off offset:2048
	v_mfma_f32_16x16x32_bf16 v[46:49], v[142:145], v[226:229], v[46:49]
	v_mfma_f32_16x16x32_bf16 v[42:45], v[146:149], v[226:229], v[42:45]
	v_mfma_f32_16x16x32_bf16 v[38:41], v[150:153], v[226:229], v[38:41]
	v_mfma_f32_16x16x32_bf16 v[34:37], v[154:157], v[226:229], v[34:37]
	v_lshl_add_u64 v[166:167], v[132:133], 0, s[36:37]
	global_load_dwordx2 v[210:211], v[166:167], off
	global_load_dwordx2 v[212:213], v[166:167], off offset:2048
	v_mfma_f32_16x16x32_bf16 v[18:21], v[142:145], v[230:233], v[18:21]
	v_mfma_f32_16x16x32_bf16 v[22:25], v[146:149], v[230:233], v[22:25]
	v_mfma_f32_16x16x32_bf16 v[26:29], v[150:153], v[230:233], v[26:29]
	v_mfma_f32_16x16x32_bf16 v[30:33], v[154:157], v[230:233], v[30:33]
	v_lshl_add_u64 v[166:167], v[132:133], 0, s[38:39]
	global_load_dwordx2 v[214:215], v[166:167], off
	global_load_dwordx2 v[216:217], v[166:167], off offset:2048
	s_waitcnt vmcnt(21)
	s_mov_b32 s47, s42
	s_mov_b32 s42, s43
	s_mov_b32 s43, s44
	s_mov_b32 s44, s47
	s_waitcnt lgkmcnt(0)
	s_barrier
	v_mul_f32_e32 v98, s12, v98
	v_mul_f32_e32 v99, s12, v99
	v_mul_f32_e32 v100, s13, v100
	v_mul_f32_e32 v101, s13, v101
	v_mul_f32_e32 v102, s14, v102
	v_mul_f32_e32 v103, s14, v103
	v_mul_f32_e32 v104, s15, v104
	v_mul_f32_e32 v105, s15, v105
	v_mul_f32_e32 v106, s16, v106
	v_mul_f32_e32 v107, s16, v107
	v_mul_f32_e32 v108, s17, v108
	v_mul_f32_e32 v109, s17, v109
	v_mul_f32_e32 v110, s18, v110
	v_mul_f32_e32 v111, s18, v111
	v_mul_f32_e32 v112, s19, v112
	v_mul_f32_e32 v113, s19, v113
	v_cvt_pk_bf16_f32 v158, v98, v100
	v_cvt_pk_bf16_f32 v159, v102, v104
	v_cvt_pk_bf16_f32 v160, v106, v108
	v_cvt_pk_bf16_f32 v161, v110, v112
	v_cvt_pk_bf16_f32 v162, v99, v101
	v_cvt_pk_bf16_f32 v163, v103, v105
	v_cvt_pk_bf16_f32 v164, v107, v109
	v_cvt_pk_bf16_f32 v165, v111, v113
	ds_write_b128 v1, v[158:161] offset:0
	ds_write_b128 v1, v[162:165] offset:128
	v_add_u32_e32 v91, s42, v135
	v_add_u32_e32 v93, s42, v137
	ds_read_b128 v[238:241], v139 offset:19456
	ds_read_b128 v[242:245], v139 offset:21504
	ds_read_b128 v[246:249], v139 offset:23552
	ds_read_b128 v[250:253], v139 offset:25600
	ds_read_b128 v[218:221], v91 offset:0
	ds_read_b128 v[222:225], v91 offset:2048
	ds_read_b128 v[226:229], v91 offset:4096
	ds_read_b128 v[230:233], v91 offset:6144
	s_add_i32 s47, s44, s6
	s_add_u32 s30, s30, 0x80
	s_addc_u32 s31, s31, 0
	s_waitcnt lgkmcnt(0)
; #define MU_GLDS_A(buf, kt) do { _Pragma("unroll") for (int i = 0; i < NMU; ++i) \
;         __builtin_amdgcn_global_load_lds((const unsigned*)((const char*)A + aoff[i] + (size_t)(kt) * 128), (PG8_LAS unsigned*)(MU_SA(buf) + wid * 1024 + i * 8192), 16, 0, 0); } while (0)
; #define MU_B_ISSUE(sb, kt) do { const char* kb_ = Bb + (size_t)(kt) * (64 * (size_t)RB); _Pragma("unroll") for (int j = 0; j < 8; ++j) { const char* p_ = kb_ + (size_t)j * RB; \
;         asm volatile("global_load_dwordx2 %0, %1, off" : "=&v"(sb[j]) : "v"(p_) : "memory"); } } while (0)
; #define MU_B_WAIT(sb, N) asm volatile("s_waitcnt vmcnt(%8)" : "+v"(sb[0]), "+v"(sb[1]), "+v"(sb[2]), "+v"(sb[3]), "+v"(sb[4]), "+v"(sb[5]), "+v"(sb[6]), "+v"(sb[7]) : "n"(N) : "memory")
; #define MU_COMPUTE(buf) MU_COMPUTE_N(buf, NMU)
; template <int MODE>
; __device__ __forceinline__ void moe_unit(PG8_LAS unsigned char* lds, int e, int cb, int slot0  , int nv  , const bf16_t* A, const int* slot_tok,
;                                          const float* W0, const float* W1, bf16_t* OUT, const float* slot_rs  , const int* slot_dst) {
;     ...
;     f32x4 acc[NMU][4];
; #pragma unroll
;     for (int m = 0; m < NMU; ++m)
; #pragma unroll
;         for (int n = 0; n < 4; ++n) acc[m][n] = (f32x4){0.f, 0.f, 0.f, 0.f};
;     f32x2 s0[8], s1[8];
;     float g0[8];
;     MU_GLDS_A(0, 0); MU_B_ISSUE(s0, 0); MU_G_LOAD(g0, 0); MU_B_ISSUE(s1, 1);
;     MU_B_WAIT(s0, 8); MU_B_WRITE(s0, 0, g0); __builtin_amdgcn_sched_barrier(0); MU_B_ISSUE(s0, 2);
;     asm volatile("s_waitcnt vmcnt(16)" ::: "memory");
;     asm volatile("s_waitcnt lgkmcnt(0)" ::: "memory"); __builtin_amdgcn_s_barrier(); asm volatile("" ::: "memory");
; #pragma unroll 1
;     for (int t = 0; t < nt; t += 2) {
;         if (t + 2 < nt) MU_B_WAIT(s1, 8); else MU_B_WAIT(s1, 0);
;         MU_G_LOAD(g0, t + 1); MU_B_WRITE(s1, 1, g0); __builtin_amdgcn_sched_barrier(0); MU_GLDS_A(1, t + 1); __builtin_amdgcn_sched_barrier(0);
;         if (t + 3 < nt) { MU_B_ISSUE(s1, t + 3); }
;         MU_COMPUTE(0);
;         MU_END(t + 3 >= nt);
;         if (t + 2 < nt) { MU_B_WAIT(s0, 8); MU_G_LOAD(g0, t + 2); MU_B_WRITE(s0, 0, g0); __builtin_amdgcn_sched_barrier(0); MU_GLDS_A(0, t + 2); __builtin_amdgcn_sched_barrier(0); }
;         if (t + 4 < nt) { MU_B_ISSUE(s0, t + 4); }
;         MU_COMPUTE(1);
;         MU_END(t + 4 >= nt);
	v_mfma_f32_16x16x32_bf16 v[78:81], v[238:241], v[218:221], v[78:81]
	v_mfma_f32_16x16x32_bf16 v[74:77], v[242:245], v[218:221], v[74:77]
	v_mfma_f32_16x16x32_bf16 v[70:73], v[246:249], v[218:221], v[70:73]
	v_mfma_f32_16x16x32_bf16 v[66:69], v[250:253], v[218:221], v[66:69]
	ds_read_b128 v[218:221], v93 offset:0
	ds_read_b128 v[142:145], v141 offset:19456
	s_mov_b32 m0, s47
	s_nop 0
	global_load_lds_dwordx4 v86, s[30:31]
	v_mfma_f32_16x16x32_bf16 v[62:65], v[238:241], v[222:225], v[62:65]
	v_mfma_f32_16x16x32_bf16 v[58:61], v[242:245], v[222:225], v[58:61]
	v_mfma_f32_16x16x32_bf16 v[54:57], v[246:249], v[222:225], v[54:57]
	v_mfma_f32_16x16x32_bf16 v[50:53], v[250:253], v[222:225], v[50:53]
	ds_read_b128 v[222:225], v93 offset:2048
	ds_read_b128 v[146:149], v141 offset:21504
	s_add_i32 m0, s47, 0x2000
	s_nop 0
	global_load_lds_dwordx4 v134, s[30:31]
	v_mfma_f32_16x16x32_bf16 v[46:49], v[238:241], v[226:229], v[46:49]
	v_mfma_f32_16x16x32_bf16 v[42:45], v[242:245], v[226:229], v[42:45]
	v_mfma_f32_16x16x32_bf16 v[38:41], v[246:249], v[226:229], v[38:41]
	v_mfma_f32_16x16x32_bf16 v[34:37], v[250:253], v[226:229], v[34:37]
	ds_read_b128 v[226:229], v93 offset:4096
	ds_read_b128 v[150:153], v141 offset:23552
	s_add_i32 m0, s47, 0x4000
	s_nop 0
	global_load_lds_dwordx4 v136, s[30:31]
	v_mfma_f32_16x16x32_bf16 v[18:21], v[238:241], v[230:233], v[18:21]
	v_mfma_f32_16x16x32_bf16 v[22:25], v[242:245], v[230:233], v[22:25]
	v_mfma_f32_16x16x32_bf16 v[26:29], v[246:249], v[230:233], v[26:29]
	v_mfma_f32_16x16x32_bf16 v[30:33], v[250:253], v[230:233], v[30:33]
	ds_read_b128 v[230:233], v93 offset:6144
	ds_read_b128 v[154:157], v141 offset:25600
	s_add_i32 m0, s47, 0x6000
	s_nop 0
	global_load_lds_dwordx4 v138, s[30:31]
	s_add_i32 m0, s47, 0x8000
	s_nop 0
	global_load_lds_dwordx4 v140, s[30:31]
	s_waitcnt lgkmcnt(0)
	s_load_dwordx8 s[20:27], s[28:29], 0x0
	s_add_u32 s28, s28, 0x100
	s_addc_u32 s29, s29, 0
	v_mfma_f32_16x16x32_bf16 v[78:81], v[142:145], v[218:221], v[78:81]
	v_mfma_f32_16x16x32_bf16 v[74:77], v[146:149], v[218:221], v[74:77]
	v_mfma_f32_16x16x32_bf16 v[70:73], v[150:153], v[218:221], v[70:73]
	v_mfma_f32_16x16x32_bf16 v[66:69], v[154:157], v[218:221], v[66:69]
	v_lshl_add_u64 v[132:133], v[132:133], 0, s[40:41]
	global_load_dwordx2 v[98:99], v[132:133], off
	global_load_dwordx2 v[100:101], v[132:133], off offset:2048
	v_mfma_f32_16x16x32_bf16 v[62:65], v[142:145], v[222:225], v[62:65]
	v_mfma_f32_16x16x32_bf16 v[58:61], v[146:149], v[222:225], v[58:61]
	v_mfma_f32_16x16x32_bf16 v[54:57], v[150:153], v[222:225], v[54:57]
	v_mfma_f32_16x16x32_bf16 v[50:53], v[154:157], v[222:225], v[50:53]
	v_lshl_add_u64 v[166:167], v[132:133], 0, s[34:35]
	global_load_dwordx2 v[102:103], v[166:167], off
	global_load_dwordx2 v[104:105], v[166:167], off offset:2048
	v_mfma_f32_16x16x32_bf16 v[46:49], v[142:145], v[226:229], v[46:49]
	v_mfma_f32_16x16x32_bf16 v[42:45], v[146:149], v[226:229], v[42:45]
	v_mfma_f32_16x16x32_bf16 v[38:41], v[150:153], v[226:229], v[38:41]
	v_mfma_f32_16x16x32_bf16 v[34:37], v[154:157], v[226:229], v[34:37]
	v_lshl_add_u64 v[166:167], v[132:133], 0, s[36:37]
	global_load_dwordx2 v[106:107], v[166:167], off
	global_load_dwordx2 v[108:109], v[166:167], off offset:2048
	v_mfma_f32_16x16x32_bf16 v[18:21], v[142:145], v[230:233], v[18:21]
	v_mfma_f32_16x16x32_bf16 v[22:25], v[146:149], v[230:233], v[22:25]
	v_mfma_f32_16x16x32_bf16 v[26:29], v[150:153], v[230:233], v[26:29]
	v_mfma_f32_16x16x32_bf16 v[30:33], v[154:157], v[230:233], v[30:33]
	v_lshl_add_u64 v[166:167], v[132:133], 0, s[38:39]
	global_load_dwordx2 v[110:111], v[166:167], off
	global_load_dwordx2 v[112:113], v[166:167], off offset:2048
	s_waitcnt vmcnt(21)
	s_mov_b32 s47, s42
	s_mov_b32 s42, s43
	s_mov_b32 s43, s44
	s_mov_b32 s44, s47
	s_waitcnt lgkmcnt(0)
	s_barrier
	s_mov_b32 s46, 13
.Lmu_loop_X4:
	v_mul_f32_e32 v114, s20, v114
	v_mul_f32_e32 v115, s20, v115
	v_mul_f32_e32 v116, s21, v116
	v_mul_f32_e32 v117, s21, v117
	v_mul_f32_e32 v118, s22, v118
	v_mul_f32_e32 v119, s22, v119
	v_mul_f32_e32 v120, s23, v120
	v_mul_f32_e32 v121, s23, v121
	v_mul_f32_e32 v122, s24, v122
	v_mul_f32_e32 v123, s24, v123
	v_mul_f32_e32 v124, s25, v124
	v_mul_f32_e32 v125, s25, v125
	v_mul_f32_e32 v126, s26, v126
	v_mul_f32_e32 v127, s26, v127
	v_mul_f32_e32 v128, s27, v128
	v_mul_f32_e32 v129, s27, v129
	v_cvt_pk_bf16_f32 v158, v114, v116
	v_cvt_pk_bf16_f32 v159, v118, v120
	v_cvt_pk_bf16_f32 v160, v122, v124
	v_cvt_pk_bf16_f32 v161, v126, v128
	v_cvt_pk_bf16_f32 v162, v115, v117
	v_cvt_pk_bf16_f32 v163, v119, v121
	v_cvt_pk_bf16_f32 v164, v123, v125
	v_cvt_pk_bf16_f32 v165, v127, v129
	ds_write_b128 v1, v[158:161] offset:19456
	ds_write_b128 v1, v[162:165] offset:19584
	v_add_u32_e32 v91, s42, v135
	v_add_u32_e32 v93, s42, v137
	ds_read_b128 v[238:241], v139 offset:0
	ds_read_b128 v[242:245], v139 offset:2048
	ds_read_b128 v[246:249], v139 offset:4096
	ds_read_b128 v[250:253], v139 offset:6144
	ds_read_b128 v[218:221], v91 offset:0
	ds_read_b128 v[222:225], v91 offset:2048
	ds_read_b128 v[226:229], v91 offset:4096
	ds_read_b128 v[230:233], v91 offset:6144
	s_add_i32 s47, s44, s6
	s_add_u32 s30, s30, 0x80
	s_addc_u32 s31, s31, 0
	s_waitcnt lgkmcnt(0)
; #define MU_GLDS_A(buf, kt) do { _Pragma("unroll") for (int i = 0; i < NMU; ++i) \
;         __builtin_amdgcn_global_load_lds((const unsigned*)((const char*)A + aoff[i] + (size_t)(kt) * 128), (PG8_LAS unsigned*)(MU_SA(buf) + wid * 1024 + i * 8192), 16, 0, 0); } while (0)
; #define MU_B_ISSUE(sb, kt) do { const char* kb_ = Bb + (size_t)(kt) * (64 * (size_t)RB); _Pragma("unroll") for (int j = 0; j < 8; ++j) { const char* p_ = kb_ + (size_t)j * RB; \
;         asm volatile("global_load_dwordx2 %0, %1, off" : "=&v"(sb[j]) : "v"(p_) : "memory"); } } while (0)
; #define MU_B_WAIT(sb, N) asm volatile("s_waitcnt vmcnt(%8)" : "+v"(sb[0]), "+v"(sb[1]), "+v"(sb[2]), "+v"(sb[3]), "+v"(sb[4]), "+v"(sb[5]), "+v"(sb[6]), "+v"(sb[7]) : "n"(N) : "memory")
; #define MU_COMPUTE(buf) MU_COMPUTE_N(buf, NMU)
; template <int MODE>
; __device__ __forceinline__ void moe_unit(PG8_LAS unsigned char* lds, int e, int cb, int slot0  , int nv  , const bf16_t* A, const int* slot_tok,
;                                          const float* W0, const float* W1, bf16_t* OUT, const float* slot_rs  , const int* slot_dst) {
;     ...
;     f32x4 acc[NMU][4];
; #pragma unroll
;     for (int m = 0; m < NMU; ++m)
; #pragma unroll
;         for (int n = 0; n < 4; ++n) acc[m][n] = (f32x4){0.f, 0.f, 0.f, 0.f};
;     f32x2 s0[8], s1[8];
;     float g0[8];
;     MU_GLDS_A(0, 0); MU_B_ISSUE(s0, 0); MU_G_LOAD(g0, 0); MU_B_ISSUE(s1, 1);
;     MU_B_WAIT(s0, 8); MU_B_WRITE(s0, 0, g0); __builtin_amdgcn_sched_barrier(0); MU_B_ISSUE(s0, 2);
;     asm volatile("s_waitcnt vmcnt(16)" ::: "memory");
;     asm volatile("s_waitcnt lgkmcnt(0)" ::: "memory"); __builtin_amdgcn_s_barrier(); asm volatile("" ::: "memory");
; #pragma unroll 1
;     for (int t = 0; t < nt; t += 2) {
;         if (t + 2 < nt) MU_B_WAIT(s1, 8); else MU_B_WAIT(s1, 0);
;         MU_G_LOAD(g0, t + 1); MU_B_WRITE(s1, 1, g0); __builtin_amdgcn_sched_barrier(0); MU_GLDS_A(1, t + 1); __builtin_amdgcn_sched_barrier(0);
;         if (t + 3 < nt) { MU_B_ISSUE(s1, t + 3); }
;         MU_COMPUTE(0);
;         MU_END(t + 3 >= nt);
;         if (t + 2 < nt) { MU_B_WAIT(s0, 8); MU_G_LOAD(g0, t + 2); MU_B_WRITE(s0, 0, g0); __builtin_amdgcn_sched_barrier(0); MU_GLDS_A(0, t + 2); __builtin_amdgcn_sched_barrier(0); }
;         if (t + 4 < nt) { MU_B_ISSUE(s0, t + 4); }
;         MU_COMPUTE(1);
;         MU_END(t + 4 >= nt);
	v_mfma_f32_16x16x32_bf16 v[78:81], v[238:241], v[218:221], v[78:81]
	v_mfma_f32_16x16x32_bf16 v[74:77], v[242:245], v[218:221], v[74:77]
	v_mfma_f32_16x16x32_bf16 v[70:73], v[246:249], v[218:221], v[70:73]
	v_mfma_f32_16x16x32_bf16 v[66:69], v[250:253], v[218:221], v[66:69]
	ds_read_b128 v[218:221], v93 offset:0
	ds_read_b128 v[142:145], v141 offset:0
	s_mov_b32 m0, s47
	s_nop 0
	global_load_lds_dwordx4 v86, s[30:31]
	v_mfma_f32_16x16x32_bf16 v[62:65], v[238:241], v[222:225], v[62:65]
	v_mfma_f32_16x16x32_bf16 v[58:61], v[242:245], v[222:225], v[58:61]
	v_mfma_f32_16x16x32_bf16 v[54:57], v[246:249], v[222:225], v[54:57]
	v_mfma_f32_16x16x32_bf16 v[50:53], v[250:253], v[222:225], v[50:53]
	ds_read_b128 v[222:225], v93 offset:2048
	ds_read_b128 v[146:149], v141 offset:2048
	s_add_i32 m0, s47, 0x2000
	s_nop 0
	global_load_lds_dwordx4 v134, s[30:31]
	v_mfma_f32_16x16x32_bf16 v[46:49], v[238:241], v[226:229], v[46:49]
	v_mfma_f32_16x16x32_bf16 v[42:45], v[242:245], v[226:229], v[42:45]
	v_mfma_f32_16x16x32_bf16 v[38:41], v[246:249], v[226:229], v[38:41]
	v_mfma_f32_16x16x32_bf16 v[34:37], v[250:253], v[226:229], v[34:37]
	ds_read_b128 v[226:229], v93 offset:4096
	ds_read_b128 v[150:153], v141 offset:4096
	s_add_i32 m0, s47, 0x4000
	s_nop 0
	global_load_lds_dwordx4 v136, s[30:31]
	v_mfma_f32_16x16x32_bf16 v[18:21], v[238:241], v[230:233], v[18:21]
	v_mfma_f32_16x16x32_bf16 v[22:25], v[242:245], v[230:233], v[22:25]
	v_mfma_f32_16x16x32_bf16 v[26:29], v[246:249], v[230:233], v[26:29]
	v_mfma_f32_16x16x32_bf16 v[30:33], v[250:253], v[230:233], v[30:33]
	ds_read_b128 v[230:233], v93 offset:6144
	ds_read_b128 v[154:157], v141 offset:6144
	s_add_i32 m0, s47, 0x6000
	s_nop 0
	global_load_lds_dwordx4 v138, s[30:31]
	s_add_i32 m0, s47, 0x8000
	s_nop 0
	global_load_lds_dwordx4 v140, s[30:31]
	s_waitcnt lgkmcnt(0)
	s_load_dwordx8 s[12:19], s[28:29], 0x0
	s_add_u32 s28, s28, 0x100
	s_addc_u32 s29, s29, 0
	v_mfma_f32_16x16x32_bf16 v[78:81], v[142:145], v[218:221], v[78:81]
	v_mfma_f32_16x16x32_bf16 v[74:77], v[146:149], v[218:221], v[74:77]
	v_mfma_f32_16x16x32_bf16 v[70:73], v[150:153], v[218:221], v[70:73]
	v_mfma_f32_16x16x32_bf16 v[66:69], v[154:157], v[218:221], v[66:69]
	v_lshl_add_u64 v[132:133], v[132:133], 0, s[40:41]
	global_load_dwordx2 v[114:115], v[132:133], off
	global_load_dwordx2 v[116:117], v[132:133], off offset:2048
	v_mfma_f32_16x16x32_bf16 v[62:65], v[142:145], v[222:225], v[62:65]
	v_mfma_f32_16x16x32_bf16 v[58:61], v[146:149], v[222:225], v[58:61]
	v_mfma_f32_16x16x32_bf16 v[54:57], v[150:153], v[222:225], v[54:57]
	v_mfma_f32_16x16x32_bf16 v[50:53], v[154:157], v[222:225], v[50:53]
	v_lshl_add_u64 v[166:167], v[132:133], 0, s[34:35]
	global_load_dwordx2 v[118:119], v[166:167], off
	global_load_dwordx2 v[120:121], v[166:167], off offset:2048
	v_mfma_f32_16x16x32_bf16 v[46:49], v[142:145], v[226:229], v[46:49]
	v_mfma_f32_16x16x32_bf16 v[42:45], v[146:149], v[226:229], v[42:45]
	v_mfma_f32_16x16x32_bf16 v[38:41], v[150:153], v[226:229], v[38:41]
	v_mfma_f32_16x16x32_bf16 v[34:37], v[154:157], v[226:229], v[34:37]
	v_lshl_add_u64 v[166:167], v[132:133], 0, s[36:37]
	global_load_dwordx2 v[122:123], v[166:167], off
	global_load_dwordx2 v[124:125], v[166:167], off offset:2048
	v_mfma_f32_16x16x32_bf16 v[18:21], v[142:145], v[230:233], v[18:21]
	v_mfma_f32_16x16x32_bf16 v[22:25], v[146:149], v[230:233], v[22:25]
	v_mfma_f32_16x16x32_bf16 v[26:29], v[150:153], v[230:233], v[26:29]
	v_mfma_f32_16x16x32_bf16 v[30:33], v[154:157], v[230:233], v[30:33]
	v_lshl_add_u64 v[166:167], v[132:133], 0, s[38:39]
	global_load_dwordx2 v[126:127], v[166:167], off
	global_load_dwordx2 v[128:129], v[166:167], off offset:2048
	s_waitcnt vmcnt(21)
	s_mov_b32 s47, s42
	s_mov_b32 s42, s43
	s_mov_b32 s43, s44
	s_mov_b32 s44, s47
	s_waitcnt lgkmcnt(0)
	s_barrier
	v_mul_f32_e32 v186, s12, v186
	v_mul_f32_e32 v187, s12, v187
	v_mul_f32_e32 v188, s13, v188
	v_mul_f32_e32 v189, s13, v189
	v_mul_f32_e32 v190, s14, v190
	v_mul_f32_e32 v191, s14, v191
	v_mul_f32_e32 v192, s15, v192
	v_mul_f32_e32 v193, s15, v193
	v_mul_f32_e32 v194, s16, v194
	v_mul_f32_e32 v195, s16, v195
	v_mul_f32_e32 v196, s17, v196
	v_mul_f32_e32 v197, s17, v197
	v_mul_f32_e32 v198, s18, v198
	v_mul_f32_e32 v199, s18, v199
	v_mul_f32_e32 v200, s19, v200
	v_mul_f32_e32 v201, s19, v201
	v_cvt_pk_bf16_f32 v158, v186, v188
	v_cvt_pk_bf16_f32 v159, v190, v192
	v_cvt_pk_bf16_f32 v160, v194, v196
	v_cvt_pk_bf16_f32 v161, v198, v200
	v_cvt_pk_bf16_f32 v162, v187, v189
	v_cvt_pk_bf16_f32 v163, v191, v193
	v_cvt_pk_bf16_f32 v164, v195, v197
	v_cvt_pk_bf16_f32 v165, v199, v201
	ds_write_b128 v1, v[158:161] offset:0
	ds_write_b128 v1, v[162:165] offset:128
	v_add_u32_e32 v91, s42, v135
	v_add_u32_e32 v93, s42, v137
	ds_read_b128 v[238:241], v139 offset:19456
	ds_read_b128 v[242:245], v139 offset:21504
	ds_read_b128 v[246:249], v139 offset:23552
	ds_read_b128 v[250:253], v139 offset:25600
	ds_read_b128 v[218:221], v91 offset:0
	ds_read_b128 v[222:225], v91 offset:2048
	ds_read_b128 v[226:229], v91 offset:4096
	ds_read_b128 v[230:233], v91 offset:6144
	s_add_i32 s47, s44, s6
	s_add_u32 s30, s30, 0x80
	s_addc_u32 s31, s31, 0
	s_waitcnt lgkmcnt(0)
; #define MU_GLDS_A(buf, kt) do { _Pragma("unroll") for (int i = 0; i < NMU; ++i) \
;         __builtin_amdgcn_global_load_lds((const unsigned*)((const char*)A + aoff[i] + (size_t)(kt) * 128), (PG8_LAS unsigned*)(MU_SA(buf) + wid * 1024 + i * 8192), 16, 0, 0); } while (0)
; #define MU_B_ISSUE(sb, kt) do { const char* kb_ = Bb + (size_t)(kt) * (64 * (size_t)RB); _Pragma("unroll") for (int j = 0; j < 8; ++j) { const char* p_ = kb_ + (size_t)j * RB; \
;         asm volatile("global_load_dwordx2 %0, %1, off" : "=&v"(sb[j]) : "v"(p_) : "memory"); } } while (0)
; #define MU_B_WAIT(sb, N) asm volatile("s_waitcnt vmcnt(%8)" : "+v"(sb[0]), "+v"(sb[1]), "+v"(sb[2]), "+v"(sb[3]), "+v"(sb[4]), "+v"(sb[5]), "+v"(sb[6]), "+v"(sb[7]) : "n"(N) : "memory")
; #define MU_G_LOAD(ga, kt) do { const PG8_LAS f32x4* gk_ = (const PG8_LAS f32x4*)(lds + GAIN_OFF) + 16 * (kt) + 2 * wid; const f32x4 ga_ = gk_[0], gb_ = gk_[1]; \
;         ga[0] = ga_[0]; ga[1] = ga_[1]; ga[2] = ga_[2]; ga[3] = ga_[3]; ga[4] = gb_[0]; ga[5] = gb_[1]; ga[6] = gb_[2]; ga[7] = gb_[3]; } while (0)
; #define MU_COMPUTE(buf) MU_COMPUTE_N(buf, NMU)
; #define MU_END(last) do { if (last) asm volatile("s_waitcnt vmcnt(0)" ::: "memory"); else asm volatile("s_waitcnt vmcnt(8)" ::: "memory"); \
;         asm volatile("s_waitcnt lgkmcnt(0)" ::: "memory"); __builtin_amdgcn_s_barrier(); asm volatile("" ::: "memory"); } while (0)
; template <int MODE>
; __device__ __forceinline__ void moe_unit(PG8_LAS unsigned char* lds, int e, int cb, int slot0  , int nv  , const bf16_t* A, const int* slot_tok,
;                                          const float* W0, const float* W1, bf16_t* OUT, const float* slot_rs  , const int* slot_dst) {
;     ...
;     for (int t = 0; t < nt; t += 2) {
;         if (t + 2 < nt) MU_B_WAIT(s1, 8); else MU_B_WAIT(s1, 0);
;         MU_G_LOAD(g0, t + 1); MU_B_WRITE(s1, 1, g0); __builtin_amdgcn_sched_barrier(0); MU_GLDS_A(1, t + 1); __builtin_amdgcn_sched_barrier(0);
;         if (t + 3 < nt) { MU_B_ISSUE(s1, t + 3); }
;         MU_COMPUTE(0);
;         MU_END(t + 3 >= nt);
;         if (t + 2 < nt) { MU_B_WAIT(s0, 8); MU_G_LOAD(g0, t + 2); MU_B_WRITE(s0, 0, g0); __builtin_amdgcn_sched_barrier(0); MU_GLDS_A(0, t + 2); __builtin_amdgcn_sched_barrier(0); }
;         if (t + 4 < nt) { MU_B_ISSUE(s0, t + 4); }
;         MU_COMPUTE(1);
;         MU_END(t + 4 >= nt);
	v_mfma_f32_16x16x32_bf16 v[78:81], v[238:241], v[218:221], v[78:81]
	v_mfma_f32_16x16x32_bf16 v[74:77], v[242:245], v[218:221], v[74:77]
	v_mfma_f32_16x16x32_bf16 v[70:73], v[246:249], v[218:221], v[70:73]
	v_mfma_f32_16x16x32_bf16 v[66:69], v[250:253], v[218:221], v[66:69]
	ds_read_b128 v[218:221], v93 offset:0
	ds_read_b128 v[142:145], v141 offset:19456
	s_mov_b32 m0, s47
	s_nop 0
	global_load_lds_dwordx4 v86, s[30:31]
	v_mfma_f32_16x16x32_bf16 v[62:65], v[238:241], v[222:225], v[62:65]
	v_mfma_f32_16x16x32_bf16 v[58:61], v[242:245], v[222:225], v[58:61]
	v_mfma_f32_16x16x32_bf16 v[54:57], v[246:249], v[222:225], v[54:57]
	v_mfma_f32_16x16x32_bf16 v[50:53], v[250:253], v[222:225], v[50:53]
	ds_read_b128 v[222:225], v93 offset:2048
	ds_read_b128 v[146:149], v141 offset:21504
	s_add_i32 m0, s47, 0x2000
	s_nop 0
	global_load_lds_dwordx4 v134, s[30:31]
	v_mfma_f32_16x16x32_bf16 v[46:49], v[238:241], v[226:229], v[46:49]
	v_mfma_f32_16x16x32_bf16 v[42:45], v[242:245], v[226:229], v[42:45]
	v_mfma_f32_16x16x32_bf16 v[38:41], v[246:249], v[226:229], v[38:41]
	v_mfma_f32_16x16x32_bf16 v[34:37], v[250:253], v[226:229], v[34:37]
	ds_read_b128 v[226:229], v93 offset:4096
	ds_read_b128 v[150:153], v141 offset:23552
	s_add_i32 m0, s47, 0x4000
	s_nop 0
	global_load_lds_dwordx4 v136, s[30:31]
	v_mfma_f32_16x16x32_bf16 v[18:21], v[238:241], v[230:233], v[18:21]
	v_mfma_f32_16x16x32_bf16 v[22:25], v[242:245], v[230:233], v[22:25]
	v_mfma_f32_16x16x32_bf16 v[26:29], v[246:249], v[230:233], v[26:29]
	v_mfma_f32_16x16x32_bf16 v[30:33], v[250:253], v[230:233], v[30:33]
	ds_read_b128 v[230:233], v93 offset:6144
	ds_read_b128 v[154:157], v141 offset:25600
	s_add_i32 m0, s47, 0x6000
	s_nop 0
	global_load_lds_dwordx4 v138, s[30:31]
	s_add_i32 m0, s47, 0x8000
	s_nop 0
	global_load_lds_dwordx4 v140, s[30:31]
	s_waitcnt lgkmcnt(0)
	s_load_dwordx8 s[20:27], s[28:29], 0x0
	s_add_u32 s28, s28, 0x100
	s_addc_u32 s29, s29, 0
	v_mfma_f32_16x16x32_bf16 v[78:81], v[142:145], v[218:221], v[78:81]
	v_mfma_f32_16x16x32_bf16 v[74:77], v[146:149], v[218:221], v[74:77]
	v_mfma_f32_16x16x32_bf16 v[70:73], v[150:153], v[218:221], v[70:73]
	v_mfma_f32_16x16x32_bf16 v[66:69], v[154:157], v[218:221], v[66:69]
	v_lshl_add_u64 v[132:133], v[132:133], 0, s[40:41]
	global_load_dwordx2 v[186:187], v[132:133], off
	global_load_dwordx2 v[188:189], v[132:133], off offset:2048
	v_mfma_f32_16x16x32_bf16 v[62:65], v[142:145], v[222:225], v[62:65]
	v_mfma_f32_16x16x32_bf16 v[58:61], v[146:149], v[222:225], v[58:61]
	v_mfma_f32_16x16x32_bf16 v[54:57], v[150:153], v[222:225], v[54:57]
	v_mfma_f32_16x16x32_bf16 v[50:53], v[154:157], v[222:225], v[50:53]
	v_lshl_add_u64 v[166:167], v[132:133], 0, s[34:35]
	global_load_dwordx2 v[190:191], v[166:167], off
	global_load_dwordx2 v[192:193], v[166:167], off offset:2048
	v_mfma_f32_16x16x32_bf16 v[46:49], v[142:145], v[226:229], v[46:49]
	v_mfma_f32_16x16x32_bf16 v[42:45], v[146:149], v[226:229], v[42:45]
	v_mfma_f32_16x16x32_bf16 v[38:41], v[150:153], v[226:229], v[38:41]
	v_mfma_f32_16x16x32_bf16 v[34:37], v[154:157], v[226:229], v[34:37]
	v_lshl_add_u64 v[166:167], v[132:133], 0, s[36:37]
	global_load_dwordx2 v[194:195], v[166:167], off
	global_load_dwordx2 v[196:197], v[166:167], off offset:2048
	v_mfma_f32_16x16x32_bf16 v[18:21], v[142:145], v[230:233], v[18:21]
	v_mfma_f32_16x16x32_bf16 v[22:25], v[146:149], v[230:233], v[22:25]
	v_mfma_f32_16x16x32_bf16 v[26:29], v[150:153], v[230:233], v[26:29]
	v_mfma_f32_16x16x32_bf16 v[30:33], v[154:157], v[230:233], v[30:33]
	v_lshl_add_u64 v[166:167], v[132:133], 0, s[38:39]
	global_load_dwordx2 v[198:199], v[166:167], off
	global_load_dwordx2 v[200:201], v[166:167], off offset:2048
	s_waitcnt vmcnt(21)
	s_mov_b32 s47, s42
	s_mov_b32 s42, s43
	s_mov_b32 s43, s44
	s_mov_b32 s44, s47
	s_waitcnt lgkmcnt(0)
	s_barrier
	v_mul_f32_e32 v202, s20, v202
	v_mul_f32_e32 v203, s20, v203
	v_mul_f32_e32 v204, s21, v204
	v_mul_f32_e32 v205, s21, v205
	v_mul_f32_e32 v206, s22, v206
	v_mul_f32_e32 v207, s22, v207
	v_mul_f32_e32 v208, s23, v208
	v_mul_f32_e32 v209, s23, v209
	v_mul_f32_e32 v210, s24, v210
	v_mul_f32_e32 v211, s24, v211
	v_mul_f32_e32 v212, s25, v212
	v_mul_f32_e32 v213, s25, v213
	v_mul_f32_e32 v214, s26, v214
	v_mul_f32_e32 v215, s26, v215
	v_mul_f32_e32 v216, s27, v216
	v_mul_f32_e32 v217, s27, v217
	v_cvt_pk_bf16_f32 v158, v202, v204
	v_cvt_pk_bf16_f32 v159, v206, v208
	v_cvt_pk_bf16_f32 v160, v210, v212
	v_cvt_pk_bf16_f32 v161, v214, v216
	v_cvt_pk_bf16_f32 v162, v203, v205
	v_cvt_pk_bf16_f32 v163, v207, v209
	v_cvt_pk_bf16_f32 v164, v211, v213
	v_cvt_pk_bf16_f32 v165, v215, v217
	ds_write_b128 v1, v[158:161] offset:19456
	ds_write_b128 v1, v[162:165] offset:19584
	v_add_u32_e32 v91, s42, v135
	v_add_u32_e32 v93, s42, v137
	ds_read_b128 v[238:241], v139 offset:0
	ds_read_b128 v[242:245], v139 offset:2048
	ds_read_b128 v[246:249], v139 offset:4096
	ds_read_b128 v[250:253], v139 offset:6144
	ds_read_b128 v[218:221], v91 offset:0
	ds_read_b128 v[222:225], v91 offset:2048
	ds_read_b128 v[226:229], v91 offset:4096
	ds_read_b128 v[230:233], v91 offset:6144
	s_add_i32 s47, s44, s6
	s_add_u32 s30, s30, 0x80
	s_addc_u32 s31, s31, 0
	s_waitcnt lgkmcnt(0)
; #define MU_GLDS_A(buf, kt) do { _Pragma("unroll") for (int i = 0; i < NMU; ++i) \
;         __builtin_amdgcn_global_load_lds((const unsigned*)((const char*)A + aoff[i] + (size_t)(kt) * 128), (PG8_LAS unsigned*)(MU_SA(buf) + wid * 1024 + i * 8192), 16, 0, 0); } while (0)
; #define MU_B_ISSUE(sb, kt) do { const char* kb_ = Bb + (size_t)(kt) * (64 * (size_t)RB); _Pragma("unroll") for (int j = 0; j < 8; ++j) { const char* p_ = kb_ + (size_t)j * RB; \
;         asm volatile("global_load_dwordx2 %0, %1, off" : "=&v"(sb[j]) : "v"(p_) : "memory"); } } while (0)
; #define MU_B_WAIT(sb, N) asm volatile("s_waitcnt vmcnt(%8)" : "+v"(sb[0]), "+v"(sb[1]), "+v"(sb[2]), "+v"(sb[3]), "+v"(sb[4]), "+v"(sb[5]), "+v"(sb[6]), "+v"(sb[7]) : "n"(N) : "memory")
; #define MU_G_LOAD(ga, kt) do { const PG8_LAS f32x4* gk_ = (const PG8_LAS f32x4*)(lds + GAIN_OFF) + 16 * (kt) + 2 * wid; const f32x4 ga_ = gk_[0], gb_ = gk_[1]; \
;         ga[0] = ga_[0]; ga[1] = ga_[1]; ga[2] = ga_[2]; ga[3] = ga_[3]; ga[4] = gb_[0]; ga[5] = gb_[1]; ga[6] = gb_[2]; ga[7] = gb_[3]; } while (0)
; #define MU_COMPUTE(buf) MU_COMPUTE_N(buf, NMU)
; #define MU_END(last) do { if (last) asm volatile("s_waitcnt vmcnt(0)" ::: "memory"); else asm volatile("s_waitcnt vmcnt(8)" ::: "memory"); \
;         asm volatile("s_waitcnt lgkmcnt(0)" ::: "memory"); __builtin_amdgcn_s_barrier(); asm volatile("" ::: "memory"); } while (0)
; template <int MODE>
; __device__ __forceinline__ void moe_unit(PG8_LAS unsigned char* lds, int e, int cb, int slot0  , int nv  , const bf16_t* A, const int* slot_tok,
;                                          const float* W0, const float* W1, bf16_t* OUT, const float* slot_rs  , const int* slot_dst) {
;     ...
;     for (int t = 0; t < nt; t += 2) {
;         if (t + 2 < nt) MU_B_WAIT(s1, 8); else MU_B_WAIT(s1, 0);
;         MU_G_LOAD(g0, t + 1); MU_B_WRITE(s1, 1, g0); __builtin_amdgcn_sched_barrier(0); MU_GLDS_A(1, t + 1); __builtin_amdgcn_sched_barrier(0);
;         if (t + 3 < nt) { MU_B_ISSUE(s1, t + 3); }
;         MU_COMPUTE(0);
;         MU_END(t + 3 >= nt);
;         if (t + 2 < nt) { MU_B_WAIT(s0, 8); MU_G_LOAD(g0, t + 2); MU_B_WRITE(s0, 0, g0); __builtin_amdgcn_sched_barrier(0); MU_GLDS_A(0, t + 2); __builtin_amdgcn_sched_barrier(0); }
;         if (t + 4 < nt) { MU_B_ISSUE(s0, t + 4); }
;         MU_COMPUTE(1);
;         MU_END(t + 4 >= nt);
	v_mfma_f32_16x16x32_bf16 v[78:81], v[238:241], v[218:221], v[78:81]
	v_mfma_f32_16x16x32_bf16 v[74:77], v[242:245], v[218:221], v[74:77]
	v_mfma_f32_16x16x32_bf16 v[70:73], v[246:249], v[218:221], v[70:73]
	v_mfma_f32_16x16x32_bf16 v[66:69], v[250:253], v[218:221], v[66:69]
	ds_read_b128 v[218:221], v93 offset:0
	ds_read_b128 v[142:145], v141 offset:0
	s_mov_b32 m0, s47
	s_nop 0
	global_load_lds_dwordx4 v86, s[30:31]
	v_mfma_f32_16x16x32_bf16 v[62:65], v[238:241], v[222:225], v[62:65]
	v_mfma_f32_16x16x32_bf16 v[58:61], v[242:245], v[222:225], v[58:61]
	v_mfma_f32_16x16x32_bf16 v[54:57], v[246:249], v[222:225], v[54:57]
	v_mfma_f32_16x16x32_bf16 v[50:53], v[250:253], v[222:225], v[50:53]
	ds_read_b128 v[222:225], v93 offset:2048
	ds_read_b128 v[146:149], v141 offset:2048
	s_add_i32 m0, s47, 0x2000
	s_nop 0
	global_load_lds_dwordx4 v134, s[30:31]
	v_mfma_f32_16x16x32_bf16 v[46:49], v[238:241], v[226:229], v[46:49]
	v_mfma_f32_16x16x32_bf16 v[42:45], v[242:245], v[226:229], v[42:45]
	v_mfma_f32_16x16x32_bf16 v[38:41], v[246:249], v[226:229], v[38:41]
	v_mfma_f32_16x16x32_bf16 v[34:37], v[250:253], v[226:229], v[34:37]
	ds_read_b128 v[226:229], v93 offset:4096
	ds_read_b128 v[150:153], v141 offset:4096
	s_add_i32 m0, s47, 0x4000
	s_nop 0
	global_load_lds_dwordx4 v136, s[30:31]
	v_mfma_f32_16x16x32_bf16 v[18:21], v[238:241], v[230:233], v[18:21]
	v_mfma_f32_16x16x32_bf16 v[22:25], v[242:245], v[230:233], v[22:25]
	v_mfma_f32_16x16x32_bf16 v[26:29], v[246:249], v[230:233], v[26:29]
	v_mfma_f32_16x16x32_bf16 v[30:33], v[250:253], v[230:233], v[30:33]
	ds_read_b128 v[230:233], v93 offset:6144
	ds_read_b128 v[154:157], v141 offset:6144
	s_add_i32 m0, s47, 0x6000
	s_nop 0
	global_load_lds_dwordx4 v138, s[30:31]
	s_add_i32 m0, s47, 0x8000
	s_nop 0
	global_load_lds_dwordx4 v140, s[30:31]
	s_waitcnt lgkmcnt(0)
	s_load_dwordx8 s[12:19], s[28:29], 0x0
	s_add_u32 s28, s28, 0x100
	s_addc_u32 s29, s29, 0
	v_mfma_f32_16x16x32_bf16 v[78:81], v[142:145], v[218:221], v[78:81]
	v_mfma_f32_16x16x32_bf16 v[74:77], v[146:149], v[218:221], v[74:77]
	v_mfma_f32_16x16x32_bf16 v[70:73], v[150:153], v[218:221], v[70:73]
	v_mfma_f32_16x16x32_bf16 v[66:69], v[154:157], v[218:221], v[66:69]
	v_lshl_add_u64 v[132:133], v[132:133], 0, s[40:41]
	global_load_dwordx2 v[202:203], v[132:133], off
	global_load_dwordx2 v[204:205], v[132:133], off offset:2048
	v_mfma_f32_16x16x32_bf16 v[62:65], v[142:145], v[222:225], v[62:65]
	v_mfma_f32_16x16x32_bf16 v[58:61], v[146:149], v[222:225], v[58:61]
	v_mfma_f32_16x16x32_bf16 v[54:57], v[150:153], v[222:225], v[54:57]
	v_mfma_f32_16x16x32_bf16 v[50:53], v[154:157], v[222:225], v[50:53]
	v_lshl_add_u64 v[166:167], v[132:133], 0, s[34:35]
	global_load_dwordx2 v[206:207], v[166:167], off
	global_load_dwordx2 v[208:209], v[166:167], off offset:2048
	v_mfma_f32_16x16x32_bf16 v[46:49], v[142:145], v[226:229], v[46:49]
	v_mfma_f32_16x16x32_bf16 v[42:45], v[146:149], v[226:229], v[42:45]
	v_mfma_f32_16x16x32_bf16 v[38:41], v[150:153], v[226:229], v[38:41]
	v_mfma_f32_16x16x32_bf16 v[34:37], v[154:157], v[226:229], v[34:37]
	v_lshl_add_u64 v[166:167], v[132:133], 0, s[36:37]
	global_load_dwordx2 v[210:211], v[166:167], off
	global_load_dwordx2 v[212:213], v[166:167], off offset:2048
	v_mfma_f32_16x16x32_bf16 v[18:21], v[142:145], v[230:233], v[18:21]
	v_mfma_f32_16x16x32_bf16 v[22:25], v[146:149], v[230:233], v[22:25]
	v_mfma_f32_16x16x32_bf16 v[26:29], v[150:153], v[230:233], v[26:29]
	v_mfma_f32_16x16x32_bf16 v[30:33], v[154:157], v[230:233], v[30:33]
	v_lshl_add_u64 v[166:167], v[132:133], 0, s[38:39]
	global_load_dwordx2 v[214:215], v[166:167], off
	global_load_dwordx2 v[216:217], v[166:167], off offset:2048
	s_waitcnt vmcnt(21)
	s_mov_b32 s47, s42
	s_mov_b32 s42, s43
	s_mov_b32 s43, s44
	s_mov_b32 s44, s47
	s_waitcnt lgkmcnt(0)
	s_barrier
	v_mul_f32_e32 v98, s12, v98
	v_mul_f32_e32 v99, s12, v99
	v_mul_f32_e32 v100, s13, v100
	v_mul_f32_e32 v101, s13, v101
	v_mul_f32_e32 v102, s14, v102
	v_mul_f32_e32 v103, s14, v103
	v_mul_f32_e32 v104, s15, v104
	v_mul_f32_e32 v105, s15, v105
	v_mul_f32_e32 v106, s16, v106
	v_mul_f32_e32 v107, s16, v107
	v_mul_f32_e32 v108, s17, v108
	v_mul_f32_e32 v109, s17, v109
	v_mul_f32_e32 v110, s18, v110
	v_mul_f32_e32 v111, s18, v111
	v_mul_f32_e32 v112, s19, v112
	v_mul_f32_e32 v113, s19, v113
	v_cvt_pk_bf16_f32 v158, v98, v100
	v_cvt_pk_bf16_f32 v159, v102, v104
	v_cvt_pk_bf16_f32 v160, v106, v108
	v_cvt_pk_bf16_f32 v161, v110, v112
	v_cvt_pk_bf16_f32 v162, v99, v101
	v_cvt_pk_bf16_f32 v163, v103, v105
	v_cvt_pk_bf16_f32 v164, v107, v109
	v_cvt_pk_bf16_f32 v165, v111, v113
	ds_write_b128 v1, v[158:161] offset:0
	ds_write_b128 v1, v[162:165] offset:128
	v_add_u32_e32 v91, s42, v135
	v_add_u32_e32 v93, s42, v137
	ds_read_b128 v[238:241], v139 offset:19456
	ds_read_b128 v[242:245], v139 offset:21504
	ds_read_b128 v[246:249], v139 offset:23552
	ds_read_b128 v[250:253], v139 offset:25600
	ds_read_b128 v[218:221], v91 offset:0
	ds_read_b128 v[222:225], v91 offset:2048
	ds_read_b128 v[226:229], v91 offset:4096
	ds_read_b128 v[230:233], v91 offset:6144
	s_add_i32 s47, s44, s6
	s_add_u32 s30, s30, 0x80
	s_addc_u32 s31, s31, 0
	s_waitcnt lgkmcnt(0)
; #define MU_GLDS_A(buf, kt) do { _Pragma("unroll") for (int i = 0; i < NMU; ++i) \
;         __builtin_amdgcn_global_load_lds((const unsigned*)((const char*)A + aoff[i] + (size_t)(kt) * 128), (PG8_LAS unsigned*)(MU_SA(buf) + wid * 1024 + i * 8192), 16, 0, 0); } while (0)
; #define MU_B_ISSUE(sb, kt) do { const char* kb_ = Bb + (size_t)(kt) * (64 * (size_t)RB); _Pragma("unroll") for (int j = 0; j < 8; ++j) { const char* p_ = kb_ + (size_t)j * RB; \
;         asm volatile("global_load_dwordx2 %0, %1, off" : "=&v"(sb[j]) : "v"(p_) : "memory"); } } while (0)
; #define MU_B_WAIT(sb, N) asm volatile("s_waitcnt vmcnt(%8)" : "+v"(sb[0]), "+v"(sb[1]), "+v"(sb[2]), "+v"(sb[3]), "+v"(sb[4]), "+v"(sb[5]), "+v"(sb[6]), "+v"(sb[7]) : "n"(N) : "memory")
; #define MU_G_LOAD(ga, kt) do { const PG8_LAS f32x4* gk_ = (const PG8_LAS f32x4*)(lds + GAIN_OFF) + 16 * (kt) + 2 * wid; const f32x4 ga_ = gk_[0], gb_ = gk_[1]; \
;         ga[0] = ga_[0]; ga[1] = ga_[1]; ga[2] = ga_[2]; ga[3] = ga_[3]; ga[4] = gb_[0]; ga[5] = gb_[1]; ga[6] = gb_[2]; ga[7] = gb_[3]; } while (0)
; #define MU_COMPUTE(buf) MU_COMPUTE_N(buf, NMU)
; #define MU_END(last) do { if (last) asm volatile("s_waitcnt vmcnt(0)" ::: "memory"); else asm volatile("s_waitcnt vmcnt(8)" ::: "memory"); \
;         asm volatile("s_waitcnt lgkmcnt(0)" ::: "memory"); __builtin_amdgcn_s_barrier(); asm volatile("" ::: "memory"); } while (0)
; template <int MODE>
; __device__ __forceinline__ void moe_unit(PG8_LAS unsigned char* lds, int e, int cb, int slot0  , int nv  , const bf16_t* A, const int* slot_tok,
;                                          const float* W0, const float* W1, bf16_t* OUT, const float* slot_rs  , const int* slot_dst) {
;     ...
;     for (int t = 0; t < nt; t += 2) {
;         if (t + 2 < nt) MU_B_WAIT(s1, 8); else MU_B_WAIT(s1, 0);
;         MU_G_LOAD(g0, t + 1); MU_B_WRITE(s1, 1, g0); __builtin_amdgcn_sched_barrier(0); MU_GLDS_A(1, t + 1); __builtin_amdgcn_sched_barrier(0);
;         if (t + 3 < nt) { MU_B_ISSUE(s1, t + 3); }
;         MU_COMPUTE(0);
;         MU_END(t + 3 >= nt);
;         if (t + 2 < nt) { MU_B_WAIT(s0, 8); MU_G_LOAD(g0, t + 2); MU_B_WRITE(s0, 0, g0); __builtin_amdgcn_sched_barrier(0); MU_GLDS_A(0, t + 2); __builtin_amdgcn_sched_barrier(0); }
;         if (t + 4 < nt) { MU_B_ISSUE(s0, t + 4); }
;         MU_COMPUTE(1);
;         MU_END(t + 4 >= nt);
	v_mfma_f32_16x16x32_bf16 v[78:81], v[238:241], v[218:221], v[78:81]
	v_mfma_f32_16x16x32_bf16 v[74:77], v[242:245], v[218:221], v[74:77]
	v_mfma_f32_16x16x32_bf16 v[70:73], v[246:249], v[218:221], v[70:73]
	v_mfma_f32_16x16x32_bf16 v[66:69], v[250:253], v[218:221], v[66:69]
	ds_read_b128 v[218:221], v93 offset:0
	ds_read_b128 v[142:145], v141 offset:19456
	s_mov_b32 m0, s47
	s_nop 0
	global_load_lds_dwordx4 v86, s[30:31]
	v_mfma_f32_16x16x32_bf16 v[62:65], v[238:241], v[222:225], v[62:65]
	v_mfma_f32_16x16x32_bf16 v[58:61], v[242:245], v[222:225], v[58:61]
	v_mfma_f32_16x16x32_bf16 v[54:57], v[246:249], v[222:225], v[54:57]
	v_mfma_f32_16x16x32_bf16 v[50:53], v[250:253], v[222:225], v[50:53]
	ds_read_b128 v[222:225], v93 offset:2048
	ds_read_b128 v[146:149], v141 offset:21504
	s_add_i32 m0, s47, 0x2000
	s_nop 0
	global_load_lds_dwordx4 v134, s[30:31]
	v_mfma_f32_16x16x32_bf16 v[46:49], v[238:241], v[226:229], v[46:49]
	v_mfma_f32_16x16x32_bf16 v[42:45], v[242:245], v[226:229], v[42:45]
	v_mfma_f32_16x16x32_bf16 v[38:41], v[246:249], v[226:229], v[38:41]
	v_mfma_f32_16x16x32_bf16 v[34:37], v[250:253], v[226:229], v[34:37]
	ds_read_b128 v[226:229], v93 offset:4096
	ds_read_b128 v[150:153], v141 offset:23552
	s_add_i32 m0, s47, 0x4000
	s_nop 0
	global_load_lds_dwordx4 v136, s[30:31]
	v_mfma_f32_16x16x32_bf16 v[18:21], v[238:241], v[230:233], v[18:21]
	v_mfma_f32_16x16x32_bf16 v[22:25], v[242:245], v[230:233], v[22:25]
	v_mfma_f32_16x16x32_bf16 v[26:29], v[246:249], v[230:233], v[26:29]
	v_mfma_f32_16x16x32_bf16 v[30:33], v[250:253], v[230:233], v[30:33]
	ds_read_b128 v[230:233], v93 offset:6144
	ds_read_b128 v[154:157], v141 offset:25600
	s_add_i32 m0, s47, 0x6000
	s_nop 0
	global_load_lds_dwordx4 v138, s[30:31]
	s_add_i32 m0, s47, 0x8000
	s_nop 0
	global_load_lds_dwordx4 v140, s[30:31]
	s_waitcnt lgkmcnt(0)
	s_load_dwordx8 s[20:27], s[28:29], 0x0
	s_add_u32 s28, s28, 0x100
	s_addc_u32 s29, s29, 0
	v_mfma_f32_16x16x32_bf16 v[78:81], v[142:145], v[218:221], v[78:81]
	v_mfma_f32_16x16x32_bf16 v[74:77], v[146:149], v[218:221], v[74:77]
	v_mfma_f32_16x16x32_bf16 v[70:73], v[150:153], v[218:221], v[70:73]
	v_mfma_f32_16x16x32_bf16 v[66:69], v[154:157], v[218:221], v[66:69]
	v_lshl_add_u64 v[132:133], v[132:133], 0, s[40:41]
	global_load_dwordx2 v[98:99], v[132:133], off
	global_load_dwordx2 v[100:101], v[132:133], off offset:2048
	v_mfma_f32_16x16x32_bf16 v[62:65], v[142:145], v[222:225], v[62:65]
	v_mfma_f32_16x16x32_bf16 v[58:61], v[146:149], v[222:225], v[58:61]
	v_mfma_f32_16x16x32_bf16 v[54:57], v[150:153], v[222:225], v[54:57]
	v_mfma_f32_16x16x32_bf16 v[50:53], v[154:157], v[222:225], v[50:53]
	v_lshl_add_u64 v[166:167], v[132:133], 0, s[34:35]
	global_load_dwordx2 v[102:103], v[166:167], off
	global_load_dwordx2 v[104:105], v[166:167], off offset:2048
	v_mfma_f32_16x16x32_bf16 v[46:49], v[142:145], v[226:229], v[46:49]
	v_mfma_f32_16x16x32_bf16 v[42:45], v[146:149], v[226:229], v[42:45]
	v_mfma_f32_16x16x32_bf16 v[38:41], v[150:153], v[226:229], v[38:41]
	v_mfma_f32_16x16x32_bf16 v[34:37], v[154:157], v[226:229], v[34:37]
	v_lshl_add_u64 v[166:167], v[132:133], 0, s[36:37]
	global_load_dwordx2 v[106:107], v[166:167], off
	global_load_dwordx2 v[108:109], v[166:167], off offset:2048
	v_mfma_f32_16x16x32_bf16 v[18:21], v[142:145], v[230:233], v[18:21]
	v_mfma_f32_16x16x32_bf16 v[22:25], v[146:149], v[230:233], v[22:25]
	v_mfma_f32_16x16x32_bf16 v[26:29], v[150:153], v[230:233], v[26:29]
	v_mfma_f32_16x16x32_bf16 v[30:33], v[154:157], v[230:233], v[30:33]
	v_lshl_add_u64 v[166:167], v[132:133], 0, s[38:39]
	global_load_dwordx2 v[110:111], v[166:167], off
	global_load_dwordx2 v[112:113], v[166:167], off offset:2048
	s_waitcnt vmcnt(21)
	s_mov_b32 s47, s42
	s_mov_b32 s42, s43
	s_mov_b32 s43, s44
	s_mov_b32 s44, s47
	s_waitcnt lgkmcnt(0)
	s_barrier
	s_sub_u32 s46, s46, 1
	s_cmp_lg_u32 s46, 0
	s_cbranch_scc1 .Lmu_loop_X4
	v_mul_f32_e32 v114, s20, v114
	v_mul_f32_e32 v115, s20, v115
	v_mul_f32_e32 v116, s21, v116
	v_mul_f32_e32 v117, s21, v117
	v_mul_f32_e32 v118, s22, v118
	v_mul_f32_e32 v119, s22, v119
	v_mul_f32_e32 v120, s23, v120
	v_mul_f32_e32 v121, s23, v121
	v_mul_f32_e32 v122, s24, v122
	v_mul_f32_e32 v123, s24, v123
	v_mul_f32_e32 v124, s25, v124
	v_mul_f32_e32 v125, s25, v125
	v_mul_f32_e32 v126, s26, v126
	v_mul_f32_e32 v127, s26, v127
	v_mul_f32_e32 v128, s27, v128
	v_mul_f32_e32 v129, s27, v129
	v_cvt_pk_bf16_f32 v158, v114, v116
	v_cvt_pk_bf16_f32 v159, v118, v120
	v_cvt_pk_bf16_f32 v160, v122, v124
	v_cvt_pk_bf16_f32 v161, v126, v128
	v_cvt_pk_bf16_f32 v162, v115, v117
	v_cvt_pk_bf16_f32 v163, v119, v121
	v_cvt_pk_bf16_f32 v164, v123, v125
	v_cvt_pk_bf16_f32 v165, v127, v129
	ds_write_b128 v1, v[158:161] offset:19456
	ds_write_b128 v1, v[162:165] offset:19584
	v_add_u32_e32 v91, s42, v135
	v_add_u32_e32 v93, s42, v137
	ds_read_b128 v[238:241], v139 offset:0
	ds_read_b128 v[242:245], v139 offset:2048
	ds_read_b128 v[246:249], v139 offset:4096
	ds_read_b128 v[250:253], v139 offset:6144
	ds_read_b128 v[218:221], v91 offset:0
	ds_read_b128 v[222:225], v91 offset:2048
	ds_read_b128 v[226:229], v91 offset:4096
	ds_read_b128 v[230:233], v91 offset:6144
	s_add_i32 s47, s44, s6
	s_add_u32 s30, s30, 0x80
	s_addc_u32 s31, s31, 0
	s_waitcnt lgkmcnt(0)
; #define MU_GLDS_A(buf, kt) do { _Pragma("unroll") for (int i = 0; i < NMU; ++i) \
;         __builtin_amdgcn_global_load_lds((const unsigned*)((const char*)A + aoff[i] + (size_t)(kt) * 128), (PG8_LAS unsigned*)(MU_SA(buf) + wid * 1024 + i * 8192), 16, 0, 0); } while (0)
; #define MU_B_ISSUE(sb, kt) do { const char* kb_ = Bb + (size_t)(kt) * (64 * (size_t)RB); _Pragma("unroll") for (int j = 0; j < 8; ++j) { const char* p_ = kb_ + (size_t)j * RB; \
;         asm volatile("global_load_dwordx2 %0, %1, off" : "=&v"(sb[j]) : "v"(p_) : "memory"); } } while (0)
; #define MU_B_WAIT(sb, N) asm volatile("s_waitcnt vmcnt(%8)" : "+v"(sb[0]), "+v"(sb[1]), "+v"(sb[2]), "+v"(sb[3]), "+v"(sb[4]), "+v"(sb[5]), "+v"(sb[6]), "+v"(sb[7]) : "n"(N) : "memory")
; #define MU_G_LOAD(ga, kt) do { const PG8_LAS f32x4* gk_ = (const PG8_LAS f32x4*)(lds + GAIN_OFF) + 16 * (kt) + 2 * wid; const f32x4 ga_ = gk_[0], gb_ = gk_[1]; \
;         ga[0] = ga_[0]; ga[1] = ga_[1]; ga[2] = ga_[2]; ga[3] = ga_[3]; ga[4] = gb_[0]; ga[5] = gb_[1]; ga[6] = gb_[2]; ga[7] = gb_[3]; } while (0)
; #define MU_COMPUTE(buf) MU_COMPUTE_N(buf, NMU)
; #define MU_END(last) do { if (last) asm volatile("s_waitcnt vmcnt(0)" ::: "memory"); else asm volatile("s_waitcnt vmcnt(8)" ::: "memory"); \
;         asm volatile("s_waitcnt lgkmcnt(0)" ::: "memory"); __builtin_amdgcn_s_barrier(); asm volatile("" ::: "memory"); } while (0)
; template <int MODE>
; __device__ __forceinline__ void moe_unit(PG8_LAS unsigned char* lds, int e, int cb, int slot0  , int nv  , const bf16_t* A, const int* slot_tok,
;                                          const float* W0, const float* W1, bf16_t* OUT, const float* slot_rs  , const int* slot_dst) {
;     ...
;     for (int t = 0; t < nt; t += 2) {
;         if (t + 2 < nt) MU_B_WAIT(s1, 8); else MU_B_WAIT(s1, 0);
;         MU_G_LOAD(g0, t + 1); MU_B_WRITE(s1, 1, g0); __builtin_amdgcn_sched_barrier(0); MU_GLDS_A(1, t + 1); __builtin_amdgcn_sched_barrier(0);
;         if (t + 3 < nt) { MU_B_ISSUE(s1, t + 3); }
;         MU_COMPUTE(0);
;         MU_END(t + 3 >= nt);
;         if (t + 2 < nt) { MU_B_WAIT(s0, 8); MU_G_LOAD(g0, t + 2); MU_B_WRITE(s0, 0, g0); __builtin_amdgcn_sched_barrier(0); MU_GLDS_A(0, t + 2); __builtin_amdgcn_sched_barrier(0); }
;         if (t + 4 < nt) { MU_B_ISSUE(s0, t + 4); }
;         MU_COMPUTE(1);
;         MU_END(t + 4 >= nt);
	v_mfma_f32_16x16x32_bf16 v[78:81], v[238:241], v[218:221], v[78:81]
	v_mfma_f32_16x16x32_bf16 v[74:77], v[242:245], v[218:221], v[74:77]
	v_mfma_f32_16x16x32_bf16 v[70:73], v[246:249], v[218:221], v[70:73]
	v_mfma_f32_16x16x32_bf16 v[66:69], v[250:253], v[218:221], v[66:69]
	ds_read_b128 v[218:221], v93 offset:0
	ds_read_b128 v[142:145], v141 offset:0
	s_mov_b32 m0, s47
	s_nop 0
	global_load_lds_dwordx4 v86, s[30:31]
	v_mfma_f32_16x16x32_bf16 v[62:65], v[238:241], v[222:225], v[62:65]
	v_mfma_f32_16x16x32_bf16 v[58:61], v[242:245], v[222:225], v[58:61]
	v_mfma_f32_16x16x32_bf16 v[54:57], v[246:249], v[222:225], v[54:57]
	v_mfma_f32_16x16x32_bf16 v[50:53], v[250:253], v[222:225], v[50:53]
	ds_read_b128 v[222:225], v93 offset:2048
	ds_read_b128 v[146:149], v141 offset:2048
	s_add_i32 m0, s47, 0x2000
	s_nop 0
	global_load_lds_dwordx4 v134, s[30:31]
	v_mfma_f32_16x16x32_bf16 v[46:49], v[238:241], v[226:229], v[46:49]
	v_mfma_f32_16x16x32_bf16 v[42:45], v[242:245], v[226:229], v[42:45]
	v_mfma_f32_16x16x32_bf16 v[38:41], v[246:249], v[226:229], v[38:41]
	v_mfma_f32_16x16x32_bf16 v[34:37], v[250:253], v[226:229], v[34:37]
	ds_read_b128 v[226:229], v93 offset:4096
	ds_read_b128 v[150:153], v141 offset:4096
	s_add_i32 m0, s47, 0x4000
	s_nop 0
	global_load_lds_dwordx4 v136, s[30:31]
	v_mfma_f32_16x16x32_bf16 v[18:21], v[238:241], v[230:233], v[18:21]
	v_mfma_f32_16x16x32_bf16 v[22:25], v[242:245], v[230:233], v[22:25]
	v_mfma_f32_16x16x32_bf16 v[26:29], v[246:249], v[230:233], v[26:29]
	v_mfma_f32_16x16x32_bf16 v[30:33], v[250:253], v[230:233], v[30:33]
	ds_read_b128 v[230:233], v93 offset:6144
	ds_read_b128 v[154:157], v141 offset:6144
	s_add_i32 m0, s47, 0x6000
	s_nop 0
	global_load_lds_dwordx4 v138, s[30:31]
	s_add_i32 m0, s47, 0x8000
	s_nop 0
	global_load_lds_dwordx4 v140, s[30:31]
	s_waitcnt lgkmcnt(0)
	s_load_dwordx8 s[12:19], s[28:29], 0x0
	s_add_u32 s28, s28, 0x100
	s_addc_u32 s29, s29, 0
	v_mfma_f32_16x16x32_bf16 v[78:81], v[142:145], v[218:221], v[78:81]
	v_mfma_f32_16x16x32_bf16 v[74:77], v[146:149], v[218:221], v[74:77]
	v_mfma_f32_16x16x32_bf16 v[70:73], v[150:153], v[218:221], v[70:73]
	v_mfma_f32_16x16x32_bf16 v[66:69], v[154:157], v[218:221], v[66:69]
	v_lshl_add_u64 v[132:133], v[132:133], 0, s[40:41]
	global_load_dwordx2 v[114:115], v[132:133], off
	global_load_dwordx2 v[116:117], v[132:133], off offset:2048
	v_mfma_f32_16x16x32_bf16 v[62:65], v[142:145], v[222:225], v[62:65]
	v_mfma_f32_16x16x32_bf16 v[58:61], v[146:149], v[222:225], v[58:61]
	v_mfma_f32_16x16x32_bf16 v[54:57], v[150:153], v[222:225], v[54:57]
	v_mfma_f32_16x16x32_bf16 v[50:53], v[154:157], v[222:225], v[50:53]
	v_lshl_add_u64 v[166:167], v[132:133], 0, s[34:35]
	global_load_dwordx2 v[118:119], v[166:167], off
	global_load_dwordx2 v[120:121], v[166:167], off offset:2048
	v_mfma_f32_16x16x32_bf16 v[46:49], v[142:145], v[226:229], v[46:49]
	v_mfma_f32_16x16x32_bf16 v[42:45], v[146:149], v[226:229], v[42:45]
	v_mfma_f32_16x16x32_bf16 v[38:41], v[150:153], v[226:229], v[38:41]
	v_mfma_f32_16x16x32_bf16 v[34:37], v[154:157], v[226:229], v[34:37]
	v_lshl_add_u64 v[166:167], v[132:133], 0, s[36:37]
	global_load_dwordx2 v[122:123], v[166:167], off
	global_load_dwordx2 v[124:125], v[166:167], off offset:2048
	v_mfma_f32_16x16x32_bf16 v[18:21], v[142:145], v[230:233], v[18:21]
	v_mfma_f32_16x16x32_bf16 v[22:25], v[146:149], v[230:233], v[22:25]
	v_mfma_f32_16x16x32_bf16 v[26:29], v[150:153], v[230:233], v[26:29]
	v_mfma_f32_16x16x32_bf16 v[30:33], v[154:157], v[230:233], v[30:33]
	v_lshl_add_u64 v[166:167], v[132:133], 0, s[38:39]
	global_load_dwordx2 v[126:127], v[166:167], off
	global_load_dwordx2 v[128:129], v[166:167], off offset:2048
	s_waitcnt vmcnt(21)
	s_mov_b32 s47, s42
	s_mov_b32 s42, s43
	s_mov_b32 s43, s44
	s_mov_b32 s44, s47
	s_waitcnt lgkmcnt(0)
	s_barrier
	v_mul_f32_e32 v186, s12, v186
	v_mul_f32_e32 v187, s12, v187
	v_mul_f32_e32 v188, s13, v188
	v_mul_f32_e32 v189, s13, v189
	v_mul_f32_e32 v190, s14, v190
	v_mul_f32_e32 v191, s14, v191
	v_mul_f32_e32 v192, s15, v192
	v_mul_f32_e32 v193, s15, v193
	v_mul_f32_e32 v194, s16, v194
	v_mul_f32_e32 v195, s16, v195
	v_mul_f32_e32 v196, s17, v196
	v_mul_f32_e32 v197, s17, v197
	v_mul_f32_e32 v198, s18, v198
	v_mul_f32_e32 v199, s18, v199
	v_mul_f32_e32 v200, s19, v200
	v_mul_f32_e32 v201, s19, v201
	v_cvt_pk_bf16_f32 v158, v186, v188
	v_cvt_pk_bf16_f32 v159, v190, v192
	v_cvt_pk_bf16_f32 v160, v194, v196
	v_cvt_pk_bf16_f32 v161, v198, v200
	v_cvt_pk_bf16_f32 v162, v187, v189
	v_cvt_pk_bf16_f32 v163, v191, v193
	v_cvt_pk_bf16_f32 v164, v195, v197
	v_cvt_pk_bf16_f32 v165, v199, v201
	ds_write_b128 v1, v[158:161] offset:0
	ds_write_b128 v1, v[162:165] offset:128
	v_add_u32_e32 v91, s42, v135
	v_add_u32_e32 v93, s42, v137
	ds_read_b128 v[238:241], v139 offset:19456
	ds_read_b128 v[242:245], v139 offset:21504
	ds_read_b128 v[246:249], v139 offset:23552
	ds_read_b128 v[250:253], v139 offset:25600
	ds_read_b128 v[218:221], v91 offset:0
	ds_read_b128 v[222:225], v91 offset:2048
	ds_read_b128 v[226:229], v91 offset:4096
	ds_read_b128 v[230:233], v91 offset:6144
	s_add_i32 s47, s44, s6
	s_add_u32 s30, s30, 0x80
	s_addc_u32 s31, s31, 0
	s_waitcnt lgkmcnt(0)
; #define MU_GLDS_A(buf, kt) do { _Pragma("unroll") for (int i = 0; i < NMU; ++i) \
;         __builtin_amdgcn_global_load_lds((const unsigned*)((const char*)A + aoff[i] + (size_t)(kt) * 128), (PG8_LAS unsigned*)(MU_SA(buf) + wid * 1024 + i * 8192), 16, 0, 0); } while (0)
; #define MU_B_ISSUE(sb, kt) do { const char* kb_ = Bb + (size_t)(kt) * (64 * (size_t)RB); _Pragma("unroll") for (int j = 0; j < 8; ++j) { const char* p_ = kb_ + (size_t)j * RB; \
;         asm volatile("global_load_dwordx2 %0, %1, off" : "=&v"(sb[j]) : "v"(p_) : "memory"); } } while (0)
; #define MU_B_WAIT(sb, N) asm volatile("s_waitcnt vmcnt(%8)" : "+v"(sb[0]), "+v"(sb[1]), "+v"(sb[2]), "+v"(sb[3]), "+v"(sb[4]), "+v"(sb[5]), "+v"(sb[6]), "+v"(sb[7]) : "n"(N) : "memory")
; #define MU_G_LOAD(ga, kt) do { const PG8_LAS f32x4* gk_ = (const PG8_LAS f32x4*)(lds + GAIN_OFF) + 16 * (kt) + 2 * wid; const f32x4 ga_ = gk_[0], gb_ = gk_[1]; \
;         ga[0] = ga_[0]; ga[1] = ga_[1]; ga[2] = ga_[2]; ga[3] = ga_[3]; ga[4] = gb_[0]; ga[5] = gb_[1]; ga[6] = gb_[2]; ga[7] = gb_[3]; } while (0)
; #define MU_COMPUTE(buf) MU_COMPUTE_N(buf, NMU)
; #define MU_END(last) do { if (last) asm volatile("s_waitcnt vmcnt(0)" ::: "memory"); else asm volatile("s_waitcnt vmcnt(8)" ::: "memory"); \
;         asm volatile("s_waitcnt lgkmcnt(0)" ::: "memory"); __builtin_amdgcn_s_barrier(); asm volatile("" ::: "memory"); } while (0)
; template <int MODE>
; __device__ __forceinline__ void moe_unit(PG8_LAS unsigned char* lds, int e, int cb, int slot0  , int nv  , const bf16_t* A, const int* slot_tok,
;                                          const float* W0, const float* W1, bf16_t* OUT, const float* slot_rs  , const int* slot_dst) {
;     ...
;     for (int t = 0; t < nt; t += 2) {
;         if (t + 2 < nt) MU_B_WAIT(s1, 8); else MU_B_WAIT(s1, 0);
;         MU_G_LOAD(g0, t + 1); MU_B_WRITE(s1, 1, g0); __builtin_amdgcn_sched_barrier(0); MU_GLDS_A(1, t + 1); __builtin_amdgcn_sched_barrier(0);
;         if (t + 3 < nt) { MU_B_ISSUE(s1, t + 3); }
;         MU_COMPUTE(0);
;         MU_END(t + 3 >= nt);
;         if (t + 2 < nt) { MU_B_WAIT(s0, 8); MU_G_LOAD(g0, t + 2); MU_B_WRITE(s0, 0, g0); __builtin_amdgcn_sched_barrier(0); MU_GLDS_A(0, t + 2); __builtin_amdgcn_sched_barrier(0); }
;         if (t + 4 < nt) { MU_B_ISSUE(s0, t + 4); }
;         MU_COMPUTE(1);
;         MU_END(t + 4 >= nt);
	v_mfma_f32_16x16x32_bf16 v[78:81], v[238:241], v[218:221], v[78:81]
	v_mfma_f32_16x16x32_bf16 v[74:77], v[242:245], v[218:221], v[74:77]
	v_mfma_f32_16x16x32_bf16 v[70:73], v[246:249], v[218:221], v[70:73]
	v_mfma_f32_16x16x32_bf16 v[66:69], v[250:253], v[218:221], v[66:69]
	ds_read_b128 v[218:221], v93 offset:0
	ds_read_b128 v[142:145], v141 offset:19456
	s_mov_b32 m0, s47
	s_nop 0
	global_load_lds_dwordx4 v86, s[30:31]
	v_mfma_f32_16x16x32_bf16 v[62:65], v[238:241], v[222:225], v[62:65]
	v_mfma_f32_16x16x32_bf16 v[58:61], v[242:245], v[222:225], v[58:61]
	v_mfma_f32_16x16x32_bf16 v[54:57], v[246:249], v[222:225], v[54:57]
	v_mfma_f32_16x16x32_bf16 v[50:53], v[250:253], v[222:225], v[50:53]
	ds_read_b128 v[222:225], v93 offset:2048
	ds_read_b128 v[146:149], v141 offset:21504
	s_add_i32 m0, s47, 0x2000
	s_nop 0
	global_load_lds_dwordx4 v134, s[30:31]
	v_mfma_f32_16x16x32_bf16 v[46:49], v[238:241], v[226:229], v[46:49]
	v_mfma_f32_16x16x32_bf16 v[42:45], v[242:245], v[226:229], v[42:45]
	v_mfma_f32_16x16x32_bf16 v[38:41], v[246:249], v[226:229], v[38:41]
	v_mfma_f32_16x16x32_bf16 v[34:37], v[250:253], v[226:229], v[34:37]
	ds_read_b128 v[226:229], v93 offset:4096
	ds_read_b128 v[150:153], v141 offset:23552
	s_add_i32 m0, s47, 0x4000
	s_nop 0
	global_load_lds_dwordx4 v136, s[30:31]
	v_mfma_f32_16x16x32_bf16 v[18:21], v[238:241], v[230:233], v[18:21]
	v_mfma_f32_16x16x32_bf16 v[22:25], v[242:245], v[230:233], v[22:25]
	v_mfma_f32_16x16x32_bf16 v[26:29], v[246:249], v[230:233], v[26:29]
	v_mfma_f32_16x16x32_bf16 v[30:33], v[250:253], v[230:233], v[30:33]
	ds_read_b128 v[230:233], v93 offset:6144
	ds_read_b128 v[154:157], v141 offset:25600
	s_add_i32 m0, s47, 0x6000
	s_nop 0
	global_load_lds_dwordx4 v138, s[30:31]
	s_add_i32 m0, s47, 0x8000
	s_nop 0
	global_load_lds_dwordx4 v140, s[30:31]
	s_waitcnt lgkmcnt(0)
	s_load_dwordx8 s[20:27], s[28:29], 0x0
	s_add_u32 s28, s28, 0x100
	s_addc_u32 s29, s29, 0
	v_mfma_f32_16x16x32_bf16 v[78:81], v[142:145], v[218:221], v[78:81]
	v_mfma_f32_16x16x32_bf16 v[74:77], v[146:149], v[218:221], v[74:77]
	v_mfma_f32_16x16x32_bf16 v[70:73], v[150:153], v[218:221], v[70:73]
	v_mfma_f32_16x16x32_bf16 v[66:69], v[154:157], v[218:221], v[66:69]
	v_lshl_add_u64 v[132:133], v[132:133], 0, s[40:41]
	global_load_dwordx2 v[186:187], v[132:133], off
	global_load_dwordx2 v[188:189], v[132:133], off offset:2048
	v_mfma_f32_16x16x32_bf16 v[62:65], v[142:145], v[222:225], v[62:65]
	v_mfma_f32_16x16x32_bf16 v[58:61], v[146:149], v[222:225], v[58:61]
	v_mfma_f32_16x16x32_bf16 v[54:57], v[150:153], v[222:225], v[54:57]
	v_mfma_f32_16x16x32_bf16 v[50:53], v[154:157], v[222:225], v[50:53]
	v_lshl_add_u64 v[166:167], v[132:133], 0, s[34:35]
	global_load_dwordx2 v[190:191], v[166:167], off
	global_load_dwordx2 v[192:193], v[166:167], off offset:2048
	v_mfma_f32_16x16x32_bf16 v[46:49], v[142:145], v[226:229], v[46:49]
	v_mfma_f32_16x16x32_bf16 v[42:45], v[146:149], v[226:229], v[42:45]
	v_mfma_f32_16x16x32_bf16 v[38:41], v[150:153], v[226:229], v[38:41]
	v_mfma_f32_16x16x32_bf16 v[34:37], v[154:157], v[226:229], v[34:37]
	v_lshl_add_u64 v[166:167], v[132:133], 0, s[36:37]
	global_load_dwordx2 v[194:195], v[166:167], off
	global_load_dwordx2 v[196:197], v[166:167], off offset:2048
	v_mfma_f32_16x16x32_bf16 v[18:21], v[142:145], v[230:233], v[18:21]
	v_mfma_f32_16x16x32_bf16 v[22:25], v[146:149], v[230:233], v[22:25]
	v_mfma_f32_16x16x32_bf16 v[26:29], v[150:153], v[230:233], v[26:29]
	v_mfma_f32_16x16x32_bf16 v[30:33], v[154:157], v[230:233], v[30:33]
	v_lshl_add_u64 v[166:167], v[132:133], 0, s[38:39]
	global_load_dwordx2 v[198:199], v[166:167], off
	global_load_dwordx2 v[200:201], v[166:167], off offset:2048
	s_waitcnt vmcnt(21)
	s_mov_b32 s47, s42
	s_mov_b32 s42, s43
	s_mov_b32 s43, s44
	s_mov_b32 s44, s47
	s_waitcnt lgkmcnt(0)
	s_barrier
	v_mul_f32_e32 v202, s20, v202
	v_mul_f32_e32 v203, s20, v203
	v_mul_f32_e32 v204, s21, v204
	v_mul_f32_e32 v205, s21, v205
	v_mul_f32_e32 v206, s22, v206
	v_mul_f32_e32 v207, s22, v207
	v_mul_f32_e32 v208, s23, v208
	v_mul_f32_e32 v209, s23, v209
	v_mul_f32_e32 v210, s24, v210
	v_mul_f32_e32 v211, s24, v211
	v_mul_f32_e32 v212, s25, v212
	v_mul_f32_e32 v213, s25, v213
	v_mul_f32_e32 v214, s26, v214
	v_mul_f32_e32 v215, s26, v215
	v_mul_f32_e32 v216, s27, v216
	v_mul_f32_e32 v217, s27, v217
	v_cvt_pk_bf16_f32 v158, v202, v204
	v_cvt_pk_bf16_f32 v159, v206, v208
	v_cvt_pk_bf16_f32 v160, v210, v212
	v_cvt_pk_bf16_f32 v161, v214, v216
	v_cvt_pk_bf16_f32 v162, v203, v205
	v_cvt_pk_bf16_f32 v163, v207, v209
	v_cvt_pk_bf16_f32 v164, v211, v213
	v_cvt_pk_bf16_f32 v165, v215, v217
	ds_write_b128 v1, v[158:161] offset:19456
	ds_write_b128 v1, v[162:165] offset:19584
	v_add_u32_e32 v91, s42, v135
	v_add_u32_e32 v93, s42, v137
	ds_read_b128 v[238:241], v139 offset:0
	ds_read_b128 v[242:245], v139 offset:2048
	ds_read_b128 v[246:249], v139 offset:4096
	ds_read_b128 v[250:253], v139 offset:6144
	ds_read_b128 v[218:221], v91 offset:0
	ds_read_b128 v[222:225], v91 offset:2048
	ds_read_b128 v[226:229], v91 offset:4096
	ds_read_b128 v[230:233], v91 offset:6144
	s_add_i32 s47, s44, s6
	s_add_u32 s30, s30, 0x80
	s_addc_u32 s31, s31, 0
	s_waitcnt lgkmcnt(0)
; #define MU_GLDS_A(buf, kt) do { _Pragma("unroll") for (int i = 0; i < NMU; ++i) \
;         __builtin_amdgcn_global_load_lds((const unsigned*)((const char*)A + aoff[i] + (size_t)(kt) * 128), (PG8_LAS unsigned*)(MU_SA(buf) + wid * 1024 + i * 8192), 16, 0, 0); } while (0)
; #define MU_B_ISSUE(sb, kt) do { const char* kb_ = Bb + (size_t)(kt) * (64 * (size_t)RB); _Pragma("unroll") for (int j = 0; j < 8; ++j) { const char* p_ = kb_ + (size_t)j * RB; \
;         asm volatile("global_load_dwordx2 %0, %1, off" : "=&v"(sb[j]) : "v"(p_) : "memory"); } } while (0)
; #define MU_B_WAIT(sb, N) asm volatile("s_waitcnt vmcnt(%8)" : "+v"(sb[0]), "+v"(sb[1]), "+v"(sb[2]), "+v"(sb[3]), "+v"(sb[4]), "+v"(sb[5]), "+v"(sb[6]), "+v"(sb[7]) : "n"(N) : "memory")
; #define MU_G_LOAD(ga, kt) do { const PG8_LAS f32x4* gk_ = (const PG8_LAS f32x4*)(lds + GAIN_OFF) + 16 * (kt) + 2 * wid; const f32x4 ga_ = gk_[0], gb_ = gk_[1]; \
;         ga[0] = ga_[0]; ga[1] = ga_[1]; ga[2] = ga_[2]; ga[3] = ga_[3]; ga[4] = gb_[0]; ga[5] = gb_[1]; ga[6] = gb_[2]; ga[7] = gb_[3]; } while (0)
; #define MU_COMPUTE(buf) MU_COMPUTE_N(buf, NMU)
; #define MU_END(last) do { if (last) asm volatile("s_waitcnt vmcnt(0)" ::: "memory"); else asm volatile("s_waitcnt vmcnt(8)" ::: "memory"); \
;         asm volatile("s_waitcnt lgkmcnt(0)" ::: "memory"); __builtin_amdgcn_s_barrier(); asm volatile("" ::: "memory"); } while (0)
; template <int MODE>
; __device__ __forceinline__ void moe_unit(PG8_LAS unsigned char* lds, int e, int cb, int slot0  , int nv  , const bf16_t* A, const int* slot_tok,
;                                          const float* W0, const float* W1, bf16_t* OUT, const float* slot_rs  , const int* slot_dst) {
;     ...
;     for (int t = 0; t < nt; t += 2) {
;         if (t + 2 < nt) MU_B_WAIT(s1, 8); else MU_B_WAIT(s1, 0);
;         MU_G_LOAD(g0, t + 1); MU_B_WRITE(s1, 1, g0); __builtin_amdgcn_sched_barrier(0); MU_GLDS_A(1, t + 1); __builtin_amdgcn_sched_barrier(0);
;         if (t + 3 < nt) { MU_B_ISSUE(s1, t + 3); }
;         MU_COMPUTE(0);
;         MU_END(t + 3 >= nt);
;         if (t + 2 < nt) { MU_B_WAIT(s0, 8); MU_G_LOAD(g0, t + 2); MU_B_WRITE(s0, 0, g0); __builtin_amdgcn_sched_barrier(0); MU_GLDS_A(0, t + 2); __builtin_amdgcn_sched_barrier(0); }
;         if (t + 4 < nt) { MU_B_ISSUE(s0, t + 4); }
;         MU_COMPUTE(1);
;         MU_END(t + 4 >= nt);
	v_mfma_f32_16x16x32_bf16 v[78:81], v[238:241], v[218:221], v[78:81]
	v_mfma_f32_16x16x32_bf16 v[74:77], v[242:245], v[218:221], v[74:77]
	v_mfma_f32_16x16x32_bf16 v[70:73], v[246:249], v[218:221], v[70:73]
	v_mfma_f32_16x16x32_bf16 v[66:69], v[250:253], v[218:221], v[66:69]
	ds_read_b128 v[218:221], v93 offset:0
	ds_read_b128 v[142:145], v141 offset:0
	s_mov_b32 m0, s47
	s_nop 0
	global_load_lds_dwordx4 v86, s[30:31]
	v_mfma_f32_16x16x32_bf16 v[62:65], v[238:241], v[222:225], v[62:65]
	v_mfma_f32_16x16x32_bf16 v[58:61], v[242:245], v[222:225], v[58:61]
	v_mfma_f32_16x16x32_bf16 v[54:57], v[246:249], v[222:225], v[54:57]
	v_mfma_f32_16x16x32_bf16 v[50:53], v[250:253], v[222:225], v[50:53]
	ds_read_b128 v[222:225], v93 offset:2048
	ds_read_b128 v[146:149], v141 offset:2048
	s_add_i32 m0, s47, 0x2000
	s_nop 0
	global_load_lds_dwordx4 v134, s[30:31]
	v_mfma_f32_16x16x32_bf16 v[46:49], v[238:241], v[226:229], v[46:49]
	v_mfma_f32_16x16x32_bf16 v[42:45], v[242:245], v[226:229], v[42:45]
	v_mfma_f32_16x16x32_bf16 v[38:41], v[246:249], v[226:229], v[38:41]
	v_mfma_f32_16x16x32_bf16 v[34:37], v[250:253], v[226:229], v[34:37]
	ds_read_b128 v[226:229], v93 offset:4096
	ds_read_b128 v[150:153], v141 offset:4096
	s_add_i32 m0, s47, 0x4000
	s_nop 0
	global_load_lds_dwordx4 v136, s[30:31]
	v_mfma_f32_16x16x32_bf16 v[18:21], v[238:241], v[230:233], v[18:21]
	v_mfma_f32_16x16x32_bf16 v[22:25], v[242:245], v[230:233], v[22:25]
	v_mfma_f32_16x16x32_bf16 v[26:29], v[246:249], v[230:233], v[26:29]
	v_mfma_f32_16x16x32_bf16 v[30:33], v[250:253], v[230:233], v[30:33]
	ds_read_b128 v[230:233], v93 offset:6144
	ds_read_b128 v[154:157], v141 offset:6144
	s_add_i32 m0, s47, 0x6000
	s_nop 0
	global_load_lds_dwordx4 v138, s[30:31]
	s_add_i32 m0, s47, 0x8000
	s_nop 0
	global_load_lds_dwordx4 v140, s[30:31]
	s_waitcnt lgkmcnt(0)
	s_load_dwordx8 s[12:19], s[28:29], 0x0
	s_add_u32 s28, s28, 0x100
	s_addc_u32 s29, s29, 0
	v_mfma_f32_16x16x32_bf16 v[78:81], v[142:145], v[218:221], v[78:81]
	v_mfma_f32_16x16x32_bf16 v[74:77], v[146:149], v[218:221], v[74:77]
	v_mfma_f32_16x16x32_bf16 v[70:73], v[150:153], v[218:221], v[70:73]
	v_mfma_f32_16x16x32_bf16 v[66:69], v[154:157], v[218:221], v[66:69]
	v_lshl_add_u64 v[132:133], v[132:133], 0, s[40:41]
	global_load_dwordx2 v[202:203], v[132:133], off
	global_load_dwordx2 v[204:205], v[132:133], off offset:2048
	v_mfma_f32_16x16x32_bf16 v[62:65], v[142:145], v[222:225], v[62:65]
	v_mfma_f32_16x16x32_bf16 v[58:61], v[146:149], v[222:225], v[58:61]
	v_mfma_f32_16x16x32_bf16 v[54:57], v[150:153], v[222:225], v[54:57]
	v_mfma_f32_16x16x32_bf16 v[50:53], v[154:157], v[222:225], v[50:53]
	v_lshl_add_u64 v[166:167], v[132:133], 0, s[34:35]
	global_load_dwordx2 v[206:207], v[166:167], off
	global_load_dwordx2 v[208:209], v[166:167], off offset:2048
	v_mfma_f32_16x16x32_bf16 v[46:49], v[142:145], v[226:229], v[46:49]
	v_mfma_f32_16x16x32_bf16 v[42:45], v[146:149], v[226:229], v[42:45]
	v_mfma_f32_16x16x32_bf16 v[38:41], v[150:153], v[226:229], v[38:41]
	v_mfma_f32_16x16x32_bf16 v[34:37], v[154:157], v[226:229], v[34:37]
	v_lshl_add_u64 v[166:167], v[132:133], 0, s[36:37]
	global_load_dwordx2 v[210:211], v[166:167], off
	global_load_dwordx2 v[212:213], v[166:167], off offset:2048
	v_mfma_f32_16x16x32_bf16 v[18:21], v[142:145], v[230:233], v[18:21]
	v_mfma_f32_16x16x32_bf16 v[22:25], v[146:149], v[230:233], v[22:25]
	v_mfma_f32_16x16x32_bf16 v[26:29], v[150:153], v[230:233], v[26:29]
	v_mfma_f32_16x16x32_bf16 v[30:33], v[154:157], v[230:233], v[30:33]
	v_lshl_add_u64 v[166:167], v[132:133], 0, s[38:39]
	global_load_dwordx2 v[214:215], v[166:167], off
	global_load_dwordx2 v[216:217], v[166:167], off offset:2048
	s_waitcnt vmcnt(21)
	s_mov_b32 s47, s42
	s_mov_b32 s42, s43
	s_mov_b32 s43, s44
	s_mov_b32 s44, s47
	s_waitcnt lgkmcnt(0)
	s_barrier
	v_mul_f32_e32 v98, s12, v98
	v_mul_f32_e32 v99, s12, v99
	v_mul_f32_e32 v100, s13, v100
	v_mul_f32_e32 v101, s13, v101
	v_mul_f32_e32 v102, s14, v102
	v_mul_f32_e32 v103, s14, v103
	v_mul_f32_e32 v104, s15, v104
	v_mul_f32_e32 v105, s15, v105
	v_mul_f32_e32 v106, s16, v106
	v_mul_f32_e32 v107, s16, v107
	v_mul_f32_e32 v108, s17, v108
	v_mul_f32_e32 v109, s17, v109
	v_mul_f32_e32 v110, s18, v110
	v_mul_f32_e32 v111, s18, v111
	v_mul_f32_e32 v112, s19, v112
	v_mul_f32_e32 v113, s19, v113
	v_cvt_pk_bf16_f32 v158, v98, v100
	v_cvt_pk_bf16_f32 v159, v102, v104
	v_cvt_pk_bf16_f32 v160, v106, v108
	v_cvt_pk_bf16_f32 v161, v110, v112
	v_cvt_pk_bf16_f32 v162, v99, v101
	v_cvt_pk_bf16_f32 v163, v103, v105
	v_cvt_pk_bf16_f32 v164, v107, v109
	v_cvt_pk_bf16_f32 v165, v111, v113
	ds_write_b128 v1, v[158:161] offset:0
	ds_write_b128 v1, v[162:165] offset:128
	v_add_u32_e32 v91, s42, v135
	v_add_u32_e32 v93, s42, v137
	ds_read_b128 v[238:241], v139 offset:19456
	ds_read_b128 v[242:245], v139 offset:21504
	ds_read_b128 v[246:249], v139 offset:23552
	ds_read_b128 v[250:253], v139 offset:25600
	ds_read_b128 v[218:221], v91 offset:0
	ds_read_b128 v[222:225], v91 offset:2048
	ds_read_b128 v[226:229], v91 offset:4096
	ds_read_b128 v[230:233], v91 offset:6144
	s_add_i32 s47, s44, s6
	s_add_u32 s30, s30, 0x80
	s_addc_u32 s31, s31, 0
	s_waitcnt lgkmcnt(0)
; #define MU_GLDS_A(buf, kt) do { _Pragma("unroll") for (int i = 0; i < NMU; ++i) \
;         __builtin_amdgcn_global_load_lds((const unsigned*)((const char*)A + aoff[i] + (size_t)(kt) * 128), (PG8_LAS unsigned*)(MU_SA(buf) + wid * 1024 + i * 8192), 16, 0, 0); } while (0)
; #define MU_B_ISSUE(sb, kt) do { const char* kb_ = Bb + (size_t)(kt) * (64 * (size_t)RB); _Pragma("unroll") for (int j = 0; j < 8; ++j) { const char* p_ = kb_ + (size_t)j * RB; \
;         asm volatile("global_load_dwordx2 %0, %1, off" : "=&v"(sb[j]) : "v"(p_) : "memory"); } } while (0)
; #define MU_B_WAIT(sb, N) asm volatile("s_waitcnt vmcnt(%8)" : "+v"(sb[0]), "+v"(sb[1]), "+v"(sb[2]), "+v"(sb[3]), "+v"(sb[4]), "+v"(sb[5]), "+v"(sb[6]), "+v"(sb[7]) : "n"(N) : "memory")
; #define MU_G_LOAD(ga, kt) do { const PG8_LAS f32x4* gk_ = (const PG8_LAS f32x4*)(lds + GAIN_OFF) + 16 * (kt) + 2 * wid; const f32x4 ga_ = gk_[0], gb_ = gk_[1]; \
;         ga[0] = ga_[0]; ga[1] = ga_[1]; ga[2] = ga_[2]; ga[3] = ga_[3]; ga[4] = gb_[0]; ga[5] = gb_[1]; ga[6] = gb_[2]; ga[7] = gb_[3]; } while (0)
; #define MU_COMPUTE(buf) MU_COMPUTE_N(buf, NMU)
; #define MU_END(last) do { if (last) asm volatile("s_waitcnt vmcnt(0)" ::: "memory"); else asm volatile("s_waitcnt vmcnt(8)" ::: "memory"); \
;         asm volatile("s_waitcnt lgkmcnt(0)" ::: "memory"); __builtin_amdgcn_s_barrier(); asm volatile("" ::: "memory"); } while (0)
; template <int MODE>
; __device__ __forceinline__ void moe_unit(PG8_LAS unsigned char* lds, int e, int cb, int slot0  , int nv  , const bf16_t* A, const int* slot_tok,
;                                          const float* W0, const float* W1, bf16_t* OUT, const float* slot_rs  , const int* slot_dst) {
;     ...
;     for (int t = 0; t < nt; t += 2) {
;         if (t + 2 < nt) MU_B_WAIT(s1, 8); else MU_B_WAIT(s1, 0);
;         MU_G_LOAD(g0, t + 1); MU_B_WRITE(s1, 1, g0); __builtin_amdgcn_sched_barrier(0); MU_GLDS_A(1, t + 1); __builtin_amdgcn_sched_barrier(0);
;         if (t + 3 < nt) { MU_B_ISSUE(s1, t + 3); }
;         MU_COMPUTE(0);
;         MU_END(t + 3 >= nt);
;         if (t + 2 < nt) { MU_B_WAIT(s0, 8); MU_G_LOAD(g0, t + 2); MU_B_WRITE(s0, 0, g0); __builtin_amdgcn_sched_barrier(0); MU_GLDS_A(0, t + 2); __builtin_amdgcn_sched_barrier(0); }
;         if (t + 4 < nt) { MU_B_ISSUE(s0, t + 4); }
;         MU_COMPUTE(1);
;         MU_END(t + 4 >= nt);
	v_mfma_f32_16x16x32_bf16 v[78:81], v[238:241], v[218:221], v[78:81]
	v_mfma_f32_16x16x32_bf16 v[74:77], v[242:245], v[218:221], v[74:77]
	v_mfma_f32_16x16x32_bf16 v[70:73], v[246:249], v[218:221], v[70:73]
	v_mfma_f32_16x16x32_bf16 v[66:69], v[250:253], v[218:221], v[66:69]
	ds_read_b128 v[218:221], v93 offset:0
	ds_read_b128 v[142:145], v141 offset:19456
	s_mov_b32 m0, s47
	s_nop 0
	global_load_lds_dwordx4 v86, s[30:31]
	v_mfma_f32_16x16x32_bf16 v[62:65], v[238:241], v[222:225], v[62:65]
	v_mfma_f32_16x16x32_bf16 v[58:61], v[242:245], v[222:225], v[58:61]
	v_mfma_f32_16x16x32_bf16 v[54:57], v[246:249], v[222:225], v[54:57]
	v_mfma_f32_16x16x32_bf16 v[50:53], v[250:253], v[222:225], v[50:53]
	ds_read_b128 v[222:225], v93 offset:2048
	ds_read_b128 v[146:149], v141 offset:21504
	s_add_i32 m0, s47, 0x2000
	s_nop 0
	global_load_lds_dwordx4 v134, s[30:31]
	v_mfma_f32_16x16x32_bf16 v[46:49], v[238:241], v[226:229], v[46:49]
	v_mfma_f32_16x16x32_bf16 v[42:45], v[242:245], v[226:229], v[42:45]
	v_mfma_f32_16x16x32_bf16 v[38:41], v[246:249], v[226:229], v[38:41]
	v_mfma_f32_16x16x32_bf16 v[34:37], v[250:253], v[226:229], v[34:37]
	ds_read_b128 v[226:229], v93 offset:4096
	ds_read_b128 v[150:153], v141 offset:23552
	s_add_i32 m0, s47, 0x4000
	s_nop 0
	global_load_lds_dwordx4 v136, s[30:31]
	v_mfma_f32_16x16x32_bf16 v[18:21], v[238:241], v[230:233], v[18:21]
	v_mfma_f32_16x16x32_bf16 v[22:25], v[242:245], v[230:233], v[22:25]
	v_mfma_f32_16x16x32_bf16 v[26:29], v[246:249], v[230:233], v[26:29]
	v_mfma_f32_16x16x32_bf16 v[30:33], v[250:253], v[230:233], v[30:33]
	ds_read_b128 v[230:233], v93 offset:6144
	ds_read_b128 v[154:157], v141 offset:25600
	s_add_i32 m0, s47, 0x6000
	s_nop 0
	global_load_lds_dwordx4 v138, s[30:31]
	s_add_i32 m0, s47, 0x8000
	s_nop 0
	global_load_lds_dwordx4 v140, s[30:31]
	s_waitcnt lgkmcnt(0)
	s_load_dwordx8 s[20:27], s[28:29], 0x0
	s_add_u32 s28, s28, 0x100
	s_addc_u32 s29, s29, 0
	v_mfma_f32_16x16x32_bf16 v[78:81], v[142:145], v[218:221], v[78:81]
	v_mfma_f32_16x16x32_bf16 v[74:77], v[146:149], v[218:221], v[74:77]
	v_mfma_f32_16x16x32_bf16 v[70:73], v[150:153], v[218:221], v[70:73]
	v_mfma_f32_16x16x32_bf16 v[66:69], v[154:157], v[218:221], v[66:69]
	v_mfma_f32_16x16x32_bf16 v[62:65], v[142:145], v[222:225], v[62:65]
	v_mfma_f32_16x16x32_bf16 v[58:61], v[146:149], v[222:225], v[58:61]
	v_mfma_f32_16x16x32_bf16 v[54:57], v[150:153], v[222:225], v[54:57]
	v_mfma_f32_16x16x32_bf16 v[50:53], v[154:157], v[222:225], v[50:53]
	v_mfma_f32_16x16x32_bf16 v[46:49], v[142:145], v[226:229], v[46:49]
	v_mfma_f32_16x16x32_bf16 v[42:45], v[146:149], v[226:229], v[42:45]
	v_mfma_f32_16x16x32_bf16 v[38:41], v[150:153], v[226:229], v[38:41]
	v_mfma_f32_16x16x32_bf16 v[34:37], v[154:157], v[226:229], v[34:37]
	v_mfma_f32_16x16x32_bf16 v[18:21], v[142:145], v[230:233], v[18:21]
	v_mfma_f32_16x16x32_bf16 v[22:25], v[146:149], v[230:233], v[22:25]
	v_mfma_f32_16x16x32_bf16 v[26:29], v[150:153], v[230:233], v[26:29]
	v_mfma_f32_16x16x32_bf16 v[30:33], v[154:157], v[230:233], v[30:33]
	s_waitcnt vmcnt(13)
	s_mov_b32 s47, s42
	s_mov_b32 s42, s43
	s_mov_b32 s43, s44
	s_mov_b32 s44, s47
	s_waitcnt lgkmcnt(0)
	s_barrier
	v_mul_f32_e32 v114, s20, v114
	v_mul_f32_e32 v115, s20, v115
	v_mul_f32_e32 v116, s21, v116
	v_mul_f32_e32 v117, s21, v117
	v_mul_f32_e32 v118, s22, v118
	v_mul_f32_e32 v119, s22, v119
	v_mul_f32_e32 v120, s23, v120
	v_mul_f32_e32 v121, s23, v121
	v_mul_f32_e32 v122, s24, v122
	v_mul_f32_e32 v123, s24, v123
	v_mul_f32_e32 v124, s25, v124
	v_mul_f32_e32 v125, s25, v125
	v_mul_f32_e32 v126, s26, v126
	v_mul_f32_e32 v127, s26, v127
	v_mul_f32_e32 v128, s27, v128
	v_mul_f32_e32 v129, s27, v129
	v_cvt_pk_bf16_f32 v158, v114, v116
	v_cvt_pk_bf16_f32 v159, v118, v120
	v_cvt_pk_bf16_f32 v160, v122, v124
	v_cvt_pk_bf16_f32 v161, v126, v128
	v_cvt_pk_bf16_f32 v162, v115, v117
	v_cvt_pk_bf16_f32 v163, v119, v121
	v_cvt_pk_bf16_f32 v164, v123, v125
	v_cvt_pk_bf16_f32 v165, v127, v129
	ds_write_b128 v1, v[158:161] offset:19456
	ds_write_b128 v1, v[162:165] offset:19584
	v_add_u32_e32 v91, s42, v135
	v_add_u32_e32 v93, s42, v137
	ds_read_b128 v[238:241], v139 offset:0
	ds_read_b128 v[242:245], v139 offset:2048
	ds_read_b128 v[246:249], v139 offset:4096
	ds_read_b128 v[250:253], v139 offset:6144
	ds_read_b128 v[218:221], v91 offset:0
	ds_read_b128 v[222:225], v91 offset:2048
	ds_read_b128 v[226:229], v91 offset:4096
	ds_read_b128 v[230:233], v91 offset:6144
	s_add_i32 s47, s44, s6
	s_add_u32 s30, s30, 0x80
	s_addc_u32 s31, s31, 0
	s_waitcnt lgkmcnt(0)
	v_mfma_f32_16x16x32_bf16 v[78:81], v[238:241], v[218:221], v[78:81]
	v_mfma_f32_16x16x32_bf16 v[74:77], v[242:245], v[218:221], v[74:77]
	v_mfma_f32_16x16x32_bf16 v[70:73], v[246:249], v[218:221], v[70:73]
	v_mfma_f32_16x16x32_bf16 v[66:69], v[250:253], v[218:221], v[66:69]
	ds_read_b128 v[218:221], v93 offset:0
	ds_read_b128 v[142:145], v141 offset:0
	s_mov_b32 m0, s47
	s_nop 0
	global_load_lds_dwordx4 v86, s[30:31]
	v_mfma_f32_16x16x32_bf16 v[62:65], v[238:241], v[222:225], v[62:65]
	v_mfma_f32_16x16x32_bf16 v[58:61], v[242:245], v[222:225], v[58:61]
	v_mfma_f32_16x16x32_bf16 v[54:57], v[246:249], v[222:225], v[54:57]
	v_mfma_f32_16x16x32_bf16 v[50:53], v[250:253], v[222:225], v[50:53]
	ds_read_b128 v[222:225], v93 offset:2048
	ds_read_b128 v[146:149], v141 offset:2048
	s_add_i32 m0, s47, 0x2000
	s_nop 0
	global_load_lds_dwordx4 v134, s[30:31]
	v_mfma_f32_16x16x32_bf16 v[46:49], v[238:241], v[226:229], v[46:49]
	v_mfma_f32_16x16x32_bf16 v[42:45], v[242:245], v[226:229], v[42:45]
	v_mfma_f32_16x16x32_bf16 v[38:41], v[246:249], v[226:229], v[38:41]
	v_mfma_f32_16x16x32_bf16 v[34:37], v[250:253], v[226:229], v[34:37]
	ds_read_b128 v[226:229], v93 offset:4096
	ds_read_b128 v[150:153], v141 offset:4096
	s_add_i32 m0, s47, 0x4000
	s_nop 0
	global_load_lds_dwordx4 v136, s[30:31]
	v_mfma_f32_16x16x32_bf16 v[18:21], v[238:241], v[230:233], v[18:21]
	v_mfma_f32_16x16x32_bf16 v[22:25], v[242:245], v[230:233], v[22:25]
	v_mfma_f32_16x16x32_bf16 v[26:29], v[246:249], v[230:233], v[26:29]
	v_mfma_f32_16x16x32_bf16 v[30:33], v[250:253], v[230:233], v[30:33]
	ds_read_b128 v[230:233], v93 offset:6144
	ds_read_b128 v[154:157], v141 offset:6144
	s_add_i32 m0, s47, 0x6000
	s_nop 0
	global_load_lds_dwordx4 v138, s[30:31]
	s_add_i32 m0, s47, 0x8000
	s_nop 0
	global_load_lds_dwordx4 v140, s[30:31]
	s_waitcnt lgkmcnt(0)
; #define MU_GLDS_A(buf, kt) do { _Pragma("unroll") for (int i = 0; i < NMU; ++i) \
;         __builtin_amdgcn_global_load_lds((const unsigned*)((const char*)A + aoff[i] + (size_t)(kt) * 128), (PG8_LAS unsigned*)(MU_SA(buf) + wid * 1024 + i * 8192), 16, 0, 0); } while (0)
; #define MU_B_ISSUE(sb, kt) do { const char* kb_ = Bb + (size_t)(kt) * (64 * (size_t)RB); _Pragma("unroll") for (int j = 0; j < 8; ++j) { const char* p_ = kb_ + (size_t)j * RB; \
;         asm volatile("global_load_dwordx2 %0, %1, off" : "=&v"(sb[j]) : "v"(p_) : "memory"); } } while (0)
; #define MU_B_WAIT(sb, N) asm volatile("s_waitcnt vmcnt(%8)" : "+v"(sb[0]), "+v"(sb[1]), "+v"(sb[2]), "+v"(sb[3]), "+v"(sb[4]), "+v"(sb[5]), "+v"(sb[6]), "+v"(sb[7]) : "n"(N) : "memory")
; #define MU_G_LOAD(ga, kt) do { const PG8_LAS f32x4* gk_ = (const PG8_LAS f32x4*)(lds + GAIN_OFF) + 16 * (kt) + 2 * wid; const f32x4 ga_ = gk_[0], gb_ = gk_[1]; \
;         ga[0] = ga_[0]; ga[1] = ga_[1]; ga[2] = ga_[2]; ga[3] = ga_[3]; ga[4] = gb_[0]; ga[5] = gb_[1]; ga[6] = gb_[2]; ga[7] = gb_[3]; } while (0)
; #define MU_COMPUTE(buf) MU_COMPUTE_N(buf, NMU)
; #define MU_END(last) do { if (last) asm volatile("s_waitcnt vmcnt(0)" ::: "memory"); else asm volatile("s_waitcnt vmcnt(8)" ::: "memory"); \
;         asm volatile("s_waitcnt lgkmcnt(0)" ::: "memory"); __builtin_amdgcn_s_barrier(); asm volatile("" ::: "memory"); } while (0)
; template <int MODE>
; __device__ __forceinline__ void moe_unit(PG8_LAS unsigned char* lds, int e, int cb, int slot0  , int nv  , const bf16_t* A, const int* slot_tok,
;                                          const float* W0, const float* W1, bf16_t* OUT, const float* slot_rs  , const int* slot_dst) {
;     ...
;     for (int t = 0; t < nt; t += 2) {
;         if (t + 2 < nt) MU_B_WAIT(s1, 8); else MU_B_WAIT(s1, 0);
;         MU_G_LOAD(g0, t + 1); MU_B_WRITE(s1, 1, g0); __builtin_amdgcn_sched_barrier(0); MU_GLDS_A(1, t + 1); __builtin_amdgcn_sched_barrier(0);
;         if (t + 3 < nt) { MU_B_ISSUE(s1, t + 3); }
;         MU_COMPUTE(0);
;         MU_END(t + 3 >= nt);
;         if (t + 2 < nt) { MU_B_WAIT(s0, 8); MU_G_LOAD(g0, t + 2); MU_B_WRITE(s0, 0, g0); __builtin_amdgcn_sched_barrier(0); MU_GLDS_A(0, t + 2); __builtin_amdgcn_sched_barrier(0); }
;         if (t + 4 < nt) { MU_B_ISSUE(s0, t + 4); }
;         MU_COMPUTE(1);
;         MU_END(t + 4 >= nt);
	s_load_dwordx8 s[12:19], s[28:29], 0x0
	s_add_u32 s28, s28, 0x100
	s_addc_u32 s29, s29, 0
	v_mfma_f32_16x16x32_bf16 v[78:81], v[142:145], v[218:221], v[78:81]
	v_mfma_f32_16x16x32_bf16 v[74:77], v[146:149], v[218:221], v[74:77]
	v_mfma_f32_16x16x32_bf16 v[70:73], v[150:153], v[218:221], v[70:73]
	v_mfma_f32_16x16x32_bf16 v[66:69], v[154:157], v[218:221], v[66:69]
	v_mfma_f32_16x16x32_bf16 v[62:65], v[142:145], v[222:225], v[62:65]
	v_mfma_f32_16x16x32_bf16 v[58:61], v[146:149], v[222:225], v[58:61]
	v_mfma_f32_16x16x32_bf16 v[54:57], v[150:153], v[222:225], v[54:57]
	v_mfma_f32_16x16x32_bf16 v[50:53], v[154:157], v[222:225], v[50:53]
	v_mfma_f32_16x16x32_bf16 v[46:49], v[142:145], v[226:229], v[46:49]
	v_mfma_f32_16x16x32_bf16 v[42:45], v[146:149], v[226:229], v[42:45]
	v_mfma_f32_16x16x32_bf16 v[38:41], v[150:153], v[226:229], v[38:41]
	v_mfma_f32_16x16x32_bf16 v[34:37], v[154:157], v[226:229], v[34:37]
	v_mfma_f32_16x16x32_bf16 v[18:21], v[142:145], v[230:233], v[18:21]
	v_mfma_f32_16x16x32_bf16 v[22:25], v[146:149], v[230:233], v[22:25]
	v_mfma_f32_16x16x32_bf16 v[26:29], v[150:153], v[230:233], v[26:29]
	v_mfma_f32_16x16x32_bf16 v[30:33], v[154:157], v[230:233], v[30:33]
	s_waitcnt vmcnt(5)
	s_mov_b32 s47, s42
	s_mov_b32 s42, s43
	s_mov_b32 s43, s44
	s_mov_b32 s44, s47
	s_waitcnt lgkmcnt(0)
	s_barrier
	v_mul_f32_e32 v186, s12, v186
	v_mul_f32_e32 v187, s12, v187
	v_mul_f32_e32 v188, s13, v188
	v_mul_f32_e32 v189, s13, v189
	v_mul_f32_e32 v190, s14, v190
	v_mul_f32_e32 v191, s14, v191
	v_mul_f32_e32 v192, s15, v192
	v_mul_f32_e32 v193, s15, v193
	v_mul_f32_e32 v194, s16, v194
	v_mul_f32_e32 v195, s16, v195
	v_mul_f32_e32 v196, s17, v196
	v_mul_f32_e32 v197, s17, v197
	v_mul_f32_e32 v198, s18, v198
	v_mul_f32_e32 v199, s18, v199
	v_mul_f32_e32 v200, s19, v200
	v_mul_f32_e32 v201, s19, v201
	v_cvt_pk_bf16_f32 v158, v186, v188
	v_cvt_pk_bf16_f32 v159, v190, v192
	v_cvt_pk_bf16_f32 v160, v194, v196
	v_cvt_pk_bf16_f32 v161, v198, v200
	v_cvt_pk_bf16_f32 v162, v187, v189
	v_cvt_pk_bf16_f32 v163, v191, v193
	v_cvt_pk_bf16_f32 v164, v195, v197
	v_cvt_pk_bf16_f32 v165, v199, v201
	ds_write_b128 v1, v[158:161] offset:0
	ds_write_b128 v1, v[162:165] offset:128
	v_add_u32_e32 v91, s42, v135
	v_add_u32_e32 v93, s42, v137
	ds_read_b128 v[238:241], v139 offset:19456
	ds_read_b128 v[242:245], v139 offset:21504
	ds_read_b128 v[246:249], v139 offset:23552
	ds_read_b128 v[250:253], v139 offset:25600
	ds_read_b128 v[218:221], v91 offset:0
	ds_read_b128 v[222:225], v91 offset:2048
	ds_read_b128 v[226:229], v91 offset:4096
	ds_read_b128 v[230:233], v91 offset:6144
	s_add_i32 s47, s44, s6
	s_add_u32 s30, s30, 0x80
	s_addc_u32 s31, s31, 0
	s_waitcnt lgkmcnt(0)
	v_mfma_f32_16x16x32_bf16 v[78:81], v[238:241], v[218:221], v[78:81]
	v_mfma_f32_16x16x32_bf16 v[74:77], v[242:245], v[218:221], v[74:77]
	v_mfma_f32_16x16x32_bf16 v[70:73], v[246:249], v[218:221], v[70:73]
	v_mfma_f32_16x16x32_bf16 v[66:69], v[250:253], v[218:221], v[66:69]
	ds_read_b128 v[218:221], v93 offset:0
	ds_read_b128 v[142:145], v141 offset:19456
	s_mov_b32 m0, s47
	s_nop 0
	global_load_lds_dwordx4 v86, s[30:31]
	v_mfma_f32_16x16x32_bf16 v[62:65], v[238:241], v[222:225], v[62:65]
	v_mfma_f32_16x16x32_bf16 v[58:61], v[242:245], v[222:225], v[58:61]
	v_mfma_f32_16x16x32_bf16 v[54:57], v[246:249], v[222:225], v[54:57]
	v_mfma_f32_16x16x32_bf16 v[50:53], v[250:253], v[222:225], v[50:53]
	ds_read_b128 v[222:225], v93 offset:2048
	ds_read_b128 v[146:149], v141 offset:21504
	s_add_i32 m0, s47, 0x2000
	s_nop 0
	global_load_lds_dwordx4 v134, s[30:31]
	v_mfma_f32_16x16x32_bf16 v[46:49], v[238:241], v[226:229], v[46:49]
	v_mfma_f32_16x16x32_bf16 v[42:45], v[242:245], v[226:229], v[42:45]
	v_mfma_f32_16x16x32_bf16 v[38:41], v[246:249], v[226:229], v[38:41]
	v_mfma_f32_16x16x32_bf16 v[34:37], v[250:253], v[226:229], v[34:37]
	ds_read_b128 v[226:229], v93 offset:4096
	ds_read_b128 v[150:153], v141 offset:23552
	s_add_i32 m0, s47, 0x4000
	s_nop 0
	global_load_lds_dwordx4 v136, s[30:31]
	v_mfma_f32_16x16x32_bf16 v[18:21], v[238:241], v[230:233], v[18:21]
	v_mfma_f32_16x16x32_bf16 v[22:25], v[242:245], v[230:233], v[22:25]
	v_mfma_f32_16x16x32_bf16 v[26:29], v[246:249], v[230:233], v[26:29]
	v_mfma_f32_16x16x32_bf16 v[30:33], v[250:253], v[230:233], v[30:33]
	ds_read_b128 v[230:233], v93 offset:6144
	ds_read_b128 v[154:157], v141 offset:25600
	s_add_i32 m0, s47, 0x6000
	s_nop 0
	global_load_lds_dwordx4 v138, s[30:31]
	s_add_i32 m0, s47, 0x8000
	s_nop 0
	global_load_lds_dwordx4 v140, s[30:31]
	s_waitcnt lgkmcnt(0)
	s_load_dwordx8 s[20:27], s[28:29], 0x0
	s_add_u32 s28, s28, 0x100
	s_addc_u32 s29, s29, 0
	v_mfma_f32_16x16x32_bf16 v[78:81], v[142:145], v[218:221], v[78:81]
	v_mfma_f32_16x16x32_bf16 v[74:77], v[146:149], v[218:221], v[74:77]
	v_mfma_f32_16x16x32_bf16 v[70:73], v[150:153], v[218:221], v[70:73]
	v_mfma_f32_16x16x32_bf16 v[66:69], v[154:157], v[218:221], v[66:69]
	v_mfma_f32_16x16x32_bf16 v[62:65], v[142:145], v[222:225], v[62:65]
	v_mfma_f32_16x16x32_bf16 v[58:61], v[146:149], v[222:225], v[58:61]
	v_mfma_f32_16x16x32_bf16 v[54:57], v[150:153], v[222:225], v[54:57]
	v_mfma_f32_16x16x32_bf16 v[50:53], v[154:157], v[222:225], v[50:53]
	v_mfma_f32_16x16x32_bf16 v[46:49], v[142:145], v[226:229], v[46:49]
	v_mfma_f32_16x16x32_bf16 v[42:45], v[146:149], v[226:229], v[42:45]
	v_mfma_f32_16x16x32_bf16 v[38:41], v[150:153], v[226:229], v[38:41]
	v_mfma_f32_16x16x32_bf16 v[34:37], v[154:157], v[226:229], v[34:37]
	v_mfma_f32_16x16x32_bf16 v[18:21], v[142:145], v[230:233], v[18:21]
	v_mfma_f32_16x16x32_bf16 v[22:25], v[146:149], v[230:233], v[22:25]
	v_mfma_f32_16x16x32_bf16 v[26:29], v[150:153], v[230:233], v[26:29]
	v_mfma_f32_16x16x32_bf16 v[30:33], v[154:157], v[230:233], v[30:33]
	s_waitcnt vmcnt(5)
	s_mov_b32 s47, s42
	s_mov_b32 s42, s43
	s_mov_b32 s43, s44
	s_mov_b32 s44, s47
	s_waitcnt lgkmcnt(0)
	s_barrier
; #define MU_GLDS_A(buf, kt) do { _Pragma("unroll") for (int i = 0; i < NMU; ++i) \
;         __builtin_amdgcn_global_load_lds((const unsigned*)((const char*)A + aoff[i] + (size_t)(kt) * 128), (PG8_LAS unsigned*)(MU_SA(buf) + wid * 1024 + i * 8192), 16, 0, 0); } while (0)
; #define MU_B_ISSUE(sb, kt) do { const char* kb_ = Bb + (size_t)(kt) * (64 * (size_t)RB); _Pragma("unroll") for (int j = 0; j < 8; ++j) { const char* p_ = kb_ + (size_t)j * RB; \
;         asm volatile("global_load_dwordx2 %0, %1, off" : "=&v"(sb[j]) : "v"(p_) : "memory"); } } while (0)
; #define MU_B_WAIT(sb, N) asm volatile("s_waitcnt vmcnt(%8)" : "+v"(sb[0]), "+v"(sb[1]), "+v"(sb[2]), "+v"(sb[3]), "+v"(sb[4]), "+v"(sb[5]), "+v"(sb[6]), "+v"(sb[7]) : "n"(N) : "memory")
; #define MU_G_LOAD(ga, kt) do { const PG8_LAS f32x4* gk_ = (const PG8_LAS f32x4*)(lds + GAIN_OFF) + 16 * (kt) + 2 * wid; const f32x4 ga_ = gk_[0], gb_ = gk_[1]; \
;         ga[0] = ga_[0]; ga[1] = ga_[1]; ga[2] = ga_[2]; ga[3] = ga_[3]; ga[4] = gb_[0]; ga[5] = gb_[1]; ga[6] = gb_[2]; ga[7] = gb_[3]; } while (0)
; #define MU_COMPUTE(buf) MU_COMPUTE_N(buf, NMU)
; #define MU_END(last) do { if (last) asm volatile("s_waitcnt vmcnt(0)" ::: "memory"); else asm volatile("s_waitcnt vmcnt(8)" ::: "memory"); \
;         asm volatile("s_waitcnt lgkmcnt(0)" ::: "memory"); __builtin_amdgcn_s_barrier(); asm volatile("" ::: "memory"); } while (0)
; template <int MODE>
; __device__ __forceinline__ void moe_unit(PG8_LAS unsigned char* lds, int e, int cb, int slot0  , int nv  , const bf16_t* A, const int* slot_tok,
;                                          const float* W0, const float* W1, bf16_t* OUT, const float* slot_rs  , const int* slot_dst) {
;     ...
;     for (int t = 0; t < nt; t += 2) {
;         if (t + 2 < nt) MU_B_WAIT(s1, 8); else MU_B_WAIT(s1, 0);
;         MU_G_LOAD(g0, t + 1); MU_B_WRITE(s1, 1, g0); __builtin_amdgcn_sched_barrier(0); MU_GLDS_A(1, t + 1); __builtin_amdgcn_sched_barrier(0);
;         if (t + 3 < nt) { MU_B_ISSUE(s1, t + 3); }
;         MU_COMPUTE(0);
;         MU_END(t + 3 >= nt);
;         if (t + 2 < nt) { MU_B_WAIT(s0, 8); MU_G_LOAD(g0, t + 2); MU_B_WRITE(s0, 0, g0); __builtin_amdgcn_sched_barrier(0); MU_GLDS_A(0, t + 2); __builtin_amdgcn_sched_barrier(0); }
;         if (t + 4 < nt) { MU_B_ISSUE(s0, t + 4); }
;         MU_COMPUTE(1);
;         MU_END(t + 4 >= nt);
	v_mul_f32_e32 v202, s20, v202
	v_mul_f32_e32 v203, s20, v203
	v_mul_f32_e32 v204, s21, v204
	v_mul_f32_e32 v205, s21, v205
	v_mul_f32_e32 v206, s22, v206
	v_mul_f32_e32 v207, s22, v207
	v_mul_f32_e32 v208, s23, v208
	v_mul_f32_e32 v209, s23, v209
	v_mul_f32_e32 v210, s24, v210
	v_mul_f32_e32 v211, s24, v211
	v_mul_f32_e32 v212, s25, v212
	v_mul_f32_e32 v213, s25, v213
	v_mul_f32_e32 v214, s26, v214
	v_mul_f32_e32 v215, s26, v215
	v_mul_f32_e32 v216, s27, v216
	v_mul_f32_e32 v217, s27, v217
	v_cvt_pk_bf16_f32 v158, v202, v204
	v_cvt_pk_bf16_f32 v159, v206, v208
	v_cvt_pk_bf16_f32 v160, v210, v212
	v_cvt_pk_bf16_f32 v161, v214, v216
	v_cvt_pk_bf16_f32 v162, v203, v205
	v_cvt_pk_bf16_f32 v163, v207, v209
	v_cvt_pk_bf16_f32 v164, v211, v213
	v_cvt_pk_bf16_f32 v165, v215, v217
	ds_write_b128 v1, v[158:161] offset:19456
	ds_write_b128 v1, v[162:165] offset:19584
	v_add_u32_e32 v91, s42, v135
	v_add_u32_e32 v93, s42, v137
	ds_read_b128 v[238:241], v139 offset:0
	ds_read_b128 v[242:245], v139 offset:2048
	ds_read_b128 v[246:249], v139 offset:4096
	ds_read_b128 v[250:253], v139 offset:6144
	ds_read_b128 v[218:221], v91 offset:0
	ds_read_b128 v[222:225], v91 offset:2048
	ds_read_b128 v[226:229], v91 offset:4096
	ds_read_b128 v[230:233], v91 offset:6144
	s_waitcnt lgkmcnt(0)
	v_mfma_f32_16x16x32_bf16 v[78:81], v[238:241], v[218:221], v[78:81]
	v_mfma_f32_16x16x32_bf16 v[74:77], v[242:245], v[218:221], v[74:77]
	v_mfma_f32_16x16x32_bf16 v[70:73], v[246:249], v[218:221], v[70:73]
	v_mfma_f32_16x16x32_bf16 v[66:69], v[250:253], v[218:221], v[66:69]
	ds_read_b128 v[218:221], v93 offset:0
	ds_read_b128 v[142:145], v141 offset:0
	v_mfma_f32_16x16x32_bf16 v[62:65], v[238:241], v[222:225], v[62:65]
	v_mfma_f32_16x16x32_bf16 v[58:61], v[242:245], v[222:225], v[58:61]
	v_mfma_f32_16x16x32_bf16 v[54:57], v[246:249], v[222:225], v[54:57]
	v_mfma_f32_16x16x32_bf16 v[50:53], v[250:253], v[222:225], v[50:53]
	ds_read_b128 v[222:225], v93 offset:2048
	ds_read_b128 v[146:149], v141 offset:2048
	v_mfma_f32_16x16x32_bf16 v[46:49], v[238:241], v[226:229], v[46:49]
	v_mfma_f32_16x16x32_bf16 v[42:45], v[242:245], v[226:229], v[42:45]
	v_mfma_f32_16x16x32_bf16 v[38:41], v[246:249], v[226:229], v[38:41]
	v_mfma_f32_16x16x32_bf16 v[34:37], v[250:253], v[226:229], v[34:37]
	ds_read_b128 v[226:229], v93 offset:4096
	ds_read_b128 v[150:153], v141 offset:4096
	v_mfma_f32_16x16x32_bf16 v[18:21], v[238:241], v[230:233], v[18:21]
	v_mfma_f32_16x16x32_bf16 v[22:25], v[242:245], v[230:233], v[22:25]
	v_mfma_f32_16x16x32_bf16 v[26:29], v[246:249], v[230:233], v[26:29]
	v_mfma_f32_16x16x32_bf16 v[30:33], v[250:253], v[230:233], v[30:33]
	ds_read_b128 v[230:233], v93 offset:6144
	ds_read_b128 v[154:157], v141 offset:6144
	s_waitcnt lgkmcnt(0)
	v_mfma_f32_16x16x32_bf16 v[78:81], v[142:145], v[218:221], v[78:81]
	v_mfma_f32_16x16x32_bf16 v[74:77], v[146:149], v[218:221], v[74:77]
	v_mfma_f32_16x16x32_bf16 v[70:73], v[150:153], v[218:221], v[70:73]
	v_mfma_f32_16x16x32_bf16 v[66:69], v[154:157], v[218:221], v[66:69]
	v_mfma_f32_16x16x32_bf16 v[62:65], v[142:145], v[222:225], v[62:65]
	v_mfma_f32_16x16x32_bf16 v[58:61], v[146:149], v[222:225], v[58:61]
	v_mfma_f32_16x16x32_bf16 v[54:57], v[150:153], v[222:225], v[54:57]
	v_mfma_f32_16x16x32_bf16 v[50:53], v[154:157], v[222:225], v[50:53]
	v_mfma_f32_16x16x32_bf16 v[46:49], v[142:145], v[226:229], v[46:49]
	v_mfma_f32_16x16x32_bf16 v[42:45], v[146:149], v[226:229], v[42:45]
	v_mfma_f32_16x16x32_bf16 v[38:41], v[150:153], v[226:229], v[38:41]
	v_mfma_f32_16x16x32_bf16 v[34:37], v[154:157], v[226:229], v[34:37]
	v_mfma_f32_16x16x32_bf16 v[18:21], v[142:145], v[230:233], v[18:21]
	v_mfma_f32_16x16x32_bf16 v[22:25], v[146:149], v[230:233], v[22:25]
	v_mfma_f32_16x16x32_bf16 v[26:29], v[150:153], v[230:233], v[26:29]
	v_mfma_f32_16x16x32_bf16 v[30:33], v[154:157], v[230:233], v[30:33]
	s_waitcnt vmcnt(0)
	s_mov_b32 s47, s42
	s_mov_b32 s42, s43
	s_mov_b32 s43, s44
	s_mov_b32 s44, s47
	s_waitcnt lgkmcnt(0)
	s_barrier
	v_add_u32_e32 v91, s42, v135
	v_add_u32_e32 v93, s42, v137
	ds_read_b128 v[238:241], v139 offset:19456
	ds_read_b128 v[242:245], v139 offset:21504
	ds_read_b128 v[246:249], v139 offset:23552
	ds_read_b128 v[250:253], v139 offset:25600
	ds_read_b128 v[218:221], v91 offset:0
	ds_read_b128 v[222:225], v91 offset:2048
	ds_read_b128 v[226:229], v91 offset:4096
	ds_read_b128 v[230:233], v91 offset:6144
	s_waitcnt lgkmcnt(0)
	v_mfma_f32_16x16x32_bf16 v[78:81], v[238:241], v[218:221], v[78:81]
	v_mfma_f32_16x16x32_bf16 v[74:77], v[242:245], v[218:221], v[74:77]
	v_mfma_f32_16x16x32_bf16 v[70:73], v[246:249], v[218:221], v[70:73]
	v_mfma_f32_16x16x32_bf16 v[66:69], v[250:253], v[218:221], v[66:69]
	ds_read_b128 v[218:221], v93 offset:0
	ds_read_b128 v[142:145], v141 offset:19456
	v_mfma_f32_16x16x32_bf16 v[62:65], v[238:241], v[222:225], v[62:65]
	v_mfma_f32_16x16x32_bf16 v[58:61], v[242:245], v[222:225], v[58:61]
	v_mfma_f32_16x16x32_bf16 v[54:57], v[246:249], v[222:225], v[54:57]
	v_mfma_f32_16x16x32_bf16 v[50:53], v[250:253], v[222:225], v[50:53]
	ds_read_b128 v[222:225], v93 offset:2048
	ds_read_b128 v[146:149], v141 offset:21504
	v_mfma_f32_16x16x32_bf16 v[46:49], v[238:241], v[226:229], v[46:49]
	v_mfma_f32_16x16x32_bf16 v[42:45], v[242:245], v[226:229], v[42:45]
	v_mfma_f32_16x16x32_bf16 v[38:41], v[246:249], v[226:229], v[38:41]
	v_mfma_f32_16x16x32_bf16 v[34:37], v[250:253], v[226:229], v[34:37]
	ds_read_b128 v[226:229], v93 offset:4096
	ds_read_b128 v[150:153], v141 offset:23552
	v_mfma_f32_16x16x32_bf16 v[18:21], v[238:241], v[230:233], v[18:21]
	v_mfma_f32_16x16x32_bf16 v[22:25], v[242:245], v[230:233], v[22:25]
	v_mfma_f32_16x16x32_bf16 v[26:29], v[246:249], v[230:233], v[26:29]
	v_mfma_f32_16x16x32_bf16 v[30:33], v[250:253], v[230:233], v[30:33]
	ds_read_b128 v[230:233], v93 offset:6144
	ds_read_b128 v[154:157], v141 offset:25600
	s_waitcnt lgkmcnt(0)
; #define MU_GLDS_A(buf, kt) do { _Pragma("unroll") for (int i = 0; i < NMU; ++i) \
;         __builtin_amdgcn_global_load_lds((const unsigned*)((const char*)A + aoff[i] + (size_t)(kt) * 128), (PG8_LAS unsigned*)(MU_SA(buf) + wid * 1024 + i * 8192), 16, 0, 0); } while (0)
; #define MU_B_ISSUE(sb, kt) do { const char* kb_ = Bb + (size_t)(kt) * (64 * (size_t)RB); _Pragma("unroll") for (int j = 0; j < 8; ++j) { const char* p_ = kb_ + (size_t)j * RB; \
;         asm volatile("global_load_dwordx2 %0, %1, off" : "=&v"(sb[j]) : "v"(p_) : "memory"); } } while (0)
; #define MU_B_WAIT(sb, N) asm volatile("s_waitcnt vmcnt(%8)" : "+v"(sb[0]), "+v"(sb[1]), "+v"(sb[2]), "+v"(sb[3]), "+v"(sb[4]), "+v"(sb[5]), "+v"(sb[6]), "+v"(sb[7]) : "n"(N) : "memory")
; #define MU_G_LOAD(ga, kt) do { const PG8_LAS f32x4* gk_ = (const PG8_LAS f32x4*)(lds + GAIN_OFF) + 16 * (kt) + 2 * wid; const f32x4 ga_ = gk_[0], gb_ = gk_[1]; \
;         ga[0] = ga_[0]; ga[1] = ga_[1]; ga[2] = ga_[2]; ga[3] = ga_[3]; ga[4] = gb_[0]; ga[5] = gb_[1]; ga[6] = gb_[2]; ga[7] = gb_[3]; } while (0)
; #define MU_COMPUTE(buf) MU_COMPUTE_N(buf, NMU)
; #define MU_END(last) do { if (last) asm volatile("s_waitcnt vmcnt(0)" ::: "memory"); else asm volatile("s_waitcnt vmcnt(8)" ::: "memory"); \
;         asm volatile("s_waitcnt lgkmcnt(0)" ::: "memory"); __builtin_amdgcn_s_barrier(); asm volatile("" ::: "memory"); } while (0)
; template <int MODE>
; __device__ __forceinline__ void moe_unit(PG8_LAS unsigned char* lds, int e, int cb, int slot0  , int nv  , const bf16_t* A, const int* slot_tok,
;                                          const float* W0, const float* W1, bf16_t* OUT, const float* slot_rs  , const int* slot_dst) {
;     ...
;     for (int t = 0; t < nt; t += 2) {
;         if (t + 2 < nt) MU_B_WAIT(s1, 8); else MU_B_WAIT(s1, 0);
;         MU_G_LOAD(g0, t + 1); MU_B_WRITE(s1, 1, g0); __builtin_amdgcn_sched_barrier(0); MU_GLDS_A(1, t + 1); __builtin_amdgcn_sched_barrier(0);
;         if (t + 3 < nt) { MU_B_ISSUE(s1, t + 3); }
;         MU_COMPUTE(0);
;         MU_END(t + 3 >= nt);
;         if (t + 2 < nt) { MU_B_WAIT(s0, 8); MU_G_LOAD(g0, t + 2); MU_B_WRITE(s0, 0, g0); __builtin_amdgcn_sched_barrier(0); MU_GLDS_A(0, t + 2); __builtin_amdgcn_sched_barrier(0); }
;         if (t + 4 < nt) { MU_B_ISSUE(s0, t + 4); }
;         MU_COMPUTE(1);
;         MU_END(t + 4 >= nt);
	v_mfma_f32_16x16x32_bf16 v[78:81], v[142:145], v[218:221], v[78:81]
	v_mfma_f32_16x16x32_bf16 v[74:77], v[146:149], v[218:221], v[74:77]
	v_mfma_f32_16x16x32_bf16 v[70:73], v[150:153], v[218:221], v[70:73]
	v_mfma_f32_16x16x32_bf16 v[66:69], v[154:157], v[218:221], v[66:69]
	v_mfma_f32_16x16x32_bf16 v[62:65], v[142:145], v[222:225], v[62:65]
	v_mfma_f32_16x16x32_bf16 v[58:61], v[146:149], v[222:225], v[58:61]
	v_mfma_f32_16x16x32_bf16 v[54:57], v[150:153], v[222:225], v[54:57]
	v_mfma_f32_16x16x32_bf16 v[50:53], v[154:157], v[222:225], v[50:53]
	v_mfma_f32_16x16x32_bf16 v[46:49], v[142:145], v[226:229], v[46:49]
	v_mfma_f32_16x16x32_bf16 v[42:45], v[146:149], v[226:229], v[42:45]
	v_mfma_f32_16x16x32_bf16 v[38:41], v[150:153], v[226:229], v[38:41]
	v_mfma_f32_16x16x32_bf16 v[34:37], v[154:157], v[226:229], v[34:37]
	v_mfma_f32_16x16x32_bf16 v[18:21], v[142:145], v[230:233], v[18:21]
	v_mfma_f32_16x16x32_bf16 v[22:25], v[146:149], v[230:233], v[22:25]
	v_mfma_f32_16x16x32_bf16 v[26:29], v[150:153], v[230:233], v[26:29]
	v_mfma_f32_16x16x32_bf16 v[30:33], v[154:157], v[230:233], v[30:33]
	s_mov_b32 s47, s42
	s_mov_b32 s42, s43
	s_mov_b32 s43, s44
	s_mov_b32 s44, s47
	s_waitcnt lgkmcnt(0)
	s_barrier
	s_branch .Lmu_done
.Lmu_grpY4:
	s_add_i32 s47, s44, s6
	s_add_u32 s30, s30, 0x80
	s_addc_u32 s31, s31, 0
	s_mov_b32 m0, s47
	s_nop 0
	global_load_lds_dwordx4 v86, s[30:31]
	s_add_i32 m0, s47, 0x2000
	s_nop 0
	global_load_lds_dwordx4 v134, s[30:31]
	s_add_i32 m0, s47, 0x4000
	s_nop 0
	global_load_lds_dwordx4 v136, s[30:31]
	s_add_i32 m0, s47, 0x6000
	s_nop 0
	global_load_lds_dwordx4 v138, s[30:31]
	s_add_i32 m0, s47, 0x8000
	s_nop 0
	global_load_lds_dwordx4 v140, s[30:31]
	s_waitcnt vmcnt(29)
	v_mul_f32_e32 v114, s20, v114
	v_mul_f32_e32 v115, s20, v115
	v_mul_f32_e32 v116, s21, v116
	v_mul_f32_e32 v117, s21, v117
	v_mul_f32_e32 v118, s22, v118
	v_mul_f32_e32 v119, s22, v119
	v_mul_f32_e32 v120, s23, v120
	v_mul_f32_e32 v121, s23, v121
	v_mul_f32_e32 v122, s24, v122
	v_mul_f32_e32 v123, s24, v123
	v_mul_f32_e32 v124, s25, v124
	v_mul_f32_e32 v125, s25, v125
	v_mul_f32_e32 v126, s26, v126
	v_mul_f32_e32 v127, s26, v127
	v_mul_f32_e32 v128, s27, v128
	v_mul_f32_e32 v129, s27, v129
	v_cvt_pk_bf16_f32 v158, v114, v116
	v_cvt_pk_bf16_f32 v159, v118, v120
	v_cvt_pk_bf16_f32 v160, v122, v124
	v_cvt_pk_bf16_f32 v161, v126, v128
	v_cvt_pk_bf16_f32 v162, v115, v117
	v_cvt_pk_bf16_f32 v163, v119, v121
	v_cvt_pk_bf16_f32 v164, v123, v125
	v_cvt_pk_bf16_f32 v165, v127, v129
	ds_write_b128 v1, v[158:161] offset:19456
	ds_write_b128 v1, v[162:165] offset:19584
	v_add_u32_e32 v91, s42, v135
	v_add_u32_e32 v93, s42, v137
	ds_read_b128 v[238:241], v139 offset:0
	ds_read_b128 v[242:245], v139 offset:2048
	ds_read_b128 v[246:249], v139 offset:4096
	ds_read_b128 v[250:253], v139 offset:6144
	ds_read_b128 v[218:221], v91 offset:0
	ds_read_b128 v[222:225], v91 offset:2048
	ds_read_b128 v[226:229], v91 offset:4096
	ds_read_b128 v[230:233], v91 offset:6144
	s_waitcnt lgkmcnt(0)
	s_load_dwordx8 s[12:19], s[28:29], 0x0
	s_add_u32 s28, s28, 0x100
	s_addc_u32 s29, s29, 0
	v_mfma_f32_16x16x32_bf16 v[78:81], v[238:241], v[218:221], v[78:81]
	v_mfma_f32_16x16x32_bf16 v[74:77], v[242:245], v[218:221], v[74:77]
	v_mfma_f32_16x16x32_bf16 v[70:73], v[246:249], v[218:221], v[70:73]
	v_mfma_f32_16x16x32_bf16 v[66:69], v[250:253], v[218:221], v[66:69]
	ds_read_b128 v[218:221], v93 offset:0
	ds_read_b128 v[142:145], v141 offset:0
	v_lshl_add_u64 v[132:133], v[132:133], 0, s[40:41]
	global_load_dwordx2 v[114:115], v[132:133], off
	global_load_dwordx2 v[116:117], v[132:133], off offset:2048
	v_mfma_f32_16x16x32_bf16 v[62:65], v[238:241], v[222:225], v[62:65]
	v_mfma_f32_16x16x32_bf16 v[58:61], v[242:245], v[222:225], v[58:61]
	v_mfma_f32_16x16x32_bf16 v[54:57], v[246:249], v[222:225], v[54:57]
	v_mfma_f32_16x16x32_bf16 v[50:53], v[250:253], v[222:225], v[50:53]
	ds_read_b128 v[222:225], v93 offset:2048
	ds_read_b128 v[146:149], v141 offset:2048
	v_lshl_add_u64 v[166:167], v[132:133], 0, s[34:35]
	global_load_dwordx2 v[118:119], v[166:167], off
	global_load_dwordx2 v[120:121], v[166:167], off offset:2048
	v_mfma_f32_16x16x32_bf16 v[46:49], v[238:241], v[226:229], v[46:49]
	v_mfma_f32_16x16x32_bf16 v[42:45], v[242:245], v[226:229], v[42:45]
	v_mfma_f32_16x16x32_bf16 v[38:41], v[246:249], v[226:229], v[38:41]
	v_mfma_f32_16x16x32_bf16 v[34:37], v[250:253], v[226:229], v[34:37]
	ds_read_b128 v[226:229], v93 offset:4096
	ds_read_b128 v[150:153], v141 offset:4096
	v_lshl_add_u64 v[166:167], v[132:133], 0, s[36:37]
	global_load_dwordx2 v[122:123], v[166:167], off
	global_load_dwordx2 v[124:125], v[166:167], off offset:2048
	v_mfma_f32_16x16x32_bf16 v[18:21], v[238:241], v[230:233], v[18:21]
	v_mfma_f32_16x16x32_bf16 v[22:25], v[242:245], v[230:233], v[22:25]
	v_mfma_f32_16x16x32_bf16 v[26:29], v[246:249], v[230:233], v[26:29]
	v_mfma_f32_16x16x32_bf16 v[30:33], v[250:253], v[230:233], v[30:33]
	ds_read_b128 v[230:233], v93 offset:6144
	ds_read_b128 v[154:157], v141 offset:6144
	v_lshl_add_u64 v[166:167], v[132:133], 0, s[38:39]
	global_load_dwordx2 v[126:127], v[166:167], off
	global_load_dwordx2 v[128:129], v[166:167], off offset:2048
	s_mov_b32 s47, s42
	s_mov_b32 s42, s43
	s_mov_b32 s43, s44
	s_mov_b32 s44, s47
	s_waitcnt lgkmcnt(0)
	s_barrier
; #define MU_GLDS_A(buf, kt) do { _Pragma("unroll") for (int i = 0; i < NMU; ++i) \
;         __builtin_amdgcn_global_load_lds((const unsigned*)((const char*)A + aoff[i] + (size_t)(kt) * 128), (PG8_LAS unsigned*)(MU_SA(buf) + wid * 1024 + i * 8192), 16, 0, 0); } while (0)
; #define MU_B_ISSUE(sb, kt) do { const char* kb_ = Bb + (size_t)(kt) * (64 * (size_t)RB); _Pragma("unroll") for (int j = 0; j < 8; ++j) { const char* p_ = kb_ + (size_t)j * RB; \
;         asm volatile("global_load_dwordx2 %0, %1, off" : "=&v"(sb[j]) : "v"(p_) : "memory"); } } while (0)
; #define MU_B_WAIT(sb, N) asm volatile("s_waitcnt vmcnt(%8)" : "+v"(sb[0]), "+v"(sb[1]), "+v"(sb[2]), "+v"(sb[3]), "+v"(sb[4]), "+v"(sb[5]), "+v"(sb[6]), "+v"(sb[7]) : "n"(N) : "memory")
; #define MU_G_LOAD(ga, kt) do { const PG8_LAS f32x4* gk_ = (const PG8_LAS f32x4*)(lds + GAIN_OFF) + 16 * (kt) + 2 * wid; const f32x4 ga_ = gk_[0], gb_ = gk_[1]; \
;         ga[0] = ga_[0]; ga[1] = ga_[1]; ga[2] = ga_[2]; ga[3] = ga_[3]; ga[4] = gb_[0]; ga[5] = gb_[1]; ga[6] = gb_[2]; ga[7] = gb_[3]; } while (0)
; #define MU_COMPUTE(buf) MU_COMPUTE_N(buf, NMU)
; #define MU_END(last) do { if (last) asm volatile("s_waitcnt vmcnt(0)" ::: "memory"); else asm volatile("s_waitcnt vmcnt(8)" ::: "memory"); \
;         asm volatile("s_waitcnt lgkmcnt(0)" ::: "memory"); __builtin_amdgcn_s_barrier(); asm volatile("" ::: "memory"); } while (0)
; template <int MODE>
; __device__ __forceinline__ void moe_unit(PG8_LAS unsigned char* lds, int e, int cb, int slot0  , int nv  , const bf16_t* A, const int* slot_tok,
;                                          const float* W0, const float* W1, bf16_t* OUT, const float* slot_rs  , const int* slot_dst) {
;     ...
;     for (int t = 0; t < nt; t += 2) {
;         if (t + 2 < nt) MU_B_WAIT(s1, 8); else MU_B_WAIT(s1, 0);
;         MU_G_LOAD(g0, t + 1); MU_B_WRITE(s1, 1, g0); __builtin_amdgcn_sched_barrier(0); MU_GLDS_A(1, t + 1); __builtin_amdgcn_sched_barrier(0);
;         if (t + 3 < nt) { MU_B_ISSUE(s1, t + 3); }
;         MU_COMPUTE(0);
;         MU_END(t + 3 >= nt);
;         if (t + 2 < nt) { MU_B_WAIT(s0, 8); MU_G_LOAD(g0, t + 2); MU_B_WRITE(s0, 0, g0); __builtin_amdgcn_sched_barrier(0); MU_GLDS_A(0, t + 2); __builtin_amdgcn_sched_barrier(0); }
;         if (t + 4 < nt) { MU_B_ISSUE(s0, t + 4); }
;         MU_COMPUTE(1);
;         MU_END(t + 4 >= nt);
	s_add_i32 s47, s44, s6
	s_add_u32 s30, s30, 0x80
	s_addc_u32 s31, s31, 0
	v_mfma_f32_16x16x32_bf16 v[78:81], v[142:145], v[218:221], v[78:81]
	v_mfma_f32_16x16x32_bf16 v[74:77], v[146:149], v[218:221], v[74:77]
	v_mfma_f32_16x16x32_bf16 v[70:73], v[150:153], v[218:221], v[70:73]
	v_mfma_f32_16x16x32_bf16 v[66:69], v[154:157], v[218:221], v[66:69]
	s_mov_b32 m0, s47
	s_nop 0
	global_load_lds_dwordx4 v86, s[30:31]
	v_mfma_f32_16x16x32_bf16 v[62:65], v[142:145], v[222:225], v[62:65]
	v_mfma_f32_16x16x32_bf16 v[58:61], v[146:149], v[222:225], v[58:61]
	v_mfma_f32_16x16x32_bf16 v[54:57], v[150:153], v[222:225], v[54:57]
	v_mfma_f32_16x16x32_bf16 v[50:53], v[154:157], v[222:225], v[50:53]
	s_add_i32 m0, s47, 0x2000
	s_nop 0
	global_load_lds_dwordx4 v134, s[30:31]
	v_mfma_f32_16x16x32_bf16 v[46:49], v[142:145], v[226:229], v[46:49]
	v_mfma_f32_16x16x32_bf16 v[42:45], v[146:149], v[226:229], v[42:45]
	v_mfma_f32_16x16x32_bf16 v[38:41], v[150:153], v[226:229], v[38:41]
	v_mfma_f32_16x16x32_bf16 v[34:37], v[154:157], v[226:229], v[34:37]
	s_add_i32 m0, s47, 0x4000
	s_nop 0
	global_load_lds_dwordx4 v136, s[30:31]
	v_mfma_f32_16x16x32_bf16 v[18:21], v[142:145], v[230:233], v[18:21]
	v_mfma_f32_16x16x32_bf16 v[22:25], v[146:149], v[230:233], v[22:25]
	v_mfma_f32_16x16x32_bf16 v[26:29], v[150:153], v[230:233], v[26:29]
	v_mfma_f32_16x16x32_bf16 v[30:33], v[154:157], v[230:233], v[30:33]
	s_add_i32 m0, s47, 0x6000
	s_nop 0
	global_load_lds_dwordx4 v138, s[30:31]
	s_add_i32 m0, s47, 0x8000
	s_nop 0
	global_load_lds_dwordx4 v140, s[30:31]
	s_waitcnt vmcnt(34)
	v_mul_f32_e32 v186, s12, v186
	v_mul_f32_e32 v187, s12, v187
	v_mul_f32_e32 v188, s13, v188
	v_mul_f32_e32 v189, s13, v189
	v_mul_f32_e32 v190, s14, v190
	v_mul_f32_e32 v191, s14, v191
	v_mul_f32_e32 v192, s15, v192
	v_mul_f32_e32 v193, s15, v193
	v_mul_f32_e32 v194, s16, v194
	v_mul_f32_e32 v195, s16, v195
	v_mul_f32_e32 v196, s17, v196
	v_mul_f32_e32 v197, s17, v197
	v_mul_f32_e32 v198, s18, v198
	v_mul_f32_e32 v199, s18, v199
	v_mul_f32_e32 v200, s19, v200
	v_mul_f32_e32 v201, s19, v201
	v_cvt_pk_bf16_f32 v158, v186, v188
	v_cvt_pk_bf16_f32 v159, v190, v192
	v_cvt_pk_bf16_f32 v160, v194, v196
	v_cvt_pk_bf16_f32 v161, v198, v200
	v_cvt_pk_bf16_f32 v162, v187, v189
	v_cvt_pk_bf16_f32 v163, v191, v193
	v_cvt_pk_bf16_f32 v164, v195, v197
	v_cvt_pk_bf16_f32 v165, v199, v201
	ds_write_b128 v1, v[158:161] offset:0
	ds_write_b128 v1, v[162:165] offset:128
	v_add_u32_e32 v91, s42, v135
	v_add_u32_e32 v93, s42, v137
	ds_read_b128 v[238:241], v139 offset:19456
	ds_read_b128 v[242:245], v139 offset:21504
	ds_read_b128 v[246:249], v139 offset:23552
	ds_read_b128 v[250:253], v139 offset:25600
	ds_read_b128 v[218:221], v91 offset:0
	ds_read_b128 v[222:225], v91 offset:2048
	ds_read_b128 v[226:229], v91 offset:4096
	ds_read_b128 v[230:233], v91 offset:6144
	s_waitcnt lgkmcnt(0)
	s_load_dwordx8 s[20:27], s[28:29], 0x0
	s_add_u32 s28, s28, 0x100
	s_addc_u32 s29, s29, 0
	v_mfma_f32_16x16x32_bf16 v[78:81], v[238:241], v[218:221], v[78:81]
	v_mfma_f32_16x16x32_bf16 v[74:77], v[242:245], v[218:221], v[74:77]
	v_mfma_f32_16x16x32_bf16 v[70:73], v[246:249], v[218:221], v[70:73]
	v_mfma_f32_16x16x32_bf16 v[66:69], v[250:253], v[218:221], v[66:69]
	ds_read_b128 v[218:221], v93 offset:0
	ds_read_b128 v[142:145], v141 offset:19456
	v_lshl_add_u64 v[132:133], v[132:133], 0, s[40:41]
	global_load_dwordx2 v[186:187], v[132:133], off
	global_load_dwordx2 v[188:189], v[132:133], off offset:2048
	v_mfma_f32_16x16x32_bf16 v[62:65], v[238:241], v[222:225], v[62:65]
	v_mfma_f32_16x16x32_bf16 v[58:61], v[242:245], v[222:225], v[58:61]
	v_mfma_f32_16x16x32_bf16 v[54:57], v[246:249], v[222:225], v[54:57]
	v_mfma_f32_16x16x32_bf16 v[50:53], v[250:253], v[222:225], v[50:53]
	ds_read_b128 v[222:225], v93 offset:2048
	ds_read_b128 v[146:149], v141 offset:21504
	v_lshl_add_u64 v[166:167], v[132:133], 0, s[34:35]
	global_load_dwordx2 v[190:191], v[166:167], off
	global_load_dwordx2 v[192:193], v[166:167], off offset:2048
	v_mfma_f32_16x16x32_bf16 v[46:49], v[238:241], v[226:229], v[46:49]
	v_mfma_f32_16x16x32_bf16 v[42:45], v[242:245], v[226:229], v[42:45]
	v_mfma_f32_16x16x32_bf16 v[38:41], v[246:249], v[226:229], v[38:41]
	v_mfma_f32_16x16x32_bf16 v[34:37], v[250:253], v[226:229], v[34:37]
	ds_read_b128 v[226:229], v93 offset:4096
	ds_read_b128 v[150:153], v141 offset:23552
	v_lshl_add_u64 v[166:167], v[132:133], 0, s[36:37]
	global_load_dwordx2 v[194:195], v[166:167], off
	global_load_dwordx2 v[196:197], v[166:167], off offset:2048
	v_mfma_f32_16x16x32_bf16 v[18:21], v[238:241], v[230:233], v[18:21]
	v_mfma_f32_16x16x32_bf16 v[22:25], v[242:245], v[230:233], v[22:25]
	v_mfma_f32_16x16x32_bf16 v[26:29], v[246:249], v[230:233], v[26:29]
	v_mfma_f32_16x16x32_bf16 v[30:33], v[250:253], v[230:233], v[30:33]
	ds_read_b128 v[230:233], v93 offset:6144
	ds_read_b128 v[154:157], v141 offset:25600
	v_lshl_add_u64 v[166:167], v[132:133], 0, s[38:39]
	global_load_dwordx2 v[198:199], v[166:167], off
	global_load_dwordx2 v[200:201], v[166:167], off offset:2048
	s_waitcnt vmcnt(21)
	s_mov_b32 s47, s42
	s_mov_b32 s42, s43
	s_mov_b32 s43, s44
	s_mov_b32 s44, s47
	s_waitcnt lgkmcnt(0)
	s_barrier
; #define MU_GLDS_A(buf, kt) do { _Pragma("unroll") for (int i = 0; i < NMU; ++i) \
;         __builtin_amdgcn_global_load_lds((const unsigned*)((const char*)A + aoff[i] + (size_t)(kt) * 128), (PG8_LAS unsigned*)(MU_SA(buf) + wid * 1024 + i * 8192), 16, 0, 0); } while (0)
; #define MU_B_ISSUE(sb, kt) do { const char* kb_ = Bb + (size_t)(kt) * (64 * (size_t)RB); _Pragma("unroll") for (int j = 0; j < 8; ++j) { const char* p_ = kb_ + (size_t)j * RB; \
;         asm volatile("global_load_dwordx2 %0, %1, off" : "=&v"(sb[j]) : "v"(p_) : "memory"); } } while (0)
; #define MU_B_WAIT(sb, N) asm volatile("s_waitcnt vmcnt(%8)" : "+v"(sb[0]), "+v"(sb[1]), "+v"(sb[2]), "+v"(sb[3]), "+v"(sb[4]), "+v"(sb[5]), "+v"(sb[6]), "+v"(sb[7]) : "n"(N) : "memory")
; #define MU_G_LOAD(ga, kt) do { const PG8_LAS f32x4* gk_ = (const PG8_LAS f32x4*)(lds + GAIN_OFF) + 16 * (kt) + 2 * wid; const f32x4 ga_ = gk_[0], gb_ = gk_[1]; \
;         ga[0] = ga_[0]; ga[1] = ga_[1]; ga[2] = ga_[2]; ga[3] = ga_[3]; ga[4] = gb_[0]; ga[5] = gb_[1]; ga[6] = gb_[2]; ga[7] = gb_[3]; } while (0)
; #define MU_COMPUTE(buf) MU_COMPUTE_N(buf, NMU)
; #define MU_END(last) do { if (last) asm volatile("s_waitcnt vmcnt(0)" ::: "memory"); else asm volatile("s_waitcnt vmcnt(8)" ::: "memory"); \
;         asm volatile("s_waitcnt lgkmcnt(0)" ::: "memory"); __builtin_amdgcn_s_barrier(); asm volatile("" ::: "memory"); } while (0)
; template <int MODE>
; __device__ __forceinline__ void moe_unit(PG8_LAS unsigned char* lds, int e, int cb, int slot0  , int nv  , const bf16_t* A, const int* slot_tok,
;                                          const float* W0, const float* W1, bf16_t* OUT, const float* slot_rs  , const int* slot_dst) {
;     ...
;     for (int t = 0; t < nt; t += 2) {
;         if (t + 2 < nt) MU_B_WAIT(s1, 8); else MU_B_WAIT(s1, 0);
;         MU_G_LOAD(g0, t + 1); MU_B_WRITE(s1, 1, g0); __builtin_amdgcn_sched_barrier(0); MU_GLDS_A(1, t + 1); __builtin_amdgcn_sched_barrier(0);
;         if (t + 3 < nt) { MU_B_ISSUE(s1, t + 3); }
;         MU_COMPUTE(0);
;         MU_END(t + 3 >= nt);
;         if (t + 2 < nt) { MU_B_WAIT(s0, 8); MU_G_LOAD(g0, t + 2); MU_B_WRITE(s0, 0, g0); __builtin_amdgcn_sched_barrier(0); MU_GLDS_A(0, t + 2); __builtin_amdgcn_sched_barrier(0); }
;         if (t + 4 < nt) { MU_B_ISSUE(s0, t + 4); }
;         MU_COMPUTE(1);
;         MU_END(t + 4 >= nt);
	s_add_i32 s47, s44, s6
	s_add_u32 s30, s30, 0x80
	s_addc_u32 s31, s31, 0
	v_mfma_f32_16x16x32_bf16 v[78:81], v[142:145], v[218:221], v[78:81]
	v_mfma_f32_16x16x32_bf16 v[74:77], v[146:149], v[218:221], v[74:77]
	v_mfma_f32_16x16x32_bf16 v[70:73], v[150:153], v[218:221], v[70:73]
	v_mfma_f32_16x16x32_bf16 v[66:69], v[154:157], v[218:221], v[66:69]
	s_mov_b32 m0, s47
	s_nop 0
	global_load_lds_dwordx4 v86, s[30:31]
	v_mfma_f32_16x16x32_bf16 v[62:65], v[142:145], v[222:225], v[62:65]
	v_mfma_f32_16x16x32_bf16 v[58:61], v[146:149], v[222:225], v[58:61]
	v_mfma_f32_16x16x32_bf16 v[54:57], v[150:153], v[222:225], v[54:57]
	v_mfma_f32_16x16x32_bf16 v[50:53], v[154:157], v[222:225], v[50:53]
	s_add_i32 m0, s47, 0x2000
	s_nop 0
	global_load_lds_dwordx4 v134, s[30:31]
	v_mfma_f32_16x16x32_bf16 v[46:49], v[142:145], v[226:229], v[46:49]
	v_mfma_f32_16x16x32_bf16 v[42:45], v[146:149], v[226:229], v[42:45]
	v_mfma_f32_16x16x32_bf16 v[38:41], v[150:153], v[226:229], v[38:41]
	v_mfma_f32_16x16x32_bf16 v[34:37], v[154:157], v[226:229], v[34:37]
	s_add_i32 m0, s47, 0x4000
	s_nop 0
	global_load_lds_dwordx4 v136, s[30:31]
	v_mfma_f32_16x16x32_bf16 v[18:21], v[142:145], v[230:233], v[18:21]
	v_mfma_f32_16x16x32_bf16 v[22:25], v[146:149], v[230:233], v[22:25]
	v_mfma_f32_16x16x32_bf16 v[26:29], v[150:153], v[230:233], v[26:29]
	v_mfma_f32_16x16x32_bf16 v[30:33], v[154:157], v[230:233], v[30:33]
	s_add_i32 m0, s47, 0x6000
	s_nop 0
	global_load_lds_dwordx4 v138, s[30:31]
	s_add_i32 m0, s47, 0x8000
	s_nop 0
	global_load_lds_dwordx4 v140, s[30:31]
	v_mul_f32_e32 v202, s20, v202
	v_mul_f32_e32 v203, s20, v203
	v_mul_f32_e32 v204, s21, v204
	v_mul_f32_e32 v205, s21, v205
	v_mul_f32_e32 v206, s22, v206
	v_mul_f32_e32 v207, s22, v207
	v_mul_f32_e32 v208, s23, v208
	v_mul_f32_e32 v209, s23, v209
	v_mul_f32_e32 v210, s24, v210
	v_mul_f32_e32 v211, s24, v211
	v_mul_f32_e32 v212, s25, v212
	v_mul_f32_e32 v213, s25, v213
	v_mul_f32_e32 v214, s26, v214
	v_mul_f32_e32 v215, s26, v215
	v_mul_f32_e32 v216, s27, v216
	v_mul_f32_e32 v217, s27, v217
	v_cvt_pk_bf16_f32 v158, v202, v204
	v_cvt_pk_bf16_f32 v159, v206, v208
	v_cvt_pk_bf16_f32 v160, v210, v212
	v_cvt_pk_bf16_f32 v161, v214, v216
	v_cvt_pk_bf16_f32 v162, v203, v205
	v_cvt_pk_bf16_f32 v163, v207, v209
	v_cvt_pk_bf16_f32 v164, v211, v213
	v_cvt_pk_bf16_f32 v165, v215, v217
	ds_write_b128 v1, v[158:161] offset:19456
	ds_write_b128 v1, v[162:165] offset:19584
	v_add_u32_e32 v91, s42, v135
	v_add_u32_e32 v93, s42, v137
	ds_read_b128 v[238:241], v139 offset:0
	ds_read_b128 v[242:245], v139 offset:2048
	ds_read_b128 v[246:249], v139 offset:4096
	ds_read_b128 v[250:253], v139 offset:6144
	ds_read_b128 v[218:221], v91 offset:0
	ds_read_b128 v[222:225], v91 offset:2048
	ds_read_b128 v[226:229], v91 offset:4096
	ds_read_b128 v[230:233], v91 offset:6144
	s_waitcnt lgkmcnt(0)
	s_load_dwordx8 s[12:19], s[28:29], 0x0
	s_add_u32 s28, s28, 0x100
	s_addc_u32 s29, s29, 0
	v_mfma_f32_16x16x32_bf16 v[78:81], v[238:241], v[218:221], v[78:81]
	v_mfma_f32_16x16x32_bf16 v[74:77], v[242:245], v[218:221], v[74:77]
	v_mfma_f32_16x16x32_bf16 v[70:73], v[246:249], v[218:221], v[70:73]
	v_mfma_f32_16x16x32_bf16 v[66:69], v[250:253], v[218:221], v[66:69]
	ds_read_b128 v[218:221], v93 offset:0
	ds_read_b128 v[142:145], v141 offset:0
	v_lshl_add_u64 v[132:133], v[132:133], 0, s[40:41]
	global_load_dwordx2 v[202:203], v[132:133], off
	global_load_dwordx2 v[204:205], v[132:133], off offset:2048
	v_mfma_f32_16x16x32_bf16 v[62:65], v[238:241], v[222:225], v[62:65]
	v_mfma_f32_16x16x32_bf16 v[58:61], v[242:245], v[222:225], v[58:61]
	v_mfma_f32_16x16x32_bf16 v[54:57], v[246:249], v[222:225], v[54:57]
	v_mfma_f32_16x16x32_bf16 v[50:53], v[250:253], v[222:225], v[50:53]
	ds_read_b128 v[222:225], v93 offset:2048
	ds_read_b128 v[146:149], v141 offset:2048
	v_lshl_add_u64 v[166:167], v[132:133], 0, s[34:35]
	global_load_dwordx2 v[206:207], v[166:167], off
	global_load_dwordx2 v[208:209], v[166:167], off offset:2048
	v_mfma_f32_16x16x32_bf16 v[46:49], v[238:241], v[226:229], v[46:49]
	v_mfma_f32_16x16x32_bf16 v[42:45], v[242:245], v[226:229], v[42:45]
	v_mfma_f32_16x16x32_bf16 v[38:41], v[246:249], v[226:229], v[38:41]
	v_mfma_f32_16x16x32_bf16 v[34:37], v[250:253], v[226:229], v[34:37]
	ds_read_b128 v[226:229], v93 offset:4096
	ds_read_b128 v[150:153], v141 offset:4096
	v_lshl_add_u64 v[166:167], v[132:133], 0, s[36:37]
	global_load_dwordx2 v[210:211], v[166:167], off
	global_load_dwordx2 v[212:213], v[166:167], off offset:2048
	v_mfma_f32_16x16x32_bf16 v[18:21], v[238:241], v[230:233], v[18:21]
	v_mfma_f32_16x16x32_bf16 v[22:25], v[242:245], v[230:233], v[22:25]
	v_mfma_f32_16x16x32_bf16 v[26:29], v[246:249], v[230:233], v[26:29]
	v_mfma_f32_16x16x32_bf16 v[30:33], v[250:253], v[230:233], v[30:33]
	ds_read_b128 v[230:233], v93 offset:6144
	ds_read_b128 v[154:157], v141 offset:6144
	v_lshl_add_u64 v[166:167], v[132:133], 0, s[38:39]
	global_load_dwordx2 v[214:215], v[166:167], off
	global_load_dwordx2 v[216:217], v[166:167], off offset:2048
	s_waitcnt vmcnt(21)
	s_mov_b32 s47, s42
	s_mov_b32 s42, s43
	s_mov_b32 s43, s44
	s_mov_b32 s44, s47
	s_waitcnt lgkmcnt(0)
	s_barrier
; #define MU_GLDS_A(buf, kt) do { _Pragma("unroll") for (int i = 0; i < NMU; ++i) \
;         __builtin_amdgcn_global_load_lds((const unsigned*)((const char*)A + aoff[i] + (size_t)(kt) * 128), (PG8_LAS unsigned*)(MU_SA(buf) + wid * 1024 + i * 8192), 16, 0, 0); } while (0)
; #define MU_B_ISSUE(sb, kt) do { const char* kb_ = Bb + (size_t)(kt) * (64 * (size_t)RB); _Pragma("unroll") for (int j = 0; j < 8; ++j) { const char* p_ = kb_ + (size_t)j * RB; \
;         asm volatile("global_load_dwordx2 %0, %1, off" : "=&v"(sb[j]) : "v"(p_) : "memory"); } } while (0)
; #define MU_B_WAIT(sb, N) asm volatile("s_waitcnt vmcnt(%8)" : "+v"(sb[0]), "+v"(sb[1]), "+v"(sb[2]), "+v"(sb[3]), "+v"(sb[4]), "+v"(sb[5]), "+v"(sb[6]), "+v"(sb[7]) : "n"(N) : "memory")
; #define MU_G_LOAD(ga, kt) do { const PG8_LAS f32x4* gk_ = (const PG8_LAS f32x4*)(lds + GAIN_OFF) + 16 * (kt) + 2 * wid; const f32x4 ga_ = gk_[0], gb_ = gk_[1]; \
;         ga[0] = ga_[0]; ga[1] = ga_[1]; ga[2] = ga_[2]; ga[3] = ga_[3]; ga[4] = gb_[0]; ga[5] = gb_[1]; ga[6] = gb_[2]; ga[7] = gb_[3]; } while (0)
; #define MU_COMPUTE(buf) MU_COMPUTE_N(buf, NMU)
; #define MU_END(last) do { if (last) asm volatile("s_waitcnt vmcnt(0)" ::: "memory"); else asm volatile("s_waitcnt vmcnt(8)" ::: "memory"); \
;         asm volatile("s_waitcnt lgkmcnt(0)" ::: "memory"); __builtin_amdgcn_s_barrier(); asm volatile("" ::: "memory"); } while (0)
; template <int MODE>
; __device__ __forceinline__ void moe_unit(PG8_LAS unsigned char* lds, int e, int cb, int slot0  , int nv  , const bf16_t* A, const int* slot_tok,
;                                          const float* W0, const float* W1, bf16_t* OUT, const float* slot_rs  , const int* slot_dst) {
;     ...
;     for (int t = 0; t < nt; t += 2) {
;         if (t + 2 < nt) MU_B_WAIT(s1, 8); else MU_B_WAIT(s1, 0);
;         MU_G_LOAD(g0, t + 1); MU_B_WRITE(s1, 1, g0); __builtin_amdgcn_sched_barrier(0); MU_GLDS_A(1, t + 1); __builtin_amdgcn_sched_barrier(0);
;         if (t + 3 < nt) { MU_B_ISSUE(s1, t + 3); }
;         MU_COMPUTE(0);
;         MU_END(t + 3 >= nt);
;         if (t + 2 < nt) { MU_B_WAIT(s0, 8); MU_G_LOAD(g0, t + 2); MU_B_WRITE(s0, 0, g0); __builtin_amdgcn_sched_barrier(0); MU_GLDS_A(0, t + 2); __builtin_amdgcn_sched_barrier(0); }
;         if (t + 4 < nt) { MU_B_ISSUE(s0, t + 4); }
;         MU_COMPUTE(1);
;         MU_END(t + 4 >= nt);
	s_add_i32 s47, s44, s6
	s_add_u32 s30, s30, 0x80
	s_addc_u32 s31, s31, 0
	v_mfma_f32_16x16x32_bf16 v[78:81], v[142:145], v[218:221], v[78:81]
	v_mfma_f32_16x16x32_bf16 v[74:77], v[146:149], v[218:221], v[74:77]
	v_mfma_f32_16x16x32_bf16 v[70:73], v[150:153], v[218:221], v[70:73]
	v_mfma_f32_16x16x32_bf16 v[66:69], v[154:157], v[218:221], v[66:69]
	s_mov_b32 m0, s47
	s_nop 0
	global_load_lds_dwordx4 v86, s[30:31]
	v_mfma_f32_16x16x32_bf16 v[62:65], v[142:145], v[222:225], v[62:65]
	v_mfma_f32_16x16x32_bf16 v[58:61], v[146:149], v[222:225], v[58:61]
	v_mfma_f32_16x16x32_bf16 v[54:57], v[150:153], v[222:225], v[54:57]
	v_mfma_f32_16x16x32_bf16 v[50:53], v[154:157], v[222:225], v[50:53]
	s_add_i32 m0, s47, 0x2000
	s_nop 0
	global_load_lds_dwordx4 v134, s[30:31]
	v_mfma_f32_16x16x32_bf16 v[46:49], v[142:145], v[226:229], v[46:49]
	v_mfma_f32_16x16x32_bf16 v[42:45], v[146:149], v[226:229], v[42:45]
	v_mfma_f32_16x16x32_bf16 v[38:41], v[150:153], v[226:229], v[38:41]
	v_mfma_f32_16x16x32_bf16 v[34:37], v[154:157], v[226:229], v[34:37]
	s_add_i32 m0, s47, 0x4000
	s_nop 0
	global_load_lds_dwordx4 v136, s[30:31]
	v_mfma_f32_16x16x32_bf16 v[18:21], v[142:145], v[230:233], v[18:21]
	v_mfma_f32_16x16x32_bf16 v[22:25], v[146:149], v[230:233], v[22:25]
	v_mfma_f32_16x16x32_bf16 v[26:29], v[150:153], v[230:233], v[26:29]
	v_mfma_f32_16x16x32_bf16 v[30:33], v[154:157], v[230:233], v[30:33]
	s_add_i32 m0, s47, 0x6000
	s_nop 0
	global_load_lds_dwordx4 v138, s[30:31]
	s_add_i32 m0, s47, 0x8000
	s_nop 0
	global_load_lds_dwordx4 v140, s[30:31]
	v_mul_f32_e32 v98, s12, v98
	v_mul_f32_e32 v99, s12, v99
	v_mul_f32_e32 v100, s13, v100
	v_mul_f32_e32 v101, s13, v101
	v_mul_f32_e32 v102, s14, v102
	v_mul_f32_e32 v103, s14, v103
	v_mul_f32_e32 v104, s15, v104
	v_mul_f32_e32 v105, s15, v105
	v_mul_f32_e32 v106, s16, v106
	v_mul_f32_e32 v107, s16, v107
	v_mul_f32_e32 v108, s17, v108
	v_mul_f32_e32 v109, s17, v109
	v_mul_f32_e32 v110, s18, v110
	v_mul_f32_e32 v111, s18, v111
	v_mul_f32_e32 v112, s19, v112
	v_mul_f32_e32 v113, s19, v113
	v_cvt_pk_bf16_f32 v158, v98, v100
	v_cvt_pk_bf16_f32 v159, v102, v104
	v_cvt_pk_bf16_f32 v160, v106, v108
	v_cvt_pk_bf16_f32 v161, v110, v112
	v_cvt_pk_bf16_f32 v162, v99, v101
	v_cvt_pk_bf16_f32 v163, v103, v105
	v_cvt_pk_bf16_f32 v164, v107, v109
	v_cvt_pk_bf16_f32 v165, v111, v113
	ds_write_b128 v1, v[158:161] offset:0
	ds_write_b128 v1, v[162:165] offset:128
	v_add_u32_e32 v91, s42, v135
	v_add_u32_e32 v93, s42, v137
	ds_read_b128 v[238:241], v139 offset:19456
	ds_read_b128 v[242:245], v139 offset:21504
	ds_read_b128 v[246:249], v139 offset:23552
	ds_read_b128 v[250:253], v139 offset:25600
	ds_read_b128 v[218:221], v91 offset:0
	ds_read_b128 v[222:225], v91 offset:2048
	ds_read_b128 v[226:229], v91 offset:4096
	ds_read_b128 v[230:233], v91 offset:6144
	s_waitcnt lgkmcnt(0)
	s_load_dwordx8 s[20:27], s[28:29], 0x0
	s_add_u32 s28, s28, 0x100
	s_addc_u32 s29, s29, 0
	v_mfma_f32_16x16x32_bf16 v[78:81], v[238:241], v[218:221], v[78:81]
	v_mfma_f32_16x16x32_bf16 v[74:77], v[242:245], v[218:221], v[74:77]
	v_mfma_f32_16x16x32_bf16 v[70:73], v[246:249], v[218:221], v[70:73]
	v_mfma_f32_16x16x32_bf16 v[66:69], v[250:253], v[218:221], v[66:69]
	ds_read_b128 v[218:221], v93 offset:0
	ds_read_b128 v[142:145], v141 offset:19456
	v_lshl_add_u64 v[132:133], v[132:133], 0, s[40:41]
	global_load_dwordx2 v[98:99], v[132:133], off
	global_load_dwordx2 v[100:101], v[132:133], off offset:2048
	v_mfma_f32_16x16x32_bf16 v[62:65], v[238:241], v[222:225], v[62:65]
	v_mfma_f32_16x16x32_bf16 v[58:61], v[242:245], v[222:225], v[58:61]
	v_mfma_f32_16x16x32_bf16 v[54:57], v[246:249], v[222:225], v[54:57]
	v_mfma_f32_16x16x32_bf16 v[50:53], v[250:253], v[222:225], v[50:53]
	ds_read_b128 v[222:225], v93 offset:2048
	ds_read_b128 v[146:149], v141 offset:21504
	v_lshl_add_u64 v[166:167], v[132:133], 0, s[34:35]
	global_load_dwordx2 v[102:103], v[166:167], off
	global_load_dwordx2 v[104:105], v[166:167], off offset:2048
	v_mfma_f32_16x16x32_bf16 v[46:49], v[238:241], v[226:229], v[46:49]
	v_mfma_f32_16x16x32_bf16 v[42:45], v[242:245], v[226:229], v[42:45]
	v_mfma_f32_16x16x32_bf16 v[38:41], v[246:249], v[226:229], v[38:41]
	v_mfma_f32_16x16x32_bf16 v[34:37], v[250:253], v[226:229], v[34:37]
	ds_read_b128 v[226:229], v93 offset:4096
	ds_read_b128 v[150:153], v141 offset:23552
	v_lshl_add_u64 v[166:167], v[132:133], 0, s[36:37]
	global_load_dwordx2 v[106:107], v[166:167], off
	global_load_dwordx2 v[108:109], v[166:167], off offset:2048
	v_mfma_f32_16x16x32_bf16 v[18:21], v[238:241], v[230:233], v[18:21]
	v_mfma_f32_16x16x32_bf16 v[22:25], v[242:245], v[230:233], v[22:25]
	v_mfma_f32_16x16x32_bf16 v[26:29], v[246:249], v[230:233], v[26:29]
	v_mfma_f32_16x16x32_bf16 v[30:33], v[250:253], v[230:233], v[30:33]
	ds_read_b128 v[230:233], v93 offset:6144
	ds_read_b128 v[154:157], v141 offset:25600
	v_lshl_add_u64 v[166:167], v[132:133], 0, s[38:39]
	global_load_dwordx2 v[110:111], v[166:167], off
	global_load_dwordx2 v[112:113], v[166:167], off offset:2048
	s_waitcnt vmcnt(21)
	s_mov_b32 s47, s42
	s_mov_b32 s42, s43
	s_mov_b32 s43, s44
	s_mov_b32 s44, s47
	s_waitcnt lgkmcnt(0)
	s_barrier
	s_mov_b32 s46, 13
; #define MU_GLDS_A(buf, kt) do { _Pragma("unroll") for (int i = 0; i < NMU; ++i) \
;         __builtin_amdgcn_global_load_lds((const unsigned*)((const char*)A + aoff[i] + (size_t)(kt) * 128), (PG8_LAS unsigned*)(MU_SA(buf) + wid * 1024 + i * 8192), 16, 0, 0); } while (0)
; #define MU_B_ISSUE(sb, kt) do { const char* kb_ = Bb + (size_t)(kt) * (64 * (size_t)RB); _Pragma("unroll") for (int j = 0; j < 8; ++j) { const char* p_ = kb_ + (size_t)j * RB; \
;         asm volatile("global_load_dwordx2 %0, %1, off" : "=&v"(sb[j]) : "v"(p_) : "memory"); } } while (0)
; #define MU_B_WAIT(sb, N) asm volatile("s_waitcnt vmcnt(%8)" : "+v"(sb[0]), "+v"(sb[1]), "+v"(sb[2]), "+v"(sb[3]), "+v"(sb[4]), "+v"(sb[5]), "+v"(sb[6]), "+v"(sb[7]) : "n"(N) : "memory")
; #define MU_G_LOAD(ga, kt) do { const PG8_LAS f32x4* gk_ = (const PG8_LAS f32x4*)(lds + GAIN_OFF) + 16 * (kt) + 2 * wid; const f32x4 ga_ = gk_[0], gb_ = gk_[1]; \
;         ga[0] = ga_[0]; ga[1] = ga_[1]; ga[2] = ga_[2]; ga[3] = ga_[3]; ga[4] = gb_[0]; ga[5] = gb_[1]; ga[6] = gb_[2]; ga[7] = gb_[3]; } while (0)
; #define MU_COMPUTE(buf) MU_COMPUTE_N(buf, NMU)
; #define MU_END(last) do { if (last) asm volatile("s_waitcnt vmcnt(0)" ::: "memory"); else asm volatile("s_waitcnt vmcnt(8)" ::: "memory"); \
;         asm volatile("s_waitcnt lgkmcnt(0)" ::: "memory"); __builtin_amdgcn_s_barrier(); asm volatile("" ::: "memory"); } while (0)
; template <int MODE>
; __device__ __forceinline__ void moe_unit(PG8_LAS unsigned char* lds, int e, int cb, int slot0  , int nv  , const bf16_t* A, const int* slot_tok,
;                                          const float* W0, const float* W1, bf16_t* OUT, const float* slot_rs  , const int* slot_dst) {
;     ...
;     for (int t = 0; t < nt; t += 2) {
;         if (t + 2 < nt) MU_B_WAIT(s1, 8); else MU_B_WAIT(s1, 0);
;         MU_G_LOAD(g0, t + 1); MU_B_WRITE(s1, 1, g0); __builtin_amdgcn_sched_barrier(0); MU_GLDS_A(1, t + 1); __builtin_amdgcn_sched_barrier(0);
;         if (t + 3 < nt) { MU_B_ISSUE(s1, t + 3); }
;         MU_COMPUTE(0);
;         MU_END(t + 3 >= nt);
;         if (t + 2 < nt) { MU_B_WAIT(s0, 8); MU_G_LOAD(g0, t + 2); MU_B_WRITE(s0, 0, g0); __builtin_amdgcn_sched_barrier(0); MU_GLDS_A(0, t + 2); __builtin_amdgcn_sched_barrier(0); }
;         if (t + 4 < nt) { MU_B_ISSUE(s0, t + 4); }
;         MU_COMPUTE(1);
;         MU_END(t + 4 >= nt);
.Lmu_loop_Y4:
	s_add_i32 s47, s44, s6
	s_add_u32 s30, s30, 0x80
	s_addc_u32 s31, s31, 0
	v_mfma_f32_16x16x32_bf16 v[78:81], v[142:145], v[218:221], v[78:81]
	v_mfma_f32_16x16x32_bf16 v[74:77], v[146:149], v[218:221], v[74:77]
	v_mfma_f32_16x16x32_bf16 v[70:73], v[150:153], v[218:221], v[70:73]
	v_mfma_f32_16x16x32_bf16 v[66:69], v[154:157], v[218:221], v[66:69]
	s_mov_b32 m0, s47
	s_nop 0
	global_load_lds_dwordx4 v86, s[30:31]
	v_mfma_f32_16x16x32_bf16 v[62:65], v[142:145], v[222:225], v[62:65]
	v_mfma_f32_16x16x32_bf16 v[58:61], v[146:149], v[222:225], v[58:61]
	v_mfma_f32_16x16x32_bf16 v[54:57], v[150:153], v[222:225], v[54:57]
	v_mfma_f32_16x16x32_bf16 v[50:53], v[154:157], v[222:225], v[50:53]
	s_add_i32 m0, s47, 0x2000
	s_nop 0
	global_load_lds_dwordx4 v134, s[30:31]
	v_mfma_f32_16x16x32_bf16 v[46:49], v[142:145], v[226:229], v[46:49]
	v_mfma_f32_16x16x32_bf16 v[42:45], v[146:149], v[226:229], v[42:45]
	v_mfma_f32_16x16x32_bf16 v[38:41], v[150:153], v[226:229], v[38:41]
	v_mfma_f32_16x16x32_bf16 v[34:37], v[154:157], v[226:229], v[34:37]
	s_add_i32 m0, s47, 0x4000
	s_nop 0
	global_load_lds_dwordx4 v136, s[30:31]
	v_mfma_f32_16x16x32_bf16 v[18:21], v[142:145], v[230:233], v[18:21]
	v_mfma_f32_16x16x32_bf16 v[22:25], v[146:149], v[230:233], v[22:25]
	v_mfma_f32_16x16x32_bf16 v[26:29], v[150:153], v[230:233], v[26:29]
	v_mfma_f32_16x16x32_bf16 v[30:33], v[154:157], v[230:233], v[30:33]
	s_add_i32 m0, s47, 0x6000
	s_nop 0
	global_load_lds_dwordx4 v138, s[30:31]
	s_add_i32 m0, s47, 0x8000
	s_nop 0
	global_load_lds_dwordx4 v140, s[30:31]
	v_mul_f32_e32 v114, s20, v114
	v_mul_f32_e32 v115, s20, v115
	v_mul_f32_e32 v116, s21, v116
	v_mul_f32_e32 v117, s21, v117
	v_mul_f32_e32 v118, s22, v118
	v_mul_f32_e32 v119, s22, v119
	v_mul_f32_e32 v120, s23, v120
	v_mul_f32_e32 v121, s23, v121
	v_mul_f32_e32 v122, s24, v122
	v_mul_f32_e32 v123, s24, v123
	v_mul_f32_e32 v124, s25, v124
	v_mul_f32_e32 v125, s25, v125
	v_mul_f32_e32 v126, s26, v126
	v_mul_f32_e32 v127, s26, v127
	v_mul_f32_e32 v128, s27, v128
	v_mul_f32_e32 v129, s27, v129
	v_cvt_pk_bf16_f32 v158, v114, v116
	v_cvt_pk_bf16_f32 v159, v118, v120
	v_cvt_pk_bf16_f32 v160, v122, v124
	v_cvt_pk_bf16_f32 v161, v126, v128
	v_cvt_pk_bf16_f32 v162, v115, v117
	v_cvt_pk_bf16_f32 v163, v119, v121
	v_cvt_pk_bf16_f32 v164, v123, v125
	v_cvt_pk_bf16_f32 v165, v127, v129
	ds_write_b128 v1, v[158:161] offset:19456
	ds_write_b128 v1, v[162:165] offset:19584
	v_add_u32_e32 v91, s42, v135
	v_add_u32_e32 v93, s42, v137
	ds_read_b128 v[238:241], v139 offset:0
	ds_read_b128 v[242:245], v139 offset:2048
	ds_read_b128 v[246:249], v139 offset:4096
	ds_read_b128 v[250:253], v139 offset:6144
	ds_read_b128 v[218:221], v91 offset:0
	ds_read_b128 v[222:225], v91 offset:2048
	ds_read_b128 v[226:229], v91 offset:4096
	ds_read_b128 v[230:233], v91 offset:6144
	s_waitcnt lgkmcnt(0)
	s_load_dwordx8 s[12:19], s[28:29], 0x0
	s_add_u32 s28, s28, 0x100
	s_addc_u32 s29, s29, 0
	v_mfma_f32_16x16x32_bf16 v[78:81], v[238:241], v[218:221], v[78:81]
	v_mfma_f32_16x16x32_bf16 v[74:77], v[242:245], v[218:221], v[74:77]
	v_mfma_f32_16x16x32_bf16 v[70:73], v[246:249], v[218:221], v[70:73]
	v_mfma_f32_16x16x32_bf16 v[66:69], v[250:253], v[218:221], v[66:69]
	ds_read_b128 v[218:221], v93 offset:0
	ds_read_b128 v[142:145], v141 offset:0
	v_lshl_add_u64 v[132:133], v[132:133], 0, s[40:41]
	global_load_dwordx2 v[114:115], v[132:133], off
	global_load_dwordx2 v[116:117], v[132:133], off offset:2048
	v_mfma_f32_16x16x32_bf16 v[62:65], v[238:241], v[222:225], v[62:65]
	v_mfma_f32_16x16x32_bf16 v[58:61], v[242:245], v[222:225], v[58:61]
	v_mfma_f32_16x16x32_bf16 v[54:57], v[246:249], v[222:225], v[54:57]
	v_mfma_f32_16x16x32_bf16 v[50:53], v[250:253], v[222:225], v[50:53]
	ds_read_b128 v[222:225], v93 offset:2048
	ds_read_b128 v[146:149], v141 offset:2048
	v_lshl_add_u64 v[166:167], v[132:133], 0, s[34:35]
	global_load_dwordx2 v[118:119], v[166:167], off
	global_load_dwordx2 v[120:121], v[166:167], off offset:2048
	v_mfma_f32_16x16x32_bf16 v[46:49], v[238:241], v[226:229], v[46:49]
	v_mfma_f32_16x16x32_bf16 v[42:45], v[242:245], v[226:229], v[42:45]
	v_mfma_f32_16x16x32_bf16 v[38:41], v[246:249], v[226:229], v[38:41]
	v_mfma_f32_16x16x32_bf16 v[34:37], v[250:253], v[226:229], v[34:37]
	ds_read_b128 v[226:229], v93 offset:4096
	ds_read_b128 v[150:153], v141 offset:4096
	v_lshl_add_u64 v[166:167], v[132:133], 0, s[36:37]
	global_load_dwordx2 v[122:123], v[166:167], off
	global_load_dwordx2 v[124:125], v[166:167], off offset:2048
	v_mfma_f32_16x16x32_bf16 v[18:21], v[238:241], v[230:233], v[18:21]
	v_mfma_f32_16x16x32_bf16 v[22:25], v[242:245], v[230:233], v[22:25]
	v_mfma_f32_16x16x32_bf16 v[26:29], v[246:249], v[230:233], v[26:29]
	v_mfma_f32_16x16x32_bf16 v[30:33], v[250:253], v[230:233], v[30:33]
	ds_read_b128 v[230:233], v93 offset:6144
	ds_read_b128 v[154:157], v141 offset:6144
	v_lshl_add_u64 v[166:167], v[132:133], 0, s[38:39]
	global_load_dwordx2 v[126:127], v[166:167], off
	global_load_dwordx2 v[128:129], v[166:167], off offset:2048
	s_waitcnt vmcnt(21)
	s_mov_b32 s47, s42
	s_mov_b32 s42, s43
	s_mov_b32 s43, s44
	s_mov_b32 s44, s47
	s_waitcnt lgkmcnt(0)
	s_barrier
; #define MU_GLDS_A(buf, kt) do { _Pragma("unroll") for (int i = 0; i < NMU; ++i) \
;         __builtin_amdgcn_global_load_lds((const unsigned*)((const char*)A + aoff[i] + (size_t)(kt) * 128), (PG8_LAS unsigned*)(MU_SA(buf) + wid * 1024 + i * 8192), 16, 0, 0); } while (0)
; #define MU_B_ISSUE(sb, kt) do { const char* kb_ = Bb + (size_t)(kt) * (64 * (size_t)RB); _Pragma("unroll") for (int j = 0; j < 8; ++j) { const char* p_ = kb_ + (size_t)j * RB; \
;         asm volatile("global_load_dwordx2 %0, %1, off" : "=&v"(sb[j]) : "v"(p_) : "memory"); } } while (0)
; #define MU_B_WAIT(sb, N) asm volatile("s_waitcnt vmcnt(%8)" : "+v"(sb[0]), "+v"(sb[1]), "+v"(sb[2]), "+v"(sb[3]), "+v"(sb[4]), "+v"(sb[5]), "+v"(sb[6]), "+v"(sb[7]) : "n"(N) : "memory")
; #define MU_G_LOAD(ga, kt) do { const PG8_LAS f32x4* gk_ = (const PG8_LAS f32x4*)(lds + GAIN_OFF) + 16 * (kt) + 2 * wid; const f32x4 ga_ = gk_[0], gb_ = gk_[1]; \
;         ga[0] = ga_[0]; ga[1] = ga_[1]; ga[2] = ga_[2]; ga[3] = ga_[3]; ga[4] = gb_[0]; ga[5] = gb_[1]; ga[6] = gb_[2]; ga[7] = gb_[3]; } while (0)
; #define MU_COMPUTE(buf) MU_COMPUTE_N(buf, NMU)
; #define MU_END(last) do { if (last) asm volatile("s_waitcnt vmcnt(0)" ::: "memory"); else asm volatile("s_waitcnt vmcnt(8)" ::: "memory"); \
;         asm volatile("s_waitcnt lgkmcnt(0)" ::: "memory"); __builtin_amdgcn_s_barrier(); asm volatile("" ::: "memory"); } while (0)
; template <int MODE>
; __device__ __forceinline__ void moe_unit(PG8_LAS unsigned char* lds, int e, int cb, int slot0  , int nv  , const bf16_t* A, const int* slot_tok,
;                                          const float* W0, const float* W1, bf16_t* OUT, const float* slot_rs  , const int* slot_dst) {
;     ...
;     for (int t = 0; t < nt; t += 2) {
;         if (t + 2 < nt) MU_B_WAIT(s1, 8); else MU_B_WAIT(s1, 0);
;         MU_G_LOAD(g0, t + 1); MU_B_WRITE(s1, 1, g0); __builtin_amdgcn_sched_barrier(0); MU_GLDS_A(1, t + 1); __builtin_amdgcn_sched_barrier(0);
;         if (t + 3 < nt) { MU_B_ISSUE(s1, t + 3); }
;         MU_COMPUTE(0);
;         MU_END(t + 3 >= nt);
;         if (t + 2 < nt) { MU_B_WAIT(s0, 8); MU_G_LOAD(g0, t + 2); MU_B_WRITE(s0, 0, g0); __builtin_amdgcn_sched_barrier(0); MU_GLDS_A(0, t + 2); __builtin_amdgcn_sched_barrier(0); }
;         if (t + 4 < nt) { MU_B_ISSUE(s0, t + 4); }
;         MU_COMPUTE(1);
;         MU_END(t + 4 >= nt);
	s_add_i32 s47, s44, s6
	s_add_u32 s30, s30, 0x80
	s_addc_u32 s31, s31, 0
	v_mfma_f32_16x16x32_bf16 v[78:81], v[142:145], v[218:221], v[78:81]
	v_mfma_f32_16x16x32_bf16 v[74:77], v[146:149], v[218:221], v[74:77]
	v_mfma_f32_16x16x32_bf16 v[70:73], v[150:153], v[218:221], v[70:73]
	v_mfma_f32_16x16x32_bf16 v[66:69], v[154:157], v[218:221], v[66:69]
	s_mov_b32 m0, s47
	s_nop 0
	global_load_lds_dwordx4 v86, s[30:31]
	v_mfma_f32_16x16x32_bf16 v[62:65], v[142:145], v[222:225], v[62:65]
	v_mfma_f32_16x16x32_bf16 v[58:61], v[146:149], v[222:225], v[58:61]
	v_mfma_f32_16x16x32_bf16 v[54:57], v[150:153], v[222:225], v[54:57]
	v_mfma_f32_16x16x32_bf16 v[50:53], v[154:157], v[222:225], v[50:53]
	s_add_i32 m0, s47, 0x2000
	s_nop 0
	global_load_lds_dwordx4 v134, s[30:31]
	v_mfma_f32_16x16x32_bf16 v[46:49], v[142:145], v[226:229], v[46:49]
	v_mfma_f32_16x16x32_bf16 v[42:45], v[146:149], v[226:229], v[42:45]
	v_mfma_f32_16x16x32_bf16 v[38:41], v[150:153], v[226:229], v[38:41]
	v_mfma_f32_16x16x32_bf16 v[34:37], v[154:157], v[226:229], v[34:37]
	s_add_i32 m0, s47, 0x4000
	s_nop 0
	global_load_lds_dwordx4 v136, s[30:31]
	v_mfma_f32_16x16x32_bf16 v[18:21], v[142:145], v[230:233], v[18:21]
	v_mfma_f32_16x16x32_bf16 v[22:25], v[146:149], v[230:233], v[22:25]
	v_mfma_f32_16x16x32_bf16 v[26:29], v[150:153], v[230:233], v[26:29]
	v_mfma_f32_16x16x32_bf16 v[30:33], v[154:157], v[230:233], v[30:33]
	s_add_i32 m0, s47, 0x6000
	s_nop 0
	global_load_lds_dwordx4 v138, s[30:31]
	s_add_i32 m0, s47, 0x8000
	s_nop 0
	global_load_lds_dwordx4 v140, s[30:31]
	v_mul_f32_e32 v186, s12, v186
	v_mul_f32_e32 v187, s12, v187
	v_mul_f32_e32 v188, s13, v188
	v_mul_f32_e32 v189, s13, v189
	v_mul_f32_e32 v190, s14, v190
	v_mul_f32_e32 v191, s14, v191
	v_mul_f32_e32 v192, s15, v192
	v_mul_f32_e32 v193, s15, v193
	v_mul_f32_e32 v194, s16, v194
	v_mul_f32_e32 v195, s16, v195
	v_mul_f32_e32 v196, s17, v196
	v_mul_f32_e32 v197, s17, v197
	v_mul_f32_e32 v198, s18, v198
	v_mul_f32_e32 v199, s18, v199
	v_mul_f32_e32 v200, s19, v200
	v_mul_f32_e32 v201, s19, v201
	v_cvt_pk_bf16_f32 v158, v186, v188
	v_cvt_pk_bf16_f32 v159, v190, v192
	v_cvt_pk_bf16_f32 v160, v194, v196
	v_cvt_pk_bf16_f32 v161, v198, v200
	v_cvt_pk_bf16_f32 v162, v187, v189
	v_cvt_pk_bf16_f32 v163, v191, v193
	v_cvt_pk_bf16_f32 v164, v195, v197
	v_cvt_pk_bf16_f32 v165, v199, v201
	ds_write_b128 v1, v[158:161] offset:0
	ds_write_b128 v1, v[162:165] offset:128
	v_add_u32_e32 v91, s42, v135
	v_add_u32_e32 v93, s42, v137
	ds_read_b128 v[238:241], v139 offset:19456
	ds_read_b128 v[242:245], v139 offset:21504
	ds_read_b128 v[246:249], v139 offset:23552
	ds_read_b128 v[250:253], v139 offset:25600
	ds_read_b128 v[218:221], v91 offset:0
	ds_read_b128 v[222:225], v91 offset:2048
	ds_read_b128 v[226:229], v91 offset:4096
	ds_read_b128 v[230:233], v91 offset:6144
	s_waitcnt lgkmcnt(0)
	s_load_dwordx8 s[20:27], s[28:29], 0x0
	s_add_u32 s28, s28, 0x100
	s_addc_u32 s29, s29, 0
	v_mfma_f32_16x16x32_bf16 v[78:81], v[238:241], v[218:221], v[78:81]
	v_mfma_f32_16x16x32_bf16 v[74:77], v[242:245], v[218:221], v[74:77]
	v_mfma_f32_16x16x32_bf16 v[70:73], v[246:249], v[218:221], v[70:73]
	v_mfma_f32_16x16x32_bf16 v[66:69], v[250:253], v[218:221], v[66:69]
	ds_read_b128 v[218:221], v93 offset:0
	ds_read_b128 v[142:145], v141 offset:19456
	v_lshl_add_u64 v[132:133], v[132:133], 0, s[40:41]
	global_load_dwordx2 v[186:187], v[132:133], off
	global_load_dwordx2 v[188:189], v[132:133], off offset:2048
	v_mfma_f32_16x16x32_bf16 v[62:65], v[238:241], v[222:225], v[62:65]
	v_mfma_f32_16x16x32_bf16 v[58:61], v[242:245], v[222:225], v[58:61]
	v_mfma_f32_16x16x32_bf16 v[54:57], v[246:249], v[222:225], v[54:57]
	v_mfma_f32_16x16x32_bf16 v[50:53], v[250:253], v[222:225], v[50:53]
	ds_read_b128 v[222:225], v93 offset:2048
	ds_read_b128 v[146:149], v141 offset:21504
	v_lshl_add_u64 v[166:167], v[132:133], 0, s[34:35]
	global_load_dwordx2 v[190:191], v[166:167], off
	global_load_dwordx2 v[192:193], v[166:167], off offset:2048
	v_mfma_f32_16x16x32_bf16 v[46:49], v[238:241], v[226:229], v[46:49]
	v_mfma_f32_16x16x32_bf16 v[42:45], v[242:245], v[226:229], v[42:45]
	v_mfma_f32_16x16x32_bf16 v[38:41], v[246:249], v[226:229], v[38:41]
	v_mfma_f32_16x16x32_bf16 v[34:37], v[250:253], v[226:229], v[34:37]
	ds_read_b128 v[226:229], v93 offset:4096
	ds_read_b128 v[150:153], v141 offset:23552
	v_lshl_add_u64 v[166:167], v[132:133], 0, s[36:37]
	global_load_dwordx2 v[194:195], v[166:167], off
	global_load_dwordx2 v[196:197], v[166:167], off offset:2048
	v_mfma_f32_16x16x32_bf16 v[18:21], v[238:241], v[230:233], v[18:21]
	v_mfma_f32_16x16x32_bf16 v[22:25], v[242:245], v[230:233], v[22:25]
	v_mfma_f32_16x16x32_bf16 v[26:29], v[246:249], v[230:233], v[26:29]
	v_mfma_f32_16x16x32_bf16 v[30:33], v[250:253], v[230:233], v[30:33]
	ds_read_b128 v[230:233], v93 offset:6144
	ds_read_b128 v[154:157], v141 offset:25600
	v_lshl_add_u64 v[166:167], v[132:133], 0, s[38:39]
	global_load_dwordx2 v[198:199], v[166:167], off
	global_load_dwordx2 v[200:201], v[166:167], off offset:2048
	s_waitcnt vmcnt(21)
	s_mov_b32 s47, s42
	s_mov_b32 s42, s43
	s_mov_b32 s43, s44
	s_mov_b32 s44, s47
	s_waitcnt lgkmcnt(0)
	s_barrier
; #define MU_GLDS_A(buf, kt) do { _Pragma("unroll") for (int i = 0; i < NMU; ++i) \
;         __builtin_amdgcn_global_load_lds((const unsigned*)((const char*)A + aoff[i] + (size_t)(kt) * 128), (PG8_LAS unsigned*)(MU_SA(buf) + wid * 1024 + i * 8192), 16, 0, 0); } while (0)
; #define MU_B_ISSUE(sb, kt) do { const char* kb_ = Bb + (size_t)(kt) * (64 * (size_t)RB); _Pragma("unroll") for (int j = 0; j < 8; ++j) { const char* p_ = kb_ + (size_t)j * RB; \
;         asm volatile("global_load_dwordx2 %0, %1, off" : "=&v"(sb[j]) : "v"(p_) : "memory"); } } while (0)
; #define MU_B_WAIT(sb, N) asm volatile("s_waitcnt vmcnt(%8)" : "+v"(sb[0]), "+v"(sb[1]), "+v"(sb[2]), "+v"(sb[3]), "+v"(sb[4]), "+v"(sb[5]), "+v"(sb[6]), "+v"(sb[7]) : "n"(N) : "memory")
; #define MU_G_LOAD(ga, kt) do { const PG8_LAS f32x4* gk_ = (const PG8_LAS f32x4*)(lds + GAIN_OFF) + 16 * (kt) + 2 * wid; const f32x4 ga_ = gk_[0], gb_ = gk_[1]; \
;         ga[0] = ga_[0]; ga[1] = ga_[1]; ga[2] = ga_[2]; ga[3] = ga_[3]; ga[4] = gb_[0]; ga[5] = gb_[1]; ga[6] = gb_[2]; ga[7] = gb_[3]; } while (0)
; #define MU_COMPUTE(buf) MU_COMPUTE_N(buf, NMU)
; #define MU_END(last) do { if (last) asm volatile("s_waitcnt vmcnt(0)" ::: "memory"); else asm volatile("s_waitcnt vmcnt(8)" ::: "memory"); \
;         asm volatile("s_waitcnt lgkmcnt(0)" ::: "memory"); __builtin_amdgcn_s_barrier(); asm volatile("" ::: "memory"); } while (0)
; template <int MODE>
; __device__ __forceinline__ void moe_unit(PG8_LAS unsigned char* lds, int e, int cb, int slot0  , int nv  , const bf16_t* A, const int* slot_tok,
;                                          const float* W0, const float* W1, bf16_t* OUT, const float* slot_rs  , const int* slot_dst) {
;     ...
;     for (int t = 0; t < nt; t += 2) {
;         if (t + 2 < nt) MU_B_WAIT(s1, 8); else MU_B_WAIT(s1, 0);
;         MU_G_LOAD(g0, t + 1); MU_B_WRITE(s1, 1, g0); __builtin_amdgcn_sched_barrier(0); MU_GLDS_A(1, t + 1); __builtin_amdgcn_sched_barrier(0);
;         if (t + 3 < nt) { MU_B_ISSUE(s1, t + 3); }
;         MU_COMPUTE(0);
;         MU_END(t + 3 >= nt);
;         if (t + 2 < nt) { MU_B_WAIT(s0, 8); MU_G_LOAD(g0, t + 2); MU_B_WRITE(s0, 0, g0); __builtin_amdgcn_sched_barrier(0); MU_GLDS_A(0, t + 2); __builtin_amdgcn_sched_barrier(0); }
;         if (t + 4 < nt) { MU_B_ISSUE(s0, t + 4); }
;         MU_COMPUTE(1);
;         MU_END(t + 4 >= nt);
	s_add_i32 s47, s44, s6
	s_add_u32 s30, s30, 0x80
	s_addc_u32 s31, s31, 0
	v_mfma_f32_16x16x32_bf16 v[78:81], v[142:145], v[218:221], v[78:81]
	v_mfma_f32_16x16x32_bf16 v[74:77], v[146:149], v[218:221], v[74:77]
	v_mfma_f32_16x16x32_bf16 v[70:73], v[150:153], v[218:221], v[70:73]
	v_mfma_f32_16x16x32_bf16 v[66:69], v[154:157], v[218:221], v[66:69]
	s_mov_b32 m0, s47
	s_nop 0
	global_load_lds_dwordx4 v86, s[30:31]
	v_mfma_f32_16x16x32_bf16 v[62:65], v[142:145], v[222:225], v[62:65]
	v_mfma_f32_16x16x32_bf16 v[58:61], v[146:149], v[222:225], v[58:61]
	v_mfma_f32_16x16x32_bf16 v[54:57], v[150:153], v[222:225], v[54:57]
	v_mfma_f32_16x16x32_bf16 v[50:53], v[154:157], v[222:225], v[50:53]
	s_add_i32 m0, s47, 0x2000
	s_nop 0
	global_load_lds_dwordx4 v134, s[30:31]
	v_mfma_f32_16x16x32_bf16 v[46:49], v[142:145], v[226:229], v[46:49]
	v_mfma_f32_16x16x32_bf16 v[42:45], v[146:149], v[226:229], v[42:45]
	v_mfma_f32_16x16x32_bf16 v[38:41], v[150:153], v[226:229], v[38:41]
	v_mfma_f32_16x16x32_bf16 v[34:37], v[154:157], v[226:229], v[34:37]
	s_add_i32 m0, s47, 0x4000
	s_nop 0
	global_load_lds_dwordx4 v136, s[30:31]
	v_mfma_f32_16x16x32_bf16 v[18:21], v[142:145], v[230:233], v[18:21]
	v_mfma_f32_16x16x32_bf16 v[22:25], v[146:149], v[230:233], v[22:25]
	v_mfma_f32_16x16x32_bf16 v[26:29], v[150:153], v[230:233], v[26:29]
	v_mfma_f32_16x16x32_bf16 v[30:33], v[154:157], v[230:233], v[30:33]
	s_add_i32 m0, s47, 0x6000
	s_nop 0
	global_load_lds_dwordx4 v138, s[30:31]
	s_add_i32 m0, s47, 0x8000
	s_nop 0
	global_load_lds_dwordx4 v140, s[30:31]
	v_mul_f32_e32 v202, s20, v202
	v_mul_f32_e32 v203, s20, v203
	v_mul_f32_e32 v204, s21, v204
	v_mul_f32_e32 v205, s21, v205
	v_mul_f32_e32 v206, s22, v206
	v_mul_f32_e32 v207, s22, v207
	v_mul_f32_e32 v208, s23, v208
	v_mul_f32_e32 v209, s23, v209
	v_mul_f32_e32 v210, s24, v210
	v_mul_f32_e32 v211, s24, v211
	v_mul_f32_e32 v212, s25, v212
	v_mul_f32_e32 v213, s25, v213
	v_mul_f32_e32 v214, s26, v214
	v_mul_f32_e32 v215, s26, v215
	v_mul_f32_e32 v216, s27, v216
	v_mul_f32_e32 v217, s27, v217
	v_cvt_pk_bf16_f32 v158, v202, v204
	v_cvt_pk_bf16_f32 v159, v206, v208
	v_cvt_pk_bf16_f32 v160, v210, v212
	v_cvt_pk_bf16_f32 v161, v214, v216
	v_cvt_pk_bf16_f32 v162, v203, v205
	v_cvt_pk_bf16_f32 v163, v207, v209
	v_cvt_pk_bf16_f32 v164, v211, v213
	v_cvt_pk_bf16_f32 v165, v215, v217
	ds_write_b128 v1, v[158:161] offset:19456
	ds_write_b128 v1, v[162:165] offset:19584
	v_add_u32_e32 v91, s42, v135
	v_add_u32_e32 v93, s42, v137
	ds_read_b128 v[238:241], v139 offset:0
	ds_read_b128 v[242:245], v139 offset:2048
	ds_read_b128 v[246:249], v139 offset:4096
	ds_read_b128 v[250:253], v139 offset:6144
	ds_read_b128 v[218:221], v91 offset:0
	ds_read_b128 v[222:225], v91 offset:2048
	ds_read_b128 v[226:229], v91 offset:4096
	ds_read_b128 v[230:233], v91 offset:6144
	s_waitcnt lgkmcnt(0)
	s_load_dwordx8 s[12:19], s[28:29], 0x0
	s_add_u32 s28, s28, 0x100
	s_addc_u32 s29, s29, 0
	v_mfma_f32_16x16x32_bf16 v[78:81], v[238:241], v[218:221], v[78:81]
	v_mfma_f32_16x16x32_bf16 v[74:77], v[242:245], v[218:221], v[74:77]
	v_mfma_f32_16x16x32_bf16 v[70:73], v[246:249], v[218:221], v[70:73]
	v_mfma_f32_16x16x32_bf16 v[66:69], v[250:253], v[218:221], v[66:69]
	ds_read_b128 v[218:221], v93 offset:0
	ds_read_b128 v[142:145], v141 offset:0
	v_lshl_add_u64 v[132:133], v[132:133], 0, s[40:41]
	global_load_dwordx2 v[202:203], v[132:133], off
	global_load_dwordx2 v[204:205], v[132:133], off offset:2048
	v_mfma_f32_16x16x32_bf16 v[62:65], v[238:241], v[222:225], v[62:65]
	v_mfma_f32_16x16x32_bf16 v[58:61], v[242:245], v[222:225], v[58:61]
	v_mfma_f32_16x16x32_bf16 v[54:57], v[246:249], v[222:225], v[54:57]
	v_mfma_f32_16x16x32_bf16 v[50:53], v[250:253], v[222:225], v[50:53]
	ds_read_b128 v[222:225], v93 offset:2048
	ds_read_b128 v[146:149], v141 offset:2048
	v_lshl_add_u64 v[166:167], v[132:133], 0, s[34:35]
	global_load_dwordx2 v[206:207], v[166:167], off
	global_load_dwordx2 v[208:209], v[166:167], off offset:2048
	v_mfma_f32_16x16x32_bf16 v[46:49], v[238:241], v[226:229], v[46:49]
	v_mfma_f32_16x16x32_bf16 v[42:45], v[242:245], v[226:229], v[42:45]
	v_mfma_f32_16x16x32_bf16 v[38:41], v[246:249], v[226:229], v[38:41]
	v_mfma_f32_16x16x32_bf16 v[34:37], v[250:253], v[226:229], v[34:37]
	ds_read_b128 v[226:229], v93 offset:4096
	ds_read_b128 v[150:153], v141 offset:4096
	v_lshl_add_u64 v[166:167], v[132:133], 0, s[36:37]
	global_load_dwordx2 v[210:211], v[166:167], off
	global_load_dwordx2 v[212:213], v[166:167], off offset:2048
	v_mfma_f32_16x16x32_bf16 v[18:21], v[238:241], v[230:233], v[18:21]
	v_mfma_f32_16x16x32_bf16 v[22:25], v[242:245], v[230:233], v[22:25]
	v_mfma_f32_16x16x32_bf16 v[26:29], v[246:249], v[230:233], v[26:29]
	v_mfma_f32_16x16x32_bf16 v[30:33], v[250:253], v[230:233], v[30:33]
	ds_read_b128 v[230:233], v93 offset:6144
	ds_read_b128 v[154:157], v141 offset:6144
	v_lshl_add_u64 v[166:167], v[132:133], 0, s[38:39]
	global_load_dwordx2 v[214:215], v[166:167], off
	global_load_dwordx2 v[216:217], v[166:167], off offset:2048
	s_waitcnt vmcnt(21)
	s_mov_b32 s47, s42
	s_mov_b32 s42, s43
	s_mov_b32 s43, s44
	s_mov_b32 s44, s47
	s_waitcnt lgkmcnt(0)
	s_barrier
; #define MU_GLDS_A(buf, kt) do { _Pragma("unroll") for (int i = 0; i < NMU; ++i) \
;         __builtin_amdgcn_global_load_lds((const unsigned*)((const char*)A + aoff[i] + (size_t)(kt) * 128), (PG8_LAS unsigned*)(MU_SA(buf) + wid * 1024 + i * 8192), 16, 0, 0); } while (0)
; #define MU_B_ISSUE(sb, kt) do { const char* kb_ = Bb + (size_t)(kt) * (64 * (size_t)RB); _Pragma("unroll") for (int j = 0; j < 8; ++j) { const char* p_ = kb_ + (size_t)j * RB; \
;         asm volatile("global_load_dwordx2 %0, %1, off" : "=&v"(sb[j]) : "v"(p_) : "memory"); } } while (0)
; #define MU_B_WAIT(sb, N) asm volatile("s_waitcnt vmcnt(%8)" : "+v"(sb[0]), "+v"(sb[1]), "+v"(sb[2]), "+v"(sb[3]), "+v"(sb[4]), "+v"(sb[5]), "+v"(sb[6]), "+v"(sb[7]) : "n"(N) : "memory")
; #define MU_G_LOAD(ga, kt) do { const PG8_LAS f32x4* gk_ = (const PG8_LAS f32x4*)(lds + GAIN_OFF) + 16 * (kt) + 2 * wid; const f32x4 ga_ = gk_[0], gb_ = gk_[1]; \
;         ga[0] = ga_[0]; ga[1] = ga_[1]; ga[2] = ga_[2]; ga[3] = ga_[3]; ga[4] = gb_[0]; ga[5] = gb_[1]; ga[6] = gb_[2]; ga[7] = gb_[3]; } while (0)
; #define MU_COMPUTE(buf) MU_COMPUTE_N(buf, NMU)
; #define MU_END(last) do { if (last) asm volatile("s_waitcnt vmcnt(0)" ::: "memory"); else asm volatile("s_waitcnt vmcnt(8)" ::: "memory"); \
;         asm volatile("s_waitcnt lgkmcnt(0)" ::: "memory"); __builtin_amdgcn_s_barrier(); asm volatile("" ::: "memory"); } while (0)
; template <int MODE>
; __device__ __forceinline__ void moe_unit(PG8_LAS unsigned char* lds, int e, int cb, int slot0  , int nv  , const bf16_t* A, const int* slot_tok,
;                                          const float* W0, const float* W1, bf16_t* OUT, const float* slot_rs  , const int* slot_dst) {
;     ...
;     for (int t = 0; t < nt; t += 2) {
;         if (t + 2 < nt) MU_B_WAIT(s1, 8); else MU_B_WAIT(s1, 0);
;         MU_G_LOAD(g0, t + 1); MU_B_WRITE(s1, 1, g0); __builtin_amdgcn_sched_barrier(0); MU_GLDS_A(1, t + 1); __builtin_amdgcn_sched_barrier(0);
;         if (t + 3 < nt) { MU_B_ISSUE(s1, t + 3); }
;         MU_COMPUTE(0);
;         MU_END(t + 3 >= nt);
;         if (t + 2 < nt) { MU_B_WAIT(s0, 8); MU_G_LOAD(g0, t + 2); MU_B_WRITE(s0, 0, g0); __builtin_amdgcn_sched_barrier(0); MU_GLDS_A(0, t + 2); __builtin_amdgcn_sched_barrier(0); }
;         if (t + 4 < nt) { MU_B_ISSUE(s0, t + 4); }
;         MU_COMPUTE(1);
;         MU_END(t + 4 >= nt);
	s_add_i32 s47, s44, s6
	s_add_u32 s30, s30, 0x80
	s_addc_u32 s31, s31, 0
	v_mfma_f32_16x16x32_bf16 v[78:81], v[142:145], v[218:221], v[78:81]
	v_mfma_f32_16x16x32_bf16 v[74:77], v[146:149], v[218:221], v[74:77]
	v_mfma_f32_16x16x32_bf16 v[70:73], v[150:153], v[218:221], v[70:73]
	v_mfma_f32_16x16x32_bf16 v[66:69], v[154:157], v[218:221], v[66:69]
	s_mov_b32 m0, s47
	s_nop 0
	global_load_lds_dwordx4 v86, s[30:31]
	v_mfma_f32_16x16x32_bf16 v[62:65], v[142:145], v[222:225], v[62:65]
	v_mfma_f32_16x16x32_bf16 v[58:61], v[146:149], v[222:225], v[58:61]
	v_mfma_f32_16x16x32_bf16 v[54:57], v[150:153], v[222:225], v[54:57]
	v_mfma_f32_16x16x32_bf16 v[50:53], v[154:157], v[222:225], v[50:53]
	s_add_i32 m0, s47, 0x2000
	s_nop 0
	global_load_lds_dwordx4 v134, s[30:31]
	v_mfma_f32_16x16x32_bf16 v[46:49], v[142:145], v[226:229], v[46:49]
	v_mfma_f32_16x16x32_bf16 v[42:45], v[146:149], v[226:229], v[42:45]
	v_mfma_f32_16x16x32_bf16 v[38:41], v[150:153], v[226:229], v[38:41]
	v_mfma_f32_16x16x32_bf16 v[34:37], v[154:157], v[226:229], v[34:37]
	s_add_i32 m0, s47, 0x4000
	s_nop 0
	global_load_lds_dwordx4 v136, s[30:31]
	v_mfma_f32_16x16x32_bf16 v[18:21], v[142:145], v[230:233], v[18:21]
	v_mfma_f32_16x16x32_bf16 v[22:25], v[146:149], v[230:233], v[22:25]
	v_mfma_f32_16x16x32_bf16 v[26:29], v[150:153], v[230:233], v[26:29]
	v_mfma_f32_16x16x32_bf16 v[30:33], v[154:157], v[230:233], v[30:33]
	s_add_i32 m0, s47, 0x6000
	s_nop 0
	global_load_lds_dwordx4 v138, s[30:31]
	s_add_i32 m0, s47, 0x8000
	s_nop 0
	global_load_lds_dwordx4 v140, s[30:31]
	v_mul_f32_e32 v98, s12, v98
	v_mul_f32_e32 v99, s12, v99
	v_mul_f32_e32 v100, s13, v100
	v_mul_f32_e32 v101, s13, v101
	v_mul_f32_e32 v102, s14, v102
	v_mul_f32_e32 v103, s14, v103
	v_mul_f32_e32 v104, s15, v104
	v_mul_f32_e32 v105, s15, v105
	v_mul_f32_e32 v106, s16, v106
	v_mul_f32_e32 v107, s16, v107
	v_mul_f32_e32 v108, s17, v108
	v_mul_f32_e32 v109, s17, v109
	v_mul_f32_e32 v110, s18, v110
	v_mul_f32_e32 v111, s18, v111
	v_mul_f32_e32 v112, s19, v112
	v_mul_f32_e32 v113, s19, v113
	v_cvt_pk_bf16_f32 v158, v98, v100
	v_cvt_pk_bf16_f32 v159, v102, v104
	v_cvt_pk_bf16_f32 v160, v106, v108
	v_cvt_pk_bf16_f32 v161, v110, v112
	v_cvt_pk_bf16_f32 v162, v99, v101
	v_cvt_pk_bf16_f32 v163, v103, v105
	v_cvt_pk_bf16_f32 v164, v107, v109
	v_cvt_pk_bf16_f32 v165, v111, v113
	ds_write_b128 v1, v[158:161] offset:0
	ds_write_b128 v1, v[162:165] offset:128
	v_add_u32_e32 v91, s42, v135
	v_add_u32_e32 v93, s42, v137
	ds_read_b128 v[238:241], v139 offset:19456
	ds_read_b128 v[242:245], v139 offset:21504
	ds_read_b128 v[246:249], v139 offset:23552
	ds_read_b128 v[250:253], v139 offset:25600
	ds_read_b128 v[218:221], v91 offset:0
	ds_read_b128 v[222:225], v91 offset:2048
	ds_read_b128 v[226:229], v91 offset:4096
	ds_read_b128 v[230:233], v91 offset:6144
	s_waitcnt lgkmcnt(0)
	s_load_dwordx8 s[20:27], s[28:29], 0x0
	s_add_u32 s28, s28, 0x100
	s_addc_u32 s29, s29, 0
	v_mfma_f32_16x16x32_bf16 v[78:81], v[238:241], v[218:221], v[78:81]
	v_mfma_f32_16x16x32_bf16 v[74:77], v[242:245], v[218:221], v[74:77]
	v_mfma_f32_16x16x32_bf16 v[70:73], v[246:249], v[218:221], v[70:73]
	v_mfma_f32_16x16x32_bf16 v[66:69], v[250:253], v[218:221], v[66:69]
	ds_read_b128 v[218:221], v93 offset:0
	ds_read_b128 v[142:145], v141 offset:19456
	v_lshl_add_u64 v[132:133], v[132:133], 0, s[40:41]
	global_load_dwordx2 v[98:99], v[132:133], off
	global_load_dwordx2 v[100:101], v[132:133], off offset:2048
	v_mfma_f32_16x16x32_bf16 v[62:65], v[238:241], v[222:225], v[62:65]
	v_mfma_f32_16x16x32_bf16 v[58:61], v[242:245], v[222:225], v[58:61]
	v_mfma_f32_16x16x32_bf16 v[54:57], v[246:249], v[222:225], v[54:57]
	v_mfma_f32_16x16x32_bf16 v[50:53], v[250:253], v[222:225], v[50:53]
	ds_read_b128 v[222:225], v93 offset:2048
	ds_read_b128 v[146:149], v141 offset:21504
	v_lshl_add_u64 v[166:167], v[132:133], 0, s[34:35]
	global_load_dwordx2 v[102:103], v[166:167], off
	global_load_dwordx2 v[104:105], v[166:167], off offset:2048
	v_mfma_f32_16x16x32_bf16 v[46:49], v[238:241], v[226:229], v[46:49]
	v_mfma_f32_16x16x32_bf16 v[42:45], v[242:245], v[226:229], v[42:45]
	v_mfma_f32_16x16x32_bf16 v[38:41], v[246:249], v[226:229], v[38:41]
	v_mfma_f32_16x16x32_bf16 v[34:37], v[250:253], v[226:229], v[34:37]
	ds_read_b128 v[226:229], v93 offset:4096
	ds_read_b128 v[150:153], v141 offset:23552
	v_lshl_add_u64 v[166:167], v[132:133], 0, s[36:37]
	global_load_dwordx2 v[106:107], v[166:167], off
	global_load_dwordx2 v[108:109], v[166:167], off offset:2048
	v_mfma_f32_16x16x32_bf16 v[18:21], v[238:241], v[230:233], v[18:21]
	v_mfma_f32_16x16x32_bf16 v[22:25], v[242:245], v[230:233], v[22:25]
	v_mfma_f32_16x16x32_bf16 v[26:29], v[246:249], v[230:233], v[26:29]
	v_mfma_f32_16x16x32_bf16 v[30:33], v[250:253], v[230:233], v[30:33]
	ds_read_b128 v[230:233], v93 offset:6144
	ds_read_b128 v[154:157], v141 offset:25600
	v_lshl_add_u64 v[166:167], v[132:133], 0, s[38:39]
	global_load_dwordx2 v[110:111], v[166:167], off
	global_load_dwordx2 v[112:113], v[166:167], off offset:2048
	s_waitcnt vmcnt(21)
	s_mov_b32 s47, s42
	s_mov_b32 s42, s43
	s_mov_b32 s43, s44
	s_mov_b32 s44, s47
	s_waitcnt lgkmcnt(0)
	s_barrier
	s_sub_u32 s46, s46, 1
	s_cmp_lg_u32 s46, 0
	s_cbranch_scc1 .Lmu_loop_Y4
; #define MU_GLDS_A(buf, kt) do { _Pragma("unroll") for (int i = 0; i < NMU; ++i) \
;         __builtin_amdgcn_global_load_lds((const unsigned*)((const char*)A + aoff[i] + (size_t)(kt) * 128), (PG8_LAS unsigned*)(MU_SA(buf) + wid * 1024 + i * 8192), 16, 0, 0); } while (0)
; #define MU_B_ISSUE(sb, kt) do { const char* kb_ = Bb + (size_t)(kt) * (64 * (size_t)RB); _Pragma("unroll") for (int j = 0; j < 8; ++j) { const char* p_ = kb_ + (size_t)j * RB; \
;         asm volatile("global_load_dwordx2 %0, %1, off" : "=&v"(sb[j]) : "v"(p_) : "memory"); } } while (0)
; #define MU_B_WAIT(sb, N) asm volatile("s_waitcnt vmcnt(%8)" : "+v"(sb[0]), "+v"(sb[1]), "+v"(sb[2]), "+v"(sb[3]), "+v"(sb[4]), "+v"(sb[5]), "+v"(sb[6]), "+v"(sb[7]) : "n"(N) : "memory")
; #define MU_G_LOAD(ga, kt) do { const PG8_LAS f32x4* gk_ = (const PG8_LAS f32x4*)(lds + GAIN_OFF) + 16 * (kt) + 2 * wid; const f32x4 ga_ = gk_[0], gb_ = gk_[1]; \
;         ga[0] = ga_[0]; ga[1] = ga_[1]; ga[2] = ga_[2]; ga[3] = ga_[3]; ga[4] = gb_[0]; ga[5] = gb_[1]; ga[6] = gb_[2]; ga[7] = gb_[3]; } while (0)
; #define MU_COMPUTE(buf) MU_COMPUTE_N(buf, NMU)
; #define MU_END(last) do { if (last) asm volatile("s_waitcnt vmcnt(0)" ::: "memory"); else asm volatile("s_waitcnt vmcnt(8)" ::: "memory"); \
;         asm volatile("s_waitcnt lgkmcnt(0)" ::: "memory"); __builtin_amdgcn_s_barrier(); asm volatile("" ::: "memory"); } while (0)
; template <int MODE>
; __device__ __forceinline__ void moe_unit(PG8_LAS unsigned char* lds, int e, int cb, int slot0  , int nv  , const bf16_t* A, const int* slot_tok,
;                                          const float* W0, const float* W1, bf16_t* OUT, const float* slot_rs  , const int* slot_dst) {
;     ...
;     for (int t = 0; t < nt; t += 2) {
;         if (t + 2 < nt) MU_B_WAIT(s1, 8); else MU_B_WAIT(s1, 0);
;         MU_G_LOAD(g0, t + 1); MU_B_WRITE(s1, 1, g0); __builtin_amdgcn_sched_barrier(0); MU_GLDS_A(1, t + 1); __builtin_amdgcn_sched_barrier(0);
;         if (t + 3 < nt) { MU_B_ISSUE(s1, t + 3); }
;         MU_COMPUTE(0);
;         MU_END(t + 3 >= nt);
;         if (t + 2 < nt) { MU_B_WAIT(s0, 8); MU_G_LOAD(g0, t + 2); MU_B_WRITE(s0, 0, g0); __builtin_amdgcn_sched_barrier(0); MU_GLDS_A(0, t + 2); __builtin_amdgcn_sched_barrier(0); }
;         if (t + 4 < nt) { MU_B_ISSUE(s0, t + 4); }
;         MU_COMPUTE(1);
;         MU_END(t + 4 >= nt);
	s_add_i32 s47, s44, s6
	s_add_u32 s30, s30, 0x80
	s_addc_u32 s31, s31, 0
	v_mfma_f32_16x16x32_bf16 v[78:81], v[142:145], v[218:221], v[78:81]
	v_mfma_f32_16x16x32_bf16 v[74:77], v[146:149], v[218:221], v[74:77]
	v_mfma_f32_16x16x32_bf16 v[70:73], v[150:153], v[218:221], v[70:73]
	v_mfma_f32_16x16x32_bf16 v[66:69], v[154:157], v[218:221], v[66:69]
	s_mov_b32 m0, s47
	s_nop 0
	global_load_lds_dwordx4 v86, s[30:31]
	v_mfma_f32_16x16x32_bf16 v[62:65], v[142:145], v[222:225], v[62:65]
	v_mfma_f32_16x16x32_bf16 v[58:61], v[146:149], v[222:225], v[58:61]
	v_mfma_f32_16x16x32_bf16 v[54:57], v[150:153], v[222:225], v[54:57]
	v_mfma_f32_16x16x32_bf16 v[50:53], v[154:157], v[222:225], v[50:53]
	s_add_i32 m0, s47, 0x2000
	s_nop 0
	global_load_lds_dwordx4 v134, s[30:31]
	v_mfma_f32_16x16x32_bf16 v[46:49], v[142:145], v[226:229], v[46:49]
	v_mfma_f32_16x16x32_bf16 v[42:45], v[146:149], v[226:229], v[42:45]
	v_mfma_f32_16x16x32_bf16 v[38:41], v[150:153], v[226:229], v[38:41]
	v_mfma_f32_16x16x32_bf16 v[34:37], v[154:157], v[226:229], v[34:37]
	s_add_i32 m0, s47, 0x4000
	s_nop 0
	global_load_lds_dwordx4 v136, s[30:31]
	v_mfma_f32_16x16x32_bf16 v[18:21], v[142:145], v[230:233], v[18:21]
	v_mfma_f32_16x16x32_bf16 v[22:25], v[146:149], v[230:233], v[22:25]
	v_mfma_f32_16x16x32_bf16 v[26:29], v[150:153], v[230:233], v[26:29]
	v_mfma_f32_16x16x32_bf16 v[30:33], v[154:157], v[230:233], v[30:33]
	s_add_i32 m0, s47, 0x6000
	s_nop 0
	global_load_lds_dwordx4 v138, s[30:31]
	s_add_i32 m0, s47, 0x8000
	s_nop 0
	global_load_lds_dwordx4 v140, s[30:31]
	v_mul_f32_e32 v114, s20, v114
	v_mul_f32_e32 v115, s20, v115
	v_mul_f32_e32 v116, s21, v116
	v_mul_f32_e32 v117, s21, v117
	v_mul_f32_e32 v118, s22, v118
	v_mul_f32_e32 v119, s22, v119
	v_mul_f32_e32 v120, s23, v120
	v_mul_f32_e32 v121, s23, v121
	v_mul_f32_e32 v122, s24, v122
	v_mul_f32_e32 v123, s24, v123
	v_mul_f32_e32 v124, s25, v124
	v_mul_f32_e32 v125, s25, v125
	v_mul_f32_e32 v126, s26, v126
	v_mul_f32_e32 v127, s26, v127
	v_mul_f32_e32 v128, s27, v128
	v_mul_f32_e32 v129, s27, v129
	v_cvt_pk_bf16_f32 v158, v114, v116
	v_cvt_pk_bf16_f32 v159, v118, v120
	v_cvt_pk_bf16_f32 v160, v122, v124
	v_cvt_pk_bf16_f32 v161, v126, v128
	v_cvt_pk_bf16_f32 v162, v115, v117
	v_cvt_pk_bf16_f32 v163, v119, v121
	v_cvt_pk_bf16_f32 v164, v123, v125
	v_cvt_pk_bf16_f32 v165, v127, v129
	ds_write_b128 v1, v[158:161] offset:19456
	ds_write_b128 v1, v[162:165] offset:19584
	v_add_u32_e32 v91, s42, v135
	v_add_u32_e32 v93, s42, v137
	ds_read_b128 v[238:241], v139 offset:0
	ds_read_b128 v[242:245], v139 offset:2048
	ds_read_b128 v[246:249], v139 offset:4096
	ds_read_b128 v[250:253], v139 offset:6144
	ds_read_b128 v[218:221], v91 offset:0
	ds_read_b128 v[222:225], v91 offset:2048
	ds_read_b128 v[226:229], v91 offset:4096
	ds_read_b128 v[230:233], v91 offset:6144
	s_waitcnt lgkmcnt(0)
	s_load_dwordx8 s[12:19], s[28:29], 0x0
	s_add_u32 s28, s28, 0x100
	s_addc_u32 s29, s29, 0
	v_mfma_f32_16x16x32_bf16 v[78:81], v[238:241], v[218:221], v[78:81]
	v_mfma_f32_16x16x32_bf16 v[74:77], v[242:245], v[218:221], v[74:77]
	v_mfma_f32_16x16x32_bf16 v[70:73], v[246:249], v[218:221], v[70:73]
	v_mfma_f32_16x16x32_bf16 v[66:69], v[250:253], v[218:221], v[66:69]
	ds_read_b128 v[218:221], v93 offset:0
	ds_read_b128 v[142:145], v141 offset:0
	v_lshl_add_u64 v[132:133], v[132:133], 0, s[40:41]
	global_load_dwordx2 v[114:115], v[132:133], off
	global_load_dwordx2 v[116:117], v[132:133], off offset:2048
	v_mfma_f32_16x16x32_bf16 v[62:65], v[238:241], v[222:225], v[62:65]
	v_mfma_f32_16x16x32_bf16 v[58:61], v[242:245], v[222:225], v[58:61]
	v_mfma_f32_16x16x32_bf16 v[54:57], v[246:249], v[222:225], v[54:57]
	v_mfma_f32_16x16x32_bf16 v[50:53], v[250:253], v[222:225], v[50:53]
	ds_read_b128 v[222:225], v93 offset:2048
	ds_read_b128 v[146:149], v141 offset:2048
	v_lshl_add_u64 v[166:167], v[132:133], 0, s[34:35]
	global_load_dwordx2 v[118:119], v[166:167], off
	global_load_dwordx2 v[120:121], v[166:167], off offset:2048
	v_mfma_f32_16x16x32_bf16 v[46:49], v[238:241], v[226:229], v[46:49]
	v_mfma_f32_16x16x32_bf16 v[42:45], v[242:245], v[226:229], v[42:45]
	v_mfma_f32_16x16x32_bf16 v[38:41], v[246:249], v[226:229], v[38:41]
	v_mfma_f32_16x16x32_bf16 v[34:37], v[250:253], v[226:229], v[34:37]
	ds_read_b128 v[226:229], v93 offset:4096
	ds_read_b128 v[150:153], v141 offset:4096
	v_lshl_add_u64 v[166:167], v[132:133], 0, s[36:37]
	global_load_dwordx2 v[122:123], v[166:167], off
	global_load_dwordx2 v[124:125], v[166:167], off offset:2048
	v_mfma_f32_16x16x32_bf16 v[18:21], v[238:241], v[230:233], v[18:21]
	v_mfma_f32_16x16x32_bf16 v[22:25], v[242:245], v[230:233], v[22:25]
	v_mfma_f32_16x16x32_bf16 v[26:29], v[246:249], v[230:233], v[26:29]
	v_mfma_f32_16x16x32_bf16 v[30:33], v[250:253], v[230:233], v[30:33]
	ds_read_b128 v[230:233], v93 offset:6144
	ds_read_b128 v[154:157], v141 offset:6144
	v_lshl_add_u64 v[166:167], v[132:133], 0, s[38:39]
	global_load_dwordx2 v[126:127], v[166:167], off
	global_load_dwordx2 v[128:129], v[166:167], off offset:2048
	s_waitcnt vmcnt(21)
	s_mov_b32 s47, s42
	s_mov_b32 s42, s43
	s_mov_b32 s43, s44
	s_mov_b32 s44, s47
	s_waitcnt lgkmcnt(0)
	s_barrier
; #define MU_GLDS_A(buf, kt) do { _Pragma("unroll") for (int i = 0; i < NMU; ++i) \
;         __builtin_amdgcn_global_load_lds((const unsigned*)((const char*)A + aoff[i] + (size_t)(kt) * 128), (PG8_LAS unsigned*)(MU_SA(buf) + wid * 1024 + i * 8192), 16, 0, 0); } while (0)
; #define MU_B_ISSUE(sb, kt) do { const char* kb_ = Bb + (size_t)(kt) * (64 * (size_t)RB); _Pragma("unroll") for (int j = 0; j < 8; ++j) { const char* p_ = kb_ + (size_t)j * RB; \
;         asm volatile("global_load_dwordx2 %0, %1, off" : "=&v"(sb[j]) : "v"(p_) : "memory"); } } while (0)
; #define MU_B_WAIT(sb, N) asm volatile("s_waitcnt vmcnt(%8)" : "+v"(sb[0]), "+v"(sb[1]), "+v"(sb[2]), "+v"(sb[3]), "+v"(sb[4]), "+v"(sb[5]), "+v"(sb[6]), "+v"(sb[7]) : "n"(N) : "memory")
; #define MU_G_LOAD(ga, kt) do { const PG8_LAS f32x4* gk_ = (const PG8_LAS f32x4*)(lds + GAIN_OFF) + 16 * (kt) + 2 * wid; const f32x4 ga_ = gk_[0], gb_ = gk_[1]; \
;         ga[0] = ga_[0]; ga[1] = ga_[1]; ga[2] = ga_[2]; ga[3] = ga_[3]; ga[4] = gb_[0]; ga[5] = gb_[1]; ga[6] = gb_[2]; ga[7] = gb_[3]; } while (0)
; #define MU_COMPUTE(buf) MU_COMPUTE_N(buf, NMU)
; #define MU_END(last) do { if (last) asm volatile("s_waitcnt vmcnt(0)" ::: "memory"); else asm volatile("s_waitcnt vmcnt(8)" ::: "memory"); \
;         asm volatile("s_waitcnt lgkmcnt(0)" ::: "memory"); __builtin_amdgcn_s_barrier(); asm volatile("" ::: "memory"); } while (0)
; template <int MODE>
; __device__ __forceinline__ void moe_unit(PG8_LAS unsigned char* lds, int e, int cb, int slot0  , int nv  , const bf16_t* A, const int* slot_tok,
;                                          const float* W0, const float* W1, bf16_t* OUT, const float* slot_rs  , const int* slot_dst) {
;     ...
;     for (int t = 0; t < nt; t += 2) {
;         if (t + 2 < nt) MU_B_WAIT(s1, 8); else MU_B_WAIT(s1, 0);
;         MU_G_LOAD(g0, t + 1); MU_B_WRITE(s1, 1, g0); __builtin_amdgcn_sched_barrier(0); MU_GLDS_A(1, t + 1); __builtin_amdgcn_sched_barrier(0);
;         if (t + 3 < nt) { MU_B_ISSUE(s1, t + 3); }
;         MU_COMPUTE(0);
;         MU_END(t + 3 >= nt);
;         if (t + 2 < nt) { MU_B_WAIT(s0, 8); MU_G_LOAD(g0, t + 2); MU_B_WRITE(s0, 0, g0); __builtin_amdgcn_sched_barrier(0); MU_GLDS_A(0, t + 2); __builtin_amdgcn_sched_barrier(0); }
;         if (t + 4 < nt) { MU_B_ISSUE(s0, t + 4); }
;         MU_COMPUTE(1);
;         MU_END(t + 4 >= nt);
	s_add_i32 s47, s44, s6
	s_add_u32 s30, s30, 0x80
	s_addc_u32 s31, s31, 0
	v_mfma_f32_16x16x32_bf16 v[78:81], v[142:145], v[218:221], v[78:81]
	v_mfma_f32_16x16x32_bf16 v[74:77], v[146:149], v[218:221], v[74:77]
	v_mfma_f32_16x16x32_bf16 v[70:73], v[150:153], v[218:221], v[70:73]
	v_mfma_f32_16x16x32_bf16 v[66:69], v[154:157], v[218:221], v[66:69]
	s_mov_b32 m0, s47
	s_nop 0
	global_load_lds_dwordx4 v86, s[30:31]
	v_mfma_f32_16x16x32_bf16 v[62:65], v[142:145], v[222:225], v[62:65]
	v_mfma_f32_16x16x32_bf16 v[58:61], v[146:149], v[222:225], v[58:61]
	v_mfma_f32_16x16x32_bf16 v[54:57], v[150:153], v[222:225], v[54:57]
	v_mfma_f32_16x16x32_bf16 v[50:53], v[154:157], v[222:225], v[50:53]
	s_add_i32 m0, s47, 0x2000
	s_nop 0
	global_load_lds_dwordx4 v134, s[30:31]
	v_mfma_f32_16x16x32_bf16 v[46:49], v[142:145], v[226:229], v[46:49]
	v_mfma_f32_16x16x32_bf16 v[42:45], v[146:149], v[226:229], v[42:45]
	v_mfma_f32_16x16x32_bf16 v[38:41], v[150:153], v[226:229], v[38:41]
	v_mfma_f32_16x16x32_bf16 v[34:37], v[154:157], v[226:229], v[34:37]
	s_add_i32 m0, s47, 0x4000
	s_nop 0
	global_load_lds_dwordx4 v136, s[30:31]
	v_mfma_f32_16x16x32_bf16 v[18:21], v[142:145], v[230:233], v[18:21]
	v_mfma_f32_16x16x32_bf16 v[22:25], v[146:149], v[230:233], v[22:25]
	v_mfma_f32_16x16x32_bf16 v[26:29], v[150:153], v[230:233], v[26:29]
	v_mfma_f32_16x16x32_bf16 v[30:33], v[154:157], v[230:233], v[30:33]
	s_add_i32 m0, s47, 0x6000
	s_nop 0
	global_load_lds_dwordx4 v138, s[30:31]
	s_add_i32 m0, s47, 0x8000
	s_nop 0
	global_load_lds_dwordx4 v140, s[30:31]
	v_mul_f32_e32 v186, s12, v186
	v_mul_f32_e32 v187, s12, v187
	v_mul_f32_e32 v188, s13, v188
	v_mul_f32_e32 v189, s13, v189
	v_mul_f32_e32 v190, s14, v190
	v_mul_f32_e32 v191, s14, v191
	v_mul_f32_e32 v192, s15, v192
	v_mul_f32_e32 v193, s15, v193
	v_mul_f32_e32 v194, s16, v194
	v_mul_f32_e32 v195, s16, v195
	v_mul_f32_e32 v196, s17, v196
	v_mul_f32_e32 v197, s17, v197
	v_mul_f32_e32 v198, s18, v198
	v_mul_f32_e32 v199, s18, v199
	v_mul_f32_e32 v200, s19, v200
	v_mul_f32_e32 v201, s19, v201
	v_cvt_pk_bf16_f32 v158, v186, v188
	v_cvt_pk_bf16_f32 v159, v190, v192
	v_cvt_pk_bf16_f32 v160, v194, v196
	v_cvt_pk_bf16_f32 v161, v198, v200
	v_cvt_pk_bf16_f32 v162, v187, v189
	v_cvt_pk_bf16_f32 v163, v191, v193
	v_cvt_pk_bf16_f32 v164, v195, v197
	v_cvt_pk_bf16_f32 v165, v199, v201
	ds_write_b128 v1, v[158:161] offset:0
	ds_write_b128 v1, v[162:165] offset:128
	v_add_u32_e32 v91, s42, v135
	v_add_u32_e32 v93, s42, v137
	ds_read_b128 v[238:241], v139 offset:19456
	ds_read_b128 v[242:245], v139 offset:21504
	ds_read_b128 v[246:249], v139 offset:23552
	ds_read_b128 v[250:253], v139 offset:25600
	ds_read_b128 v[218:221], v91 offset:0
	ds_read_b128 v[222:225], v91 offset:2048
	ds_read_b128 v[226:229], v91 offset:4096
	ds_read_b128 v[230:233], v91 offset:6144
	s_waitcnt lgkmcnt(0)
	s_load_dwordx8 s[20:27], s[28:29], 0x0
	s_add_u32 s28, s28, 0x100
	s_addc_u32 s29, s29, 0
	v_mfma_f32_16x16x32_bf16 v[78:81], v[238:241], v[218:221], v[78:81]
	v_mfma_f32_16x16x32_bf16 v[74:77], v[242:245], v[218:221], v[74:77]
	v_mfma_f32_16x16x32_bf16 v[70:73], v[246:249], v[218:221], v[70:73]
	v_mfma_f32_16x16x32_bf16 v[66:69], v[250:253], v[218:221], v[66:69]
	ds_read_b128 v[218:221], v93 offset:0
	ds_read_b128 v[142:145], v141 offset:19456
	v_lshl_add_u64 v[132:133], v[132:133], 0, s[40:41]
	global_load_dwordx2 v[186:187], v[132:133], off
	global_load_dwordx2 v[188:189], v[132:133], off offset:2048
	v_mfma_f32_16x16x32_bf16 v[62:65], v[238:241], v[222:225], v[62:65]
	v_mfma_f32_16x16x32_bf16 v[58:61], v[242:245], v[222:225], v[58:61]
	v_mfma_f32_16x16x32_bf16 v[54:57], v[246:249], v[222:225], v[54:57]
	v_mfma_f32_16x16x32_bf16 v[50:53], v[250:253], v[222:225], v[50:53]
	ds_read_b128 v[222:225], v93 offset:2048
	ds_read_b128 v[146:149], v141 offset:21504
	v_lshl_add_u64 v[166:167], v[132:133], 0, s[34:35]
	global_load_dwordx2 v[190:191], v[166:167], off
	global_load_dwordx2 v[192:193], v[166:167], off offset:2048
	v_mfma_f32_16x16x32_bf16 v[46:49], v[238:241], v[226:229], v[46:49]
	v_mfma_f32_16x16x32_bf16 v[42:45], v[242:245], v[226:229], v[42:45]
	v_mfma_f32_16x16x32_bf16 v[38:41], v[246:249], v[226:229], v[38:41]
	v_mfma_f32_16x16x32_bf16 v[34:37], v[250:253], v[226:229], v[34:37]
	ds_read_b128 v[226:229], v93 offset:4096
	ds_read_b128 v[150:153], v141 offset:23552
	v_lshl_add_u64 v[166:167], v[132:133], 0, s[36:37]
	global_load_dwordx2 v[194:195], v[166:167], off
	global_load_dwordx2 v[196:197], v[166:167], off offset:2048
	v_mfma_f32_16x16x32_bf16 v[18:21], v[238:241], v[230:233], v[18:21]
	v_mfma_f32_16x16x32_bf16 v[22:25], v[242:245], v[230:233], v[22:25]
	v_mfma_f32_16x16x32_bf16 v[26:29], v[246:249], v[230:233], v[26:29]
	v_mfma_f32_16x16x32_bf16 v[30:33], v[250:253], v[230:233], v[30:33]
	ds_read_b128 v[230:233], v93 offset:6144
	ds_read_b128 v[154:157], v141 offset:25600
	v_lshl_add_u64 v[166:167], v[132:133], 0, s[38:39]
	global_load_dwordx2 v[198:199], v[166:167], off
	global_load_dwordx2 v[200:201], v[166:167], off offset:2048
	s_waitcnt vmcnt(21)
	s_mov_b32 s47, s42
	s_mov_b32 s42, s43
	s_mov_b32 s43, s44
	s_mov_b32 s44, s47
	s_waitcnt lgkmcnt(0)
	s_barrier
; #define MU_GLDS_A(buf, kt) do { _Pragma("unroll") for (int i = 0; i < NMU; ++i) \
;         __builtin_amdgcn_global_load_lds((const unsigned*)((const char*)A + aoff[i] + (size_t)(kt) * 128), (PG8_LAS unsigned*)(MU_SA(buf) + wid * 1024 + i * 8192), 16, 0, 0); } while (0)
; #define MU_B_ISSUE(sb, kt) do { const char* kb_ = Bb + (size_t)(kt) * (64 * (size_t)RB); _Pragma("unroll") for (int j = 0; j < 8; ++j) { const char* p_ = kb_ + (size_t)j * RB; \
;         asm volatile("global_load_dwordx2 %0, %1, off" : "=&v"(sb[j]) : "v"(p_) : "memory"); } } while (0)
; #define MU_B_WAIT(sb, N) asm volatile("s_waitcnt vmcnt(%8)" : "+v"(sb[0]), "+v"(sb[1]), "+v"(sb[2]), "+v"(sb[3]), "+v"(sb[4]), "+v"(sb[5]), "+v"(sb[6]), "+v"(sb[7]) : "n"(N) : "memory")
; #define MU_G_LOAD(ga, kt) do { const PG8_LAS f32x4* gk_ = (const PG8_LAS f32x4*)(lds + GAIN_OFF) + 16 * (kt) + 2 * wid; const f32x4 ga_ = gk_[0], gb_ = gk_[1]; \
;         ga[0] = ga_[0]; ga[1] = ga_[1]; ga[2] = ga_[2]; ga[3] = ga_[3]; ga[4] = gb_[0]; ga[5] = gb_[1]; ga[6] = gb_[2]; ga[7] = gb_[3]; } while (0)
; #define MU_COMPUTE(buf) MU_COMPUTE_N(buf, NMU)
; #define MU_END(last) do { if (last) asm volatile("s_waitcnt vmcnt(0)" ::: "memory"); else asm volatile("s_waitcnt vmcnt(8)" ::: "memory"); \
;         asm volatile("s_waitcnt lgkmcnt(0)" ::: "memory"); __builtin_amdgcn_s_barrier(); asm volatile("" ::: "memory"); } while (0)
; template <int MODE>
; __device__ __forceinline__ void moe_unit(PG8_LAS unsigned char* lds, int e, int cb, int slot0  , int nv  , const bf16_t* A, const int* slot_tok,
;                                          const float* W0, const float* W1, bf16_t* OUT, const float* slot_rs  , const int* slot_dst) {
;     ...
;     for (int t = 0; t < nt; t += 2) {
;         if (t + 2 < nt) MU_B_WAIT(s1, 8); else MU_B_WAIT(s1, 0);
;         MU_G_LOAD(g0, t + 1); MU_B_WRITE(s1, 1, g0); __builtin_amdgcn_sched_barrier(0); MU_GLDS_A(1, t + 1); __builtin_amdgcn_sched_barrier(0);
;         if (t + 3 < nt) { MU_B_ISSUE(s1, t + 3); }
;         MU_COMPUTE(0);
;         MU_END(t + 3 >= nt);
;         if (t + 2 < nt) { MU_B_WAIT(s0, 8); MU_G_LOAD(g0, t + 2); MU_B_WRITE(s0, 0, g0); __builtin_amdgcn_sched_barrier(0); MU_GLDS_A(0, t + 2); __builtin_amdgcn_sched_barrier(0); }
;         if (t + 4 < nt) { MU_B_ISSUE(s0, t + 4); }
;         MU_COMPUTE(1);
;         MU_END(t + 4 >= nt);
	s_add_i32 s47, s44, s6
	s_add_u32 s30, s30, 0x80
	s_addc_u32 s31, s31, 0
	v_mfma_f32_16x16x32_bf16 v[78:81], v[142:145], v[218:221], v[78:81]
	v_mfma_f32_16x16x32_bf16 v[74:77], v[146:149], v[218:221], v[74:77]
	v_mfma_f32_16x16x32_bf16 v[70:73], v[150:153], v[218:221], v[70:73]
	v_mfma_f32_16x16x32_bf16 v[66:69], v[154:157], v[218:221], v[66:69]
	s_mov_b32 m0, s47
	s_nop 0
	global_load_lds_dwordx4 v86, s[30:31]
	v_mfma_f32_16x16x32_bf16 v[62:65], v[142:145], v[222:225], v[62:65]
	v_mfma_f32_16x16x32_bf16 v[58:61], v[146:149], v[222:225], v[58:61]
	v_mfma_f32_16x16x32_bf16 v[54:57], v[150:153], v[222:225], v[54:57]
	v_mfma_f32_16x16x32_bf16 v[50:53], v[154:157], v[222:225], v[50:53]
	s_add_i32 m0, s47, 0x2000
	s_nop 0
	global_load_lds_dwordx4 v134, s[30:31]
	v_mfma_f32_16x16x32_bf16 v[46:49], v[142:145], v[226:229], v[46:49]
	v_mfma_f32_16x16x32_bf16 v[42:45], v[146:149], v[226:229], v[42:45]
	v_mfma_f32_16x16x32_bf16 v[38:41], v[150:153], v[226:229], v[38:41]
	v_mfma_f32_16x16x32_bf16 v[34:37], v[154:157], v[226:229], v[34:37]
	s_add_i32 m0, s47, 0x4000
	s_nop 0
	global_load_lds_dwordx4 v136, s[30:31]
	v_mfma_f32_16x16x32_bf16 v[18:21], v[142:145], v[230:233], v[18:21]
	v_mfma_f32_16x16x32_bf16 v[22:25], v[146:149], v[230:233], v[22:25]
	v_mfma_f32_16x16x32_bf16 v[26:29], v[150:153], v[230:233], v[26:29]
	v_mfma_f32_16x16x32_bf16 v[30:33], v[154:157], v[230:233], v[30:33]
	s_add_i32 m0, s47, 0x6000
	s_nop 0
	global_load_lds_dwordx4 v138, s[30:31]
	s_add_i32 m0, s47, 0x8000
	s_nop 0
	global_load_lds_dwordx4 v140, s[30:31]
	v_mul_f32_e32 v202, s20, v202
	v_mul_f32_e32 v203, s20, v203
	v_mul_f32_e32 v204, s21, v204
	v_mul_f32_e32 v205, s21, v205
	v_mul_f32_e32 v206, s22, v206
	v_mul_f32_e32 v207, s22, v207
	v_mul_f32_e32 v208, s23, v208
	v_mul_f32_e32 v209, s23, v209
	v_mul_f32_e32 v210, s24, v210
	v_mul_f32_e32 v211, s24, v211
	v_mul_f32_e32 v212, s25, v212
	v_mul_f32_e32 v213, s25, v213
	v_mul_f32_e32 v214, s26, v214
	v_mul_f32_e32 v215, s26, v215
	v_mul_f32_e32 v216, s27, v216
	v_mul_f32_e32 v217, s27, v217
	v_cvt_pk_bf16_f32 v158, v202, v204
	v_cvt_pk_bf16_f32 v159, v206, v208
	v_cvt_pk_bf16_f32 v160, v210, v212
	v_cvt_pk_bf16_f32 v161, v214, v216
	v_cvt_pk_bf16_f32 v162, v203, v205
	v_cvt_pk_bf16_f32 v163, v207, v209
	v_cvt_pk_bf16_f32 v164, v211, v213
	v_cvt_pk_bf16_f32 v165, v215, v217
	ds_write_b128 v1, v[158:161] offset:19456
	ds_write_b128 v1, v[162:165] offset:19584
	v_add_u32_e32 v91, s42, v135
	v_add_u32_e32 v93, s42, v137
	ds_read_b128 v[238:241], v139 offset:0
	ds_read_b128 v[242:245], v139 offset:2048
	ds_read_b128 v[246:249], v139 offset:4096
	ds_read_b128 v[250:253], v139 offset:6144
	ds_read_b128 v[218:221], v91 offset:0
	ds_read_b128 v[222:225], v91 offset:2048
	ds_read_b128 v[226:229], v91 offset:4096
	ds_read_b128 v[230:233], v91 offset:6144
	s_waitcnt lgkmcnt(0)
	s_load_dwordx8 s[12:19], s[28:29], 0x0
	s_add_u32 s28, s28, 0x100
	s_addc_u32 s29, s29, 0
	v_mfma_f32_16x16x32_bf16 v[78:81], v[238:241], v[218:221], v[78:81]
	v_mfma_f32_16x16x32_bf16 v[74:77], v[242:245], v[218:221], v[74:77]
	v_mfma_f32_16x16x32_bf16 v[70:73], v[246:249], v[218:221], v[70:73]
	v_mfma_f32_16x16x32_bf16 v[66:69], v[250:253], v[218:221], v[66:69]
	ds_read_b128 v[218:221], v93 offset:0
	ds_read_b128 v[142:145], v141 offset:0
	v_lshl_add_u64 v[132:133], v[132:133], 0, s[40:41]
	global_load_dwordx2 v[202:203], v[132:133], off
	global_load_dwordx2 v[204:205], v[132:133], off offset:2048
	v_mfma_f32_16x16x32_bf16 v[62:65], v[238:241], v[222:225], v[62:65]
	v_mfma_f32_16x16x32_bf16 v[58:61], v[242:245], v[222:225], v[58:61]
	v_mfma_f32_16x16x32_bf16 v[54:57], v[246:249], v[222:225], v[54:57]
	v_mfma_f32_16x16x32_bf16 v[50:53], v[250:253], v[222:225], v[50:53]
	ds_read_b128 v[222:225], v93 offset:2048
	ds_read_b128 v[146:149], v141 offset:2048
	v_lshl_add_u64 v[166:167], v[132:133], 0, s[34:35]
	global_load_dwordx2 v[206:207], v[166:167], off
	global_load_dwordx2 v[208:209], v[166:167], off offset:2048
	v_mfma_f32_16x16x32_bf16 v[46:49], v[238:241], v[226:229], v[46:49]
	v_mfma_f32_16x16x32_bf16 v[42:45], v[242:245], v[226:229], v[42:45]
	v_mfma_f32_16x16x32_bf16 v[38:41], v[246:249], v[226:229], v[38:41]
	v_mfma_f32_16x16x32_bf16 v[34:37], v[250:253], v[226:229], v[34:37]
	ds_read_b128 v[226:229], v93 offset:4096
	ds_read_b128 v[150:153], v141 offset:4096
	v_lshl_add_u64 v[166:167], v[132:133], 0, s[36:37]
	global_load_dwordx2 v[210:211], v[166:167], off
	global_load_dwordx2 v[212:213], v[166:167], off offset:2048
	v_mfma_f32_16x16x32_bf16 v[18:21], v[238:241], v[230:233], v[18:21]
	v_mfma_f32_16x16x32_bf16 v[22:25], v[242:245], v[230:233], v[22:25]
	v_mfma_f32_16x16x32_bf16 v[26:29], v[246:249], v[230:233], v[26:29]
	v_mfma_f32_16x16x32_bf16 v[30:33], v[250:253], v[230:233], v[30:33]
	ds_read_b128 v[230:233], v93 offset:6144
	ds_read_b128 v[154:157], v141 offset:6144
	v_lshl_add_u64 v[166:167], v[132:133], 0, s[38:39]
	global_load_dwordx2 v[214:215], v[166:167], off
	global_load_dwordx2 v[216:217], v[166:167], off offset:2048
	s_waitcnt vmcnt(21)
	s_mov_b32 s47, s42
	s_mov_b32 s42, s43
	s_mov_b32 s43, s44
	s_mov_b32 s44, s47
	s_waitcnt lgkmcnt(0)
	s_barrier
; #define MU_GLDS_A(buf, kt) do { _Pragma("unroll") for (int i = 0; i < NMU; ++i) \
;         __builtin_amdgcn_global_load_lds((const unsigned*)((const char*)A + aoff[i] + (size_t)(kt) * 128), (PG8_LAS unsigned*)(MU_SA(buf) + wid * 1024 + i * 8192), 16, 0, 0); } while (0)
; #define MU_B_ISSUE(sb, kt) do { const char* kb_ = Bb + (size_t)(kt) * (64 * (size_t)RB); _Pragma("unroll") for (int j = 0; j < 8; ++j) { const char* p_ = kb_ + (size_t)j * RB; \
;         asm volatile("global_load_dwordx2 %0, %1, off" : "=&v"(sb[j]) : "v"(p_) : "memory"); } } while (0)
; #define MU_B_WAIT(sb, N) asm volatile("s_waitcnt vmcnt(%8)" : "+v"(sb[0]), "+v"(sb[1]), "+v"(sb[2]), "+v"(sb[3]), "+v"(sb[4]), "+v"(sb[5]), "+v"(sb[6]), "+v"(sb[7]) : "n"(N) : "memory")
; #define MU_G_LOAD(ga, kt) do { const PG8_LAS f32x4* gk_ = (const PG8_LAS f32x4*)(lds + GAIN_OFF) + 16 * (kt) + 2 * wid; const f32x4 ga_ = gk_[0], gb_ = gk_[1]; \
;         ga[0] = ga_[0]; ga[1] = ga_[1]; ga[2] = ga_[2]; ga[3] = ga_[3]; ga[4] = gb_[0]; ga[5] = gb_[1]; ga[6] = gb_[2]; ga[7] = gb_[3]; } while (0)
; #define MU_COMPUTE(buf) MU_COMPUTE_N(buf, NMU)
; #define MU_END(last) do { if (last) asm volatile("s_waitcnt vmcnt(0)" ::: "memory"); else asm volatile("s_waitcnt vmcnt(8)" ::: "memory"); \
;         asm volatile("s_waitcnt lgkmcnt(0)" ::: "memory"); __builtin_amdgcn_s_barrier(); asm volatile("" ::: "memory"); } while (0)
; template <int MODE>
; __device__ __forceinline__ void moe_unit(PG8_LAS unsigned char* lds, int e, int cb, int slot0  , int nv  , const bf16_t* A, const int* slot_tok,
;                                          const float* W0, const float* W1, bf16_t* OUT, const float* slot_rs  , const int* slot_dst) {
;     ...
;     for (int t = 0; t < nt; t += 2) {
;         if (t + 2 < nt) MU_B_WAIT(s1, 8); else MU_B_WAIT(s1, 0);
;         MU_G_LOAD(g0, t + 1); MU_B_WRITE(s1, 1, g0); __builtin_amdgcn_sched_barrier(0); MU_GLDS_A(1, t + 1); __builtin_amdgcn_sched_barrier(0);
;         if (t + 3 < nt) { MU_B_ISSUE(s1, t + 3); }
;         MU_COMPUTE(0);
;         MU_END(t + 3 >= nt);
;         if (t + 2 < nt) { MU_B_WAIT(s0, 8); MU_G_LOAD(g0, t + 2); MU_B_WRITE(s0, 0, g0); __builtin_amdgcn_sched_barrier(0); MU_GLDS_A(0, t + 2); __builtin_amdgcn_sched_barrier(0); }
;         if (t + 4 < nt) { MU_B_ISSUE(s0, t + 4); }
;         MU_COMPUTE(1);
;         MU_END(t + 4 >= nt);
	s_add_i32 s47, s44, s6
	s_add_u32 s30, s30, 0x80
	s_addc_u32 s31, s31, 0
	v_mfma_f32_16x16x32_bf16 v[78:81], v[142:145], v[218:221], v[78:81]
	v_mfma_f32_16x16x32_bf16 v[74:77], v[146:149], v[218:221], v[74:77]
	v_mfma_f32_16x16x32_bf16 v[70:73], v[150:153], v[218:221], v[70:73]
	v_mfma_f32_16x16x32_bf16 v[66:69], v[154:157], v[218:221], v[66:69]
	s_mov_b32 m0, s47
	s_nop 0
	global_load_lds_dwordx4 v86, s[30:31]
	v_mfma_f32_16x16x32_bf16 v[62:65], v[142:145], v[222:225], v[62:65]
	v_mfma_f32_16x16x32_bf16 v[58:61], v[146:149], v[222:225], v[58:61]
	v_mfma_f32_16x16x32_bf16 v[54:57], v[150:153], v[222:225], v[54:57]
	v_mfma_f32_16x16x32_bf16 v[50:53], v[154:157], v[222:225], v[50:53]
	s_add_i32 m0, s47, 0x2000
	s_nop 0
	global_load_lds_dwordx4 v134, s[30:31]
	v_mfma_f32_16x16x32_bf16 v[46:49], v[142:145], v[226:229], v[46:49]
	v_mfma_f32_16x16x32_bf16 v[42:45], v[146:149], v[226:229], v[42:45]
	v_mfma_f32_16x16x32_bf16 v[38:41], v[150:153], v[226:229], v[38:41]
	v_mfma_f32_16x16x32_bf16 v[34:37], v[154:157], v[226:229], v[34:37]
	s_add_i32 m0, s47, 0x4000
	s_nop 0
	global_load_lds_dwordx4 v136, s[30:31]
	v_mfma_f32_16x16x32_bf16 v[18:21], v[142:145], v[230:233], v[18:21]
	v_mfma_f32_16x16x32_bf16 v[22:25], v[146:149], v[230:233], v[22:25]
	v_mfma_f32_16x16x32_bf16 v[26:29], v[150:153], v[230:233], v[26:29]
	v_mfma_f32_16x16x32_bf16 v[30:33], v[154:157], v[230:233], v[30:33]
	s_add_i32 m0, s47, 0x6000
	s_nop 0
	global_load_lds_dwordx4 v138, s[30:31]
	s_add_i32 m0, s47, 0x8000
	s_nop 0
	global_load_lds_dwordx4 v140, s[30:31]
	v_mul_f32_e32 v98, s12, v98
	v_mul_f32_e32 v99, s12, v99
	v_mul_f32_e32 v100, s13, v100
	v_mul_f32_e32 v101, s13, v101
	v_mul_f32_e32 v102, s14, v102
	v_mul_f32_e32 v103, s14, v103
	v_mul_f32_e32 v104, s15, v104
	v_mul_f32_e32 v105, s15, v105
	v_mul_f32_e32 v106, s16, v106
	v_mul_f32_e32 v107, s16, v107
	v_mul_f32_e32 v108, s17, v108
	v_mul_f32_e32 v109, s17, v109
	v_mul_f32_e32 v110, s18, v110
	v_mul_f32_e32 v111, s18, v111
	v_mul_f32_e32 v112, s19, v112
	v_mul_f32_e32 v113, s19, v113
	v_cvt_pk_bf16_f32 v158, v98, v100
	v_cvt_pk_bf16_f32 v159, v102, v104
	v_cvt_pk_bf16_f32 v160, v106, v108
	v_cvt_pk_bf16_f32 v161, v110, v112
	v_cvt_pk_bf16_f32 v162, v99, v101
	v_cvt_pk_bf16_f32 v163, v103, v105
	v_cvt_pk_bf16_f32 v164, v107, v109
	v_cvt_pk_bf16_f32 v165, v111, v113
	ds_write_b128 v1, v[158:161] offset:0
	ds_write_b128 v1, v[162:165] offset:128
	v_add_u32_e32 v91, s42, v135
	v_add_u32_e32 v93, s42, v137
	ds_read_b128 v[238:241], v139 offset:19456
	ds_read_b128 v[242:245], v139 offset:21504
	ds_read_b128 v[246:249], v139 offset:23552
	ds_read_b128 v[250:253], v139 offset:25600
	ds_read_b128 v[218:221], v91 offset:0
	ds_read_b128 v[222:225], v91 offset:2048
	ds_read_b128 v[226:229], v91 offset:4096
	ds_read_b128 v[230:233], v91 offset:6144
	s_waitcnt lgkmcnt(0)
	s_load_dwordx8 s[20:27], s[28:29], 0x0
	s_add_u32 s28, s28, 0x100
	s_addc_u32 s29, s29, 0
	v_mfma_f32_16x16x32_bf16 v[78:81], v[238:241], v[218:221], v[78:81]
	v_mfma_f32_16x16x32_bf16 v[74:77], v[242:245], v[218:221], v[74:77]
	v_mfma_f32_16x16x32_bf16 v[70:73], v[246:249], v[218:221], v[70:73]
	v_mfma_f32_16x16x32_bf16 v[66:69], v[250:253], v[218:221], v[66:69]
	ds_read_b128 v[218:221], v93 offset:0
	ds_read_b128 v[142:145], v141 offset:19456
	v_mfma_f32_16x16x32_bf16 v[62:65], v[238:241], v[222:225], v[62:65]
	v_mfma_f32_16x16x32_bf16 v[58:61], v[242:245], v[222:225], v[58:61]
	v_mfma_f32_16x16x32_bf16 v[54:57], v[246:249], v[222:225], v[54:57]
	v_mfma_f32_16x16x32_bf16 v[50:53], v[250:253], v[222:225], v[50:53]
	ds_read_b128 v[222:225], v93 offset:2048
	ds_read_b128 v[146:149], v141 offset:21504
	v_mfma_f32_16x16x32_bf16 v[46:49], v[238:241], v[226:229], v[46:49]
	v_mfma_f32_16x16x32_bf16 v[42:45], v[242:245], v[226:229], v[42:45]
	v_mfma_f32_16x16x32_bf16 v[38:41], v[246:249], v[226:229], v[38:41]
	v_mfma_f32_16x16x32_bf16 v[34:37], v[250:253], v[226:229], v[34:37]
	ds_read_b128 v[226:229], v93 offset:4096
	ds_read_b128 v[150:153], v141 offset:23552
	v_mfma_f32_16x16x32_bf16 v[18:21], v[238:241], v[230:233], v[18:21]
	v_mfma_f32_16x16x32_bf16 v[22:25], v[242:245], v[230:233], v[22:25]
	v_mfma_f32_16x16x32_bf16 v[26:29], v[246:249], v[230:233], v[26:29]
	v_mfma_f32_16x16x32_bf16 v[30:33], v[250:253], v[230:233], v[30:33]
	ds_read_b128 v[230:233], v93 offset:6144
	ds_read_b128 v[154:157], v141 offset:25600
	s_waitcnt vmcnt(13)
	s_mov_b32 s47, s42
	s_mov_b32 s42, s43
	s_mov_b32 s43, s44
	s_mov_b32 s44, s47
	s_waitcnt lgkmcnt(0)
	s_barrier
; #define MU_GLDS_A(buf, kt) do { _Pragma("unroll") for (int i = 0; i < NMU; ++i) \
;         __builtin_amdgcn_global_load_lds((const unsigned*)((const char*)A + aoff[i] + (size_t)(kt) * 128), (PG8_LAS unsigned*)(MU_SA(buf) + wid * 1024 + i * 8192), 16, 0, 0); } while (0)
; #define MU_B_ISSUE(sb, kt) do { const char* kb_ = Bb + (size_t)(kt) * (64 * (size_t)RB); _Pragma("unroll") for (int j = 0; j < 8; ++j) { const char* p_ = kb_ + (size_t)j * RB; \
;         asm volatile("global_load_dwordx2 %0, %1, off" : "=&v"(sb[j]) : "v"(p_) : "memory"); } } while (0)
; #define MU_B_WAIT(sb, N) asm volatile("s_waitcnt vmcnt(%8)" : "+v"(sb[0]), "+v"(sb[1]), "+v"(sb[2]), "+v"(sb[3]), "+v"(sb[4]), "+v"(sb[5]), "+v"(sb[6]), "+v"(sb[7]) : "n"(N) : "memory")
; #define MU_G_LOAD(ga, kt) do { const PG8_LAS f32x4* gk_ = (const PG8_LAS f32x4*)(lds + GAIN_OFF) + 16 * (kt) + 2 * wid; const f32x4 ga_ = gk_[0], gb_ = gk_[1]; \
;         ga[0] = ga_[0]; ga[1] = ga_[1]; ga[2] = ga_[2]; ga[3] = ga_[3]; ga[4] = gb_[0]; ga[5] = gb_[1]; ga[6] = gb_[2]; ga[7] = gb_[3]; } while (0)
; #define MU_COMPUTE(buf) MU_COMPUTE_N(buf, NMU)
; #define MU_END(last) do { if (last) asm volatile("s_waitcnt vmcnt(0)" ::: "memory"); else asm volatile("s_waitcnt vmcnt(8)" ::: "memory"); \
;         asm volatile("s_waitcnt lgkmcnt(0)" ::: "memory"); __builtin_amdgcn_s_barrier(); asm volatile("" ::: "memory"); } while (0)
; template <int MODE>
; __device__ __forceinline__ void moe_unit(PG8_LAS unsigned char* lds, int e, int cb, int slot0  , int nv  , const bf16_t* A, const int* slot_tok,
;                                          const float* W0, const float* W1, bf16_t* OUT, const float* slot_rs  , const int* slot_dst) {
;     ...
;     for (int t = 0; t < nt; t += 2) {
;         if (t + 2 < nt) MU_B_WAIT(s1, 8); else MU_B_WAIT(s1, 0);
;         MU_G_LOAD(g0, t + 1); MU_B_WRITE(s1, 1, g0); __builtin_amdgcn_sched_barrier(0); MU_GLDS_A(1, t + 1); __builtin_amdgcn_sched_barrier(0);
;         if (t + 3 < nt) { MU_B_ISSUE(s1, t + 3); }
;         MU_COMPUTE(0);
;         MU_END(t + 3 >= nt);
;         if (t + 2 < nt) { MU_B_WAIT(s0, 8); MU_G_LOAD(g0, t + 2); MU_B_WRITE(s0, 0, g0); __builtin_amdgcn_sched_barrier(0); MU_GLDS_A(0, t + 2); __builtin_amdgcn_sched_barrier(0); }
;         if (t + 4 < nt) { MU_B_ISSUE(s0, t + 4); }
;         MU_COMPUTE(1);
;         MU_END(t + 4 >= nt);
	s_add_i32 s47, s44, s6
	s_add_u32 s30, s30, 0x80
	s_addc_u32 s31, s31, 0
	v_mfma_f32_16x16x32_bf16 v[78:81], v[142:145], v[218:221], v[78:81]
	v_mfma_f32_16x16x32_bf16 v[74:77], v[146:149], v[218:221], v[74:77]
	v_mfma_f32_16x16x32_bf16 v[70:73], v[150:153], v[218:221], v[70:73]
	v_mfma_f32_16x16x32_bf16 v[66:69], v[154:157], v[218:221], v[66:69]
	s_mov_b32 m0, s47
	s_nop 0
	global_load_lds_dwordx4 v86, s[30:31]
	v_mfma_f32_16x16x32_bf16 v[62:65], v[142:145], v[222:225], v[62:65]
	v_mfma_f32_16x16x32_bf16 v[58:61], v[146:149], v[222:225], v[58:61]
	v_mfma_f32_16x16x32_bf16 v[54:57], v[150:153], v[222:225], v[54:57]
	v_mfma_f32_16x16x32_bf16 v[50:53], v[154:157], v[222:225], v[50:53]
	s_add_i32 m0, s47, 0x2000
	s_nop 0
	global_load_lds_dwordx4 v134, s[30:31]
	v_mfma_f32_16x16x32_bf16 v[46:49], v[142:145], v[226:229], v[46:49]
	v_mfma_f32_16x16x32_bf16 v[42:45], v[146:149], v[226:229], v[42:45]
	v_mfma_f32_16x16x32_bf16 v[38:41], v[150:153], v[226:229], v[38:41]
	v_mfma_f32_16x16x32_bf16 v[34:37], v[154:157], v[226:229], v[34:37]
	s_add_i32 m0, s47, 0x4000
	s_nop 0
	global_load_lds_dwordx4 v136, s[30:31]
	v_mfma_f32_16x16x32_bf16 v[18:21], v[142:145], v[230:233], v[18:21]
	v_mfma_f32_16x16x32_bf16 v[22:25], v[146:149], v[230:233], v[22:25]
	v_mfma_f32_16x16x32_bf16 v[26:29], v[150:153], v[230:233], v[26:29]
	v_mfma_f32_16x16x32_bf16 v[30:33], v[154:157], v[230:233], v[30:33]
	s_add_i32 m0, s47, 0x6000
	s_nop 0
	global_load_lds_dwordx4 v138, s[30:31]
	s_add_i32 m0, s47, 0x8000
	s_nop 0
	global_load_lds_dwordx4 v140, s[30:31]
	v_mul_f32_e32 v114, s20, v114
	v_mul_f32_e32 v115, s20, v115
	v_mul_f32_e32 v116, s21, v116
	v_mul_f32_e32 v117, s21, v117
	v_mul_f32_e32 v118, s22, v118
	v_mul_f32_e32 v119, s22, v119
	v_mul_f32_e32 v120, s23, v120
	v_mul_f32_e32 v121, s23, v121
	v_mul_f32_e32 v122, s24, v122
	v_mul_f32_e32 v123, s24, v123
	v_mul_f32_e32 v124, s25, v124
	v_mul_f32_e32 v125, s25, v125
	v_mul_f32_e32 v126, s26, v126
	v_mul_f32_e32 v127, s26, v127
	v_mul_f32_e32 v128, s27, v128
	v_mul_f32_e32 v129, s27, v129
	v_cvt_pk_bf16_f32 v158, v114, v116
	v_cvt_pk_bf16_f32 v159, v118, v120
	v_cvt_pk_bf16_f32 v160, v122, v124
	v_cvt_pk_bf16_f32 v161, v126, v128
	v_cvt_pk_bf16_f32 v162, v115, v117
	v_cvt_pk_bf16_f32 v163, v119, v121
	v_cvt_pk_bf16_f32 v164, v123, v125
	v_cvt_pk_bf16_f32 v165, v127, v129
	ds_write_b128 v1, v[158:161] offset:19456
	ds_write_b128 v1, v[162:165] offset:19584
	v_add_u32_e32 v91, s42, v135
	v_add_u32_e32 v93, s42, v137
	ds_read_b128 v[238:241], v139 offset:0
	ds_read_b128 v[242:245], v139 offset:2048
	ds_read_b128 v[246:249], v139 offset:4096
	ds_read_b128 v[250:253], v139 offset:6144
	ds_read_b128 v[218:221], v91 offset:0
	ds_read_b128 v[222:225], v91 offset:2048
	ds_read_b128 v[226:229], v91 offset:4096
	ds_read_b128 v[230:233], v91 offset:6144
	s_waitcnt lgkmcnt(0)
	s_load_dwordx8 s[12:19], s[28:29], 0x0
	s_add_u32 s28, s28, 0x100
	s_addc_u32 s29, s29, 0
	v_mfma_f32_16x16x32_bf16 v[78:81], v[238:241], v[218:221], v[78:81]
	v_mfma_f32_16x16x32_bf16 v[74:77], v[242:245], v[218:221], v[74:77]
	v_mfma_f32_16x16x32_bf16 v[70:73], v[246:249], v[218:221], v[70:73]
	v_mfma_f32_16x16x32_bf16 v[66:69], v[250:253], v[218:221], v[66:69]
	ds_read_b128 v[218:221], v93 offset:0
	ds_read_b128 v[142:145], v141 offset:0
	v_mfma_f32_16x16x32_bf16 v[62:65], v[238:241], v[222:225], v[62:65]
	v_mfma_f32_16x16x32_bf16 v[58:61], v[242:245], v[222:225], v[58:61]
	v_mfma_f32_16x16x32_bf16 v[54:57], v[246:249], v[222:225], v[54:57]
	v_mfma_f32_16x16x32_bf16 v[50:53], v[250:253], v[222:225], v[50:53]
	ds_read_b128 v[222:225], v93 offset:2048
	ds_read_b128 v[146:149], v141 offset:2048
	v_mfma_f32_16x16x32_bf16 v[46:49], v[238:241], v[226:229], v[46:49]
	v_mfma_f32_16x16x32_bf16 v[42:45], v[242:245], v[226:229], v[42:45]
	v_mfma_f32_16x16x32_bf16 v[38:41], v[246:249], v[226:229], v[38:41]
	v_mfma_f32_16x16x32_bf16 v[34:37], v[250:253], v[226:229], v[34:37]
	ds_read_b128 v[226:229], v93 offset:4096
	ds_read_b128 v[150:153], v141 offset:4096
	v_mfma_f32_16x16x32_bf16 v[18:21], v[238:241], v[230:233], v[18:21]
	v_mfma_f32_16x16x32_bf16 v[22:25], v[242:245], v[230:233], v[22:25]
	v_mfma_f32_16x16x32_bf16 v[26:29], v[246:249], v[230:233], v[26:29]
	v_mfma_f32_16x16x32_bf16 v[30:33], v[250:253], v[230:233], v[30:33]
	ds_read_b128 v[230:233], v93 offset:6144
	ds_read_b128 v[154:157], v141 offset:6144
	s_waitcnt vmcnt(5)
	s_mov_b32 s47, s42
	s_mov_b32 s42, s43
	s_mov_b32 s43, s44
	s_mov_b32 s44, s47
	s_waitcnt lgkmcnt(0)
	s_barrier
; #define MU_GLDS_A(buf, kt) do { _Pragma("unroll") for (int i = 0; i < NMU; ++i) \
;         __builtin_amdgcn_global_load_lds((const unsigned*)((const char*)A + aoff[i] + (size_t)(kt) * 128), (PG8_LAS unsigned*)(MU_SA(buf) + wid * 1024 + i * 8192), 16, 0, 0); } while (0)
; #define MU_B_ISSUE(sb, kt) do { const char* kb_ = Bb + (size_t)(kt) * (64 * (size_t)RB); _Pragma("unroll") for (int j = 0; j < 8; ++j) { const char* p_ = kb_ + (size_t)j * RB; \
;         asm volatile("global_load_dwordx2 %0, %1, off" : "=&v"(sb[j]) : "v"(p_) : "memory"); } } while (0)
; #define MU_B_WAIT(sb, N) asm volatile("s_waitcnt vmcnt(%8)" : "+v"(sb[0]), "+v"(sb[1]), "+v"(sb[2]), "+v"(sb[3]), "+v"(sb[4]), "+v"(sb[5]), "+v"(sb[6]), "+v"(sb[7]) : "n"(N) : "memory")
; #define MU_G_LOAD(ga, kt) do { const PG8_LAS f32x4* gk_ = (const PG8_LAS f32x4*)(lds + GAIN_OFF) + 16 * (kt) + 2 * wid; const f32x4 ga_ = gk_[0], gb_ = gk_[1]; \
;         ga[0] = ga_[0]; ga[1] = ga_[1]; ga[2] = ga_[2]; ga[3] = ga_[3]; ga[4] = gb_[0]; ga[5] = gb_[1]; ga[6] = gb_[2]; ga[7] = gb_[3]; } while (0)
; #define MU_COMPUTE(buf) MU_COMPUTE_N(buf, NMU)
; #define MU_END(last) do { if (last) asm volatile("s_waitcnt vmcnt(0)" ::: "memory"); else asm volatile("s_waitcnt vmcnt(8)" ::: "memory"); \
;         asm volatile("s_waitcnt lgkmcnt(0)" ::: "memory"); __builtin_amdgcn_s_barrier(); asm volatile("" ::: "memory"); } while (0)
; template <int MODE>
; __device__ __forceinline__ void moe_unit(PG8_LAS unsigned char* lds, int e, int cb, int slot0  , int nv  , const bf16_t* A, const int* slot_tok,
;                                          const float* W0, const float* W1, bf16_t* OUT, const float* slot_rs  , const int* slot_dst) {
;     ...
;     for (int t = 0; t < nt; t += 2) {
;         if (t + 2 < nt) MU_B_WAIT(s1, 8); else MU_B_WAIT(s1, 0);
;         MU_G_LOAD(g0, t + 1); MU_B_WRITE(s1, 1, g0); __builtin_amdgcn_sched_barrier(0); MU_GLDS_A(1, t + 1); __builtin_amdgcn_sched_barrier(0);
;         if (t + 3 < nt) { MU_B_ISSUE(s1, t + 3); }
;         MU_COMPUTE(0);
;         MU_END(t + 3 >= nt);
;         if (t + 2 < nt) { MU_B_WAIT(s0, 8); MU_G_LOAD(g0, t + 2); MU_B_WRITE(s0, 0, g0); __builtin_amdgcn_sched_barrier(0); MU_GLDS_A(0, t + 2); __builtin_amdgcn_sched_barrier(0); }
;         if (t + 4 < nt) { MU_B_ISSUE(s0, t + 4); }
;         MU_COMPUTE(1);
;         MU_END(t + 4 >= nt);
	s_add_i32 s47, s44, s6
	s_add_u32 s30, s30, 0x80
	s_addc_u32 s31, s31, 0
	v_mfma_f32_16x16x32_bf16 v[78:81], v[142:145], v[218:221], v[78:81]
	v_mfma_f32_16x16x32_bf16 v[74:77], v[146:149], v[218:221], v[74:77]
	v_mfma_f32_16x16x32_bf16 v[70:73], v[150:153], v[218:221], v[70:73]
	v_mfma_f32_16x16x32_bf16 v[66:69], v[154:157], v[218:221], v[66:69]
	s_mov_b32 m0, s47
	s_nop 0
	global_load_lds_dwordx4 v86, s[30:31]
	v_mfma_f32_16x16x32_bf16 v[62:65], v[142:145], v[222:225], v[62:65]
	v_mfma_f32_16x16x32_bf16 v[58:61], v[146:149], v[222:225], v[58:61]
	v_mfma_f32_16x16x32_bf16 v[54:57], v[150:153], v[222:225], v[54:57]
	v_mfma_f32_16x16x32_bf16 v[50:53], v[154:157], v[222:225], v[50:53]
	s_add_i32 m0, s47, 0x2000
	s_nop 0
	global_load_lds_dwordx4 v134, s[30:31]
	v_mfma_f32_16x16x32_bf16 v[46:49], v[142:145], v[226:229], v[46:49]
	v_mfma_f32_16x16x32_bf16 v[42:45], v[146:149], v[226:229], v[42:45]
	v_mfma_f32_16x16x32_bf16 v[38:41], v[150:153], v[226:229], v[38:41]
	v_mfma_f32_16x16x32_bf16 v[34:37], v[154:157], v[226:229], v[34:37]
	s_add_i32 m0, s47, 0x4000
	s_nop 0
	global_load_lds_dwordx4 v136, s[30:31]
	v_mfma_f32_16x16x32_bf16 v[18:21], v[142:145], v[230:233], v[18:21]
	v_mfma_f32_16x16x32_bf16 v[22:25], v[146:149], v[230:233], v[22:25]
	v_mfma_f32_16x16x32_bf16 v[26:29], v[150:153], v[230:233], v[26:29]
	v_mfma_f32_16x16x32_bf16 v[30:33], v[154:157], v[230:233], v[30:33]
	s_add_i32 m0, s47, 0x6000
	s_nop 0
	global_load_lds_dwordx4 v138, s[30:31]
	s_add_i32 m0, s47, 0x8000
	s_nop 0
	global_load_lds_dwordx4 v140, s[30:31]
	v_mul_f32_e32 v186, s12, v186
	v_mul_f32_e32 v187, s12, v187
	v_mul_f32_e32 v188, s13, v188
	v_mul_f32_e32 v189, s13, v189
	v_mul_f32_e32 v190, s14, v190
	v_mul_f32_e32 v191, s14, v191
	v_mul_f32_e32 v192, s15, v192
	v_mul_f32_e32 v193, s15, v193
	v_mul_f32_e32 v194, s16, v194
	v_mul_f32_e32 v195, s16, v195
	v_mul_f32_e32 v196, s17, v196
	v_mul_f32_e32 v197, s17, v197
	v_mul_f32_e32 v198, s18, v198
	v_mul_f32_e32 v199, s18, v199
	v_mul_f32_e32 v200, s19, v200
	v_mul_f32_e32 v201, s19, v201
	v_cvt_pk_bf16_f32 v158, v186, v188
	v_cvt_pk_bf16_f32 v159, v190, v192
	v_cvt_pk_bf16_f32 v160, v194, v196
	v_cvt_pk_bf16_f32 v161, v198, v200
	v_cvt_pk_bf16_f32 v162, v187, v189
	v_cvt_pk_bf16_f32 v163, v191, v193
	v_cvt_pk_bf16_f32 v164, v195, v197
	v_cvt_pk_bf16_f32 v165, v199, v201
	ds_write_b128 v1, v[158:161] offset:0
	ds_write_b128 v1, v[162:165] offset:128
	v_add_u32_e32 v91, s42, v135
	v_add_u32_e32 v93, s42, v137
	ds_read_b128 v[238:241], v139 offset:19456
	ds_read_b128 v[242:245], v139 offset:21504
	ds_read_b128 v[246:249], v139 offset:23552
	ds_read_b128 v[250:253], v139 offset:25600
	ds_read_b128 v[218:221], v91 offset:0
	ds_read_b128 v[222:225], v91 offset:2048
	ds_read_b128 v[226:229], v91 offset:4096
	ds_read_b128 v[230:233], v91 offset:6144
	s_waitcnt lgkmcnt(0)
	s_load_dwordx8 s[20:27], s[28:29], 0x0
	s_add_u32 s28, s28, 0x100
	s_addc_u32 s29, s29, 0
	v_mfma_f32_16x16x32_bf16 v[78:81], v[238:241], v[218:221], v[78:81]
	v_mfma_f32_16x16x32_bf16 v[74:77], v[242:245], v[218:221], v[74:77]
	v_mfma_f32_16x16x32_bf16 v[70:73], v[246:249], v[218:221], v[70:73]
	v_mfma_f32_16x16x32_bf16 v[66:69], v[250:253], v[218:221], v[66:69]
	ds_read_b128 v[218:221], v93 offset:0
	ds_read_b128 v[142:145], v141 offset:19456
	v_mfma_f32_16x16x32_bf16 v[62:65], v[238:241], v[222:225], v[62:65]
	v_mfma_f32_16x16x32_bf16 v[58:61], v[242:245], v[222:225], v[58:61]
	v_mfma_f32_16x16x32_bf16 v[54:57], v[246:249], v[222:225], v[54:57]
	v_mfma_f32_16x16x32_bf16 v[50:53], v[250:253], v[222:225], v[50:53]
	ds_read_b128 v[222:225], v93 offset:2048
	ds_read_b128 v[146:149], v141 offset:21504
	v_mfma_f32_16x16x32_bf16 v[46:49], v[238:241], v[226:229], v[46:49]
	v_mfma_f32_16x16x32_bf16 v[42:45], v[242:245], v[226:229], v[42:45]
	v_mfma_f32_16x16x32_bf16 v[38:41], v[246:249], v[226:229], v[38:41]
	v_mfma_f32_16x16x32_bf16 v[34:37], v[250:253], v[226:229], v[34:37]
	ds_read_b128 v[226:229], v93 offset:4096
	ds_read_b128 v[150:153], v141 offset:23552
	v_mfma_f32_16x16x32_bf16 v[18:21], v[238:241], v[230:233], v[18:21]
	v_mfma_f32_16x16x32_bf16 v[22:25], v[242:245], v[230:233], v[22:25]
	v_mfma_f32_16x16x32_bf16 v[26:29], v[246:249], v[230:233], v[26:29]
	v_mfma_f32_16x16x32_bf16 v[30:33], v[250:253], v[230:233], v[30:33]
	ds_read_b128 v[230:233], v93 offset:6144
	ds_read_b128 v[154:157], v141 offset:25600
	s_waitcnt vmcnt(5)
	s_mov_b32 s47, s42
	s_mov_b32 s42, s43
	s_mov_b32 s43, s44
	s_mov_b32 s44, s47
	s_waitcnt lgkmcnt(0)
	s_barrier
; #define MU_GLDS_A(buf, kt) do { _Pragma("unroll") for (int i = 0; i < NMU; ++i) \
;         __builtin_amdgcn_global_load_lds((const unsigned*)((const char*)A + aoff[i] + (size_t)(kt) * 128), (PG8_LAS unsigned*)(MU_SA(buf) + wid * 1024 + i * 8192), 16, 0, 0); } while (0)
; #define MU_B_ISSUE(sb, kt) do { const char* kb_ = Bb + (size_t)(kt) * (64 * (size_t)RB); _Pragma("unroll") for (int j = 0; j < 8; ++j) { const char* p_ = kb_ + (size_t)j * RB; \
;         asm volatile("global_load_dwordx2 %0, %1, off" : "=&v"(sb[j]) : "v"(p_) : "memory"); } } while (0)
; #define MU_B_WAIT(sb, N) asm volatile("s_waitcnt vmcnt(%8)" : "+v"(sb[0]), "+v"(sb[1]), "+v"(sb[2]), "+v"(sb[3]), "+v"(sb[4]), "+v"(sb[5]), "+v"(sb[6]), "+v"(sb[7]) : "n"(N) : "memory")
; #define MU_G_LOAD(ga, kt) do { const PG8_LAS f32x4* gk_ = (const PG8_LAS f32x4*)(lds + GAIN_OFF) + 16 * (kt) + 2 * wid; const f32x4 ga_ = gk_[0], gb_ = gk_[1]; \
;         ga[0] = ga_[0]; ga[1] = ga_[1]; ga[2] = ga_[2]; ga[3] = ga_[3]; ga[4] = gb_[0]; ga[5] = gb_[1]; ga[6] = gb_[2]; ga[7] = gb_[3]; } while (0)
; #define MU_COMPUTE(buf) MU_COMPUTE_N(buf, NMU)
; #define MU_END(last) do { if (last) asm volatile("s_waitcnt vmcnt(0)" ::: "memory"); else asm volatile("s_waitcnt vmcnt(8)" ::: "memory"); \
;         asm volatile("s_waitcnt lgkmcnt(0)" ::: "memory"); __builtin_amdgcn_s_barrier(); asm volatile("" ::: "memory"); } while (0)
; template <int MODE>
; __device__ __forceinline__ void moe_unit(PG8_LAS unsigned char* lds, int e, int cb, int slot0  , int nv  , const bf16_t* A, const int* slot_tok,
;                                          const float* W0, const float* W1, bf16_t* OUT, const float* slot_rs  , const int* slot_dst) {
;     ...
;     for (int t = 0; t < nt; t += 2) {
;         if (t + 2 < nt) MU_B_WAIT(s1, 8); else MU_B_WAIT(s1, 0);
;         MU_G_LOAD(g0, t + 1); MU_B_WRITE(s1, 1, g0); __builtin_amdgcn_sched_barrier(0); MU_GLDS_A(1, t + 1); __builtin_amdgcn_sched_barrier(0);
;         if (t + 3 < nt) { MU_B_ISSUE(s1, t + 3); }
;         MU_COMPUTE(0);
;         MU_END(t + 3 >= nt);
;         if (t + 2 < nt) { MU_B_WAIT(s0, 8); MU_G_LOAD(g0, t + 2); MU_B_WRITE(s0, 0, g0); __builtin_amdgcn_sched_barrier(0); MU_GLDS_A(0, t + 2); __builtin_amdgcn_sched_barrier(0); }
;         if (t + 4 < nt) { MU_B_ISSUE(s0, t + 4); }
;         MU_COMPUTE(1);
;         MU_END(t + 4 >= nt);
	v_mfma_f32_16x16x32_bf16 v[78:81], v[142:145], v[218:221], v[78:81]
	v_mfma_f32_16x16x32_bf16 v[74:77], v[146:149], v[218:221], v[74:77]
	v_mfma_f32_16x16x32_bf16 v[70:73], v[150:153], v[218:221], v[70:73]
	v_mfma_f32_16x16x32_bf16 v[66:69], v[154:157], v[218:221], v[66:69]
	v_mfma_f32_16x16x32_bf16 v[62:65], v[142:145], v[222:225], v[62:65]
	v_mfma_f32_16x16x32_bf16 v[58:61], v[146:149], v[222:225], v[58:61]
	v_mfma_f32_16x16x32_bf16 v[54:57], v[150:153], v[222:225], v[54:57]
	v_mfma_f32_16x16x32_bf16 v[50:53], v[154:157], v[222:225], v[50:53]
	v_mfma_f32_16x16x32_bf16 v[46:49], v[142:145], v[226:229], v[46:49]
	v_mfma_f32_16x16x32_bf16 v[42:45], v[146:149], v[226:229], v[42:45]
	v_mfma_f32_16x16x32_bf16 v[38:41], v[150:153], v[226:229], v[38:41]
	v_mfma_f32_16x16x32_bf16 v[34:37], v[154:157], v[226:229], v[34:37]
	v_mfma_f32_16x16x32_bf16 v[18:21], v[142:145], v[230:233], v[18:21]
	v_mfma_f32_16x16x32_bf16 v[22:25], v[146:149], v[230:233], v[22:25]
	v_mfma_f32_16x16x32_bf16 v[26:29], v[150:153], v[230:233], v[26:29]
	v_mfma_f32_16x16x32_bf16 v[30:33], v[154:157], v[230:233], v[30:33]
	v_mul_f32_e32 v202, s20, v202
	v_mul_f32_e32 v203, s20, v203
	v_mul_f32_e32 v204, s21, v204
	v_mul_f32_e32 v205, s21, v205
	v_mul_f32_e32 v206, s22, v206
	v_mul_f32_e32 v207, s22, v207
	v_mul_f32_e32 v208, s23, v208
	v_mul_f32_e32 v209, s23, v209
	v_mul_f32_e32 v210, s24, v210
	v_mul_f32_e32 v211, s24, v211
	v_mul_f32_e32 v212, s25, v212
	v_mul_f32_e32 v213, s25, v213
	v_mul_f32_e32 v214, s26, v214
	v_mul_f32_e32 v215, s26, v215
	v_mul_f32_e32 v216, s27, v216
	v_mul_f32_e32 v217, s27, v217
	v_cvt_pk_bf16_f32 v158, v202, v204
	v_cvt_pk_bf16_f32 v159, v206, v208
	v_cvt_pk_bf16_f32 v160, v210, v212
	v_cvt_pk_bf16_f32 v161, v214, v216
	v_cvt_pk_bf16_f32 v162, v203, v205
	v_cvt_pk_bf16_f32 v163, v207, v209
	v_cvt_pk_bf16_f32 v164, v211, v213
	v_cvt_pk_bf16_f32 v165, v215, v217
	ds_write_b128 v1, v[158:161] offset:19456
	ds_write_b128 v1, v[162:165] offset:19584
	v_add_u32_e32 v91, s42, v135
	v_add_u32_e32 v93, s42, v137
	ds_read_b128 v[238:241], v139 offset:0
	ds_read_b128 v[242:245], v139 offset:2048
	ds_read_b128 v[246:249], v139 offset:4096
	ds_read_b128 v[250:253], v139 offset:6144
	ds_read_b128 v[218:221], v91 offset:0
	ds_read_b128 v[222:225], v91 offset:2048
	ds_read_b128 v[226:229], v91 offset:4096
	ds_read_b128 v[230:233], v91 offset:6144
	s_waitcnt lgkmcnt(0)
	v_mfma_f32_16x16x32_bf16 v[78:81], v[238:241], v[218:221], v[78:81]
	v_mfma_f32_16x16x32_bf16 v[74:77], v[242:245], v[218:221], v[74:77]
	v_mfma_f32_16x16x32_bf16 v[70:73], v[246:249], v[218:221], v[70:73]
	v_mfma_f32_16x16x32_bf16 v[66:69], v[250:253], v[218:221], v[66:69]
	ds_read_b128 v[218:221], v93 offset:0
	ds_read_b128 v[142:145], v141 offset:0
	v_mfma_f32_16x16x32_bf16 v[62:65], v[238:241], v[222:225], v[62:65]
	v_mfma_f32_16x16x32_bf16 v[58:61], v[242:245], v[222:225], v[58:61]
	v_mfma_f32_16x16x32_bf16 v[54:57], v[246:249], v[222:225], v[54:57]
	v_mfma_f32_16x16x32_bf16 v[50:53], v[250:253], v[222:225], v[50:53]
	ds_read_b128 v[222:225], v93 offset:2048
	ds_read_b128 v[146:149], v141 offset:2048
	v_mfma_f32_16x16x32_bf16 v[46:49], v[238:241], v[226:229], v[46:49]
	v_mfma_f32_16x16x32_bf16 v[42:45], v[242:245], v[226:229], v[42:45]
	v_mfma_f32_16x16x32_bf16 v[38:41], v[246:249], v[226:229], v[38:41]
	v_mfma_f32_16x16x32_bf16 v[34:37], v[250:253], v[226:229], v[34:37]
	ds_read_b128 v[226:229], v93 offset:4096
	ds_read_b128 v[150:153], v141 offset:4096
	v_mfma_f32_16x16x32_bf16 v[18:21], v[238:241], v[230:233], v[18:21]
	v_mfma_f32_16x16x32_bf16 v[22:25], v[242:245], v[230:233], v[22:25]
	v_mfma_f32_16x16x32_bf16 v[26:29], v[246:249], v[230:233], v[26:29]
	v_mfma_f32_16x16x32_bf16 v[30:33], v[250:253], v[230:233], v[30:33]
	ds_read_b128 v[230:233], v93 offset:6144
	ds_read_b128 v[154:157], v141 offset:6144
	s_waitcnt vmcnt(0)
	s_mov_b32 s47, s42
	s_mov_b32 s42, s43
	s_mov_b32 s43, s44
	s_mov_b32 s44, s47
	s_waitcnt lgkmcnt(0)
	s_barrier
	v_mfma_f32_16x16x32_bf16 v[78:81], v[142:145], v[218:221], v[78:81]
	v_mfma_f32_16x16x32_bf16 v[74:77], v[146:149], v[218:221], v[74:77]
	v_mfma_f32_16x16x32_bf16 v[70:73], v[150:153], v[218:221], v[70:73]
	v_mfma_f32_16x16x32_bf16 v[66:69], v[154:157], v[218:221], v[66:69]
	v_mfma_f32_16x16x32_bf16 v[62:65], v[142:145], v[222:225], v[62:65]
	v_mfma_f32_16x16x32_bf16 v[58:61], v[146:149], v[222:225], v[58:61]
	v_mfma_f32_16x16x32_bf16 v[54:57], v[150:153], v[222:225], v[54:57]
	v_mfma_f32_16x16x32_bf16 v[50:53], v[154:157], v[222:225], v[50:53]
	v_mfma_f32_16x16x32_bf16 v[46:49], v[142:145], v[226:229], v[46:49]
	v_mfma_f32_16x16x32_bf16 v[42:45], v[146:149], v[226:229], v[42:45]
	v_mfma_f32_16x16x32_bf16 v[38:41], v[150:153], v[226:229], v[38:41]
	v_mfma_f32_16x16x32_bf16 v[34:37], v[154:157], v[226:229], v[34:37]
	v_mfma_f32_16x16x32_bf16 v[18:21], v[142:145], v[230:233], v[18:21]
	v_mfma_f32_16x16x32_bf16 v[22:25], v[146:149], v[230:233], v[22:25]
	v_mfma_f32_16x16x32_bf16 v[26:29], v[150:153], v[230:233], v[26:29]
	v_mfma_f32_16x16x32_bf16 v[30:33], v[154:157], v[230:233], v[30:33]
	v_add_u32_e32 v91, s42, v135
	v_add_u32_e32 v93, s42, v137
	ds_read_b128 v[238:241], v139 offset:19456
	ds_read_b128 v[242:245], v139 offset:21504
	ds_read_b128 v[246:249], v139 offset:23552
	ds_read_b128 v[250:253], v139 offset:25600
	ds_read_b128 v[218:221], v91 offset:0
	ds_read_b128 v[222:225], v91 offset:2048
	ds_read_b128 v[226:229], v91 offset:4096
	ds_read_b128 v[230:233], v91 offset:6144
	s_waitcnt lgkmcnt(0)
	v_mfma_f32_16x16x32_bf16 v[78:81], v[238:241], v[218:221], v[78:81]
	v_mfma_f32_16x16x32_bf16 v[74:77], v[242:245], v[218:221], v[74:77]
	v_mfma_f32_16x16x32_bf16 v[70:73], v[246:249], v[218:221], v[70:73]
	v_mfma_f32_16x16x32_bf16 v[66:69], v[250:253], v[218:221], v[66:69]
	ds_read_b128 v[218:221], v93 offset:0
	ds_read_b128 v[142:145], v141 offset:19456
	v_mfma_f32_16x16x32_bf16 v[62:65], v[238:241], v[222:225], v[62:65]
	v_mfma_f32_16x16x32_bf16 v[58:61], v[242:245], v[222:225], v[58:61]
	v_mfma_f32_16x16x32_bf16 v[54:57], v[246:249], v[222:225], v[54:57]
	v_mfma_f32_16x16x32_bf16 v[50:53], v[250:253], v[222:225], v[50:53]
	ds_read_b128 v[222:225], v93 offset:2048
	ds_read_b128 v[146:149], v141 offset:21504
	v_mfma_f32_16x16x32_bf16 v[46:49], v[238:241], v[226:229], v[46:49]
	v_mfma_f32_16x16x32_bf16 v[42:45], v[242:245], v[226:229], v[42:45]
	v_mfma_f32_16x16x32_bf16 v[38:41], v[246:249], v[226:229], v[38:41]
	v_mfma_f32_16x16x32_bf16 v[34:37], v[250:253], v[226:229], v[34:37]
	ds_read_b128 v[226:229], v93 offset:4096
	ds_read_b128 v[150:153], v141 offset:23552
	v_mfma_f32_16x16x32_bf16 v[18:21], v[238:241], v[230:233], v[18:21]
	v_mfma_f32_16x16x32_bf16 v[22:25], v[242:245], v[230:233], v[22:25]
	v_mfma_f32_16x16x32_bf16 v[26:29], v[246:249], v[230:233], v[26:29]
	v_mfma_f32_16x16x32_bf16 v[30:33], v[250:253], v[230:233], v[30:33]
	ds_read_b128 v[230:233], v93 offset:6144
	ds_read_b128 v[154:157], v141 offset:25600
	s_mov_b32 s47, s42
	s_mov_b32 s42, s43
	s_mov_b32 s43, s44
	s_mov_b32 s44, s47
	s_waitcnt lgkmcnt(0)
	s_barrier
; #define MU_GLDS_A(buf, kt) do { _Pragma("unroll") for (int i = 0; i < NMU; ++i) \
;         __builtin_amdgcn_global_load_lds((const unsigned*)((const char*)A + aoff[i] + (size_t)(kt) * 128), (PG8_LAS unsigned*)(MU_SA(buf) + wid * 1024 + i * 8192), 16, 0, 0); } while (0)
; #define MU_B_ISSUE(sb, kt) do { const char* kb_ = Bb + (size_t)(kt) * (64 * (size_t)RB); _Pragma("unroll") for (int j = 0; j < 8; ++j) { const char* p_ = kb_ + (size_t)j * RB; \
;         asm volatile("global_load_dwordx2 %0, %1, off" : "=&v"(sb[j]) : "v"(p_) : "memory"); } } while (0)
; #define MU_B_WAIT(sb, N) asm volatile("s_waitcnt vmcnt(%8)" : "+v"(sb[0]), "+v"(sb[1]), "+v"(sb[2]), "+v"(sb[3]), "+v"(sb[4]), "+v"(sb[5]), "+v"(sb[6]), "+v"(sb[7]) : "n"(N) : "memory")
; #define MU_G_LOAD(ga, kt) do { const PG8_LAS f32x4* gk_ = (const PG8_LAS f32x4*)(lds + GAIN_OFF) + 16 * (kt) + 2 * wid; const f32x4 ga_ = gk_[0], gb_ = gk_[1]; \
;         ga[0] = ga_[0]; ga[1] = ga_[1]; ga[2] = ga_[2]; ga[3] = ga_[3]; ga[4] = gb_[0]; ga[5] = gb_[1]; ga[6] = gb_[2]; ga[7] = gb_[3]; } while (0)
; #define MU_COMPUTE(buf) MU_COMPUTE_N(buf, NMU)
; #define MU_END(last) do { if (last) asm volatile("s_waitcnt vmcnt(0)" ::: "memory"); else asm volatile("s_waitcnt vmcnt(8)" ::: "memory"); \
;         asm volatile("s_waitcnt lgkmcnt(0)" ::: "memory"); __builtin_amdgcn_s_barrier(); asm volatile("" ::: "memory"); } while (0)
; template <int MODE>
; __device__ __forceinline__ void moe_unit(PG8_LAS unsigned char* lds, int e, int cb, int slot0  , int nv  , const bf16_t* A, const int* slot_tok,
;                                          const float* W0, const float* W1, bf16_t* OUT, const float* slot_rs  , const int* slot_dst) {
;     ...
;     for (int t = 0; t < nt; t += 2) {
;         if (t + 2 < nt) MU_B_WAIT(s1, 8); else MU_B_WAIT(s1, 0);
;         MU_G_LOAD(g0, t + 1); MU_B_WRITE(s1, 1, g0); __builtin_amdgcn_sched_barrier(0); MU_GLDS_A(1, t + 1); __builtin_amdgcn_sched_barrier(0);
;         if (t + 3 < nt) { MU_B_ISSUE(s1, t + 3); }
;         MU_COMPUTE(0);
;         MU_END(t + 3 >= nt);
;         if (t + 2 < nt) { MU_B_WAIT(s0, 8); MU_G_LOAD(g0, t + 2); MU_B_WRITE(s0, 0, g0); __builtin_amdgcn_sched_barrier(0); MU_GLDS_A(0, t + 2); __builtin_amdgcn_sched_barrier(0); }
;         if (t + 4 < nt) { MU_B_ISSUE(s0, t + 4); }
	v_mfma_f32_16x16x32_bf16 v[78:81], v[142:145], v[218:221], v[78:81]
	v_mfma_f32_16x16x32_bf16 v[74:77], v[146:149], v[218:221], v[74:77]
	v_mfma_f32_16x16x32_bf16 v[70:73], v[150:153], v[218:221], v[70:73]
	v_mfma_f32_16x16x32_bf16 v[66:69], v[154:157], v[218:221], v[66:69]
	v_mfma_f32_16x16x32_bf16 v[62:65], v[142:145], v[222:225], v[62:65]
	v_mfma_f32_16x16x32_bf16 v[58:61], v[146:149], v[222:225], v[58:61]
	v_mfma_f32_16x16x32_bf16 v[54:57], v[150:153], v[222:225], v[54:57]
	v_mfma_f32_16x16x32_bf16 v[50:53], v[154:157], v[222:225], v[50:53]
	v_mfma_f32_16x16x32_bf16 v[46:49], v[142:145], v[226:229], v[46:49]
	v_mfma_f32_16x16x32_bf16 v[42:45], v[146:149], v[226:229], v[42:45]
	v_mfma_f32_16x16x32_bf16 v[38:41], v[150:153], v[226:229], v[38:41]
	v_mfma_f32_16x16x32_bf16 v[34:37], v[154:157], v[226:229], v[34:37]
	v_mfma_f32_16x16x32_bf16 v[18:21], v[142:145], v[230:233], v[18:21]
	v_mfma_f32_16x16x32_bf16 v[22:25], v[146:149], v[230:233], v[22:25]
	v_mfma_f32_16x16x32_bf16 v[26:29], v[150:153], v[230:233], v[26:29]
	v_mfma_f32_16x16x32_bf16 v[30:33], v[154:157], v[230:233], v[30:33]
	s_branch .Lmu_done
.Lmu_frag5:
	s_cmp_gt_u32 s62, 3
	s_cbranch_scc1 .Lmu_grpY5
	s_waitcnt vmcnt(24)
	v_mul_f32_e32 v114, s20, v114
	v_mul_f32_e32 v115, s20, v115
	v_mul_f32_e32 v116, s21, v116
	v_mul_f32_e32 v117, s21, v117
	v_mul_f32_e32 v118, s22, v118
	v_mul_f32_e32 v119, s22, v119
	v_mul_f32_e32 v120, s23, v120
	v_mul_f32_e32 v121, s23, v121
	v_mul_f32_e32 v122, s24, v122
	v_mul_f32_e32 v123, s24, v123
	v_mul_f32_e32 v124, s25, v124
	v_mul_f32_e32 v125, s25, v125
	v_mul_f32_e32 v126, s26, v126
	v_mul_f32_e32 v127, s26, v127
	v_mul_f32_e32 v128, s27, v128
	v_mul_f32_e32 v129, s27, v129
	v_cvt_pk_bf16_f32 v158, v114, v116
	v_cvt_pk_bf16_f32 v159, v118, v120
	v_cvt_pk_bf16_f32 v160, v122, v124
	v_cvt_pk_bf16_f32 v161, v126, v128
	v_cvt_pk_bf16_f32 v162, v115, v117
	v_cvt_pk_bf16_f32 v163, v119, v121
	v_cvt_pk_bf16_f32 v164, v123, v125
	v_cvt_pk_bf16_f32 v165, v127, v129
	ds_write_b128 v1, v[158:161] offset:19456
	ds_write_b128 v1, v[162:165] offset:19584
	v_add_u32_e32 v91, s42, v135
	v_add_u32_e32 v93, s42, v137
	ds_read_b128 v[238:241], v139 offset:0
	ds_read_b128 v[242:245], v139 offset:2048
	ds_read_b128 v[246:249], v139 offset:4096
	ds_read_b128 v[250:253], v139 offset:6144
	ds_read_b128 v[218:221], v91 offset:0
	ds_read_b128 v[222:225], v91 offset:2048
	ds_read_b128 v[226:229], v91 offset:4096
	ds_read_b128 v[230:233], v91 offset:6144
	ds_read_b128 v[234:237], v91 offset:8192
	s_add_i32 s47, s44, s6
	s_add_u32 s30, s30, 0x80
	s_addc_u32 s31, s31, 0
	s_waitcnt lgkmcnt(0)
	v_mfma_f32_16x16x32_bf16 v[78:81], v[238:241], v[218:221], v[78:81]
	v_mfma_f32_16x16x32_bf16 v[74:77], v[242:245], v[218:221], v[74:77]
	v_mfma_f32_16x16x32_bf16 v[70:73], v[246:249], v[218:221], v[70:73]
	v_mfma_f32_16x16x32_bf16 v[66:69], v[250:253], v[218:221], v[66:69]
	ds_read_b128 v[218:221], v93 offset:0
	ds_read_b128 v[142:145], v141 offset:0
	s_mov_b32 m0, s47
	s_nop 0
	global_load_lds_dwordx4 v86, s[30:31]
	v_mfma_f32_16x16x32_bf16 v[62:65], v[238:241], v[222:225], v[62:65]
	v_mfma_f32_16x16x32_bf16 v[58:61], v[242:245], v[222:225], v[58:61]
	v_mfma_f32_16x16x32_bf16 v[54:57], v[246:249], v[222:225], v[54:57]
	v_mfma_f32_16x16x32_bf16 v[50:53], v[250:253], v[222:225], v[50:53]
	ds_read_b128 v[222:225], v93 offset:2048
	ds_read_b128 v[146:149], v141 offset:2048
	s_add_i32 m0, s47, 0x2000
	s_nop 0
	global_load_lds_dwordx4 v134, s[30:31]
	v_mfma_f32_16x16x32_bf16 v[46:49], v[238:241], v[226:229], v[46:49]
	v_mfma_f32_16x16x32_bf16 v[42:45], v[242:245], v[226:229], v[42:45]
	v_mfma_f32_16x16x32_bf16 v[38:41], v[246:249], v[226:229], v[38:41]
	v_mfma_f32_16x16x32_bf16 v[34:37], v[250:253], v[226:229], v[34:37]
	ds_read_b128 v[226:229], v93 offset:4096
	ds_read_b128 v[150:153], v141 offset:4096
	s_add_i32 m0, s47, 0x4000
	s_nop 0
	global_load_lds_dwordx4 v136, s[30:31]
	v_mfma_f32_16x16x32_bf16 v[18:21], v[238:241], v[230:233], v[18:21]
	v_mfma_f32_16x16x32_bf16 v[22:25], v[242:245], v[230:233], v[22:25]
	v_mfma_f32_16x16x32_bf16 v[26:29], v[246:249], v[230:233], v[26:29]
	v_mfma_f32_16x16x32_bf16 v[30:33], v[250:253], v[230:233], v[30:33]
	ds_read_b128 v[230:233], v93 offset:6144
	ds_read_b128 v[154:157], v141 offset:6144
	s_add_i32 m0, s47, 0x6000
	s_nop 0
	global_load_lds_dwordx4 v138, s[30:31]
	v_mfma_f32_16x16x32_bf16 v[2:5], v[238:241], v[234:237], v[2:5]
	v_mfma_f32_16x16x32_bf16 v[6:9], v[242:245], v[234:237], v[6:9]
	v_mfma_f32_16x16x32_bf16 v[10:13], v[246:249], v[234:237], v[10:13]
	v_mfma_f32_16x16x32_bf16 v[14:17], v[250:253], v[234:237], v[14:17]
	ds_read_b128 v[234:237], v93 offset:8192
	s_add_i32 m0, s47, 0x8000
	s_nop 0
	global_load_lds_dwordx4 v140, s[30:31]
	s_waitcnt lgkmcnt(0)
	s_load_dwordx8 s[12:19], s[28:29], 0x0
	s_add_u32 s28, s28, 0x100
	s_addc_u32 s29, s29, 0
	v_mfma_f32_16x16x32_bf16 v[78:81], v[142:145], v[218:221], v[78:81]
	v_mfma_f32_16x16x32_bf16 v[74:77], v[146:149], v[218:221], v[74:77]
	v_mfma_f32_16x16x32_bf16 v[70:73], v[150:153], v[218:221], v[70:73]
	v_mfma_f32_16x16x32_bf16 v[66:69], v[154:157], v[218:221], v[66:69]
	v_lshl_add_u64 v[132:133], v[132:133], 0, s[40:41]
	global_load_dwordx2 v[114:115], v[132:133], off
	global_load_dwordx2 v[116:117], v[132:133], off offset:2048
	v_mfma_f32_16x16x32_bf16 v[62:65], v[142:145], v[222:225], v[62:65]
	v_mfma_f32_16x16x32_bf16 v[58:61], v[146:149], v[222:225], v[58:61]
	v_mfma_f32_16x16x32_bf16 v[54:57], v[150:153], v[222:225], v[54:57]
	v_mfma_f32_16x16x32_bf16 v[50:53], v[154:157], v[222:225], v[50:53]
	v_lshl_add_u64 v[166:167], v[132:133], 0, s[34:35]
	global_load_dwordx2 v[118:119], v[166:167], off
	global_load_dwordx2 v[120:121], v[166:167], off offset:2048
	v_mfma_f32_16x16x32_bf16 v[46:49], v[142:145], v[226:229], v[46:49]
	v_mfma_f32_16x16x32_bf16 v[42:45], v[146:149], v[226:229], v[42:45]
	v_mfma_f32_16x16x32_bf16 v[38:41], v[150:153], v[226:229], v[38:41]
	v_mfma_f32_16x16x32_bf16 v[34:37], v[154:157], v[226:229], v[34:37]
	v_lshl_add_u64 v[166:167], v[132:133], 0, s[36:37]
	global_load_dwordx2 v[122:123], v[166:167], off
	global_load_dwordx2 v[124:125], v[166:167], off offset:2048
	v_mfma_f32_16x16x32_bf16 v[18:21], v[142:145], v[230:233], v[18:21]
	v_mfma_f32_16x16x32_bf16 v[22:25], v[146:149], v[230:233], v[22:25]
	v_mfma_f32_16x16x32_bf16 v[26:29], v[150:153], v[230:233], v[26:29]
	v_mfma_f32_16x16x32_bf16 v[30:33], v[154:157], v[230:233], v[30:33]
	v_lshl_add_u64 v[166:167], v[132:133], 0, s[38:39]
	global_load_dwordx2 v[126:127], v[166:167], off
	global_load_dwordx2 v[128:129], v[166:167], off offset:2048
	v_mfma_f32_16x16x32_bf16 v[2:5], v[142:145], v[234:237], v[2:5]
	v_mfma_f32_16x16x32_bf16 v[6:9], v[146:149], v[234:237], v[6:9]
	v_mfma_f32_16x16x32_bf16 v[10:13], v[150:153], v[234:237], v[10:13]
	v_mfma_f32_16x16x32_bf16 v[14:17], v[154:157], v[234:237], v[14:17]
	s_mov_b32 s47, s42
	s_mov_b32 s42, s43
	s_mov_b32 s43, s44
	s_mov_b32 s44, s47
	s_waitcnt lgkmcnt(0)
	s_barrier
; #define MU_GLDS_A(buf, kt) do { _Pragma("unroll") for (int i = 0; i < NMU; ++i) \
;         __builtin_amdgcn_global_load_lds((const unsigned*)((const char*)A + aoff[i] + (size_t)(kt) * 128), (PG8_LAS unsigned*)(MU_SA(buf) + wid * 1024 + i * 8192), 16, 0, 0); } while (0)
; #define MU_B_ISSUE(sb, kt) do { const char* kb_ = Bb + (size_t)(kt) * (64 * (size_t)RB); _Pragma("unroll") for (int j = 0; j < 8; ++j) { const char* p_ = kb_ + (size_t)j * RB; \
;         asm volatile("global_load_dwordx2 %0, %1, off" : "=&v"(sb[j]) : "v"(p_) : "memory"); } } while (0)
; #define MU_G_LOAD(ga, kt) do { const PG8_LAS f32x4* gk_ = (const PG8_LAS f32x4*)(lds + GAIN_OFF) + 16 * (kt) + 2 * wid; const f32x4 ga_ = gk_[0], gb_ = gk_[1]; \
;         ga[0] = ga_[0]; ga[1] = ga_[1]; ga[2] = ga_[2]; ga[3] = ga_[3]; ga[4] = gb_[0]; ga[5] = gb_[1]; ga[6] = gb_[2]; ga[7] = gb_[3]; } while (0)
; #define MU_COMPUTE(buf) MU_COMPUTE_N(buf, NMU)
; #define MU_END(last) do { if (last) asm volatile("s_waitcnt vmcnt(0)" ::: "memory"); else asm volatile("s_waitcnt vmcnt(8)" ::: "memory"); \
;         asm volatile("s_waitcnt lgkmcnt(0)" ::: "memory"); __builtin_amdgcn_s_barrier(); asm volatile("" ::: "memory"); } while (0)
; template <int MODE>
; __device__ __forceinline__ void moe_unit(PG8_LAS unsigned char* lds, int e, int cb, int slot0  , int nv  , const bf16_t* A, const int* slot_tok,
;                                          const float* W0, const float* W1, bf16_t* OUT, const float* slot_rs  , const int* slot_dst) {
;     ...
;         MU_G_LOAD(g0, t + 1); MU_B_WRITE(s1, 1, g0); __builtin_amdgcn_sched_barrier(0); MU_GLDS_A(1, t + 1); __builtin_amdgcn_sched_barrier(0);
;         if (t + 3 < nt) { MU_B_ISSUE(s1, t + 3); }
;         MU_COMPUTE(0);
;         MU_END(t + 3 >= nt);
	s_waitcnt vmcnt(29)
	v_mul_f32_e32 v186, s12, v186
	v_mul_f32_e32 v187, s12, v187
	v_mul_f32_e32 v188, s13, v188
	v_mul_f32_e32 v189, s13, v189
	v_mul_f32_e32 v190, s14, v190
	v_mul_f32_e32 v191, s14, v191
	v_mul_f32_e32 v192, s15, v192
	v_mul_f32_e32 v193, s15, v193
	v_mul_f32_e32 v194, s16, v194
	v_mul_f32_e32 v195, s16, v195
	v_mul_f32_e32 v196, s17, v196
	v_mul_f32_e32 v197, s17, v197
	v_mul_f32_e32 v198, s18, v198
	v_mul_f32_e32 v199, s18, v199
	v_mul_f32_e32 v200, s19, v200
	v_mul_f32_e32 v201, s19, v201
	v_cvt_pk_bf16_f32 v158, v186, v188
	v_cvt_pk_bf16_f32 v159, v190, v192
	v_cvt_pk_bf16_f32 v160, v194, v196
	v_cvt_pk_bf16_f32 v161, v198, v200
	v_cvt_pk_bf16_f32 v162, v187, v189
	v_cvt_pk_bf16_f32 v163, v191, v193
	v_cvt_pk_bf16_f32 v164, v195, v197
	v_cvt_pk_bf16_f32 v165, v199, v201
	ds_write_b128 v1, v[158:161] offset:0
	ds_write_b128 v1, v[162:165] offset:128
	v_add_u32_e32 v91, s42, v135
	v_add_u32_e32 v93, s42, v137
	ds_read_b128 v[238:241], v139 offset:19456
	ds_read_b128 v[242:245], v139 offset:21504
	ds_read_b128 v[246:249], v139 offset:23552
	ds_read_b128 v[250:253], v139 offset:25600
	ds_read_b128 v[218:221], v91 offset:0
	ds_read_b128 v[222:225], v91 offset:2048
	ds_read_b128 v[226:229], v91 offset:4096
	ds_read_b128 v[230:233], v91 offset:6144
	ds_read_b128 v[234:237], v91 offset:8192
	s_add_i32 s47, s44, s6
	s_add_u32 s30, s30, 0x80
	s_addc_u32 s31, s31, 0
	s_waitcnt lgkmcnt(0)
	v_mfma_f32_16x16x32_bf16 v[78:81], v[238:241], v[218:221], v[78:81]
	v_mfma_f32_16x16x32_bf16 v[74:77], v[242:245], v[218:221], v[74:77]
	v_mfma_f32_16x16x32_bf16 v[70:73], v[246:249], v[218:221], v[70:73]
	v_mfma_f32_16x16x32_bf16 v[66:69], v[250:253], v[218:221], v[66:69]
	ds_read_b128 v[218:221], v93 offset:0
	ds_read_b128 v[142:145], v141 offset:19456
	s_mov_b32 m0, s47
	s_nop 0
	global_load_lds_dwordx4 v86, s[30:31]
	v_mfma_f32_16x16x32_bf16 v[62:65], v[238:241], v[222:225], v[62:65]
	v_mfma_f32_16x16x32_bf16 v[58:61], v[242:245], v[222:225], v[58:61]
	v_mfma_f32_16x16x32_bf16 v[54:57], v[246:249], v[222:225], v[54:57]
	v_mfma_f32_16x16x32_bf16 v[50:53], v[250:253], v[222:225], v[50:53]
	ds_read_b128 v[222:225], v93 offset:2048
	ds_read_b128 v[146:149], v141 offset:21504
	s_add_i32 m0, s47, 0x2000
	s_nop 0
	global_load_lds_dwordx4 v134, s[30:31]
	v_mfma_f32_16x16x32_bf16 v[46:49], v[238:241], v[226:229], v[46:49]
	v_mfma_f32_16x16x32_bf16 v[42:45], v[242:245], v[226:229], v[42:45]
	v_mfma_f32_16x16x32_bf16 v[38:41], v[246:249], v[226:229], v[38:41]
	v_mfma_f32_16x16x32_bf16 v[34:37], v[250:253], v[226:229], v[34:37]
	ds_read_b128 v[226:229], v93 offset:4096
	ds_read_b128 v[150:153], v141 offset:23552
	s_add_i32 m0, s47, 0x4000
	s_nop 0
	global_load_lds_dwordx4 v136, s[30:31]
	v_mfma_f32_16x16x32_bf16 v[18:21], v[238:241], v[230:233], v[18:21]
	v_mfma_f32_16x16x32_bf16 v[22:25], v[242:245], v[230:233], v[22:25]
	v_mfma_f32_16x16x32_bf16 v[26:29], v[246:249], v[230:233], v[26:29]
	v_mfma_f32_16x16x32_bf16 v[30:33], v[250:253], v[230:233], v[30:33]
	ds_read_b128 v[230:233], v93 offset:6144
	ds_read_b128 v[154:157], v141 offset:25600
	s_add_i32 m0, s47, 0x6000
	s_nop 0
	global_load_lds_dwordx4 v138, s[30:31]
	v_mfma_f32_16x16x32_bf16 v[2:5], v[238:241], v[234:237], v[2:5]
	v_mfma_f32_16x16x32_bf16 v[6:9], v[242:245], v[234:237], v[6:9]
	v_mfma_f32_16x16x32_bf16 v[10:13], v[246:249], v[234:237], v[10:13]
	v_mfma_f32_16x16x32_bf16 v[14:17], v[250:253], v[234:237], v[14:17]
	ds_read_b128 v[234:237], v93 offset:8192
	s_add_i32 m0, s47, 0x8000
	s_nop 0
	global_load_lds_dwordx4 v140, s[30:31]
	s_waitcnt lgkmcnt(0)
	s_load_dwordx8 s[20:27], s[28:29], 0x0
	s_add_u32 s28, s28, 0x100
	s_addc_u32 s29, s29, 0
	v_mfma_f32_16x16x32_bf16 v[78:81], v[142:145], v[218:221], v[78:81]
	v_mfma_f32_16x16x32_bf16 v[74:77], v[146:149], v[218:221], v[74:77]
	v_mfma_f32_16x16x32_bf16 v[70:73], v[150:153], v[218:221], v[70:73]
	v_mfma_f32_16x16x32_bf16 v[66:69], v[154:157], v[218:221], v[66:69]
	v_lshl_add_u64 v[132:133], v[132:133], 0, s[40:41]
	global_load_dwordx2 v[186:187], v[132:133], off
	global_load_dwordx2 v[188:189], v[132:133], off offset:2048
	v_mfma_f32_16x16x32_bf16 v[62:65], v[142:145], v[222:225], v[62:65]
	v_mfma_f32_16x16x32_bf16 v[58:61], v[146:149], v[222:225], v[58:61]
	v_mfma_f32_16x16x32_bf16 v[54:57], v[150:153], v[222:225], v[54:57]
	v_mfma_f32_16x16x32_bf16 v[50:53], v[154:157], v[222:225], v[50:53]
	v_lshl_add_u64 v[166:167], v[132:133], 0, s[34:35]
	global_load_dwordx2 v[190:191], v[166:167], off
	global_load_dwordx2 v[192:193], v[166:167], off offset:2048
	v_mfma_f32_16x16x32_bf16 v[46:49], v[142:145], v[226:229], v[46:49]
	v_mfma_f32_16x16x32_bf16 v[42:45], v[146:149], v[226:229], v[42:45]
	v_mfma_f32_16x16x32_bf16 v[38:41], v[150:153], v[226:229], v[38:41]
	v_mfma_f32_16x16x32_bf16 v[34:37], v[154:157], v[226:229], v[34:37]
	v_lshl_add_u64 v[166:167], v[132:133], 0, s[36:37]
	global_load_dwordx2 v[194:195], v[166:167], off
	global_load_dwordx2 v[196:197], v[166:167], off offset:2048
	v_mfma_f32_16x16x32_bf16 v[18:21], v[142:145], v[230:233], v[18:21]
	v_mfma_f32_16x16x32_bf16 v[22:25], v[146:149], v[230:233], v[22:25]
	v_mfma_f32_16x16x32_bf16 v[26:29], v[150:153], v[230:233], v[26:29]
	v_mfma_f32_16x16x32_bf16 v[30:33], v[154:157], v[230:233], v[30:33]
	v_lshl_add_u64 v[166:167], v[132:133], 0, s[38:39]
	global_load_dwordx2 v[198:199], v[166:167], off
	global_load_dwordx2 v[200:201], v[166:167], off offset:2048
	v_mfma_f32_16x16x32_bf16 v[2:5], v[142:145], v[234:237], v[2:5]
	v_mfma_f32_16x16x32_bf16 v[6:9], v[146:149], v[234:237], v[6:9]
	v_mfma_f32_16x16x32_bf16 v[10:13], v[150:153], v[234:237], v[10:13]
	v_mfma_f32_16x16x32_bf16 v[14:17], v[154:157], v[234:237], v[14:17]
	s_waitcnt vmcnt(21)
	s_mov_b32 s47, s42
	s_mov_b32 s42, s43
	s_mov_b32 s43, s44
	s_mov_b32 s44, s47
	s_waitcnt lgkmcnt(0)
	s_barrier
; #define MU_GLDS_A(buf, kt) do { _Pragma("unroll") for (int i = 0; i < NMU; ++i) \
;         __builtin_amdgcn_global_load_lds((const unsigned*)((const char*)A + aoff[i] + (size_t)(kt) * 128), (PG8_LAS unsigned*)(MU_SA(buf) + wid * 1024 + i * 8192), 16, 0, 0); } while (0)
; #define MU_B_ISSUE(sb, kt) do { const char* kb_ = Bb + (size_t)(kt) * (64 * (size_t)RB); _Pragma("unroll") for (int j = 0; j < 8; ++j) { const char* p_ = kb_ + (size_t)j * RB; \
;         asm volatile("global_load_dwordx2 %0, %1, off" : "=&v"(sb[j]) : "v"(p_) : "memory"); } } while (0)
; #define MU_B_WAIT(sb, N) asm volatile("s_waitcnt vmcnt(%8)" : "+v"(sb[0]), "+v"(sb[1]), "+v"(sb[2]), "+v"(sb[3]), "+v"(sb[4]), "+v"(sb[5]), "+v"(sb[6]), "+v"(sb[7]) : "n"(N) : "memory")
; #define MU_G_LOAD(ga, kt) do { const PG8_LAS f32x4* gk_ = (const PG8_LAS f32x4*)(lds + GAIN_OFF) + 16 * (kt) + 2 * wid; const f32x4 ga_ = gk_[0], gb_ = gk_[1]; \
;         ga[0] = ga_[0]; ga[1] = ga_[1]; ga[2] = ga_[2]; ga[3] = ga_[3]; ga[4] = gb_[0]; ga[5] = gb_[1]; ga[6] = gb_[2]; ga[7] = gb_[3]; } while (0)
; #define MU_COMPUTE(buf) MU_COMPUTE_N(buf, NMU)
; #define MU_END(last) do { if (last) asm volatile("s_waitcnt vmcnt(0)" ::: "memory"); else asm volatile("s_waitcnt vmcnt(8)" ::: "memory"); \
;         asm volatile("s_waitcnt lgkmcnt(0)" ::: "memory"); __builtin_amdgcn_s_barrier(); asm volatile("" ::: "memory"); } while (0)
; template <int MODE>
; __device__ __forceinline__ void moe_unit(PG8_LAS unsigned char* lds, int e, int cb, int slot0  , int nv  , const bf16_t* A, const int* slot_tok,
;                                          const float* W0, const float* W1, bf16_t* OUT, const float* slot_rs  , const int* slot_dst) {
;     ...
;         if (t + 2 < nt) { MU_B_WAIT(s0, 8); MU_G_LOAD(g0, t + 2); MU_B_WRITE(s0, 0, g0); __builtin_amdgcn_sched_barrier(0); MU_GLDS_A(0, t + 2); __builtin_amdgcn_sched_barrier(0); }
;         if (t + 4 < nt) { MU_B_ISSUE(s0, t + 4); }
;         MU_COMPUTE(1);
;         MU_END(t + 4 >= nt);
	v_mul_f32_e32 v202, s20, v202
	v_mul_f32_e32 v203, s20, v203
	v_mul_f32_e32 v204, s21, v204
	v_mul_f32_e32 v205, s21, v205
	v_mul_f32_e32 v206, s22, v206
	v_mul_f32_e32 v207, s22, v207
	v_mul_f32_e32 v208, s23, v208
	v_mul_f32_e32 v209, s23, v209
	v_mul_f32_e32 v210, s24, v210
	v_mul_f32_e32 v211, s24, v211
	v_mul_f32_e32 v212, s25, v212
	v_mul_f32_e32 v213, s25, v213
	v_mul_f32_e32 v214, s26, v214
	v_mul_f32_e32 v215, s26, v215
	v_mul_f32_e32 v216, s27, v216
	v_mul_f32_e32 v217, s27, v217
	v_cvt_pk_bf16_f32 v158, v202, v204
	v_cvt_pk_bf16_f32 v159, v206, v208
	v_cvt_pk_bf16_f32 v160, v210, v212
	v_cvt_pk_bf16_f32 v161, v214, v216
	v_cvt_pk_bf16_f32 v162, v203, v205
	v_cvt_pk_bf16_f32 v163, v207, v209
	v_cvt_pk_bf16_f32 v164, v211, v213
	v_cvt_pk_bf16_f32 v165, v215, v217
	ds_write_b128 v1, v[158:161] offset:19456
	ds_write_b128 v1, v[162:165] offset:19584
	v_add_u32_e32 v91, s42, v135
	v_add_u32_e32 v93, s42, v137
	ds_read_b128 v[238:241], v139 offset:0
	ds_read_b128 v[242:245], v139 offset:2048
	ds_read_b128 v[246:249], v139 offset:4096
	ds_read_b128 v[250:253], v139 offset:6144
	ds_read_b128 v[218:221], v91 offset:0
	ds_read_b128 v[222:225], v91 offset:2048
	ds_read_b128 v[226:229], v91 offset:4096
	ds_read_b128 v[230:233], v91 offset:6144
	ds_read_b128 v[234:237], v91 offset:8192
	s_add_i32 s47, s44, s6
	s_add_u32 s30, s30, 0x80
	s_addc_u32 s31, s31, 0
	s_waitcnt lgkmcnt(0)
	v_mfma_f32_16x16x32_bf16 v[78:81], v[238:241], v[218:221], v[78:81]
	v_mfma_f32_16x16x32_bf16 v[74:77], v[242:245], v[218:221], v[74:77]
	v_mfma_f32_16x16x32_bf16 v[70:73], v[246:249], v[218:221], v[70:73]
	v_mfma_f32_16x16x32_bf16 v[66:69], v[250:253], v[218:221], v[66:69]
	ds_read_b128 v[218:221], v93 offset:0
	ds_read_b128 v[142:145], v141 offset:0
	s_mov_b32 m0, s47
	s_nop 0
	global_load_lds_dwordx4 v86, s[30:31]
	v_mfma_f32_16x16x32_bf16 v[62:65], v[238:241], v[222:225], v[62:65]
	v_mfma_f32_16x16x32_bf16 v[58:61], v[242:245], v[222:225], v[58:61]
	v_mfma_f32_16x16x32_bf16 v[54:57], v[246:249], v[222:225], v[54:57]
	v_mfma_f32_16x16x32_bf16 v[50:53], v[250:253], v[222:225], v[50:53]
	ds_read_b128 v[222:225], v93 offset:2048
	ds_read_b128 v[146:149], v141 offset:2048
	s_add_i32 m0, s47, 0x2000
	s_nop 0
	global_load_lds_dwordx4 v134, s[30:31]
	v_mfma_f32_16x16x32_bf16 v[46:49], v[238:241], v[226:229], v[46:49]
	v_mfma_f32_16x16x32_bf16 v[42:45], v[242:245], v[226:229], v[42:45]
	v_mfma_f32_16x16x32_bf16 v[38:41], v[246:249], v[226:229], v[38:41]
	v_mfma_f32_16x16x32_bf16 v[34:37], v[250:253], v[226:229], v[34:37]
	ds_read_b128 v[226:229], v93 offset:4096
	ds_read_b128 v[150:153], v141 offset:4096
	s_add_i32 m0, s47, 0x4000
	s_nop 0
	global_load_lds_dwordx4 v136, s[30:31]
	v_mfma_f32_16x16x32_bf16 v[18:21], v[238:241], v[230:233], v[18:21]
	v_mfma_f32_16x16x32_bf16 v[22:25], v[242:245], v[230:233], v[22:25]
	v_mfma_f32_16x16x32_bf16 v[26:29], v[246:249], v[230:233], v[26:29]
	v_mfma_f32_16x16x32_bf16 v[30:33], v[250:253], v[230:233], v[30:33]
	ds_read_b128 v[230:233], v93 offset:6144
	ds_read_b128 v[154:157], v141 offset:6144
	s_add_i32 m0, s47, 0x6000
	s_nop 0
	global_load_lds_dwordx4 v138, s[30:31]
	v_mfma_f32_16x16x32_bf16 v[2:5], v[238:241], v[234:237], v[2:5]
	v_mfma_f32_16x16x32_bf16 v[6:9], v[242:245], v[234:237], v[6:9]
	v_mfma_f32_16x16x32_bf16 v[10:13], v[246:249], v[234:237], v[10:13]
	v_mfma_f32_16x16x32_bf16 v[14:17], v[250:253], v[234:237], v[14:17]
	ds_read_b128 v[234:237], v93 offset:8192
	s_add_i32 m0, s47, 0x8000
	s_nop 0
	global_load_lds_dwordx4 v140, s[30:31]
	s_waitcnt lgkmcnt(0)
	s_load_dwordx8 s[12:19], s[28:29], 0x0
	s_add_u32 s28, s28, 0x100
	s_addc_u32 s29, s29, 0
	v_mfma_f32_16x16x32_bf16 v[78:81], v[142:145], v[218:221], v[78:81]
	v_mfma_f32_16x16x32_bf16 v[74:77], v[146:149], v[218:221], v[74:77]
	v_mfma_f32_16x16x32_bf16 v[70:73], v[150:153], v[218:221], v[70:73]
	v_mfma_f32_16x16x32_bf16 v[66:69], v[154:157], v[218:221], v[66:69]
	v_lshl_add_u64 v[132:133], v[132:133], 0, s[40:41]
	global_load_dwordx2 v[202:203], v[132:133], off
	global_load_dwordx2 v[204:205], v[132:133], off offset:2048
	v_mfma_f32_16x16x32_bf16 v[62:65], v[142:145], v[222:225], v[62:65]
	v_mfma_f32_16x16x32_bf16 v[58:61], v[146:149], v[222:225], v[58:61]
	v_mfma_f32_16x16x32_bf16 v[54:57], v[150:153], v[222:225], v[54:57]
	v_mfma_f32_16x16x32_bf16 v[50:53], v[154:157], v[222:225], v[50:53]
	v_lshl_add_u64 v[166:167], v[132:133], 0, s[34:35]
	global_load_dwordx2 v[206:207], v[166:167], off
	global_load_dwordx2 v[208:209], v[166:167], off offset:2048
	v_mfma_f32_16x16x32_bf16 v[46:49], v[142:145], v[226:229], v[46:49]
	v_mfma_f32_16x16x32_bf16 v[42:45], v[146:149], v[226:229], v[42:45]
	v_mfma_f32_16x16x32_bf16 v[38:41], v[150:153], v[226:229], v[38:41]
	v_mfma_f32_16x16x32_bf16 v[34:37], v[154:157], v[226:229], v[34:37]
	v_lshl_add_u64 v[166:167], v[132:133], 0, s[36:37]
	global_load_dwordx2 v[210:211], v[166:167], off
	global_load_dwordx2 v[212:213], v[166:167], off offset:2048
	v_mfma_f32_16x16x32_bf16 v[18:21], v[142:145], v[230:233], v[18:21]
	v_mfma_f32_16x16x32_bf16 v[22:25], v[146:149], v[230:233], v[22:25]
	v_mfma_f32_16x16x32_bf16 v[26:29], v[150:153], v[230:233], v[26:29]
	v_mfma_f32_16x16x32_bf16 v[30:33], v[154:157], v[230:233], v[30:33]
	v_lshl_add_u64 v[166:167], v[132:133], 0, s[38:39]
	global_load_dwordx2 v[214:215], v[166:167], off
	global_load_dwordx2 v[216:217], v[166:167], off offset:2048
	v_mfma_f32_16x16x32_bf16 v[2:5], v[142:145], v[234:237], v[2:5]
	v_mfma_f32_16x16x32_bf16 v[6:9], v[146:149], v[234:237], v[6:9]
	v_mfma_f32_16x16x32_bf16 v[10:13], v[150:153], v[234:237], v[10:13]
	v_mfma_f32_16x16x32_bf16 v[14:17], v[154:157], v[234:237], v[14:17]
	s_waitcnt vmcnt(21)
	s_mov_b32 s47, s42
	s_mov_b32 s42, s43
	s_mov_b32 s43, s44
	s_mov_b32 s44, s47
	s_waitcnt lgkmcnt(0)
	s_barrier
; #define MU_GLDS_A(buf, kt) do { _Pragma("unroll") for (int i = 0; i < NMU; ++i) \
;         __builtin_amdgcn_global_load_lds((const unsigned*)((const char*)A + aoff[i] + (size_t)(kt) * 128), (PG8_LAS unsigned*)(MU_SA(buf) + wid * 1024 + i * 8192), 16, 0, 0); } while (0)
; #define MU_B_ISSUE(sb, kt) do { const char* kb_ = Bb + (size_t)(kt) * (64 * (size_t)RB); _Pragma("unroll") for (int j = 0; j < 8; ++j) { const char* p_ = kb_ + (size_t)j * RB; \
;         asm volatile("global_load_dwordx2 %0, %1, off" : "=&v"(sb[j]) : "v"(p_) : "memory"); } } while (0)
; #define MU_B_WAIT(sb, N) asm volatile("s_waitcnt vmcnt(%8)" : "+v"(sb[0]), "+v"(sb[1]), "+v"(sb[2]), "+v"(sb[3]), "+v"(sb[4]), "+v"(sb[5]), "+v"(sb[6]), "+v"(sb[7]) : "n"(N) : "memory")
; #define MU_G_LOAD(ga, kt) do { const PG8_LAS f32x4* gk_ = (const PG8_LAS f32x4*)(lds + GAIN_OFF) + 16 * (kt) + 2 * wid; const f32x4 ga_ = gk_[0], gb_ = gk_[1]; \
;         ga[0] = ga_[0]; ga[1] = ga_[1]; ga[2] = ga_[2]; ga[3] = ga_[3]; ga[4] = gb_[0]; ga[5] = gb_[1]; ga[6] = gb_[2]; ga[7] = gb_[3]; } while (0)
; #define MU_COMPUTE(buf) MU_COMPUTE_N(buf, NMU)
; #define MU_END(last) do { if (last) asm volatile("s_waitcnt vmcnt(0)" ::: "memory"); else asm volatile("s_waitcnt vmcnt(8)" ::: "memory"); \
;         asm volatile("s_waitcnt lgkmcnt(0)" ::: "memory"); __builtin_amdgcn_s_barrier(); asm volatile("" ::: "memory"); } while (0)
; template <int MODE>
; __device__ __forceinline__ void moe_unit(PG8_LAS unsigned char* lds, int e, int cb, int slot0  , int nv  , const bf16_t* A, const int* slot_tok,
;                                          const float* W0, const float* W1, bf16_t* OUT, const float* slot_rs  , const int* slot_dst) {
;     ...
;     for (int t = 0; t < nt; t += 2) {
;         if (t + 2 < nt) MU_B_WAIT(s1, 8); else MU_B_WAIT(s1, 0);
;         MU_G_LOAD(g0, t + 1); MU_B_WRITE(s1, 1, g0); __builtin_amdgcn_sched_barrier(0); MU_GLDS_A(1, t + 1); __builtin_amdgcn_sched_barrier(0);
;         if (t + 3 < nt) { MU_B_ISSUE(s1, t + 3); }
;         MU_COMPUTE(0);
;         MU_END(t + 3 >= nt);
;         if (t + 2 < nt) { MU_B_WAIT(s0, 8); MU_G_LOAD(g0, t + 2); MU_B_WRITE(s0, 0, g0); __builtin_amdgcn_sched_barrier(0); MU_GLDS_A(0, t + 2); __builtin_amdgcn_sched_barrier(0); }
;         if (t + 4 < nt) { MU_B_ISSUE(s0, t + 4); }
;         MU_COMPUTE(1);
;         MU_END(t + 4 >= nt);
	v_mul_f32_e32 v98, s12, v98
	v_mul_f32_e32 v99, s12, v99
	v_mul_f32_e32 v100, s13, v100
	v_mul_f32_e32 v101, s13, v101
	v_mul_f32_e32 v102, s14, v102
	v_mul_f32_e32 v103, s14, v103
	v_mul_f32_e32 v104, s15, v104
	v_mul_f32_e32 v105, s15, v105
	v_mul_f32_e32 v106, s16, v106
	v_mul_f32_e32 v107, s16, v107
	v_mul_f32_e32 v108, s17, v108
	v_mul_f32_e32 v109, s17, v109
	v_mul_f32_e32 v110, s18, v110
	v_mul_f32_e32 v111, s18, v111
	v_mul_f32_e32 v112, s19, v112
	v_mul_f32_e32 v113, s19, v113
	v_cvt_pk_bf16_f32 v158, v98, v100
	v_cvt_pk_bf16_f32 v159, v102, v104
	v_cvt_pk_bf16_f32 v160, v106, v108
	v_cvt_pk_bf16_f32 v161, v110, v112
	v_cvt_pk_bf16_f32 v162, v99, v101
	v_cvt_pk_bf16_f32 v163, v103, v105
	v_cvt_pk_bf16_f32 v164, v107, v109
	v_cvt_pk_bf16_f32 v165, v111, v113
	ds_write_b128 v1, v[158:161] offset:0
	ds_write_b128 v1, v[162:165] offset:128
	v_add_u32_e32 v91, s42, v135
	v_add_u32_e32 v93, s42, v137
	ds_read_b128 v[238:241], v139 offset:19456
	ds_read_b128 v[242:245], v139 offset:21504
	ds_read_b128 v[246:249], v139 offset:23552
	ds_read_b128 v[250:253], v139 offset:25600
	ds_read_b128 v[218:221], v91 offset:0
	ds_read_b128 v[222:225], v91 offset:2048
	ds_read_b128 v[226:229], v91 offset:4096
	ds_read_b128 v[230:233], v91 offset:6144
	ds_read_b128 v[234:237], v91 offset:8192
	s_add_i32 s47, s44, s6
	s_add_u32 s30, s30, 0x80
	s_addc_u32 s31, s31, 0
	s_waitcnt lgkmcnt(0)
	v_mfma_f32_16x16x32_bf16 v[78:81], v[238:241], v[218:221], v[78:81]
	v_mfma_f32_16x16x32_bf16 v[74:77], v[242:245], v[218:221], v[74:77]
	v_mfma_f32_16x16x32_bf16 v[70:73], v[246:249], v[218:221], v[70:73]
	v_mfma_f32_16x16x32_bf16 v[66:69], v[250:253], v[218:221], v[66:69]
	ds_read_b128 v[218:221], v93 offset:0
	ds_read_b128 v[142:145], v141 offset:19456
	s_mov_b32 m0, s47
	s_nop 0
	global_load_lds_dwordx4 v86, s[30:31]
	v_mfma_f32_16x16x32_bf16 v[62:65], v[238:241], v[222:225], v[62:65]
	v_mfma_f32_16x16x32_bf16 v[58:61], v[242:245], v[222:225], v[58:61]
	v_mfma_f32_16x16x32_bf16 v[54:57], v[246:249], v[222:225], v[54:57]
	v_mfma_f32_16x16x32_bf16 v[50:53], v[250:253], v[222:225], v[50:53]
	ds_read_b128 v[222:225], v93 offset:2048
	ds_read_b128 v[146:149], v141 offset:21504
	s_add_i32 m0, s47, 0x2000
	s_nop 0
	global_load_lds_dwordx4 v134, s[30:31]
	v_mfma_f32_16x16x32_bf16 v[46:49], v[238:241], v[226:229], v[46:49]
	v_mfma_f32_16x16x32_bf16 v[42:45], v[242:245], v[226:229], v[42:45]
	v_mfma_f32_16x16x32_bf16 v[38:41], v[246:249], v[226:229], v[38:41]
	v_mfma_f32_16x16x32_bf16 v[34:37], v[250:253], v[226:229], v[34:37]
	ds_read_b128 v[226:229], v93 offset:4096
	ds_read_b128 v[150:153], v141 offset:23552
	s_add_i32 m0, s47, 0x4000
	s_nop 0
	global_load_lds_dwordx4 v136, s[30:31]
	v_mfma_f32_16x16x32_bf16 v[18:21], v[238:241], v[230:233], v[18:21]
	v_mfma_f32_16x16x32_bf16 v[22:25], v[242:245], v[230:233], v[22:25]
	v_mfma_f32_16x16x32_bf16 v[26:29], v[246:249], v[230:233], v[26:29]
	v_mfma_f32_16x16x32_bf16 v[30:33], v[250:253], v[230:233], v[30:33]
	ds_read_b128 v[230:233], v93 offset:6144
	ds_read_b128 v[154:157], v141 offset:25600
	s_add_i32 m0, s47, 0x6000
	s_nop 0
	global_load_lds_dwordx4 v138, s[30:31]
	v_mfma_f32_16x16x32_bf16 v[2:5], v[238:241], v[234:237], v[2:5]
	v_mfma_f32_16x16x32_bf16 v[6:9], v[242:245], v[234:237], v[6:9]
	v_mfma_f32_16x16x32_bf16 v[10:13], v[246:249], v[234:237], v[10:13]
	v_mfma_f32_16x16x32_bf16 v[14:17], v[250:253], v[234:237], v[14:17]
	ds_read_b128 v[234:237], v93 offset:8192
	s_add_i32 m0, s47, 0x8000
	s_nop 0
	global_load_lds_dwordx4 v140, s[30:31]
	s_waitcnt lgkmcnt(0)
	s_load_dwordx8 s[20:27], s[28:29], 0x0
	s_add_u32 s28, s28, 0x100
	s_addc_u32 s29, s29, 0
	v_mfma_f32_16x16x32_bf16 v[78:81], v[142:145], v[218:221], v[78:81]
	v_mfma_f32_16x16x32_bf16 v[74:77], v[146:149], v[218:221], v[74:77]
	v_mfma_f32_16x16x32_bf16 v[70:73], v[150:153], v[218:221], v[70:73]
	v_mfma_f32_16x16x32_bf16 v[66:69], v[154:157], v[218:221], v[66:69]
	v_lshl_add_u64 v[132:133], v[132:133], 0, s[40:41]
	global_load_dwordx2 v[98:99], v[132:133], off
	global_load_dwordx2 v[100:101], v[132:133], off offset:2048
	v_mfma_f32_16x16x32_bf16 v[62:65], v[142:145], v[222:225], v[62:65]
	v_mfma_f32_16x16x32_bf16 v[58:61], v[146:149], v[222:225], v[58:61]
	v_mfma_f32_16x16x32_bf16 v[54:57], v[150:153], v[222:225], v[54:57]
	v_mfma_f32_16x16x32_bf16 v[50:53], v[154:157], v[222:225], v[50:53]
	v_lshl_add_u64 v[166:167], v[132:133], 0, s[34:35]
	global_load_dwordx2 v[102:103], v[166:167], off
	global_load_dwordx2 v[104:105], v[166:167], off offset:2048
	v_mfma_f32_16x16x32_bf16 v[46:49], v[142:145], v[226:229], v[46:49]
	v_mfma_f32_16x16x32_bf16 v[42:45], v[146:149], v[226:229], v[42:45]
	v_mfma_f32_16x16x32_bf16 v[38:41], v[150:153], v[226:229], v[38:41]
	v_mfma_f32_16x16x32_bf16 v[34:37], v[154:157], v[226:229], v[34:37]
	v_lshl_add_u64 v[166:167], v[132:133], 0, s[36:37]
	global_load_dwordx2 v[106:107], v[166:167], off
	global_load_dwordx2 v[108:109], v[166:167], off offset:2048
	v_mfma_f32_16x16x32_bf16 v[18:21], v[142:145], v[230:233], v[18:21]
	v_mfma_f32_16x16x32_bf16 v[22:25], v[146:149], v[230:233], v[22:25]
	v_mfma_f32_16x16x32_bf16 v[26:29], v[150:153], v[230:233], v[26:29]
	v_mfma_f32_16x16x32_bf16 v[30:33], v[154:157], v[230:233], v[30:33]
	v_lshl_add_u64 v[166:167], v[132:133], 0, s[38:39]
	global_load_dwordx2 v[110:111], v[166:167], off
	global_load_dwordx2 v[112:113], v[166:167], off offset:2048
	v_mfma_f32_16x16x32_bf16 v[2:5], v[142:145], v[234:237], v[2:5]
	v_mfma_f32_16x16x32_bf16 v[6:9], v[146:149], v[234:237], v[6:9]
	v_mfma_f32_16x16x32_bf16 v[10:13], v[150:153], v[234:237], v[10:13]
	v_mfma_f32_16x16x32_bf16 v[14:17], v[154:157], v[234:237], v[14:17]
	s_waitcnt vmcnt(21)
	s_mov_b32 s47, s42
	s_mov_b32 s42, s43
	s_mov_b32 s43, s44
	s_mov_b32 s44, s47
	s_waitcnt lgkmcnt(0)
	s_barrier
	s_mov_b32 s46, 13
; #define MU_GLDS_A(buf, kt) do { _Pragma("unroll") for (int i = 0; i < NMU; ++i) \
;         __builtin_amdgcn_global_load_lds((const unsigned*)((const char*)A + aoff[i] + (size_t)(kt) * 128), (PG8_LAS unsigned*)(MU_SA(buf) + wid * 1024 + i * 8192), 16, 0, 0); } while (0)
; #define MU_B_ISSUE(sb, kt) do { const char* kb_ = Bb + (size_t)(kt) * (64 * (size_t)RB); _Pragma("unroll") for (int j = 0; j < 8; ++j) { const char* p_ = kb_ + (size_t)j * RB; \
;         asm volatile("global_load_dwordx2 %0, %1, off" : "=&v"(sb[j]) : "v"(p_) : "memory"); } } while (0)
; #define MU_B_WAIT(sb, N) asm volatile("s_waitcnt vmcnt(%8)" : "+v"(sb[0]), "+v"(sb[1]), "+v"(sb[2]), "+v"(sb[3]), "+v"(sb[4]), "+v"(sb[5]), "+v"(sb[6]), "+v"(sb[7]) : "n"(N) : "memory")
; #define MU_G_LOAD(ga, kt) do { const PG8_LAS f32x4* gk_ = (const PG8_LAS f32x4*)(lds + GAIN_OFF) + 16 * (kt) + 2 * wid; const f32x4 ga_ = gk_[0], gb_ = gk_[1]; \
;         ga[0] = ga_[0]; ga[1] = ga_[1]; ga[2] = ga_[2]; ga[3] = ga_[3]; ga[4] = gb_[0]; ga[5] = gb_[1]; ga[6] = gb_[2]; ga[7] = gb_[3]; } while (0)
; #define MU_COMPUTE(buf) MU_COMPUTE_N(buf, NMU)
; #define MU_END(last) do { if (last) asm volatile("s_waitcnt vmcnt(0)" ::: "memory"); else asm volatile("s_waitcnt vmcnt(8)" ::: "memory"); \
;         asm volatile("s_waitcnt lgkmcnt(0)" ::: "memory"); __builtin_amdgcn_s_barrier(); asm volatile("" ::: "memory"); } while (0)
; template <int MODE>
; __device__ __forceinline__ void moe_unit(PG8_LAS unsigned char* lds, int e, int cb, int slot0  , int nv  , const bf16_t* A, const int* slot_tok,
;                                          const float* W0, const float* W1, bf16_t* OUT, const float* slot_rs  , const int* slot_dst) {
;     ...
;     for (int t = 0; t < nt; t += 2) {
;         if (t + 2 < nt) MU_B_WAIT(s1, 8); else MU_B_WAIT(s1, 0);
;         MU_G_LOAD(g0, t + 1); MU_B_WRITE(s1, 1, g0); __builtin_amdgcn_sched_barrier(0); MU_GLDS_A(1, t + 1); __builtin_amdgcn_sched_barrier(0);
;         if (t + 3 < nt) { MU_B_ISSUE(s1, t + 3); }
;         MU_COMPUTE(0);
;         MU_END(t + 3 >= nt);
;         if (t + 2 < nt) { MU_B_WAIT(s0, 8); MU_G_LOAD(g0, t + 2); MU_B_WRITE(s0, 0, g0); __builtin_amdgcn_sched_barrier(0); MU_GLDS_A(0, t + 2); __builtin_amdgcn_sched_barrier(0); }
;         if (t + 4 < nt) { MU_B_ISSUE(s0, t + 4); }
;         MU_COMPUTE(1);
;         MU_END(t + 4 >= nt);
.Lmu_loop_X5:
	v_mul_f32_e32 v114, s20, v114
	v_mul_f32_e32 v115, s20, v115
	v_mul_f32_e32 v116, s21, v116
	v_mul_f32_e32 v117, s21, v117
	v_mul_f32_e32 v118, s22, v118
	v_mul_f32_e32 v119, s22, v119
	v_mul_f32_e32 v120, s23, v120
	v_mul_f32_e32 v121, s23, v121
	v_mul_f32_e32 v122, s24, v122
	v_mul_f32_e32 v123, s24, v123
	v_mul_f32_e32 v124, s25, v124
	v_mul_f32_e32 v125, s25, v125
	v_mul_f32_e32 v126, s26, v126
	v_mul_f32_e32 v127, s26, v127
	v_mul_f32_e32 v128, s27, v128
	v_mul_f32_e32 v129, s27, v129
	v_cvt_pk_bf16_f32 v158, v114, v116
	v_cvt_pk_bf16_f32 v159, v118, v120
	v_cvt_pk_bf16_f32 v160, v122, v124
	v_cvt_pk_bf16_f32 v161, v126, v128
	v_cvt_pk_bf16_f32 v162, v115, v117
	v_cvt_pk_bf16_f32 v163, v119, v121
	v_cvt_pk_bf16_f32 v164, v123, v125
	v_cvt_pk_bf16_f32 v165, v127, v129
	ds_write_b128 v1, v[158:161] offset:19456
	ds_write_b128 v1, v[162:165] offset:19584
	v_add_u32_e32 v91, s42, v135
	v_add_u32_e32 v93, s42, v137
	ds_read_b128 v[238:241], v139 offset:0
	ds_read_b128 v[242:245], v139 offset:2048
	ds_read_b128 v[246:249], v139 offset:4096
	ds_read_b128 v[250:253], v139 offset:6144
	ds_read_b128 v[218:221], v91 offset:0
	ds_read_b128 v[222:225], v91 offset:2048
	ds_read_b128 v[226:229], v91 offset:4096
	ds_read_b128 v[230:233], v91 offset:6144
	ds_read_b128 v[234:237], v91 offset:8192
	s_add_i32 s47, s44, s6
	s_add_u32 s30, s30, 0x80
	s_addc_u32 s31, s31, 0
	s_waitcnt lgkmcnt(0)
	v_mfma_f32_16x16x32_bf16 v[78:81], v[238:241], v[218:221], v[78:81]
	v_mfma_f32_16x16x32_bf16 v[74:77], v[242:245], v[218:221], v[74:77]
	v_mfma_f32_16x16x32_bf16 v[70:73], v[246:249], v[218:221], v[70:73]
	v_mfma_f32_16x16x32_bf16 v[66:69], v[250:253], v[218:221], v[66:69]
	ds_read_b128 v[218:221], v93 offset:0
	ds_read_b128 v[142:145], v141 offset:0
	s_mov_b32 m0, s47
	s_nop 0
	global_load_lds_dwordx4 v86, s[30:31]
	v_mfma_f32_16x16x32_bf16 v[62:65], v[238:241], v[222:225], v[62:65]
	v_mfma_f32_16x16x32_bf16 v[58:61], v[242:245], v[222:225], v[58:61]
	v_mfma_f32_16x16x32_bf16 v[54:57], v[246:249], v[222:225], v[54:57]
	v_mfma_f32_16x16x32_bf16 v[50:53], v[250:253], v[222:225], v[50:53]
	ds_read_b128 v[222:225], v93 offset:2048
	ds_read_b128 v[146:149], v141 offset:2048
	s_add_i32 m0, s47, 0x2000
	s_nop 0
	global_load_lds_dwordx4 v134, s[30:31]
	v_mfma_f32_16x16x32_bf16 v[46:49], v[238:241], v[226:229], v[46:49]
	v_mfma_f32_16x16x32_bf16 v[42:45], v[242:245], v[226:229], v[42:45]
	v_mfma_f32_16x16x32_bf16 v[38:41], v[246:249], v[226:229], v[38:41]
	v_mfma_f32_16x16x32_bf16 v[34:37], v[250:253], v[226:229], v[34:37]
	ds_read_b128 v[226:229], v93 offset:4096
	ds_read_b128 v[150:153], v141 offset:4096
	s_add_i32 m0, s47, 0x4000
	s_nop 0
	global_load_lds_dwordx4 v136, s[30:31]
	v_mfma_f32_16x16x32_bf16 v[18:21], v[238:241], v[230:233], v[18:21]
	v_mfma_f32_16x16x32_bf16 v[22:25], v[242:245], v[230:233], v[22:25]
	v_mfma_f32_16x16x32_bf16 v[26:29], v[246:249], v[230:233], v[26:29]
	v_mfma_f32_16x16x32_bf16 v[30:33], v[250:253], v[230:233], v[30:33]
	ds_read_b128 v[230:233], v93 offset:6144
	ds_read_b128 v[154:157], v141 offset:6144
	s_add_i32 m0, s47, 0x6000
	s_nop 0
	global_load_lds_dwordx4 v138, s[30:31]
	v_mfma_f32_16x16x32_bf16 v[2:5], v[238:241], v[234:237], v[2:5]
	v_mfma_f32_16x16x32_bf16 v[6:9], v[242:245], v[234:237], v[6:9]
	v_mfma_f32_16x16x32_bf16 v[10:13], v[246:249], v[234:237], v[10:13]
	v_mfma_f32_16x16x32_bf16 v[14:17], v[250:253], v[234:237], v[14:17]
	ds_read_b128 v[234:237], v93 offset:8192
	s_add_i32 m0, s47, 0x8000
	s_nop 0
	global_load_lds_dwordx4 v140, s[30:31]
	s_waitcnt lgkmcnt(0)
	s_load_dwordx8 s[12:19], s[28:29], 0x0
	s_add_u32 s28, s28, 0x100
	s_addc_u32 s29, s29, 0
	v_mfma_f32_16x16x32_bf16 v[78:81], v[142:145], v[218:221], v[78:81]
	v_mfma_f32_16x16x32_bf16 v[74:77], v[146:149], v[218:221], v[74:77]
	v_mfma_f32_16x16x32_bf16 v[70:73], v[150:153], v[218:221], v[70:73]
	v_mfma_f32_16x16x32_bf16 v[66:69], v[154:157], v[218:221], v[66:69]
	v_lshl_add_u64 v[132:133], v[132:133], 0, s[40:41]
	global_load_dwordx2 v[114:115], v[132:133], off
	global_load_dwordx2 v[116:117], v[132:133], off offset:2048
	v_mfma_f32_16x16x32_bf16 v[62:65], v[142:145], v[222:225], v[62:65]
	v_mfma_f32_16x16x32_bf16 v[58:61], v[146:149], v[222:225], v[58:61]
	v_mfma_f32_16x16x32_bf16 v[54:57], v[150:153], v[222:225], v[54:57]
	v_mfma_f32_16x16x32_bf16 v[50:53], v[154:157], v[222:225], v[50:53]
	v_lshl_add_u64 v[166:167], v[132:133], 0, s[34:35]
	global_load_dwordx2 v[118:119], v[166:167], off
	global_load_dwordx2 v[120:121], v[166:167], off offset:2048
	v_mfma_f32_16x16x32_bf16 v[46:49], v[142:145], v[226:229], v[46:49]
	v_mfma_f32_16x16x32_bf16 v[42:45], v[146:149], v[226:229], v[42:45]
	v_mfma_f32_16x16x32_bf16 v[38:41], v[150:153], v[226:229], v[38:41]
	v_mfma_f32_16x16x32_bf16 v[34:37], v[154:157], v[226:229], v[34:37]
	v_lshl_add_u64 v[166:167], v[132:133], 0, s[36:37]
	global_load_dwordx2 v[122:123], v[166:167], off
	global_load_dwordx2 v[124:125], v[166:167], off offset:2048
	v_mfma_f32_16x16x32_bf16 v[18:21], v[142:145], v[230:233], v[18:21]
	v_mfma_f32_16x16x32_bf16 v[22:25], v[146:149], v[230:233], v[22:25]
	v_mfma_f32_16x16x32_bf16 v[26:29], v[150:153], v[230:233], v[26:29]
	v_mfma_f32_16x16x32_bf16 v[30:33], v[154:157], v[230:233], v[30:33]
	v_lshl_add_u64 v[166:167], v[132:133], 0, s[38:39]
	global_load_dwordx2 v[126:127], v[166:167], off
	global_load_dwordx2 v[128:129], v[166:167], off offset:2048
	v_mfma_f32_16x16x32_bf16 v[2:5], v[142:145], v[234:237], v[2:5]
	v_mfma_f32_16x16x32_bf16 v[6:9], v[146:149], v[234:237], v[6:9]
	v_mfma_f32_16x16x32_bf16 v[10:13], v[150:153], v[234:237], v[10:13]
	v_mfma_f32_16x16x32_bf16 v[14:17], v[154:157], v[234:237], v[14:17]
	s_waitcnt vmcnt(21)
	s_mov_b32 s47, s42
	s_mov_b32 s42, s43
	s_mov_b32 s43, s44
	s_mov_b32 s44, s47
	s_waitcnt lgkmcnt(0)
	s_barrier
; #define MU_GLDS_A(buf, kt) do { _Pragma("unroll") for (int i = 0; i < NMU; ++i) \
;         __builtin_amdgcn_global_load_lds((const unsigned*)((const char*)A + aoff[i] + (size_t)(kt) * 128), (PG8_LAS unsigned*)(MU_SA(buf) + wid * 1024 + i * 8192), 16, 0, 0); } while (0)
; #define MU_B_ISSUE(sb, kt) do { const char* kb_ = Bb + (size_t)(kt) * (64 * (size_t)RB); _Pragma("unroll") for (int j = 0; j < 8; ++j) { const char* p_ = kb_ + (size_t)j * RB; \
;         asm volatile("global_load_dwordx2 %0, %1, off" : "=&v"(sb[j]) : "v"(p_) : "memory"); } } while (0)
; #define MU_B_WAIT(sb, N) asm volatile("s_waitcnt vmcnt(%8)" : "+v"(sb[0]), "+v"(sb[1]), "+v"(sb[2]), "+v"(sb[3]), "+v"(sb[4]), "+v"(sb[5]), "+v"(sb[6]), "+v"(sb[7]) : "n"(N) : "memory")
; #define MU_G_LOAD(ga, kt) do { const PG8_LAS f32x4* gk_ = (const PG8_LAS f32x4*)(lds + GAIN_OFF) + 16 * (kt) + 2 * wid; const f32x4 ga_ = gk_[0], gb_ = gk_[1]; \
;         ga[0] = ga_[0]; ga[1] = ga_[1]; ga[2] = ga_[2]; ga[3] = ga_[3]; ga[4] = gb_[0]; ga[5] = gb_[1]; ga[6] = gb_[2]; ga[7] = gb_[3]; } while (0)
; #define MU_COMPUTE(buf) MU_COMPUTE_N(buf, NMU)
; #define MU_END(last) do { if (last) asm volatile("s_waitcnt vmcnt(0)" ::: "memory"); else asm volatile("s_waitcnt vmcnt(8)" ::: "memory"); \
;         asm volatile("s_waitcnt lgkmcnt(0)" ::: "memory"); __builtin_amdgcn_s_barrier(); asm volatile("" ::: "memory"); } while (0)
; template <int MODE>
; __device__ __forceinline__ void moe_unit(PG8_LAS unsigned char* lds, int e, int cb, int slot0  , int nv  , const bf16_t* A, const int* slot_tok,
;                                          const float* W0, const float* W1, bf16_t* OUT, const float* slot_rs  , const int* slot_dst) {
;     ...
;     for (int t = 0; t < nt; t += 2) {
;         if (t + 2 < nt) MU_B_WAIT(s1, 8); else MU_B_WAIT(s1, 0);
;         MU_G_LOAD(g0, t + 1); MU_B_WRITE(s1, 1, g0); __builtin_amdgcn_sched_barrier(0); MU_GLDS_A(1, t + 1); __builtin_amdgcn_sched_barrier(0);
;         if (t + 3 < nt) { MU_B_ISSUE(s1, t + 3); }
;         MU_COMPUTE(0);
;         MU_END(t + 3 >= nt);
;         if (t + 2 < nt) { MU_B_WAIT(s0, 8); MU_G_LOAD(g0, t + 2); MU_B_WRITE(s0, 0, g0); __builtin_amdgcn_sched_barrier(0); MU_GLDS_A(0, t + 2); __builtin_amdgcn_sched_barrier(0); }
;         if (t + 4 < nt) { MU_B_ISSUE(s0, t + 4); }
;         MU_COMPUTE(1);
;         MU_END(t + 4 >= nt);
	v_mul_f32_e32 v186, s12, v186
	v_mul_f32_e32 v187, s12, v187
	v_mul_f32_e32 v188, s13, v188
	v_mul_f32_e32 v189, s13, v189
	v_mul_f32_e32 v190, s14, v190
	v_mul_f32_e32 v191, s14, v191
	v_mul_f32_e32 v192, s15, v192
	v_mul_f32_e32 v193, s15, v193
	v_mul_f32_e32 v194, s16, v194
	v_mul_f32_e32 v195, s16, v195
	v_mul_f32_e32 v196, s17, v196
	v_mul_f32_e32 v197, s17, v197
	v_mul_f32_e32 v198, s18, v198
	v_mul_f32_e32 v199, s18, v199
	v_mul_f32_e32 v200, s19, v200
	v_mul_f32_e32 v201, s19, v201
	v_cvt_pk_bf16_f32 v158, v186, v188
	v_cvt_pk_bf16_f32 v159, v190, v192
	v_cvt_pk_bf16_f32 v160, v194, v196
	v_cvt_pk_bf16_f32 v161, v198, v200
	v_cvt_pk_bf16_f32 v162, v187, v189
	v_cvt_pk_bf16_f32 v163, v191, v193
	v_cvt_pk_bf16_f32 v164, v195, v197
	v_cvt_pk_bf16_f32 v165, v199, v201
	ds_write_b128 v1, v[158:161] offset:0
	ds_write_b128 v1, v[162:165] offset:128
	v_add_u32_e32 v91, s42, v135
	v_add_u32_e32 v93, s42, v137
	ds_read_b128 v[238:241], v139 offset:19456
	ds_read_b128 v[242:245], v139 offset:21504
	ds_read_b128 v[246:249], v139 offset:23552
	ds_read_b128 v[250:253], v139 offset:25600
	ds_read_b128 v[218:221], v91 offset:0
	ds_read_b128 v[222:225], v91 offset:2048
	ds_read_b128 v[226:229], v91 offset:4096
	ds_read_b128 v[230:233], v91 offset:6144
	ds_read_b128 v[234:237], v91 offset:8192
	s_add_i32 s47, s44, s6
	s_add_u32 s30, s30, 0x80
	s_addc_u32 s31, s31, 0
	s_waitcnt lgkmcnt(0)
	v_mfma_f32_16x16x32_bf16 v[78:81], v[238:241], v[218:221], v[78:81]
	v_mfma_f32_16x16x32_bf16 v[74:77], v[242:245], v[218:221], v[74:77]
	v_mfma_f32_16x16x32_bf16 v[70:73], v[246:249], v[218:221], v[70:73]
	v_mfma_f32_16x16x32_bf16 v[66:69], v[250:253], v[218:221], v[66:69]
	ds_read_b128 v[218:221], v93 offset:0
	ds_read_b128 v[142:145], v141 offset:19456
	s_mov_b32 m0, s47
	s_nop 0
	global_load_lds_dwordx4 v86, s[30:31]
	v_mfma_f32_16x16x32_bf16 v[62:65], v[238:241], v[222:225], v[62:65]
	v_mfma_f32_16x16x32_bf16 v[58:61], v[242:245], v[222:225], v[58:61]
	v_mfma_f32_16x16x32_bf16 v[54:57], v[246:249], v[222:225], v[54:57]
	v_mfma_f32_16x16x32_bf16 v[50:53], v[250:253], v[222:225], v[50:53]
	ds_read_b128 v[222:225], v93 offset:2048
	ds_read_b128 v[146:149], v141 offset:21504
	s_add_i32 m0, s47, 0x2000
	s_nop 0
	global_load_lds_dwordx4 v134, s[30:31]
	v_mfma_f32_16x16x32_bf16 v[46:49], v[238:241], v[226:229], v[46:49]
	v_mfma_f32_16x16x32_bf16 v[42:45], v[242:245], v[226:229], v[42:45]
	v_mfma_f32_16x16x32_bf16 v[38:41], v[246:249], v[226:229], v[38:41]
	v_mfma_f32_16x16x32_bf16 v[34:37], v[250:253], v[226:229], v[34:37]
	ds_read_b128 v[226:229], v93 offset:4096
	ds_read_b128 v[150:153], v141 offset:23552
	s_add_i32 m0, s47, 0x4000
	s_nop 0
	global_load_lds_dwordx4 v136, s[30:31]
	v_mfma_f32_16x16x32_bf16 v[18:21], v[238:241], v[230:233], v[18:21]
	v_mfma_f32_16x16x32_bf16 v[22:25], v[242:245], v[230:233], v[22:25]
	v_mfma_f32_16x16x32_bf16 v[26:29], v[246:249], v[230:233], v[26:29]
	v_mfma_f32_16x16x32_bf16 v[30:33], v[250:253], v[230:233], v[30:33]
	ds_read_b128 v[230:233], v93 offset:6144
	ds_read_b128 v[154:157], v141 offset:25600
	s_add_i32 m0, s47, 0x6000
	s_nop 0
	global_load_lds_dwordx4 v138, s[30:31]
	v_mfma_f32_16x16x32_bf16 v[2:5], v[238:241], v[234:237], v[2:5]
	v_mfma_f32_16x16x32_bf16 v[6:9], v[242:245], v[234:237], v[6:9]
	v_mfma_f32_16x16x32_bf16 v[10:13], v[246:249], v[234:237], v[10:13]
	v_mfma_f32_16x16x32_bf16 v[14:17], v[250:253], v[234:237], v[14:17]
	ds_read_b128 v[234:237], v93 offset:8192
	s_add_i32 m0, s47, 0x8000
	s_nop 0
	global_load_lds_dwordx4 v140, s[30:31]
	s_waitcnt lgkmcnt(0)
	s_load_dwordx8 s[20:27], s[28:29], 0x0
	s_add_u32 s28, s28, 0x100
	s_addc_u32 s29, s29, 0
	v_mfma_f32_16x16x32_bf16 v[78:81], v[142:145], v[218:221], v[78:81]
	v_mfma_f32_16x16x32_bf16 v[74:77], v[146:149], v[218:221], v[74:77]
	v_mfma_f32_16x16x32_bf16 v[70:73], v[150:153], v[218:221], v[70:73]
	v_mfma_f32_16x16x32_bf16 v[66:69], v[154:157], v[218:221], v[66:69]
	v_lshl_add_u64 v[132:133], v[132:133], 0, s[40:41]
	global_load_dwordx2 v[186:187], v[132:133], off
	global_load_dwordx2 v[188:189], v[132:133], off offset:2048
	v_mfma_f32_16x16x32_bf16 v[62:65], v[142:145], v[222:225], v[62:65]
	v_mfma_f32_16x16x32_bf16 v[58:61], v[146:149], v[222:225], v[58:61]
	v_mfma_f32_16x16x32_bf16 v[54:57], v[150:153], v[222:225], v[54:57]
	v_mfma_f32_16x16x32_bf16 v[50:53], v[154:157], v[222:225], v[50:53]
	v_lshl_add_u64 v[166:167], v[132:133], 0, s[34:35]
	global_load_dwordx2 v[190:191], v[166:167], off
	global_load_dwordx2 v[192:193], v[166:167], off offset:2048
	v_mfma_f32_16x16x32_bf16 v[46:49], v[142:145], v[226:229], v[46:49]
	v_mfma_f32_16x16x32_bf16 v[42:45], v[146:149], v[226:229], v[42:45]
	v_mfma_f32_16x16x32_bf16 v[38:41], v[150:153], v[226:229], v[38:41]
	v_mfma_f32_16x16x32_bf16 v[34:37], v[154:157], v[226:229], v[34:37]
	v_lshl_add_u64 v[166:167], v[132:133], 0, s[36:37]
	global_load_dwordx2 v[194:195], v[166:167], off
	global_load_dwordx2 v[196:197], v[166:167], off offset:2048
	v_mfma_f32_16x16x32_bf16 v[18:21], v[142:145], v[230:233], v[18:21]
	v_mfma_f32_16x16x32_bf16 v[22:25], v[146:149], v[230:233], v[22:25]
	v_mfma_f32_16x16x32_bf16 v[26:29], v[150:153], v[230:233], v[26:29]
	v_mfma_f32_16x16x32_bf16 v[30:33], v[154:157], v[230:233], v[30:33]
	v_lshl_add_u64 v[166:167], v[132:133], 0, s[38:39]
	global_load_dwordx2 v[198:199], v[166:167], off
	global_load_dwordx2 v[200:201], v[166:167], off offset:2048
	v_mfma_f32_16x16x32_bf16 v[2:5], v[142:145], v[234:237], v[2:5]
	v_mfma_f32_16x16x32_bf16 v[6:9], v[146:149], v[234:237], v[6:9]
	v_mfma_f32_16x16x32_bf16 v[10:13], v[150:153], v[234:237], v[10:13]
	v_mfma_f32_16x16x32_bf16 v[14:17], v[154:157], v[234:237], v[14:17]
	s_waitcnt vmcnt(21)
	s_mov_b32 s47, s42
	s_mov_b32 s42, s43
	s_mov_b32 s43, s44
	s_mov_b32 s44, s47
	s_waitcnt lgkmcnt(0)
	s_barrier
; #define MU_GLDS_A(buf, kt) do { _Pragma("unroll") for (int i = 0; i < NMU; ++i) \
;         __builtin_amdgcn_global_load_lds((const unsigned*)((const char*)A + aoff[i] + (size_t)(kt) * 128), (PG8_LAS unsigned*)(MU_SA(buf) + wid * 1024 + i * 8192), 16, 0, 0); } while (0)
; #define MU_B_ISSUE(sb, kt) do { const char* kb_ = Bb + (size_t)(kt) * (64 * (size_t)RB); _Pragma("unroll") for (int j = 0; j < 8; ++j) { const char* p_ = kb_ + (size_t)j * RB; \
;         asm volatile("global_load_dwordx2 %0, %1, off" : "=&v"(sb[j]) : "v"(p_) : "memory"); } } while (0)
; #define MU_B_WAIT(sb, N) asm volatile("s_waitcnt vmcnt(%8)" : "+v"(sb[0]), "+v"(sb[1]), "+v"(sb[2]), "+v"(sb[3]), "+v"(sb[4]), "+v"(sb[5]), "+v"(sb[6]), "+v"(sb[7]) : "n"(N) : "memory")
; #define MU_G_LOAD(ga, kt) do { const PG8_LAS f32x4* gk_ = (const PG8_LAS f32x4*)(lds + GAIN_OFF) + 16 * (kt) + 2 * wid; const f32x4 ga_ = gk_[0], gb_ = gk_[1]; \
;         ga[0] = ga_[0]; ga[1] = ga_[1]; ga[2] = ga_[2]; ga[3] = ga_[3]; ga[4] = gb_[0]; ga[5] = gb_[1]; ga[6] = gb_[2]; ga[7] = gb_[3]; } while (0)
; #define MU_COMPUTE(buf) MU_COMPUTE_N(buf, NMU)
; #define MU_END(last) do { if (last) asm volatile("s_waitcnt vmcnt(0)" ::: "memory"); else asm volatile("s_waitcnt vmcnt(8)" ::: "memory"); \
;         asm volatile("s_waitcnt lgkmcnt(0)" ::: "memory"); __builtin_amdgcn_s_barrier(); asm volatile("" ::: "memory"); } while (0)
; template <int MODE>
; __device__ __forceinline__ void moe_unit(PG8_LAS unsigned char* lds, int e, int cb, int slot0  , int nv  , const bf16_t* A, const int* slot_tok,
;                                          const float* W0, const float* W1, bf16_t* OUT, const float* slot_rs  , const int* slot_dst) {
;     ...
;     for (int t = 0; t < nt; t += 2) {
;         if (t + 2 < nt) MU_B_WAIT(s1, 8); else MU_B_WAIT(s1, 0);
;         MU_G_LOAD(g0, t + 1); MU_B_WRITE(s1, 1, g0); __builtin_amdgcn_sched_barrier(0); MU_GLDS_A(1, t + 1); __builtin_amdgcn_sched_barrier(0);
;         if (t + 3 < nt) { MU_B_ISSUE(s1, t + 3); }
;         MU_COMPUTE(0);
;         MU_END(t + 3 >= nt);
;         if (t + 2 < nt) { MU_B_WAIT(s0, 8); MU_G_LOAD(g0, t + 2); MU_B_WRITE(s0, 0, g0); __builtin_amdgcn_sched_barrier(0); MU_GLDS_A(0, t + 2); __builtin_amdgcn_sched_barrier(0); }
;         if (t + 4 < nt) { MU_B_ISSUE(s0, t + 4); }
;         MU_COMPUTE(1);
;         MU_END(t + 4 >= nt);
	v_mul_f32_e32 v202, s20, v202
	v_mul_f32_e32 v203, s20, v203
	v_mul_f32_e32 v204, s21, v204
	v_mul_f32_e32 v205, s21, v205
	v_mul_f32_e32 v206, s22, v206
	v_mul_f32_e32 v207, s22, v207
	v_mul_f32_e32 v208, s23, v208
	v_mul_f32_e32 v209, s23, v209
	v_mul_f32_e32 v210, s24, v210
	v_mul_f32_e32 v211, s24, v211
	v_mul_f32_e32 v212, s25, v212
	v_mul_f32_e32 v213, s25, v213
	v_mul_f32_e32 v214, s26, v214
	v_mul_f32_e32 v215, s26, v215
	v_mul_f32_e32 v216, s27, v216
	v_mul_f32_e32 v217, s27, v217
	v_cvt_pk_bf16_f32 v158, v202, v204
	v_cvt_pk_bf16_f32 v159, v206, v208
	v_cvt_pk_bf16_f32 v160, v210, v212
	v_cvt_pk_bf16_f32 v161, v214, v216
	v_cvt_pk_bf16_f32 v162, v203, v205
	v_cvt_pk_bf16_f32 v163, v207, v209
	v_cvt_pk_bf16_f32 v164, v211, v213
	v_cvt_pk_bf16_f32 v165, v215, v217
	ds_write_b128 v1, v[158:161] offset:19456
	ds_write_b128 v1, v[162:165] offset:19584
	v_add_u32_e32 v91, s42, v135
	v_add_u32_e32 v93, s42, v137
	ds_read_b128 v[238:241], v139 offset:0
	ds_read_b128 v[242:245], v139 offset:2048
	ds_read_b128 v[246:249], v139 offset:4096
	ds_read_b128 v[250:253], v139 offset:6144
	ds_read_b128 v[218:221], v91 offset:0
	ds_read_b128 v[222:225], v91 offset:2048
	ds_read_b128 v[226:229], v91 offset:4096
	ds_read_b128 v[230:233], v91 offset:6144
	ds_read_b128 v[234:237], v91 offset:8192
	s_add_i32 s47, s44, s6
	s_add_u32 s30, s30, 0x80
	s_addc_u32 s31, s31, 0
	s_waitcnt lgkmcnt(0)
	v_mfma_f32_16x16x32_bf16 v[78:81], v[238:241], v[218:221], v[78:81]
	v_mfma_f32_16x16x32_bf16 v[74:77], v[242:245], v[218:221], v[74:77]
	v_mfma_f32_16x16x32_bf16 v[70:73], v[246:249], v[218:221], v[70:73]
	v_mfma_f32_16x16x32_bf16 v[66:69], v[250:253], v[218:221], v[66:69]
	ds_read_b128 v[218:221], v93 offset:0
	ds_read_b128 v[142:145], v141 offset:0
	s_mov_b32 m0, s47
	s_nop 0
	global_load_lds_dwordx4 v86, s[30:31]
	v_mfma_f32_16x16x32_bf16 v[62:65], v[238:241], v[222:225], v[62:65]
	v_mfma_f32_16x16x32_bf16 v[58:61], v[242:245], v[222:225], v[58:61]
	v_mfma_f32_16x16x32_bf16 v[54:57], v[246:249], v[222:225], v[54:57]
	v_mfma_f32_16x16x32_bf16 v[50:53], v[250:253], v[222:225], v[50:53]
	ds_read_b128 v[222:225], v93 offset:2048
	ds_read_b128 v[146:149], v141 offset:2048
	s_add_i32 m0, s47, 0x2000
	s_nop 0
	global_load_lds_dwordx4 v134, s[30:31]
	v_mfma_f32_16x16x32_bf16 v[46:49], v[238:241], v[226:229], v[46:49]
	v_mfma_f32_16x16x32_bf16 v[42:45], v[242:245], v[226:229], v[42:45]
	v_mfma_f32_16x16x32_bf16 v[38:41], v[246:249], v[226:229], v[38:41]
	v_mfma_f32_16x16x32_bf16 v[34:37], v[250:253], v[226:229], v[34:37]
	ds_read_b128 v[226:229], v93 offset:4096
	ds_read_b128 v[150:153], v141 offset:4096
	s_add_i32 m0, s47, 0x4000
	s_nop 0
	global_load_lds_dwordx4 v136, s[30:31]
	v_mfma_f32_16x16x32_bf16 v[18:21], v[238:241], v[230:233], v[18:21]
	v_mfma_f32_16x16x32_bf16 v[22:25], v[242:245], v[230:233], v[22:25]
	v_mfma_f32_16x16x32_bf16 v[26:29], v[246:249], v[230:233], v[26:29]
	v_mfma_f32_16x16x32_bf16 v[30:33], v[250:253], v[230:233], v[30:33]
	ds_read_b128 v[230:233], v93 offset:6144
	ds_read_b128 v[154:157], v141 offset:6144
	s_add_i32 m0, s47, 0x6000
	s_nop 0
	global_load_lds_dwordx4 v138, s[30:31]
	v_mfma_f32_16x16x32_bf16 v[2:5], v[238:241], v[234:237], v[2:5]
	v_mfma_f32_16x16x32_bf16 v[6:9], v[242:245], v[234:237], v[6:9]
	v_mfma_f32_16x16x32_bf16 v[10:13], v[246:249], v[234:237], v[10:13]
	v_mfma_f32_16x16x32_bf16 v[14:17], v[250:253], v[234:237], v[14:17]
	ds_read_b128 v[234:237], v93 offset:8192
	s_add_i32 m0, s47, 0x8000
	s_nop 0
	global_load_lds_dwordx4 v140, s[30:31]
	s_waitcnt lgkmcnt(0)
	s_load_dwordx8 s[12:19], s[28:29], 0x0
	s_add_u32 s28, s28, 0x100
	s_addc_u32 s29, s29, 0
	v_mfma_f32_16x16x32_bf16 v[78:81], v[142:145], v[218:221], v[78:81]
	v_mfma_f32_16x16x32_bf16 v[74:77], v[146:149], v[218:221], v[74:77]
	v_mfma_f32_16x16x32_bf16 v[70:73], v[150:153], v[218:221], v[70:73]
	v_mfma_f32_16x16x32_bf16 v[66:69], v[154:157], v[218:221], v[66:69]
	v_lshl_add_u64 v[132:133], v[132:133], 0, s[40:41]
	global_load_dwordx2 v[202:203], v[132:133], off
	global_load_dwordx2 v[204:205], v[132:133], off offset:2048
	v_mfma_f32_16x16x32_bf16 v[62:65], v[142:145], v[222:225], v[62:65]
	v_mfma_f32_16x16x32_bf16 v[58:61], v[146:149], v[222:225], v[58:61]
	v_mfma_f32_16x16x32_bf16 v[54:57], v[150:153], v[222:225], v[54:57]
	v_mfma_f32_16x16x32_bf16 v[50:53], v[154:157], v[222:225], v[50:53]
	v_lshl_add_u64 v[166:167], v[132:133], 0, s[34:35]
	global_load_dwordx2 v[206:207], v[166:167], off
	global_load_dwordx2 v[208:209], v[166:167], off offset:2048
	v_mfma_f32_16x16x32_bf16 v[46:49], v[142:145], v[226:229], v[46:49]
	v_mfma_f32_16x16x32_bf16 v[42:45], v[146:149], v[226:229], v[42:45]
	v_mfma_f32_16x16x32_bf16 v[38:41], v[150:153], v[226:229], v[38:41]
	v_mfma_f32_16x16x32_bf16 v[34:37], v[154:157], v[226:229], v[34:37]
	v_lshl_add_u64 v[166:167], v[132:133], 0, s[36:37]
	global_load_dwordx2 v[210:211], v[166:167], off
	global_load_dwordx2 v[212:213], v[166:167], off offset:2048
	v_mfma_f32_16x16x32_bf16 v[18:21], v[142:145], v[230:233], v[18:21]
	v_mfma_f32_16x16x32_bf16 v[22:25], v[146:149], v[230:233], v[22:25]
	v_mfma_f32_16x16x32_bf16 v[26:29], v[150:153], v[230:233], v[26:29]
	v_mfma_f32_16x16x32_bf16 v[30:33], v[154:157], v[230:233], v[30:33]
	v_lshl_add_u64 v[166:167], v[132:133], 0, s[38:39]
	global_load_dwordx2 v[214:215], v[166:167], off
	global_load_dwordx2 v[216:217], v[166:167], off offset:2048
	v_mfma_f32_16x16x32_bf16 v[2:5], v[142:145], v[234:237], v[2:5]
	v_mfma_f32_16x16x32_bf16 v[6:9], v[146:149], v[234:237], v[6:9]
	v_mfma_f32_16x16x32_bf16 v[10:13], v[150:153], v[234:237], v[10:13]
	v_mfma_f32_16x16x32_bf16 v[14:17], v[154:157], v[234:237], v[14:17]
	s_waitcnt vmcnt(21)
	s_mov_b32 s47, s42
	s_mov_b32 s42, s43
	s_mov_b32 s43, s44
	s_mov_b32 s44, s47
	s_waitcnt lgkmcnt(0)
	s_barrier
; #define MU_GLDS_A(buf, kt) do { _Pragma("unroll") for (int i = 0; i < NMU; ++i) \
;         __builtin_amdgcn_global_load_lds((const unsigned*)((const char*)A + aoff[i] + (size_t)(kt) * 128), (PG8_LAS unsigned*)(MU_SA(buf) + wid * 1024 + i * 8192), 16, 0, 0); } while (0)
; #define MU_B_ISSUE(sb, kt) do { const char* kb_ = Bb + (size_t)(kt) * (64 * (size_t)RB); _Pragma("unroll") for (int j = 0; j < 8; ++j) { const char* p_ = kb_ + (size_t)j * RB; \
;         asm volatile("global_load_dwordx2 %0, %1, off" : "=&v"(sb[j]) : "v"(p_) : "memory"); } } while (0)
; #define MU_B_WAIT(sb, N) asm volatile("s_waitcnt vmcnt(%8)" : "+v"(sb[0]), "+v"(sb[1]), "+v"(sb[2]), "+v"(sb[3]), "+v"(sb[4]), "+v"(sb[5]), "+v"(sb[6]), "+v"(sb[7]) : "n"(N) : "memory")
; #define MU_G_LOAD(ga, kt) do { const PG8_LAS f32x4* gk_ = (const PG8_LAS f32x4*)(lds + GAIN_OFF) + 16 * (kt) + 2 * wid; const f32x4 ga_ = gk_[0], gb_ = gk_[1]; \
;         ga[0] = ga_[0]; ga[1] = ga_[1]; ga[2] = ga_[2]; ga[3] = ga_[3]; ga[4] = gb_[0]; ga[5] = gb_[1]; ga[6] = gb_[2]; ga[7] = gb_[3]; } while (0)
; #define MU_COMPUTE(buf) MU_COMPUTE_N(buf, NMU)
; #define MU_END(last) do { if (last) asm volatile("s_waitcnt vmcnt(0)" ::: "memory"); else asm volatile("s_waitcnt vmcnt(8)" ::: "memory"); \
;         asm volatile("s_waitcnt lgkmcnt(0)" ::: "memory"); __builtin_amdgcn_s_barrier(); asm volatile("" ::: "memory"); } while (0)
; template <int MODE>
; __device__ __forceinline__ void moe_unit(PG8_LAS unsigned char* lds, int e, int cb, int slot0  , int nv  , const bf16_t* A, const int* slot_tok,
;                                          const float* W0, const float* W1, bf16_t* OUT, const float* slot_rs  , const int* slot_dst) {
;     ...
;     for (int t = 0; t < nt; t += 2) {
;         if (t + 2 < nt) MU_B_WAIT(s1, 8); else MU_B_WAIT(s1, 0);
;         MU_G_LOAD(g0, t + 1); MU_B_WRITE(s1, 1, g0); __builtin_amdgcn_sched_barrier(0); MU_GLDS_A(1, t + 1); __builtin_amdgcn_sched_barrier(0);
;         if (t + 3 < nt) { MU_B_ISSUE(s1, t + 3); }
;         MU_COMPUTE(0);
;         MU_END(t + 3 >= nt);
;         if (t + 2 < nt) { MU_B_WAIT(s0, 8); MU_G_LOAD(g0, t + 2); MU_B_WRITE(s0, 0, g0); __builtin_amdgcn_sched_barrier(0); MU_GLDS_A(0, t + 2); __builtin_amdgcn_sched_barrier(0); }
;         if (t + 4 < nt) { MU_B_ISSUE(s0, t + 4); }
;         MU_COMPUTE(1);
;         MU_END(t + 4 >= nt);
	v_mul_f32_e32 v98, s12, v98
	v_mul_f32_e32 v99, s12, v99
	v_mul_f32_e32 v100, s13, v100
	v_mul_f32_e32 v101, s13, v101
	v_mul_f32_e32 v102, s14, v102
	v_mul_f32_e32 v103, s14, v103
	v_mul_f32_e32 v104, s15, v104
	v_mul_f32_e32 v105, s15, v105
	v_mul_f32_e32 v106, s16, v106
	v_mul_f32_e32 v107, s16, v107
	v_mul_f32_e32 v108, s17, v108
	v_mul_f32_e32 v109, s17, v109
	v_mul_f32_e32 v110, s18, v110
	v_mul_f32_e32 v111, s18, v111
	v_mul_f32_e32 v112, s19, v112
	v_mul_f32_e32 v113, s19, v113
	v_cvt_pk_bf16_f32 v158, v98, v100
	v_cvt_pk_bf16_f32 v159, v102, v104
	v_cvt_pk_bf16_f32 v160, v106, v108
	v_cvt_pk_bf16_f32 v161, v110, v112
	v_cvt_pk_bf16_f32 v162, v99, v101
	v_cvt_pk_bf16_f32 v163, v103, v105
	v_cvt_pk_bf16_f32 v164, v107, v109
	v_cvt_pk_bf16_f32 v165, v111, v113
	ds_write_b128 v1, v[158:161] offset:0
	ds_write_b128 v1, v[162:165] offset:128
	v_add_u32_e32 v91, s42, v135
	v_add_u32_e32 v93, s42, v137
	ds_read_b128 v[238:241], v139 offset:19456
	ds_read_b128 v[242:245], v139 offset:21504
	ds_read_b128 v[246:249], v139 offset:23552
	ds_read_b128 v[250:253], v139 offset:25600
	ds_read_b128 v[218:221], v91 offset:0
	ds_read_b128 v[222:225], v91 offset:2048
	ds_read_b128 v[226:229], v91 offset:4096
	ds_read_b128 v[230:233], v91 offset:6144
	ds_read_b128 v[234:237], v91 offset:8192
	s_add_i32 s47, s44, s6
	s_add_u32 s30, s30, 0x80
	s_addc_u32 s31, s31, 0
	s_waitcnt lgkmcnt(0)
	v_mfma_f32_16x16x32_bf16 v[78:81], v[238:241], v[218:221], v[78:81]
	v_mfma_f32_16x16x32_bf16 v[74:77], v[242:245], v[218:221], v[74:77]
	v_mfma_f32_16x16x32_bf16 v[70:73], v[246:249], v[218:221], v[70:73]
	v_mfma_f32_16x16x32_bf16 v[66:69], v[250:253], v[218:221], v[66:69]
	ds_read_b128 v[218:221], v93 offset:0
	ds_read_b128 v[142:145], v141 offset:19456
	s_mov_b32 m0, s47
	s_nop 0
	global_load_lds_dwordx4 v86, s[30:31]
	v_mfma_f32_16x16x32_bf16 v[62:65], v[238:241], v[222:225], v[62:65]
	v_mfma_f32_16x16x32_bf16 v[58:61], v[242:245], v[222:225], v[58:61]
	v_mfma_f32_16x16x32_bf16 v[54:57], v[246:249], v[222:225], v[54:57]
	v_mfma_f32_16x16x32_bf16 v[50:53], v[250:253], v[222:225], v[50:53]
	ds_read_b128 v[222:225], v93 offset:2048
	ds_read_b128 v[146:149], v141 offset:21504
	s_add_i32 m0, s47, 0x2000
	s_nop 0
	global_load_lds_dwordx4 v134, s[30:31]
	v_mfma_f32_16x16x32_bf16 v[46:49], v[238:241], v[226:229], v[46:49]
	v_mfma_f32_16x16x32_bf16 v[42:45], v[242:245], v[226:229], v[42:45]
	v_mfma_f32_16x16x32_bf16 v[38:41], v[246:249], v[226:229], v[38:41]
	v_mfma_f32_16x16x32_bf16 v[34:37], v[250:253], v[226:229], v[34:37]
	ds_read_b128 v[226:229], v93 offset:4096
	ds_read_b128 v[150:153], v141 offset:23552
	s_add_i32 m0, s47, 0x4000
	s_nop 0
	global_load_lds_dwordx4 v136, s[30:31]
	v_mfma_f32_16x16x32_bf16 v[18:21], v[238:241], v[230:233], v[18:21]
	v_mfma_f32_16x16x32_bf16 v[22:25], v[242:245], v[230:233], v[22:25]
	v_mfma_f32_16x16x32_bf16 v[26:29], v[246:249], v[230:233], v[26:29]
	v_mfma_f32_16x16x32_bf16 v[30:33], v[250:253], v[230:233], v[30:33]
	ds_read_b128 v[230:233], v93 offset:6144
	ds_read_b128 v[154:157], v141 offset:25600
	s_add_i32 m0, s47, 0x6000
	s_nop 0
	global_load_lds_dwordx4 v138, s[30:31]
	v_mfma_f32_16x16x32_bf16 v[2:5], v[238:241], v[234:237], v[2:5]
	v_mfma_f32_16x16x32_bf16 v[6:9], v[242:245], v[234:237], v[6:9]
	v_mfma_f32_16x16x32_bf16 v[10:13], v[246:249], v[234:237], v[10:13]
	v_mfma_f32_16x16x32_bf16 v[14:17], v[250:253], v[234:237], v[14:17]
	ds_read_b128 v[234:237], v93 offset:8192
	s_add_i32 m0, s47, 0x8000
	s_nop 0
	global_load_lds_dwordx4 v140, s[30:31]
	s_waitcnt lgkmcnt(0)
	s_load_dwordx8 s[20:27], s[28:29], 0x0
	s_add_u32 s28, s28, 0x100
	s_addc_u32 s29, s29, 0
	v_mfma_f32_16x16x32_bf16 v[78:81], v[142:145], v[218:221], v[78:81]
	v_mfma_f32_16x16x32_bf16 v[74:77], v[146:149], v[218:221], v[74:77]
	v_mfma_f32_16x16x32_bf16 v[70:73], v[150:153], v[218:221], v[70:73]
	v_mfma_f32_16x16x32_bf16 v[66:69], v[154:157], v[218:221], v[66:69]
	v_lshl_add_u64 v[132:133], v[132:133], 0, s[40:41]
	global_load_dwordx2 v[98:99], v[132:133], off
	global_load_dwordx2 v[100:101], v[132:133], off offset:2048
	v_mfma_f32_16x16x32_bf16 v[62:65], v[142:145], v[222:225], v[62:65]
	v_mfma_f32_16x16x32_bf16 v[58:61], v[146:149], v[222:225], v[58:61]
	v_mfma_f32_16x16x32_bf16 v[54:57], v[150:153], v[222:225], v[54:57]
	v_mfma_f32_16x16x32_bf16 v[50:53], v[154:157], v[222:225], v[50:53]
	v_lshl_add_u64 v[166:167], v[132:133], 0, s[34:35]
	global_load_dwordx2 v[102:103], v[166:167], off
	global_load_dwordx2 v[104:105], v[166:167], off offset:2048
	v_mfma_f32_16x16x32_bf16 v[46:49], v[142:145], v[226:229], v[46:49]
	v_mfma_f32_16x16x32_bf16 v[42:45], v[146:149], v[226:229], v[42:45]
	v_mfma_f32_16x16x32_bf16 v[38:41], v[150:153], v[226:229], v[38:41]
	v_mfma_f32_16x16x32_bf16 v[34:37], v[154:157], v[226:229], v[34:37]
	v_lshl_add_u64 v[166:167], v[132:133], 0, s[36:37]
	global_load_dwordx2 v[106:107], v[166:167], off
	global_load_dwordx2 v[108:109], v[166:167], off offset:2048
	v_mfma_f32_16x16x32_bf16 v[18:21], v[142:145], v[230:233], v[18:21]
	v_mfma_f32_16x16x32_bf16 v[22:25], v[146:149], v[230:233], v[22:25]
	v_mfma_f32_16x16x32_bf16 v[26:29], v[150:153], v[230:233], v[26:29]
	v_mfma_f32_16x16x32_bf16 v[30:33], v[154:157], v[230:233], v[30:33]
	v_lshl_add_u64 v[166:167], v[132:133], 0, s[38:39]
	global_load_dwordx2 v[110:111], v[166:167], off
	global_load_dwordx2 v[112:113], v[166:167], off offset:2048
	v_mfma_f32_16x16x32_bf16 v[2:5], v[142:145], v[234:237], v[2:5]
	v_mfma_f32_16x16x32_bf16 v[6:9], v[146:149], v[234:237], v[6:9]
	v_mfma_f32_16x16x32_bf16 v[10:13], v[150:153], v[234:237], v[10:13]
	v_mfma_f32_16x16x32_bf16 v[14:17], v[154:157], v[234:237], v[14:17]
	s_waitcnt vmcnt(21)
	s_mov_b32 s47, s42
	s_mov_b32 s42, s43
	s_mov_b32 s43, s44
	s_mov_b32 s44, s47
	s_waitcnt lgkmcnt(0)
	s_barrier
; #define MU_GLDS_A(buf, kt) do { _Pragma("unroll") for (int i = 0; i < NMU; ++i) \
;         __builtin_amdgcn_global_load_lds((const unsigned*)((const char*)A + aoff[i] + (size_t)(kt) * 128), (PG8_LAS unsigned*)(MU_SA(buf) + wid * 1024 + i * 8192), 16, 0, 0); } while (0)
; #define MU_B_ISSUE(sb, kt) do { const char* kb_ = Bb + (size_t)(kt) * (64 * (size_t)RB); _Pragma("unroll") for (int j = 0; j < 8; ++j) { const char* p_ = kb_ + (size_t)j * RB; \
;         asm volatile("global_load_dwordx2 %0, %1, off" : "=&v"(sb[j]) : "v"(p_) : "memory"); } } while (0)
; #define MU_B_WAIT(sb, N) asm volatile("s_waitcnt vmcnt(%8)" : "+v"(sb[0]), "+v"(sb[1]), "+v"(sb[2]), "+v"(sb[3]), "+v"(sb[4]), "+v"(sb[5]), "+v"(sb[6]), "+v"(sb[7]) : "n"(N) : "memory")
; #define MU_G_LOAD(ga, kt) do { const PG8_LAS f32x4* gk_ = (const PG8_LAS f32x4*)(lds + GAIN_OFF) + 16 * (kt) + 2 * wid; const f32x4 ga_ = gk_[0], gb_ = gk_[1]; \
;         ga[0] = ga_[0]; ga[1] = ga_[1]; ga[2] = ga_[2]; ga[3] = ga_[3]; ga[4] = gb_[0]; ga[5] = gb_[1]; ga[6] = gb_[2]; ga[7] = gb_[3]; } while (0)
; #define MU_COMPUTE(buf) MU_COMPUTE_N(buf, NMU)
; #define MU_END(last) do { if (last) asm volatile("s_waitcnt vmcnt(0)" ::: "memory"); else asm volatile("s_waitcnt vmcnt(8)" ::: "memory"); \
;         asm volatile("s_waitcnt lgkmcnt(0)" ::: "memory"); __builtin_amdgcn_s_barrier(); asm volatile("" ::: "memory"); } while (0)
; template <int MODE>
; __device__ __forceinline__ void moe_unit(PG8_LAS unsigned char* lds, int e, int cb, int slot0  , int nv  , const bf16_t* A, const int* slot_tok,
;                                          const float* W0, const float* W1, bf16_t* OUT, const float* slot_rs  , const int* slot_dst) {
;     ...
;     for (int t = 0; t < nt; t += 2) {
;         if (t + 2 < nt) MU_B_WAIT(s1, 8); else MU_B_WAIT(s1, 0);
;         MU_G_LOAD(g0, t + 1); MU_B_WRITE(s1, 1, g0); __builtin_amdgcn_sched_barrier(0); MU_GLDS_A(1, t + 1); __builtin_amdgcn_sched_barrier(0);
;         if (t + 3 < nt) { MU_B_ISSUE(s1, t + 3); }
;         MU_COMPUTE(0);
;         MU_END(t + 3 >= nt);
;         if (t + 2 < nt) { MU_B_WAIT(s0, 8); MU_G_LOAD(g0, t + 2); MU_B_WRITE(s0, 0, g0); __builtin_amdgcn_sched_barrier(0); MU_GLDS_A(0, t + 2); __builtin_amdgcn_sched_barrier(0); }
;         if (t + 4 < nt) { MU_B_ISSUE(s0, t + 4); }
;         MU_COMPUTE(1);
;         MU_END(t + 4 >= nt);
	s_sub_u32 s46, s46, 1
	s_cmp_lg_u32 s46, 0
	s_cbranch_scc1 .Lmu_loop_X5
	v_mul_f32_e32 v114, s20, v114
	v_mul_f32_e32 v115, s20, v115
	v_mul_f32_e32 v116, s21, v116
	v_mul_f32_e32 v117, s21, v117
	v_mul_f32_e32 v118, s22, v118
	v_mul_f32_e32 v119, s22, v119
	v_mul_f32_e32 v120, s23, v120
	v_mul_f32_e32 v121, s23, v121
	v_mul_f32_e32 v122, s24, v122
	v_mul_f32_e32 v123, s24, v123
	v_mul_f32_e32 v124, s25, v124
	v_mul_f32_e32 v125, s25, v125
	v_mul_f32_e32 v126, s26, v126
	v_mul_f32_e32 v127, s26, v127
	v_mul_f32_e32 v128, s27, v128
	v_mul_f32_e32 v129, s27, v129
	v_cvt_pk_bf16_f32 v158, v114, v116
	v_cvt_pk_bf16_f32 v159, v118, v120
	v_cvt_pk_bf16_f32 v160, v122, v124
	v_cvt_pk_bf16_f32 v161, v126, v128
	v_cvt_pk_bf16_f32 v162, v115, v117
	v_cvt_pk_bf16_f32 v163, v119, v121
	v_cvt_pk_bf16_f32 v164, v123, v125
	v_cvt_pk_bf16_f32 v165, v127, v129
	ds_write_b128 v1, v[158:161] offset:19456
	ds_write_b128 v1, v[162:165] offset:19584
	v_add_u32_e32 v91, s42, v135
	v_add_u32_e32 v93, s42, v137
	ds_read_b128 v[238:241], v139 offset:0
	ds_read_b128 v[242:245], v139 offset:2048
	ds_read_b128 v[246:249], v139 offset:4096
	ds_read_b128 v[250:253], v139 offset:6144
	ds_read_b128 v[218:221], v91 offset:0
	ds_read_b128 v[222:225], v91 offset:2048
	ds_read_b128 v[226:229], v91 offset:4096
	ds_read_b128 v[230:233], v91 offset:6144
	ds_read_b128 v[234:237], v91 offset:8192
	s_add_i32 s47, s44, s6
	s_add_u32 s30, s30, 0x80
	s_addc_u32 s31, s31, 0
	s_waitcnt lgkmcnt(0)
	v_mfma_f32_16x16x32_bf16 v[78:81], v[238:241], v[218:221], v[78:81]
	v_mfma_f32_16x16x32_bf16 v[74:77], v[242:245], v[218:221], v[74:77]
	v_mfma_f32_16x16x32_bf16 v[70:73], v[246:249], v[218:221], v[70:73]
	v_mfma_f32_16x16x32_bf16 v[66:69], v[250:253], v[218:221], v[66:69]
	ds_read_b128 v[218:221], v93 offset:0
	ds_read_b128 v[142:145], v141 offset:0
	s_mov_b32 m0, s47
	s_nop 0
	global_load_lds_dwordx4 v86, s[30:31]
	v_mfma_f32_16x16x32_bf16 v[62:65], v[238:241], v[222:225], v[62:65]
	v_mfma_f32_16x16x32_bf16 v[58:61], v[242:245], v[222:225], v[58:61]
	v_mfma_f32_16x16x32_bf16 v[54:57], v[246:249], v[222:225], v[54:57]
	v_mfma_f32_16x16x32_bf16 v[50:53], v[250:253], v[222:225], v[50:53]
	ds_read_b128 v[222:225], v93 offset:2048
	ds_read_b128 v[146:149], v141 offset:2048
	s_add_i32 m0, s47, 0x2000
	s_nop 0
	global_load_lds_dwordx4 v134, s[30:31]
	v_mfma_f32_16x16x32_bf16 v[46:49], v[238:241], v[226:229], v[46:49]
	v_mfma_f32_16x16x32_bf16 v[42:45], v[242:245], v[226:229], v[42:45]
	v_mfma_f32_16x16x32_bf16 v[38:41], v[246:249], v[226:229], v[38:41]
	v_mfma_f32_16x16x32_bf16 v[34:37], v[250:253], v[226:229], v[34:37]
	ds_read_b128 v[226:229], v93 offset:4096
	ds_read_b128 v[150:153], v141 offset:4096
	s_add_i32 m0, s47, 0x4000
	s_nop 0
	global_load_lds_dwordx4 v136, s[30:31]
	v_mfma_f32_16x16x32_bf16 v[18:21], v[238:241], v[230:233], v[18:21]
	v_mfma_f32_16x16x32_bf16 v[22:25], v[242:245], v[230:233], v[22:25]
	v_mfma_f32_16x16x32_bf16 v[26:29], v[246:249], v[230:233], v[26:29]
	v_mfma_f32_16x16x32_bf16 v[30:33], v[250:253], v[230:233], v[30:33]
	ds_read_b128 v[230:233], v93 offset:6144
	ds_read_b128 v[154:157], v141 offset:6144
	s_add_i32 m0, s47, 0x6000
	s_nop 0
	global_load_lds_dwordx4 v138, s[30:31]
	v_mfma_f32_16x16x32_bf16 v[2:5], v[238:241], v[234:237], v[2:5]
	v_mfma_f32_16x16x32_bf16 v[6:9], v[242:245], v[234:237], v[6:9]
	v_mfma_f32_16x16x32_bf16 v[10:13], v[246:249], v[234:237], v[10:13]
	v_mfma_f32_16x16x32_bf16 v[14:17], v[250:253], v[234:237], v[14:17]
	ds_read_b128 v[234:237], v93 offset:8192
	s_add_i32 m0, s47, 0x8000
	s_nop 0
	global_load_lds_dwordx4 v140, s[30:31]
	s_waitcnt lgkmcnt(0)
	s_load_dwordx8 s[12:19], s[28:29], 0x0
	s_add_u32 s28, s28, 0x100
	s_addc_u32 s29, s29, 0
	v_mfma_f32_16x16x32_bf16 v[78:81], v[142:145], v[218:221], v[78:81]
	v_mfma_f32_16x16x32_bf16 v[74:77], v[146:149], v[218:221], v[74:77]
	v_mfma_f32_16x16x32_bf16 v[70:73], v[150:153], v[218:221], v[70:73]
	v_mfma_f32_16x16x32_bf16 v[66:69], v[154:157], v[218:221], v[66:69]
	v_lshl_add_u64 v[132:133], v[132:133], 0, s[40:41]
	global_load_dwordx2 v[114:115], v[132:133], off
	global_load_dwordx2 v[116:117], v[132:133], off offset:2048
	v_mfma_f32_16x16x32_bf16 v[62:65], v[142:145], v[222:225], v[62:65]
	v_mfma_f32_16x16x32_bf16 v[58:61], v[146:149], v[222:225], v[58:61]
	v_mfma_f32_16x16x32_bf16 v[54:57], v[150:153], v[222:225], v[54:57]
	v_mfma_f32_16x16x32_bf16 v[50:53], v[154:157], v[222:225], v[50:53]
	v_lshl_add_u64 v[166:167], v[132:133], 0, s[34:35]
	global_load_dwordx2 v[118:119], v[166:167], off
	global_load_dwordx2 v[120:121], v[166:167], off offset:2048
	v_mfma_f32_16x16x32_bf16 v[46:49], v[142:145], v[226:229], v[46:49]
	v_mfma_f32_16x16x32_bf16 v[42:45], v[146:149], v[226:229], v[42:45]
	v_mfma_f32_16x16x32_bf16 v[38:41], v[150:153], v[226:229], v[38:41]
	v_mfma_f32_16x16x32_bf16 v[34:37], v[154:157], v[226:229], v[34:37]
	v_lshl_add_u64 v[166:167], v[132:133], 0, s[36:37]
	global_load_dwordx2 v[122:123], v[166:167], off
	global_load_dwordx2 v[124:125], v[166:167], off offset:2048
	v_mfma_f32_16x16x32_bf16 v[18:21], v[142:145], v[230:233], v[18:21]
	v_mfma_f32_16x16x32_bf16 v[22:25], v[146:149], v[230:233], v[22:25]
	v_mfma_f32_16x16x32_bf16 v[26:29], v[150:153], v[230:233], v[26:29]
	v_mfma_f32_16x16x32_bf16 v[30:33], v[154:157], v[230:233], v[30:33]
	v_lshl_add_u64 v[166:167], v[132:133], 0, s[38:39]
	global_load_dwordx2 v[126:127], v[166:167], off
	global_load_dwordx2 v[128:129], v[166:167], off offset:2048
	v_mfma_f32_16x16x32_bf16 v[2:5], v[142:145], v[234:237], v[2:5]
	v_mfma_f32_16x16x32_bf16 v[6:9], v[146:149], v[234:237], v[6:9]
	v_mfma_f32_16x16x32_bf16 v[10:13], v[150:153], v[234:237], v[10:13]
	v_mfma_f32_16x16x32_bf16 v[14:17], v[154:157], v[234:237], v[14:17]
	s_waitcnt vmcnt(21)
	s_mov_b32 s47, s42
	s_mov_b32 s42, s43
	s_mov_b32 s43, s44
	s_mov_b32 s44, s47
	s_waitcnt lgkmcnt(0)
	s_barrier
; #define MU_GLDS_A(buf, kt) do { _Pragma("unroll") for (int i = 0; i < NMU; ++i) \
;         __builtin_amdgcn_global_load_lds((const unsigned*)((const char*)A + aoff[i] + (size_t)(kt) * 128), (PG8_LAS unsigned*)(MU_SA(buf) + wid * 1024 + i * 8192), 16, 0, 0); } while (0)
; #define MU_B_ISSUE(sb, kt) do { const char* kb_ = Bb + (size_t)(kt) * (64 * (size_t)RB); _Pragma("unroll") for (int j = 0; j < 8; ++j) { const char* p_ = kb_ + (size_t)j * RB; \
;         asm volatile("global_load_dwordx2 %0, %1, off" : "=&v"(sb[j]) : "v"(p_) : "memory"); } } while (0)
; #define MU_B_WAIT(sb, N) asm volatile("s_waitcnt vmcnt(%8)" : "+v"(sb[0]), "+v"(sb[1]), "+v"(sb[2]), "+v"(sb[3]), "+v"(sb[4]), "+v"(sb[5]), "+v"(sb[6]), "+v"(sb[7]) : "n"(N) : "memory")
; #define MU_G_LOAD(ga, kt) do { const PG8_LAS f32x4* gk_ = (const PG8_LAS f32x4*)(lds + GAIN_OFF) + 16 * (kt) + 2 * wid; const f32x4 ga_ = gk_[0], gb_ = gk_[1]; \
;         ga[0] = ga_[0]; ga[1] = ga_[1]; ga[2] = ga_[2]; ga[3] = ga_[3]; ga[4] = gb_[0]; ga[5] = gb_[1]; ga[6] = gb_[2]; ga[7] = gb_[3]; } while (0)
; #define MU_COMPUTE(buf) MU_COMPUTE_N(buf, NMU)
; #define MU_END(last) do { if (last) asm volatile("s_waitcnt vmcnt(0)" ::: "memory"); else asm volatile("s_waitcnt vmcnt(8)" ::: "memory"); \
;         asm volatile("s_waitcnt lgkmcnt(0)" ::: "memory"); __builtin_amdgcn_s_barrier(); asm volatile("" ::: "memory"); } while (0)
; template <int MODE>
; __device__ __forceinline__ void moe_unit(PG8_LAS unsigned char* lds, int e, int cb, int slot0  , int nv  , const bf16_t* A, const int* slot_tok,
;                                          const float* W0, const float* W1, bf16_t* OUT, const float* slot_rs  , const int* slot_dst) {
;     ...
;     for (int t = 0; t < nt; t += 2) {
;         if (t + 2 < nt) MU_B_WAIT(s1, 8); else MU_B_WAIT(s1, 0);
;         MU_G_LOAD(g0, t + 1); MU_B_WRITE(s1, 1, g0); __builtin_amdgcn_sched_barrier(0); MU_GLDS_A(1, t + 1); __builtin_amdgcn_sched_barrier(0);
;         if (t + 3 < nt) { MU_B_ISSUE(s1, t + 3); }
;         MU_COMPUTE(0);
;         MU_END(t + 3 >= nt);
;         if (t + 2 < nt) { MU_B_WAIT(s0, 8); MU_G_LOAD(g0, t + 2); MU_B_WRITE(s0, 0, g0); __builtin_amdgcn_sched_barrier(0); MU_GLDS_A(0, t + 2); __builtin_amdgcn_sched_barrier(0); }
;         if (t + 4 < nt) { MU_B_ISSUE(s0, t + 4); }
;         MU_COMPUTE(1);
;         MU_END(t + 4 >= nt);
	v_mul_f32_e32 v186, s12, v186
	v_mul_f32_e32 v187, s12, v187
	v_mul_f32_e32 v188, s13, v188
	v_mul_f32_e32 v189, s13, v189
	v_mul_f32_e32 v190, s14, v190
	v_mul_f32_e32 v191, s14, v191
	v_mul_f32_e32 v192, s15, v192
	v_mul_f32_e32 v193, s15, v193
	v_mul_f32_e32 v194, s16, v194
	v_mul_f32_e32 v195, s16, v195
	v_mul_f32_e32 v196, s17, v196
	v_mul_f32_e32 v197, s17, v197
	v_mul_f32_e32 v198, s18, v198
	v_mul_f32_e32 v199, s18, v199
	v_mul_f32_e32 v200, s19, v200
	v_mul_f32_e32 v201, s19, v201
	v_cvt_pk_bf16_f32 v158, v186, v188
	v_cvt_pk_bf16_f32 v159, v190, v192
	v_cvt_pk_bf16_f32 v160, v194, v196
	v_cvt_pk_bf16_f32 v161, v198, v200
	v_cvt_pk_bf16_f32 v162, v187, v189
	v_cvt_pk_bf16_f32 v163, v191, v193
	v_cvt_pk_bf16_f32 v164, v195, v197
	v_cvt_pk_bf16_f32 v165, v199, v201
	ds_write_b128 v1, v[158:161] offset:0
	ds_write_b128 v1, v[162:165] offset:128
	v_add_u32_e32 v91, s42, v135
	v_add_u32_e32 v93, s42, v137
	ds_read_b128 v[238:241], v139 offset:19456
	ds_read_b128 v[242:245], v139 offset:21504
	ds_read_b128 v[246:249], v139 offset:23552
	ds_read_b128 v[250:253], v139 offset:25600
	ds_read_b128 v[218:221], v91 offset:0
	ds_read_b128 v[222:225], v91 offset:2048
	ds_read_b128 v[226:229], v91 offset:4096
	ds_read_b128 v[230:233], v91 offset:6144
	ds_read_b128 v[234:237], v91 offset:8192
	s_add_i32 s47, s44, s6
	s_add_u32 s30, s30, 0x80
	s_addc_u32 s31, s31, 0
	s_waitcnt lgkmcnt(0)
	v_mfma_f32_16x16x32_bf16 v[78:81], v[238:241], v[218:221], v[78:81]
	v_mfma_f32_16x16x32_bf16 v[74:77], v[242:245], v[218:221], v[74:77]
	v_mfma_f32_16x16x32_bf16 v[70:73], v[246:249], v[218:221], v[70:73]
	v_mfma_f32_16x16x32_bf16 v[66:69], v[250:253], v[218:221], v[66:69]
	ds_read_b128 v[218:221], v93 offset:0
	ds_read_b128 v[142:145], v141 offset:19456
	s_mov_b32 m0, s47
	s_nop 0
	global_load_lds_dwordx4 v86, s[30:31]
	v_mfma_f32_16x16x32_bf16 v[62:65], v[238:241], v[222:225], v[62:65]
	v_mfma_f32_16x16x32_bf16 v[58:61], v[242:245], v[222:225], v[58:61]
	v_mfma_f32_16x16x32_bf16 v[54:57], v[246:249], v[222:225], v[54:57]
	v_mfma_f32_16x16x32_bf16 v[50:53], v[250:253], v[222:225], v[50:53]
	ds_read_b128 v[222:225], v93 offset:2048
	ds_read_b128 v[146:149], v141 offset:21504
	s_add_i32 m0, s47, 0x2000
	s_nop 0
	global_load_lds_dwordx4 v134, s[30:31]
	v_mfma_f32_16x16x32_bf16 v[46:49], v[238:241], v[226:229], v[46:49]
	v_mfma_f32_16x16x32_bf16 v[42:45], v[242:245], v[226:229], v[42:45]
	v_mfma_f32_16x16x32_bf16 v[38:41], v[246:249], v[226:229], v[38:41]
	v_mfma_f32_16x16x32_bf16 v[34:37], v[250:253], v[226:229], v[34:37]
	ds_read_b128 v[226:229], v93 offset:4096
	ds_read_b128 v[150:153], v141 offset:23552
	s_add_i32 m0, s47, 0x4000
	s_nop 0
	global_load_lds_dwordx4 v136, s[30:31]
	v_mfma_f32_16x16x32_bf16 v[18:21], v[238:241], v[230:233], v[18:21]
	v_mfma_f32_16x16x32_bf16 v[22:25], v[242:245], v[230:233], v[22:25]
	v_mfma_f32_16x16x32_bf16 v[26:29], v[246:249], v[230:233], v[26:29]
	v_mfma_f32_16x16x32_bf16 v[30:33], v[250:253], v[230:233], v[30:33]
	ds_read_b128 v[230:233], v93 offset:6144
	ds_read_b128 v[154:157], v141 offset:25600
	s_add_i32 m0, s47, 0x6000
	s_nop 0
	global_load_lds_dwordx4 v138, s[30:31]
	v_mfma_f32_16x16x32_bf16 v[2:5], v[238:241], v[234:237], v[2:5]
	v_mfma_f32_16x16x32_bf16 v[6:9], v[242:245], v[234:237], v[6:9]
	v_mfma_f32_16x16x32_bf16 v[10:13], v[246:249], v[234:237], v[10:13]
	v_mfma_f32_16x16x32_bf16 v[14:17], v[250:253], v[234:237], v[14:17]
	ds_read_b128 v[234:237], v93 offset:8192
	s_add_i32 m0, s47, 0x8000
	s_nop 0
	global_load_lds_dwordx4 v140, s[30:31]
	s_waitcnt lgkmcnt(0)
	s_load_dwordx8 s[20:27], s[28:29], 0x0
	s_add_u32 s28, s28, 0x100
	s_addc_u32 s29, s29, 0
	v_mfma_f32_16x16x32_bf16 v[78:81], v[142:145], v[218:221], v[78:81]
	v_mfma_f32_16x16x32_bf16 v[74:77], v[146:149], v[218:221], v[74:77]
	v_mfma_f32_16x16x32_bf16 v[70:73], v[150:153], v[218:221], v[70:73]
	v_mfma_f32_16x16x32_bf16 v[66:69], v[154:157], v[218:221], v[66:69]
	v_lshl_add_u64 v[132:133], v[132:133], 0, s[40:41]
	global_load_dwordx2 v[186:187], v[132:133], off
	global_load_dwordx2 v[188:189], v[132:133], off offset:2048
	v_mfma_f32_16x16x32_bf16 v[62:65], v[142:145], v[222:225], v[62:65]
	v_mfma_f32_16x16x32_bf16 v[58:61], v[146:149], v[222:225], v[58:61]
	v_mfma_f32_16x16x32_bf16 v[54:57], v[150:153], v[222:225], v[54:57]
	v_mfma_f32_16x16x32_bf16 v[50:53], v[154:157], v[222:225], v[50:53]
	v_lshl_add_u64 v[166:167], v[132:133], 0, s[34:35]
	global_load_dwordx2 v[190:191], v[166:167], off
	global_load_dwordx2 v[192:193], v[166:167], off offset:2048
	v_mfma_f32_16x16x32_bf16 v[46:49], v[142:145], v[226:229], v[46:49]
	v_mfma_f32_16x16x32_bf16 v[42:45], v[146:149], v[226:229], v[42:45]
	v_mfma_f32_16x16x32_bf16 v[38:41], v[150:153], v[226:229], v[38:41]
	v_mfma_f32_16x16x32_bf16 v[34:37], v[154:157], v[226:229], v[34:37]
	v_lshl_add_u64 v[166:167], v[132:133], 0, s[36:37]
	global_load_dwordx2 v[194:195], v[166:167], off
	global_load_dwordx2 v[196:197], v[166:167], off offset:2048
	v_mfma_f32_16x16x32_bf16 v[18:21], v[142:145], v[230:233], v[18:21]
	v_mfma_f32_16x16x32_bf16 v[22:25], v[146:149], v[230:233], v[22:25]
	v_mfma_f32_16x16x32_bf16 v[26:29], v[150:153], v[230:233], v[26:29]
	v_mfma_f32_16x16x32_bf16 v[30:33], v[154:157], v[230:233], v[30:33]
	v_lshl_add_u64 v[166:167], v[132:133], 0, s[38:39]
	global_load_dwordx2 v[198:199], v[166:167], off
	global_load_dwordx2 v[200:201], v[166:167], off offset:2048
	v_mfma_f32_16x16x32_bf16 v[2:5], v[142:145], v[234:237], v[2:5]
	v_mfma_f32_16x16x32_bf16 v[6:9], v[146:149], v[234:237], v[6:9]
	v_mfma_f32_16x16x32_bf16 v[10:13], v[150:153], v[234:237], v[10:13]
	v_mfma_f32_16x16x32_bf16 v[14:17], v[154:157], v[234:237], v[14:17]
	s_waitcnt vmcnt(21)
	s_mov_b32 s47, s42
	s_mov_b32 s42, s43
	s_mov_b32 s43, s44
	s_mov_b32 s44, s47
	s_waitcnt lgkmcnt(0)
	s_barrier
; #define MU_GLDS_A(buf, kt) do { _Pragma("unroll") for (int i = 0; i < NMU; ++i) \
;         __builtin_amdgcn_global_load_lds((const unsigned*)((const char*)A + aoff[i] + (size_t)(kt) * 128), (PG8_LAS unsigned*)(MU_SA(buf) + wid * 1024 + i * 8192), 16, 0, 0); } while (0)
; #define MU_B_ISSUE(sb, kt) do { const char* kb_ = Bb + (size_t)(kt) * (64 * (size_t)RB); _Pragma("unroll") for (int j = 0; j < 8; ++j) { const char* p_ = kb_ + (size_t)j * RB; \
;         asm volatile("global_load_dwordx2 %0, %1, off" : "=&v"(sb[j]) : "v"(p_) : "memory"); } } while (0)
; #define MU_B_WAIT(sb, N) asm volatile("s_waitcnt vmcnt(%8)" : "+v"(sb[0]), "+v"(sb[1]), "+v"(sb[2]), "+v"(sb[3]), "+v"(sb[4]), "+v"(sb[5]), "+v"(sb[6]), "+v"(sb[7]) : "n"(N) : "memory")
; #define MU_G_LOAD(ga, kt) do { const PG8_LAS f32x4* gk_ = (const PG8_LAS f32x4*)(lds + GAIN_OFF) + 16 * (kt) + 2 * wid; const f32x4 ga_ = gk_[0], gb_ = gk_[1]; \
;         ga[0] = ga_[0]; ga[1] = ga_[1]; ga[2] = ga_[2]; ga[3] = ga_[3]; ga[4] = gb_[0]; ga[5] = gb_[1]; ga[6] = gb_[2]; ga[7] = gb_[3]; } while (0)
; #define MU_COMPUTE(buf) MU_COMPUTE_N(buf, NMU)
; #define MU_END(last) do { if (last) asm volatile("s_waitcnt vmcnt(0)" ::: "memory"); else asm volatile("s_waitcnt vmcnt(8)" ::: "memory"); \
;         asm volatile("s_waitcnt lgkmcnt(0)" ::: "memory"); __builtin_amdgcn_s_barrier(); asm volatile("" ::: "memory"); } while (0)
; template <int MODE>
; __device__ __forceinline__ void moe_unit(PG8_LAS unsigned char* lds, int e, int cb, int slot0  , int nv  , const bf16_t* A, const int* slot_tok,
;                                          const float* W0, const float* W1, bf16_t* OUT, const float* slot_rs  , const int* slot_dst) {
;     ...
;     for (int t = 0; t < nt; t += 2) {
;         if (t + 2 < nt) MU_B_WAIT(s1, 8); else MU_B_WAIT(s1, 0);
;         MU_G_LOAD(g0, t + 1); MU_B_WRITE(s1, 1, g0); __builtin_amdgcn_sched_barrier(0); MU_GLDS_A(1, t + 1); __builtin_amdgcn_sched_barrier(0);
;         if (t + 3 < nt) { MU_B_ISSUE(s1, t + 3); }
;         MU_COMPUTE(0);
;         MU_END(t + 3 >= nt);
;         if (t + 2 < nt) { MU_B_WAIT(s0, 8); MU_G_LOAD(g0, t + 2); MU_B_WRITE(s0, 0, g0); __builtin_amdgcn_sched_barrier(0); MU_GLDS_A(0, t + 2); __builtin_amdgcn_sched_barrier(0); }
;         if (t + 4 < nt) { MU_B_ISSUE(s0, t + 4); }
;         MU_COMPUTE(1);
;         MU_END(t + 4 >= nt);
	v_mul_f32_e32 v202, s20, v202
	v_mul_f32_e32 v203, s20, v203
	v_mul_f32_e32 v204, s21, v204
	v_mul_f32_e32 v205, s21, v205
	v_mul_f32_e32 v206, s22, v206
	v_mul_f32_e32 v207, s22, v207
	v_mul_f32_e32 v208, s23, v208
	v_mul_f32_e32 v209, s23, v209
	v_mul_f32_e32 v210, s24, v210
	v_mul_f32_e32 v211, s24, v211
	v_mul_f32_e32 v212, s25, v212
	v_mul_f32_e32 v213, s25, v213
	v_mul_f32_e32 v214, s26, v214
	v_mul_f32_e32 v215, s26, v215
	v_mul_f32_e32 v216, s27, v216
	v_mul_f32_e32 v217, s27, v217
	v_cvt_pk_bf16_f32 v158, v202, v204
	v_cvt_pk_bf16_f32 v159, v206, v208
	v_cvt_pk_bf16_f32 v160, v210, v212
	v_cvt_pk_bf16_f32 v161, v214, v216
	v_cvt_pk_bf16_f32 v162, v203, v205
	v_cvt_pk_bf16_f32 v163, v207, v209
	v_cvt_pk_bf16_f32 v164, v211, v213
	v_cvt_pk_bf16_f32 v165, v215, v217
	ds_write_b128 v1, v[158:161] offset:19456
	ds_write_b128 v1, v[162:165] offset:19584
	v_add_u32_e32 v91, s42, v135
	v_add_u32_e32 v93, s42, v137
	ds_read_b128 v[238:241], v139 offset:0
	ds_read_b128 v[242:245], v139 offset:2048
	ds_read_b128 v[246:249], v139 offset:4096
	ds_read_b128 v[250:253], v139 offset:6144
	ds_read_b128 v[218:221], v91 offset:0
	ds_read_b128 v[222:225], v91 offset:2048
	ds_read_b128 v[226:229], v91 offset:4096
	ds_read_b128 v[230:233], v91 offset:6144
	ds_read_b128 v[234:237], v91 offset:8192
	s_add_i32 s47, s44, s6
	s_add_u32 s30, s30, 0x80
	s_addc_u32 s31, s31, 0
	s_waitcnt lgkmcnt(0)
	v_mfma_f32_16x16x32_bf16 v[78:81], v[238:241], v[218:221], v[78:81]
	v_mfma_f32_16x16x32_bf16 v[74:77], v[242:245], v[218:221], v[74:77]
	v_mfma_f32_16x16x32_bf16 v[70:73], v[246:249], v[218:221], v[70:73]
	v_mfma_f32_16x16x32_bf16 v[66:69], v[250:253], v[218:221], v[66:69]
	ds_read_b128 v[218:221], v93 offset:0
	ds_read_b128 v[142:145], v141 offset:0
	s_mov_b32 m0, s47
	s_nop 0
	global_load_lds_dwordx4 v86, s[30:31]
	v_mfma_f32_16x16x32_bf16 v[62:65], v[238:241], v[222:225], v[62:65]
	v_mfma_f32_16x16x32_bf16 v[58:61], v[242:245], v[222:225], v[58:61]
	v_mfma_f32_16x16x32_bf16 v[54:57], v[246:249], v[222:225], v[54:57]
	v_mfma_f32_16x16x32_bf16 v[50:53], v[250:253], v[222:225], v[50:53]
	ds_read_b128 v[222:225], v93 offset:2048
	ds_read_b128 v[146:149], v141 offset:2048
	s_add_i32 m0, s47, 0x2000
	s_nop 0
	global_load_lds_dwordx4 v134, s[30:31]
	v_mfma_f32_16x16x32_bf16 v[46:49], v[238:241], v[226:229], v[46:49]
	v_mfma_f32_16x16x32_bf16 v[42:45], v[242:245], v[226:229], v[42:45]
	v_mfma_f32_16x16x32_bf16 v[38:41], v[246:249], v[226:229], v[38:41]
	v_mfma_f32_16x16x32_bf16 v[34:37], v[250:253], v[226:229], v[34:37]
	ds_read_b128 v[226:229], v93 offset:4096
	ds_read_b128 v[150:153], v141 offset:4096
	s_add_i32 m0, s47, 0x4000
	s_nop 0
	global_load_lds_dwordx4 v136, s[30:31]
	v_mfma_f32_16x16x32_bf16 v[18:21], v[238:241], v[230:233], v[18:21]
	v_mfma_f32_16x16x32_bf16 v[22:25], v[242:245], v[230:233], v[22:25]
	v_mfma_f32_16x16x32_bf16 v[26:29], v[246:249], v[230:233], v[26:29]
	v_mfma_f32_16x16x32_bf16 v[30:33], v[250:253], v[230:233], v[30:33]
	ds_read_b128 v[230:233], v93 offset:6144
	ds_read_b128 v[154:157], v141 offset:6144
	s_add_i32 m0, s47, 0x6000
	s_nop 0
	global_load_lds_dwordx4 v138, s[30:31]
	v_mfma_f32_16x16x32_bf16 v[2:5], v[238:241], v[234:237], v[2:5]
	v_mfma_f32_16x16x32_bf16 v[6:9], v[242:245], v[234:237], v[6:9]
	v_mfma_f32_16x16x32_bf16 v[10:13], v[246:249], v[234:237], v[10:13]
	v_mfma_f32_16x16x32_bf16 v[14:17], v[250:253], v[234:237], v[14:17]
	ds_read_b128 v[234:237], v93 offset:8192
	s_add_i32 m0, s47, 0x8000
	s_nop 0
	global_load_lds_dwordx4 v140, s[30:31]
	s_waitcnt lgkmcnt(0)
	s_load_dwordx8 s[12:19], s[28:29], 0x0
	s_add_u32 s28, s28, 0x100
	s_addc_u32 s29, s29, 0
	v_mfma_f32_16x16x32_bf16 v[78:81], v[142:145], v[218:221], v[78:81]
	v_mfma_f32_16x16x32_bf16 v[74:77], v[146:149], v[218:221], v[74:77]
	v_mfma_f32_16x16x32_bf16 v[70:73], v[150:153], v[218:221], v[70:73]
	v_mfma_f32_16x16x32_bf16 v[66:69], v[154:157], v[218:221], v[66:69]
	v_lshl_add_u64 v[132:133], v[132:133], 0, s[40:41]
	global_load_dwordx2 v[202:203], v[132:133], off
	global_load_dwordx2 v[204:205], v[132:133], off offset:2048
	v_mfma_f32_16x16x32_bf16 v[62:65], v[142:145], v[222:225], v[62:65]
	v_mfma_f32_16x16x32_bf16 v[58:61], v[146:149], v[222:225], v[58:61]
	v_mfma_f32_16x16x32_bf16 v[54:57], v[150:153], v[222:225], v[54:57]
	v_mfma_f32_16x16x32_bf16 v[50:53], v[154:157], v[222:225], v[50:53]
	v_lshl_add_u64 v[166:167], v[132:133], 0, s[34:35]
	global_load_dwordx2 v[206:207], v[166:167], off
	global_load_dwordx2 v[208:209], v[166:167], off offset:2048
	v_mfma_f32_16x16x32_bf16 v[46:49], v[142:145], v[226:229], v[46:49]
	v_mfma_f32_16x16x32_bf16 v[42:45], v[146:149], v[226:229], v[42:45]
	v_mfma_f32_16x16x32_bf16 v[38:41], v[150:153], v[226:229], v[38:41]
	v_mfma_f32_16x16x32_bf16 v[34:37], v[154:157], v[226:229], v[34:37]
	v_lshl_add_u64 v[166:167], v[132:133], 0, s[36:37]
	global_load_dwordx2 v[210:211], v[166:167], off
	global_load_dwordx2 v[212:213], v[166:167], off offset:2048
	v_mfma_f32_16x16x32_bf16 v[18:21], v[142:145], v[230:233], v[18:21]
	v_mfma_f32_16x16x32_bf16 v[22:25], v[146:149], v[230:233], v[22:25]
	v_mfma_f32_16x16x32_bf16 v[26:29], v[150:153], v[230:233], v[26:29]
	v_mfma_f32_16x16x32_bf16 v[30:33], v[154:157], v[230:233], v[30:33]
	v_lshl_add_u64 v[166:167], v[132:133], 0, s[38:39]
	global_load_dwordx2 v[214:215], v[166:167], off
	global_load_dwordx2 v[216:217], v[166:167], off offset:2048
	v_mfma_f32_16x16x32_bf16 v[2:5], v[142:145], v[234:237], v[2:5]
	v_mfma_f32_16x16x32_bf16 v[6:9], v[146:149], v[234:237], v[6:9]
	v_mfma_f32_16x16x32_bf16 v[10:13], v[150:153], v[234:237], v[10:13]
	v_mfma_f32_16x16x32_bf16 v[14:17], v[154:157], v[234:237], v[14:17]
	s_waitcnt vmcnt(21)
	s_mov_b32 s47, s42
	s_mov_b32 s42, s43
	s_mov_b32 s43, s44
	s_mov_b32 s44, s47
	s_waitcnt lgkmcnt(0)
	s_barrier
; #define MU_GLDS_A(buf, kt) do { _Pragma("unroll") for (int i = 0; i < NMU; ++i) \
;         __builtin_amdgcn_global_load_lds((const unsigned*)((const char*)A + aoff[i] + (size_t)(kt) * 128), (PG8_LAS unsigned*)(MU_SA(buf) + wid * 1024 + i * 8192), 16, 0, 0); } while (0)
; #define MU_B_ISSUE(sb, kt) do { const char* kb_ = Bb + (size_t)(kt) * (64 * (size_t)RB); _Pragma("unroll") for (int j = 0; j < 8; ++j) { const char* p_ = kb_ + (size_t)j * RB; \
;         asm volatile("global_load_dwordx2 %0, %1, off" : "=&v"(sb[j]) : "v"(p_) : "memory"); } } while (0)
; #define MU_B_WAIT(sb, N) asm volatile("s_waitcnt vmcnt(%8)" : "+v"(sb[0]), "+v"(sb[1]), "+v"(sb[2]), "+v"(sb[3]), "+v"(sb[4]), "+v"(sb[5]), "+v"(sb[6]), "+v"(sb[7]) : "n"(N) : "memory")
; #define MU_G_LOAD(ga, kt) do { const PG8_LAS f32x4* gk_ = (const PG8_LAS f32x4*)(lds + GAIN_OFF) + 16 * (kt) + 2 * wid; const f32x4 ga_ = gk_[0], gb_ = gk_[1]; \
;         ga[0] = ga_[0]; ga[1] = ga_[1]; ga[2] = ga_[2]; ga[3] = ga_[3]; ga[4] = gb_[0]; ga[5] = gb_[1]; ga[6] = gb_[2]; ga[7] = gb_[3]; } while (0)
; #define MU_COMPUTE(buf) MU_COMPUTE_N(buf, NMU)
; #define MU_END(last) do { if (last) asm volatile("s_waitcnt vmcnt(0)" ::: "memory"); else asm volatile("s_waitcnt vmcnt(8)" ::: "memory"); \
;         asm volatile("s_waitcnt lgkmcnt(0)" ::: "memory"); __builtin_amdgcn_s_barrier(); asm volatile("" ::: "memory"); } while (0)
; template <int MODE>
; __device__ __forceinline__ void moe_unit(PG8_LAS unsigned char* lds, int e, int cb, int slot0  , int nv  , const bf16_t* A, const int* slot_tok,
;                                          const float* W0, const float* W1, bf16_t* OUT, const float* slot_rs  , const int* slot_dst) {
;     ...
;     for (int t = 0; t < nt; t += 2) {
;         if (t + 2 < nt) MU_B_WAIT(s1, 8); else MU_B_WAIT(s1, 0);
;         MU_G_LOAD(g0, t + 1); MU_B_WRITE(s1, 1, g0); __builtin_amdgcn_sched_barrier(0); MU_GLDS_A(1, t + 1); __builtin_amdgcn_sched_barrier(0);
;         if (t + 3 < nt) { MU_B_ISSUE(s1, t + 3); }
;         MU_COMPUTE(0);
;         MU_END(t + 3 >= nt);
;         if (t + 2 < nt) { MU_B_WAIT(s0, 8); MU_G_LOAD(g0, t + 2); MU_B_WRITE(s0, 0, g0); __builtin_amdgcn_sched_barrier(0); MU_GLDS_A(0, t + 2); __builtin_amdgcn_sched_barrier(0); }
;         if (t + 4 < nt) { MU_B_ISSUE(s0, t + 4); }
;         MU_COMPUTE(1);
;         MU_END(t + 4 >= nt);
	v_mul_f32_e32 v98, s12, v98
	v_mul_f32_e32 v99, s12, v99
	v_mul_f32_e32 v100, s13, v100
	v_mul_f32_e32 v101, s13, v101
	v_mul_f32_e32 v102, s14, v102
	v_mul_f32_e32 v103, s14, v103
	v_mul_f32_e32 v104, s15, v104
	v_mul_f32_e32 v105, s15, v105
	v_mul_f32_e32 v106, s16, v106
	v_mul_f32_e32 v107, s16, v107
	v_mul_f32_e32 v108, s17, v108
	v_mul_f32_e32 v109, s17, v109
	v_mul_f32_e32 v110, s18, v110
	v_mul_f32_e32 v111, s18, v111
	v_mul_f32_e32 v112, s19, v112
	v_mul_f32_e32 v113, s19, v113
	v_cvt_pk_bf16_f32 v158, v98, v100
	v_cvt_pk_bf16_f32 v159, v102, v104
	v_cvt_pk_bf16_f32 v160, v106, v108
	v_cvt_pk_bf16_f32 v161, v110, v112
	v_cvt_pk_bf16_f32 v162, v99, v101
	v_cvt_pk_bf16_f32 v163, v103, v105
	v_cvt_pk_bf16_f32 v164, v107, v109
	v_cvt_pk_bf16_f32 v165, v111, v113
	ds_write_b128 v1, v[158:161] offset:0
	ds_write_b128 v1, v[162:165] offset:128
	v_add_u32_e32 v91, s42, v135
	v_add_u32_e32 v93, s42, v137
	ds_read_b128 v[238:241], v139 offset:19456
	ds_read_b128 v[242:245], v139 offset:21504
	ds_read_b128 v[246:249], v139 offset:23552
	ds_read_b128 v[250:253], v139 offset:25600
	ds_read_b128 v[218:221], v91 offset:0
	ds_read_b128 v[222:225], v91 offset:2048
	ds_read_b128 v[226:229], v91 offset:4096
	ds_read_b128 v[230:233], v91 offset:6144
	ds_read_b128 v[234:237], v91 offset:8192
	s_add_i32 s47, s44, s6
	s_add_u32 s30, s30, 0x80
	s_addc_u32 s31, s31, 0
	s_waitcnt lgkmcnt(0)
	v_mfma_f32_16x16x32_bf16 v[78:81], v[238:241], v[218:221], v[78:81]
	v_mfma_f32_16x16x32_bf16 v[74:77], v[242:245], v[218:221], v[74:77]
	v_mfma_f32_16x16x32_bf16 v[70:73], v[246:249], v[218:221], v[70:73]
	v_mfma_f32_16x16x32_bf16 v[66:69], v[250:253], v[218:221], v[66:69]
	ds_read_b128 v[218:221], v93 offset:0
	ds_read_b128 v[142:145], v141 offset:19456
	s_mov_b32 m0, s47
	s_nop 0
	global_load_lds_dwordx4 v86, s[30:31]
	v_mfma_f32_16x16x32_bf16 v[62:65], v[238:241], v[222:225], v[62:65]
	v_mfma_f32_16x16x32_bf16 v[58:61], v[242:245], v[222:225], v[58:61]
	v_mfma_f32_16x16x32_bf16 v[54:57], v[246:249], v[222:225], v[54:57]
	v_mfma_f32_16x16x32_bf16 v[50:53], v[250:253], v[222:225], v[50:53]
	ds_read_b128 v[222:225], v93 offset:2048
	ds_read_b128 v[146:149], v141 offset:21504
	s_add_i32 m0, s47, 0x2000
	s_nop 0
	global_load_lds_dwordx4 v134, s[30:31]
	v_mfma_f32_16x16x32_bf16 v[46:49], v[238:241], v[226:229], v[46:49]
	v_mfma_f32_16x16x32_bf16 v[42:45], v[242:245], v[226:229], v[42:45]
	v_mfma_f32_16x16x32_bf16 v[38:41], v[246:249], v[226:229], v[38:41]
	v_mfma_f32_16x16x32_bf16 v[34:37], v[250:253], v[226:229], v[34:37]
	ds_read_b128 v[226:229], v93 offset:4096
	ds_read_b128 v[150:153], v141 offset:23552
	s_add_i32 m0, s47, 0x4000
	s_nop 0
	global_load_lds_dwordx4 v136, s[30:31]
	v_mfma_f32_16x16x32_bf16 v[18:21], v[238:241], v[230:233], v[18:21]
	v_mfma_f32_16x16x32_bf16 v[22:25], v[242:245], v[230:233], v[22:25]
	v_mfma_f32_16x16x32_bf16 v[26:29], v[246:249], v[230:233], v[26:29]
	v_mfma_f32_16x16x32_bf16 v[30:33], v[250:253], v[230:233], v[30:33]
	ds_read_b128 v[230:233], v93 offset:6144
	ds_read_b128 v[154:157], v141 offset:25600
	s_add_i32 m0, s47, 0x6000
	s_nop 0
	global_load_lds_dwordx4 v138, s[30:31]
	v_mfma_f32_16x16x32_bf16 v[2:5], v[238:241], v[234:237], v[2:5]
	v_mfma_f32_16x16x32_bf16 v[6:9], v[242:245], v[234:237], v[6:9]
	v_mfma_f32_16x16x32_bf16 v[10:13], v[246:249], v[234:237], v[10:13]
	v_mfma_f32_16x16x32_bf16 v[14:17], v[250:253], v[234:237], v[14:17]
	ds_read_b128 v[234:237], v93 offset:8192
	s_add_i32 m0, s47, 0x8000
	s_nop 0
	global_load_lds_dwordx4 v140, s[30:31]
	s_waitcnt lgkmcnt(0)
	s_load_dwordx8 s[20:27], s[28:29], 0x0
	s_add_u32 s28, s28, 0x100
	s_addc_u32 s29, s29, 0
	v_mfma_f32_16x16x32_bf16 v[78:81], v[142:145], v[218:221], v[78:81]
	v_mfma_f32_16x16x32_bf16 v[74:77], v[146:149], v[218:221], v[74:77]
	v_mfma_f32_16x16x32_bf16 v[70:73], v[150:153], v[218:221], v[70:73]
	v_mfma_f32_16x16x32_bf16 v[66:69], v[154:157], v[218:221], v[66:69]
	v_mfma_f32_16x16x32_bf16 v[62:65], v[142:145], v[222:225], v[62:65]
	v_mfma_f32_16x16x32_bf16 v[58:61], v[146:149], v[222:225], v[58:61]
	v_mfma_f32_16x16x32_bf16 v[54:57], v[150:153], v[222:225], v[54:57]
	v_mfma_f32_16x16x32_bf16 v[50:53], v[154:157], v[222:225], v[50:53]
	v_mfma_f32_16x16x32_bf16 v[46:49], v[142:145], v[226:229], v[46:49]
	v_mfma_f32_16x16x32_bf16 v[42:45], v[146:149], v[226:229], v[42:45]
	v_mfma_f32_16x16x32_bf16 v[38:41], v[150:153], v[226:229], v[38:41]
	v_mfma_f32_16x16x32_bf16 v[34:37], v[154:157], v[226:229], v[34:37]
	v_mfma_f32_16x16x32_bf16 v[18:21], v[142:145], v[230:233], v[18:21]
	v_mfma_f32_16x16x32_bf16 v[22:25], v[146:149], v[230:233], v[22:25]
	v_mfma_f32_16x16x32_bf16 v[26:29], v[150:153], v[230:233], v[26:29]
	v_mfma_f32_16x16x32_bf16 v[30:33], v[154:157], v[230:233], v[30:33]
	v_mfma_f32_16x16x32_bf16 v[2:5], v[142:145], v[234:237], v[2:5]
	v_mfma_f32_16x16x32_bf16 v[6:9], v[146:149], v[234:237], v[6:9]
	v_mfma_f32_16x16x32_bf16 v[10:13], v[150:153], v[234:237], v[10:13]
	v_mfma_f32_16x16x32_bf16 v[14:17], v[154:157], v[234:237], v[14:17]
	s_waitcnt vmcnt(13)
	s_mov_b32 s47, s42
	s_mov_b32 s42, s43
	s_mov_b32 s43, s44
	s_mov_b32 s44, s47
	s_waitcnt lgkmcnt(0)
	s_barrier
; #define MU_GLDS_A(buf, kt) do { _Pragma("unroll") for (int i = 0; i < NMU; ++i) \
;         __builtin_amdgcn_global_load_lds((const unsigned*)((const char*)A + aoff[i] + (size_t)(kt) * 128), (PG8_LAS unsigned*)(MU_SA(buf) + wid * 1024 + i * 8192), 16, 0, 0); } while (0)
; #define MU_B_ISSUE(sb, kt) do { const char* kb_ = Bb + (size_t)(kt) * (64 * (size_t)RB); _Pragma("unroll") for (int j = 0; j < 8; ++j) { const char* p_ = kb_ + (size_t)j * RB; \
;         asm volatile("global_load_dwordx2 %0, %1, off" : "=&v"(sb[j]) : "v"(p_) : "memory"); } } while (0)
; #define MU_B_WAIT(sb, N) asm volatile("s_waitcnt vmcnt(%8)" : "+v"(sb[0]), "+v"(sb[1]), "+v"(sb[2]), "+v"(sb[3]), "+v"(sb[4]), "+v"(sb[5]), "+v"(sb[6]), "+v"(sb[7]) : "n"(N) : "memory")
; #define MU_G_LOAD(ga, kt) do { const PG8_LAS f32x4* gk_ = (const PG8_LAS f32x4*)(lds + GAIN_OFF) + 16 * (kt) + 2 * wid; const f32x4 ga_ = gk_[0], gb_ = gk_[1]; \
;         ga[0] = ga_[0]; ga[1] = ga_[1]; ga[2] = ga_[2]; ga[3] = ga_[3]; ga[4] = gb_[0]; ga[5] = gb_[1]; ga[6] = gb_[2]; ga[7] = gb_[3]; } while (0)
; #define MU_COMPUTE(buf) MU_COMPUTE_N(buf, NMU)
; #define MU_END(last) do { if (last) asm volatile("s_waitcnt vmcnt(0)" ::: "memory"); else asm volatile("s_waitcnt vmcnt(8)" ::: "memory"); \
;         asm volatile("s_waitcnt lgkmcnt(0)" ::: "memory"); __builtin_amdgcn_s_barrier(); asm volatile("" ::: "memory"); } while (0)
; template <int MODE>
; __device__ __forceinline__ void moe_unit(PG8_LAS unsigned char* lds, int e, int cb, int slot0  , int nv  , const bf16_t* A, const int* slot_tok,
;                                          const float* W0, const float* W1, bf16_t* OUT, const float* slot_rs  , const int* slot_dst) {
;     ...
;     for (int t = 0; t < nt; t += 2) {
;         if (t + 2 < nt) MU_B_WAIT(s1, 8); else MU_B_WAIT(s1, 0);
;         MU_G_LOAD(g0, t + 1); MU_B_WRITE(s1, 1, g0); __builtin_amdgcn_sched_barrier(0); MU_GLDS_A(1, t + 1); __builtin_amdgcn_sched_barrier(0);
;         if (t + 3 < nt) { MU_B_ISSUE(s1, t + 3); }
;         MU_COMPUTE(0);
;         MU_END(t + 3 >= nt);
;         if (t + 2 < nt) { MU_B_WAIT(s0, 8); MU_G_LOAD(g0, t + 2); MU_B_WRITE(s0, 0, g0); __builtin_amdgcn_sched_barrier(0); MU_GLDS_A(0, t + 2); __builtin_amdgcn_sched_barrier(0); }
;         if (t + 4 < nt) { MU_B_ISSUE(s0, t + 4); }
;         MU_COMPUTE(1);
;         MU_END(t + 4 >= nt);
	v_mul_f32_e32 v114, s20, v114
	v_mul_f32_e32 v115, s20, v115
	v_mul_f32_e32 v116, s21, v116
	v_mul_f32_e32 v117, s21, v117
	v_mul_f32_e32 v118, s22, v118
	v_mul_f32_e32 v119, s22, v119
	v_mul_f32_e32 v120, s23, v120
	v_mul_f32_e32 v121, s23, v121
	v_mul_f32_e32 v122, s24, v122
	v_mul_f32_e32 v123, s24, v123
	v_mul_f32_e32 v124, s25, v124
	v_mul_f32_e32 v125, s25, v125
	v_mul_f32_e32 v126, s26, v126
	v_mul_f32_e32 v127, s26, v127
	v_mul_f32_e32 v128, s27, v128
	v_mul_f32_e32 v129, s27, v129
	v_cvt_pk_bf16_f32 v158, v114, v116
	v_cvt_pk_bf16_f32 v159, v118, v120
	v_cvt_pk_bf16_f32 v160, v122, v124
	v_cvt_pk_bf16_f32 v161, v126, v128
	v_cvt_pk_bf16_f32 v162, v115, v117
	v_cvt_pk_bf16_f32 v163, v119, v121
	v_cvt_pk_bf16_f32 v164, v123, v125
	v_cvt_pk_bf16_f32 v165, v127, v129
	ds_write_b128 v1, v[158:161] offset:19456
	ds_write_b128 v1, v[162:165] offset:19584
	v_add_u32_e32 v91, s42, v135
	v_add_u32_e32 v93, s42, v137
	ds_read_b128 v[238:241], v139 offset:0
	ds_read_b128 v[242:245], v139 offset:2048
	ds_read_b128 v[246:249], v139 offset:4096
	ds_read_b128 v[250:253], v139 offset:6144
	ds_read_b128 v[218:221], v91 offset:0
	ds_read_b128 v[222:225], v91 offset:2048
	ds_read_b128 v[226:229], v91 offset:4096
	ds_read_b128 v[230:233], v91 offset:6144
	ds_read_b128 v[234:237], v91 offset:8192
	s_add_i32 s47, s44, s6
	s_add_u32 s30, s30, 0x80
	s_addc_u32 s31, s31, 0
	s_waitcnt lgkmcnt(0)
	v_mfma_f32_16x16x32_bf16 v[78:81], v[238:241], v[218:221], v[78:81]
	v_mfma_f32_16x16x32_bf16 v[74:77], v[242:245], v[218:221], v[74:77]
	v_mfma_f32_16x16x32_bf16 v[70:73], v[246:249], v[218:221], v[70:73]
	v_mfma_f32_16x16x32_bf16 v[66:69], v[250:253], v[218:221], v[66:69]
	ds_read_b128 v[218:221], v93 offset:0
	ds_read_b128 v[142:145], v141 offset:0
	s_mov_b32 m0, s47
	s_nop 0
	global_load_lds_dwordx4 v86, s[30:31]
	v_mfma_f32_16x16x32_bf16 v[62:65], v[238:241], v[222:225], v[62:65]
	v_mfma_f32_16x16x32_bf16 v[58:61], v[242:245], v[222:225], v[58:61]
	v_mfma_f32_16x16x32_bf16 v[54:57], v[246:249], v[222:225], v[54:57]
	v_mfma_f32_16x16x32_bf16 v[50:53], v[250:253], v[222:225], v[50:53]
	ds_read_b128 v[222:225], v93 offset:2048
	ds_read_b128 v[146:149], v141 offset:2048
	s_add_i32 m0, s47, 0x2000
	s_nop 0
	global_load_lds_dwordx4 v134, s[30:31]
	v_mfma_f32_16x16x32_bf16 v[46:49], v[238:241], v[226:229], v[46:49]
	v_mfma_f32_16x16x32_bf16 v[42:45], v[242:245], v[226:229], v[42:45]
	v_mfma_f32_16x16x32_bf16 v[38:41], v[246:249], v[226:229], v[38:41]
	v_mfma_f32_16x16x32_bf16 v[34:37], v[250:253], v[226:229], v[34:37]
	ds_read_b128 v[226:229], v93 offset:4096
	ds_read_b128 v[150:153], v141 offset:4096
	s_add_i32 m0, s47, 0x4000
	s_nop 0
	global_load_lds_dwordx4 v136, s[30:31]
	v_mfma_f32_16x16x32_bf16 v[18:21], v[238:241], v[230:233], v[18:21]
	v_mfma_f32_16x16x32_bf16 v[22:25], v[242:245], v[230:233], v[22:25]
	v_mfma_f32_16x16x32_bf16 v[26:29], v[246:249], v[230:233], v[26:29]
	v_mfma_f32_16x16x32_bf16 v[30:33], v[250:253], v[230:233], v[30:33]
	ds_read_b128 v[230:233], v93 offset:6144
	ds_read_b128 v[154:157], v141 offset:6144
	s_add_i32 m0, s47, 0x6000
	s_nop 0
	global_load_lds_dwordx4 v138, s[30:31]
	v_mfma_f32_16x16x32_bf16 v[2:5], v[238:241], v[234:237], v[2:5]
	v_mfma_f32_16x16x32_bf16 v[6:9], v[242:245], v[234:237], v[6:9]
	v_mfma_f32_16x16x32_bf16 v[10:13], v[246:249], v[234:237], v[10:13]
	v_mfma_f32_16x16x32_bf16 v[14:17], v[250:253], v[234:237], v[14:17]
	ds_read_b128 v[234:237], v93 offset:8192
	s_add_i32 m0, s47, 0x8000
	s_nop 0
	global_load_lds_dwordx4 v140, s[30:31]
	s_waitcnt lgkmcnt(0)
	s_load_dwordx8 s[12:19], s[28:29], 0x0
	s_add_u32 s28, s28, 0x100
	s_addc_u32 s29, s29, 0
	v_mfma_f32_16x16x32_bf16 v[78:81], v[142:145], v[218:221], v[78:81]
	v_mfma_f32_16x16x32_bf16 v[74:77], v[146:149], v[218:221], v[74:77]
	v_mfma_f32_16x16x32_bf16 v[70:73], v[150:153], v[218:221], v[70:73]
	v_mfma_f32_16x16x32_bf16 v[66:69], v[154:157], v[218:221], v[66:69]
	v_mfma_f32_16x16x32_bf16 v[62:65], v[142:145], v[222:225], v[62:65]
	v_mfma_f32_16x16x32_bf16 v[58:61], v[146:149], v[222:225], v[58:61]
	v_mfma_f32_16x16x32_bf16 v[54:57], v[150:153], v[222:225], v[54:57]
	v_mfma_f32_16x16x32_bf16 v[50:53], v[154:157], v[222:225], v[50:53]
	v_mfma_f32_16x16x32_bf16 v[46:49], v[142:145], v[226:229], v[46:49]
	v_mfma_f32_16x16x32_bf16 v[42:45], v[146:149], v[226:229], v[42:45]
	v_mfma_f32_16x16x32_bf16 v[38:41], v[150:153], v[226:229], v[38:41]
	v_mfma_f32_16x16x32_bf16 v[34:37], v[154:157], v[226:229], v[34:37]
	v_mfma_f32_16x16x32_bf16 v[18:21], v[142:145], v[230:233], v[18:21]
	v_mfma_f32_16x16x32_bf16 v[22:25], v[146:149], v[230:233], v[22:25]
	v_mfma_f32_16x16x32_bf16 v[26:29], v[150:153], v[230:233], v[26:29]
	v_mfma_f32_16x16x32_bf16 v[30:33], v[154:157], v[230:233], v[30:33]
	v_mfma_f32_16x16x32_bf16 v[2:5], v[142:145], v[234:237], v[2:5]
	v_mfma_f32_16x16x32_bf16 v[6:9], v[146:149], v[234:237], v[6:9]
	v_mfma_f32_16x16x32_bf16 v[10:13], v[150:153], v[234:237], v[10:13]
	v_mfma_f32_16x16x32_bf16 v[14:17], v[154:157], v[234:237], v[14:17]
	s_waitcnt vmcnt(5)
	s_mov_b32 s47, s42
	s_mov_b32 s42, s43
	s_mov_b32 s43, s44
	s_mov_b32 s44, s47
	s_waitcnt lgkmcnt(0)
	s_barrier
; #define MU_GLDS_A(buf, kt) do { _Pragma("unroll") for (int i = 0; i < NMU; ++i) \
;         __builtin_amdgcn_global_load_lds((const unsigned*)((const char*)A + aoff[i] + (size_t)(kt) * 128), (PG8_LAS unsigned*)(MU_SA(buf) + wid * 1024 + i * 8192), 16, 0, 0); } while (0)
; #define MU_B_ISSUE(sb, kt) do { const char* kb_ = Bb + (size_t)(kt) * (64 * (size_t)RB); _Pragma("unroll") for (int j = 0; j < 8; ++j) { const char* p_ = kb_ + (size_t)j * RB; \
;         asm volatile("global_load_dwordx2 %0, %1, off" : "=&v"(sb[j]) : "v"(p_) : "memory"); } } while (0)
; #define MU_B_WAIT(sb, N) asm volatile("s_waitcnt vmcnt(%8)" : "+v"(sb[0]), "+v"(sb[1]), "+v"(sb[2]), "+v"(sb[3]), "+v"(sb[4]), "+v"(sb[5]), "+v"(sb[6]), "+v"(sb[7]) : "n"(N) : "memory")
; #define MU_G_LOAD(ga, kt) do { const PG8_LAS f32x4* gk_ = (const PG8_LAS f32x4*)(lds + GAIN_OFF) + 16 * (kt) + 2 * wid; const f32x4 ga_ = gk_[0], gb_ = gk_[1]; \
;         ga[0] = ga_[0]; ga[1] = ga_[1]; ga[2] = ga_[2]; ga[3] = ga_[3]; ga[4] = gb_[0]; ga[5] = gb_[1]; ga[6] = gb_[2]; ga[7] = gb_[3]; } while (0)
; #define MU_COMPUTE(buf) MU_COMPUTE_N(buf, NMU)
; #define MU_END(last) do { if (last) asm volatile("s_waitcnt vmcnt(0)" ::: "memory"); else asm volatile("s_waitcnt vmcnt(8)" ::: "memory"); \
;         asm volatile("s_waitcnt lgkmcnt(0)" ::: "memory"); __builtin_amdgcn_s_barrier(); asm volatile("" ::: "memory"); } while (0)
; template <int MODE>
; __device__ __forceinline__ void moe_unit(PG8_LAS unsigned char* lds, int e, int cb, int slot0  , int nv  , const bf16_t* A, const int* slot_tok,
;                                          const float* W0, const float* W1, bf16_t* OUT, const float* slot_rs  , const int* slot_dst) {
;     ...
;     for (int t = 0; t < nt; t += 2) {
;         if (t + 2 < nt) MU_B_WAIT(s1, 8); else MU_B_WAIT(s1, 0);
;         MU_G_LOAD(g0, t + 1); MU_B_WRITE(s1, 1, g0); __builtin_amdgcn_sched_barrier(0); MU_GLDS_A(1, t + 1); __builtin_amdgcn_sched_barrier(0);
;         if (t + 3 < nt) { MU_B_ISSUE(s1, t + 3); }
;         MU_COMPUTE(0);
;         MU_END(t + 3 >= nt);
;         if (t + 2 < nt) { MU_B_WAIT(s0, 8); MU_G_LOAD(g0, t + 2); MU_B_WRITE(s0, 0, g0); __builtin_amdgcn_sched_barrier(0); MU_GLDS_A(0, t + 2); __builtin_amdgcn_sched_barrier(0); }
;         if (t + 4 < nt) { MU_B_ISSUE(s0, t + 4); }
;         MU_COMPUTE(1);
;         MU_END(t + 4 >= nt);
	v_mul_f32_e32 v186, s12, v186
	v_mul_f32_e32 v187, s12, v187
	v_mul_f32_e32 v188, s13, v188
	v_mul_f32_e32 v189, s13, v189
	v_mul_f32_e32 v190, s14, v190
	v_mul_f32_e32 v191, s14, v191
	v_mul_f32_e32 v192, s15, v192
	v_mul_f32_e32 v193, s15, v193
	v_mul_f32_e32 v194, s16, v194
	v_mul_f32_e32 v195, s16, v195
	v_mul_f32_e32 v196, s17, v196
	v_mul_f32_e32 v197, s17, v197
	v_mul_f32_e32 v198, s18, v198
	v_mul_f32_e32 v199, s18, v199
	v_mul_f32_e32 v200, s19, v200
	v_mul_f32_e32 v201, s19, v201
	v_cvt_pk_bf16_f32 v158, v186, v188
	v_cvt_pk_bf16_f32 v159, v190, v192
	v_cvt_pk_bf16_f32 v160, v194, v196
	v_cvt_pk_bf16_f32 v161, v198, v200
	v_cvt_pk_bf16_f32 v162, v187, v189
	v_cvt_pk_bf16_f32 v163, v191, v193
	v_cvt_pk_bf16_f32 v164, v195, v197
	v_cvt_pk_bf16_f32 v165, v199, v201
	ds_write_b128 v1, v[158:161] offset:0
	ds_write_b128 v1, v[162:165] offset:128
	v_add_u32_e32 v91, s42, v135
	v_add_u32_e32 v93, s42, v137
	ds_read_b128 v[238:241], v139 offset:19456
	ds_read_b128 v[242:245], v139 offset:21504
	ds_read_b128 v[246:249], v139 offset:23552
	ds_read_b128 v[250:253], v139 offset:25600
	ds_read_b128 v[218:221], v91 offset:0
	ds_read_b128 v[222:225], v91 offset:2048
	ds_read_b128 v[226:229], v91 offset:4096
	ds_read_b128 v[230:233], v91 offset:6144
	ds_read_b128 v[234:237], v91 offset:8192
	s_add_i32 s47, s44, s6
	s_add_u32 s30, s30, 0x80
	s_addc_u32 s31, s31, 0
	s_waitcnt lgkmcnt(0)
	v_mfma_f32_16x16x32_bf16 v[78:81], v[238:241], v[218:221], v[78:81]
	v_mfma_f32_16x16x32_bf16 v[74:77], v[242:245], v[218:221], v[74:77]
	v_mfma_f32_16x16x32_bf16 v[70:73], v[246:249], v[218:221], v[70:73]
	v_mfma_f32_16x16x32_bf16 v[66:69], v[250:253], v[218:221], v[66:69]
	ds_read_b128 v[218:221], v93 offset:0
	ds_read_b128 v[142:145], v141 offset:19456
	s_mov_b32 m0, s47
	s_nop 0
	global_load_lds_dwordx4 v86, s[30:31]
	v_mfma_f32_16x16x32_bf16 v[62:65], v[238:241], v[222:225], v[62:65]
	v_mfma_f32_16x16x32_bf16 v[58:61], v[242:245], v[222:225], v[58:61]
	v_mfma_f32_16x16x32_bf16 v[54:57], v[246:249], v[222:225], v[54:57]
	v_mfma_f32_16x16x32_bf16 v[50:53], v[250:253], v[222:225], v[50:53]
	ds_read_b128 v[222:225], v93 offset:2048
	ds_read_b128 v[146:149], v141 offset:21504
	s_add_i32 m0, s47, 0x2000
	s_nop 0
	global_load_lds_dwordx4 v134, s[30:31]
	v_mfma_f32_16x16x32_bf16 v[46:49], v[238:241], v[226:229], v[46:49]
	v_mfma_f32_16x16x32_bf16 v[42:45], v[242:245], v[226:229], v[42:45]
	v_mfma_f32_16x16x32_bf16 v[38:41], v[246:249], v[226:229], v[38:41]
	v_mfma_f32_16x16x32_bf16 v[34:37], v[250:253], v[226:229], v[34:37]
	ds_read_b128 v[226:229], v93 offset:4096
	ds_read_b128 v[150:153], v141 offset:23552
	s_add_i32 m0, s47, 0x4000
	s_nop 0
	global_load_lds_dwordx4 v136, s[30:31]
	v_mfma_f32_16x16x32_bf16 v[18:21], v[238:241], v[230:233], v[18:21]
	v_mfma_f32_16x16x32_bf16 v[22:25], v[242:245], v[230:233], v[22:25]
	v_mfma_f32_16x16x32_bf16 v[26:29], v[246:249], v[230:233], v[26:29]
	v_mfma_f32_16x16x32_bf16 v[30:33], v[250:253], v[230:233], v[30:33]
	ds_read_b128 v[230:233], v93 offset:6144
	ds_read_b128 v[154:157], v141 offset:25600
	s_add_i32 m0, s47, 0x6000
	s_nop 0
	global_load_lds_dwordx4 v138, s[30:31]
	v_mfma_f32_16x16x32_bf16 v[2:5], v[238:241], v[234:237], v[2:5]
	v_mfma_f32_16x16x32_bf16 v[6:9], v[242:245], v[234:237], v[6:9]
	v_mfma_f32_16x16x32_bf16 v[10:13], v[246:249], v[234:237], v[10:13]
	v_mfma_f32_16x16x32_bf16 v[14:17], v[250:253], v[234:237], v[14:17]
	ds_read_b128 v[234:237], v93 offset:8192
	s_add_i32 m0, s47, 0x8000
	s_nop 0
	global_load_lds_dwordx4 v140, s[30:31]
	s_waitcnt lgkmcnt(0)
	s_load_dwordx8 s[20:27], s[28:29], 0x0
	s_add_u32 s28, s28, 0x100
	s_addc_u32 s29, s29, 0
	v_mfma_f32_16x16x32_bf16 v[78:81], v[142:145], v[218:221], v[78:81]
	v_mfma_f32_16x16x32_bf16 v[74:77], v[146:149], v[218:221], v[74:77]
	v_mfma_f32_16x16x32_bf16 v[70:73], v[150:153], v[218:221], v[70:73]
	v_mfma_f32_16x16x32_bf16 v[66:69], v[154:157], v[218:221], v[66:69]
	v_mfma_f32_16x16x32_bf16 v[62:65], v[142:145], v[222:225], v[62:65]
	v_mfma_f32_16x16x32_bf16 v[58:61], v[146:149], v[222:225], v[58:61]
	v_mfma_f32_16x16x32_bf16 v[54:57], v[150:153], v[222:225], v[54:57]
	v_mfma_f32_16x16x32_bf16 v[50:53], v[154:157], v[222:225], v[50:53]
	v_mfma_f32_16x16x32_bf16 v[46:49], v[142:145], v[226:229], v[46:49]
	v_mfma_f32_16x16x32_bf16 v[42:45], v[146:149], v[226:229], v[42:45]
	v_mfma_f32_16x16x32_bf16 v[38:41], v[150:153], v[226:229], v[38:41]
	v_mfma_f32_16x16x32_bf16 v[34:37], v[154:157], v[226:229], v[34:37]
	v_mfma_f32_16x16x32_bf16 v[18:21], v[142:145], v[230:233], v[18:21]
	v_mfma_f32_16x16x32_bf16 v[22:25], v[146:149], v[230:233], v[22:25]
	v_mfma_f32_16x16x32_bf16 v[26:29], v[150:153], v[230:233], v[26:29]
	v_mfma_f32_16x16x32_bf16 v[30:33], v[154:157], v[230:233], v[30:33]
	v_mfma_f32_16x16x32_bf16 v[2:5], v[142:145], v[234:237], v[2:5]
	v_mfma_f32_16x16x32_bf16 v[6:9], v[146:149], v[234:237], v[6:9]
	v_mfma_f32_16x16x32_bf16 v[10:13], v[150:153], v[234:237], v[10:13]
	v_mfma_f32_16x16x32_bf16 v[14:17], v[154:157], v[234:237], v[14:17]
	s_waitcnt vmcnt(5)
	s_mov_b32 s47, s42
	s_mov_b32 s42, s43
	s_mov_b32 s43, s44
	s_mov_b32 s44, s47
	s_waitcnt lgkmcnt(0)
	s_barrier
; #define MU_GLDS_A(buf, kt) do { _Pragma("unroll") for (int i = 0; i < NMU; ++i) \
;         __builtin_amdgcn_global_load_lds((const unsigned*)((const char*)A + aoff[i] + (size_t)(kt) * 128), (PG8_LAS unsigned*)(MU_SA(buf) + wid * 1024 + i * 8192), 16, 0, 0); } while (0)
; #define MU_B_ISSUE(sb, kt) do { const char* kb_ = Bb + (size_t)(kt) * (64 * (size_t)RB); _Pragma("unroll") for (int j = 0; j < 8; ++j) { const char* p_ = kb_ + (size_t)j * RB; \
;         asm volatile("global_load_dwordx2 %0, %1, off" : "=&v"(sb[j]) : "v"(p_) : "memory"); } } while (0)
; #define MU_B_WAIT(sb, N) asm volatile("s_waitcnt vmcnt(%8)" : "+v"(sb[0]), "+v"(sb[1]), "+v"(sb[2]), "+v"(sb[3]), "+v"(sb[4]), "+v"(sb[5]), "+v"(sb[6]), "+v"(sb[7]) : "n"(N) : "memory")
; #define MU_G_LOAD(ga, kt) do { const PG8_LAS f32x4* gk_ = (const PG8_LAS f32x4*)(lds + GAIN_OFF) + 16 * (kt) + 2 * wid; const f32x4 ga_ = gk_[0], gb_ = gk_[1]; \
;         ga[0] = ga_[0]; ga[1] = ga_[1]; ga[2] = ga_[2]; ga[3] = ga_[3]; ga[4] = gb_[0]; ga[5] = gb_[1]; ga[6] = gb_[2]; ga[7] = gb_[3]; } while (0)
; #define MU_COMPUTE(buf) MU_COMPUTE_N(buf, NMU)
; #define MU_END(last) do { if (last) asm volatile("s_waitcnt vmcnt(0)" ::: "memory"); else asm volatile("s_waitcnt vmcnt(8)" ::: "memory"); \
;         asm volatile("s_waitcnt lgkmcnt(0)" ::: "memory"); __builtin_amdgcn_s_barrier(); asm volatile("" ::: "memory"); } while (0)
; template <int MODE>
; __device__ __forceinline__ void moe_unit(PG8_LAS unsigned char* lds, int e, int cb, int slot0  , int nv  , const bf16_t* A, const int* slot_tok,
;                                          const float* W0, const float* W1, bf16_t* OUT, const float* slot_rs  , const int* slot_dst) {
;     ...
;     for (int t = 0; t < nt; t += 2) {
;         if (t + 2 < nt) MU_B_WAIT(s1, 8); else MU_B_WAIT(s1, 0);
;         MU_G_LOAD(g0, t + 1); MU_B_WRITE(s1, 1, g0); __builtin_amdgcn_sched_barrier(0); MU_GLDS_A(1, t + 1); __builtin_amdgcn_sched_barrier(0);
;         if (t + 3 < nt) { MU_B_ISSUE(s1, t + 3); }
;         MU_COMPUTE(0);
;         MU_END(t + 3 >= nt);
;         if (t + 2 < nt) { MU_B_WAIT(s0, 8); MU_G_LOAD(g0, t + 2); MU_B_WRITE(s0, 0, g0); __builtin_amdgcn_sched_barrier(0); MU_GLDS_A(0, t + 2); __builtin_amdgcn_sched_barrier(0); }
;         if (t + 4 < nt) { MU_B_ISSUE(s0, t + 4); }
;         MU_COMPUTE(1);
;         MU_END(t + 4 >= nt);
	v_mul_f32_e32 v202, s20, v202
	v_mul_f32_e32 v203, s20, v203
	v_mul_f32_e32 v204, s21, v204
	v_mul_f32_e32 v205, s21, v205
	v_mul_f32_e32 v206, s22, v206
	v_mul_f32_e32 v207, s22, v207
	v_mul_f32_e32 v208, s23, v208
	v_mul_f32_e32 v209, s23, v209
	v_mul_f32_e32 v210, s24, v210
	v_mul_f32_e32 v211, s24, v211
	v_mul_f32_e32 v212, s25, v212
	v_mul_f32_e32 v213, s25, v213
	v_mul_f32_e32 v214, s26, v214
	v_mul_f32_e32 v215, s26, v215
	v_mul_f32_e32 v216, s27, v216
	v_mul_f32_e32 v217, s27, v217
	v_cvt_pk_bf16_f32 v158, v202, v204
	v_cvt_pk_bf16_f32 v159, v206, v208
	v_cvt_pk_bf16_f32 v160, v210, v212
	v_cvt_pk_bf16_f32 v161, v214, v216
	v_cvt_pk_bf16_f32 v162, v203, v205
	v_cvt_pk_bf16_f32 v163, v207, v209
	v_cvt_pk_bf16_f32 v164, v211, v213
	v_cvt_pk_bf16_f32 v165, v215, v217
	ds_write_b128 v1, v[158:161] offset:19456
	ds_write_b128 v1, v[162:165] offset:19584
	v_add_u32_e32 v91, s42, v135
	v_add_u32_e32 v93, s42, v137
	ds_read_b128 v[238:241], v139 offset:0
	ds_read_b128 v[242:245], v139 offset:2048
	ds_read_b128 v[246:249], v139 offset:4096
	ds_read_b128 v[250:253], v139 offset:6144
	ds_read_b128 v[218:221], v91 offset:0
	ds_read_b128 v[222:225], v91 offset:2048
	ds_read_b128 v[226:229], v91 offset:4096
	ds_read_b128 v[230:233], v91 offset:6144
	ds_read_b128 v[234:237], v91 offset:8192
	s_waitcnt lgkmcnt(0)
	v_mfma_f32_16x16x32_bf16 v[78:81], v[238:241], v[218:221], v[78:81]
	v_mfma_f32_16x16x32_bf16 v[74:77], v[242:245], v[218:221], v[74:77]
	v_mfma_f32_16x16x32_bf16 v[70:73], v[246:249], v[218:221], v[70:73]
	v_mfma_f32_16x16x32_bf16 v[66:69], v[250:253], v[218:221], v[66:69]
	ds_read_b128 v[218:221], v93 offset:0
	ds_read_b128 v[142:145], v141 offset:0
	v_mfma_f32_16x16x32_bf16 v[62:65], v[238:241], v[222:225], v[62:65]
	v_mfma_f32_16x16x32_bf16 v[58:61], v[242:245], v[222:225], v[58:61]
	v_mfma_f32_16x16x32_bf16 v[54:57], v[246:249], v[222:225], v[54:57]
	v_mfma_f32_16x16x32_bf16 v[50:53], v[250:253], v[222:225], v[50:53]
	ds_read_b128 v[222:225], v93 offset:2048
	ds_read_b128 v[146:149], v141 offset:2048
	v_mfma_f32_16x16x32_bf16 v[46:49], v[238:241], v[226:229], v[46:49]
	v_mfma_f32_16x16x32_bf16 v[42:45], v[242:245], v[226:229], v[42:45]
	v_mfma_f32_16x16x32_bf16 v[38:41], v[246:249], v[226:229], v[38:41]
	v_mfma_f32_16x16x32_bf16 v[34:37], v[250:253], v[226:229], v[34:37]
	ds_read_b128 v[226:229], v93 offset:4096
	ds_read_b128 v[150:153], v141 offset:4096
	v_mfma_f32_16x16x32_bf16 v[18:21], v[238:241], v[230:233], v[18:21]
	v_mfma_f32_16x16x32_bf16 v[22:25], v[242:245], v[230:233], v[22:25]
	v_mfma_f32_16x16x32_bf16 v[26:29], v[246:249], v[230:233], v[26:29]
	v_mfma_f32_16x16x32_bf16 v[30:33], v[250:253], v[230:233], v[30:33]
	ds_read_b128 v[230:233], v93 offset:6144
	ds_read_b128 v[154:157], v141 offset:6144
	v_mfma_f32_16x16x32_bf16 v[2:5], v[238:241], v[234:237], v[2:5]
	v_mfma_f32_16x16x32_bf16 v[6:9], v[242:245], v[234:237], v[6:9]
	v_mfma_f32_16x16x32_bf16 v[10:13], v[246:249], v[234:237], v[10:13]
	v_mfma_f32_16x16x32_bf16 v[14:17], v[250:253], v[234:237], v[14:17]
	ds_read_b128 v[234:237], v93 offset:8192
	s_waitcnt lgkmcnt(0)
	v_mfma_f32_16x16x32_bf16 v[78:81], v[142:145], v[218:221], v[78:81]
	v_mfma_f32_16x16x32_bf16 v[74:77], v[146:149], v[218:221], v[74:77]
	v_mfma_f32_16x16x32_bf16 v[70:73], v[150:153], v[218:221], v[70:73]
	v_mfma_f32_16x16x32_bf16 v[66:69], v[154:157], v[218:221], v[66:69]
	v_mfma_f32_16x16x32_bf16 v[62:65], v[142:145], v[222:225], v[62:65]
	v_mfma_f32_16x16x32_bf16 v[58:61], v[146:149], v[222:225], v[58:61]
	v_mfma_f32_16x16x32_bf16 v[54:57], v[150:153], v[222:225], v[54:57]
	v_mfma_f32_16x16x32_bf16 v[50:53], v[154:157], v[222:225], v[50:53]
	v_mfma_f32_16x16x32_bf16 v[46:49], v[142:145], v[226:229], v[46:49]
	v_mfma_f32_16x16x32_bf16 v[42:45], v[146:149], v[226:229], v[42:45]
	v_mfma_f32_16x16x32_bf16 v[38:41], v[150:153], v[226:229], v[38:41]
	v_mfma_f32_16x16x32_bf16 v[34:37], v[154:157], v[226:229], v[34:37]
	v_mfma_f32_16x16x32_bf16 v[18:21], v[142:145], v[230:233], v[18:21]
	v_mfma_f32_16x16x32_bf16 v[22:25], v[146:149], v[230:233], v[22:25]
	v_mfma_f32_16x16x32_bf16 v[26:29], v[150:153], v[230:233], v[26:29]
	v_mfma_f32_16x16x32_bf16 v[30:33], v[154:157], v[230:233], v[30:33]
	v_mfma_f32_16x16x32_bf16 v[2:5], v[142:145], v[234:237], v[2:5]
	v_mfma_f32_16x16x32_bf16 v[6:9], v[146:149], v[234:237], v[6:9]
	v_mfma_f32_16x16x32_bf16 v[10:13], v[150:153], v[234:237], v[10:13]
	v_mfma_f32_16x16x32_bf16 v[14:17], v[154:157], v[234:237], v[14:17]
	s_waitcnt vmcnt(0)
	s_mov_b32 s47, s42
	s_mov_b32 s42, s43
	s_mov_b32 s43, s44
	s_mov_b32 s44, s47
	s_waitcnt lgkmcnt(0)
	s_barrier
; #define MU_COMPUTE(buf) MU_COMPUTE_N(buf, NMU)
; #define MU_END(last) do { if (last) asm volatile("s_waitcnt vmcnt(0)" ::: "memory"); else asm volatile("s_waitcnt vmcnt(8)" ::: "memory"); \
;         asm volatile("s_waitcnt lgkmcnt(0)" ::: "memory"); __builtin_amdgcn_s_barrier(); asm volatile("" ::: "memory"); } while (0)
; template <int MODE>
; __device__ __forceinline__ void moe_unit(PG8_LAS unsigned char* lds, int e, int cb, int slot0  , int nv  , const bf16_t* A, const int* slot_tok,
;                                          const float* W0, const float* W1, bf16_t* OUT, const float* slot_rs  , const int* slot_dst) {
;     ...
;         MU_COMPUTE(1);
;         MU_END(t + 4 >= nt);
	v_add_u32_e32 v91, s42, v135
	v_add_u32_e32 v93, s42, v137
	ds_read_b128 v[238:241], v139 offset:19456
	ds_read_b128 v[242:245], v139 offset:21504
	ds_read_b128 v[246:249], v139 offset:23552
	ds_read_b128 v[250:253], v139 offset:25600
	ds_read_b128 v[218:221], v91 offset:0
	ds_read_b128 v[222:225], v91 offset:2048
	ds_read_b128 v[226:229], v91 offset:4096
	ds_read_b128 v[230:233], v91 offset:6144
	ds_read_b128 v[234:237], v91 offset:8192
	s_waitcnt lgkmcnt(0)
	v_mfma_f32_16x16x32_bf16 v[78:81], v[238:241], v[218:221], v[78:81]
	v_mfma_f32_16x16x32_bf16 v[74:77], v[242:245], v[218:221], v[74:77]
	v_mfma_f32_16x16x32_bf16 v[70:73], v[246:249], v[218:221], v[70:73]
	v_mfma_f32_16x16x32_bf16 v[66:69], v[250:253], v[218:221], v[66:69]
	ds_read_b128 v[218:221], v93 offset:0
	ds_read_b128 v[142:145], v141 offset:19456
	v_mfma_f32_16x16x32_bf16 v[62:65], v[238:241], v[222:225], v[62:65]
	v_mfma_f32_16x16x32_bf16 v[58:61], v[242:245], v[222:225], v[58:61]
	v_mfma_f32_16x16x32_bf16 v[54:57], v[246:249], v[222:225], v[54:57]
	v_mfma_f32_16x16x32_bf16 v[50:53], v[250:253], v[222:225], v[50:53]
	ds_read_b128 v[222:225], v93 offset:2048
	ds_read_b128 v[146:149], v141 offset:21504
	v_mfma_f32_16x16x32_bf16 v[46:49], v[238:241], v[226:229], v[46:49]
	v_mfma_f32_16x16x32_bf16 v[42:45], v[242:245], v[226:229], v[42:45]
	v_mfma_f32_16x16x32_bf16 v[38:41], v[246:249], v[226:229], v[38:41]
	v_mfma_f32_16x16x32_bf16 v[34:37], v[250:253], v[226:229], v[34:37]
	ds_read_b128 v[226:229], v93 offset:4096
	ds_read_b128 v[150:153], v141 offset:23552
	v_mfma_f32_16x16x32_bf16 v[18:21], v[238:241], v[230:233], v[18:21]
	v_mfma_f32_16x16x32_bf16 v[22:25], v[242:245], v[230:233], v[22:25]
	v_mfma_f32_16x16x32_bf16 v[26:29], v[246:249], v[230:233], v[26:29]
	v_mfma_f32_16x16x32_bf16 v[30:33], v[250:253], v[230:233], v[30:33]
	ds_read_b128 v[230:233], v93 offset:6144
	ds_read_b128 v[154:157], v141 offset:25600
	v_mfma_f32_16x16x32_bf16 v[2:5], v[238:241], v[234:237], v[2:5]
	v_mfma_f32_16x16x32_bf16 v[6:9], v[242:245], v[234:237], v[6:9]
	v_mfma_f32_16x16x32_bf16 v[10:13], v[246:249], v[234:237], v[10:13]
	v_mfma_f32_16x16x32_bf16 v[14:17], v[250:253], v[234:237], v[14:17]
	ds_read_b128 v[234:237], v93 offset:8192
	s_waitcnt lgkmcnt(0)
	v_mfma_f32_16x16x32_bf16 v[78:81], v[142:145], v[218:221], v[78:81]
	v_mfma_f32_16x16x32_bf16 v[74:77], v[146:149], v[218:221], v[74:77]
	v_mfma_f32_16x16x32_bf16 v[70:73], v[150:153], v[218:221], v[70:73]
	v_mfma_f32_16x16x32_bf16 v[66:69], v[154:157], v[218:221], v[66:69]
	v_mfma_f32_16x16x32_bf16 v[62:65], v[142:145], v[222:225], v[62:65]
	v_mfma_f32_16x16x32_bf16 v[58:61], v[146:149], v[222:225], v[58:61]
	v_mfma_f32_16x16x32_bf16 v[54:57], v[150:153], v[222:225], v[54:57]
	v_mfma_f32_16x16x32_bf16 v[50:53], v[154:157], v[222:225], v[50:53]
	v_mfma_f32_16x16x32_bf16 v[46:49], v[142:145], v[226:229], v[46:49]
	v_mfma_f32_16x16x32_bf16 v[42:45], v[146:149], v[226:229], v[42:45]
	v_mfma_f32_16x16x32_bf16 v[38:41], v[150:153], v[226:229], v[38:41]
	v_mfma_f32_16x16x32_bf16 v[34:37], v[154:157], v[226:229], v[34:37]
	v_mfma_f32_16x16x32_bf16 v[18:21], v[142:145], v[230:233], v[18:21]
	v_mfma_f32_16x16x32_bf16 v[22:25], v[146:149], v[230:233], v[22:25]
	v_mfma_f32_16x16x32_bf16 v[26:29], v[150:153], v[230:233], v[26:29]
	v_mfma_f32_16x16x32_bf16 v[30:33], v[154:157], v[230:233], v[30:33]
	v_mfma_f32_16x16x32_bf16 v[2:5], v[142:145], v[234:237], v[2:5]
	v_mfma_f32_16x16x32_bf16 v[6:9], v[146:149], v[234:237], v[6:9]
	v_mfma_f32_16x16x32_bf16 v[10:13], v[150:153], v[234:237], v[10:13]
	v_mfma_f32_16x16x32_bf16 v[14:17], v[154:157], v[234:237], v[14:17]
	s_mov_b32 s47, s42
	s_mov_b32 s42, s43
	s_mov_b32 s43, s44
	s_mov_b32 s44, s47
	s_waitcnt lgkmcnt(0)
	s_barrier
	s_branch .Lmu_done
.Lmu_grpY5:
	s_add_i32 s47, s44, s6
	s_add_u32 s30, s30, 0x80
	s_addc_u32 s31, s31, 0
	s_mov_b32 m0, s47
	s_nop 0
	global_load_lds_dwordx4 v86, s[30:31]
	s_add_i32 m0, s47, 0x2000
	s_nop 0
	global_load_lds_dwordx4 v134, s[30:31]
	s_add_i32 m0, s47, 0x4000
	s_nop 0
	global_load_lds_dwordx4 v136, s[30:31]
	s_add_i32 m0, s47, 0x6000
	s_nop 0
	global_load_lds_dwordx4 v138, s[30:31]
	s_add_i32 m0, s47, 0x8000
	s_nop 0
	global_load_lds_dwordx4 v140, s[30:31]
	s_waitcnt vmcnt(29)
	v_mul_f32_e32 v114, s20, v114
	v_mul_f32_e32 v115, s20, v115
	v_mul_f32_e32 v116, s21, v116
	v_mul_f32_e32 v117, s21, v117
	v_mul_f32_e32 v118, s22, v118
	v_mul_f32_e32 v119, s22, v119
	v_mul_f32_e32 v120, s23, v120
	v_mul_f32_e32 v121, s23, v121
	v_mul_f32_e32 v122, s24, v122
	v_mul_f32_e32 v123, s24, v123
	v_mul_f32_e32 v124, s25, v124
	v_mul_f32_e32 v125, s25, v125
	v_mul_f32_e32 v126, s26, v126
	v_mul_f32_e32 v127, s26, v127
	v_mul_f32_e32 v128, s27, v128
	v_mul_f32_e32 v129, s27, v129
	v_cvt_pk_bf16_f32 v158, v114, v116
	v_cvt_pk_bf16_f32 v159, v118, v120
	v_cvt_pk_bf16_f32 v160, v122, v124
	v_cvt_pk_bf16_f32 v161, v126, v128
	v_cvt_pk_bf16_f32 v162, v115, v117
	v_cvt_pk_bf16_f32 v163, v119, v121
	v_cvt_pk_bf16_f32 v164, v123, v125
	v_cvt_pk_bf16_f32 v165, v127, v129
	ds_write_b128 v1, v[158:161] offset:19456
	ds_write_b128 v1, v[162:165] offset:19584
	v_add_u32_e32 v91, s42, v135
	v_add_u32_e32 v93, s42, v137
	ds_read_b128 v[238:241], v139 offset:0
	ds_read_b128 v[242:245], v139 offset:2048
	ds_read_b128 v[246:249], v139 offset:4096
	ds_read_b128 v[250:253], v139 offset:6144
	ds_read_b128 v[218:221], v91 offset:0
	ds_read_b128 v[222:225], v91 offset:2048
	ds_read_b128 v[226:229], v91 offset:4096
	ds_read_b128 v[230:233], v91 offset:6144
	ds_read_b128 v[234:237], v91 offset:8192
	s_waitcnt lgkmcnt(0)
; #define MU_GLDS_A(buf, kt) do { _Pragma("unroll") for (int i = 0; i < NMU; ++i) \
;         __builtin_amdgcn_global_load_lds((const unsigned*)((const char*)A + aoff[i] + (size_t)(kt) * 128), (PG8_LAS unsigned*)(MU_SA(buf) + wid * 1024 + i * 8192), 16, 0, 0); } while (0)
; #define MU_B_ISSUE(sb, kt) do { const char* kb_ = Bb + (size_t)(kt) * (64 * (size_t)RB); _Pragma("unroll") for (int j = 0; j < 8; ++j) { const char* p_ = kb_ + (size_t)j * RB; \
;         asm volatile("global_load_dwordx2 %0, %1, off" : "=&v"(sb[j]) : "v"(p_) : "memory"); } } while (0)
; #define MU_B_WAIT(sb, N) asm volatile("s_waitcnt vmcnt(%8)" : "+v"(sb[0]), "+v"(sb[1]), "+v"(sb[2]), "+v"(sb[3]), "+v"(sb[4]), "+v"(sb[5]), "+v"(sb[6]), "+v"(sb[7]) : "n"(N) : "memory")
; #define MU_G_LOAD(ga, kt) do { const PG8_LAS f32x4* gk_ = (const PG8_LAS f32x4*)(lds + GAIN_OFF) + 16 * (kt) + 2 * wid; const f32x4 ga_ = gk_[0], gb_ = gk_[1]; \
;         ga[0] = ga_[0]; ga[1] = ga_[1]; ga[2] = ga_[2]; ga[3] = ga_[3]; ga[4] = gb_[0]; ga[5] = gb_[1]; ga[6] = gb_[2]; ga[7] = gb_[3]; } while (0)
; #define MU_COMPUTE(buf) MU_COMPUTE_N(buf, NMU)
; #define MU_END(last) do { if (last) asm volatile("s_waitcnt vmcnt(0)" ::: "memory"); else asm volatile("s_waitcnt vmcnt(8)" ::: "memory"); \
;         asm volatile("s_waitcnt lgkmcnt(0)" ::: "memory"); __builtin_amdgcn_s_barrier(); asm volatile("" ::: "memory"); } while (0)
; template <int MODE>
; __device__ __forceinline__ void moe_unit(PG8_LAS unsigned char* lds, int e, int cb, int slot0  , int nv  , const bf16_t* A, const int* slot_tok,
;                                          const float* W0, const float* W1, bf16_t* OUT, const float* slot_rs  , const int* slot_dst) {
;     ...
;     for (int t = 0; t < nt; t += 2) {
;         if (t + 2 < nt) MU_B_WAIT(s1, 8); else MU_B_WAIT(s1, 0);
;         MU_G_LOAD(g0, t + 1); MU_B_WRITE(s1, 1, g0); __builtin_amdgcn_sched_barrier(0); MU_GLDS_A(1, t + 1); __builtin_amdgcn_sched_barrier(0);
;         if (t + 3 < nt) { MU_B_ISSUE(s1, t + 3); }
;         MU_COMPUTE(0);
;         MU_END(t + 3 >= nt);
;         if (t + 2 < nt) { MU_B_WAIT(s0, 8); MU_G_LOAD(g0, t + 2); MU_B_WRITE(s0, 0, g0); __builtin_amdgcn_sched_barrier(0); MU_GLDS_A(0, t + 2); __builtin_amdgcn_sched_barrier(0); }
;         if (t + 4 < nt) { MU_B_ISSUE(s0, t + 4); }
;         MU_COMPUTE(1);
;         MU_END(t + 4 >= nt);
	s_load_dwordx8 s[12:19], s[28:29], 0x0
	s_add_u32 s28, s28, 0x100
	s_addc_u32 s29, s29, 0
	v_mfma_f32_16x16x32_bf16 v[78:81], v[238:241], v[218:221], v[78:81]
	v_mfma_f32_16x16x32_bf16 v[74:77], v[242:245], v[218:221], v[74:77]
	v_mfma_f32_16x16x32_bf16 v[70:73], v[246:249], v[218:221], v[70:73]
	v_mfma_f32_16x16x32_bf16 v[66:69], v[250:253], v[218:221], v[66:69]
	ds_read_b128 v[218:221], v93 offset:0
	ds_read_b128 v[142:145], v141 offset:0
	v_lshl_add_u64 v[132:133], v[132:133], 0, s[40:41]
	global_load_dwordx2 v[114:115], v[132:133], off
	global_load_dwordx2 v[116:117], v[132:133], off offset:2048
	v_mfma_f32_16x16x32_bf16 v[62:65], v[238:241], v[222:225], v[62:65]
	v_mfma_f32_16x16x32_bf16 v[58:61], v[242:245], v[222:225], v[58:61]
	v_mfma_f32_16x16x32_bf16 v[54:57], v[246:249], v[222:225], v[54:57]
	v_mfma_f32_16x16x32_bf16 v[50:53], v[250:253], v[222:225], v[50:53]
	ds_read_b128 v[222:225], v93 offset:2048
	ds_read_b128 v[146:149], v141 offset:2048
	v_lshl_add_u64 v[166:167], v[132:133], 0, s[34:35]
	global_load_dwordx2 v[118:119], v[166:167], off
	global_load_dwordx2 v[120:121], v[166:167], off offset:2048
	v_mfma_f32_16x16x32_bf16 v[46:49], v[238:241], v[226:229], v[46:49]
	v_mfma_f32_16x16x32_bf16 v[42:45], v[242:245], v[226:229], v[42:45]
	v_mfma_f32_16x16x32_bf16 v[38:41], v[246:249], v[226:229], v[38:41]
	v_mfma_f32_16x16x32_bf16 v[34:37], v[250:253], v[226:229], v[34:37]
	ds_read_b128 v[226:229], v93 offset:4096
	ds_read_b128 v[150:153], v141 offset:4096
	v_lshl_add_u64 v[166:167], v[132:133], 0, s[36:37]
	global_load_dwordx2 v[122:123], v[166:167], off
	global_load_dwordx2 v[124:125], v[166:167], off offset:2048
	v_mfma_f32_16x16x32_bf16 v[18:21], v[238:241], v[230:233], v[18:21]
	v_mfma_f32_16x16x32_bf16 v[22:25], v[242:245], v[230:233], v[22:25]
	v_mfma_f32_16x16x32_bf16 v[26:29], v[246:249], v[230:233], v[26:29]
	v_mfma_f32_16x16x32_bf16 v[30:33], v[250:253], v[230:233], v[30:33]
	ds_read_b128 v[230:233], v93 offset:6144
	ds_read_b128 v[154:157], v141 offset:6144
	v_lshl_add_u64 v[166:167], v[132:133], 0, s[38:39]
	global_load_dwordx2 v[126:127], v[166:167], off
	global_load_dwordx2 v[128:129], v[166:167], off offset:2048
	v_mfma_f32_16x16x32_bf16 v[2:5], v[238:241], v[234:237], v[2:5]
	v_mfma_f32_16x16x32_bf16 v[6:9], v[242:245], v[234:237], v[6:9]
	v_mfma_f32_16x16x32_bf16 v[10:13], v[246:249], v[234:237], v[10:13]
	v_mfma_f32_16x16x32_bf16 v[14:17], v[250:253], v[234:237], v[14:17]
	ds_read_b128 v[234:237], v93 offset:8192
	s_mov_b32 s47, s42
	s_mov_b32 s42, s43
	s_mov_b32 s43, s44
	s_mov_b32 s44, s47
	s_waitcnt lgkmcnt(0)
	s_barrier
	s_add_i32 s47, s44, s6
	s_add_u32 s30, s30, 0x80
	s_addc_u32 s31, s31, 0
	v_mfma_f32_16x16x32_bf16 v[78:81], v[142:145], v[218:221], v[78:81]
	v_mfma_f32_16x16x32_bf16 v[74:77], v[146:149], v[218:221], v[74:77]
	v_mfma_f32_16x16x32_bf16 v[70:73], v[150:153], v[218:221], v[70:73]
	v_mfma_f32_16x16x32_bf16 v[66:69], v[154:157], v[218:221], v[66:69]
	s_mov_b32 m0, s47
	s_nop 0
	global_load_lds_dwordx4 v86, s[30:31]
	v_mfma_f32_16x16x32_bf16 v[62:65], v[142:145], v[222:225], v[62:65]
	v_mfma_f32_16x16x32_bf16 v[58:61], v[146:149], v[222:225], v[58:61]
	v_mfma_f32_16x16x32_bf16 v[54:57], v[150:153], v[222:225], v[54:57]
	v_mfma_f32_16x16x32_bf16 v[50:53], v[154:157], v[222:225], v[50:53]
	s_add_i32 m0, s47, 0x2000
	s_nop 0
	global_load_lds_dwordx4 v134, s[30:31]
	v_mfma_f32_16x16x32_bf16 v[46:49], v[142:145], v[226:229], v[46:49]
	v_mfma_f32_16x16x32_bf16 v[42:45], v[146:149], v[226:229], v[42:45]
	v_mfma_f32_16x16x32_bf16 v[38:41], v[150:153], v[226:229], v[38:41]
	v_mfma_f32_16x16x32_bf16 v[34:37], v[154:157], v[226:229], v[34:37]
	s_add_i32 m0, s47, 0x4000
	s_nop 0
	global_load_lds_dwordx4 v136, s[30:31]
	v_mfma_f32_16x16x32_bf16 v[18:21], v[142:145], v[230:233], v[18:21]
	v_mfma_f32_16x16x32_bf16 v[22:25], v[146:149], v[230:233], v[22:25]
	v_mfma_f32_16x16x32_bf16 v[26:29], v[150:153], v[230:233], v[26:29]
	v_mfma_f32_16x16x32_bf16 v[30:33], v[154:157], v[230:233], v[30:33]
	s_add_i32 m0, s47, 0x6000
	s_nop 0
	global_load_lds_dwordx4 v138, s[30:31]
	v_mfma_f32_16x16x32_bf16 v[2:5], v[142:145], v[234:237], v[2:5]
	v_mfma_f32_16x16x32_bf16 v[6:9], v[146:149], v[234:237], v[6:9]
	v_mfma_f32_16x16x32_bf16 v[10:13], v[150:153], v[234:237], v[10:13]
	v_mfma_f32_16x16x32_bf16 v[14:17], v[154:157], v[234:237], v[14:17]
	s_add_i32 m0, s47, 0x8000
	s_nop 0
	global_load_lds_dwordx4 v140, s[30:31]
	s_waitcnt vmcnt(34)
	v_mul_f32_e32 v186, s12, v186
	v_mul_f32_e32 v187, s12, v187
	v_mul_f32_e32 v188, s13, v188
	v_mul_f32_e32 v189, s13, v189
	v_mul_f32_e32 v190, s14, v190
	v_mul_f32_e32 v191, s14, v191
	v_mul_f32_e32 v192, s15, v192
	v_mul_f32_e32 v193, s15, v193
	v_mul_f32_e32 v194, s16, v194
	v_mul_f32_e32 v195, s16, v195
	v_mul_f32_e32 v196, s17, v196
	v_mul_f32_e32 v197, s17, v197
	v_mul_f32_e32 v198, s18, v198
	v_mul_f32_e32 v199, s18, v199
	v_mul_f32_e32 v200, s19, v200
	v_mul_f32_e32 v201, s19, v201
	v_cvt_pk_bf16_f32 v158, v186, v188
	v_cvt_pk_bf16_f32 v159, v190, v192
	v_cvt_pk_bf16_f32 v160, v194, v196
	v_cvt_pk_bf16_f32 v161, v198, v200
	v_cvt_pk_bf16_f32 v162, v187, v189
	v_cvt_pk_bf16_f32 v163, v191, v193
	v_cvt_pk_bf16_f32 v164, v195, v197
	v_cvt_pk_bf16_f32 v165, v199, v201
	ds_write_b128 v1, v[158:161] offset:0
	ds_write_b128 v1, v[162:165] offset:128
	v_add_u32_e32 v91, s42, v135
	v_add_u32_e32 v93, s42, v137
	ds_read_b128 v[238:241], v139 offset:19456
	ds_read_b128 v[242:245], v139 offset:21504
	ds_read_b128 v[246:249], v139 offset:23552
	ds_read_b128 v[250:253], v139 offset:25600
	ds_read_b128 v[218:221], v91 offset:0
	ds_read_b128 v[222:225], v91 offset:2048
	ds_read_b128 v[226:229], v91 offset:4096
	ds_read_b128 v[230:233], v91 offset:6144
	ds_read_b128 v[234:237], v91 offset:8192
	s_waitcnt lgkmcnt(0)
; #define MU_GLDS_A(buf, kt) do { _Pragma("unroll") for (int i = 0; i < NMU; ++i) \
;         __builtin_amdgcn_global_load_lds((const unsigned*)((const char*)A + aoff[i] + (size_t)(kt) * 128), (PG8_LAS unsigned*)(MU_SA(buf) + wid * 1024 + i * 8192), 16, 0, 0); } while (0)
; #define MU_B_ISSUE(sb, kt) do { const char* kb_ = Bb + (size_t)(kt) * (64 * (size_t)RB); _Pragma("unroll") for (int j = 0; j < 8; ++j) { const char* p_ = kb_ + (size_t)j * RB; \
;         asm volatile("global_load_dwordx2 %0, %1, off" : "=&v"(sb[j]) : "v"(p_) : "memory"); } } while (0)
; #define MU_B_WAIT(sb, N) asm volatile("s_waitcnt vmcnt(%8)" : "+v"(sb[0]), "+v"(sb[1]), "+v"(sb[2]), "+v"(sb[3]), "+v"(sb[4]), "+v"(sb[5]), "+v"(sb[6]), "+v"(sb[7]) : "n"(N) : "memory")
; #define MU_G_LOAD(ga, kt) do { const PG8_LAS f32x4* gk_ = (const PG8_LAS f32x4*)(lds + GAIN_OFF) + 16 * (kt) + 2 * wid; const f32x4 ga_ = gk_[0], gb_ = gk_[1]; \
;         ga[0] = ga_[0]; ga[1] = ga_[1]; ga[2] = ga_[2]; ga[3] = ga_[3]; ga[4] = gb_[0]; ga[5] = gb_[1]; ga[6] = gb_[2]; ga[7] = gb_[3]; } while (0)
; #define MU_COMPUTE(buf) MU_COMPUTE_N(buf, NMU)
; #define MU_END(last) do { if (last) asm volatile("s_waitcnt vmcnt(0)" ::: "memory"); else asm volatile("s_waitcnt vmcnt(8)" ::: "memory"); \
;         asm volatile("s_waitcnt lgkmcnt(0)" ::: "memory"); __builtin_amdgcn_s_barrier(); asm volatile("" ::: "memory"); } while (0)
; template <int MODE>
; __device__ __forceinline__ void moe_unit(PG8_LAS unsigned char* lds, int e, int cb, int slot0  , int nv  , const bf16_t* A, const int* slot_tok,
;                                          const float* W0, const float* W1, bf16_t* OUT, const float* slot_rs  , const int* slot_dst) {
;     ...
;     for (int t = 0; t < nt; t += 2) {
;         if (t + 2 < nt) MU_B_WAIT(s1, 8); else MU_B_WAIT(s1, 0);
;         MU_G_LOAD(g0, t + 1); MU_B_WRITE(s1, 1, g0); __builtin_amdgcn_sched_barrier(0); MU_GLDS_A(1, t + 1); __builtin_amdgcn_sched_barrier(0);
;         if (t + 3 < nt) { MU_B_ISSUE(s1, t + 3); }
;         MU_COMPUTE(0);
;         MU_END(t + 3 >= nt);
;         if (t + 2 < nt) { MU_B_WAIT(s0, 8); MU_G_LOAD(g0, t + 2); MU_B_WRITE(s0, 0, g0); __builtin_amdgcn_sched_barrier(0); MU_GLDS_A(0, t + 2); __builtin_amdgcn_sched_barrier(0); }
;         if (t + 4 < nt) { MU_B_ISSUE(s0, t + 4); }
;         MU_COMPUTE(1);
;         MU_END(t + 4 >= nt);
	s_load_dwordx8 s[20:27], s[28:29], 0x0
	s_add_u32 s28, s28, 0x100
	s_addc_u32 s29, s29, 0
	v_mfma_f32_16x16x32_bf16 v[78:81], v[238:241], v[218:221], v[78:81]
	v_mfma_f32_16x16x32_bf16 v[74:77], v[242:245], v[218:221], v[74:77]
	v_mfma_f32_16x16x32_bf16 v[70:73], v[246:249], v[218:221], v[70:73]
	v_mfma_f32_16x16x32_bf16 v[66:69], v[250:253], v[218:221], v[66:69]
	ds_read_b128 v[218:221], v93 offset:0
	ds_read_b128 v[142:145], v141 offset:19456
	v_lshl_add_u64 v[132:133], v[132:133], 0, s[40:41]
	global_load_dwordx2 v[186:187], v[132:133], off
	global_load_dwordx2 v[188:189], v[132:133], off offset:2048
	v_mfma_f32_16x16x32_bf16 v[62:65], v[238:241], v[222:225], v[62:65]
	v_mfma_f32_16x16x32_bf16 v[58:61], v[242:245], v[222:225], v[58:61]
	v_mfma_f32_16x16x32_bf16 v[54:57], v[246:249], v[222:225], v[54:57]
	v_mfma_f32_16x16x32_bf16 v[50:53], v[250:253], v[222:225], v[50:53]
	ds_read_b128 v[222:225], v93 offset:2048
	ds_read_b128 v[146:149], v141 offset:21504
	v_lshl_add_u64 v[166:167], v[132:133], 0, s[34:35]
	global_load_dwordx2 v[190:191], v[166:167], off
	global_load_dwordx2 v[192:193], v[166:167], off offset:2048
	v_mfma_f32_16x16x32_bf16 v[46:49], v[238:241], v[226:229], v[46:49]
	v_mfma_f32_16x16x32_bf16 v[42:45], v[242:245], v[226:229], v[42:45]
	v_mfma_f32_16x16x32_bf16 v[38:41], v[246:249], v[226:229], v[38:41]
	v_mfma_f32_16x16x32_bf16 v[34:37], v[250:253], v[226:229], v[34:37]
	ds_read_b128 v[226:229], v93 offset:4096
	ds_read_b128 v[150:153], v141 offset:23552
	v_lshl_add_u64 v[166:167], v[132:133], 0, s[36:37]
	global_load_dwordx2 v[194:195], v[166:167], off
	global_load_dwordx2 v[196:197], v[166:167], off offset:2048
	v_mfma_f32_16x16x32_bf16 v[18:21], v[238:241], v[230:233], v[18:21]
	v_mfma_f32_16x16x32_bf16 v[22:25], v[242:245], v[230:233], v[22:25]
	v_mfma_f32_16x16x32_bf16 v[26:29], v[246:249], v[230:233], v[26:29]
	v_mfma_f32_16x16x32_bf16 v[30:33], v[250:253], v[230:233], v[30:33]
	ds_read_b128 v[230:233], v93 offset:6144
	ds_read_b128 v[154:157], v141 offset:25600
	v_lshl_add_u64 v[166:167], v[132:133], 0, s[38:39]
	global_load_dwordx2 v[198:199], v[166:167], off
	global_load_dwordx2 v[200:201], v[166:167], off offset:2048
	v_mfma_f32_16x16x32_bf16 v[2:5], v[238:241], v[234:237], v[2:5]
	v_mfma_f32_16x16x32_bf16 v[6:9], v[242:245], v[234:237], v[6:9]
	v_mfma_f32_16x16x32_bf16 v[10:13], v[246:249], v[234:237], v[10:13]
	v_mfma_f32_16x16x32_bf16 v[14:17], v[250:253], v[234:237], v[14:17]
	ds_read_b128 v[234:237], v93 offset:8192
	s_waitcnt vmcnt(21)
	s_mov_b32 s47, s42
	s_mov_b32 s42, s43
	s_mov_b32 s43, s44
	s_mov_b32 s44, s47
	s_waitcnt lgkmcnt(0)
	s_barrier
	s_add_i32 s47, s44, s6
	s_add_u32 s30, s30, 0x80
	s_addc_u32 s31, s31, 0
	v_mfma_f32_16x16x32_bf16 v[78:81], v[142:145], v[218:221], v[78:81]
	v_mfma_f32_16x16x32_bf16 v[74:77], v[146:149], v[218:221], v[74:77]
	v_mfma_f32_16x16x32_bf16 v[70:73], v[150:153], v[218:221], v[70:73]
	v_mfma_f32_16x16x32_bf16 v[66:69], v[154:157], v[218:221], v[66:69]
	s_mov_b32 m0, s47
	s_nop 0
	global_load_lds_dwordx4 v86, s[30:31]
	v_mfma_f32_16x16x32_bf16 v[62:65], v[142:145], v[222:225], v[62:65]
	v_mfma_f32_16x16x32_bf16 v[58:61], v[146:149], v[222:225], v[58:61]
	v_mfma_f32_16x16x32_bf16 v[54:57], v[150:153], v[222:225], v[54:57]
	v_mfma_f32_16x16x32_bf16 v[50:53], v[154:157], v[222:225], v[50:53]
	s_add_i32 m0, s47, 0x2000
	s_nop 0
	global_load_lds_dwordx4 v134, s[30:31]
	v_mfma_f32_16x16x32_bf16 v[46:49], v[142:145], v[226:229], v[46:49]
	v_mfma_f32_16x16x32_bf16 v[42:45], v[146:149], v[226:229], v[42:45]
	v_mfma_f32_16x16x32_bf16 v[38:41], v[150:153], v[226:229], v[38:41]
	v_mfma_f32_16x16x32_bf16 v[34:37], v[154:157], v[226:229], v[34:37]
	s_add_i32 m0, s47, 0x4000
	s_nop 0
	global_load_lds_dwordx4 v136, s[30:31]
	v_mfma_f32_16x16x32_bf16 v[18:21], v[142:145], v[230:233], v[18:21]
	v_mfma_f32_16x16x32_bf16 v[22:25], v[146:149], v[230:233], v[22:25]
	v_mfma_f32_16x16x32_bf16 v[26:29], v[150:153], v[230:233], v[26:29]
	v_mfma_f32_16x16x32_bf16 v[30:33], v[154:157], v[230:233], v[30:33]
	s_add_i32 m0, s47, 0x6000
	s_nop 0
	global_load_lds_dwordx4 v138, s[30:31]
	v_mfma_f32_16x16x32_bf16 v[2:5], v[142:145], v[234:237], v[2:5]
	v_mfma_f32_16x16x32_bf16 v[6:9], v[146:149], v[234:237], v[6:9]
	v_mfma_f32_16x16x32_bf16 v[10:13], v[150:153], v[234:237], v[10:13]
	v_mfma_f32_16x16x32_bf16 v[14:17], v[154:157], v[234:237], v[14:17]
	s_add_i32 m0, s47, 0x8000
	s_nop 0
	global_load_lds_dwordx4 v140, s[30:31]
	v_mul_f32_e32 v202, s20, v202
	v_mul_f32_e32 v203, s20, v203
	v_mul_f32_e32 v204, s21, v204
	v_mul_f32_e32 v205, s21, v205
	v_mul_f32_e32 v206, s22, v206
	v_mul_f32_e32 v207, s22, v207
	v_mul_f32_e32 v208, s23, v208
	v_mul_f32_e32 v209, s23, v209
	v_mul_f32_e32 v210, s24, v210
	v_mul_f32_e32 v211, s24, v211
	v_mul_f32_e32 v212, s25, v212
	v_mul_f32_e32 v213, s25, v213
	v_mul_f32_e32 v214, s26, v214
	v_mul_f32_e32 v215, s26, v215
	v_mul_f32_e32 v216, s27, v216
	v_mul_f32_e32 v217, s27, v217
	v_cvt_pk_bf16_f32 v158, v202, v204
	v_cvt_pk_bf16_f32 v159, v206, v208
	v_cvt_pk_bf16_f32 v160, v210, v212
	v_cvt_pk_bf16_f32 v161, v214, v216
	v_cvt_pk_bf16_f32 v162, v203, v205
	v_cvt_pk_bf16_f32 v163, v207, v209
	v_cvt_pk_bf16_f32 v164, v211, v213
	v_cvt_pk_bf16_f32 v165, v215, v217
	ds_write_b128 v1, v[158:161] offset:19456
	ds_write_b128 v1, v[162:165] offset:19584
	v_add_u32_e32 v91, s42, v135
	v_add_u32_e32 v93, s42, v137
	ds_read_b128 v[238:241], v139 offset:0
	ds_read_b128 v[242:245], v139 offset:2048
	ds_read_b128 v[246:249], v139 offset:4096
	ds_read_b128 v[250:253], v139 offset:6144
	ds_read_b128 v[218:221], v91 offset:0
	ds_read_b128 v[222:225], v91 offset:2048
	ds_read_b128 v[226:229], v91 offset:4096
	ds_read_b128 v[230:233], v91 offset:6144
	ds_read_b128 v[234:237], v91 offset:8192
	s_waitcnt lgkmcnt(0)
; #define MU_GLDS_A(buf, kt) do { _Pragma("unroll") for (int i = 0; i < NMU; ++i) \
;         __builtin_amdgcn_global_load_lds((const unsigned*)((const char*)A + aoff[i] + (size_t)(kt) * 128), (PG8_LAS unsigned*)(MU_SA(buf) + wid * 1024 + i * 8192), 16, 0, 0); } while (0)
; #define MU_B_ISSUE(sb, kt) do { const char* kb_ = Bb + (size_t)(kt) * (64 * (size_t)RB); _Pragma("unroll") for (int j = 0; j < 8; ++j) { const char* p_ = kb_ + (size_t)j * RB; \
;         asm volatile("global_load_dwordx2 %0, %1, off" : "=&v"(sb[j]) : "v"(p_) : "memory"); } } while (0)
; #define MU_B_WAIT(sb, N) asm volatile("s_waitcnt vmcnt(%8)" : "+v"(sb[0]), "+v"(sb[1]), "+v"(sb[2]), "+v"(sb[3]), "+v"(sb[4]), "+v"(sb[5]), "+v"(sb[6]), "+v"(sb[7]) : "n"(N) : "memory")
; #define MU_G_LOAD(ga, kt) do { const PG8_LAS f32x4* gk_ = (const PG8_LAS f32x4*)(lds + GAIN_OFF) + 16 * (kt) + 2 * wid; const f32x4 ga_ = gk_[0], gb_ = gk_[1]; \
;         ga[0] = ga_[0]; ga[1] = ga_[1]; ga[2] = ga_[2]; ga[3] = ga_[3]; ga[4] = gb_[0]; ga[5] = gb_[1]; ga[6] = gb_[2]; ga[7] = gb_[3]; } while (0)
; #define MU_COMPUTE(buf) MU_COMPUTE_N(buf, NMU)
; #define MU_END(last) do { if (last) asm volatile("s_waitcnt vmcnt(0)" ::: "memory"); else asm volatile("s_waitcnt vmcnt(8)" ::: "memory"); \
;         asm volatile("s_waitcnt lgkmcnt(0)" ::: "memory"); __builtin_amdgcn_s_barrier(); asm volatile("" ::: "memory"); } while (0)
; template <int MODE>
; __device__ __forceinline__ void moe_unit(PG8_LAS unsigned char* lds, int e, int cb, int slot0  , int nv  , const bf16_t* A, const int* slot_tok,
;                                          const float* W0, const float* W1, bf16_t* OUT, const float* slot_rs  , const int* slot_dst) {
;     ...
;     for (int t = 0; t < nt; t += 2) {
;         if (t + 2 < nt) MU_B_WAIT(s1, 8); else MU_B_WAIT(s1, 0);
;         MU_G_LOAD(g0, t + 1); MU_B_WRITE(s1, 1, g0); __builtin_amdgcn_sched_barrier(0); MU_GLDS_A(1, t + 1); __builtin_amdgcn_sched_barrier(0);
;         if (t + 3 < nt) { MU_B_ISSUE(s1, t + 3); }
;         MU_COMPUTE(0);
;         MU_END(t + 3 >= nt);
;         if (t + 2 < nt) { MU_B_WAIT(s0, 8); MU_G_LOAD(g0, t + 2); MU_B_WRITE(s0, 0, g0); __builtin_amdgcn_sched_barrier(0); MU_GLDS_A(0, t + 2); __builtin_amdgcn_sched_barrier(0); }
;         if (t + 4 < nt) { MU_B_ISSUE(s0, t + 4); }
;         MU_COMPUTE(1);
;         MU_END(t + 4 >= nt);
	s_load_dwordx8 s[12:19], s[28:29], 0x0
	s_add_u32 s28, s28, 0x100
	s_addc_u32 s29, s29, 0
	v_mfma_f32_16x16x32_bf16 v[78:81], v[238:241], v[218:221], v[78:81]
	v_mfma_f32_16x16x32_bf16 v[74:77], v[242:245], v[218:221], v[74:77]
	v_mfma_f32_16x16x32_bf16 v[70:73], v[246:249], v[218:221], v[70:73]
	v_mfma_f32_16x16x32_bf16 v[66:69], v[250:253], v[218:221], v[66:69]
	ds_read_b128 v[218:221], v93 offset:0
	ds_read_b128 v[142:145], v141 offset:0
	v_lshl_add_u64 v[132:133], v[132:133], 0, s[40:41]
	global_load_dwordx2 v[202:203], v[132:133], off
	global_load_dwordx2 v[204:205], v[132:133], off offset:2048
	v_mfma_f32_16x16x32_bf16 v[62:65], v[238:241], v[222:225], v[62:65]
	v_mfma_f32_16x16x32_bf16 v[58:61], v[242:245], v[222:225], v[58:61]
	v_mfma_f32_16x16x32_bf16 v[54:57], v[246:249], v[222:225], v[54:57]
	v_mfma_f32_16x16x32_bf16 v[50:53], v[250:253], v[222:225], v[50:53]
	ds_read_b128 v[222:225], v93 offset:2048
	ds_read_b128 v[146:149], v141 offset:2048
	v_lshl_add_u64 v[166:167], v[132:133], 0, s[34:35]
	global_load_dwordx2 v[206:207], v[166:167], off
	global_load_dwordx2 v[208:209], v[166:167], off offset:2048
	v_mfma_f32_16x16x32_bf16 v[46:49], v[238:241], v[226:229], v[46:49]
	v_mfma_f32_16x16x32_bf16 v[42:45], v[242:245], v[226:229], v[42:45]
	v_mfma_f32_16x16x32_bf16 v[38:41], v[246:249], v[226:229], v[38:41]
	v_mfma_f32_16x16x32_bf16 v[34:37], v[250:253], v[226:229], v[34:37]
	ds_read_b128 v[226:229], v93 offset:4096
	ds_read_b128 v[150:153], v141 offset:4096
	v_lshl_add_u64 v[166:167], v[132:133], 0, s[36:37]
	global_load_dwordx2 v[210:211], v[166:167], off
	global_load_dwordx2 v[212:213], v[166:167], off offset:2048
	v_mfma_f32_16x16x32_bf16 v[18:21], v[238:241], v[230:233], v[18:21]
	v_mfma_f32_16x16x32_bf16 v[22:25], v[242:245], v[230:233], v[22:25]
	v_mfma_f32_16x16x32_bf16 v[26:29], v[246:249], v[230:233], v[26:29]
	v_mfma_f32_16x16x32_bf16 v[30:33], v[250:253], v[230:233], v[30:33]
	ds_read_b128 v[230:233], v93 offset:6144
	ds_read_b128 v[154:157], v141 offset:6144
	v_lshl_add_u64 v[166:167], v[132:133], 0, s[38:39]
	global_load_dwordx2 v[214:215], v[166:167], off
	global_load_dwordx2 v[216:217], v[166:167], off offset:2048
	v_mfma_f32_16x16x32_bf16 v[2:5], v[238:241], v[234:237], v[2:5]
	v_mfma_f32_16x16x32_bf16 v[6:9], v[242:245], v[234:237], v[6:9]
	v_mfma_f32_16x16x32_bf16 v[10:13], v[246:249], v[234:237], v[10:13]
	v_mfma_f32_16x16x32_bf16 v[14:17], v[250:253], v[234:237], v[14:17]
	ds_read_b128 v[234:237], v93 offset:8192
	s_waitcnt vmcnt(21)
	s_mov_b32 s47, s42
	s_mov_b32 s42, s43
	s_mov_b32 s43, s44
	s_mov_b32 s44, s47
	s_waitcnt lgkmcnt(0)
	s_barrier
	s_add_i32 s47, s44, s6
	s_add_u32 s30, s30, 0x80
	s_addc_u32 s31, s31, 0
	v_mfma_f32_16x16x32_bf16 v[78:81], v[142:145], v[218:221], v[78:81]
	v_mfma_f32_16x16x32_bf16 v[74:77], v[146:149], v[218:221], v[74:77]
	v_mfma_f32_16x16x32_bf16 v[70:73], v[150:153], v[218:221], v[70:73]
	v_mfma_f32_16x16x32_bf16 v[66:69], v[154:157], v[218:221], v[66:69]
	s_mov_b32 m0, s47
	s_nop 0
	global_load_lds_dwordx4 v86, s[30:31]
	v_mfma_f32_16x16x32_bf16 v[62:65], v[142:145], v[222:225], v[62:65]
	v_mfma_f32_16x16x32_bf16 v[58:61], v[146:149], v[222:225], v[58:61]
	v_mfma_f32_16x16x32_bf16 v[54:57], v[150:153], v[222:225], v[54:57]
	v_mfma_f32_16x16x32_bf16 v[50:53], v[154:157], v[222:225], v[50:53]
	s_add_i32 m0, s47, 0x2000
	s_nop 0
	global_load_lds_dwordx4 v134, s[30:31]
	v_mfma_f32_16x16x32_bf16 v[46:49], v[142:145], v[226:229], v[46:49]
	v_mfma_f32_16x16x32_bf16 v[42:45], v[146:149], v[226:229], v[42:45]
	v_mfma_f32_16x16x32_bf16 v[38:41], v[150:153], v[226:229], v[38:41]
	v_mfma_f32_16x16x32_bf16 v[34:37], v[154:157], v[226:229], v[34:37]
	s_add_i32 m0, s47, 0x4000
	s_nop 0
	global_load_lds_dwordx4 v136, s[30:31]
	v_mfma_f32_16x16x32_bf16 v[18:21], v[142:145], v[230:233], v[18:21]
	v_mfma_f32_16x16x32_bf16 v[22:25], v[146:149], v[230:233], v[22:25]
	v_mfma_f32_16x16x32_bf16 v[26:29], v[150:153], v[230:233], v[26:29]
	v_mfma_f32_16x16x32_bf16 v[30:33], v[154:157], v[230:233], v[30:33]
	s_add_i32 m0, s47, 0x6000
	s_nop 0
	global_load_lds_dwordx4 v138, s[30:31]
	v_mfma_f32_16x16x32_bf16 v[2:5], v[142:145], v[234:237], v[2:5]
	v_mfma_f32_16x16x32_bf16 v[6:9], v[146:149], v[234:237], v[6:9]
	v_mfma_f32_16x16x32_bf16 v[10:13], v[150:153], v[234:237], v[10:13]
	v_mfma_f32_16x16x32_bf16 v[14:17], v[154:157], v[234:237], v[14:17]
	s_add_i32 m0, s47, 0x8000
	s_nop 0
	global_load_lds_dwordx4 v140, s[30:31]
	v_mul_f32_e32 v98, s12, v98
	v_mul_f32_e32 v99, s12, v99
	v_mul_f32_e32 v100, s13, v100
	v_mul_f32_e32 v101, s13, v101
	v_mul_f32_e32 v102, s14, v102
	v_mul_f32_e32 v103, s14, v103
	v_mul_f32_e32 v104, s15, v104
	v_mul_f32_e32 v105, s15, v105
	v_mul_f32_e32 v106, s16, v106
	v_mul_f32_e32 v107, s16, v107
	v_mul_f32_e32 v108, s17, v108
	v_mul_f32_e32 v109, s17, v109
	v_mul_f32_e32 v110, s18, v110
	v_mul_f32_e32 v111, s18, v111
	v_mul_f32_e32 v112, s19, v112
	v_mul_f32_e32 v113, s19, v113
	v_cvt_pk_bf16_f32 v158, v98, v100
	v_cvt_pk_bf16_f32 v159, v102, v104
	v_cvt_pk_bf16_f32 v160, v106, v108
	v_cvt_pk_bf16_f32 v161, v110, v112
	v_cvt_pk_bf16_f32 v162, v99, v101
	v_cvt_pk_bf16_f32 v163, v103, v105
	v_cvt_pk_bf16_f32 v164, v107, v109
	v_cvt_pk_bf16_f32 v165, v111, v113
	ds_write_b128 v1, v[158:161] offset:0
	ds_write_b128 v1, v[162:165] offset:128
	v_add_u32_e32 v91, s42, v135
	v_add_u32_e32 v93, s42, v137
	ds_read_b128 v[238:241], v139 offset:19456
	ds_read_b128 v[242:245], v139 offset:21504
	ds_read_b128 v[246:249], v139 offset:23552
	ds_read_b128 v[250:253], v139 offset:25600
	ds_read_b128 v[218:221], v91 offset:0
	ds_read_b128 v[222:225], v91 offset:2048
	ds_read_b128 v[226:229], v91 offset:4096
	ds_read_b128 v[230:233], v91 offset:6144
	ds_read_b128 v[234:237], v91 offset:8192
	s_waitcnt lgkmcnt(0)
; #define MU_GLDS_A(buf, kt) do { _Pragma("unroll") for (int i = 0; i < NMU; ++i) \
;         __builtin_amdgcn_global_load_lds((const unsigned*)((const char*)A + aoff[i] + (size_t)(kt) * 128), (PG8_LAS unsigned*)(MU_SA(buf) + wid * 1024 + i * 8192), 16, 0, 0); } while (0)
; #define MU_B_ISSUE(sb, kt) do { const char* kb_ = Bb + (size_t)(kt) * (64 * (size_t)RB); _Pragma("unroll") for (int j = 0; j < 8; ++j) { const char* p_ = kb_ + (size_t)j * RB; \
;         asm volatile("global_load_dwordx2 %0, %1, off" : "=&v"(sb[j]) : "v"(p_) : "memory"); } } while (0)
; #define MU_B_WAIT(sb, N) asm volatile("s_waitcnt vmcnt(%8)" : "+v"(sb[0]), "+v"(sb[1]), "+v"(sb[2]), "+v"(sb[3]), "+v"(sb[4]), "+v"(sb[5]), "+v"(sb[6]), "+v"(sb[7]) : "n"(N) : "memory")
; #define MU_G_LOAD(ga, kt) do { const PG8_LAS f32x4* gk_ = (const PG8_LAS f32x4*)(lds + GAIN_OFF) + 16 * (kt) + 2 * wid; const f32x4 ga_ = gk_[0], gb_ = gk_[1]; \
;         ga[0] = ga_[0]; ga[1] = ga_[1]; ga[2] = ga_[2]; ga[3] = ga_[3]; ga[4] = gb_[0]; ga[5] = gb_[1]; ga[6] = gb_[2]; ga[7] = gb_[3]; } while (0)
; #define MU_COMPUTE(buf) MU_COMPUTE_N(buf, NMU)
; #define MU_END(last) do { if (last) asm volatile("s_waitcnt vmcnt(0)" ::: "memory"); else asm volatile("s_waitcnt vmcnt(8)" ::: "memory"); \
;         asm volatile("s_waitcnt lgkmcnt(0)" ::: "memory"); __builtin_amdgcn_s_barrier(); asm volatile("" ::: "memory"); } while (0)
; template <int MODE>
; __device__ __forceinline__ void moe_unit(PG8_LAS unsigned char* lds, int e, int cb, int slot0  , int nv  , const bf16_t* A, const int* slot_tok,
;                                          const float* W0, const float* W1, bf16_t* OUT, const float* slot_rs  , const int* slot_dst) {
;     ...
;     for (int t = 0; t < nt; t += 2) {
;         if (t + 2 < nt) MU_B_WAIT(s1, 8); else MU_B_WAIT(s1, 0);
;         MU_G_LOAD(g0, t + 1); MU_B_WRITE(s1, 1, g0); __builtin_amdgcn_sched_barrier(0); MU_GLDS_A(1, t + 1); __builtin_amdgcn_sched_barrier(0);
;         if (t + 3 < nt) { MU_B_ISSUE(s1, t + 3); }
;         MU_COMPUTE(0);
;         MU_END(t + 3 >= nt);
;         if (t + 2 < nt) { MU_B_WAIT(s0, 8); MU_G_LOAD(g0, t + 2); MU_B_WRITE(s0, 0, g0); __builtin_amdgcn_sched_barrier(0); MU_GLDS_A(0, t + 2); __builtin_amdgcn_sched_barrier(0); }
;         if (t + 4 < nt) { MU_B_ISSUE(s0, t + 4); }
;         MU_COMPUTE(1);
;         MU_END(t + 4 >= nt);
	s_load_dwordx8 s[20:27], s[28:29], 0x0
	s_add_u32 s28, s28, 0x100
	s_addc_u32 s29, s29, 0
	v_mfma_f32_16x16x32_bf16 v[78:81], v[238:241], v[218:221], v[78:81]
	v_mfma_f32_16x16x32_bf16 v[74:77], v[242:245], v[218:221], v[74:77]
	v_mfma_f32_16x16x32_bf16 v[70:73], v[246:249], v[218:221], v[70:73]
	v_mfma_f32_16x16x32_bf16 v[66:69], v[250:253], v[218:221], v[66:69]
	ds_read_b128 v[218:221], v93 offset:0
	ds_read_b128 v[142:145], v141 offset:19456
	v_lshl_add_u64 v[132:133], v[132:133], 0, s[40:41]
	global_load_dwordx2 v[98:99], v[132:133], off
	global_load_dwordx2 v[100:101], v[132:133], off offset:2048
	v_mfma_f32_16x16x32_bf16 v[62:65], v[238:241], v[222:225], v[62:65]
	v_mfma_f32_16x16x32_bf16 v[58:61], v[242:245], v[222:225], v[58:61]
	v_mfma_f32_16x16x32_bf16 v[54:57], v[246:249], v[222:225], v[54:57]
	v_mfma_f32_16x16x32_bf16 v[50:53], v[250:253], v[222:225], v[50:53]
	ds_read_b128 v[222:225], v93 offset:2048
	ds_read_b128 v[146:149], v141 offset:21504
	v_lshl_add_u64 v[166:167], v[132:133], 0, s[34:35]
	global_load_dwordx2 v[102:103], v[166:167], off
	global_load_dwordx2 v[104:105], v[166:167], off offset:2048
	v_mfma_f32_16x16x32_bf16 v[46:49], v[238:241], v[226:229], v[46:49]
	v_mfma_f32_16x16x32_bf16 v[42:45], v[242:245], v[226:229], v[42:45]
	v_mfma_f32_16x16x32_bf16 v[38:41], v[246:249], v[226:229], v[38:41]
	v_mfma_f32_16x16x32_bf16 v[34:37], v[250:253], v[226:229], v[34:37]
	ds_read_b128 v[226:229], v93 offset:4096
	ds_read_b128 v[150:153], v141 offset:23552
	v_lshl_add_u64 v[166:167], v[132:133], 0, s[36:37]
	global_load_dwordx2 v[106:107], v[166:167], off
	global_load_dwordx2 v[108:109], v[166:167], off offset:2048
	v_mfma_f32_16x16x32_bf16 v[18:21], v[238:241], v[230:233], v[18:21]
	v_mfma_f32_16x16x32_bf16 v[22:25], v[242:245], v[230:233], v[22:25]
	v_mfma_f32_16x16x32_bf16 v[26:29], v[246:249], v[230:233], v[26:29]
	v_mfma_f32_16x16x32_bf16 v[30:33], v[250:253], v[230:233], v[30:33]
	ds_read_b128 v[230:233], v93 offset:6144
	ds_read_b128 v[154:157], v141 offset:25600
	v_lshl_add_u64 v[166:167], v[132:133], 0, s[38:39]
	global_load_dwordx2 v[110:111], v[166:167], off
	global_load_dwordx2 v[112:113], v[166:167], off offset:2048
	v_mfma_f32_16x16x32_bf16 v[2:5], v[238:241], v[234:237], v[2:5]
	v_mfma_f32_16x16x32_bf16 v[6:9], v[242:245], v[234:237], v[6:9]
	v_mfma_f32_16x16x32_bf16 v[10:13], v[246:249], v[234:237], v[10:13]
	v_mfma_f32_16x16x32_bf16 v[14:17], v[250:253], v[234:237], v[14:17]
	ds_read_b128 v[234:237], v93 offset:8192
	s_waitcnt vmcnt(21)
	s_mov_b32 s47, s42
	s_mov_b32 s42, s43
	s_mov_b32 s43, s44
	s_mov_b32 s44, s47
	s_waitcnt lgkmcnt(0)
	s_barrier
	s_mov_b32 s46, 13
.Lmu_loop_Y5:
	s_add_i32 s47, s44, s6
	s_add_u32 s30, s30, 0x80
	s_addc_u32 s31, s31, 0
	v_mfma_f32_16x16x32_bf16 v[78:81], v[142:145], v[218:221], v[78:81]
	v_mfma_f32_16x16x32_bf16 v[74:77], v[146:149], v[218:221], v[74:77]
	v_mfma_f32_16x16x32_bf16 v[70:73], v[150:153], v[218:221], v[70:73]
	v_mfma_f32_16x16x32_bf16 v[66:69], v[154:157], v[218:221], v[66:69]
	s_mov_b32 m0, s47
	s_nop 0
	global_load_lds_dwordx4 v86, s[30:31]
	v_mfma_f32_16x16x32_bf16 v[62:65], v[142:145], v[222:225], v[62:65]
	v_mfma_f32_16x16x32_bf16 v[58:61], v[146:149], v[222:225], v[58:61]
	v_mfma_f32_16x16x32_bf16 v[54:57], v[150:153], v[222:225], v[54:57]
	v_mfma_f32_16x16x32_bf16 v[50:53], v[154:157], v[222:225], v[50:53]
	s_add_i32 m0, s47, 0x2000
	s_nop 0
	global_load_lds_dwordx4 v134, s[30:31]
	v_mfma_f32_16x16x32_bf16 v[46:49], v[142:145], v[226:229], v[46:49]
	v_mfma_f32_16x16x32_bf16 v[42:45], v[146:149], v[226:229], v[42:45]
	v_mfma_f32_16x16x32_bf16 v[38:41], v[150:153], v[226:229], v[38:41]
	v_mfma_f32_16x16x32_bf16 v[34:37], v[154:157], v[226:229], v[34:37]
	s_add_i32 m0, s47, 0x4000
	s_nop 0
	global_load_lds_dwordx4 v136, s[30:31]
	v_mfma_f32_16x16x32_bf16 v[18:21], v[142:145], v[230:233], v[18:21]
	v_mfma_f32_16x16x32_bf16 v[22:25], v[146:149], v[230:233], v[22:25]
	v_mfma_f32_16x16x32_bf16 v[26:29], v[150:153], v[230:233], v[26:29]
	v_mfma_f32_16x16x32_bf16 v[30:33], v[154:157], v[230:233], v[30:33]
	s_add_i32 m0, s47, 0x6000
	s_nop 0
	global_load_lds_dwordx4 v138, s[30:31]
	v_mfma_f32_16x16x32_bf16 v[2:5], v[142:145], v[234:237], v[2:5]
	v_mfma_f32_16x16x32_bf16 v[6:9], v[146:149], v[234:237], v[6:9]
	v_mfma_f32_16x16x32_bf16 v[10:13], v[150:153], v[234:237], v[10:13]
	v_mfma_f32_16x16x32_bf16 v[14:17], v[154:157], v[234:237], v[14:17]
	s_add_i32 m0, s47, 0x8000
	s_nop 0
	global_load_lds_dwordx4 v140, s[30:31]
	v_mul_f32_e32 v114, s20, v114
	v_mul_f32_e32 v115, s20, v115
	v_mul_f32_e32 v116, s21, v116
	v_mul_f32_e32 v117, s21, v117
	v_mul_f32_e32 v118, s22, v118
	v_mul_f32_e32 v119, s22, v119
	v_mul_f32_e32 v120, s23, v120
	v_mul_f32_e32 v121, s23, v121
	v_mul_f32_e32 v122, s24, v122
	v_mul_f32_e32 v123, s24, v123
	v_mul_f32_e32 v124, s25, v124
	v_mul_f32_e32 v125, s25, v125
	v_mul_f32_e32 v126, s26, v126
	v_mul_f32_e32 v127, s26, v127
	v_mul_f32_e32 v128, s27, v128
	v_mul_f32_e32 v129, s27, v129
	v_cvt_pk_bf16_f32 v158, v114, v116
	v_cvt_pk_bf16_f32 v159, v118, v120
	v_cvt_pk_bf16_f32 v160, v122, v124
	v_cvt_pk_bf16_f32 v161, v126, v128
	v_cvt_pk_bf16_f32 v162, v115, v117
	v_cvt_pk_bf16_f32 v163, v119, v121
	v_cvt_pk_bf16_f32 v164, v123, v125
	v_cvt_pk_bf16_f32 v165, v127, v129
	ds_write_b128 v1, v[158:161] offset:19456
	ds_write_b128 v1, v[162:165] offset:19584
	v_add_u32_e32 v91, s42, v135
	v_add_u32_e32 v93, s42, v137
	ds_read_b128 v[238:241], v139 offset:0
	ds_read_b128 v[242:245], v139 offset:2048
	ds_read_b128 v[246:249], v139 offset:4096
	ds_read_b128 v[250:253], v139 offset:6144
	ds_read_b128 v[218:221], v91 offset:0
	ds_read_b128 v[222:225], v91 offset:2048
	ds_read_b128 v[226:229], v91 offset:4096
	ds_read_b128 v[230:233], v91 offset:6144
	ds_read_b128 v[234:237], v91 offset:8192
	s_waitcnt lgkmcnt(0)
; #define MU_GLDS_A(buf, kt) do { _Pragma("unroll") for (int i = 0; i < NMU; ++i) \
;         __builtin_amdgcn_global_load_lds((const unsigned*)((const char*)A + aoff[i] + (size_t)(kt) * 128), (PG8_LAS unsigned*)(MU_SA(buf) + wid * 1024 + i * 8192), 16, 0, 0); } while (0)
; #define MU_B_ISSUE(sb, kt) do { const char* kb_ = Bb + (size_t)(kt) * (64 * (size_t)RB); _Pragma("unroll") for (int j = 0; j < 8; ++j) { const char* p_ = kb_ + (size_t)j * RB; \
;         asm volatile("global_load_dwordx2 %0, %1, off" : "=&v"(sb[j]) : "v"(p_) : "memory"); } } while (0)
; #define MU_B_WAIT(sb, N) asm volatile("s_waitcnt vmcnt(%8)" : "+v"(sb[0]), "+v"(sb[1]), "+v"(sb[2]), "+v"(sb[3]), "+v"(sb[4]), "+v"(sb[5]), "+v"(sb[6]), "+v"(sb[7]) : "n"(N) : "memory")
; #define MU_COMPUTE(buf) MU_COMPUTE_N(buf, NMU)
; template <int MODE>
; __device__ __forceinline__ void moe_unit(PG8_LAS unsigned char* lds, int e, int cb, int slot0  , int nv  , const bf16_t* A, const int* slot_tok,
;                                          const float* W0, const float* W1, bf16_t* OUT, const float* slot_rs  , const int* slot_dst) {
;     ...
;     f32x4 acc[NMU][4];
; #pragma unroll
;     for (int m = 0; m < NMU; ++m)
; #pragma unroll
;         for (int n = 0; n < 4; ++n) acc[m][n] = (f32x4){0.f, 0.f, 0.f, 0.f};
;     f32x2 s0[8], s1[8];
;     float g0[8];
;     MU_GLDS_A(0, 0); MU_B_ISSUE(s0, 0); MU_G_LOAD(g0, 0); MU_B_ISSUE(s1, 1);
;     MU_B_WAIT(s0, 8); MU_B_WRITE(s0, 0, g0); __builtin_amdgcn_sched_barrier(0); MU_B_ISSUE(s0, 2);
;     asm volatile("s_waitcnt vmcnt(16)" ::: "memory");
;     asm volatile("s_waitcnt lgkmcnt(0)" ::: "memory"); __builtin_amdgcn_s_barrier(); asm volatile("" ::: "memory");
; #pragma unroll 1
;     for (int t = 0; t < nt; t += 2) {
;         if (t + 2 < nt) MU_B_WAIT(s1, 8); else MU_B_WAIT(s1, 0);
;         MU_G_LOAD(g0, t + 1); MU_B_WRITE(s1, 1, g0); __builtin_amdgcn_sched_barrier(0); MU_GLDS_A(1, t + 1); __builtin_amdgcn_sched_barrier(0);
;         if (t + 3 < nt) { MU_B_ISSUE(s1, t + 3); }
;         MU_COMPUTE(0);
;         MU_END(t + 3 >= nt);
;         if (t + 2 < nt) { MU_B_WAIT(s0, 8); MU_G_LOAD(g0, t + 2); MU_B_WRITE(s0, 0, g0); __builtin_amdgcn_sched_barrier(0); MU_GLDS_A(0, t + 2); __builtin_amdgcn_sched_barrier(0); }
;         if (t + 4 < nt) { MU_B_ISSUE(s0, t + 4); }
;         MU_COMPUTE(1);
;         MU_END(t + 4 >= nt);
	s_load_dwordx8 s[12:19], s[28:29], 0x0
	s_add_u32 s28, s28, 0x100
	s_addc_u32 s29, s29, 0
	v_mfma_f32_16x16x32_bf16 v[78:81], v[238:241], v[218:221], v[78:81]
	v_mfma_f32_16x16x32_bf16 v[74:77], v[242:245], v[218:221], v[74:77]
	v_mfma_f32_16x16x32_bf16 v[70:73], v[246:249], v[218:221], v[70:73]
	v_mfma_f32_16x16x32_bf16 v[66:69], v[250:253], v[218:221], v[66:69]
	ds_read_b128 v[218:221], v93 offset:0
	ds_read_b128 v[142:145], v141 offset:0
	v_lshl_add_u64 v[132:133], v[132:133], 0, s[40:41]
	global_load_dwordx2 v[114:115], v[132:133], off
	global_load_dwordx2 v[116:117], v[132:133], off offset:2048
	v_mfma_f32_16x16x32_bf16 v[62:65], v[238:241], v[222:225], v[62:65]
	v_mfma_f32_16x16x32_bf16 v[58:61], v[242:245], v[222:225], v[58:61]
	v_mfma_f32_16x16x32_bf16 v[54:57], v[246:249], v[222:225], v[54:57]
	v_mfma_f32_16x16x32_bf16 v[50:53], v[250:253], v[222:225], v[50:53]
	ds_read_b128 v[222:225], v93 offset:2048
	ds_read_b128 v[146:149], v141 offset:2048
	v_lshl_add_u64 v[166:167], v[132:133], 0, s[34:35]
	global_load_dwordx2 v[118:119], v[166:167], off
	global_load_dwordx2 v[120:121], v[166:167], off offset:2048
	v_mfma_f32_16x16x32_bf16 v[46:49], v[238:241], v[226:229], v[46:49]
	v_mfma_f32_16x16x32_bf16 v[42:45], v[242:245], v[226:229], v[42:45]
	v_mfma_f32_16x16x32_bf16 v[38:41], v[246:249], v[226:229], v[38:41]
	v_mfma_f32_16x16x32_bf16 v[34:37], v[250:253], v[226:229], v[34:37]
	ds_read_b128 v[226:229], v93 offset:4096
	ds_read_b128 v[150:153], v141 offset:4096
	v_lshl_add_u64 v[166:167], v[132:133], 0, s[36:37]
	global_load_dwordx2 v[122:123], v[166:167], off
	global_load_dwordx2 v[124:125], v[166:167], off offset:2048
	v_mfma_f32_16x16x32_bf16 v[18:21], v[238:241], v[230:233], v[18:21]
	v_mfma_f32_16x16x32_bf16 v[22:25], v[242:245], v[230:233], v[22:25]
	v_mfma_f32_16x16x32_bf16 v[26:29], v[246:249], v[230:233], v[26:29]
	v_mfma_f32_16x16x32_bf16 v[30:33], v[250:253], v[230:233], v[30:33]
	ds_read_b128 v[230:233], v93 offset:6144
	ds_read_b128 v[154:157], v141 offset:6144
	v_lshl_add_u64 v[166:167], v[132:133], 0, s[38:39]
	global_load_dwordx2 v[126:127], v[166:167], off
	global_load_dwordx2 v[128:129], v[166:167], off offset:2048
	v_mfma_f32_16x16x32_bf16 v[2:5], v[238:241], v[234:237], v[2:5]
	v_mfma_f32_16x16x32_bf16 v[6:9], v[242:245], v[234:237], v[6:9]
	v_mfma_f32_16x16x32_bf16 v[10:13], v[246:249], v[234:237], v[10:13]
	v_mfma_f32_16x16x32_bf16 v[14:17], v[250:253], v[234:237], v[14:17]
	ds_read_b128 v[234:237], v93 offset:8192
	s_waitcnt vmcnt(21)
	s_mov_b32 s47, s42
	s_mov_b32 s42, s43
	s_mov_b32 s43, s44
	s_mov_b32 s44, s47
	s_waitcnt lgkmcnt(0)
	s_barrier
	s_add_i32 s47, s44, s6
	s_add_u32 s30, s30, 0x80
	s_addc_u32 s31, s31, 0
	v_mfma_f32_16x16x32_bf16 v[78:81], v[142:145], v[218:221], v[78:81]
	v_mfma_f32_16x16x32_bf16 v[74:77], v[146:149], v[218:221], v[74:77]
	v_mfma_f32_16x16x32_bf16 v[70:73], v[150:153], v[218:221], v[70:73]
	v_mfma_f32_16x16x32_bf16 v[66:69], v[154:157], v[218:221], v[66:69]
	s_mov_b32 m0, s47
	s_nop 0
	global_load_lds_dwordx4 v86, s[30:31]
	v_mfma_f32_16x16x32_bf16 v[62:65], v[142:145], v[222:225], v[62:65]
	v_mfma_f32_16x16x32_bf16 v[58:61], v[146:149], v[222:225], v[58:61]
	v_mfma_f32_16x16x32_bf16 v[54:57], v[150:153], v[222:225], v[54:57]
	v_mfma_f32_16x16x32_bf16 v[50:53], v[154:157], v[222:225], v[50:53]
	s_add_i32 m0, s47, 0x2000
	s_nop 0
	global_load_lds_dwordx4 v134, s[30:31]
	v_mfma_f32_16x16x32_bf16 v[46:49], v[142:145], v[226:229], v[46:49]
	v_mfma_f32_16x16x32_bf16 v[42:45], v[146:149], v[226:229], v[42:45]
	v_mfma_f32_16x16x32_bf16 v[38:41], v[150:153], v[226:229], v[38:41]
	v_mfma_f32_16x16x32_bf16 v[34:37], v[154:157], v[226:229], v[34:37]
	s_add_i32 m0, s47, 0x4000
	s_nop 0
	global_load_lds_dwordx4 v136, s[30:31]
	v_mfma_f32_16x16x32_bf16 v[18:21], v[142:145], v[230:233], v[18:21]
	v_mfma_f32_16x16x32_bf16 v[22:25], v[146:149], v[230:233], v[22:25]
	v_mfma_f32_16x16x32_bf16 v[26:29], v[150:153], v[230:233], v[26:29]
	v_mfma_f32_16x16x32_bf16 v[30:33], v[154:157], v[230:233], v[30:33]
	s_add_i32 m0, s47, 0x6000
	s_nop 0
	global_load_lds_dwordx4 v138, s[30:31]
	v_mfma_f32_16x16x32_bf16 v[2:5], v[142:145], v[234:237], v[2:5]
	v_mfma_f32_16x16x32_bf16 v[6:9], v[146:149], v[234:237], v[6:9]
	v_mfma_f32_16x16x32_bf16 v[10:13], v[150:153], v[234:237], v[10:13]
	v_mfma_f32_16x16x32_bf16 v[14:17], v[154:157], v[234:237], v[14:17]
	s_add_i32 m0, s47, 0x8000
	s_nop 0
	global_load_lds_dwordx4 v140, s[30:31]
	v_mul_f32_e32 v186, s12, v186
	v_mul_f32_e32 v187, s12, v187
	v_mul_f32_e32 v188, s13, v188
	v_mul_f32_e32 v189, s13, v189
	v_mul_f32_e32 v190, s14, v190
	v_mul_f32_e32 v191, s14, v191
	v_mul_f32_e32 v192, s15, v192
	v_mul_f32_e32 v193, s15, v193
	v_mul_f32_e32 v194, s16, v194
	v_mul_f32_e32 v195, s16, v195
	v_mul_f32_e32 v196, s17, v196
	v_mul_f32_e32 v197, s17, v197
	v_mul_f32_e32 v198, s18, v198
	v_mul_f32_e32 v199, s18, v199
	v_mul_f32_e32 v200, s19, v200
	v_mul_f32_e32 v201, s19, v201
	v_cvt_pk_bf16_f32 v158, v186, v188
	v_cvt_pk_bf16_f32 v159, v190, v192
	v_cvt_pk_bf16_f32 v160, v194, v196
	v_cvt_pk_bf16_f32 v161, v198, v200
	v_cvt_pk_bf16_f32 v162, v187, v189
	v_cvt_pk_bf16_f32 v163, v191, v193
	v_cvt_pk_bf16_f32 v164, v195, v197
	v_cvt_pk_bf16_f32 v165, v199, v201
	ds_write_b128 v1, v[158:161] offset:0
	ds_write_b128 v1, v[162:165] offset:128
	v_add_u32_e32 v91, s42, v135
	v_add_u32_e32 v93, s42, v137
	ds_read_b128 v[238:241], v139 offset:19456
	ds_read_b128 v[242:245], v139 offset:21504
	ds_read_b128 v[246:249], v139 offset:23552
	ds_read_b128 v[250:253], v139 offset:25600
	ds_read_b128 v[218:221], v91 offset:0
	ds_read_b128 v[222:225], v91 offset:2048
	ds_read_b128 v[226:229], v91 offset:4096
	ds_read_b128 v[230:233], v91 offset:6144
	ds_read_b128 v[234:237], v91 offset:8192
	s_waitcnt lgkmcnt(0)
; #define MU_GLDS_A(buf, kt) do { _Pragma("unroll") for (int i = 0; i < NMU; ++i) \
;         __builtin_amdgcn_global_load_lds((const unsigned*)((const char*)A + aoff[i] + (size_t)(kt) * 128), (PG8_LAS unsigned*)(MU_SA(buf) + wid * 1024 + i * 8192), 16, 0, 0); } while (0)
; #define MU_B_ISSUE(sb, kt) do { const char* kb_ = Bb + (size_t)(kt) * (64 * (size_t)RB); _Pragma("unroll") for (int j = 0; j < 8; ++j) { const char* p_ = kb_ + (size_t)j * RB; \
;         asm volatile("global_load_dwordx2 %0, %1, off" : "=&v"(sb[j]) : "v"(p_) : "memory"); } } while (0)
; #define MU_B_WAIT(sb, N) asm volatile("s_waitcnt vmcnt(%8)" : "+v"(sb[0]), "+v"(sb[1]), "+v"(sb[2]), "+v"(sb[3]), "+v"(sb[4]), "+v"(sb[5]), "+v"(sb[6]), "+v"(sb[7]) : "n"(N) : "memory")
; #define MU_COMPUTE(buf) MU_COMPUTE_N(buf, NMU)
; template <int MODE>
; __device__ __forceinline__ void moe_unit(PG8_LAS unsigned char* lds, int e, int cb, int slot0  , int nv  , const bf16_t* A, const int* slot_tok,
;                                          const float* W0, const float* W1, bf16_t* OUT, const float* slot_rs  , const int* slot_dst) {
;     ...
;     f32x4 acc[NMU][4];
; #pragma unroll
;     for (int m = 0; m < NMU; ++m)
; #pragma unroll
;         for (int n = 0; n < 4; ++n) acc[m][n] = (f32x4){0.f, 0.f, 0.f, 0.f};
;     f32x2 s0[8], s1[8];
;     float g0[8];
;     MU_GLDS_A(0, 0); MU_B_ISSUE(s0, 0); MU_G_LOAD(g0, 0); MU_B_ISSUE(s1, 1);
;     MU_B_WAIT(s0, 8); MU_B_WRITE(s0, 0, g0); __builtin_amdgcn_sched_barrier(0); MU_B_ISSUE(s0, 2);
;     asm volatile("s_waitcnt vmcnt(16)" ::: "memory");
;     asm volatile("s_waitcnt lgkmcnt(0)" ::: "memory"); __builtin_amdgcn_s_barrier(); asm volatile("" ::: "memory");
; #pragma unroll 1
;     for (int t = 0; t < nt; t += 2) {
;         if (t + 2 < nt) MU_B_WAIT(s1, 8); else MU_B_WAIT(s1, 0);
;         MU_G_LOAD(g0, t + 1); MU_B_WRITE(s1, 1, g0); __builtin_amdgcn_sched_barrier(0); MU_GLDS_A(1, t + 1); __builtin_amdgcn_sched_barrier(0);
;         if (t + 3 < nt) { MU_B_ISSUE(s1, t + 3); }
;         MU_COMPUTE(0);
;         MU_END(t + 3 >= nt);
;         if (t + 2 < nt) { MU_B_WAIT(s0, 8); MU_G_LOAD(g0, t + 2); MU_B_WRITE(s0, 0, g0); __builtin_amdgcn_sched_barrier(0); MU_GLDS_A(0, t + 2); __builtin_amdgcn_sched_barrier(0); }
;         if (t + 4 < nt) { MU_B_ISSUE(s0, t + 4); }
;         MU_COMPUTE(1);
;         MU_END(t + 4 >= nt);
	s_load_dwordx8 s[20:27], s[28:29], 0x0
	s_add_u32 s28, s28, 0x100
	s_addc_u32 s29, s29, 0
	v_mfma_f32_16x16x32_bf16 v[78:81], v[238:241], v[218:221], v[78:81]
	v_mfma_f32_16x16x32_bf16 v[74:77], v[242:245], v[218:221], v[74:77]
	v_mfma_f32_16x16x32_bf16 v[70:73], v[246:249], v[218:221], v[70:73]
	v_mfma_f32_16x16x32_bf16 v[66:69], v[250:253], v[218:221], v[66:69]
	ds_read_b128 v[218:221], v93 offset:0
	ds_read_b128 v[142:145], v141 offset:19456
	v_lshl_add_u64 v[132:133], v[132:133], 0, s[40:41]
	global_load_dwordx2 v[186:187], v[132:133], off
	global_load_dwordx2 v[188:189], v[132:133], off offset:2048
	v_mfma_f32_16x16x32_bf16 v[62:65], v[238:241], v[222:225], v[62:65]
	v_mfma_f32_16x16x32_bf16 v[58:61], v[242:245], v[222:225], v[58:61]
	v_mfma_f32_16x16x32_bf16 v[54:57], v[246:249], v[222:225], v[54:57]
	v_mfma_f32_16x16x32_bf16 v[50:53], v[250:253], v[222:225], v[50:53]
	ds_read_b128 v[222:225], v93 offset:2048
	ds_read_b128 v[146:149], v141 offset:21504
	v_lshl_add_u64 v[166:167], v[132:133], 0, s[34:35]
	global_load_dwordx2 v[190:191], v[166:167], off
	global_load_dwordx2 v[192:193], v[166:167], off offset:2048
	v_mfma_f32_16x16x32_bf16 v[46:49], v[238:241], v[226:229], v[46:49]
	v_mfma_f32_16x16x32_bf16 v[42:45], v[242:245], v[226:229], v[42:45]
	v_mfma_f32_16x16x32_bf16 v[38:41], v[246:249], v[226:229], v[38:41]
	v_mfma_f32_16x16x32_bf16 v[34:37], v[250:253], v[226:229], v[34:37]
	ds_read_b128 v[226:229], v93 offset:4096
	ds_read_b128 v[150:153], v141 offset:23552
	v_lshl_add_u64 v[166:167], v[132:133], 0, s[36:37]
	global_load_dwordx2 v[194:195], v[166:167], off
	global_load_dwordx2 v[196:197], v[166:167], off offset:2048
	v_mfma_f32_16x16x32_bf16 v[18:21], v[238:241], v[230:233], v[18:21]
	v_mfma_f32_16x16x32_bf16 v[22:25], v[242:245], v[230:233], v[22:25]
	v_mfma_f32_16x16x32_bf16 v[26:29], v[246:249], v[230:233], v[26:29]
	v_mfma_f32_16x16x32_bf16 v[30:33], v[250:253], v[230:233], v[30:33]
	ds_read_b128 v[230:233], v93 offset:6144
	ds_read_b128 v[154:157], v141 offset:25600
	v_lshl_add_u64 v[166:167], v[132:133], 0, s[38:39]
	global_load_dwordx2 v[198:199], v[166:167], off
	global_load_dwordx2 v[200:201], v[166:167], off offset:2048
	v_mfma_f32_16x16x32_bf16 v[2:5], v[238:241], v[234:237], v[2:5]
	v_mfma_f32_16x16x32_bf16 v[6:9], v[242:245], v[234:237], v[6:9]
	v_mfma_f32_16x16x32_bf16 v[10:13], v[246:249], v[234:237], v[10:13]
	v_mfma_f32_16x16x32_bf16 v[14:17], v[250:253], v[234:237], v[14:17]
	ds_read_b128 v[234:237], v93 offset:8192
	s_waitcnt vmcnt(21)
	s_mov_b32 s47, s42
	s_mov_b32 s42, s43
	s_mov_b32 s43, s44
	s_mov_b32 s44, s47
	s_waitcnt lgkmcnt(0)
	s_barrier
	s_add_i32 s47, s44, s6
	s_add_u32 s30, s30, 0x80
	s_addc_u32 s31, s31, 0
	v_mfma_f32_16x16x32_bf16 v[78:81], v[142:145], v[218:221], v[78:81]
	v_mfma_f32_16x16x32_bf16 v[74:77], v[146:149], v[218:221], v[74:77]
	v_mfma_f32_16x16x32_bf16 v[70:73], v[150:153], v[218:221], v[70:73]
	v_mfma_f32_16x16x32_bf16 v[66:69], v[154:157], v[218:221], v[66:69]
	s_mov_b32 m0, s47
	s_nop 0
	global_load_lds_dwordx4 v86, s[30:31]
	v_mfma_f32_16x16x32_bf16 v[62:65], v[142:145], v[222:225], v[62:65]
	v_mfma_f32_16x16x32_bf16 v[58:61], v[146:149], v[222:225], v[58:61]
	v_mfma_f32_16x16x32_bf16 v[54:57], v[150:153], v[222:225], v[54:57]
	v_mfma_f32_16x16x32_bf16 v[50:53], v[154:157], v[222:225], v[50:53]
	s_add_i32 m0, s47, 0x2000
	s_nop 0
	global_load_lds_dwordx4 v134, s[30:31]
	v_mfma_f32_16x16x32_bf16 v[46:49], v[142:145], v[226:229], v[46:49]
	v_mfma_f32_16x16x32_bf16 v[42:45], v[146:149], v[226:229], v[42:45]
	v_mfma_f32_16x16x32_bf16 v[38:41], v[150:153], v[226:229], v[38:41]
	v_mfma_f32_16x16x32_bf16 v[34:37], v[154:157], v[226:229], v[34:37]
	s_add_i32 m0, s47, 0x4000
	s_nop 0
	global_load_lds_dwordx4 v136, s[30:31]
	v_mfma_f32_16x16x32_bf16 v[18:21], v[142:145], v[230:233], v[18:21]
	v_mfma_f32_16x16x32_bf16 v[22:25], v[146:149], v[230:233], v[22:25]
	v_mfma_f32_16x16x32_bf16 v[26:29], v[150:153], v[230:233], v[26:29]
	v_mfma_f32_16x16x32_bf16 v[30:33], v[154:157], v[230:233], v[30:33]
	s_add_i32 m0, s47, 0x6000
	s_nop 0
	global_load_lds_dwordx4 v138, s[30:31]
	v_mfma_f32_16x16x32_bf16 v[2:5], v[142:145], v[234:237], v[2:5]
	v_mfma_f32_16x16x32_bf16 v[6:9], v[146:149], v[234:237], v[6:9]
	v_mfma_f32_16x16x32_bf16 v[10:13], v[150:153], v[234:237], v[10:13]
	v_mfma_f32_16x16x32_bf16 v[14:17], v[154:157], v[234:237], v[14:17]
	s_add_i32 m0, s47, 0x8000
	s_nop 0
	global_load_lds_dwordx4 v140, s[30:31]
	v_mul_f32_e32 v202, s20, v202
	v_mul_f32_e32 v203, s20, v203
	v_mul_f32_e32 v204, s21, v204
	v_mul_f32_e32 v205, s21, v205
	v_mul_f32_e32 v206, s22, v206
	v_mul_f32_e32 v207, s22, v207
	v_mul_f32_e32 v208, s23, v208
	v_mul_f32_e32 v209, s23, v209
	v_mul_f32_e32 v210, s24, v210
	v_mul_f32_e32 v211, s24, v211
	v_mul_f32_e32 v212, s25, v212
	v_mul_f32_e32 v213, s25, v213
	v_mul_f32_e32 v214, s26, v214
	v_mul_f32_e32 v215, s26, v215
	v_mul_f32_e32 v216, s27, v216
	v_mul_f32_e32 v217, s27, v217
	v_cvt_pk_bf16_f32 v158, v202, v204
	v_cvt_pk_bf16_f32 v159, v206, v208
	v_cvt_pk_bf16_f32 v160, v210, v212
	v_cvt_pk_bf16_f32 v161, v214, v216
	v_cvt_pk_bf16_f32 v162, v203, v205
	v_cvt_pk_bf16_f32 v163, v207, v209
	v_cvt_pk_bf16_f32 v164, v211, v213
	v_cvt_pk_bf16_f32 v165, v215, v217
	ds_write_b128 v1, v[158:161] offset:19456
	ds_write_b128 v1, v[162:165] offset:19584
	v_add_u32_e32 v91, s42, v135
	v_add_u32_e32 v93, s42, v137
	ds_read_b128 v[238:241], v139 offset:0
	ds_read_b128 v[242:245], v139 offset:2048
	ds_read_b128 v[246:249], v139 offset:4096
	ds_read_b128 v[250:253], v139 offset:6144
	ds_read_b128 v[218:221], v91 offset:0
	ds_read_b128 v[222:225], v91 offset:2048
	ds_read_b128 v[226:229], v91 offset:4096
	ds_read_b128 v[230:233], v91 offset:6144
	ds_read_b128 v[234:237], v91 offset:8192
	s_waitcnt lgkmcnt(0)
; #define MU_GLDS_A(buf, kt) do { _Pragma("unroll") for (int i = 0; i < NMU; ++i) \
;         __builtin_amdgcn_global_load_lds((const unsigned*)((const char*)A + aoff[i] + (size_t)(kt) * 128), (PG8_LAS unsigned*)(MU_SA(buf) + wid * 1024 + i * 8192), 16, 0, 0); } while (0)
; #define MU_B_ISSUE(sb, kt) do { const char* kb_ = Bb + (size_t)(kt) * (64 * (size_t)RB); _Pragma("unroll") for (int j = 0; j < 8; ++j) { const char* p_ = kb_ + (size_t)j * RB; \
;         asm volatile("global_load_dwordx2 %0, %1, off" : "=&v"(sb[j]) : "v"(p_) : "memory"); } } while (0)
; #define MU_B_WAIT(sb, N) asm volatile("s_waitcnt vmcnt(%8)" : "+v"(sb[0]), "+v"(sb[1]), "+v"(sb[2]), "+v"(sb[3]), "+v"(sb[4]), "+v"(sb[5]), "+v"(sb[6]), "+v"(sb[7]) : "n"(N) : "memory")
; #define MU_COMPUTE(buf) MU_COMPUTE_N(buf, NMU)
; template <int MODE>
; __device__ __forceinline__ void moe_unit(PG8_LAS unsigned char* lds, int e, int cb, int slot0  , int nv  , const bf16_t* A, const int* slot_tok,
;                                          const float* W0, const float* W1, bf16_t* OUT, const float* slot_rs  , const int* slot_dst) {
;     ...
;     f32x4 acc[NMU][4];
; #pragma unroll
;     for (int m = 0; m < NMU; ++m)
; #pragma unroll
;         for (int n = 0; n < 4; ++n) acc[m][n] = (f32x4){0.f, 0.f, 0.f, 0.f};
;     f32x2 s0[8], s1[8];
;     float g0[8];
;     MU_GLDS_A(0, 0); MU_B_ISSUE(s0, 0); MU_G_LOAD(g0, 0); MU_B_ISSUE(s1, 1);
;     MU_B_WAIT(s0, 8); MU_B_WRITE(s0, 0, g0); __builtin_amdgcn_sched_barrier(0); MU_B_ISSUE(s0, 2);
;     asm volatile("s_waitcnt vmcnt(16)" ::: "memory");
;     asm volatile("s_waitcnt lgkmcnt(0)" ::: "memory"); __builtin_amdgcn_s_barrier(); asm volatile("" ::: "memory");
; #pragma unroll 1
;     for (int t = 0; t < nt; t += 2) {
;         if (t + 2 < nt) MU_B_WAIT(s1, 8); else MU_B_WAIT(s1, 0);
;         MU_G_LOAD(g0, t + 1); MU_B_WRITE(s1, 1, g0); __builtin_amdgcn_sched_barrier(0); MU_GLDS_A(1, t + 1); __builtin_amdgcn_sched_barrier(0);
;         if (t + 3 < nt) { MU_B_ISSUE(s1, t + 3); }
;         MU_COMPUTE(0);
;         MU_END(t + 3 >= nt);
;         if (t + 2 < nt) { MU_B_WAIT(s0, 8); MU_G_LOAD(g0, t + 2); MU_B_WRITE(s0, 0, g0); __builtin_amdgcn_sched_barrier(0); MU_GLDS_A(0, t + 2); __builtin_amdgcn_sched_barrier(0); }
;         if (t + 4 < nt) { MU_B_ISSUE(s0, t + 4); }
;         MU_COMPUTE(1);
;         MU_END(t + 4 >= nt);
	s_load_dwordx8 s[12:19], s[28:29], 0x0
	s_add_u32 s28, s28, 0x100
	s_addc_u32 s29, s29, 0
	v_mfma_f32_16x16x32_bf16 v[78:81], v[238:241], v[218:221], v[78:81]
	v_mfma_f32_16x16x32_bf16 v[74:77], v[242:245], v[218:221], v[74:77]
	v_mfma_f32_16x16x32_bf16 v[70:73], v[246:249], v[218:221], v[70:73]
	v_mfma_f32_16x16x32_bf16 v[66:69], v[250:253], v[218:221], v[66:69]
	ds_read_b128 v[218:221], v93 offset:0
	ds_read_b128 v[142:145], v141 offset:0
	v_lshl_add_u64 v[132:133], v[132:133], 0, s[40:41]
	global_load_dwordx2 v[202:203], v[132:133], off
	global_load_dwordx2 v[204:205], v[132:133], off offset:2048
	v_mfma_f32_16x16x32_bf16 v[62:65], v[238:241], v[222:225], v[62:65]
	v_mfma_f32_16x16x32_bf16 v[58:61], v[242:245], v[222:225], v[58:61]
	v_mfma_f32_16x16x32_bf16 v[54:57], v[246:249], v[222:225], v[54:57]
	v_mfma_f32_16x16x32_bf16 v[50:53], v[250:253], v[222:225], v[50:53]
	ds_read_b128 v[222:225], v93 offset:2048
	ds_read_b128 v[146:149], v141 offset:2048
	v_lshl_add_u64 v[166:167], v[132:133], 0, s[34:35]
	global_load_dwordx2 v[206:207], v[166:167], off
	global_load_dwordx2 v[208:209], v[166:167], off offset:2048
	v_mfma_f32_16x16x32_bf16 v[46:49], v[238:241], v[226:229], v[46:49]
	v_mfma_f32_16x16x32_bf16 v[42:45], v[242:245], v[226:229], v[42:45]
	v_mfma_f32_16x16x32_bf16 v[38:41], v[246:249], v[226:229], v[38:41]
	v_mfma_f32_16x16x32_bf16 v[34:37], v[250:253], v[226:229], v[34:37]
	ds_read_b128 v[226:229], v93 offset:4096
	ds_read_b128 v[150:153], v141 offset:4096
	v_lshl_add_u64 v[166:167], v[132:133], 0, s[36:37]
	global_load_dwordx2 v[210:211], v[166:167], off
	global_load_dwordx2 v[212:213], v[166:167], off offset:2048
	v_mfma_f32_16x16x32_bf16 v[18:21], v[238:241], v[230:233], v[18:21]
	v_mfma_f32_16x16x32_bf16 v[22:25], v[242:245], v[230:233], v[22:25]
	v_mfma_f32_16x16x32_bf16 v[26:29], v[246:249], v[230:233], v[26:29]
	v_mfma_f32_16x16x32_bf16 v[30:33], v[250:253], v[230:233], v[30:33]
	ds_read_b128 v[230:233], v93 offset:6144
	ds_read_b128 v[154:157], v141 offset:6144
	v_lshl_add_u64 v[166:167], v[132:133], 0, s[38:39]
	global_load_dwordx2 v[214:215], v[166:167], off
	global_load_dwordx2 v[216:217], v[166:167], off offset:2048
	v_mfma_f32_16x16x32_bf16 v[2:5], v[238:241], v[234:237], v[2:5]
	v_mfma_f32_16x16x32_bf16 v[6:9], v[242:245], v[234:237], v[6:9]
	v_mfma_f32_16x16x32_bf16 v[10:13], v[246:249], v[234:237], v[10:13]
	v_mfma_f32_16x16x32_bf16 v[14:17], v[250:253], v[234:237], v[14:17]
	ds_read_b128 v[234:237], v93 offset:8192
	s_waitcnt vmcnt(21)
	s_mov_b32 s47, s42
	s_mov_b32 s42, s43
	s_mov_b32 s43, s44
	s_mov_b32 s44, s47
	s_waitcnt lgkmcnt(0)
	s_barrier
	s_add_i32 s47, s44, s6
	s_add_u32 s30, s30, 0x80
	s_addc_u32 s31, s31, 0
	v_mfma_f32_16x16x32_bf16 v[78:81], v[142:145], v[218:221], v[78:81]
	v_mfma_f32_16x16x32_bf16 v[74:77], v[146:149], v[218:221], v[74:77]
	v_mfma_f32_16x16x32_bf16 v[70:73], v[150:153], v[218:221], v[70:73]
	v_mfma_f32_16x16x32_bf16 v[66:69], v[154:157], v[218:221], v[66:69]
	s_mov_b32 m0, s47
	s_nop 0
	global_load_lds_dwordx4 v86, s[30:31]
	v_mfma_f32_16x16x32_bf16 v[62:65], v[142:145], v[222:225], v[62:65]
	v_mfma_f32_16x16x32_bf16 v[58:61], v[146:149], v[222:225], v[58:61]
	v_mfma_f32_16x16x32_bf16 v[54:57], v[150:153], v[222:225], v[54:57]
	v_mfma_f32_16x16x32_bf16 v[50:53], v[154:157], v[222:225], v[50:53]
	s_add_i32 m0, s47, 0x2000
	s_nop 0
	global_load_lds_dwordx4 v134, s[30:31]
	v_mfma_f32_16x16x32_bf16 v[46:49], v[142:145], v[226:229], v[46:49]
	v_mfma_f32_16x16x32_bf16 v[42:45], v[146:149], v[226:229], v[42:45]
	v_mfma_f32_16x16x32_bf16 v[38:41], v[150:153], v[226:229], v[38:41]
	v_mfma_f32_16x16x32_bf16 v[34:37], v[154:157], v[226:229], v[34:37]
	s_add_i32 m0, s47, 0x4000
	s_nop 0
	global_load_lds_dwordx4 v136, s[30:31]
	v_mfma_f32_16x16x32_bf16 v[18:21], v[142:145], v[230:233], v[18:21]
	v_mfma_f32_16x16x32_bf16 v[22:25], v[146:149], v[230:233], v[22:25]
	v_mfma_f32_16x16x32_bf16 v[26:29], v[150:153], v[230:233], v[26:29]
	v_mfma_f32_16x16x32_bf16 v[30:33], v[154:157], v[230:233], v[30:33]
	s_add_i32 m0, s47, 0x6000
	s_nop 0
	global_load_lds_dwordx4 v138, s[30:31]
	v_mfma_f32_16x16x32_bf16 v[2:5], v[142:145], v[234:237], v[2:5]
	v_mfma_f32_16x16x32_bf16 v[6:9], v[146:149], v[234:237], v[6:9]
	v_mfma_f32_16x16x32_bf16 v[10:13], v[150:153], v[234:237], v[10:13]
	v_mfma_f32_16x16x32_bf16 v[14:17], v[154:157], v[234:237], v[14:17]
	s_add_i32 m0, s47, 0x8000
	s_nop 0
	global_load_lds_dwordx4 v140, s[30:31]
	v_mul_f32_e32 v98, s12, v98
	v_mul_f32_e32 v99, s12, v99
	v_mul_f32_e32 v100, s13, v100
	v_mul_f32_e32 v101, s13, v101
	v_mul_f32_e32 v102, s14, v102
	v_mul_f32_e32 v103, s14, v103
	v_mul_f32_e32 v104, s15, v104
	v_mul_f32_e32 v105, s15, v105
	v_mul_f32_e32 v106, s16, v106
	v_mul_f32_e32 v107, s16, v107
	v_mul_f32_e32 v108, s17, v108
	v_mul_f32_e32 v109, s17, v109
	v_mul_f32_e32 v110, s18, v110
	v_mul_f32_e32 v111, s18, v111
	v_mul_f32_e32 v112, s19, v112
	v_mul_f32_e32 v113, s19, v113
	v_cvt_pk_bf16_f32 v158, v98, v100
	v_cvt_pk_bf16_f32 v159, v102, v104
	v_cvt_pk_bf16_f32 v160, v106, v108
	v_cvt_pk_bf16_f32 v161, v110, v112
	v_cvt_pk_bf16_f32 v162, v99, v101
	v_cvt_pk_bf16_f32 v163, v103, v105
	v_cvt_pk_bf16_f32 v164, v107, v109
	v_cvt_pk_bf16_f32 v165, v111, v113
	ds_write_b128 v1, v[158:161] offset:0
	ds_write_b128 v1, v[162:165] offset:128
	v_add_u32_e32 v91, s42, v135
	v_add_u32_e32 v93, s42, v137
	ds_read_b128 v[238:241], v139 offset:19456
	ds_read_b128 v[242:245], v139 offset:21504
	ds_read_b128 v[246:249], v139 offset:23552
	ds_read_b128 v[250:253], v139 offset:25600
	ds_read_b128 v[218:221], v91 offset:0
	ds_read_b128 v[222:225], v91 offset:2048
	ds_read_b128 v[226:229], v91 offset:4096
	ds_read_b128 v[230:233], v91 offset:6144
	ds_read_b128 v[234:237], v91 offset:8192
	s_waitcnt lgkmcnt(0)
; #define MU_GLDS_A(buf, kt) do { _Pragma("unroll") for (int i = 0; i < NMU; ++i) \
;         __builtin_amdgcn_global_load_lds((const unsigned*)((const char*)A + aoff[i] + (size_t)(kt) * 128), (PG8_LAS unsigned*)(MU_SA(buf) + wid * 1024 + i * 8192), 16, 0, 0); } while (0)
; #define MU_B_ISSUE(sb, kt) do { const char* kb_ = Bb + (size_t)(kt) * (64 * (size_t)RB); _Pragma("unroll") for (int j = 0; j < 8; ++j) { const char* p_ = kb_ + (size_t)j * RB; \
;         asm volatile("global_load_dwordx2 %0, %1, off" : "=&v"(sb[j]) : "v"(p_) : "memory"); } } while (0)
; #define MU_B_WAIT(sb, N) asm volatile("s_waitcnt vmcnt(%8)" : "+v"(sb[0]), "+v"(sb[1]), "+v"(sb[2]), "+v"(sb[3]), "+v"(sb[4]), "+v"(sb[5]), "+v"(sb[6]), "+v"(sb[7]) : "n"(N) : "memory")
; #define MU_COMPUTE(buf) MU_COMPUTE_N(buf, NMU)
; template <int MODE>
; __device__ __forceinline__ void moe_unit(PG8_LAS unsigned char* lds, int e, int cb, int slot0  , int nv  , const bf16_t* A, const int* slot_tok,
;                                          const float* W0, const float* W1, bf16_t* OUT, const float* slot_rs  , const int* slot_dst) {
;     ...
;     f32x4 acc[NMU][4];
; #pragma unroll
;     for (int m = 0; m < NMU; ++m)
; #pragma unroll
;         for (int n = 0; n < 4; ++n) acc[m][n] = (f32x4){0.f, 0.f, 0.f, 0.f};
;     f32x2 s0[8], s1[8];
;     float g0[8];
;     MU_GLDS_A(0, 0); MU_B_ISSUE(s0, 0); MU_G_LOAD(g0, 0); MU_B_ISSUE(s1, 1);
;     MU_B_WAIT(s0, 8); MU_B_WRITE(s0, 0, g0); __builtin_amdgcn_sched_barrier(0); MU_B_ISSUE(s0, 2);
;     asm volatile("s_waitcnt vmcnt(16)" ::: "memory");
;     asm volatile("s_waitcnt lgkmcnt(0)" ::: "memory"); __builtin_amdgcn_s_barrier(); asm volatile("" ::: "memory");
; #pragma unroll 1
;     for (int t = 0; t < nt; t += 2) {
;         if (t + 2 < nt) MU_B_WAIT(s1, 8); else MU_B_WAIT(s1, 0);
;         MU_G_LOAD(g0, t + 1); MU_B_WRITE(s1, 1, g0); __builtin_amdgcn_sched_barrier(0); MU_GLDS_A(1, t + 1); __builtin_amdgcn_sched_barrier(0);
;         if (t + 3 < nt) { MU_B_ISSUE(s1, t + 3); }
;         MU_COMPUTE(0);
;         MU_END(t + 3 >= nt);
;         if (t + 2 < nt) { MU_B_WAIT(s0, 8); MU_G_LOAD(g0, t + 2); MU_B_WRITE(s0, 0, g0); __builtin_amdgcn_sched_barrier(0); MU_GLDS_A(0, t + 2); __builtin_amdgcn_sched_barrier(0); }
;         if (t + 4 < nt) { MU_B_ISSUE(s0, t + 4); }
;         MU_COMPUTE(1);
;         MU_END(t + 4 >= nt);
	s_load_dwordx8 s[20:27], s[28:29], 0x0
	s_add_u32 s28, s28, 0x100
	s_addc_u32 s29, s29, 0
	v_mfma_f32_16x16x32_bf16 v[78:81], v[238:241], v[218:221], v[78:81]
	v_mfma_f32_16x16x32_bf16 v[74:77], v[242:245], v[218:221], v[74:77]
	v_mfma_f32_16x16x32_bf16 v[70:73], v[246:249], v[218:221], v[70:73]
	v_mfma_f32_16x16x32_bf16 v[66:69], v[250:253], v[218:221], v[66:69]
	ds_read_b128 v[218:221], v93 offset:0
	ds_read_b128 v[142:145], v141 offset:19456
	v_lshl_add_u64 v[132:133], v[132:133], 0, s[40:41]
	global_load_dwordx2 v[98:99], v[132:133], off
	global_load_dwordx2 v[100:101], v[132:133], off offset:2048
	v_mfma_f32_16x16x32_bf16 v[62:65], v[238:241], v[222:225], v[62:65]
	v_mfma_f32_16x16x32_bf16 v[58:61], v[242:245], v[222:225], v[58:61]
	v_mfma_f32_16x16x32_bf16 v[54:57], v[246:249], v[222:225], v[54:57]
	v_mfma_f32_16x16x32_bf16 v[50:53], v[250:253], v[222:225], v[50:53]
	ds_read_b128 v[222:225], v93 offset:2048
	ds_read_b128 v[146:149], v141 offset:21504
	v_lshl_add_u64 v[166:167], v[132:133], 0, s[34:35]
	global_load_dwordx2 v[102:103], v[166:167], off
	global_load_dwordx2 v[104:105], v[166:167], off offset:2048
	v_mfma_f32_16x16x32_bf16 v[46:49], v[238:241], v[226:229], v[46:49]
	v_mfma_f32_16x16x32_bf16 v[42:45], v[242:245], v[226:229], v[42:45]
	v_mfma_f32_16x16x32_bf16 v[38:41], v[246:249], v[226:229], v[38:41]
	v_mfma_f32_16x16x32_bf16 v[34:37], v[250:253], v[226:229], v[34:37]
	ds_read_b128 v[226:229], v93 offset:4096
	ds_read_b128 v[150:153], v141 offset:23552
	v_lshl_add_u64 v[166:167], v[132:133], 0, s[36:37]
	global_load_dwordx2 v[106:107], v[166:167], off
	global_load_dwordx2 v[108:109], v[166:167], off offset:2048
	v_mfma_f32_16x16x32_bf16 v[18:21], v[238:241], v[230:233], v[18:21]
	v_mfma_f32_16x16x32_bf16 v[22:25], v[242:245], v[230:233], v[22:25]
	v_mfma_f32_16x16x32_bf16 v[26:29], v[246:249], v[230:233], v[26:29]
	v_mfma_f32_16x16x32_bf16 v[30:33], v[250:253], v[230:233], v[30:33]
	ds_read_b128 v[230:233], v93 offset:6144
	ds_read_b128 v[154:157], v141 offset:25600
	v_lshl_add_u64 v[166:167], v[132:133], 0, s[38:39]
	global_load_dwordx2 v[110:111], v[166:167], off
	global_load_dwordx2 v[112:113], v[166:167], off offset:2048
	v_mfma_f32_16x16x32_bf16 v[2:5], v[238:241], v[234:237], v[2:5]
	v_mfma_f32_16x16x32_bf16 v[6:9], v[242:245], v[234:237], v[6:9]
	v_mfma_f32_16x16x32_bf16 v[10:13], v[246:249], v[234:237], v[10:13]
	v_mfma_f32_16x16x32_bf16 v[14:17], v[250:253], v[234:237], v[14:17]
	ds_read_b128 v[234:237], v93 offset:8192
	s_waitcnt vmcnt(21)
	s_mov_b32 s47, s42
	s_mov_b32 s42, s43
	s_mov_b32 s43, s44
	s_mov_b32 s44, s47
	s_waitcnt lgkmcnt(0)
	s_barrier
	s_sub_u32 s46, s46, 1
	s_cmp_lg_u32 s46, 0
	s_cbranch_scc1 .Lmu_loop_Y5
	s_add_i32 s47, s44, s6
	s_add_u32 s30, s30, 0x80
	s_addc_u32 s31, s31, 0
	v_mfma_f32_16x16x32_bf16 v[78:81], v[142:145], v[218:221], v[78:81]
	v_mfma_f32_16x16x32_bf16 v[74:77], v[146:149], v[218:221], v[74:77]
	v_mfma_f32_16x16x32_bf16 v[70:73], v[150:153], v[218:221], v[70:73]
	v_mfma_f32_16x16x32_bf16 v[66:69], v[154:157], v[218:221], v[66:69]
	s_mov_b32 m0, s47
	s_nop 0
	global_load_lds_dwordx4 v86, s[30:31]
	v_mfma_f32_16x16x32_bf16 v[62:65], v[142:145], v[222:225], v[62:65]
	v_mfma_f32_16x16x32_bf16 v[58:61], v[146:149], v[222:225], v[58:61]
	v_mfma_f32_16x16x32_bf16 v[54:57], v[150:153], v[222:225], v[54:57]
	v_mfma_f32_16x16x32_bf16 v[50:53], v[154:157], v[222:225], v[50:53]
	s_add_i32 m0, s47, 0x2000
	s_nop 0
	global_load_lds_dwordx4 v134, s[30:31]
	v_mfma_f32_16x16x32_bf16 v[46:49], v[142:145], v[226:229], v[46:49]
	v_mfma_f32_16x16x32_bf16 v[42:45], v[146:149], v[226:229], v[42:45]
	v_mfma_f32_16x16x32_bf16 v[38:41], v[150:153], v[226:229], v[38:41]
	v_mfma_f32_16x16x32_bf16 v[34:37], v[154:157], v[226:229], v[34:37]
	s_add_i32 m0, s47, 0x4000
	s_nop 0
	global_load_lds_dwordx4 v136, s[30:31]
	v_mfma_f32_16x16x32_bf16 v[18:21], v[142:145], v[230:233], v[18:21]
	v_mfma_f32_16x16x32_bf16 v[22:25], v[146:149], v[230:233], v[22:25]
	v_mfma_f32_16x16x32_bf16 v[26:29], v[150:153], v[230:233], v[26:29]
	v_mfma_f32_16x16x32_bf16 v[30:33], v[154:157], v[230:233], v[30:33]
	s_add_i32 m0, s47, 0x6000
	s_nop 0
	global_load_lds_dwordx4 v138, s[30:31]
	v_mfma_f32_16x16x32_bf16 v[2:5], v[142:145], v[234:237], v[2:5]
	v_mfma_f32_16x16x32_bf16 v[6:9], v[146:149], v[234:237], v[6:9]
	v_mfma_f32_16x16x32_bf16 v[10:13], v[150:153], v[234:237], v[10:13]
	v_mfma_f32_16x16x32_bf16 v[14:17], v[154:157], v[234:237], v[14:17]
	s_add_i32 m0, s47, 0x8000
	s_nop 0
	global_load_lds_dwordx4 v140, s[30:31]
	v_mul_f32_e32 v114, s20, v114
	v_mul_f32_e32 v115, s20, v115
	v_mul_f32_e32 v116, s21, v116
	v_mul_f32_e32 v117, s21, v117
	v_mul_f32_e32 v118, s22, v118
	v_mul_f32_e32 v119, s22, v119
	v_mul_f32_e32 v120, s23, v120
	v_mul_f32_e32 v121, s23, v121
	v_mul_f32_e32 v122, s24, v122
	v_mul_f32_e32 v123, s24, v123
	v_mul_f32_e32 v124, s25, v124
	v_mul_f32_e32 v125, s25, v125
	v_mul_f32_e32 v126, s26, v126
	v_mul_f32_e32 v127, s26, v127
	v_mul_f32_e32 v128, s27, v128
	v_mul_f32_e32 v129, s27, v129
	v_cvt_pk_bf16_f32 v158, v114, v116
	v_cvt_pk_bf16_f32 v159, v118, v120
	v_cvt_pk_bf16_f32 v160, v122, v124
	v_cvt_pk_bf16_f32 v161, v126, v128
	v_cvt_pk_bf16_f32 v162, v115, v117
	v_cvt_pk_bf16_f32 v163, v119, v121
	v_cvt_pk_bf16_f32 v164, v123, v125
	v_cvt_pk_bf16_f32 v165, v127, v129
	ds_write_b128 v1, v[158:161] offset:19456
	ds_write_b128 v1, v[162:165] offset:19584
	v_add_u32_e32 v91, s42, v135
	v_add_u32_e32 v93, s42, v137
	ds_read_b128 v[238:241], v139 offset:0
	ds_read_b128 v[242:245], v139 offset:2048
	ds_read_b128 v[246:249], v139 offset:4096
	ds_read_b128 v[250:253], v139 offset:6144
	ds_read_b128 v[218:221], v91 offset:0
	ds_read_b128 v[222:225], v91 offset:2048
	ds_read_b128 v[226:229], v91 offset:4096
	ds_read_b128 v[230:233], v91 offset:6144
	ds_read_b128 v[234:237], v91 offset:8192
	s_waitcnt lgkmcnt(0)
; #define MU_GLDS_A(buf, kt) do { _Pragma("unroll") for (int i = 0; i < NMU; ++i) \
;         __builtin_amdgcn_global_load_lds((const unsigned*)((const char*)A + aoff[i] + (size_t)(kt) * 128), (PG8_LAS unsigned*)(MU_SA(buf) + wid * 1024 + i * 8192), 16, 0, 0); } while (0)
; #define MU_B_ISSUE(sb, kt) do { const char* kb_ = Bb + (size_t)(kt) * (64 * (size_t)RB); _Pragma("unroll") for (int j = 0; j < 8; ++j) { const char* p_ = kb_ + (size_t)j * RB; \
;         asm volatile("global_load_dwordx2 %0, %1, off" : "=&v"(sb[j]) : "v"(p_) : "memory"); } } while (0)
; #define MU_B_WAIT(sb, N) asm volatile("s_waitcnt vmcnt(%8)" : "+v"(sb[0]), "+v"(sb[1]), "+v"(sb[2]), "+v"(sb[3]), "+v"(sb[4]), "+v"(sb[5]), "+v"(sb[6]), "+v"(sb[7]) : "n"(N) : "memory")
; #define MU_COMPUTE(buf) MU_COMPUTE_N(buf, NMU)
; template <int MODE>
; __device__ __forceinline__ void moe_unit(PG8_LAS unsigned char* lds, int e, int cb, int slot0  , int nv  , const bf16_t* A, const int* slot_tok,
;                                          const float* W0, const float* W1, bf16_t* OUT, const float* slot_rs  , const int* slot_dst) {
;     ...
;     f32x4 acc[NMU][4];
; #pragma unroll
;     for (int m = 0; m < NMU; ++m)
; #pragma unroll
;         for (int n = 0; n < 4; ++n) acc[m][n] = (f32x4){0.f, 0.f, 0.f, 0.f};
;     f32x2 s0[8], s1[8];
;     float g0[8];
;     MU_GLDS_A(0, 0); MU_B_ISSUE(s0, 0); MU_G_LOAD(g0, 0); MU_B_ISSUE(s1, 1);
;     MU_B_WAIT(s0, 8); MU_B_WRITE(s0, 0, g0); __builtin_amdgcn_sched_barrier(0); MU_B_ISSUE(s0, 2);
;     asm volatile("s_waitcnt vmcnt(16)" ::: "memory");
;     asm volatile("s_waitcnt lgkmcnt(0)" ::: "memory"); __builtin_amdgcn_s_barrier(); asm volatile("" ::: "memory");
; #pragma unroll 1
;     for (int t = 0; t < nt; t += 2) {
;         if (t + 2 < nt) MU_B_WAIT(s1, 8); else MU_B_WAIT(s1, 0);
;         MU_G_LOAD(g0, t + 1); MU_B_WRITE(s1, 1, g0); __builtin_amdgcn_sched_barrier(0); MU_GLDS_A(1, t + 1); __builtin_amdgcn_sched_barrier(0);
;         if (t + 3 < nt) { MU_B_ISSUE(s1, t + 3); }
;         MU_COMPUTE(0);
;         MU_END(t + 3 >= nt);
;         if (t + 2 < nt) { MU_B_WAIT(s0, 8); MU_G_LOAD(g0, t + 2); MU_B_WRITE(s0, 0, g0); __builtin_amdgcn_sched_barrier(0); MU_GLDS_A(0, t + 2); __builtin_amdgcn_sched_barrier(0); }
;         if (t + 4 < nt) { MU_B_ISSUE(s0, t + 4); }
;         MU_COMPUTE(1);
;         MU_END(t + 4 >= nt);
	s_load_dwordx8 s[12:19], s[28:29], 0x0
	s_add_u32 s28, s28, 0x100
	s_addc_u32 s29, s29, 0
	v_mfma_f32_16x16x32_bf16 v[78:81], v[238:241], v[218:221], v[78:81]
	v_mfma_f32_16x16x32_bf16 v[74:77], v[242:245], v[218:221], v[74:77]
	v_mfma_f32_16x16x32_bf16 v[70:73], v[246:249], v[218:221], v[70:73]
	v_mfma_f32_16x16x32_bf16 v[66:69], v[250:253], v[218:221], v[66:69]
	ds_read_b128 v[218:221], v93 offset:0
	ds_read_b128 v[142:145], v141 offset:0
	v_lshl_add_u64 v[132:133], v[132:133], 0, s[40:41]
	global_load_dwordx2 v[114:115], v[132:133], off
	global_load_dwordx2 v[116:117], v[132:133], off offset:2048
	v_mfma_f32_16x16x32_bf16 v[62:65], v[238:241], v[222:225], v[62:65]
	v_mfma_f32_16x16x32_bf16 v[58:61], v[242:245], v[222:225], v[58:61]
	v_mfma_f32_16x16x32_bf16 v[54:57], v[246:249], v[222:225], v[54:57]
	v_mfma_f32_16x16x32_bf16 v[50:53], v[250:253], v[222:225], v[50:53]
	ds_read_b128 v[222:225], v93 offset:2048
	ds_read_b128 v[146:149], v141 offset:2048
	v_lshl_add_u64 v[166:167], v[132:133], 0, s[34:35]
	global_load_dwordx2 v[118:119], v[166:167], off
	global_load_dwordx2 v[120:121], v[166:167], off offset:2048
	v_mfma_f32_16x16x32_bf16 v[46:49], v[238:241], v[226:229], v[46:49]
	v_mfma_f32_16x16x32_bf16 v[42:45], v[242:245], v[226:229], v[42:45]
	v_mfma_f32_16x16x32_bf16 v[38:41], v[246:249], v[226:229], v[38:41]
	v_mfma_f32_16x16x32_bf16 v[34:37], v[250:253], v[226:229], v[34:37]
	ds_read_b128 v[226:229], v93 offset:4096
	ds_read_b128 v[150:153], v141 offset:4096
	v_lshl_add_u64 v[166:167], v[132:133], 0, s[36:37]
	global_load_dwordx2 v[122:123], v[166:167], off
	global_load_dwordx2 v[124:125], v[166:167], off offset:2048
	v_mfma_f32_16x16x32_bf16 v[18:21], v[238:241], v[230:233], v[18:21]
	v_mfma_f32_16x16x32_bf16 v[22:25], v[242:245], v[230:233], v[22:25]
	v_mfma_f32_16x16x32_bf16 v[26:29], v[246:249], v[230:233], v[26:29]
	v_mfma_f32_16x16x32_bf16 v[30:33], v[250:253], v[230:233], v[30:33]
	ds_read_b128 v[230:233], v93 offset:6144
	ds_read_b128 v[154:157], v141 offset:6144
	v_lshl_add_u64 v[166:167], v[132:133], 0, s[38:39]
	global_load_dwordx2 v[126:127], v[166:167], off
	global_load_dwordx2 v[128:129], v[166:167], off offset:2048
	v_mfma_f32_16x16x32_bf16 v[2:5], v[238:241], v[234:237], v[2:5]
	v_mfma_f32_16x16x32_bf16 v[6:9], v[242:245], v[234:237], v[6:9]
	v_mfma_f32_16x16x32_bf16 v[10:13], v[246:249], v[234:237], v[10:13]
	v_mfma_f32_16x16x32_bf16 v[14:17], v[250:253], v[234:237], v[14:17]
	ds_read_b128 v[234:237], v93 offset:8192
	s_waitcnt vmcnt(21)
	s_mov_b32 s47, s42
	s_mov_b32 s42, s43
	s_mov_b32 s43, s44
	s_mov_b32 s44, s47
	s_waitcnt lgkmcnt(0)
	s_barrier
	s_add_i32 s47, s44, s6
	s_add_u32 s30, s30, 0x80
	s_addc_u32 s31, s31, 0
	v_mfma_f32_16x16x32_bf16 v[78:81], v[142:145], v[218:221], v[78:81]
	v_mfma_f32_16x16x32_bf16 v[74:77], v[146:149], v[218:221], v[74:77]
	v_mfma_f32_16x16x32_bf16 v[70:73], v[150:153], v[218:221], v[70:73]
	v_mfma_f32_16x16x32_bf16 v[66:69], v[154:157], v[218:221], v[66:69]
	s_mov_b32 m0, s47
	s_nop 0
	global_load_lds_dwordx4 v86, s[30:31]
	v_mfma_f32_16x16x32_bf16 v[62:65], v[142:145], v[222:225], v[62:65]
	v_mfma_f32_16x16x32_bf16 v[58:61], v[146:149], v[222:225], v[58:61]
	v_mfma_f32_16x16x32_bf16 v[54:57], v[150:153], v[222:225], v[54:57]
	v_mfma_f32_16x16x32_bf16 v[50:53], v[154:157], v[222:225], v[50:53]
	s_add_i32 m0, s47, 0x2000
	s_nop 0
	global_load_lds_dwordx4 v134, s[30:31]
	v_mfma_f32_16x16x32_bf16 v[46:49], v[142:145], v[226:229], v[46:49]
	v_mfma_f32_16x16x32_bf16 v[42:45], v[146:149], v[226:229], v[42:45]
	v_mfma_f32_16x16x32_bf16 v[38:41], v[150:153], v[226:229], v[38:41]
	v_mfma_f32_16x16x32_bf16 v[34:37], v[154:157], v[226:229], v[34:37]
	s_add_i32 m0, s47, 0x4000
	s_nop 0
	global_load_lds_dwordx4 v136, s[30:31]
	v_mfma_f32_16x16x32_bf16 v[18:21], v[142:145], v[230:233], v[18:21]
	v_mfma_f32_16x16x32_bf16 v[22:25], v[146:149], v[230:233], v[22:25]
	v_mfma_f32_16x16x32_bf16 v[26:29], v[150:153], v[230:233], v[26:29]
	v_mfma_f32_16x16x32_bf16 v[30:33], v[154:157], v[230:233], v[30:33]
	s_add_i32 m0, s47, 0x6000
	s_nop 0
	global_load_lds_dwordx4 v138, s[30:31]
	v_mfma_f32_16x16x32_bf16 v[2:5], v[142:145], v[234:237], v[2:5]
	v_mfma_f32_16x16x32_bf16 v[6:9], v[146:149], v[234:237], v[6:9]
	v_mfma_f32_16x16x32_bf16 v[10:13], v[150:153], v[234:237], v[10:13]
	v_mfma_f32_16x16x32_bf16 v[14:17], v[154:157], v[234:237], v[14:17]
	s_add_i32 m0, s47, 0x8000
	s_nop 0
	global_load_lds_dwordx4 v140, s[30:31]
	v_mul_f32_e32 v186, s12, v186
	v_mul_f32_e32 v187, s12, v187
	v_mul_f32_e32 v188, s13, v188
	v_mul_f32_e32 v189, s13, v189
	v_mul_f32_e32 v190, s14, v190
	v_mul_f32_e32 v191, s14, v191
	v_mul_f32_e32 v192, s15, v192
	v_mul_f32_e32 v193, s15, v193
	v_mul_f32_e32 v194, s16, v194
	v_mul_f32_e32 v195, s16, v195
	v_mul_f32_e32 v196, s17, v196
	v_mul_f32_e32 v197, s17, v197
	v_mul_f32_e32 v198, s18, v198
	v_mul_f32_e32 v199, s18, v199
	v_mul_f32_e32 v200, s19, v200
	v_mul_f32_e32 v201, s19, v201
	v_cvt_pk_bf16_f32 v158, v186, v188
	v_cvt_pk_bf16_f32 v159, v190, v192
	v_cvt_pk_bf16_f32 v160, v194, v196
	v_cvt_pk_bf16_f32 v161, v198, v200
	v_cvt_pk_bf16_f32 v162, v187, v189
	v_cvt_pk_bf16_f32 v163, v191, v193
	v_cvt_pk_bf16_f32 v164, v195, v197
	v_cvt_pk_bf16_f32 v165, v199, v201
	ds_write_b128 v1, v[158:161] offset:0
	ds_write_b128 v1, v[162:165] offset:128
	v_add_u32_e32 v91, s42, v135
	v_add_u32_e32 v93, s42, v137
	ds_read_b128 v[238:241], v139 offset:19456
	ds_read_b128 v[242:245], v139 offset:21504
	ds_read_b128 v[246:249], v139 offset:23552
	ds_read_b128 v[250:253], v139 offset:25600
	ds_read_b128 v[218:221], v91 offset:0
	ds_read_b128 v[222:225], v91 offset:2048
	ds_read_b128 v[226:229], v91 offset:4096
	ds_read_b128 v[230:233], v91 offset:6144
	ds_read_b128 v[234:237], v91 offset:8192
	s_waitcnt lgkmcnt(0)
; #define MU_GLDS_A(buf, kt) do { _Pragma("unroll") for (int i = 0; i < NMU; ++i) \
;         __builtin_amdgcn_global_load_lds((const unsigned*)((const char*)A + aoff[i] + (size_t)(kt) * 128), (PG8_LAS unsigned*)(MU_SA(buf) + wid * 1024 + i * 8192), 16, 0, 0); } while (0)
; #define MU_B_ISSUE(sb, kt) do { const char* kb_ = Bb + (size_t)(kt) * (64 * (size_t)RB); _Pragma("unroll") for (int j = 0; j < 8; ++j) { const char* p_ = kb_ + (size_t)j * RB; \
;         asm volatile("global_load_dwordx2 %0, %1, off" : "=&v"(sb[j]) : "v"(p_) : "memory"); } } while (0)
; #define MU_B_WAIT(sb, N) asm volatile("s_waitcnt vmcnt(%8)" : "+v"(sb[0]), "+v"(sb[1]), "+v"(sb[2]), "+v"(sb[3]), "+v"(sb[4]), "+v"(sb[5]), "+v"(sb[6]), "+v"(sb[7]) : "n"(N) : "memory")
; #define MU_COMPUTE(buf) MU_COMPUTE_N(buf, NMU)
; template <int MODE>
; __device__ __forceinline__ void moe_unit(PG8_LAS unsigned char* lds, int e, int cb, int slot0  , int nv  , const bf16_t* A, const int* slot_tok,
;                                          const float* W0, const float* W1, bf16_t* OUT, const float* slot_rs  , const int* slot_dst) {
;     ...
;     f32x4 acc[NMU][4];
; #pragma unroll
;     for (int m = 0; m < NMU; ++m)
; #pragma unroll
;         for (int n = 0; n < 4; ++n) acc[m][n] = (f32x4){0.f, 0.f, 0.f, 0.f};
;     f32x2 s0[8], s1[8];
;     float g0[8];
;     MU_GLDS_A(0, 0); MU_B_ISSUE(s0, 0); MU_G_LOAD(g0, 0); MU_B_ISSUE(s1, 1);
;     MU_B_WAIT(s0, 8); MU_B_WRITE(s0, 0, g0); __builtin_amdgcn_sched_barrier(0); MU_B_ISSUE(s0, 2);
;     asm volatile("s_waitcnt vmcnt(16)" ::: "memory");
;     asm volatile("s_waitcnt lgkmcnt(0)" ::: "memory"); __builtin_amdgcn_s_barrier(); asm volatile("" ::: "memory");
; #pragma unroll 1
;     for (int t = 0; t < nt; t += 2) {
;         if (t + 2 < nt) MU_B_WAIT(s1, 8); else MU_B_WAIT(s1, 0);
;         MU_G_LOAD(g0, t + 1); MU_B_WRITE(s1, 1, g0); __builtin_amdgcn_sched_barrier(0); MU_GLDS_A(1, t + 1); __builtin_amdgcn_sched_barrier(0);
;         if (t + 3 < nt) { MU_B_ISSUE(s1, t + 3); }
;         MU_COMPUTE(0);
;         MU_END(t + 3 >= nt);
;         if (t + 2 < nt) { MU_B_WAIT(s0, 8); MU_G_LOAD(g0, t + 2); MU_B_WRITE(s0, 0, g0); __builtin_amdgcn_sched_barrier(0); MU_GLDS_A(0, t + 2); __builtin_amdgcn_sched_barrier(0); }
;         if (t + 4 < nt) { MU_B_ISSUE(s0, t + 4); }
;         MU_COMPUTE(1);
;         MU_END(t + 4 >= nt);
	s_load_dwordx8 s[20:27], s[28:29], 0x0
	s_add_u32 s28, s28, 0x100
	s_addc_u32 s29, s29, 0
	v_mfma_f32_16x16x32_bf16 v[78:81], v[238:241], v[218:221], v[78:81]
	v_mfma_f32_16x16x32_bf16 v[74:77], v[242:245], v[218:221], v[74:77]
	v_mfma_f32_16x16x32_bf16 v[70:73], v[246:249], v[218:221], v[70:73]
	v_mfma_f32_16x16x32_bf16 v[66:69], v[250:253], v[218:221], v[66:69]
	ds_read_b128 v[218:221], v93 offset:0
	ds_read_b128 v[142:145], v141 offset:19456
	v_lshl_add_u64 v[132:133], v[132:133], 0, s[40:41]
	global_load_dwordx2 v[186:187], v[132:133], off
	global_load_dwordx2 v[188:189], v[132:133], off offset:2048
	v_mfma_f32_16x16x32_bf16 v[62:65], v[238:241], v[222:225], v[62:65]
	v_mfma_f32_16x16x32_bf16 v[58:61], v[242:245], v[222:225], v[58:61]
	v_mfma_f32_16x16x32_bf16 v[54:57], v[246:249], v[222:225], v[54:57]
	v_mfma_f32_16x16x32_bf16 v[50:53], v[250:253], v[222:225], v[50:53]
	ds_read_b128 v[222:225], v93 offset:2048
	ds_read_b128 v[146:149], v141 offset:21504
	v_lshl_add_u64 v[166:167], v[132:133], 0, s[34:35]
	global_load_dwordx2 v[190:191], v[166:167], off
	global_load_dwordx2 v[192:193], v[166:167], off offset:2048
	v_mfma_f32_16x16x32_bf16 v[46:49], v[238:241], v[226:229], v[46:49]
	v_mfma_f32_16x16x32_bf16 v[42:45], v[242:245], v[226:229], v[42:45]
	v_mfma_f32_16x16x32_bf16 v[38:41], v[246:249], v[226:229], v[38:41]
	v_mfma_f32_16x16x32_bf16 v[34:37], v[250:253], v[226:229], v[34:37]
	ds_read_b128 v[226:229], v93 offset:4096
	ds_read_b128 v[150:153], v141 offset:23552
	v_lshl_add_u64 v[166:167], v[132:133], 0, s[36:37]
	global_load_dwordx2 v[194:195], v[166:167], off
	global_load_dwordx2 v[196:197], v[166:167], off offset:2048
	v_mfma_f32_16x16x32_bf16 v[18:21], v[238:241], v[230:233], v[18:21]
	v_mfma_f32_16x16x32_bf16 v[22:25], v[242:245], v[230:233], v[22:25]
	v_mfma_f32_16x16x32_bf16 v[26:29], v[246:249], v[230:233], v[26:29]
	v_mfma_f32_16x16x32_bf16 v[30:33], v[250:253], v[230:233], v[30:33]
	ds_read_b128 v[230:233], v93 offset:6144
	ds_read_b128 v[154:157], v141 offset:25600
	v_lshl_add_u64 v[166:167], v[132:133], 0, s[38:39]
	global_load_dwordx2 v[198:199], v[166:167], off
	global_load_dwordx2 v[200:201], v[166:167], off offset:2048
	v_mfma_f32_16x16x32_bf16 v[2:5], v[238:241], v[234:237], v[2:5]
	v_mfma_f32_16x16x32_bf16 v[6:9], v[242:245], v[234:237], v[6:9]
	v_mfma_f32_16x16x32_bf16 v[10:13], v[246:249], v[234:237], v[10:13]
	v_mfma_f32_16x16x32_bf16 v[14:17], v[250:253], v[234:237], v[14:17]
	ds_read_b128 v[234:237], v93 offset:8192
	s_waitcnt vmcnt(21)
	s_mov_b32 s47, s42
	s_mov_b32 s42, s43
	s_mov_b32 s43, s44
	s_mov_b32 s44, s47
	s_waitcnt lgkmcnt(0)
	s_barrier
	s_add_i32 s47, s44, s6
	s_add_u32 s30, s30, 0x80
	s_addc_u32 s31, s31, 0
	v_mfma_f32_16x16x32_bf16 v[78:81], v[142:145], v[218:221], v[78:81]
	v_mfma_f32_16x16x32_bf16 v[74:77], v[146:149], v[218:221], v[74:77]
	v_mfma_f32_16x16x32_bf16 v[70:73], v[150:153], v[218:221], v[70:73]
	v_mfma_f32_16x16x32_bf16 v[66:69], v[154:157], v[218:221], v[66:69]
	s_mov_b32 m0, s47
	s_nop 0
	global_load_lds_dwordx4 v86, s[30:31]
	v_mfma_f32_16x16x32_bf16 v[62:65], v[142:145], v[222:225], v[62:65]
	v_mfma_f32_16x16x32_bf16 v[58:61], v[146:149], v[222:225], v[58:61]
	v_mfma_f32_16x16x32_bf16 v[54:57], v[150:153], v[222:225], v[54:57]
	v_mfma_f32_16x16x32_bf16 v[50:53], v[154:157], v[222:225], v[50:53]
	s_add_i32 m0, s47, 0x2000
	s_nop 0
	global_load_lds_dwordx4 v134, s[30:31]
	v_mfma_f32_16x16x32_bf16 v[46:49], v[142:145], v[226:229], v[46:49]
	v_mfma_f32_16x16x32_bf16 v[42:45], v[146:149], v[226:229], v[42:45]
	v_mfma_f32_16x16x32_bf16 v[38:41], v[150:153], v[226:229], v[38:41]
	v_mfma_f32_16x16x32_bf16 v[34:37], v[154:157], v[226:229], v[34:37]
	s_add_i32 m0, s47, 0x4000
	s_nop 0
	global_load_lds_dwordx4 v136, s[30:31]
	v_mfma_f32_16x16x32_bf16 v[18:21], v[142:145], v[230:233], v[18:21]
	v_mfma_f32_16x16x32_bf16 v[22:25], v[146:149], v[230:233], v[22:25]
	v_mfma_f32_16x16x32_bf16 v[26:29], v[150:153], v[230:233], v[26:29]
	v_mfma_f32_16x16x32_bf16 v[30:33], v[154:157], v[230:233], v[30:33]
	s_add_i32 m0, s47, 0x6000
	s_nop 0
	global_load_lds_dwordx4 v138, s[30:31]
	v_mfma_f32_16x16x32_bf16 v[2:5], v[142:145], v[234:237], v[2:5]
	v_mfma_f32_16x16x32_bf16 v[6:9], v[146:149], v[234:237], v[6:9]
	v_mfma_f32_16x16x32_bf16 v[10:13], v[150:153], v[234:237], v[10:13]
	v_mfma_f32_16x16x32_bf16 v[14:17], v[154:157], v[234:237], v[14:17]
	s_add_i32 m0, s47, 0x8000
	s_nop 0
	global_load_lds_dwordx4 v140, s[30:31]
	v_mul_f32_e32 v202, s20, v202
	v_mul_f32_e32 v203, s20, v203
	v_mul_f32_e32 v204, s21, v204
	v_mul_f32_e32 v205, s21, v205
	v_mul_f32_e32 v206, s22, v206
	v_mul_f32_e32 v207, s22, v207
	v_mul_f32_e32 v208, s23, v208
	v_mul_f32_e32 v209, s23, v209
	v_mul_f32_e32 v210, s24, v210
	v_mul_f32_e32 v211, s24, v211
	v_mul_f32_e32 v212, s25, v212
	v_mul_f32_e32 v213, s25, v213
	v_mul_f32_e32 v214, s26, v214
	v_mul_f32_e32 v215, s26, v215
	v_mul_f32_e32 v216, s27, v216
	v_mul_f32_e32 v217, s27, v217
	v_cvt_pk_bf16_f32 v158, v202, v204
	v_cvt_pk_bf16_f32 v159, v206, v208
	v_cvt_pk_bf16_f32 v160, v210, v212
	v_cvt_pk_bf16_f32 v161, v214, v216
	v_cvt_pk_bf16_f32 v162, v203, v205
	v_cvt_pk_bf16_f32 v163, v207, v209
	v_cvt_pk_bf16_f32 v164, v211, v213
	v_cvt_pk_bf16_f32 v165, v215, v217
	ds_write_b128 v1, v[158:161] offset:19456
	ds_write_b128 v1, v[162:165] offset:19584
	v_add_u32_e32 v91, s42, v135
	v_add_u32_e32 v93, s42, v137
	ds_read_b128 v[238:241], v139 offset:0
	ds_read_b128 v[242:245], v139 offset:2048
	ds_read_b128 v[246:249], v139 offset:4096
	ds_read_b128 v[250:253], v139 offset:6144
	ds_read_b128 v[218:221], v91 offset:0
	ds_read_b128 v[222:225], v91 offset:2048
	ds_read_b128 v[226:229], v91 offset:4096
	ds_read_b128 v[230:233], v91 offset:6144
	ds_read_b128 v[234:237], v91 offset:8192
	s_waitcnt lgkmcnt(0)
; #define MU_GLDS_A(buf, kt) do { _Pragma("unroll") for (int i = 0; i < NMU; ++i) \
;         __builtin_amdgcn_global_load_lds((const unsigned*)((const char*)A + aoff[i] + (size_t)(kt) * 128), (PG8_LAS unsigned*)(MU_SA(buf) + wid * 1024 + i * 8192), 16, 0, 0); } while (0)
; #define MU_B_ISSUE(sb, kt) do { const char* kb_ = Bb + (size_t)(kt) * (64 * (size_t)RB); _Pragma("unroll") for (int j = 0; j < 8; ++j) { const char* p_ = kb_ + (size_t)j * RB; \
;         asm volatile("global_load_dwordx2 %0, %1, off" : "=&v"(sb[j]) : "v"(p_) : "memory"); } } while (0)
; #define MU_B_WAIT(sb, N) asm volatile("s_waitcnt vmcnt(%8)" : "+v"(sb[0]), "+v"(sb[1]), "+v"(sb[2]), "+v"(sb[3]), "+v"(sb[4]), "+v"(sb[5]), "+v"(sb[6]), "+v"(sb[7]) : "n"(N) : "memory")
; #define MU_COMPUTE(buf) MU_COMPUTE_N(buf, NMU)
; template <int MODE>
; __device__ __forceinline__ void moe_unit(PG8_LAS unsigned char* lds, int e, int cb, int slot0  , int nv  , const bf16_t* A, const int* slot_tok,
;                                          const float* W0, const float* W1, bf16_t* OUT, const float* slot_rs  , const int* slot_dst) {
;     ...
;     f32x4 acc[NMU][4];
; #pragma unroll
;     for (int m = 0; m < NMU; ++m)
; #pragma unroll
;         for (int n = 0; n < 4; ++n) acc[m][n] = (f32x4){0.f, 0.f, 0.f, 0.f};
;     f32x2 s0[8], s1[8];
;     float g0[8];
;     MU_GLDS_A(0, 0); MU_B_ISSUE(s0, 0); MU_G_LOAD(g0, 0); MU_B_ISSUE(s1, 1);
;     MU_B_WAIT(s0, 8); MU_B_WRITE(s0, 0, g0); __builtin_amdgcn_sched_barrier(0); MU_B_ISSUE(s0, 2);
;     asm volatile("s_waitcnt vmcnt(16)" ::: "memory");
;     asm volatile("s_waitcnt lgkmcnt(0)" ::: "memory"); __builtin_amdgcn_s_barrier(); asm volatile("" ::: "memory");
; #pragma unroll 1
;     for (int t = 0; t < nt; t += 2) {
;         if (t + 2 < nt) MU_B_WAIT(s1, 8); else MU_B_WAIT(s1, 0);
;         MU_G_LOAD(g0, t + 1); MU_B_WRITE(s1, 1, g0); __builtin_amdgcn_sched_barrier(0); MU_GLDS_A(1, t + 1); __builtin_amdgcn_sched_barrier(0);
;         if (t + 3 < nt) { MU_B_ISSUE(s1, t + 3); }
;         MU_COMPUTE(0);
;         MU_END(t + 3 >= nt);
;         if (t + 2 < nt) { MU_B_WAIT(s0, 8); MU_G_LOAD(g0, t + 2); MU_B_WRITE(s0, 0, g0); __builtin_amdgcn_sched_barrier(0); MU_GLDS_A(0, t + 2); __builtin_amdgcn_sched_barrier(0); }
;         if (t + 4 < nt) { MU_B_ISSUE(s0, t + 4); }
;         MU_COMPUTE(1);
;         MU_END(t + 4 >= nt);
	s_load_dwordx8 s[12:19], s[28:29], 0x0
	s_add_u32 s28, s28, 0x100
	s_addc_u32 s29, s29, 0
	v_mfma_f32_16x16x32_bf16 v[78:81], v[238:241], v[218:221], v[78:81]
	v_mfma_f32_16x16x32_bf16 v[74:77], v[242:245], v[218:221], v[74:77]
	v_mfma_f32_16x16x32_bf16 v[70:73], v[246:249], v[218:221], v[70:73]
	v_mfma_f32_16x16x32_bf16 v[66:69], v[250:253], v[218:221], v[66:69]
	ds_read_b128 v[218:221], v93 offset:0
	ds_read_b128 v[142:145], v141 offset:0
	v_lshl_add_u64 v[132:133], v[132:133], 0, s[40:41]
	global_load_dwordx2 v[202:203], v[132:133], off
	global_load_dwordx2 v[204:205], v[132:133], off offset:2048
	v_mfma_f32_16x16x32_bf16 v[62:65], v[238:241], v[222:225], v[62:65]
	v_mfma_f32_16x16x32_bf16 v[58:61], v[242:245], v[222:225], v[58:61]
	v_mfma_f32_16x16x32_bf16 v[54:57], v[246:249], v[222:225], v[54:57]
	v_mfma_f32_16x16x32_bf16 v[50:53], v[250:253], v[222:225], v[50:53]
	ds_read_b128 v[222:225], v93 offset:2048
	ds_read_b128 v[146:149], v141 offset:2048
	v_lshl_add_u64 v[166:167], v[132:133], 0, s[34:35]
	global_load_dwordx2 v[206:207], v[166:167], off
	global_load_dwordx2 v[208:209], v[166:167], off offset:2048
	v_mfma_f32_16x16x32_bf16 v[46:49], v[238:241], v[226:229], v[46:49]
	v_mfma_f32_16x16x32_bf16 v[42:45], v[242:245], v[226:229], v[42:45]
	v_mfma_f32_16x16x32_bf16 v[38:41], v[246:249], v[226:229], v[38:41]
	v_mfma_f32_16x16x32_bf16 v[34:37], v[250:253], v[226:229], v[34:37]
	ds_read_b128 v[226:229], v93 offset:4096
	ds_read_b128 v[150:153], v141 offset:4096
	v_lshl_add_u64 v[166:167], v[132:133], 0, s[36:37]
	global_load_dwordx2 v[210:211], v[166:167], off
	global_load_dwordx2 v[212:213], v[166:167], off offset:2048
	v_mfma_f32_16x16x32_bf16 v[18:21], v[238:241], v[230:233], v[18:21]
	v_mfma_f32_16x16x32_bf16 v[22:25], v[242:245], v[230:233], v[22:25]
	v_mfma_f32_16x16x32_bf16 v[26:29], v[246:249], v[230:233], v[26:29]
	v_mfma_f32_16x16x32_bf16 v[30:33], v[250:253], v[230:233], v[30:33]
	ds_read_b128 v[230:233], v93 offset:6144
	ds_read_b128 v[154:157], v141 offset:6144
	v_lshl_add_u64 v[166:167], v[132:133], 0, s[38:39]
	global_load_dwordx2 v[214:215], v[166:167], off
	global_load_dwordx2 v[216:217], v[166:167], off offset:2048
	v_mfma_f32_16x16x32_bf16 v[2:5], v[238:241], v[234:237], v[2:5]
	v_mfma_f32_16x16x32_bf16 v[6:9], v[242:245], v[234:237], v[6:9]
	v_mfma_f32_16x16x32_bf16 v[10:13], v[246:249], v[234:237], v[10:13]
	v_mfma_f32_16x16x32_bf16 v[14:17], v[250:253], v[234:237], v[14:17]
	ds_read_b128 v[234:237], v93 offset:8192
	s_waitcnt vmcnt(21)
	s_mov_b32 s47, s42
	s_mov_b32 s42, s43
	s_mov_b32 s43, s44
	s_mov_b32 s44, s47
	s_waitcnt lgkmcnt(0)
	s_barrier
	s_add_i32 s47, s44, s6
	s_add_u32 s30, s30, 0x80
	s_addc_u32 s31, s31, 0
	v_mfma_f32_16x16x32_bf16 v[78:81], v[142:145], v[218:221], v[78:81]
	v_mfma_f32_16x16x32_bf16 v[74:77], v[146:149], v[218:221], v[74:77]
	v_mfma_f32_16x16x32_bf16 v[70:73], v[150:153], v[218:221], v[70:73]
	v_mfma_f32_16x16x32_bf16 v[66:69], v[154:157], v[218:221], v[66:69]
	s_mov_b32 m0, s47
	s_nop 0
	global_load_lds_dwordx4 v86, s[30:31]
	v_mfma_f32_16x16x32_bf16 v[62:65], v[142:145], v[222:225], v[62:65]
	v_mfma_f32_16x16x32_bf16 v[58:61], v[146:149], v[222:225], v[58:61]
	v_mfma_f32_16x16x32_bf16 v[54:57], v[150:153], v[222:225], v[54:57]
	v_mfma_f32_16x16x32_bf16 v[50:53], v[154:157], v[222:225], v[50:53]
	s_add_i32 m0, s47, 0x2000
	s_nop 0
	global_load_lds_dwordx4 v134, s[30:31]
	v_mfma_f32_16x16x32_bf16 v[46:49], v[142:145], v[226:229], v[46:49]
	v_mfma_f32_16x16x32_bf16 v[42:45], v[146:149], v[226:229], v[42:45]
	v_mfma_f32_16x16x32_bf16 v[38:41], v[150:153], v[226:229], v[38:41]
	v_mfma_f32_16x16x32_bf16 v[34:37], v[154:157], v[226:229], v[34:37]
	s_add_i32 m0, s47, 0x4000
	s_nop 0
	global_load_lds_dwordx4 v136, s[30:31]
	v_mfma_f32_16x16x32_bf16 v[18:21], v[142:145], v[230:233], v[18:21]
	v_mfma_f32_16x16x32_bf16 v[22:25], v[146:149], v[230:233], v[22:25]
	v_mfma_f32_16x16x32_bf16 v[26:29], v[150:153], v[230:233], v[26:29]
	v_mfma_f32_16x16x32_bf16 v[30:33], v[154:157], v[230:233], v[30:33]
	s_add_i32 m0, s47, 0x6000
	s_nop 0
	global_load_lds_dwordx4 v138, s[30:31]
	v_mfma_f32_16x16x32_bf16 v[2:5], v[142:145], v[234:237], v[2:5]
	v_mfma_f32_16x16x32_bf16 v[6:9], v[146:149], v[234:237], v[6:9]
	v_mfma_f32_16x16x32_bf16 v[10:13], v[150:153], v[234:237], v[10:13]
	v_mfma_f32_16x16x32_bf16 v[14:17], v[154:157], v[234:237], v[14:17]
	s_add_i32 m0, s47, 0x8000
	s_nop 0
	global_load_lds_dwordx4 v140, s[30:31]
	v_mul_f32_e32 v98, s12, v98
	v_mul_f32_e32 v99, s12, v99
	v_mul_f32_e32 v100, s13, v100
	v_mul_f32_e32 v101, s13, v101
	v_mul_f32_e32 v102, s14, v102
	v_mul_f32_e32 v103, s14, v103
	v_mul_f32_e32 v104, s15, v104
	v_mul_f32_e32 v105, s15, v105
	v_mul_f32_e32 v106, s16, v106
	v_mul_f32_e32 v107, s16, v107
	v_mul_f32_e32 v108, s17, v108
	v_mul_f32_e32 v109, s17, v109
	v_mul_f32_e32 v110, s18, v110
	v_mul_f32_e32 v111, s18, v111
	v_mul_f32_e32 v112, s19, v112
	v_mul_f32_e32 v113, s19, v113
	v_cvt_pk_bf16_f32 v158, v98, v100
	v_cvt_pk_bf16_f32 v159, v102, v104
	v_cvt_pk_bf16_f32 v160, v106, v108
	v_cvt_pk_bf16_f32 v161, v110, v112
	v_cvt_pk_bf16_f32 v162, v99, v101
	v_cvt_pk_bf16_f32 v163, v103, v105
	v_cvt_pk_bf16_f32 v164, v107, v109
	v_cvt_pk_bf16_f32 v165, v111, v113
	ds_write_b128 v1, v[158:161] offset:0
	ds_write_b128 v1, v[162:165] offset:128
	v_add_u32_e32 v91, s42, v135
	v_add_u32_e32 v93, s42, v137
	ds_read_b128 v[238:241], v139 offset:19456
	ds_read_b128 v[242:245], v139 offset:21504
	ds_read_b128 v[246:249], v139 offset:23552
	ds_read_b128 v[250:253], v139 offset:25600
	ds_read_b128 v[218:221], v91 offset:0
	ds_read_b128 v[222:225], v91 offset:2048
	ds_read_b128 v[226:229], v91 offset:4096
	ds_read_b128 v[230:233], v91 offset:6144
	ds_read_b128 v[234:237], v91 offset:8192
	s_waitcnt lgkmcnt(0)
; #define MU_GLDS_A(buf, kt) do { _Pragma("unroll") for (int i = 0; i < NMU; ++i) \
;         __builtin_amdgcn_global_load_lds((const unsigned*)((const char*)A + aoff[i] + (size_t)(kt) * 128), (PG8_LAS unsigned*)(MU_SA(buf) + wid * 1024 + i * 8192), 16, 0, 0); } while (0)
; #define MU_B_ISSUE(sb, kt) do { const char* kb_ = Bb + (size_t)(kt) * (64 * (size_t)RB); _Pragma("unroll") for (int j = 0; j < 8; ++j) { const char* p_ = kb_ + (size_t)j * RB; \
;         asm volatile("global_load_dwordx2 %0, %1, off" : "=&v"(sb[j]) : "v"(p_) : "memory"); } } while (0)
; #define MU_B_WAIT(sb, N) asm volatile("s_waitcnt vmcnt(%8)" : "+v"(sb[0]), "+v"(sb[1]), "+v"(sb[2]), "+v"(sb[3]), "+v"(sb[4]), "+v"(sb[5]), "+v"(sb[6]), "+v"(sb[7]) : "n"(N) : "memory")
; #define MU_COMPUTE(buf) MU_COMPUTE_N(buf, NMU)
; template <int MODE>
; __device__ __forceinline__ void moe_unit(PG8_LAS unsigned char* lds, int e, int cb, int slot0  , int nv  , const bf16_t* A, const int* slot_tok,
;                                          const float* W0, const float* W1, bf16_t* OUT, const float* slot_rs  , const int* slot_dst) {
;     ...
;     f32x4 acc[NMU][4];
; #pragma unroll
;     for (int m = 0; m < NMU; ++m)
; #pragma unroll
;         for (int n = 0; n < 4; ++n) acc[m][n] = (f32x4){0.f, 0.f, 0.f, 0.f};
;     f32x2 s0[8], s1[8];
;     float g0[8];
;     MU_GLDS_A(0, 0); MU_B_ISSUE(s0, 0); MU_G_LOAD(g0, 0); MU_B_ISSUE(s1, 1);
;     MU_B_WAIT(s0, 8); MU_B_WRITE(s0, 0, g0); __builtin_amdgcn_sched_barrier(0); MU_B_ISSUE(s0, 2);
;     asm volatile("s_waitcnt vmcnt(16)" ::: "memory");
;     asm volatile("s_waitcnt lgkmcnt(0)" ::: "memory"); __builtin_amdgcn_s_barrier(); asm volatile("" ::: "memory");
; #pragma unroll 1
;     for (int t = 0; t < nt; t += 2) {
;         if (t + 2 < nt) MU_B_WAIT(s1, 8); else MU_B_WAIT(s1, 0);
;         MU_G_LOAD(g0, t + 1); MU_B_WRITE(s1, 1, g0); __builtin_amdgcn_sched_barrier(0); MU_GLDS_A(1, t + 1); __builtin_amdgcn_sched_barrier(0);
;         if (t + 3 < nt) { MU_B_ISSUE(s1, t + 3); }
;         MU_COMPUTE(0);
;         MU_END(t + 3 >= nt);
;         if (t + 2 < nt) { MU_B_WAIT(s0, 8); MU_G_LOAD(g0, t + 2); MU_B_WRITE(s0, 0, g0); __builtin_amdgcn_sched_barrier(0); MU_GLDS_A(0, t + 2); __builtin_amdgcn_sched_barrier(0); }
;         if (t + 4 < nt) { MU_B_ISSUE(s0, t + 4); }
;         MU_COMPUTE(1);
;         MU_END(t + 4 >= nt);
	s_load_dwordx8 s[20:27], s[28:29], 0x0
	s_add_u32 s28, s28, 0x100
	s_addc_u32 s29, s29, 0
	v_mfma_f32_16x16x32_bf16 v[78:81], v[238:241], v[218:221], v[78:81]
	v_mfma_f32_16x16x32_bf16 v[74:77], v[242:245], v[218:221], v[74:77]
	v_mfma_f32_16x16x32_bf16 v[70:73], v[246:249], v[218:221], v[70:73]
	v_mfma_f32_16x16x32_bf16 v[66:69], v[250:253], v[218:221], v[66:69]
	ds_read_b128 v[218:221], v93 offset:0
	ds_read_b128 v[142:145], v141 offset:19456
	v_mfma_f32_16x16x32_bf16 v[62:65], v[238:241], v[222:225], v[62:65]
	v_mfma_f32_16x16x32_bf16 v[58:61], v[242:245], v[222:225], v[58:61]
	v_mfma_f32_16x16x32_bf16 v[54:57], v[246:249], v[222:225], v[54:57]
	v_mfma_f32_16x16x32_bf16 v[50:53], v[250:253], v[222:225], v[50:53]
	ds_read_b128 v[222:225], v93 offset:2048
	ds_read_b128 v[146:149], v141 offset:21504
	v_mfma_f32_16x16x32_bf16 v[46:49], v[238:241], v[226:229], v[46:49]
	v_mfma_f32_16x16x32_bf16 v[42:45], v[242:245], v[226:229], v[42:45]
	v_mfma_f32_16x16x32_bf16 v[38:41], v[246:249], v[226:229], v[38:41]
	v_mfma_f32_16x16x32_bf16 v[34:37], v[250:253], v[226:229], v[34:37]
	ds_read_b128 v[226:229], v93 offset:4096
	ds_read_b128 v[150:153], v141 offset:23552
	v_mfma_f32_16x16x32_bf16 v[18:21], v[238:241], v[230:233], v[18:21]
	v_mfma_f32_16x16x32_bf16 v[22:25], v[242:245], v[230:233], v[22:25]
	v_mfma_f32_16x16x32_bf16 v[26:29], v[246:249], v[230:233], v[26:29]
	v_mfma_f32_16x16x32_bf16 v[30:33], v[250:253], v[230:233], v[30:33]
	ds_read_b128 v[230:233], v93 offset:6144
	ds_read_b128 v[154:157], v141 offset:25600
	v_mfma_f32_16x16x32_bf16 v[2:5], v[238:241], v[234:237], v[2:5]
	v_mfma_f32_16x16x32_bf16 v[6:9], v[242:245], v[234:237], v[6:9]
	v_mfma_f32_16x16x32_bf16 v[10:13], v[246:249], v[234:237], v[10:13]
	v_mfma_f32_16x16x32_bf16 v[14:17], v[250:253], v[234:237], v[14:17]
	ds_read_b128 v[234:237], v93 offset:8192
	s_waitcnt vmcnt(13)
	s_mov_b32 s47, s42
	s_mov_b32 s42, s43
	s_mov_b32 s43, s44
	s_mov_b32 s44, s47
	s_waitcnt lgkmcnt(0)
	s_barrier
	s_add_i32 s47, s44, s6
	s_add_u32 s30, s30, 0x80
	s_addc_u32 s31, s31, 0
	v_mfma_f32_16x16x32_bf16 v[78:81], v[142:145], v[218:221], v[78:81]
	v_mfma_f32_16x16x32_bf16 v[74:77], v[146:149], v[218:221], v[74:77]
	v_mfma_f32_16x16x32_bf16 v[70:73], v[150:153], v[218:221], v[70:73]
	v_mfma_f32_16x16x32_bf16 v[66:69], v[154:157], v[218:221], v[66:69]
	s_mov_b32 m0, s47
	s_nop 0
	global_load_lds_dwordx4 v86, s[30:31]
	v_mfma_f32_16x16x32_bf16 v[62:65], v[142:145], v[222:225], v[62:65]
	v_mfma_f32_16x16x32_bf16 v[58:61], v[146:149], v[222:225], v[58:61]
	v_mfma_f32_16x16x32_bf16 v[54:57], v[150:153], v[222:225], v[54:57]
	v_mfma_f32_16x16x32_bf16 v[50:53], v[154:157], v[222:225], v[50:53]
	s_add_i32 m0, s47, 0x2000
	s_nop 0
	global_load_lds_dwordx4 v134, s[30:31]
	v_mfma_f32_16x16x32_bf16 v[46:49], v[142:145], v[226:229], v[46:49]
	v_mfma_f32_16x16x32_bf16 v[42:45], v[146:149], v[226:229], v[42:45]
	v_mfma_f32_16x16x32_bf16 v[38:41], v[150:153], v[226:229], v[38:41]
	v_mfma_f32_16x16x32_bf16 v[34:37], v[154:157], v[226:229], v[34:37]
	s_add_i32 m0, s47, 0x4000
	s_nop 0
	global_load_lds_dwordx4 v136, s[30:31]
	v_mfma_f32_16x16x32_bf16 v[18:21], v[142:145], v[230:233], v[18:21]
	v_mfma_f32_16x16x32_bf16 v[22:25], v[146:149], v[230:233], v[22:25]
	v_mfma_f32_16x16x32_bf16 v[26:29], v[150:153], v[230:233], v[26:29]
	v_mfma_f32_16x16x32_bf16 v[30:33], v[154:157], v[230:233], v[30:33]
	s_add_i32 m0, s47, 0x6000
	s_nop 0
	global_load_lds_dwordx4 v138, s[30:31]
	v_mfma_f32_16x16x32_bf16 v[2:5], v[142:145], v[234:237], v[2:5]
	v_mfma_f32_16x16x32_bf16 v[6:9], v[146:149], v[234:237], v[6:9]
	v_mfma_f32_16x16x32_bf16 v[10:13], v[150:153], v[234:237], v[10:13]
	v_mfma_f32_16x16x32_bf16 v[14:17], v[154:157], v[234:237], v[14:17]
	s_add_i32 m0, s47, 0x8000
	s_nop 0
	global_load_lds_dwordx4 v140, s[30:31]
	v_mul_f32_e32 v114, s20, v114
	v_mul_f32_e32 v115, s20, v115
	v_mul_f32_e32 v116, s21, v116
	v_mul_f32_e32 v117, s21, v117
	v_mul_f32_e32 v118, s22, v118
	v_mul_f32_e32 v119, s22, v119
	v_mul_f32_e32 v120, s23, v120
	v_mul_f32_e32 v121, s23, v121
	v_mul_f32_e32 v122, s24, v122
	v_mul_f32_e32 v123, s24, v123
	v_mul_f32_e32 v124, s25, v124
	v_mul_f32_e32 v125, s25, v125
	v_mul_f32_e32 v126, s26, v126
	v_mul_f32_e32 v127, s26, v127
	v_mul_f32_e32 v128, s27, v128
	v_mul_f32_e32 v129, s27, v129
	v_cvt_pk_bf16_f32 v158, v114, v116
	v_cvt_pk_bf16_f32 v159, v118, v120
	v_cvt_pk_bf16_f32 v160, v122, v124
	v_cvt_pk_bf16_f32 v161, v126, v128
	v_cvt_pk_bf16_f32 v162, v115, v117
	v_cvt_pk_bf16_f32 v163, v119, v121
	v_cvt_pk_bf16_f32 v164, v123, v125
	v_cvt_pk_bf16_f32 v165, v127, v129
	ds_write_b128 v1, v[158:161] offset:19456
	ds_write_b128 v1, v[162:165] offset:19584
	v_add_u32_e32 v91, s42, v135
	v_add_u32_e32 v93, s42, v137
	ds_read_b128 v[238:241], v139 offset:0
	ds_read_b128 v[242:245], v139 offset:2048
	ds_read_b128 v[246:249], v139 offset:4096
	ds_read_b128 v[250:253], v139 offset:6144
	ds_read_b128 v[218:221], v91 offset:0
	ds_read_b128 v[222:225], v91 offset:2048
	ds_read_b128 v[226:229], v91 offset:4096
	ds_read_b128 v[230:233], v91 offset:6144
	ds_read_b128 v[234:237], v91 offset:8192
	s_waitcnt lgkmcnt(0)
; #define MU_GLDS_A(buf, kt) do { _Pragma("unroll") for (int i = 0; i < NMU; ++i) \
;         __builtin_amdgcn_global_load_lds((const unsigned*)((const char*)A + aoff[i] + (size_t)(kt) * 128), (PG8_LAS unsigned*)(MU_SA(buf) + wid * 1024 + i * 8192), 16, 0, 0); } while (0)
; #define MU_B_ISSUE(sb, kt) do { const char* kb_ = Bb + (size_t)(kt) * (64 * (size_t)RB); _Pragma("unroll") for (int j = 0; j < 8; ++j) { const char* p_ = kb_ + (size_t)j * RB; \
;         asm volatile("global_load_dwordx2 %0, %1, off" : "=&v"(sb[j]) : "v"(p_) : "memory"); } } while (0)
; #define MU_B_WAIT(sb, N) asm volatile("s_waitcnt vmcnt(%8)" : "+v"(sb[0]), "+v"(sb[1]), "+v"(sb[2]), "+v"(sb[3]), "+v"(sb[4]), "+v"(sb[5]), "+v"(sb[6]), "+v"(sb[7]) : "n"(N) : "memory")
; #define MU_COMPUTE(buf) MU_COMPUTE_N(buf, NMU)
; template <int MODE>
; __device__ __forceinline__ void moe_unit(PG8_LAS unsigned char* lds, int e, int cb, int slot0  , int nv  , const bf16_t* A, const int* slot_tok,
;                                          const float* W0, const float* W1, bf16_t* OUT, const float* slot_rs  , const int* slot_dst) {
;     ...
;     f32x4 acc[NMU][4];
; #pragma unroll
;     for (int m = 0; m < NMU; ++m)
; #pragma unroll
;         for (int n = 0; n < 4; ++n) acc[m][n] = (f32x4){0.f, 0.f, 0.f, 0.f};
;     f32x2 s0[8], s1[8];
;     float g0[8];
;     MU_GLDS_A(0, 0); MU_B_ISSUE(s0, 0); MU_G_LOAD(g0, 0); MU_B_ISSUE(s1, 1);
;     MU_B_WAIT(s0, 8); MU_B_WRITE(s0, 0, g0); __builtin_amdgcn_sched_barrier(0); MU_B_ISSUE(s0, 2);
;     asm volatile("s_waitcnt vmcnt(16)" ::: "memory");
;     asm volatile("s_waitcnt lgkmcnt(0)" ::: "memory"); __builtin_amdgcn_s_barrier(); asm volatile("" ::: "memory");
; #pragma unroll 1
;     for (int t = 0; t < nt; t += 2) {
;         if (t + 2 < nt) MU_B_WAIT(s1, 8); else MU_B_WAIT(s1, 0);
;         MU_G_LOAD(g0, t + 1); MU_B_WRITE(s1, 1, g0); __builtin_amdgcn_sched_barrier(0); MU_GLDS_A(1, t + 1); __builtin_amdgcn_sched_barrier(0);
;         if (t + 3 < nt) { MU_B_ISSUE(s1, t + 3); }
;         MU_COMPUTE(0);
;         MU_END(t + 3 >= nt);
;         if (t + 2 < nt) { MU_B_WAIT(s0, 8); MU_G_LOAD(g0, t + 2); MU_B_WRITE(s0, 0, g0); __builtin_amdgcn_sched_barrier(0); MU_GLDS_A(0, t + 2); __builtin_amdgcn_sched_barrier(0); }
;         if (t + 4 < nt) { MU_B_ISSUE(s0, t + 4); }
;         MU_COMPUTE(1);
;         MU_END(t + 4 >= nt);
	s_load_dwordx8 s[12:19], s[28:29], 0x0
	s_add_u32 s28, s28, 0x100
	s_addc_u32 s29, s29, 0
	v_mfma_f32_16x16x32_bf16 v[78:81], v[238:241], v[218:221], v[78:81]
	v_mfma_f32_16x16x32_bf16 v[74:77], v[242:245], v[218:221], v[74:77]
	v_mfma_f32_16x16x32_bf16 v[70:73], v[246:249], v[218:221], v[70:73]
	v_mfma_f32_16x16x32_bf16 v[66:69], v[250:253], v[218:221], v[66:69]
	ds_read_b128 v[218:221], v93 offset:0
	ds_read_b128 v[142:145], v141 offset:0
	v_mfma_f32_16x16x32_bf16 v[62:65], v[238:241], v[222:225], v[62:65]
	v_mfma_f32_16x16x32_bf16 v[58:61], v[242:245], v[222:225], v[58:61]
	v_mfma_f32_16x16x32_bf16 v[54:57], v[246:249], v[222:225], v[54:57]
	v_mfma_f32_16x16x32_bf16 v[50:53], v[250:253], v[222:225], v[50:53]
	ds_read_b128 v[222:225], v93 offset:2048
	ds_read_b128 v[146:149], v141 offset:2048
	v_mfma_f32_16x16x32_bf16 v[46:49], v[238:241], v[226:229], v[46:49]
	v_mfma_f32_16x16x32_bf16 v[42:45], v[242:245], v[226:229], v[42:45]
	v_mfma_f32_16x16x32_bf16 v[38:41], v[246:249], v[226:229], v[38:41]
	v_mfma_f32_16x16x32_bf16 v[34:37], v[250:253], v[226:229], v[34:37]
	ds_read_b128 v[226:229], v93 offset:4096
	ds_read_b128 v[150:153], v141 offset:4096
	v_mfma_f32_16x16x32_bf16 v[18:21], v[238:241], v[230:233], v[18:21]
	v_mfma_f32_16x16x32_bf16 v[22:25], v[242:245], v[230:233], v[22:25]
	v_mfma_f32_16x16x32_bf16 v[26:29], v[246:249], v[230:233], v[26:29]
	v_mfma_f32_16x16x32_bf16 v[30:33], v[250:253], v[230:233], v[30:33]
	ds_read_b128 v[230:233], v93 offset:6144
	ds_read_b128 v[154:157], v141 offset:6144
	v_mfma_f32_16x16x32_bf16 v[2:5], v[238:241], v[234:237], v[2:5]
	v_mfma_f32_16x16x32_bf16 v[6:9], v[242:245], v[234:237], v[6:9]
	v_mfma_f32_16x16x32_bf16 v[10:13], v[246:249], v[234:237], v[10:13]
	v_mfma_f32_16x16x32_bf16 v[14:17], v[250:253], v[234:237], v[14:17]
	ds_read_b128 v[234:237], v93 offset:8192
	s_waitcnt vmcnt(5)
	s_mov_b32 s47, s42
	s_mov_b32 s42, s43
	s_mov_b32 s43, s44
	s_mov_b32 s44, s47
	s_waitcnt lgkmcnt(0)
	s_barrier
	s_add_i32 s47, s44, s6
	s_add_u32 s30, s30, 0x80
	s_addc_u32 s31, s31, 0
	v_mfma_f32_16x16x32_bf16 v[78:81], v[142:145], v[218:221], v[78:81]
	v_mfma_f32_16x16x32_bf16 v[74:77], v[146:149], v[218:221], v[74:77]
	v_mfma_f32_16x16x32_bf16 v[70:73], v[150:153], v[218:221], v[70:73]
	v_mfma_f32_16x16x32_bf16 v[66:69], v[154:157], v[218:221], v[66:69]
	s_mov_b32 m0, s47
	s_nop 0
	global_load_lds_dwordx4 v86, s[30:31]
	v_mfma_f32_16x16x32_bf16 v[62:65], v[142:145], v[222:225], v[62:65]
	v_mfma_f32_16x16x32_bf16 v[58:61], v[146:149], v[222:225], v[58:61]
	v_mfma_f32_16x16x32_bf16 v[54:57], v[150:153], v[222:225], v[54:57]
	v_mfma_f32_16x16x32_bf16 v[50:53], v[154:157], v[222:225], v[50:53]
	s_add_i32 m0, s47, 0x2000
	s_nop 0
	global_load_lds_dwordx4 v134, s[30:31]
	v_mfma_f32_16x16x32_bf16 v[46:49], v[142:145], v[226:229], v[46:49]
	v_mfma_f32_16x16x32_bf16 v[42:45], v[146:149], v[226:229], v[42:45]
	v_mfma_f32_16x16x32_bf16 v[38:41], v[150:153], v[226:229], v[38:41]
	v_mfma_f32_16x16x32_bf16 v[34:37], v[154:157], v[226:229], v[34:37]
	s_add_i32 m0, s47, 0x4000
	s_nop 0
	global_load_lds_dwordx4 v136, s[30:31]
	v_mfma_f32_16x16x32_bf16 v[18:21], v[142:145], v[230:233], v[18:21]
	v_mfma_f32_16x16x32_bf16 v[22:25], v[146:149], v[230:233], v[22:25]
	v_mfma_f32_16x16x32_bf16 v[26:29], v[150:153], v[230:233], v[26:29]
	v_mfma_f32_16x16x32_bf16 v[30:33], v[154:157], v[230:233], v[30:33]
	s_add_i32 m0, s47, 0x6000
	s_nop 0
	global_load_lds_dwordx4 v138, s[30:31]
	v_mfma_f32_16x16x32_bf16 v[2:5], v[142:145], v[234:237], v[2:5]
	v_mfma_f32_16x16x32_bf16 v[6:9], v[146:149], v[234:237], v[6:9]
	v_mfma_f32_16x16x32_bf16 v[10:13], v[150:153], v[234:237], v[10:13]
	v_mfma_f32_16x16x32_bf16 v[14:17], v[154:157], v[234:237], v[14:17]
	s_add_i32 m0, s47, 0x8000
	s_nop 0
	global_load_lds_dwordx4 v140, s[30:31]
	v_mul_f32_e32 v186, s12, v186
	v_mul_f32_e32 v187, s12, v187
	v_mul_f32_e32 v188, s13, v188
	v_mul_f32_e32 v189, s13, v189
	v_mul_f32_e32 v190, s14, v190
	v_mul_f32_e32 v191, s14, v191
	v_mul_f32_e32 v192, s15, v192
	v_mul_f32_e32 v193, s15, v193
	v_mul_f32_e32 v194, s16, v194
	v_mul_f32_e32 v195, s16, v195
	v_mul_f32_e32 v196, s17, v196
	v_mul_f32_e32 v197, s17, v197
	v_mul_f32_e32 v198, s18, v198
	v_mul_f32_e32 v199, s18, v199
	v_mul_f32_e32 v200, s19, v200
	v_mul_f32_e32 v201, s19, v201
	v_cvt_pk_bf16_f32 v158, v186, v188
	v_cvt_pk_bf16_f32 v159, v190, v192
	v_cvt_pk_bf16_f32 v160, v194, v196
	v_cvt_pk_bf16_f32 v161, v198, v200
	v_cvt_pk_bf16_f32 v162, v187, v189
	v_cvt_pk_bf16_f32 v163, v191, v193
	v_cvt_pk_bf16_f32 v164, v195, v197
	v_cvt_pk_bf16_f32 v165, v199, v201
	ds_write_b128 v1, v[158:161] offset:0
	ds_write_b128 v1, v[162:165] offset:128
	v_add_u32_e32 v91, s42, v135
	v_add_u32_e32 v93, s42, v137
	ds_read_b128 v[238:241], v139 offset:19456
	ds_read_b128 v[242:245], v139 offset:21504
	ds_read_b128 v[246:249], v139 offset:23552
	ds_read_b128 v[250:253], v139 offset:25600
	ds_read_b128 v[218:221], v91 offset:0
	ds_read_b128 v[222:225], v91 offset:2048
	ds_read_b128 v[226:229], v91 offset:4096
	ds_read_b128 v[230:233], v91 offset:6144
	ds_read_b128 v[234:237], v91 offset:8192
	s_waitcnt lgkmcnt(0)
; #define MU_GLDS_A(buf, kt) do { _Pragma("unroll") for (int i = 0; i < NMU; ++i) \
;         __builtin_amdgcn_global_load_lds((const unsigned*)((const char*)A + aoff[i] + (size_t)(kt) * 128), (PG8_LAS unsigned*)(MU_SA(buf) + wid * 1024 + i * 8192), 16, 0, 0); } while (0)
; #define MU_B_ISSUE(sb, kt) do { const char* kb_ = Bb + (size_t)(kt) * (64 * (size_t)RB); _Pragma("unroll") for (int j = 0; j < 8; ++j) { const char* p_ = kb_ + (size_t)j * RB; \
;         asm volatile("global_load_dwordx2 %0, %1, off" : "=&v"(sb[j]) : "v"(p_) : "memory"); } } while (0)
; #define MU_B_WAIT(sb, N) asm volatile("s_waitcnt vmcnt(%8)" : "+v"(sb[0]), "+v"(sb[1]), "+v"(sb[2]), "+v"(sb[3]), "+v"(sb[4]), "+v"(sb[5]), "+v"(sb[6]), "+v"(sb[7]) : "n"(N) : "memory")
; #define MU_COMPUTE(buf) MU_COMPUTE_N(buf, NMU)
; template <int MODE>
; __device__ __forceinline__ void moe_unit(PG8_LAS unsigned char* lds, int e, int cb, int slot0  , int nv  , const bf16_t* A, const int* slot_tok,
;                                          const float* W0, const float* W1, bf16_t* OUT, const float* slot_rs  , const int* slot_dst) {
;     ...
;     f32x4 acc[NMU][4];
; #pragma unroll
;     for (int m = 0; m < NMU; ++m)
; #pragma unroll
;         for (int n = 0; n < 4; ++n) acc[m][n] = (f32x4){0.f, 0.f, 0.f, 0.f};
;     f32x2 s0[8], s1[8];
;     float g0[8];
;     MU_GLDS_A(0, 0); MU_B_ISSUE(s0, 0); MU_G_LOAD(g0, 0); MU_B_ISSUE(s1, 1);
;     MU_B_WAIT(s0, 8); MU_B_WRITE(s0, 0, g0); __builtin_amdgcn_sched_barrier(0); MU_B_ISSUE(s0, 2);
;     asm volatile("s_waitcnt vmcnt(16)" ::: "memory");
;     asm volatile("s_waitcnt lgkmcnt(0)" ::: "memory"); __builtin_amdgcn_s_barrier(); asm volatile("" ::: "memory");
; #pragma unroll 1
;     for (int t = 0; t < nt; t += 2) {
;         if (t + 2 < nt) MU_B_WAIT(s1, 8); else MU_B_WAIT(s1, 0);
;         MU_G_LOAD(g0, t + 1); MU_B_WRITE(s1, 1, g0); __builtin_amdgcn_sched_barrier(0); MU_GLDS_A(1, t + 1); __builtin_amdgcn_sched_barrier(0);
;         if (t + 3 < nt) { MU_B_ISSUE(s1, t + 3); }
;         MU_COMPUTE(0);
;         MU_END(t + 3 >= nt);
;         if (t + 2 < nt) { MU_B_WAIT(s0, 8); MU_G_LOAD(g0, t + 2); MU_B_WRITE(s0, 0, g0); __builtin_amdgcn_sched_barrier(0); MU_GLDS_A(0, t + 2); __builtin_amdgcn_sched_barrier(0); }
;         if (t + 4 < nt) { MU_B_ISSUE(s0, t + 4); }
;         MU_COMPUTE(1);
;         MU_END(t + 4 >= nt);
	s_load_dwordx8 s[20:27], s[28:29], 0x0
	s_add_u32 s28, s28, 0x100
	s_addc_u32 s29, s29, 0
	v_mfma_f32_16x16x32_bf16 v[78:81], v[238:241], v[218:221], v[78:81]
	v_mfma_f32_16x16x32_bf16 v[74:77], v[242:245], v[218:221], v[74:77]
	v_mfma_f32_16x16x32_bf16 v[70:73], v[246:249], v[218:221], v[70:73]
	v_mfma_f32_16x16x32_bf16 v[66:69], v[250:253], v[218:221], v[66:69]
	ds_read_b128 v[218:221], v93 offset:0
	ds_read_b128 v[142:145], v141 offset:19456
	v_mfma_f32_16x16x32_bf16 v[62:65], v[238:241], v[222:225], v[62:65]
	v_mfma_f32_16x16x32_bf16 v[58:61], v[242:245], v[222:225], v[58:61]
	v_mfma_f32_16x16x32_bf16 v[54:57], v[246:249], v[222:225], v[54:57]
	v_mfma_f32_16x16x32_bf16 v[50:53], v[250:253], v[222:225], v[50:53]
	ds_read_b128 v[222:225], v93 offset:2048
	ds_read_b128 v[146:149], v141 offset:21504
	v_mfma_f32_16x16x32_bf16 v[46:49], v[238:241], v[226:229], v[46:49]
	v_mfma_f32_16x16x32_bf16 v[42:45], v[242:245], v[226:229], v[42:45]
	v_mfma_f32_16x16x32_bf16 v[38:41], v[246:249], v[226:229], v[38:41]
	v_mfma_f32_16x16x32_bf16 v[34:37], v[250:253], v[226:229], v[34:37]
	ds_read_b128 v[226:229], v93 offset:4096
	ds_read_b128 v[150:153], v141 offset:23552
	v_mfma_f32_16x16x32_bf16 v[18:21], v[238:241], v[230:233], v[18:21]
	v_mfma_f32_16x16x32_bf16 v[22:25], v[242:245], v[230:233], v[22:25]
	v_mfma_f32_16x16x32_bf16 v[26:29], v[246:249], v[230:233], v[26:29]
	v_mfma_f32_16x16x32_bf16 v[30:33], v[250:253], v[230:233], v[30:33]
	ds_read_b128 v[230:233], v93 offset:6144
	ds_read_b128 v[154:157], v141 offset:25600
	v_mfma_f32_16x16x32_bf16 v[2:5], v[238:241], v[234:237], v[2:5]
	v_mfma_f32_16x16x32_bf16 v[6:9], v[242:245], v[234:237], v[6:9]
	v_mfma_f32_16x16x32_bf16 v[10:13], v[246:249], v[234:237], v[10:13]
	v_mfma_f32_16x16x32_bf16 v[14:17], v[250:253], v[234:237], v[14:17]
	ds_read_b128 v[234:237], v93 offset:8192
	s_waitcnt vmcnt(5)
	s_mov_b32 s47, s42
	s_mov_b32 s42, s43
	s_mov_b32 s43, s44
	s_mov_b32 s44, s47
	s_waitcnt lgkmcnt(0)
	s_barrier
	v_mfma_f32_16x16x32_bf16 v[78:81], v[142:145], v[218:221], v[78:81]
	v_mfma_f32_16x16x32_bf16 v[74:77], v[146:149], v[218:221], v[74:77]
	v_mfma_f32_16x16x32_bf16 v[70:73], v[150:153], v[218:221], v[70:73]
	v_mfma_f32_16x16x32_bf16 v[66:69], v[154:157], v[218:221], v[66:69]
	v_mfma_f32_16x16x32_bf16 v[62:65], v[142:145], v[222:225], v[62:65]
	v_mfma_f32_16x16x32_bf16 v[58:61], v[146:149], v[222:225], v[58:61]
	v_mfma_f32_16x16x32_bf16 v[54:57], v[150:153], v[222:225], v[54:57]
	v_mfma_f32_16x16x32_bf16 v[50:53], v[154:157], v[222:225], v[50:53]
	v_mfma_f32_16x16x32_bf16 v[46:49], v[142:145], v[226:229], v[46:49]
	v_mfma_f32_16x16x32_bf16 v[42:45], v[146:149], v[226:229], v[42:45]
	v_mfma_f32_16x16x32_bf16 v[38:41], v[150:153], v[226:229], v[38:41]
	v_mfma_f32_16x16x32_bf16 v[34:37], v[154:157], v[226:229], v[34:37]
	v_mfma_f32_16x16x32_bf16 v[18:21], v[142:145], v[230:233], v[18:21]
	v_mfma_f32_16x16x32_bf16 v[22:25], v[146:149], v[230:233], v[22:25]
	v_mfma_f32_16x16x32_bf16 v[26:29], v[150:153], v[230:233], v[26:29]
	v_mfma_f32_16x16x32_bf16 v[30:33], v[154:157], v[230:233], v[30:33]
	v_mfma_f32_16x16x32_bf16 v[2:5], v[142:145], v[234:237], v[2:5]
	v_mfma_f32_16x16x32_bf16 v[6:9], v[146:149], v[234:237], v[6:9]
	v_mfma_f32_16x16x32_bf16 v[10:13], v[150:153], v[234:237], v[10:13]
	v_mfma_f32_16x16x32_bf16 v[14:17], v[154:157], v[234:237], v[14:17]
	v_mul_f32_e32 v202, s20, v202
	v_mul_f32_e32 v203, s20, v203
	v_mul_f32_e32 v204, s21, v204
	v_mul_f32_e32 v205, s21, v205
	v_mul_f32_e32 v206, s22, v206
	v_mul_f32_e32 v207, s22, v207
	v_mul_f32_e32 v208, s23, v208
	v_mul_f32_e32 v209, s23, v209
	v_mul_f32_e32 v210, s24, v210
	v_mul_f32_e32 v211, s24, v211
	v_mul_f32_e32 v212, s25, v212
	v_mul_f32_e32 v213, s25, v213
	v_mul_f32_e32 v214, s26, v214
	v_mul_f32_e32 v215, s26, v215
	v_mul_f32_e32 v216, s27, v216
	v_mul_f32_e32 v217, s27, v217
	v_cvt_pk_bf16_f32 v158, v202, v204
	v_cvt_pk_bf16_f32 v159, v206, v208
	v_cvt_pk_bf16_f32 v160, v210, v212
	v_cvt_pk_bf16_f32 v161, v214, v216
	v_cvt_pk_bf16_f32 v162, v203, v205
	v_cvt_pk_bf16_f32 v163, v207, v209
	v_cvt_pk_bf16_f32 v164, v211, v213
	v_cvt_pk_bf16_f32 v165, v215, v217
	ds_write_b128 v1, v[158:161] offset:19456
	ds_write_b128 v1, v[162:165] offset:19584
	v_add_u32_e32 v91, s42, v135
	v_add_u32_e32 v93, s42, v137
	ds_read_b128 v[238:241], v139 offset:0
	ds_read_b128 v[242:245], v139 offset:2048
	ds_read_b128 v[246:249], v139 offset:4096
	ds_read_b128 v[250:253], v139 offset:6144
	ds_read_b128 v[218:221], v91 offset:0
	ds_read_b128 v[222:225], v91 offset:2048
	ds_read_b128 v[226:229], v91 offset:4096
	ds_read_b128 v[230:233], v91 offset:6144
	ds_read_b128 v[234:237], v91 offset:8192
	s_waitcnt lgkmcnt(0)
	v_mfma_f32_16x16x32_bf16 v[78:81], v[238:241], v[218:221], v[78:81]
	v_mfma_f32_16x16x32_bf16 v[74:77], v[242:245], v[218:221], v[74:77]
	v_mfma_f32_16x16x32_bf16 v[70:73], v[246:249], v[218:221], v[70:73]
	v_mfma_f32_16x16x32_bf16 v[66:69], v[250:253], v[218:221], v[66:69]
	ds_read_b128 v[218:221], v93 offset:0
	ds_read_b128 v[142:145], v141 offset:0
	v_mfma_f32_16x16x32_bf16 v[62:65], v[238:241], v[222:225], v[62:65]
	v_mfma_f32_16x16x32_bf16 v[58:61], v[242:245], v[222:225], v[58:61]
	v_mfma_f32_16x16x32_bf16 v[54:57], v[246:249], v[222:225], v[54:57]
	v_mfma_f32_16x16x32_bf16 v[50:53], v[250:253], v[222:225], v[50:53]
	ds_read_b128 v[222:225], v93 offset:2048
	ds_read_b128 v[146:149], v141 offset:2048
	v_mfma_f32_16x16x32_bf16 v[46:49], v[238:241], v[226:229], v[46:49]
	v_mfma_f32_16x16x32_bf16 v[42:45], v[242:245], v[226:229], v[42:45]
	v_mfma_f32_16x16x32_bf16 v[38:41], v[246:249], v[226:229], v[38:41]
	v_mfma_f32_16x16x32_bf16 v[34:37], v[250:253], v[226:229], v[34:37]
	ds_read_b128 v[226:229], v93 offset:4096
	ds_read_b128 v[150:153], v141 offset:4096
	v_mfma_f32_16x16x32_bf16 v[18:21], v[238:241], v[230:233], v[18:21]
	v_mfma_f32_16x16x32_bf16 v[22:25], v[242:245], v[230:233], v[22:25]
	v_mfma_f32_16x16x32_bf16 v[26:29], v[246:249], v[230:233], v[26:29]
	v_mfma_f32_16x16x32_bf16 v[30:33], v[250:253], v[230:233], v[30:33]
	ds_read_b128 v[230:233], v93 offset:6144
	ds_read_b128 v[154:157], v141 offset:6144
	v_mfma_f32_16x16x32_bf16 v[2:5], v[238:241], v[234:237], v[2:5]
	v_mfma_f32_16x16x32_bf16 v[6:9], v[242:245], v[234:237], v[6:9]
	v_mfma_f32_16x16x32_bf16 v[10:13], v[246:249], v[234:237], v[10:13]
	v_mfma_f32_16x16x32_bf16 v[14:17], v[250:253], v[234:237], v[14:17]
	ds_read_b128 v[234:237], v93 offset:8192
	s_waitcnt vmcnt(0)
	s_mov_b32 s47, s42
	s_mov_b32 s42, s43
	s_mov_b32 s43, s44
	s_mov_b32 s44, s47
	s_waitcnt lgkmcnt(0)
	s_barrier
; #define MU_GLDS_A(buf, kt) do { _Pragma("unroll") for (int i = 0; i < NMU; ++i) \
;         __builtin_amdgcn_global_load_lds((const unsigned*)((const char*)A + aoff[i] + (size_t)(kt) * 128), (PG8_LAS unsigned*)(MU_SA(buf) + wid * 1024 + i * 8192), 16, 0, 0); } while (0)
; #define MU_B_ISSUE(sb, kt) do { const char* kb_ = Bb + (size_t)(kt) * (64 * (size_t)RB); _Pragma("unroll") for (int j = 0; j < 8; ++j) { const char* p_ = kb_ + (size_t)j * RB; \
;         asm volatile("global_load_dwordx2 %0, %1, off" : "=&v"(sb[j]) : "v"(p_) : "memory"); } } while (0)
; #define MU_B_WAIT(sb, N) asm volatile("s_waitcnt vmcnt(%8)" : "+v"(sb[0]), "+v"(sb[1]), "+v"(sb[2]), "+v"(sb[3]), "+v"(sb[4]), "+v"(sb[5]), "+v"(sb[6]), "+v"(sb[7]) : "n"(N) : "memory")
; #define MU_COMPUTE(buf) MU_COMPUTE_N(buf, NMU)
; template <int MODE>
; __device__ __forceinline__ void moe_unit(PG8_LAS unsigned char* lds, int e, int cb, int slot0  , int nv  , const bf16_t* A, const int* slot_tok,
;                                          const float* W0, const float* W1, bf16_t* OUT, const float* slot_rs  , const int* slot_dst) {
;     ...
;     f32x4 acc[NMU][4];
; #pragma unroll
;     for (int m = 0; m < NMU; ++m)
; #pragma unroll
;         for (int n = 0; n < 4; ++n) acc[m][n] = (f32x4){0.f, 0.f, 0.f, 0.f};
;     f32x2 s0[8], s1[8];
;     float g0[8];
;     MU_GLDS_A(0, 0); MU_B_ISSUE(s0, 0); MU_G_LOAD(g0, 0); MU_B_ISSUE(s1, 1);
;     MU_B_WAIT(s0, 8); MU_B_WRITE(s0, 0, g0); __builtin_amdgcn_sched_barrier(0); MU_B_ISSUE(s0, 2);
;     asm volatile("s_waitcnt vmcnt(16)" ::: "memory");
;     asm volatile("s_waitcnt lgkmcnt(0)" ::: "memory"); __builtin_amdgcn_s_barrier(); asm volatile("" ::: "memory");
; #pragma unroll 1
;     for (int t = 0; t < nt; t += 2) {
;         if (t + 2 < nt) MU_B_WAIT(s1, 8); else MU_B_WAIT(s1, 0);
;         MU_G_LOAD(g0, t + 1); MU_B_WRITE(s1, 1, g0); __builtin_amdgcn_sched_barrier(0); MU_GLDS_A(1, t + 1); __builtin_amdgcn_sched_barrier(0);
;         if (t + 3 < nt) { MU_B_ISSUE(s1, t + 3); }
;         MU_COMPUTE(0);
;         MU_END(t + 3 >= nt);
;         if (t + 2 < nt) { MU_B_WAIT(s0, 8); MU_G_LOAD(g0, t + 2); MU_B_WRITE(s0, 0, g0); __builtin_amdgcn_sched_barrier(0); MU_GLDS_A(0, t + 2); __builtin_amdgcn_sched_barrier(0); }
;         if (t + 4 < nt) { MU_B_ISSUE(s0, t + 4); }
;         MU_COMPUTE(1);
;         MU_END(t + 4 >= nt);
	v_mfma_f32_16x16x32_bf16 v[78:81], v[142:145], v[218:221], v[78:81]
	v_mfma_f32_16x16x32_bf16 v[74:77], v[146:149], v[218:221], v[74:77]
	v_mfma_f32_16x16x32_bf16 v[70:73], v[150:153], v[218:221], v[70:73]
	v_mfma_f32_16x16x32_bf16 v[66:69], v[154:157], v[218:221], v[66:69]
	v_mfma_f32_16x16x32_bf16 v[62:65], v[142:145], v[222:225], v[62:65]
	v_mfma_f32_16x16x32_bf16 v[58:61], v[146:149], v[222:225], v[58:61]
	v_mfma_f32_16x16x32_bf16 v[54:57], v[150:153], v[222:225], v[54:57]
	v_mfma_f32_16x16x32_bf16 v[50:53], v[154:157], v[222:225], v[50:53]
	v_mfma_f32_16x16x32_bf16 v[46:49], v[142:145], v[226:229], v[46:49]
	v_mfma_f32_16x16x32_bf16 v[42:45], v[146:149], v[226:229], v[42:45]
	v_mfma_f32_16x16x32_bf16 v[38:41], v[150:153], v[226:229], v[38:41]
	v_mfma_f32_16x16x32_bf16 v[34:37], v[154:157], v[226:229], v[34:37]
	v_mfma_f32_16x16x32_bf16 v[18:21], v[142:145], v[230:233], v[18:21]
	v_mfma_f32_16x16x32_bf16 v[22:25], v[146:149], v[230:233], v[22:25]
	v_mfma_f32_16x16x32_bf16 v[26:29], v[150:153], v[230:233], v[26:29]
	v_mfma_f32_16x16x32_bf16 v[30:33], v[154:157], v[230:233], v[30:33]
	v_mfma_f32_16x16x32_bf16 v[2:5], v[142:145], v[234:237], v[2:5]
	v_mfma_f32_16x16x32_bf16 v[6:9], v[146:149], v[234:237], v[6:9]
	v_mfma_f32_16x16x32_bf16 v[10:13], v[150:153], v[234:237], v[10:13]
	v_mfma_f32_16x16x32_bf16 v[14:17], v[154:157], v[234:237], v[14:17]
	v_add_u32_e32 v91, s42, v135
	v_add_u32_e32 v93, s42, v137
	ds_read_b128 v[238:241], v139 offset:19456
	ds_read_b128 v[242:245], v139 offset:21504
	ds_read_b128 v[246:249], v139 offset:23552
	ds_read_b128 v[250:253], v139 offset:25600
	ds_read_b128 v[218:221], v91 offset:0
	ds_read_b128 v[222:225], v91 offset:2048
	ds_read_b128 v[226:229], v91 offset:4096
	ds_read_b128 v[230:233], v91 offset:6144
	ds_read_b128 v[234:237], v91 offset:8192
	s_waitcnt lgkmcnt(0)
	v_mfma_f32_16x16x32_bf16 v[78:81], v[238:241], v[218:221], v[78:81]
	v_mfma_f32_16x16x32_bf16 v[74:77], v[242:245], v[218:221], v[74:77]
	v_mfma_f32_16x16x32_bf16 v[70:73], v[246:249], v[218:221], v[70:73]
	v_mfma_f32_16x16x32_bf16 v[66:69], v[250:253], v[218:221], v[66:69]
	ds_read_b128 v[218:221], v93 offset:0
	ds_read_b128 v[142:145], v141 offset:19456
	v_mfma_f32_16x16x32_bf16 v[62:65], v[238:241], v[222:225], v[62:65]
	v_mfma_f32_16x16x32_bf16 v[58:61], v[242:245], v[222:225], v[58:61]
	v_mfma_f32_16x16x32_bf16 v[54:57], v[246:249], v[222:225], v[54:57]
	v_mfma_f32_16x16x32_bf16 v[50:53], v[250:253], v[222:225], v[50:53]
	ds_read_b128 v[222:225], v93 offset:2048
	ds_read_b128 v[146:149], v141 offset:21504
	v_mfma_f32_16x16x32_bf16 v[46:49], v[238:241], v[226:229], v[46:49]
	v_mfma_f32_16x16x32_bf16 v[42:45], v[242:245], v[226:229], v[42:45]
	v_mfma_f32_16x16x32_bf16 v[38:41], v[246:249], v[226:229], v[38:41]
	v_mfma_f32_16x16x32_bf16 v[34:37], v[250:253], v[226:229], v[34:37]
	ds_read_b128 v[226:229], v93 offset:4096
	ds_read_b128 v[150:153], v141 offset:23552
	v_mfma_f32_16x16x32_bf16 v[18:21], v[238:241], v[230:233], v[18:21]
	v_mfma_f32_16x16x32_bf16 v[22:25], v[242:245], v[230:233], v[22:25]
	v_mfma_f32_16x16x32_bf16 v[26:29], v[246:249], v[230:233], v[26:29]
	v_mfma_f32_16x16x32_bf16 v[30:33], v[250:253], v[230:233], v[30:33]
	ds_read_b128 v[230:233], v93 offset:6144
	ds_read_b128 v[154:157], v141 offset:25600
	v_mfma_f32_16x16x32_bf16 v[2:5], v[238:241], v[234:237], v[2:5]
	v_mfma_f32_16x16x32_bf16 v[6:9], v[242:245], v[234:237], v[6:9]
	v_mfma_f32_16x16x32_bf16 v[10:13], v[246:249], v[234:237], v[10:13]
	v_mfma_f32_16x16x32_bf16 v[14:17], v[250:253], v[234:237], v[14:17]
	ds_read_b128 v[234:237], v93 offset:8192
	s_mov_b32 s47, s42
	s_mov_b32 s42, s43
	s_mov_b32 s43, s44
	s_mov_b32 s44, s47
	s_waitcnt lgkmcnt(0)
	s_barrier
	v_mfma_f32_16x16x32_bf16 v[78:81], v[142:145], v[218:221], v[78:81]
	v_mfma_f32_16x16x32_bf16 v[74:77], v[146:149], v[218:221], v[74:77]
	v_mfma_f32_16x16x32_bf16 v[70:73], v[150:153], v[218:221], v[70:73]
	v_mfma_f32_16x16x32_bf16 v[66:69], v[154:157], v[218:221], v[66:69]
	v_mfma_f32_16x16x32_bf16 v[62:65], v[142:145], v[222:225], v[62:65]
	v_mfma_f32_16x16x32_bf16 v[58:61], v[146:149], v[222:225], v[58:61]
	v_mfma_f32_16x16x32_bf16 v[54:57], v[150:153], v[222:225], v[54:57]
	v_mfma_f32_16x16x32_bf16 v[50:53], v[154:157], v[222:225], v[50:53]
	v_mfma_f32_16x16x32_bf16 v[46:49], v[142:145], v[226:229], v[46:49]
	v_mfma_f32_16x16x32_bf16 v[42:45], v[146:149], v[226:229], v[42:45]
	v_mfma_f32_16x16x32_bf16 v[38:41], v[150:153], v[226:229], v[38:41]
	v_mfma_f32_16x16x32_bf16 v[34:37], v[154:157], v[226:229], v[34:37]
	v_mfma_f32_16x16x32_bf16 v[18:21], v[142:145], v[230:233], v[18:21]
	v_mfma_f32_16x16x32_bf16 v[22:25], v[146:149], v[230:233], v[22:25]
	v_mfma_f32_16x16x32_bf16 v[26:29], v[150:153], v[230:233], v[26:29]
	v_mfma_f32_16x16x32_bf16 v[30:33], v[154:157], v[230:233], v[30:33]
	v_mfma_f32_16x16x32_bf16 v[2:5], v[142:145], v[234:237], v[2:5]
	v_mfma_f32_16x16x32_bf16 v[6:9], v[146:149], v[234:237], v[6:9]
	v_mfma_f32_16x16x32_bf16 v[10:13], v[150:153], v[234:237], v[10:13]
	v_mfma_f32_16x16x32_bf16 v[14:17], v[154:157], v[234:237], v[14:17]

; #define LAS __attribute__((address_space(3)))
; __device__ __forceinline__ void moe_down_stream(PG8_LAS unsigned char* lds, int e, int cb0, int slot0, int nv, const bf16_t* HIDp, const float* Wd, bf16_t* Y, const float* slot_w, const int* slot_dst) {
;     ...
;     const int tid = threadIdx.x, wid = __builtin_amdgcn_readfirstlane(tid >> 6), lane = tid & 63, wr = wid >> 1, wc = wid & 1, fr = lane & 15, fq = lane >> 4;
;     unsigned aoff[5];
; #pragma unroll
;     for (int i = 0; i < 5; ++i) { const int R = 8 * (wid + 8 * i) + (lane >> 3), C = 8 * ((lane & 7) ^ ((R >> 1) & 7)); const int w4 = R / DRW; int r = 4 * (R - DRW * w4) + w4; r = r < nv ? r : r % nv;
;         aoff[i] = ((unsigned)(slot0 + r) * (unsigned)K + (unsigned)C) * 2u; }
;     const int c0_ = 2 * lane, R0 = 64 * (c0_ >> 6) + 16 * (2 * ((c0_ >> 5) & 1) + ((c0_ >> 2) & 1)) + 4 * ((c0_ >> 3) & 3) + (c0_ & 3);
;     const char* Bb = (const char*)(Wd + (size_t)e * K * 4096 + 128 * cb0 + 2 * lane) + (size_t)(8 * wid) * RB;
;     const unsigned bw0 = (unsigned)(R0 * 128 + ((wid ^ ((R0 >> 1) & 7)) * 16)), bw1 = bw0 + 128u;
;     const int nvw = (nv - wr + 3) >> 2, mcnt = nvw <= 0 ? 0 : (((nvw + 15) >> 4) > DNM ? DNM : ((nvw + 15) >> 4));
;     unsigned amask = 0u;
; #pragma unroll
;     for (int i = 0; i < 5; ++i) { const int grp = 4 * i + (wid >> 1), w4 = grp / DNM, mf = grp % DNM, nv4 = (nv - w4 + 3) >> 2, mc4 = nv4 <= 0 ? 0 : ((nv4 + 15) >> 4); if (mf < mc4) amask |= 1u << i; }
;     LAS int* ldst = (LAS int*)(lds + MD_TAB_OFF); LAS float* lw = (LAS float*)(ldst + DR);
;     PG8_LAS unsigned char* stg = lds + MD_STG_OFF + wid * 2048;
;     __syncthreads();
;     for (int r = tid; r < DR; r += 512) { const bool ok = r < nv; ldst[r] = ok ? slot_dst[slot0 + r] : -1; lw[r] = ok ? slot_w[slot0 + r] : 0.f; }
;     asm volatile("s_waitcnt vmcnt(0)" ::: "memory");
;     ...
;     f32x4 acc[DNM][4];
; #pragma unroll
;     for (int m = 0; m < DNM; ++m)
; #pragma unroll
;         for (int n = 0; n < 4; ++n) acc[m][n] = (f32x4){0.f, 0.f, 0.f, 0.f};
;     f32x2 s0[8], s1[8];
;     MD_GLDS_A(0, 0); MD_B_ISSUE(s0, 0); MD_B_ISSUE(s1, 1);
;     MD_B_WAIT(s0, 8); MD_B_WRITE(s0, 0); __builtin_amdgcn_sched_barrier(0); MD_B_ISSUE(s0, 2);
;     asm volatile("s_waitcnt vmcnt(16)" ::: "memory");
;     asm volatile("s_waitcnt lgkmcnt(0)" ::: "memory"); __builtin_amdgcn_s_barrier(); asm volatile("" ::: "memory");
.Lmd_used_4:
	v_bfe_u32 v180, v131, 1, 3
	v_xor_b32_e32 v180, v171, v180
	v_lshlrev_b32_e32 v180, 4, v180
	v_lshl_add_u32 v180, v170, 7, v180
	s_mul_i32 s57, s67, 0x2800
	v_add_u32_e32 v135, s57, v180
	v_xor_b32_e32 v137, 64, v135
	s_lshl_b32 s57, s10, 13
	s_add_i32 s57, s57, 0x1e000
	v_add_u32_e32 v139, s57, v180
	v_xor_b32_e32 v141, 64, v139
	v_lshrrev_b32_e32 v164, 4, v131
	v_lshlrev_b32_e32 v95, 5, v164
	v_bfe_u32 v164, v131, 1, 1
	v_lshl_or_b32 v95, v164, 4, v95
	v_bfe_u32 v164, v131, 2, 2
	v_lshl_or_b32 v95, v164, 2, v95
	v_and_b32_e32 v165, 1, v131
	v_lshl_or_b32 v95, v165, 1, v95
	v_lshl_or_b32 v164, v164, 1, v165
	v_xor_b32_e32 v164, s66, v164
	v_lshlrev_b32_e32 v95, 7, v95
	v_lshl_or_b32 v95, v164, 4, v95
	v_add_u32_e32 v95, 0x1e000, v95
	s_lshl_b32 s57, s67, 2
	v_lshl_add_u32 v82, v170, 4, s57
	v_add_u32_e32 v82, 0x27340, v82
	v_lshl_add_u32 v83, v130, 4, s57
	v_add_u32_e32 v83, 0x26e40, v83
	v_and_b32_e32 v164, 7, v170
	v_xor_b32_e32 v165, v171, v164
	v_lshlrev_b32_e32 v165, 4, v165
	v_lshl_or_b32 v84, v164, 7, v165
	v_lshrrev_b32_e32 v164, 3, v170
	v_lshl_or_b32 v84, v164, 13, v84
	v_and_b32_e32 v164, 7, v131
	v_xor_b32_e32 v165, v130, v164
	v_and_b32_e32 v165, 7, v165
	v_lshlrev_b32_e32 v165, 4, v165
	v_lshl_or_b32 v85, v130, 7, v165
	s_lshl_b32 s57, s14, 8
	s_lshl_b32 s58, s10, 7
	s_add_i32 s57, s57, s58
	s_add_u32 s58, s96, s57
	s_addc_u32 s59, s97, 0
	v_lshlrev_b32_e32 v164, 4, v164
	v_mov_b32_e32 v165, 0
	v_lshl_add_u64 v[86:87], v[164:165], 0, s[58:59]
	v_readlane_b32 s58, v254, 25
	v_readlane_b32 s59, v254, 26
	s_lshl_b64 s[60:61], s[6:7], 23
	s_add_u32 s58, s58, s60
	s_addc_u32 s59, s59, s61
	s_lshl_b32 s60, s14, 9
	s_add_u32 s58, s58, s60
	s_addc_u32 s59, s59, 0
	s_lshl_b32 s60, s66, 17
	s_add_u32 s58, s58, s60
	s_addc_u32 s59, s59, 0
	v_lshlrev_b32_e32 v164, 3, v131
	v_mov_b32_e32 v165, 0
	v_lshl_add_u64 v[132:133], v[164:165], 0, s[58:59]
	s_mov_b64 s[24:25], 0x4000
	s_mov_b64 s[26:27], 0x8000
	s_mov_b64 s[28:29], 0xc000
	s_mov_b64 s[36:37], 0x10000
	s_mov_b64 s[38:39], 0x14000
	s_mov_b64 s[40:41], 0x18000
	s_mov_b64 s[42:43], 0x1c000
	s_mov_b32 s34, 0xff900800
	s_mov_b32 s35, 0x100000
	s_mov_b32 s53, 0xfffffc80
	s_mov_b32 s32, 0x80
	v_readlane_b32 s58, v254, 31
	v_readlane_b32 s59, v254, 32
	s_add_u32 s58, s58, 0x4b000000
	s_addc_u32 s59, s59, 0
	v_lshlrev_b32_e32 v164, 4, v131
	v_mov_b32_e32 v165, 0
	v_lshl_add_u64 v[168:169], v[164:165], 0, s[58:59]
	s_mov_b64 s[30:31], s[16:17]
	s_mov_b32 s46, 0
	s_mov_b32 s47, 0xa000
	s_mov_b32 s48, 0x14000
	s_mov_b32 s51, 4
	s_mov_b32 s50, 0
	s_mov_b32 s52, 1
	s_add_i32 m0, s74, 0x0
	s_nop 0
	global_load_lds_dwordx4 v88, s[30:31]
	s_add_i32 m0, s74, 0x2000
	s_nop 0
	global_load_lds_dwordx4 v90, s[30:31]
	s_add_i32 m0, s74, 0x4000
	s_nop 0
	global_load_lds_dwordx4 v92, s[30:31]
	s_add_i32 m0, s74, 0x6000
	s_nop 0
	global_load_lds_dwordx4 v94, s[30:31]
	s_add_i32 m0, s74, 0x8000
	s_nop 0
	global_load_lds_dwordx4 v96, s[30:31]
	s_add_u32 s30, s30, 0x80
	s_addc_u32 s31, s31, 0
	s_add_i32 m0, s74, 0xa000
	s_nop 0
	global_load_lds_dwordx4 v88, s[30:31]
	s_add_i32 m0, s74, 0xc000
	s_nop 0
	global_load_lds_dwordx4 v90, s[30:31]
	s_add_i32 m0, s74, 0xe000
	s_nop 0
	global_load_lds_dwordx4 v92, s[30:31]
	s_add_i32 m0, s74, 0x10000
	s_nop 0
	global_load_lds_dwordx4 v94, s[30:31]
	s_add_i32 m0, s74, 0x12000
	s_nop 0
	global_load_lds_dwordx4 v96, s[30:31]
	s_mov_b32 s44, 0x100000
	s_mov_b32 s45, 0
	global_load_dwordx2 v[98:99], v[132:133], off
	v_lshl_add_u64 v[180:181], v[132:133], 0, s[24:25]
	global_load_dwordx2 v[100:101], v[180:181], off
	v_lshl_add_u64 v[180:181], v[132:133], 0, s[26:27]
	global_load_dwordx2 v[102:103], v[180:181], off
	v_lshl_add_u64 v[180:181], v[132:133], 0, s[28:29]
	global_load_dwordx2 v[104:105], v[180:181], off
	v_lshl_add_u64 v[180:181], v[132:133], 0, s[36:37]
	global_load_dwordx2 v[106:107], v[180:181], off
	v_lshl_add_u64 v[180:181], v[132:133], 0, s[38:39]
	global_load_dwordx2 v[108:109], v[180:181], off
	v_lshl_add_u64 v[180:181], v[132:133], 0, s[40:41]
	global_load_dwordx2 v[110:111], v[180:181], off
	v_lshl_add_u64 v[180:181], v[132:133], 0, s[42:43]
	global_load_dwordx2 v[112:113], v[180:181], off
	v_lshl_add_u64 v[132:133], v[132:133], 0, s[44:45]
	global_load_dwordx2 v[114:115], v[132:133], off
	v_lshl_add_u64 v[180:181], v[132:133], 0, s[24:25]
	global_load_dwordx2 v[116:117], v[180:181], off
	v_lshl_add_u64 v[180:181], v[132:133], 0, s[26:27]
	global_load_dwordx2 v[118:119], v[180:181], off
	v_lshl_add_u64 v[180:181], v[132:133], 0, s[28:29]
	global_load_dwordx2 v[120:121], v[180:181], off
	v_lshl_add_u64 v[180:181], v[132:133], 0, s[36:37]
	global_load_dwordx2 v[122:123], v[180:181], off
	v_lshl_add_u64 v[180:181], v[132:133], 0, s[38:39]
	global_load_dwordx2 v[124:125], v[180:181], off
	v_lshl_add_u64 v[180:181], v[132:133], 0, s[40:41]
	global_load_dwordx2 v[126:127], v[180:181], off
	v_lshl_add_u64 v[180:181], v[132:133], 0, s[42:43]
	global_load_dwordx2 v[128:129], v[180:181], off
	v_lshl_add_u64 v[132:133], v[132:133], 0, s[44:45]
	global_load_dwordx2 v[186:187], v[132:133], off
	v_lshl_add_u64 v[180:181], v[132:133], 0, s[24:25]
	global_load_dwordx2 v[188:189], v[180:181], off
	v_lshl_add_u64 v[180:181], v[132:133], 0, s[26:27]
	global_load_dwordx2 v[190:191], v[180:181], off
	v_lshl_add_u64 v[180:181], v[132:133], 0, s[28:29]
	global_load_dwordx2 v[192:193], v[180:181], off
	v_lshl_add_u64 v[180:181], v[132:133], 0, s[36:37]
	global_load_dwordx2 v[194:195], v[180:181], off
	v_lshl_add_u64 v[180:181], v[132:133], 0, s[38:39]
	global_load_dwordx2 v[196:197], v[180:181], off
	v_lshl_add_u64 v[180:181], v[132:133], 0, s[40:41]
; #define MD_GLDS_A(buf, tau) do { _Pragma("unroll") for (int i = 0; i < 5; ++i) if (amask & (1u << i)) \
;         __builtin_amdgcn_global_load_lds((const unsigned*)((const char*)HIDp + aoff[i] + (size_t)((tau) & 7) * 128), (PG8_LAS unsigned*)(MD_SA(buf) + wid * 1024 + i * 8192), 16, 0, 0); } while (0)
; #define MD_B_ISSUE(sb, tau) do { const char* kb_ = Bb + (size_t)((tau) >> 3) * 512 + (size_t)((tau) & 7) * (64 * (size_t)RB); _Pragma("unroll") for (int j = 0; j < 8; ++j) { const char* p_ = kb_ + (size_t)j * RB; \
;         asm volatile("global_load_dwordx2 %0, %1, off" : "=&v"(sb[j]) : "v"(p_) : "memory"); } } while (0)
; #define MD_B_WAIT(sb, N) asm volatile("s_waitcnt vmcnt(%8)" : "+v"(sb[0]), "+v"(sb[1]), "+v"(sb[2]), "+v"(sb[3]), "+v"(sb[4]), "+v"(sb[5]), "+v"(sb[6]), "+v"(sb[7]) : "n"(N) : "memory")
; __device__ __forceinline__ void moe_down_stream(PG8_LAS unsigned char* lds, int e, int cb0, int slot0, int nv, const bf16_t* HIDp, const float* Wd, bf16_t* Y, const float* slot_w, const int* slot_dst) {
;     ...
;     f32x4 acc[DNM][4];
; #pragma unroll
;     for (int m = 0; m < DNM; ++m)
; #pragma unroll
;         for (int n = 0; n < 4; ++n) acc[m][n] = (f32x4){0.f, 0.f, 0.f, 0.f};
;     f32x2 s0[8], s1[8];
;     MD_GLDS_A(0, 0); MD_B_ISSUE(s0, 0); MD_B_ISSUE(s1, 1);
;     MD_B_WAIT(s0, 8); MD_B_WRITE(s0, 0); __builtin_amdgcn_sched_barrier(0); MD_B_ISSUE(s0, 2);
;     asm volatile("s_waitcnt vmcnt(16)" ::: "memory");
;     asm volatile("s_waitcnt lgkmcnt(0)" ::: "memory"); __builtin_amdgcn_s_barrier(); asm volatile("" ::: "memory");
; #pragma unroll 1
;     for (int t = 0; t < NT; t += 2) {
;         if (t + 2 < NT) MD_B_WAIT(s1, 8); else MD_B_WAIT(s1, 0);
;         MD_B_WRITE(s1, 1); __builtin_amdgcn_sched_barrier(0); MD_GLDS_A(1, t + 1); __builtin_amdgcn_sched_barrier(0);
	global_load_dwordx2 v[198:199], v[180:181], off
	v_lshl_add_u64 v[180:181], v[132:133], 0, s[42:43]
	global_load_dwordx2 v[200:201], v[180:181], off
	v_lshl_add_u64 v[132:133], v[132:133], 0, s[44:45]
	global_load_dwordx2 v[202:203], v[132:133], off
	v_lshl_add_u64 v[180:181], v[132:133], 0, s[24:25]
	global_load_dwordx2 v[204:205], v[180:181], off
	v_lshl_add_u64 v[180:181], v[132:133], 0, s[26:27]
	global_load_dwordx2 v[206:207], v[180:181], off
	v_lshl_add_u64 v[180:181], v[132:133], 0, s[28:29]
	global_load_dwordx2 v[208:209], v[180:181], off
	v_lshl_add_u64 v[180:181], v[132:133], 0, s[36:37]
	global_load_dwordx2 v[210:211], v[180:181], off
	v_lshl_add_u64 v[180:181], v[132:133], 0, s[38:39]
	global_load_dwordx2 v[212:213], v[180:181], off
	v_lshl_add_u64 v[180:181], v[132:133], 0, s[40:41]
	global_load_dwordx2 v[214:215], v[180:181], off
	v_lshl_add_u64 v[180:181], v[132:133], 0, s[42:43]
	global_load_dwordx2 v[216:217], v[180:181], off
	v_mov_b32_e32 v78, 0
	v_mov_b32_e32 v79, 0
	v_mov_b32_e32 v80, 0
	v_mov_b32_e32 v81, 0
	v_mov_b32_e32 v74, 0
	v_mov_b32_e32 v75, 0
	v_mov_b32_e32 v76, 0
	v_mov_b32_e32 v77, 0
	v_mov_b32_e32 v70, 0
	v_mov_b32_e32 v71, 0
	v_mov_b32_e32 v72, 0
	v_mov_b32_e32 v73, 0
	v_mov_b32_e32 v66, 0
	v_mov_b32_e32 v67, 0
	v_mov_b32_e32 v68, 0
	v_mov_b32_e32 v69, 0
	v_mov_b32_e32 v62, 0
	v_mov_b32_e32 v63, 0
	v_mov_b32_e32 v64, 0
	v_mov_b32_e32 v65, 0
	v_mov_b32_e32 v58, 0
	v_mov_b32_e32 v59, 0
	v_mov_b32_e32 v60, 0
	v_mov_b32_e32 v61, 0
	v_mov_b32_e32 v54, 0
	v_mov_b32_e32 v55, 0
	v_mov_b32_e32 v56, 0
	v_mov_b32_e32 v57, 0
	v_mov_b32_e32 v50, 0
	v_mov_b32_e32 v51, 0
	v_mov_b32_e32 v52, 0
	v_mov_b32_e32 v53, 0
	v_mov_b32_e32 v46, 0
	v_mov_b32_e32 v47, 0
	v_mov_b32_e32 v48, 0
	v_mov_b32_e32 v49, 0
	v_mov_b32_e32 v42, 0
	v_mov_b32_e32 v43, 0
	v_mov_b32_e32 v44, 0
	v_mov_b32_e32 v45, 0
	v_mov_b32_e32 v38, 0
	v_mov_b32_e32 v39, 0
	v_mov_b32_e32 v40, 0
	v_mov_b32_e32 v41, 0
	v_mov_b32_e32 v34, 0
	v_mov_b32_e32 v35, 0
	v_mov_b32_e32 v36, 0
	v_mov_b32_e32 v37, 0
	v_mov_b32_e32 v18, 0
	v_mov_b32_e32 v19, 0
	v_mov_b32_e32 v20, 0
	v_mov_b32_e32 v21, 0
	v_mov_b32_e32 v22, 0
	v_mov_b32_e32 v23, 0
	v_mov_b32_e32 v24, 0
	v_mov_b32_e32 v25, 0
	v_mov_b32_e32 v26, 0
	v_mov_b32_e32 v27, 0
	v_mov_b32_e32 v28, 0
	v_mov_b32_e32 v29, 0
	v_mov_b32_e32 v30, 0
	v_mov_b32_e32 v31, 0
	v_mov_b32_e32 v32, 0
	v_mov_b32_e32 v33, 0
	v_mov_b32_e32 v2, 0
	v_mov_b32_e32 v3, 0
	v_mov_b32_e32 v4, 0
	v_mov_b32_e32 v5, 0
	v_mov_b32_e32 v6, 0
	v_mov_b32_e32 v7, 0
	v_mov_b32_e32 v8, 0
	v_mov_b32_e32 v9, 0
	v_mov_b32_e32 v10, 0
	v_mov_b32_e32 v11, 0
	v_mov_b32_e32 v12, 0
	v_mov_b32_e32 v13, 0
	v_mov_b32_e32 v14, 0
	v_mov_b32_e32 v15, 0
	v_mov_b32_e32 v16, 0
	v_mov_b32_e32 v17, 0
	s_waitcnt vmcnt(24)
	v_cvt_pk_bf16_f32 v172, v98, v100
	v_cvt_pk_bf16_f32 v173, v102, v104
	v_cvt_pk_bf16_f32 v174, v106, v108
	v_cvt_pk_bf16_f32 v175, v110, v112
	v_cvt_pk_bf16_f32 v176, v99, v101
	v_cvt_pk_bf16_f32 v177, v103, v105
	v_cvt_pk_bf16_f32 v178, v107, v109
	v_cvt_pk_bf16_f32 v179, v111, v113
	ds_write_b128 v95, v[172:175] offset:0
	ds_write_b128 v95, v[176:179] offset:128
	v_lshl_add_u64 v[132:133], v[132:133], 0, s[44:45]
	global_load_dwordx2 v[98:99], v[132:133], off
	v_lshl_add_u64 v[180:181], v[132:133], 0, s[24:25]
	global_load_dwordx2 v[100:101], v[180:181], off
	v_lshl_add_u64 v[180:181], v[132:133], 0, s[26:27]
	global_load_dwordx2 v[102:103], v[180:181], off
	v_lshl_add_u64 v[180:181], v[132:133], 0, s[28:29]
	global_load_dwordx2 v[104:105], v[180:181], off
	v_lshl_add_u64 v[180:181], v[132:133], 0, s[36:37]
	global_load_dwordx2 v[106:107], v[180:181], off
	v_lshl_add_u64 v[180:181], v[132:133], 0, s[38:39]
	global_load_dwordx2 v[108:109], v[180:181], off
	v_lshl_add_u64 v[180:181], v[132:133], 0, s[40:41]
	global_load_dwordx2 v[110:111], v[180:181], off
	v_lshl_add_u64 v[180:181], v[132:133], 0, s[42:43]
	global_load_dwordx2 v[112:113], v[180:181], off
	s_waitcnt lgkmcnt(0)
	s_barrier
	s_cmp_gt_u32 s66, 3
	s_cbranch_scc1 .Lmd_grpY
	s_waitcnt vmcnt(24)
	v_cvt_pk_bf16_f32 v172, v114, v116
	v_cvt_pk_bf16_f32 v173, v118, v120
	v_cvt_pk_bf16_f32 v174, v122, v124
	v_cvt_pk_bf16_f32 v175, v126, v128
	v_cvt_pk_bf16_f32 v176, v115, v117
	v_cvt_pk_bf16_f32 v177, v119, v121
	v_cvt_pk_bf16_f32 v178, v123, v125
	v_cvt_pk_bf16_f32 v179, v127, v129
	ds_write_b128 v95, v[172:175] offset:19456
	ds_write_b128 v95, v[176:179] offset:19584
	v_add_u32_e32 v91, s46, v135
	v_add_u32_e32 v93, s46, v137
	ds_read_b128 v[238:241], v139 offset:0
	ds_read_b128 v[242:245], v139 offset:2048
	ds_read_b128 v[246:249], v139 offset:4096
	ds_read_b128 v[250:253], v139 offset:6144
	ds_read_b128 v[218:221], v91 offset:0
	ds_read_b128 v[222:225], v91 offset:2048
	ds_read_b128 v[226:229], v91 offset:4096
	ds_read_b128 v[230:233], v91 offset:6144
	ds_read_b128 v[234:237], v91 offset:8192
	s_add_i32 s49, s48, s74
	s_add_i32 s52, s52, 1
	s_and_b32 s54, s52, 7
	s_cmp_eq_u32 s54, 0
	s_cselect_b32 s54, s53, s32
	s_cselect_b32 s55, -1, 0
	s_add_u32 s30, s30, s54
	s_addc_u32 s31, s31, s55
	s_waitcnt lgkmcnt(0)
; #define MD_GLDS_A(buf, tau) do { _Pragma("unroll") for (int i = 0; i < 5; ++i) if (amask & (1u << i)) \
;         __builtin_amdgcn_global_load_lds((const unsigned*)((const char*)HIDp + aoff[i] + (size_t)((tau) & 7) * 128), (PG8_LAS unsigned*)(MD_SA(buf) + wid * 1024 + i * 8192), 16, 0, 0); } while (0)
; #define MD_B_ISSUE(sb, tau) do { const char* kb_ = Bb + (size_t)((tau) >> 3) * 512 + (size_t)((tau) & 7) * (64 * (size_t)RB); _Pragma("unroll") for (int j = 0; j < 8; ++j) { const char* p_ = kb_ + (size_t)j * RB; \
;         asm volatile("global_load_dwordx2 %0, %1, off" : "=&v"(sb[j]) : "v"(p_) : "memory"); } } while (0)
; #define MD_B_WAIT(sb, N) asm volatile("s_waitcnt vmcnt(%8)" : "+v"(sb[0]), "+v"(sb[1]), "+v"(sb[2]), "+v"(sb[3]), "+v"(sb[4]), "+v"(sb[5]), "+v"(sb[6]), "+v"(sb[7]) : "n"(N) : "memory")
; __device__ __forceinline__ void moe_down_stream(PG8_LAS unsigned char* lds, int e, int cb0, int slot0, int nv, const bf16_t* HIDp, const float* Wd, bf16_t* Y, const float* slot_w, const int* slot_dst) {
;     ...
;     f32x4 acc[DNM][4];
; #pragma unroll
;     for (int m = 0; m < DNM; ++m)
; #pragma unroll
;         for (int n = 0; n < 4; ++n) acc[m][n] = (f32x4){0.f, 0.f, 0.f, 0.f};
;     f32x2 s0[8], s1[8];
;     MD_GLDS_A(0, 0); MD_B_ISSUE(s0, 0); MD_B_ISSUE(s1, 1);
;     MD_B_WAIT(s0, 8); MD_B_WRITE(s0, 0); __builtin_amdgcn_sched_barrier(0); MD_B_ISSUE(s0, 2);
;     asm volatile("s_waitcnt vmcnt(16)" ::: "memory");
;     asm volatile("s_waitcnt lgkmcnt(0)" ::: "memory"); __builtin_amdgcn_s_barrier(); asm volatile("" ::: "memory");
; #pragma unroll 1
;     for (int t = 0; t < NT; t += 2) {
;         if (t + 2 < NT) MD_B_WAIT(s1, 8); else MD_B_WAIT(s1, 0);
;         MD_B_WRITE(s1, 1); __builtin_amdgcn_sched_barrier(0); MD_GLDS_A(1, t + 1); __builtin_amdgcn_sched_barrier(0);
;         if (t + 3 < NT) MD_B_ISSUE(s1, t + 3);
;         MD_COMPUTE(0);
;         MD_END(t + 3 >= NT);
;         if (t + 2 < NT) { MD_B_WAIT(s0, 8); MD_B_WRITE(s0, 0); __builtin_amdgcn_sched_barrier(0); MD_GLDS_A(0, t + 2); __builtin_amdgcn_sched_barrier(0); }
;         if (t + 4 < NT) MD_B_ISSUE(s0, t + 4);
;         MD_COMPUTE(1);
;         MD_END(t + 4 >= NT);
	v_mfma_f32_16x16x32_bf16 v[78:81], v[238:241], v[218:221], v[78:81]
	v_mfma_f32_16x16x32_bf16 v[74:77], v[242:245], v[218:221], v[74:77]
	v_mfma_f32_16x16x32_bf16 v[70:73], v[246:249], v[218:221], v[70:73]
	v_mfma_f32_16x16x32_bf16 v[66:69], v[250:253], v[218:221], v[66:69]
	ds_read_b128 v[218:221], v93 offset:0
	ds_read_b128 v[142:145], v141 offset:0
	s_mov_b32 m0, s49
	s_nop 0
	global_load_lds_dwordx4 v88, s[30:31]
	v_mfma_f32_16x16x32_bf16 v[62:65], v[238:241], v[222:225], v[62:65]
	v_mfma_f32_16x16x32_bf16 v[58:61], v[242:245], v[222:225], v[58:61]
	v_mfma_f32_16x16x32_bf16 v[54:57], v[246:249], v[222:225], v[54:57]
	v_mfma_f32_16x16x32_bf16 v[50:53], v[250:253], v[222:225], v[50:53]
	ds_read_b128 v[222:225], v93 offset:2048
	ds_read_b128 v[146:149], v141 offset:2048
	s_add_i32 m0, s49, 0x2000
	s_nop 0
	global_load_lds_dwordx4 v90, s[30:31]
	v_mfma_f32_16x16x32_bf16 v[46:49], v[238:241], v[226:229], v[46:49]
	v_mfma_f32_16x16x32_bf16 v[42:45], v[242:245], v[226:229], v[42:45]
	v_mfma_f32_16x16x32_bf16 v[38:41], v[246:249], v[226:229], v[38:41]
	v_mfma_f32_16x16x32_bf16 v[34:37], v[250:253], v[226:229], v[34:37]
	ds_read_b128 v[226:229], v93 offset:4096
	ds_read_b128 v[156:159], v141 offset:4096
	s_add_i32 m0, s49, 0x4000
	s_nop 0
	global_load_lds_dwordx4 v92, s[30:31]
	v_mfma_f32_16x16x32_bf16 v[18:21], v[238:241], v[230:233], v[18:21]
	v_mfma_f32_16x16x32_bf16 v[22:25], v[242:245], v[230:233], v[22:25]
	v_mfma_f32_16x16x32_bf16 v[26:29], v[246:249], v[230:233], v[26:29]
	v_mfma_f32_16x16x32_bf16 v[30:33], v[250:253], v[230:233], v[30:33]
	ds_read_b128 v[230:233], v93 offset:6144
	ds_read_b128 v[160:163], v141 offset:6144
	s_add_i32 m0, s49, 0x6000
	s_nop 0
	global_load_lds_dwordx4 v94, s[30:31]
	v_mfma_f32_16x16x32_bf16 v[2:5], v[238:241], v[234:237], v[2:5]
	v_mfma_f32_16x16x32_bf16 v[6:9], v[242:245], v[234:237], v[6:9]
	v_mfma_f32_16x16x32_bf16 v[10:13], v[246:249], v[234:237], v[10:13]
	v_mfma_f32_16x16x32_bf16 v[14:17], v[250:253], v[234:237], v[14:17]
	ds_read_b128 v[234:237], v93 offset:8192
	s_add_i32 m0, s49, 0x8000
	s_nop 0
	global_load_lds_dwordx4 v96, s[30:31]
	s_waitcnt lgkmcnt(0)
	v_mfma_f32_16x16x32_bf16 v[78:81], v[142:145], v[218:221], v[78:81]
	v_mfma_f32_16x16x32_bf16 v[74:77], v[146:149], v[218:221], v[74:77]
	v_mfma_f32_16x16x32_bf16 v[70:73], v[156:159], v[218:221], v[70:73]
	v_mfma_f32_16x16x32_bf16 v[66:69], v[160:163], v[218:221], v[66:69]
	s_add_i32 s51, s51, 1
	s_and_b32 s54, s51, 7
	s_cmp_eq_u32 s54, 0
	s_cselect_b32 s44, s34, s35
	s_cselect_b32 s45, -1, 0
	v_lshl_add_u64 v[132:133], v[132:133], 0, s[44:45]
	global_load_dwordx2 v[114:115], v[132:133], off
	v_lshl_add_u64 v[180:181], v[132:133], 0, s[24:25]
	global_load_dwordx2 v[116:117], v[180:181], off
	v_mfma_f32_16x16x32_bf16 v[62:65], v[142:145], v[222:225], v[62:65]
	v_mfma_f32_16x16x32_bf16 v[58:61], v[146:149], v[222:225], v[58:61]
	v_mfma_f32_16x16x32_bf16 v[54:57], v[156:159], v[222:225], v[54:57]
	v_mfma_f32_16x16x32_bf16 v[50:53], v[160:163], v[222:225], v[50:53]
	v_lshl_add_u64 v[180:181], v[132:133], 0, s[26:27]
	global_load_dwordx2 v[118:119], v[180:181], off
	v_lshl_add_u64 v[180:181], v[132:133], 0, s[28:29]
	global_load_dwordx2 v[120:121], v[180:181], off
	v_mfma_f32_16x16x32_bf16 v[46:49], v[142:145], v[226:229], v[46:49]
	v_mfma_f32_16x16x32_bf16 v[42:45], v[146:149], v[226:229], v[42:45]
	v_mfma_f32_16x16x32_bf16 v[38:41], v[156:159], v[226:229], v[38:41]
	v_mfma_f32_16x16x32_bf16 v[34:37], v[160:163], v[226:229], v[34:37]
	v_lshl_add_u64 v[180:181], v[132:133], 0, s[36:37]
	global_load_dwordx2 v[122:123], v[180:181], off
	v_lshl_add_u64 v[180:181], v[132:133], 0, s[38:39]
	global_load_dwordx2 v[124:125], v[180:181], off
	v_mfma_f32_16x16x32_bf16 v[18:21], v[142:145], v[230:233], v[18:21]
	v_mfma_f32_16x16x32_bf16 v[22:25], v[146:149], v[230:233], v[22:25]
	v_mfma_f32_16x16x32_bf16 v[26:29], v[156:159], v[230:233], v[26:29]
	v_mfma_f32_16x16x32_bf16 v[30:33], v[160:163], v[230:233], v[30:33]
	v_lshl_add_u64 v[180:181], v[132:133], 0, s[40:41]
	global_load_dwordx2 v[126:127], v[180:181], off
	v_lshl_add_u64 v[180:181], v[132:133], 0, s[42:43]
	global_load_dwordx2 v[128:129], v[180:181], off
	v_mfma_f32_16x16x32_bf16 v[2:5], v[142:145], v[234:237], v[2:5]
	v_mfma_f32_16x16x32_bf16 v[6:9], v[146:149], v[234:237], v[6:9]
	v_mfma_f32_16x16x32_bf16 v[10:13], v[156:159], v[234:237], v[10:13]
	v_mfma_f32_16x16x32_bf16 v[14:17], v[160:163], v[234:237], v[14:17]
	s_mov_b32 s49, s46
	s_mov_b32 s46, s47
	s_mov_b32 s47, s48
	s_mov_b32 s48, s49
	s_add_i32 s50, s50, 1
	s_waitcnt lgkmcnt(0)
	s_barrier
; #define MD_GLDS_A(buf, tau) do { _Pragma("unroll") for (int i = 0; i < 5; ++i) if (amask & (1u << i)) \
;         __builtin_amdgcn_global_load_lds((const unsigned*)((const char*)HIDp + aoff[i] + (size_t)((tau) & 7) * 128), (PG8_LAS unsigned*)(MD_SA(buf) + wid * 1024 + i * 8192), 16, 0, 0); } while (0)
; #define MD_B_ISSUE(sb, tau) do { const char* kb_ = Bb + (size_t)((tau) >> 3) * 512 + (size_t)((tau) & 7) * (64 * (size_t)RB); _Pragma("unroll") for (int j = 0; j < 8; ++j) { const char* p_ = kb_ + (size_t)j * RB; \
;         asm volatile("global_load_dwordx2 %0, %1, off" : "=&v"(sb[j]) : "v"(p_) : "memory"); } } while (0)
; #define MD_B_WAIT(sb, N) asm volatile("s_waitcnt vmcnt(%8)" : "+v"(sb[0]), "+v"(sb[1]), "+v"(sb[2]), "+v"(sb[3]), "+v"(sb[4]), "+v"(sb[5]), "+v"(sb[6]), "+v"(sb[7]) : "n"(N) : "memory")
; __device__ __forceinline__ void moe_down_stream(PG8_LAS unsigned char* lds, int e, int cb0, int slot0, int nv, const bf16_t* HIDp, const float* Wd, bf16_t* Y, const float* slot_w, const int* slot_dst) {
;     ...
;     f32x4 acc[DNM][4];
; #pragma unroll
;     for (int m = 0; m < DNM; ++m)
; #pragma unroll
;         for (int n = 0; n < 4; ++n) acc[m][n] = (f32x4){0.f, 0.f, 0.f, 0.f};
;     f32x2 s0[8], s1[8];
;     MD_GLDS_A(0, 0); MD_B_ISSUE(s0, 0); MD_B_ISSUE(s1, 1);
;     MD_B_WAIT(s0, 8); MD_B_WRITE(s0, 0); __builtin_amdgcn_sched_barrier(0); MD_B_ISSUE(s0, 2);
;     asm volatile("s_waitcnt vmcnt(16)" ::: "memory");
;     asm volatile("s_waitcnt lgkmcnt(0)" ::: "memory"); __builtin_amdgcn_s_barrier(); asm volatile("" ::: "memory");
; #pragma unroll 1
;     for (int t = 0; t < NT; t += 2) {
;         if (t + 2 < NT) MD_B_WAIT(s1, 8); else MD_B_WAIT(s1, 0);
;         MD_B_WRITE(s1, 1); __builtin_amdgcn_sched_barrier(0); MD_GLDS_A(1, t + 1); __builtin_amdgcn_sched_barrier(0);
;         if (t + 3 < NT) MD_B_ISSUE(s1, t + 3);
;         MD_COMPUTE(0);
;         MD_END(t + 3 >= NT);
;         if (t + 2 < NT) { MD_B_WAIT(s0, 8); MD_B_WRITE(s0, 0); __builtin_amdgcn_sched_barrier(0); MD_GLDS_A(0, t + 2); __builtin_amdgcn_sched_barrier(0); }
;         if (t + 4 < NT) MD_B_ISSUE(s0, t + 4);
;         MD_COMPUTE(1);
;         MD_END(t + 4 >= NT);
	s_waitcnt vmcnt(29)
	v_cvt_pk_bf16_f32 v172, v186, v188
	v_cvt_pk_bf16_f32 v173, v190, v192
	v_cvt_pk_bf16_f32 v174, v194, v196
	v_cvt_pk_bf16_f32 v175, v198, v200
	v_cvt_pk_bf16_f32 v176, v187, v189
	v_cvt_pk_bf16_f32 v177, v191, v193
	v_cvt_pk_bf16_f32 v178, v195, v197
	v_cvt_pk_bf16_f32 v179, v199, v201
	ds_write_b128 v95, v[172:175] offset:0
	ds_write_b128 v95, v[176:179] offset:128
	v_add_u32_e32 v91, s46, v135
	v_add_u32_e32 v93, s46, v137
	ds_read_b128 v[238:241], v139 offset:19456
	ds_read_b128 v[242:245], v139 offset:21504
	ds_read_b128 v[246:249], v139 offset:23552
	ds_read_b128 v[250:253], v139 offset:25600
	ds_read_b128 v[218:221], v91 offset:0
	ds_read_b128 v[222:225], v91 offset:2048
	ds_read_b128 v[226:229], v91 offset:4096
	ds_read_b128 v[230:233], v91 offset:6144
	ds_read_b128 v[234:237], v91 offset:8192
	s_add_i32 s49, s48, s74
	s_add_i32 s52, s52, 1
	s_and_b32 s54, s52, 7
	s_cmp_eq_u32 s54, 0
	s_cselect_b32 s54, s53, s32
	s_cselect_b32 s55, -1, 0
	s_add_u32 s30, s30, s54
	s_addc_u32 s31, s31, s55
	s_waitcnt lgkmcnt(0)
	v_mfma_f32_16x16x32_bf16 v[78:81], v[238:241], v[218:221], v[78:81]
	v_mfma_f32_16x16x32_bf16 v[74:77], v[242:245], v[218:221], v[74:77]
	v_mfma_f32_16x16x32_bf16 v[70:73], v[246:249], v[218:221], v[70:73]
	v_mfma_f32_16x16x32_bf16 v[66:69], v[250:253], v[218:221], v[66:69]
	ds_read_b128 v[218:221], v93 offset:0
	ds_read_b128 v[142:145], v141 offset:19456
	s_mov_b32 m0, s49
	s_nop 0
	global_load_lds_dwordx4 v88, s[30:31]
	v_mfma_f32_16x16x32_bf16 v[62:65], v[238:241], v[222:225], v[62:65]
	v_mfma_f32_16x16x32_bf16 v[58:61], v[242:245], v[222:225], v[58:61]
	v_mfma_f32_16x16x32_bf16 v[54:57], v[246:249], v[222:225], v[54:57]
	v_mfma_f32_16x16x32_bf16 v[50:53], v[250:253], v[222:225], v[50:53]
	ds_read_b128 v[222:225], v93 offset:2048
	ds_read_b128 v[146:149], v141 offset:21504
	s_add_i32 m0, s49, 0x2000
	s_nop 0
	global_load_lds_dwordx4 v90, s[30:31]
	v_mfma_f32_16x16x32_bf16 v[46:49], v[238:241], v[226:229], v[46:49]
	v_mfma_f32_16x16x32_bf16 v[42:45], v[242:245], v[226:229], v[42:45]
	v_mfma_f32_16x16x32_bf16 v[38:41], v[246:249], v[226:229], v[38:41]
	v_mfma_f32_16x16x32_bf16 v[34:37], v[250:253], v[226:229], v[34:37]
	ds_read_b128 v[226:229], v93 offset:4096
	ds_read_b128 v[156:159], v141 offset:23552
	s_add_i32 m0, s49, 0x4000
	s_nop 0
	global_load_lds_dwordx4 v92, s[30:31]
	v_mfma_f32_16x16x32_bf16 v[18:21], v[238:241], v[230:233], v[18:21]
	v_mfma_f32_16x16x32_bf16 v[22:25], v[242:245], v[230:233], v[22:25]
	v_mfma_f32_16x16x32_bf16 v[26:29], v[246:249], v[230:233], v[26:29]
	v_mfma_f32_16x16x32_bf16 v[30:33], v[250:253], v[230:233], v[30:33]
	ds_read_b128 v[230:233], v93 offset:6144
	ds_read_b128 v[160:163], v141 offset:25600
	s_add_i32 m0, s49, 0x6000
	s_nop 0
	global_load_lds_dwordx4 v94, s[30:31]
	v_mfma_f32_16x16x32_bf16 v[2:5], v[238:241], v[234:237], v[2:5]
	v_mfma_f32_16x16x32_bf16 v[6:9], v[242:245], v[234:237], v[6:9]
	v_mfma_f32_16x16x32_bf16 v[10:13], v[246:249], v[234:237], v[10:13]
	v_mfma_f32_16x16x32_bf16 v[14:17], v[250:253], v[234:237], v[14:17]
	ds_read_b128 v[234:237], v93 offset:8192
	s_add_i32 m0, s49, 0x8000
	s_nop 0
	global_load_lds_dwordx4 v96, s[30:31]
	s_waitcnt lgkmcnt(0)
	v_mfma_f32_16x16x32_bf16 v[78:81], v[142:145], v[218:221], v[78:81]
	v_mfma_f32_16x16x32_bf16 v[74:77], v[146:149], v[218:221], v[74:77]
	v_mfma_f32_16x16x32_bf16 v[70:73], v[156:159], v[218:221], v[70:73]
	v_mfma_f32_16x16x32_bf16 v[66:69], v[160:163], v[218:221], v[66:69]
	s_add_i32 s51, s51, 1
	s_and_b32 s54, s51, 7
	s_cmp_eq_u32 s54, 0
	s_cselect_b32 s44, s34, s35
	s_cselect_b32 s45, -1, 0
	v_lshl_add_u64 v[132:133], v[132:133], 0, s[44:45]
	global_load_dwordx2 v[186:187], v[132:133], off
	v_lshl_add_u64 v[180:181], v[132:133], 0, s[24:25]
	global_load_dwordx2 v[188:189], v[180:181], off
	v_mfma_f32_16x16x32_bf16 v[62:65], v[142:145], v[222:225], v[62:65]
	v_mfma_f32_16x16x32_bf16 v[58:61], v[146:149], v[222:225], v[58:61]
	v_mfma_f32_16x16x32_bf16 v[54:57], v[156:159], v[222:225], v[54:57]
	v_mfma_f32_16x16x32_bf16 v[50:53], v[160:163], v[222:225], v[50:53]
	v_lshl_add_u64 v[180:181], v[132:133], 0, s[26:27]
	global_load_dwordx2 v[190:191], v[180:181], off
	v_lshl_add_u64 v[180:181], v[132:133], 0, s[28:29]
	global_load_dwordx2 v[192:193], v[180:181], off
	v_mfma_f32_16x16x32_bf16 v[46:49], v[142:145], v[226:229], v[46:49]
	v_mfma_f32_16x16x32_bf16 v[42:45], v[146:149], v[226:229], v[42:45]
	v_mfma_f32_16x16x32_bf16 v[38:41], v[156:159], v[226:229], v[38:41]
	v_mfma_f32_16x16x32_bf16 v[34:37], v[160:163], v[226:229], v[34:37]
	v_lshl_add_u64 v[180:181], v[132:133], 0, s[36:37]
	global_load_dwordx2 v[194:195], v[180:181], off
	v_lshl_add_u64 v[180:181], v[132:133], 0, s[38:39]
	global_load_dwordx2 v[196:197], v[180:181], off
	v_mfma_f32_16x16x32_bf16 v[18:21], v[142:145], v[230:233], v[18:21]
	v_mfma_f32_16x16x32_bf16 v[22:25], v[146:149], v[230:233], v[22:25]
	v_mfma_f32_16x16x32_bf16 v[26:29], v[156:159], v[230:233], v[26:29]
	v_mfma_f32_16x16x32_bf16 v[30:33], v[160:163], v[230:233], v[30:33]
	v_lshl_add_u64 v[180:181], v[132:133], 0, s[40:41]
	global_load_dwordx2 v[198:199], v[180:181], off
	v_lshl_add_u64 v[180:181], v[132:133], 0, s[42:43]
	global_load_dwordx2 v[200:201], v[180:181], off
	v_mfma_f32_16x16x32_bf16 v[2:5], v[142:145], v[234:237], v[2:5]
	v_mfma_f32_16x16x32_bf16 v[6:9], v[146:149], v[234:237], v[6:9]
	v_mfma_f32_16x16x32_bf16 v[10:13], v[156:159], v[234:237], v[10:13]
	v_mfma_f32_16x16x32_bf16 v[14:17], v[160:163], v[234:237], v[14:17]
	s_waitcnt vmcnt(21)
	s_mov_b32 s49, s46
	s_mov_b32 s46, s47
	s_mov_b32 s47, s48
	s_mov_b32 s48, s49
	s_add_i32 s50, s50, 1
	s_waitcnt lgkmcnt(0)
	s_barrier
; #define MD_GLDS_A(buf, tau) do { _Pragma("unroll") for (int i = 0; i < 5; ++i) if (amask & (1u << i)) \
;         __builtin_amdgcn_global_load_lds((const unsigned*)((const char*)HIDp + aoff[i] + (size_t)((tau) & 7) * 128), (PG8_LAS unsigned*)(MD_SA(buf) + wid * 1024 + i * 8192), 16, 0, 0); } while (0)
; #define MD_B_ISSUE(sb, tau) do { const char* kb_ = Bb + (size_t)((tau) >> 3) * 512 + (size_t)((tau) & 7) * (64 * (size_t)RB); _Pragma("unroll") for (int j = 0; j < 8; ++j) { const char* p_ = kb_ + (size_t)j * RB; \
;         asm volatile("global_load_dwordx2 %0, %1, off" : "=&v"(sb[j]) : "v"(p_) : "memory"); } } while (0)
; #define MD_B_WAIT(sb, N) asm volatile("s_waitcnt vmcnt(%8)" : "+v"(sb[0]), "+v"(sb[1]), "+v"(sb[2]), "+v"(sb[3]), "+v"(sb[4]), "+v"(sb[5]), "+v"(sb[6]), "+v"(sb[7]) : "n"(N) : "memory")
; __device__ __forceinline__ void moe_down_stream(PG8_LAS unsigned char* lds, int e, int cb0, int slot0, int nv, const bf16_t* HIDp, const float* Wd, bf16_t* Y, const float* slot_w, const int* slot_dst) {
;     ...
;     f32x4 acc[DNM][4];
; #pragma unroll
;     for (int m = 0; m < DNM; ++m)
; #pragma unroll
;         for (int n = 0; n < 4; ++n) acc[m][n] = (f32x4){0.f, 0.f, 0.f, 0.f};
;     f32x2 s0[8], s1[8];
;     MD_GLDS_A(0, 0); MD_B_ISSUE(s0, 0); MD_B_ISSUE(s1, 1);
;     MD_B_WAIT(s0, 8); MD_B_WRITE(s0, 0); __builtin_amdgcn_sched_barrier(0); MD_B_ISSUE(s0, 2);
;     asm volatile("s_waitcnt vmcnt(16)" ::: "memory");
;     asm volatile("s_waitcnt lgkmcnt(0)" ::: "memory"); __builtin_amdgcn_s_barrier(); asm volatile("" ::: "memory");
; #pragma unroll 1
;     for (int t = 0; t < NT; t += 2) {
;         if (t + 2 < NT) MD_B_WAIT(s1, 8); else MD_B_WAIT(s1, 0);
;         MD_B_WRITE(s1, 1); __builtin_amdgcn_sched_barrier(0); MD_GLDS_A(1, t + 1); __builtin_amdgcn_sched_barrier(0);
;         if (t + 3 < NT) MD_B_ISSUE(s1, t + 3);
;         MD_COMPUTE(0);
;         MD_END(t + 3 >= NT);
;         if (t + 2 < NT) { MD_B_WAIT(s0, 8); MD_B_WRITE(s0, 0); __builtin_amdgcn_sched_barrier(0); MD_GLDS_A(0, t + 2); __builtin_amdgcn_sched_barrier(0); }
;         if (t + 4 < NT) MD_B_ISSUE(s0, t + 4);
;         MD_COMPUTE(1);
;         MD_END(t + 4 >= NT);
	v_cvt_pk_bf16_f32 v172, v202, v204
	v_cvt_pk_bf16_f32 v173, v206, v208
	v_cvt_pk_bf16_f32 v174, v210, v212
	v_cvt_pk_bf16_f32 v175, v214, v216
	v_cvt_pk_bf16_f32 v176, v203, v205
	v_cvt_pk_bf16_f32 v177, v207, v209
	v_cvt_pk_bf16_f32 v178, v211, v213
	v_cvt_pk_bf16_f32 v179, v215, v217
	ds_write_b128 v95, v[172:175] offset:19456
	ds_write_b128 v95, v[176:179] offset:19584
	v_add_u32_e32 v91, s46, v135
	v_add_u32_e32 v93, s46, v137
	ds_read_b128 v[238:241], v139 offset:0
	ds_read_b128 v[242:245], v139 offset:2048
	ds_read_b128 v[246:249], v139 offset:4096
	ds_read_b128 v[250:253], v139 offset:6144
	ds_read_b128 v[218:221], v91 offset:0
	ds_read_b128 v[222:225], v91 offset:2048
	ds_read_b128 v[226:229], v91 offset:4096
	ds_read_b128 v[230:233], v91 offset:6144
	ds_read_b128 v[234:237], v91 offset:8192
	s_add_i32 s49, s48, s74
	s_add_i32 s52, s52, 1
	s_and_b32 s54, s52, 7
	s_cmp_eq_u32 s54, 0
	s_cselect_b32 s54, s53, s32
	s_cselect_b32 s55, -1, 0
	s_add_u32 s30, s30, s54
	s_addc_u32 s31, s31, s55
	s_waitcnt lgkmcnt(0)
	v_mfma_f32_16x16x32_bf16 v[78:81], v[238:241], v[218:221], v[78:81]
	v_mfma_f32_16x16x32_bf16 v[74:77], v[242:245], v[218:221], v[74:77]
	v_mfma_f32_16x16x32_bf16 v[70:73], v[246:249], v[218:221], v[70:73]
	v_mfma_f32_16x16x32_bf16 v[66:69], v[250:253], v[218:221], v[66:69]
	ds_read_b128 v[218:221], v93 offset:0
	ds_read_b128 v[142:145], v141 offset:0
	s_mov_b32 m0, s49
	s_nop 0
	global_load_lds_dwordx4 v88, s[30:31]
	v_mfma_f32_16x16x32_bf16 v[62:65], v[238:241], v[222:225], v[62:65]
	v_mfma_f32_16x16x32_bf16 v[58:61], v[242:245], v[222:225], v[58:61]
	v_mfma_f32_16x16x32_bf16 v[54:57], v[246:249], v[222:225], v[54:57]
	v_mfma_f32_16x16x32_bf16 v[50:53], v[250:253], v[222:225], v[50:53]
	ds_read_b128 v[222:225], v93 offset:2048
	ds_read_b128 v[146:149], v141 offset:2048
	s_add_i32 m0, s49, 0x2000
	s_nop 0
	global_load_lds_dwordx4 v90, s[30:31]
	v_mfma_f32_16x16x32_bf16 v[46:49], v[238:241], v[226:229], v[46:49]
	v_mfma_f32_16x16x32_bf16 v[42:45], v[242:245], v[226:229], v[42:45]
	v_mfma_f32_16x16x32_bf16 v[38:41], v[246:249], v[226:229], v[38:41]
	v_mfma_f32_16x16x32_bf16 v[34:37], v[250:253], v[226:229], v[34:37]
	ds_read_b128 v[226:229], v93 offset:4096
	ds_read_b128 v[156:159], v141 offset:4096
	s_add_i32 m0, s49, 0x4000
	s_nop 0
	global_load_lds_dwordx4 v92, s[30:31]
	v_mfma_f32_16x16x32_bf16 v[18:21], v[238:241], v[230:233], v[18:21]
	v_mfma_f32_16x16x32_bf16 v[22:25], v[242:245], v[230:233], v[22:25]
	v_mfma_f32_16x16x32_bf16 v[26:29], v[246:249], v[230:233], v[26:29]
	v_mfma_f32_16x16x32_bf16 v[30:33], v[250:253], v[230:233], v[30:33]
	ds_read_b128 v[230:233], v93 offset:6144
	ds_read_b128 v[160:163], v141 offset:6144
	s_add_i32 m0, s49, 0x6000
	s_nop 0
	global_load_lds_dwordx4 v94, s[30:31]
	v_mfma_f32_16x16x32_bf16 v[2:5], v[238:241], v[234:237], v[2:5]
	v_mfma_f32_16x16x32_bf16 v[6:9], v[242:245], v[234:237], v[6:9]
	v_mfma_f32_16x16x32_bf16 v[10:13], v[246:249], v[234:237], v[10:13]
	v_mfma_f32_16x16x32_bf16 v[14:17], v[250:253], v[234:237], v[14:17]
	ds_read_b128 v[234:237], v93 offset:8192
	s_add_i32 m0, s49, 0x8000
	s_nop 0
	global_load_lds_dwordx4 v96, s[30:31]
	s_waitcnt lgkmcnt(0)
	v_mfma_f32_16x16x32_bf16 v[78:81], v[142:145], v[218:221], v[78:81]
	v_mfma_f32_16x16x32_bf16 v[74:77], v[146:149], v[218:221], v[74:77]
	v_mfma_f32_16x16x32_bf16 v[70:73], v[156:159], v[218:221], v[70:73]
	v_mfma_f32_16x16x32_bf16 v[66:69], v[160:163], v[218:221], v[66:69]
	s_add_i32 s51, s51, 1
	s_and_b32 s54, s51, 7
	s_cmp_eq_u32 s54, 0
	s_cselect_b32 s44, s34, s35
	s_cselect_b32 s45, -1, 0
	v_lshl_add_u64 v[132:133], v[132:133], 0, s[44:45]
	global_load_dwordx2 v[202:203], v[132:133], off
	v_lshl_add_u64 v[180:181], v[132:133], 0, s[24:25]
	global_load_dwordx2 v[204:205], v[180:181], off
	v_mfma_f32_16x16x32_bf16 v[62:65], v[142:145], v[222:225], v[62:65]
	v_mfma_f32_16x16x32_bf16 v[58:61], v[146:149], v[222:225], v[58:61]
	v_mfma_f32_16x16x32_bf16 v[54:57], v[156:159], v[222:225], v[54:57]
	v_mfma_f32_16x16x32_bf16 v[50:53], v[160:163], v[222:225], v[50:53]
	v_lshl_add_u64 v[180:181], v[132:133], 0, s[26:27]
	global_load_dwordx2 v[206:207], v[180:181], off
	v_lshl_add_u64 v[180:181], v[132:133], 0, s[28:29]
	global_load_dwordx2 v[208:209], v[180:181], off
	v_mfma_f32_16x16x32_bf16 v[46:49], v[142:145], v[226:229], v[46:49]
	v_mfma_f32_16x16x32_bf16 v[42:45], v[146:149], v[226:229], v[42:45]
	v_mfma_f32_16x16x32_bf16 v[38:41], v[156:159], v[226:229], v[38:41]
	v_mfma_f32_16x16x32_bf16 v[34:37], v[160:163], v[226:229], v[34:37]
	v_lshl_add_u64 v[180:181], v[132:133], 0, s[36:37]
	global_load_dwordx2 v[210:211], v[180:181], off
	v_lshl_add_u64 v[180:181], v[132:133], 0, s[38:39]
	global_load_dwordx2 v[212:213], v[180:181], off
	v_mfma_f32_16x16x32_bf16 v[18:21], v[142:145], v[230:233], v[18:21]
	v_mfma_f32_16x16x32_bf16 v[22:25], v[146:149], v[230:233], v[22:25]
	v_mfma_f32_16x16x32_bf16 v[26:29], v[156:159], v[230:233], v[26:29]
	v_mfma_f32_16x16x32_bf16 v[30:33], v[160:163], v[230:233], v[30:33]
	v_lshl_add_u64 v[180:181], v[132:133], 0, s[40:41]
	global_load_dwordx2 v[214:215], v[180:181], off
	v_lshl_add_u64 v[180:181], v[132:133], 0, s[42:43]
	global_load_dwordx2 v[216:217], v[180:181], off
	v_mfma_f32_16x16x32_bf16 v[2:5], v[142:145], v[234:237], v[2:5]
	v_mfma_f32_16x16x32_bf16 v[6:9], v[146:149], v[234:237], v[6:9]
	v_mfma_f32_16x16x32_bf16 v[10:13], v[156:159], v[234:237], v[10:13]
	v_mfma_f32_16x16x32_bf16 v[14:17], v[160:163], v[234:237], v[14:17]
	s_waitcnt vmcnt(21)
	s_mov_b32 s49, s46
	s_mov_b32 s46, s47
	s_mov_b32 s47, s48
	s_mov_b32 s48, s49
	s_add_i32 s50, s50, 1
	s_waitcnt lgkmcnt(0)
	s_barrier
; #define MD_GLDS_A(buf, tau) do { _Pragma("unroll") for (int i = 0; i < 5; ++i) if (amask & (1u << i)) \
;         __builtin_amdgcn_global_load_lds((const unsigned*)((const char*)HIDp + aoff[i] + (size_t)((tau) & 7) * 128), (PG8_LAS unsigned*)(MD_SA(buf) + wid * 1024 + i * 8192), 16, 0, 0); } while (0)
; #define MD_B_ISSUE(sb, tau) do { const char* kb_ = Bb + (size_t)((tau) >> 3) * 512 + (size_t)((tau) & 7) * (64 * (size_t)RB); _Pragma("unroll") for (int j = 0; j < 8; ++j) { const char* p_ = kb_ + (size_t)j * RB; \
;         asm volatile("global_load_dwordx2 %0, %1, off" : "=&v"(sb[j]) : "v"(p_) : "memory"); } } while (0)
; #define MD_B_WAIT(sb, N) asm volatile("s_waitcnt vmcnt(%8)" : "+v"(sb[0]), "+v"(sb[1]), "+v"(sb[2]), "+v"(sb[3]), "+v"(sb[4]), "+v"(sb[5]), "+v"(sb[6]), "+v"(sb[7]) : "n"(N) : "memory")
; __device__ __forceinline__ void moe_down_stream(PG8_LAS unsigned char* lds, int e, int cb0, int slot0, int nv, const bf16_t* HIDp, const float* Wd, bf16_t* Y, const float* slot_w, const int* slot_dst) {
;     ...
;     f32x4 acc[DNM][4];
; #pragma unroll
;     for (int m = 0; m < DNM; ++m)
; #pragma unroll
;         for (int n = 0; n < 4; ++n) acc[m][n] = (f32x4){0.f, 0.f, 0.f, 0.f};
;     f32x2 s0[8], s1[8];
;     MD_GLDS_A(0, 0); MD_B_ISSUE(s0, 0); MD_B_ISSUE(s1, 1);
;     MD_B_WAIT(s0, 8); MD_B_WRITE(s0, 0); __builtin_amdgcn_sched_barrier(0); MD_B_ISSUE(s0, 2);
;     asm volatile("s_waitcnt vmcnt(16)" ::: "memory");
;     asm volatile("s_waitcnt lgkmcnt(0)" ::: "memory"); __builtin_amdgcn_s_barrier(); asm volatile("" ::: "memory");
; #pragma unroll 1
;     for (int t = 0; t < NT; t += 2) {
;         if (t + 2 < NT) MD_B_WAIT(s1, 8); else MD_B_WAIT(s1, 0);
;         MD_B_WRITE(s1, 1); __builtin_amdgcn_sched_barrier(0); MD_GLDS_A(1, t + 1); __builtin_amdgcn_sched_barrier(0);
;         if (t + 3 < NT) MD_B_ISSUE(s1, t + 3);
;         MD_COMPUTE(0);
;         MD_END(t + 3 >= NT);
;         if (t + 2 < NT) { MD_B_WAIT(s0, 8); MD_B_WRITE(s0, 0); __builtin_amdgcn_sched_barrier(0); MD_GLDS_A(0, t + 2); __builtin_amdgcn_sched_barrier(0); }
;         if (t + 4 < NT) MD_B_ISSUE(s0, t + 4);
;         MD_COMPUTE(1);
;         MD_END(t + 4 >= NT);
	v_cvt_pk_bf16_f32 v172, v98, v100
	v_cvt_pk_bf16_f32 v173, v102, v104
	v_cvt_pk_bf16_f32 v174, v106, v108
	v_cvt_pk_bf16_f32 v175, v110, v112
	v_cvt_pk_bf16_f32 v176, v99, v101
	v_cvt_pk_bf16_f32 v177, v103, v105
	v_cvt_pk_bf16_f32 v178, v107, v109
	v_cvt_pk_bf16_f32 v179, v111, v113
	ds_write_b128 v95, v[172:175] offset:0
	ds_write_b128 v95, v[176:179] offset:128
	v_add_u32_e32 v91, s46, v135
	v_add_u32_e32 v93, s46, v137
	ds_read_b128 v[238:241], v139 offset:19456
	ds_read_b128 v[242:245], v139 offset:21504
	ds_read_b128 v[246:249], v139 offset:23552
	ds_read_b128 v[250:253], v139 offset:25600
	ds_read_b128 v[218:221], v91 offset:0
	ds_read_b128 v[222:225], v91 offset:2048
	ds_read_b128 v[226:229], v91 offset:4096
	ds_read_b128 v[230:233], v91 offset:6144
	ds_read_b128 v[234:237], v91 offset:8192
	s_add_i32 s49, s48, s74
	s_add_i32 s52, s52, 1
	s_and_b32 s54, s52, 7
	s_cmp_eq_u32 s54, 0
	s_cselect_b32 s54, s53, s32
	s_cselect_b32 s55, -1, 0
	s_add_u32 s30, s30, s54
	s_addc_u32 s31, s31, s55
	s_waitcnt lgkmcnt(0)
	v_mfma_f32_16x16x32_bf16 v[78:81], v[238:241], v[218:221], v[78:81]
	v_mfma_f32_16x16x32_bf16 v[74:77], v[242:245], v[218:221], v[74:77]
	v_mfma_f32_16x16x32_bf16 v[70:73], v[246:249], v[218:221], v[70:73]
	v_mfma_f32_16x16x32_bf16 v[66:69], v[250:253], v[218:221], v[66:69]
	ds_read_b128 v[218:221], v93 offset:0
	ds_read_b128 v[142:145], v141 offset:19456
	s_mov_b32 m0, s49
	s_nop 0
	global_load_lds_dwordx4 v88, s[30:31]
	v_mfma_f32_16x16x32_bf16 v[62:65], v[238:241], v[222:225], v[62:65]
	v_mfma_f32_16x16x32_bf16 v[58:61], v[242:245], v[222:225], v[58:61]
	v_mfma_f32_16x16x32_bf16 v[54:57], v[246:249], v[222:225], v[54:57]
	v_mfma_f32_16x16x32_bf16 v[50:53], v[250:253], v[222:225], v[50:53]
	ds_read_b128 v[222:225], v93 offset:2048
	ds_read_b128 v[146:149], v141 offset:21504
	s_add_i32 m0, s49, 0x2000
	s_nop 0
	global_load_lds_dwordx4 v90, s[30:31]
	v_mfma_f32_16x16x32_bf16 v[46:49], v[238:241], v[226:229], v[46:49]
	v_mfma_f32_16x16x32_bf16 v[42:45], v[242:245], v[226:229], v[42:45]
	v_mfma_f32_16x16x32_bf16 v[38:41], v[246:249], v[226:229], v[38:41]
	v_mfma_f32_16x16x32_bf16 v[34:37], v[250:253], v[226:229], v[34:37]
	ds_read_b128 v[226:229], v93 offset:4096
	ds_read_b128 v[156:159], v141 offset:23552
	s_add_i32 m0, s49, 0x4000
	s_nop 0
	global_load_lds_dwordx4 v92, s[30:31]
	v_mfma_f32_16x16x32_bf16 v[18:21], v[238:241], v[230:233], v[18:21]
	v_mfma_f32_16x16x32_bf16 v[22:25], v[242:245], v[230:233], v[22:25]
	v_mfma_f32_16x16x32_bf16 v[26:29], v[246:249], v[230:233], v[26:29]
	v_mfma_f32_16x16x32_bf16 v[30:33], v[250:253], v[230:233], v[30:33]
	ds_read_b128 v[230:233], v93 offset:6144
	ds_read_b128 v[160:163], v141 offset:25600
	s_add_i32 m0, s49, 0x6000
	s_nop 0
	global_load_lds_dwordx4 v94, s[30:31]
	v_mfma_f32_16x16x32_bf16 v[2:5], v[238:241], v[234:237], v[2:5]
	v_mfma_f32_16x16x32_bf16 v[6:9], v[242:245], v[234:237], v[6:9]
	v_mfma_f32_16x16x32_bf16 v[10:13], v[246:249], v[234:237], v[10:13]
	v_mfma_f32_16x16x32_bf16 v[14:17], v[250:253], v[234:237], v[14:17]
	ds_read_b128 v[234:237], v93 offset:8192
	s_add_i32 m0, s49, 0x8000
	s_nop 0
	global_load_lds_dwordx4 v96, s[30:31]
	s_waitcnt lgkmcnt(0)
	v_mfma_f32_16x16x32_bf16 v[78:81], v[142:145], v[218:221], v[78:81]
	v_mfma_f32_16x16x32_bf16 v[74:77], v[146:149], v[218:221], v[74:77]
	v_mfma_f32_16x16x32_bf16 v[70:73], v[156:159], v[218:221], v[70:73]
	v_mfma_f32_16x16x32_bf16 v[66:69], v[160:163], v[218:221], v[66:69]
	s_add_i32 s51, s51, 1
	s_and_b32 s54, s51, 7
	s_cmp_eq_u32 s54, 0
	s_cselect_b32 s44, s34, s35
	s_cselect_b32 s45, -1, 0
	v_lshl_add_u64 v[132:133], v[132:133], 0, s[44:45]
	global_load_dwordx2 v[98:99], v[132:133], off
	v_lshl_add_u64 v[180:181], v[132:133], 0, s[24:25]
	global_load_dwordx2 v[100:101], v[180:181], off
	v_mfma_f32_16x16x32_bf16 v[62:65], v[142:145], v[222:225], v[62:65]
	v_mfma_f32_16x16x32_bf16 v[58:61], v[146:149], v[222:225], v[58:61]
	v_mfma_f32_16x16x32_bf16 v[54:57], v[156:159], v[222:225], v[54:57]
	v_mfma_f32_16x16x32_bf16 v[50:53], v[160:163], v[222:225], v[50:53]
	v_lshl_add_u64 v[180:181], v[132:133], 0, s[26:27]
	global_load_dwordx2 v[102:103], v[180:181], off
	v_lshl_add_u64 v[180:181], v[132:133], 0, s[28:29]
	global_load_dwordx2 v[104:105], v[180:181], off
	v_mfma_f32_16x16x32_bf16 v[46:49], v[142:145], v[226:229], v[46:49]
	v_mfma_f32_16x16x32_bf16 v[42:45], v[146:149], v[226:229], v[42:45]
	v_mfma_f32_16x16x32_bf16 v[38:41], v[156:159], v[226:229], v[38:41]
	v_mfma_f32_16x16x32_bf16 v[34:37], v[160:163], v[226:229], v[34:37]
	v_lshl_add_u64 v[180:181], v[132:133], 0, s[36:37]
	global_load_dwordx2 v[106:107], v[180:181], off
	v_lshl_add_u64 v[180:181], v[132:133], 0, s[38:39]
	global_load_dwordx2 v[108:109], v[180:181], off
	v_mfma_f32_16x16x32_bf16 v[18:21], v[142:145], v[230:233], v[18:21]
	v_mfma_f32_16x16x32_bf16 v[22:25], v[146:149], v[230:233], v[22:25]
	v_mfma_f32_16x16x32_bf16 v[26:29], v[156:159], v[230:233], v[26:29]
	v_mfma_f32_16x16x32_bf16 v[30:33], v[160:163], v[230:233], v[30:33]
	v_lshl_add_u64 v[180:181], v[132:133], 0, s[40:41]
	global_load_dwordx2 v[110:111], v[180:181], off
	v_lshl_add_u64 v[180:181], v[132:133], 0, s[42:43]
	global_load_dwordx2 v[112:113], v[180:181], off
	v_mfma_f32_16x16x32_bf16 v[2:5], v[142:145], v[234:237], v[2:5]
	v_mfma_f32_16x16x32_bf16 v[6:9], v[146:149], v[234:237], v[6:9]
	v_mfma_f32_16x16x32_bf16 v[10:13], v[156:159], v[234:237], v[10:13]
	v_mfma_f32_16x16x32_bf16 v[14:17], v[160:163], v[234:237], v[14:17]
	s_waitcnt vmcnt(21)
	s_mov_b32 s49, s46
	s_mov_b32 s46, s47
	s_mov_b32 s47, s48
	s_mov_b32 s48, s49
	s_add_i32 s50, s50, 1
	s_waitcnt lgkmcnt(0)
	s_barrier
	s_mov_b32 s56, 13
; #define MD_GLDS_A(buf, tau) do { _Pragma("unroll") for (int i = 0; i < 5; ++i) if (amask & (1u << i)) \
;         __builtin_amdgcn_global_load_lds((const unsigned*)((const char*)HIDp + aoff[i] + (size_t)((tau) & 7) * 128), (PG8_LAS unsigned*)(MD_SA(buf) + wid * 1024 + i * 8192), 16, 0, 0); } while (0)
; #define MD_B_ISSUE(sb, tau) do { const char* kb_ = Bb + (size_t)((tau) >> 3) * 512 + (size_t)((tau) & 7) * (64 * (size_t)RB); _Pragma("unroll") for (int j = 0; j < 8; ++j) { const char* p_ = kb_ + (size_t)j * RB; \
;         asm volatile("global_load_dwordx2 %0, %1, off" : "=&v"(sb[j]) : "v"(p_) : "memory"); } } while (0)
; #define MD_B_WAIT(sb, N) asm volatile("s_waitcnt vmcnt(%8)" : "+v"(sb[0]), "+v"(sb[1]), "+v"(sb[2]), "+v"(sb[3]), "+v"(sb[4]), "+v"(sb[5]), "+v"(sb[6]), "+v"(sb[7]) : "n"(N) : "memory")
; __device__ __forceinline__ void moe_down_stream(PG8_LAS unsigned char* lds, int e, int cb0, int slot0, int nv, const bf16_t* HIDp, const float* Wd, bf16_t* Y, const float* slot_w, const int* slot_dst) {
;     ...
;     f32x4 acc[DNM][4];
; #pragma unroll
;     for (int m = 0; m < DNM; ++m)
; #pragma unroll
;         for (int n = 0; n < 4; ++n) acc[m][n] = (f32x4){0.f, 0.f, 0.f, 0.f};
;     f32x2 s0[8], s1[8];
;     MD_GLDS_A(0, 0); MD_B_ISSUE(s0, 0); MD_B_ISSUE(s1, 1);
;     MD_B_WAIT(s0, 8); MD_B_WRITE(s0, 0); __builtin_amdgcn_sched_barrier(0); MD_B_ISSUE(s0, 2);
;     asm volatile("s_waitcnt vmcnt(16)" ::: "memory");
;     asm volatile("s_waitcnt lgkmcnt(0)" ::: "memory"); __builtin_amdgcn_s_barrier(); asm volatile("" ::: "memory");
; #pragma unroll 1
;     for (int t = 0; t < NT; t += 2) {
;         if (t + 2 < NT) MD_B_WAIT(s1, 8); else MD_B_WAIT(s1, 0);
;         MD_B_WRITE(s1, 1); __builtin_amdgcn_sched_barrier(0); MD_GLDS_A(1, t + 1); __builtin_amdgcn_sched_barrier(0);
;         if (t + 3 < NT) MD_B_ISSUE(s1, t + 3);
;         MD_COMPUTE(0);
;         MD_END(t + 3 >= NT);
;         if (t + 2 < NT) { MD_B_WAIT(s0, 8); MD_B_WRITE(s0, 0); __builtin_amdgcn_sched_barrier(0); MD_GLDS_A(0, t + 2); __builtin_amdgcn_sched_barrier(0); }
;         if (t + 4 < NT) MD_B_ISSUE(s0, t + 4);
;         MD_COMPUTE(1);
;         MD_END(t + 4 >= NT);
.Lmd_loop_X:
	v_cvt_pk_bf16_f32 v172, v114, v116
	v_cvt_pk_bf16_f32 v173, v118, v120
	v_cvt_pk_bf16_f32 v174, v122, v124
	v_cvt_pk_bf16_f32 v175, v126, v128
	v_cvt_pk_bf16_f32 v176, v115, v117
	v_cvt_pk_bf16_f32 v177, v119, v121
	v_cvt_pk_bf16_f32 v178, v123, v125
	v_cvt_pk_bf16_f32 v179, v127, v129
	ds_write_b128 v95, v[172:175] offset:19456
	ds_write_b128 v95, v[176:179] offset:19584
	v_add_u32_e32 v91, s46, v135
	v_add_u32_e32 v93, s46, v137
	ds_read_b128 v[238:241], v139 offset:0
	ds_read_b128 v[242:245], v139 offset:2048
	ds_read_b128 v[246:249], v139 offset:4096
	ds_read_b128 v[250:253], v139 offset:6144
	ds_read_b128 v[218:221], v91 offset:0
	ds_read_b128 v[222:225], v91 offset:2048
	ds_read_b128 v[226:229], v91 offset:4096
	ds_read_b128 v[230:233], v91 offset:6144
	ds_read_b128 v[234:237], v91 offset:8192
	s_add_i32 s49, s48, s74
	s_add_i32 s52, s52, 1
	s_and_b32 s54, s52, 7
	s_cmp_eq_u32 s54, 0
	s_cselect_b32 s54, s53, s32
	s_cselect_b32 s55, -1, 0
	s_add_u32 s30, s30, s54
	s_addc_u32 s31, s31, s55
	s_waitcnt lgkmcnt(0)
	v_mfma_f32_16x16x32_bf16 v[78:81], v[238:241], v[218:221], v[78:81]
	v_mfma_f32_16x16x32_bf16 v[74:77], v[242:245], v[218:221], v[74:77]
	v_mfma_f32_16x16x32_bf16 v[70:73], v[246:249], v[218:221], v[70:73]
	v_mfma_f32_16x16x32_bf16 v[66:69], v[250:253], v[218:221], v[66:69]
	ds_read_b128 v[218:221], v93 offset:0
	ds_read_b128 v[142:145], v141 offset:0
	s_mov_b32 m0, s49
	s_nop 0
	global_load_lds_dwordx4 v88, s[30:31]
	v_mfma_f32_16x16x32_bf16 v[62:65], v[238:241], v[222:225], v[62:65]
	v_mfma_f32_16x16x32_bf16 v[58:61], v[242:245], v[222:225], v[58:61]
	v_mfma_f32_16x16x32_bf16 v[54:57], v[246:249], v[222:225], v[54:57]
	v_mfma_f32_16x16x32_bf16 v[50:53], v[250:253], v[222:225], v[50:53]
	ds_read_b128 v[222:225], v93 offset:2048
	ds_read_b128 v[146:149], v141 offset:2048
	s_add_i32 m0, s49, 0x2000
	s_nop 0
	global_load_lds_dwordx4 v90, s[30:31]
	v_mfma_f32_16x16x32_bf16 v[46:49], v[238:241], v[226:229], v[46:49]
	v_mfma_f32_16x16x32_bf16 v[42:45], v[242:245], v[226:229], v[42:45]
	v_mfma_f32_16x16x32_bf16 v[38:41], v[246:249], v[226:229], v[38:41]
	v_mfma_f32_16x16x32_bf16 v[34:37], v[250:253], v[226:229], v[34:37]
	ds_read_b128 v[226:229], v93 offset:4096
	ds_read_b128 v[156:159], v141 offset:4096
	s_add_i32 m0, s49, 0x4000
	s_nop 0
	global_load_lds_dwordx4 v92, s[30:31]
	v_mfma_f32_16x16x32_bf16 v[18:21], v[238:241], v[230:233], v[18:21]
	v_mfma_f32_16x16x32_bf16 v[22:25], v[242:245], v[230:233], v[22:25]
	v_mfma_f32_16x16x32_bf16 v[26:29], v[246:249], v[230:233], v[26:29]
	v_mfma_f32_16x16x32_bf16 v[30:33], v[250:253], v[230:233], v[30:33]
	ds_read_b128 v[230:233], v93 offset:6144
	ds_read_b128 v[160:163], v141 offset:6144
	s_add_i32 m0, s49, 0x6000
	s_nop 0
	global_load_lds_dwordx4 v94, s[30:31]
	v_mfma_f32_16x16x32_bf16 v[2:5], v[238:241], v[234:237], v[2:5]
	v_mfma_f32_16x16x32_bf16 v[6:9], v[242:245], v[234:237], v[6:9]
	v_mfma_f32_16x16x32_bf16 v[10:13], v[246:249], v[234:237], v[10:13]
	v_mfma_f32_16x16x32_bf16 v[14:17], v[250:253], v[234:237], v[14:17]
	ds_read_b128 v[234:237], v93 offset:8192
	s_add_i32 m0, s49, 0x8000
	s_nop 0
	global_load_lds_dwordx4 v96, s[30:31]
	s_waitcnt lgkmcnt(0)
	v_mfma_f32_16x16x32_bf16 v[78:81], v[142:145], v[218:221], v[78:81]
	v_mfma_f32_16x16x32_bf16 v[74:77], v[146:149], v[218:221], v[74:77]
	v_mfma_f32_16x16x32_bf16 v[70:73], v[156:159], v[218:221], v[70:73]
	v_mfma_f32_16x16x32_bf16 v[66:69], v[160:163], v[218:221], v[66:69]
	s_add_i32 s51, s51, 1
	s_and_b32 s54, s51, 7
	s_cmp_eq_u32 s54, 0
	s_cselect_b32 s44, s34, s35
	s_cselect_b32 s45, -1, 0
	v_lshl_add_u64 v[132:133], v[132:133], 0, s[44:45]
	global_load_dwordx2 v[114:115], v[132:133], off
	v_lshl_add_u64 v[180:181], v[132:133], 0, s[24:25]
	global_load_dwordx2 v[116:117], v[180:181], off
	v_mfma_f32_16x16x32_bf16 v[62:65], v[142:145], v[222:225], v[62:65]
	v_mfma_f32_16x16x32_bf16 v[58:61], v[146:149], v[222:225], v[58:61]
	v_mfma_f32_16x16x32_bf16 v[54:57], v[156:159], v[222:225], v[54:57]
	v_mfma_f32_16x16x32_bf16 v[50:53], v[160:163], v[222:225], v[50:53]
	v_lshl_add_u64 v[180:181], v[132:133], 0, s[26:27]
	global_load_dwordx2 v[118:119], v[180:181], off
	v_lshl_add_u64 v[180:181], v[132:133], 0, s[28:29]
	global_load_dwordx2 v[120:121], v[180:181], off
	v_mfma_f32_16x16x32_bf16 v[46:49], v[142:145], v[226:229], v[46:49]
	v_mfma_f32_16x16x32_bf16 v[42:45], v[146:149], v[226:229], v[42:45]
	v_mfma_f32_16x16x32_bf16 v[38:41], v[156:159], v[226:229], v[38:41]
	v_mfma_f32_16x16x32_bf16 v[34:37], v[160:163], v[226:229], v[34:37]
	v_lshl_add_u64 v[180:181], v[132:133], 0, s[36:37]
	global_load_dwordx2 v[122:123], v[180:181], off
	v_lshl_add_u64 v[180:181], v[132:133], 0, s[38:39]
	global_load_dwordx2 v[124:125], v[180:181], off
	v_mfma_f32_16x16x32_bf16 v[18:21], v[142:145], v[230:233], v[18:21]
	v_mfma_f32_16x16x32_bf16 v[22:25], v[146:149], v[230:233], v[22:25]
	v_mfma_f32_16x16x32_bf16 v[26:29], v[156:159], v[230:233], v[26:29]
	v_mfma_f32_16x16x32_bf16 v[30:33], v[160:163], v[230:233], v[30:33]
	v_lshl_add_u64 v[180:181], v[132:133], 0, s[40:41]
	global_load_dwordx2 v[126:127], v[180:181], off
	v_lshl_add_u64 v[180:181], v[132:133], 0, s[42:43]
	global_load_dwordx2 v[128:129], v[180:181], off
	v_mfma_f32_16x16x32_bf16 v[2:5], v[142:145], v[234:237], v[2:5]
	v_mfma_f32_16x16x32_bf16 v[6:9], v[146:149], v[234:237], v[6:9]
	v_mfma_f32_16x16x32_bf16 v[10:13], v[156:159], v[234:237], v[10:13]
	v_mfma_f32_16x16x32_bf16 v[14:17], v[160:163], v[234:237], v[14:17]
	s_waitcnt vmcnt(21)
	s_mov_b32 s49, s46
	s_mov_b32 s46, s47
	s_mov_b32 s47, s48
	s_mov_b32 s48, s49
	s_add_i32 s50, s50, 1
	s_waitcnt lgkmcnt(0)
	s_barrier
; #define MD_GLDS_A(buf, tau) do { _Pragma("unroll") for (int i = 0; i < 5; ++i) if (amask & (1u << i)) \
;         __builtin_amdgcn_global_load_lds((const unsigned*)((const char*)HIDp + aoff[i] + (size_t)((tau) & 7) * 128), (PG8_LAS unsigned*)(MD_SA(buf) + wid * 1024 + i * 8192), 16, 0, 0); } while (0)
; #define MD_B_ISSUE(sb, tau) do { const char* kb_ = Bb + (size_t)((tau) >> 3) * 512 + (size_t)((tau) & 7) * (64 * (size_t)RB); _Pragma("unroll") for (int j = 0; j < 8; ++j) { const char* p_ = kb_ + (size_t)j * RB; \
;         asm volatile("global_load_dwordx2 %0, %1, off" : "=&v"(sb[j]) : "v"(p_) : "memory"); } } while (0)
; #define MD_B_WAIT(sb, N) asm volatile("s_waitcnt vmcnt(%8)" : "+v"(sb[0]), "+v"(sb[1]), "+v"(sb[2]), "+v"(sb[3]), "+v"(sb[4]), "+v"(sb[5]), "+v"(sb[6]), "+v"(sb[7]) : "n"(N) : "memory")
; __device__ __forceinline__ void moe_down_stream(PG8_LAS unsigned char* lds, int e, int cb0, int slot0, int nv, const bf16_t* HIDp, const float* Wd, bf16_t* Y, const float* slot_w, const int* slot_dst) {
;     ...
;     f32x4 acc[DNM][4];
; #pragma unroll
;     for (int m = 0; m < DNM; ++m)
; #pragma unroll
;         for (int n = 0; n < 4; ++n) acc[m][n] = (f32x4){0.f, 0.f, 0.f, 0.f};
;     f32x2 s0[8], s1[8];
;     MD_GLDS_A(0, 0); MD_B_ISSUE(s0, 0); MD_B_ISSUE(s1, 1);
;     MD_B_WAIT(s0, 8); MD_B_WRITE(s0, 0); __builtin_amdgcn_sched_barrier(0); MD_B_ISSUE(s0, 2);
;     asm volatile("s_waitcnt vmcnt(16)" ::: "memory");
;     asm volatile("s_waitcnt lgkmcnt(0)" ::: "memory"); __builtin_amdgcn_s_barrier(); asm volatile("" ::: "memory");
; #pragma unroll 1
;     for (int t = 0; t < NT; t += 2) {
;         if (t + 2 < NT) MD_B_WAIT(s1, 8); else MD_B_WAIT(s1, 0);
;         MD_B_WRITE(s1, 1); __builtin_amdgcn_sched_barrier(0); MD_GLDS_A(1, t + 1); __builtin_amdgcn_sched_barrier(0);
;         if (t + 3 < NT) MD_B_ISSUE(s1, t + 3);
;         MD_COMPUTE(0);
;         MD_END(t + 3 >= NT);
;         if (t + 2 < NT) { MD_B_WAIT(s0, 8); MD_B_WRITE(s0, 0); __builtin_amdgcn_sched_barrier(0); MD_GLDS_A(0, t + 2); __builtin_amdgcn_sched_barrier(0); }
;         if (t + 4 < NT) MD_B_ISSUE(s0, t + 4);
;         MD_COMPUTE(1);
;         MD_END(t + 4 >= NT);
	v_cvt_pk_bf16_f32 v172, v186, v188
	v_cvt_pk_bf16_f32 v173, v190, v192
	v_cvt_pk_bf16_f32 v174, v194, v196
	v_cvt_pk_bf16_f32 v175, v198, v200
	v_cvt_pk_bf16_f32 v176, v187, v189
	v_cvt_pk_bf16_f32 v177, v191, v193
	v_cvt_pk_bf16_f32 v178, v195, v197
	v_cvt_pk_bf16_f32 v179, v199, v201
	ds_write_b128 v95, v[172:175] offset:0
	ds_write_b128 v95, v[176:179] offset:128
	v_add_u32_e32 v91, s46, v135
	v_add_u32_e32 v93, s46, v137
	ds_read_b128 v[238:241], v139 offset:19456
	ds_read_b128 v[242:245], v139 offset:21504
	ds_read_b128 v[246:249], v139 offset:23552
	ds_read_b128 v[250:253], v139 offset:25600
	ds_read_b128 v[218:221], v91 offset:0
	ds_read_b128 v[222:225], v91 offset:2048
	ds_read_b128 v[226:229], v91 offset:4096
	ds_read_b128 v[230:233], v91 offset:6144
	ds_read_b128 v[234:237], v91 offset:8192
	s_add_i32 s49, s48, s74
	s_add_i32 s52, s52, 1
	s_and_b32 s54, s52, 7
	s_cmp_eq_u32 s54, 0
	s_cselect_b32 s54, s53, s32
	s_cselect_b32 s55, -1, 0
	s_add_u32 s30, s30, s54
	s_addc_u32 s31, s31, s55
	s_waitcnt lgkmcnt(0)
	v_mfma_f32_16x16x32_bf16 v[78:81], v[238:241], v[218:221], v[78:81]
	v_mfma_f32_16x16x32_bf16 v[74:77], v[242:245], v[218:221], v[74:77]
	v_mfma_f32_16x16x32_bf16 v[70:73], v[246:249], v[218:221], v[70:73]
	v_mfma_f32_16x16x32_bf16 v[66:69], v[250:253], v[218:221], v[66:69]
	ds_read_b128 v[218:221], v93 offset:0
	ds_read_b128 v[142:145], v141 offset:19456
	s_mov_b32 m0, s49
	s_nop 0
	global_load_lds_dwordx4 v88, s[30:31]
	v_mfma_f32_16x16x32_bf16 v[62:65], v[238:241], v[222:225], v[62:65]
	v_mfma_f32_16x16x32_bf16 v[58:61], v[242:245], v[222:225], v[58:61]
	v_mfma_f32_16x16x32_bf16 v[54:57], v[246:249], v[222:225], v[54:57]
	v_mfma_f32_16x16x32_bf16 v[50:53], v[250:253], v[222:225], v[50:53]
	ds_read_b128 v[222:225], v93 offset:2048
	ds_read_b128 v[146:149], v141 offset:21504
	s_add_i32 m0, s49, 0x2000
	s_nop 0
	global_load_lds_dwordx4 v90, s[30:31]
	v_mfma_f32_16x16x32_bf16 v[46:49], v[238:241], v[226:229], v[46:49]
	v_mfma_f32_16x16x32_bf16 v[42:45], v[242:245], v[226:229], v[42:45]
	v_mfma_f32_16x16x32_bf16 v[38:41], v[246:249], v[226:229], v[38:41]
	v_mfma_f32_16x16x32_bf16 v[34:37], v[250:253], v[226:229], v[34:37]
	ds_read_b128 v[226:229], v93 offset:4096
	ds_read_b128 v[156:159], v141 offset:23552
	s_add_i32 m0, s49, 0x4000
	s_nop 0
	global_load_lds_dwordx4 v92, s[30:31]
	v_mfma_f32_16x16x32_bf16 v[18:21], v[238:241], v[230:233], v[18:21]
	v_mfma_f32_16x16x32_bf16 v[22:25], v[242:245], v[230:233], v[22:25]
	v_mfma_f32_16x16x32_bf16 v[26:29], v[246:249], v[230:233], v[26:29]
	v_mfma_f32_16x16x32_bf16 v[30:33], v[250:253], v[230:233], v[30:33]
	ds_read_b128 v[230:233], v93 offset:6144
	ds_read_b128 v[160:163], v141 offset:25600
	s_add_i32 m0, s49, 0x6000
	s_nop 0
	global_load_lds_dwordx4 v94, s[30:31]
	v_mfma_f32_16x16x32_bf16 v[2:5], v[238:241], v[234:237], v[2:5]
	v_mfma_f32_16x16x32_bf16 v[6:9], v[242:245], v[234:237], v[6:9]
	v_mfma_f32_16x16x32_bf16 v[10:13], v[246:249], v[234:237], v[10:13]
	v_mfma_f32_16x16x32_bf16 v[14:17], v[250:253], v[234:237], v[14:17]
	ds_read_b128 v[234:237], v93 offset:8192
	s_add_i32 m0, s49, 0x8000
	s_nop 0
	global_load_lds_dwordx4 v96, s[30:31]
	s_waitcnt lgkmcnt(0)
	v_mfma_f32_16x16x32_bf16 v[78:81], v[142:145], v[218:221], v[78:81]
	v_mfma_f32_16x16x32_bf16 v[74:77], v[146:149], v[218:221], v[74:77]
	v_mfma_f32_16x16x32_bf16 v[70:73], v[156:159], v[218:221], v[70:73]
	v_mfma_f32_16x16x32_bf16 v[66:69], v[160:163], v[218:221], v[66:69]
	s_add_i32 s51, s51, 1
	s_and_b32 s54, s51, 7
	s_cmp_eq_u32 s54, 0
	s_cselect_b32 s44, s34, s35
	s_cselect_b32 s45, -1, 0
	v_lshl_add_u64 v[132:133], v[132:133], 0, s[44:45]
	global_load_dwordx2 v[186:187], v[132:133], off
	v_lshl_add_u64 v[180:181], v[132:133], 0, s[24:25]
	global_load_dwordx2 v[188:189], v[180:181], off
	v_mfma_f32_16x16x32_bf16 v[62:65], v[142:145], v[222:225], v[62:65]
	v_mfma_f32_16x16x32_bf16 v[58:61], v[146:149], v[222:225], v[58:61]
	v_mfma_f32_16x16x32_bf16 v[54:57], v[156:159], v[222:225], v[54:57]
	v_mfma_f32_16x16x32_bf16 v[50:53], v[160:163], v[222:225], v[50:53]
	v_lshl_add_u64 v[180:181], v[132:133], 0, s[26:27]
	global_load_dwordx2 v[190:191], v[180:181], off
	v_lshl_add_u64 v[180:181], v[132:133], 0, s[28:29]
	global_load_dwordx2 v[192:193], v[180:181], off
	v_mfma_f32_16x16x32_bf16 v[46:49], v[142:145], v[226:229], v[46:49]
	v_mfma_f32_16x16x32_bf16 v[42:45], v[146:149], v[226:229], v[42:45]
	v_mfma_f32_16x16x32_bf16 v[38:41], v[156:159], v[226:229], v[38:41]
	v_mfma_f32_16x16x32_bf16 v[34:37], v[160:163], v[226:229], v[34:37]
	v_lshl_add_u64 v[180:181], v[132:133], 0, s[36:37]
	global_load_dwordx2 v[194:195], v[180:181], off
	v_lshl_add_u64 v[180:181], v[132:133], 0, s[38:39]
	global_load_dwordx2 v[196:197], v[180:181], off
	v_mfma_f32_16x16x32_bf16 v[18:21], v[142:145], v[230:233], v[18:21]
	v_mfma_f32_16x16x32_bf16 v[22:25], v[146:149], v[230:233], v[22:25]
	v_mfma_f32_16x16x32_bf16 v[26:29], v[156:159], v[230:233], v[26:29]
	v_mfma_f32_16x16x32_bf16 v[30:33], v[160:163], v[230:233], v[30:33]
	v_lshl_add_u64 v[180:181], v[132:133], 0, s[40:41]
	global_load_dwordx2 v[198:199], v[180:181], off
	v_lshl_add_u64 v[180:181], v[132:133], 0, s[42:43]
	global_load_dwordx2 v[200:201], v[180:181], off
	v_mfma_f32_16x16x32_bf16 v[2:5], v[142:145], v[234:237], v[2:5]
	v_mfma_f32_16x16x32_bf16 v[6:9], v[146:149], v[234:237], v[6:9]
	v_mfma_f32_16x16x32_bf16 v[10:13], v[156:159], v[234:237], v[10:13]
	v_mfma_f32_16x16x32_bf16 v[14:17], v[160:163], v[234:237], v[14:17]
	s_waitcnt vmcnt(21)
	s_mov_b32 s49, s46
	s_mov_b32 s46, s47
	s_mov_b32 s47, s48
	s_mov_b32 s48, s49
	s_add_i32 s50, s50, 1
	s_waitcnt lgkmcnt(0)
	s_barrier
; #define MD_GLDS_A(buf, tau) do { _Pragma("unroll") for (int i = 0; i < 5; ++i) if (amask & (1u << i)) \
;         __builtin_amdgcn_global_load_lds((const unsigned*)((const char*)HIDp + aoff[i] + (size_t)((tau) & 7) * 128), (PG8_LAS unsigned*)(MD_SA(buf) + wid * 1024 + i * 8192), 16, 0, 0); } while (0)
; #define MD_B_ISSUE(sb, tau) do { const char* kb_ = Bb + (size_t)((tau) >> 3) * 512 + (size_t)((tau) & 7) * (64 * (size_t)RB); _Pragma("unroll") for (int j = 0; j < 8; ++j) { const char* p_ = kb_ + (size_t)j * RB; \
;         asm volatile("global_load_dwordx2 %0, %1, off" : "=&v"(sb[j]) : "v"(p_) : "memory"); } } while (0)
; #define MD_B_WAIT(sb, N) asm volatile("s_waitcnt vmcnt(%8)" : "+v"(sb[0]), "+v"(sb[1]), "+v"(sb[2]), "+v"(sb[3]), "+v"(sb[4]), "+v"(sb[5]), "+v"(sb[6]), "+v"(sb[7]) : "n"(N) : "memory")
; __device__ __forceinline__ void moe_down_stream(PG8_LAS unsigned char* lds, int e, int cb0, int slot0, int nv, const bf16_t* HIDp, const float* Wd, bf16_t* Y, const float* slot_w, const int* slot_dst) {
;     ...
;     f32x4 acc[DNM][4];
; #pragma unroll
;     for (int m = 0; m < DNM; ++m)
; #pragma unroll
;         for (int n = 0; n < 4; ++n) acc[m][n] = (f32x4){0.f, 0.f, 0.f, 0.f};
;     f32x2 s0[8], s1[8];
;     MD_GLDS_A(0, 0); MD_B_ISSUE(s0, 0); MD_B_ISSUE(s1, 1);
;     MD_B_WAIT(s0, 8); MD_B_WRITE(s0, 0); __builtin_amdgcn_sched_barrier(0); MD_B_ISSUE(s0, 2);
;     asm volatile("s_waitcnt vmcnt(16)" ::: "memory");
;     asm volatile("s_waitcnt lgkmcnt(0)" ::: "memory"); __builtin_amdgcn_s_barrier(); asm volatile("" ::: "memory");
; #pragma unroll 1
;     for (int t = 0; t < NT; t += 2) {
;         if (t + 2 < NT) MD_B_WAIT(s1, 8); else MD_B_WAIT(s1, 0);
;         MD_B_WRITE(s1, 1); __builtin_amdgcn_sched_barrier(0); MD_GLDS_A(1, t + 1); __builtin_amdgcn_sched_barrier(0);
;         if (t + 3 < NT) MD_B_ISSUE(s1, t + 3);
;         MD_COMPUTE(0);
;         MD_END(t + 3 >= NT);
;         if (t + 2 < NT) { MD_B_WAIT(s0, 8); MD_B_WRITE(s0, 0); __builtin_amdgcn_sched_barrier(0); MD_GLDS_A(0, t + 2); __builtin_amdgcn_sched_barrier(0); }
;         if (t + 4 < NT) MD_B_ISSUE(s0, t + 4);
;         MD_COMPUTE(1);
;         MD_END(t + 4 >= NT);
	v_cvt_pk_bf16_f32 v172, v202, v204
	v_cvt_pk_bf16_f32 v173, v206, v208
	v_cvt_pk_bf16_f32 v174, v210, v212
	v_cvt_pk_bf16_f32 v175, v214, v216
	v_cvt_pk_bf16_f32 v176, v203, v205
	v_cvt_pk_bf16_f32 v177, v207, v209
	v_cvt_pk_bf16_f32 v178, v211, v213
	v_cvt_pk_bf16_f32 v179, v215, v217
	ds_write_b128 v95, v[172:175] offset:19456
	ds_write_b128 v95, v[176:179] offset:19584
	v_add_u32_e32 v91, s46, v135
	v_add_u32_e32 v93, s46, v137
	ds_read_b128 v[238:241], v139 offset:0
	ds_read_b128 v[242:245], v139 offset:2048
	ds_read_b128 v[246:249], v139 offset:4096
	ds_read_b128 v[250:253], v139 offset:6144
	ds_read_b128 v[218:221], v91 offset:0
	ds_read_b128 v[222:225], v91 offset:2048
	ds_read_b128 v[226:229], v91 offset:4096
	ds_read_b128 v[230:233], v91 offset:6144
	ds_read_b128 v[234:237], v91 offset:8192
	s_add_i32 s49, s48, s74
	s_add_i32 s52, s52, 1
	s_and_b32 s54, s52, 7
	s_cmp_eq_u32 s54, 0
	s_cselect_b32 s54, s53, s32
	s_cselect_b32 s55, -1, 0
	s_add_u32 s30, s30, s54
	s_addc_u32 s31, s31, s55
	s_waitcnt lgkmcnt(0)
	v_mfma_f32_16x16x32_bf16 v[78:81], v[238:241], v[218:221], v[78:81]
	v_mfma_f32_16x16x32_bf16 v[74:77], v[242:245], v[218:221], v[74:77]
	v_mfma_f32_16x16x32_bf16 v[70:73], v[246:249], v[218:221], v[70:73]
	v_mfma_f32_16x16x32_bf16 v[66:69], v[250:253], v[218:221], v[66:69]
	ds_read_b128 v[218:221], v93 offset:0
	ds_read_b128 v[142:145], v141 offset:0
	s_mov_b32 m0, s49
	s_nop 0
	global_load_lds_dwordx4 v88, s[30:31]
	v_mfma_f32_16x16x32_bf16 v[62:65], v[238:241], v[222:225], v[62:65]
	v_mfma_f32_16x16x32_bf16 v[58:61], v[242:245], v[222:225], v[58:61]
	v_mfma_f32_16x16x32_bf16 v[54:57], v[246:249], v[222:225], v[54:57]
	v_mfma_f32_16x16x32_bf16 v[50:53], v[250:253], v[222:225], v[50:53]
	ds_read_b128 v[222:225], v93 offset:2048
	ds_read_b128 v[146:149], v141 offset:2048
	s_add_i32 m0, s49, 0x2000
	s_nop 0
	global_load_lds_dwordx4 v90, s[30:31]
	v_mfma_f32_16x16x32_bf16 v[46:49], v[238:241], v[226:229], v[46:49]
	v_mfma_f32_16x16x32_bf16 v[42:45], v[242:245], v[226:229], v[42:45]
	v_mfma_f32_16x16x32_bf16 v[38:41], v[246:249], v[226:229], v[38:41]
	v_mfma_f32_16x16x32_bf16 v[34:37], v[250:253], v[226:229], v[34:37]
	ds_read_b128 v[226:229], v93 offset:4096
	ds_read_b128 v[156:159], v141 offset:4096
	s_add_i32 m0, s49, 0x4000
	s_nop 0
	global_load_lds_dwordx4 v92, s[30:31]
	v_mfma_f32_16x16x32_bf16 v[18:21], v[238:241], v[230:233], v[18:21]
	v_mfma_f32_16x16x32_bf16 v[22:25], v[242:245], v[230:233], v[22:25]
	v_mfma_f32_16x16x32_bf16 v[26:29], v[246:249], v[230:233], v[26:29]
	v_mfma_f32_16x16x32_bf16 v[30:33], v[250:253], v[230:233], v[30:33]
	ds_read_b128 v[230:233], v93 offset:6144
	ds_read_b128 v[160:163], v141 offset:6144
	s_add_i32 m0, s49, 0x6000
	s_nop 0
	global_load_lds_dwordx4 v94, s[30:31]
	v_mfma_f32_16x16x32_bf16 v[2:5], v[238:241], v[234:237], v[2:5]
	v_mfma_f32_16x16x32_bf16 v[6:9], v[242:245], v[234:237], v[6:9]
	v_mfma_f32_16x16x32_bf16 v[10:13], v[246:249], v[234:237], v[10:13]
	v_mfma_f32_16x16x32_bf16 v[14:17], v[250:253], v[234:237], v[14:17]
	ds_read_b128 v[234:237], v93 offset:8192
	s_add_i32 m0, s49, 0x8000
	s_nop 0
	global_load_lds_dwordx4 v96, s[30:31]
	s_waitcnt lgkmcnt(0)
	v_mfma_f32_16x16x32_bf16 v[78:81], v[142:145], v[218:221], v[78:81]
	v_mfma_f32_16x16x32_bf16 v[74:77], v[146:149], v[218:221], v[74:77]
	v_mfma_f32_16x16x32_bf16 v[70:73], v[156:159], v[218:221], v[70:73]
	v_mfma_f32_16x16x32_bf16 v[66:69], v[160:163], v[218:221], v[66:69]
	s_add_i32 s51, s51, 1
	s_and_b32 s54, s51, 7
	s_cmp_eq_u32 s54, 0
	s_cselect_b32 s44, s34, s35
	s_cselect_b32 s45, -1, 0
	v_lshl_add_u64 v[132:133], v[132:133], 0, s[44:45]
	global_load_dwordx2 v[202:203], v[132:133], off
	v_lshl_add_u64 v[180:181], v[132:133], 0, s[24:25]
	global_load_dwordx2 v[204:205], v[180:181], off
	v_mfma_f32_16x16x32_bf16 v[62:65], v[142:145], v[222:225], v[62:65]
	v_mfma_f32_16x16x32_bf16 v[58:61], v[146:149], v[222:225], v[58:61]
	v_mfma_f32_16x16x32_bf16 v[54:57], v[156:159], v[222:225], v[54:57]
	v_mfma_f32_16x16x32_bf16 v[50:53], v[160:163], v[222:225], v[50:53]
	v_lshl_add_u64 v[180:181], v[132:133], 0, s[26:27]
	global_load_dwordx2 v[206:207], v[180:181], off
	v_lshl_add_u64 v[180:181], v[132:133], 0, s[28:29]
	global_load_dwordx2 v[208:209], v[180:181], off
	v_mfma_f32_16x16x32_bf16 v[46:49], v[142:145], v[226:229], v[46:49]
	v_mfma_f32_16x16x32_bf16 v[42:45], v[146:149], v[226:229], v[42:45]
	v_mfma_f32_16x16x32_bf16 v[38:41], v[156:159], v[226:229], v[38:41]
	v_mfma_f32_16x16x32_bf16 v[34:37], v[160:163], v[226:229], v[34:37]
	v_lshl_add_u64 v[180:181], v[132:133], 0, s[36:37]
	global_load_dwordx2 v[210:211], v[180:181], off
	v_lshl_add_u64 v[180:181], v[132:133], 0, s[38:39]
	global_load_dwordx2 v[212:213], v[180:181], off
	v_mfma_f32_16x16x32_bf16 v[18:21], v[142:145], v[230:233], v[18:21]
	v_mfma_f32_16x16x32_bf16 v[22:25], v[146:149], v[230:233], v[22:25]
	v_mfma_f32_16x16x32_bf16 v[26:29], v[156:159], v[230:233], v[26:29]
	v_mfma_f32_16x16x32_bf16 v[30:33], v[160:163], v[230:233], v[30:33]
	v_lshl_add_u64 v[180:181], v[132:133], 0, s[40:41]
	global_load_dwordx2 v[214:215], v[180:181], off
	v_lshl_add_u64 v[180:181], v[132:133], 0, s[42:43]
	global_load_dwordx2 v[216:217], v[180:181], off
	v_mfma_f32_16x16x32_bf16 v[2:5], v[142:145], v[234:237], v[2:5]
	v_mfma_f32_16x16x32_bf16 v[6:9], v[146:149], v[234:237], v[6:9]
	v_mfma_f32_16x16x32_bf16 v[10:13], v[156:159], v[234:237], v[10:13]
	v_mfma_f32_16x16x32_bf16 v[14:17], v[160:163], v[234:237], v[14:17]
	s_waitcnt vmcnt(21)
	s_mov_b32 s49, s46
	s_mov_b32 s46, s47
	s_mov_b32 s47, s48
	s_mov_b32 s48, s49
	s_add_i32 s50, s50, 1
	s_waitcnt lgkmcnt(0)
	s_barrier
; #define MD_GLDS_A(buf, tau) do { _Pragma("unroll") for (int i = 0; i < 5; ++i) if (amask & (1u << i)) \
;         __builtin_amdgcn_global_load_lds((const unsigned*)((const char*)HIDp + aoff[i] + (size_t)((tau) & 7) * 128), (PG8_LAS unsigned*)(MD_SA(buf) + wid * 1024 + i * 8192), 16, 0, 0); } while (0)
; #define MD_B_ISSUE(sb, tau) do { const char* kb_ = Bb + (size_t)((tau) >> 3) * 512 + (size_t)((tau) & 7) * (64 * (size_t)RB); _Pragma("unroll") for (int j = 0; j < 8; ++j) { const char* p_ = kb_ + (size_t)j * RB; \
;         asm volatile("global_load_dwordx2 %0, %1, off" : "=&v"(sb[j]) : "v"(p_) : "memory"); } } while (0)
; #define MD_B_WAIT(sb, N) asm volatile("s_waitcnt vmcnt(%8)" : "+v"(sb[0]), "+v"(sb[1]), "+v"(sb[2]), "+v"(sb[3]), "+v"(sb[4]), "+v"(sb[5]), "+v"(sb[6]), "+v"(sb[7]) : "n"(N) : "memory")
; __device__ __forceinline__ void moe_down_stream(PG8_LAS unsigned char* lds, int e, int cb0, int slot0, int nv, const bf16_t* HIDp, const float* Wd, bf16_t* Y, const float* slot_w, const int* slot_dst) {
;     ...
;     f32x4 acc[DNM][4];
; #pragma unroll
;     for (int m = 0; m < DNM; ++m)
; #pragma unroll
;         for (int n = 0; n < 4; ++n) acc[m][n] = (f32x4){0.f, 0.f, 0.f, 0.f};
;     f32x2 s0[8], s1[8];
;     MD_GLDS_A(0, 0); MD_B_ISSUE(s0, 0); MD_B_ISSUE(s1, 1);
;     MD_B_WAIT(s0, 8); MD_B_WRITE(s0, 0); __builtin_amdgcn_sched_barrier(0); MD_B_ISSUE(s0, 2);
;     asm volatile("s_waitcnt vmcnt(16)" ::: "memory");
;     asm volatile("s_waitcnt lgkmcnt(0)" ::: "memory"); __builtin_amdgcn_s_barrier(); asm volatile("" ::: "memory");
; #pragma unroll 1
;     for (int t = 0; t < NT; t += 2) {
;         if (t + 2 < NT) MD_B_WAIT(s1, 8); else MD_B_WAIT(s1, 0);
;         MD_B_WRITE(s1, 1); __builtin_amdgcn_sched_barrier(0); MD_GLDS_A(1, t + 1); __builtin_amdgcn_sched_barrier(0);
;         if (t + 3 < NT) MD_B_ISSUE(s1, t + 3);
;         MD_COMPUTE(0);
;         MD_END(t + 3 >= NT);
;         if (t + 2 < NT) { MD_B_WAIT(s0, 8); MD_B_WRITE(s0, 0); __builtin_amdgcn_sched_barrier(0); MD_GLDS_A(0, t + 2); __builtin_amdgcn_sched_barrier(0); }
;         if (t + 4 < NT) MD_B_ISSUE(s0, t + 4);
;         MD_COMPUTE(1);
;         MD_END(t + 4 >= NT);
	v_cvt_pk_bf16_f32 v172, v98, v100
	v_cvt_pk_bf16_f32 v173, v102, v104
	v_cvt_pk_bf16_f32 v174, v106, v108
	v_cvt_pk_bf16_f32 v175, v110, v112
	v_cvt_pk_bf16_f32 v176, v99, v101
	v_cvt_pk_bf16_f32 v177, v103, v105
	v_cvt_pk_bf16_f32 v178, v107, v109
	v_cvt_pk_bf16_f32 v179, v111, v113
	ds_write_b128 v95, v[172:175] offset:0
	ds_write_b128 v95, v[176:179] offset:128
	v_add_u32_e32 v91, s46, v135
	v_add_u32_e32 v93, s46, v137
	ds_read_b128 v[238:241], v139 offset:19456
	ds_read_b128 v[242:245], v139 offset:21504
	ds_read_b128 v[246:249], v139 offset:23552
	ds_read_b128 v[250:253], v139 offset:25600
	ds_read_b128 v[218:221], v91 offset:0
	ds_read_b128 v[222:225], v91 offset:2048
	ds_read_b128 v[226:229], v91 offset:4096
	ds_read_b128 v[230:233], v91 offset:6144
	ds_read_b128 v[234:237], v91 offset:8192
	s_add_i32 s49, s48, s74
	s_add_i32 s52, s52, 1
	s_and_b32 s54, s52, 7
	s_cmp_eq_u32 s54, 0
	s_cselect_b32 s54, s53, s32
	s_cselect_b32 s55, -1, 0
	s_add_u32 s30, s30, s54
	s_addc_u32 s31, s31, s55
	s_waitcnt lgkmcnt(0)
	v_mfma_f32_16x16x32_bf16 v[78:81], v[238:241], v[218:221], v[78:81]
	v_mfma_f32_16x16x32_bf16 v[74:77], v[242:245], v[218:221], v[74:77]
	v_mfma_f32_16x16x32_bf16 v[70:73], v[246:249], v[218:221], v[70:73]
	v_mfma_f32_16x16x32_bf16 v[66:69], v[250:253], v[218:221], v[66:69]
	ds_read_b128 v[218:221], v93 offset:0
	ds_read_b128 v[142:145], v141 offset:19456
	s_mov_b32 m0, s49
	s_nop 0
	global_load_lds_dwordx4 v88, s[30:31]
	v_mfma_f32_16x16x32_bf16 v[62:65], v[238:241], v[222:225], v[62:65]
	v_mfma_f32_16x16x32_bf16 v[58:61], v[242:245], v[222:225], v[58:61]
	v_mfma_f32_16x16x32_bf16 v[54:57], v[246:249], v[222:225], v[54:57]
	v_mfma_f32_16x16x32_bf16 v[50:53], v[250:253], v[222:225], v[50:53]
	ds_read_b128 v[222:225], v93 offset:2048
	ds_read_b128 v[146:149], v141 offset:21504
	s_add_i32 m0, s49, 0x2000
	s_nop 0
	global_load_lds_dwordx4 v90, s[30:31]
	v_mfma_f32_16x16x32_bf16 v[46:49], v[238:241], v[226:229], v[46:49]
	v_mfma_f32_16x16x32_bf16 v[42:45], v[242:245], v[226:229], v[42:45]
	v_mfma_f32_16x16x32_bf16 v[38:41], v[246:249], v[226:229], v[38:41]
	v_mfma_f32_16x16x32_bf16 v[34:37], v[250:253], v[226:229], v[34:37]
	ds_read_b128 v[226:229], v93 offset:4096
	ds_read_b128 v[156:159], v141 offset:23552
	s_add_i32 m0, s49, 0x4000
	s_nop 0
	global_load_lds_dwordx4 v92, s[30:31]
	v_mfma_f32_16x16x32_bf16 v[18:21], v[238:241], v[230:233], v[18:21]
	v_mfma_f32_16x16x32_bf16 v[22:25], v[242:245], v[230:233], v[22:25]
	v_mfma_f32_16x16x32_bf16 v[26:29], v[246:249], v[230:233], v[26:29]
	v_mfma_f32_16x16x32_bf16 v[30:33], v[250:253], v[230:233], v[30:33]
	ds_read_b128 v[230:233], v93 offset:6144
	ds_read_b128 v[160:163], v141 offset:25600
	s_add_i32 m0, s49, 0x6000
	s_nop 0
	global_load_lds_dwordx4 v94, s[30:31]
	v_mfma_f32_16x16x32_bf16 v[2:5], v[238:241], v[234:237], v[2:5]
	v_mfma_f32_16x16x32_bf16 v[6:9], v[242:245], v[234:237], v[6:9]
	v_mfma_f32_16x16x32_bf16 v[10:13], v[246:249], v[234:237], v[10:13]
	v_mfma_f32_16x16x32_bf16 v[14:17], v[250:253], v[234:237], v[14:17]
	ds_read_b128 v[234:237], v93 offset:8192
	s_add_i32 m0, s49, 0x8000
	s_nop 0
	global_load_lds_dwordx4 v96, s[30:31]
	s_waitcnt lgkmcnt(0)
	v_mfma_f32_16x16x32_bf16 v[78:81], v[142:145], v[218:221], v[78:81]
	v_mfma_f32_16x16x32_bf16 v[74:77], v[146:149], v[218:221], v[74:77]
	v_mfma_f32_16x16x32_bf16 v[70:73], v[156:159], v[218:221], v[70:73]
	v_mfma_f32_16x16x32_bf16 v[66:69], v[160:163], v[218:221], v[66:69]
	s_add_i32 s51, s51, 1
	s_and_b32 s54, s51, 7
	s_cmp_eq_u32 s54, 0
	s_cselect_b32 s44, s34, s35
	s_cselect_b32 s45, -1, 0
	v_lshl_add_u64 v[132:133], v[132:133], 0, s[44:45]
	global_load_dwordx2 v[98:99], v[132:133], off
	v_lshl_add_u64 v[180:181], v[132:133], 0, s[24:25]
	global_load_dwordx2 v[100:101], v[180:181], off
	v_mfma_f32_16x16x32_bf16 v[62:65], v[142:145], v[222:225], v[62:65]
	v_mfma_f32_16x16x32_bf16 v[58:61], v[146:149], v[222:225], v[58:61]
	v_mfma_f32_16x16x32_bf16 v[54:57], v[156:159], v[222:225], v[54:57]
	v_mfma_f32_16x16x32_bf16 v[50:53], v[160:163], v[222:225], v[50:53]
	v_lshl_add_u64 v[180:181], v[132:133], 0, s[26:27]
	global_load_dwordx2 v[102:103], v[180:181], off
	v_lshl_add_u64 v[180:181], v[132:133], 0, s[28:29]
	global_load_dwordx2 v[104:105], v[180:181], off
	v_mfma_f32_16x16x32_bf16 v[46:49], v[142:145], v[226:229], v[46:49]
	v_mfma_f32_16x16x32_bf16 v[42:45], v[146:149], v[226:229], v[42:45]
	v_mfma_f32_16x16x32_bf16 v[38:41], v[156:159], v[226:229], v[38:41]
	v_mfma_f32_16x16x32_bf16 v[34:37], v[160:163], v[226:229], v[34:37]
	v_lshl_add_u64 v[180:181], v[132:133], 0, s[36:37]
	global_load_dwordx2 v[106:107], v[180:181], off
	v_lshl_add_u64 v[180:181], v[132:133], 0, s[38:39]
	global_load_dwordx2 v[108:109], v[180:181], off
	v_mfma_f32_16x16x32_bf16 v[18:21], v[142:145], v[230:233], v[18:21]
	v_mfma_f32_16x16x32_bf16 v[22:25], v[146:149], v[230:233], v[22:25]
	v_mfma_f32_16x16x32_bf16 v[26:29], v[156:159], v[230:233], v[26:29]
	v_mfma_f32_16x16x32_bf16 v[30:33], v[160:163], v[230:233], v[30:33]
	v_lshl_add_u64 v[180:181], v[132:133], 0, s[40:41]
	global_load_dwordx2 v[110:111], v[180:181], off
	v_lshl_add_u64 v[180:181], v[132:133], 0, s[42:43]
	global_load_dwordx2 v[112:113], v[180:181], off
	v_mfma_f32_16x16x32_bf16 v[2:5], v[142:145], v[234:237], v[2:5]
	v_mfma_f32_16x16x32_bf16 v[6:9], v[146:149], v[234:237], v[6:9]
	v_mfma_f32_16x16x32_bf16 v[10:13], v[156:159], v[234:237], v[10:13]
	v_mfma_f32_16x16x32_bf16 v[14:17], v[160:163], v[234:237], v[14:17]
	s_waitcnt vmcnt(21)
	s_mov_b32 s49, s46
	s_mov_b32 s46, s47
	s_mov_b32 s47, s48
	s_mov_b32 s48, s49
	s_add_i32 s50, s50, 1
	s_waitcnt lgkmcnt(0)
	s_barrier
; #define PG8_LAS __attribute__((address_space(3)))
; __device__ __forceinline__ unsigned cvtpk(float lo, float hi) { f32x2 v = {lo, hi}; bf16x2_t b = __builtin_convertvector(v, bf16x2_t); return __builtin_bit_cast(unsigned, b); }
; __device__ __forceinline__ void moe_down_stream(PG8_LAS unsigned char* lds, int e, int cb0, int slot0, int nv, const bf16_t* HIDp, const float* Wd, bf16_t* Y, const float* slot_w, const int* slot_dst) {
;     ...
;         if (((t + 1) & 7) == 7) {
;             const int cb = cb0 + ((t + 1) >> 3);
; #pragma unroll
;             for (int m = 0; m < DNM; ++m) {
;                 const float w_ = lw[4 * (16 * m + fr) + wr];
; #pragma unroll
;                 for (int p = 0; p < 2; ++p) { const f32x4 v0 = acc[m][2 * p] * w_, v1 = acc[m][2 * p + 1] * w_; u32x4 w; w.x = cvtpk(v0[0], v0[1]); w.y = cvtpk(v0[2], v0[3]); w.z = cvtpk(v1[0], v1[1]); w.w = cvtpk(v1[2], v1[3]);
;                     *(PG8_LAS u32x4*)(stg + fr * 128 + (((4 * p + fq) ^ (fr & 7)) * 16)) = w; }
; #pragma unroll
;                 for (int hh = 0; hh < 2; ++hh) { const int r = (lane >> 3) + 8 * hh, cc = lane & 7; const u32x4 d = *(const PG8_LAS u32x4*)(stg + r * 128 + ((cc ^ (r & 7)) * 16)); const int dst_ = ldst[4 * (16 * m + r) + wr];
;                     if (dst_ >= 0) *(u32x4*)(Y + (size_t)dst_ * D + 128 * cb + 64 * wc + 8 * cc) = d; }
; #pragma unroll
;                 for (int n = 0; n < 4; ++n) acc[m][n] = (f32x4){0.f, 0.f, 0.f, 0.f}; } }
	s_and_b32 s54, s50, 7
	s_cmp_lg_u32 s54, 0
	s_cbranch_scc1 .Lmd_noepi_X
	s_add_i32 s54, s48, s74
	v_add_u32_e32 v164, s54, v84
	v_add_u32_e32 v165, s54, v85
	ds_read_b32 v150, v82 offset:0
	ds_read_b32 v151, v83 offset:0
	ds_read_b32 v166, v83 offset:128
	s_waitcnt lgkmcnt(2)
	v_mul_f32_e32 v78, v150, v78
	v_mul_f32_e32 v79, v150, v79
	v_mul_f32_e32 v80, v150, v80
	v_mul_f32_e32 v81, v150, v81
	v_mul_f32_e32 v74, v150, v74
	v_mul_f32_e32 v75, v150, v75
	v_mul_f32_e32 v76, v150, v76
	v_mul_f32_e32 v77, v150, v77
	v_cvt_pk_bf16_f32 v182, v78, v79
	v_cvt_pk_bf16_f32 v183, v80, v81
	v_cvt_pk_bf16_f32 v184, v74, v75
	v_cvt_pk_bf16_f32 v185, v76, v77
	ds_write_b128 v164, v[182:185]
	v_mul_f32_e32 v70, v150, v70
	v_mul_f32_e32 v71, v150, v71
	v_mul_f32_e32 v72, v150, v72
	v_mul_f32_e32 v73, v150, v73
	v_mul_f32_e32 v66, v150, v66
	v_mul_f32_e32 v67, v150, v67
	v_mul_f32_e32 v68, v150, v68
	v_mul_f32_e32 v69, v150, v69
	v_cvt_pk_bf16_f32 v182, v70, v71
	v_cvt_pk_bf16_f32 v183, v72, v73
	v_cvt_pk_bf16_f32 v184, v66, v67
	v_cvt_pk_bf16_f32 v185, v68, v69
	v_xor_b32_e32 v167, 64, v164
	ds_write_b128 v167, v[182:185]
	v_mov_b32_e32 v78, 0
	v_mov_b32_e32 v74, 0
	v_mov_b32_e32 v70, 0
	v_mov_b32_e32 v66, 0
	v_mov_b32_e32 v79, 0
	v_mov_b32_e32 v75, 0
	v_mov_b32_e32 v71, 0
	v_mov_b32_e32 v67, 0
	v_mov_b32_e32 v80, 0
	v_mov_b32_e32 v76, 0
	v_mov_b32_e32 v72, 0
	v_mov_b32_e32 v68, 0
	v_mov_b32_e32 v81, 0
	v_mov_b32_e32 v77, 0
	v_mov_b32_e32 v73, 0
	v_mov_b32_e32 v69, 0
	ds_read_b128 v[182:185], v165 offset:0
	v_cmp_lt_i32_e32 vcc, -1, v151
	v_lshlrev_b32_e32 v148, 13, v151
	v_mov_b32_e32 v149, 0
	v_lshl_add_u64 v[148:149], v[148:149], 0, v[86:87]
	v_cndmask_b32_e32 v148, v168, v148, vcc
	v_cndmask_b32_e32 v149, v169, v149, vcc
	s_waitcnt lgkmcnt(0)
	global_store_dwordx4 v[148:149], v[182:185], off
	ds_read_b128 v[182:185], v165 offset:8192
	v_cmp_lt_i32_e32 vcc, -1, v166
	v_lshlrev_b32_e32 v148, 13, v166
	v_mov_b32_e32 v149, 0
	v_lshl_add_u64 v[148:149], v[148:149], 0, v[86:87]
	v_cndmask_b32_e32 v148, v168, v148, vcc
	v_cndmask_b32_e32 v149, v169, v149, vcc
	s_waitcnt lgkmcnt(0)
	global_store_dwordx4 v[148:149], v[182:185], off
	ds_read_b32 v150, v82 offset:256
	ds_read_b32 v151, v83 offset:256
	ds_read_b32 v166, v83 offset:384
	s_waitcnt lgkmcnt(2)
	v_mul_f32_e32 v62, v150, v62
	v_mul_f32_e32 v63, v150, v63
	v_mul_f32_e32 v64, v150, v64
	v_mul_f32_e32 v65, v150, v65
	v_mul_f32_e32 v58, v150, v58
	v_mul_f32_e32 v59, v150, v59
	v_mul_f32_e32 v60, v150, v60
	v_mul_f32_e32 v61, v150, v61
	v_cvt_pk_bf16_f32 v182, v62, v63
	v_cvt_pk_bf16_f32 v183, v64, v65
	v_cvt_pk_bf16_f32 v184, v58, v59
	v_cvt_pk_bf16_f32 v185, v60, v61
	ds_write_b128 v164, v[182:185]
	v_mul_f32_e32 v54, v150, v54
	v_mul_f32_e32 v55, v150, v55
	v_mul_f32_e32 v56, v150, v56
	v_mul_f32_e32 v57, v150, v57
	v_mul_f32_e32 v50, v150, v50
	v_mul_f32_e32 v51, v150, v51
	v_mul_f32_e32 v52, v150, v52
	v_mul_f32_e32 v53, v150, v53
	v_cvt_pk_bf16_f32 v182, v54, v55
	v_cvt_pk_bf16_f32 v183, v56, v57
	v_cvt_pk_bf16_f32 v184, v50, v51
	v_cvt_pk_bf16_f32 v185, v52, v53
	v_xor_b32_e32 v167, 64, v164
	ds_write_b128 v167, v[182:185]
	v_mov_b32_e32 v62, 0
	v_mov_b32_e32 v58, 0
	v_mov_b32_e32 v54, 0
	v_mov_b32_e32 v50, 0
	v_mov_b32_e32 v63, 0
	v_mov_b32_e32 v59, 0
	v_mov_b32_e32 v55, 0
	v_mov_b32_e32 v51, 0
	v_mov_b32_e32 v64, 0
	v_mov_b32_e32 v60, 0
	v_mov_b32_e32 v56, 0
	v_mov_b32_e32 v52, 0
	v_mov_b32_e32 v65, 0
	v_mov_b32_e32 v61, 0
	v_mov_b32_e32 v57, 0
	v_mov_b32_e32 v53, 0
	ds_read_b128 v[182:185], v165 offset:0
	v_cmp_lt_i32_e32 vcc, -1, v151
	v_lshlrev_b32_e32 v148, 13, v151
	v_mov_b32_e32 v149, 0
	v_lshl_add_u64 v[148:149], v[148:149], 0, v[86:87]
	v_cndmask_b32_e32 v148, v168, v148, vcc
	v_cndmask_b32_e32 v149, v169, v149, vcc
	s_waitcnt lgkmcnt(0)
	global_store_dwordx4 v[148:149], v[182:185], off
	ds_read_b128 v[182:185], v165 offset:8192
	v_cmp_lt_i32_e32 vcc, -1, v166
	v_lshlrev_b32_e32 v148, 13, v166
	v_mov_b32_e32 v149, 0
	v_lshl_add_u64 v[148:149], v[148:149], 0, v[86:87]
	v_cndmask_b32_e32 v148, v168, v148, vcc
	v_cndmask_b32_e32 v149, v169, v149, vcc
	s_waitcnt lgkmcnt(0)
	global_store_dwordx4 v[148:149], v[182:185], off
	ds_read_b32 v150, v82 offset:512
	ds_read_b32 v151, v83 offset:512
	ds_read_b32 v166, v83 offset:640
	s_waitcnt lgkmcnt(2)
	v_mul_f32_e32 v46, v150, v46
	v_mul_f32_e32 v47, v150, v47
	v_mul_f32_e32 v48, v150, v48
	v_mul_f32_e32 v49, v150, v49
	v_mul_f32_e32 v42, v150, v42
	v_mul_f32_e32 v43, v150, v43
	v_mul_f32_e32 v44, v150, v44
	v_mul_f32_e32 v45, v150, v45
	v_cvt_pk_bf16_f32 v182, v46, v47
	v_cvt_pk_bf16_f32 v183, v48, v49
	v_cvt_pk_bf16_f32 v184, v42, v43
	v_cvt_pk_bf16_f32 v185, v44, v45
	ds_write_b128 v164, v[182:185]
	v_mul_f32_e32 v38, v150, v38
	v_mul_f32_e32 v39, v150, v39
	v_mul_f32_e32 v40, v150, v40
	v_mul_f32_e32 v41, v150, v41
	v_mul_f32_e32 v34, v150, v34
	v_mul_f32_e32 v35, v150, v35
	v_mul_f32_e32 v36, v150, v36
	v_mul_f32_e32 v37, v150, v37
	v_cvt_pk_bf16_f32 v182, v38, v39
	v_cvt_pk_bf16_f32 v183, v40, v41
	v_cvt_pk_bf16_f32 v184, v34, v35
	v_cvt_pk_bf16_f32 v185, v36, v37
	v_xor_b32_e32 v167, 64, v164
	ds_write_b128 v167, v[182:185]
	v_mov_b32_e32 v46, 0
	v_mov_b32_e32 v42, 0
	v_mov_b32_e32 v38, 0
	v_mov_b32_e32 v34, 0
	v_mov_b32_e32 v47, 0
	v_mov_b32_e32 v43, 0
	v_mov_b32_e32 v39, 0
	v_mov_b32_e32 v35, 0
	v_mov_b32_e32 v48, 0
	v_mov_b32_e32 v44, 0
	v_mov_b32_e32 v40, 0
	v_mov_b32_e32 v36, 0
	v_mov_b32_e32 v49, 0
	v_mov_b32_e32 v45, 0
	v_mov_b32_e32 v41, 0
	v_mov_b32_e32 v37, 0
	ds_read_b128 v[182:185], v165 offset:0
	v_cmp_lt_i32_e32 vcc, -1, v151
	v_lshlrev_b32_e32 v148, 13, v151
	v_mov_b32_e32 v149, 0
	v_lshl_add_u64 v[148:149], v[148:149], 0, v[86:87]
	v_cndmask_b32_e32 v148, v168, v148, vcc
	v_cndmask_b32_e32 v149, v169, v149, vcc
	s_waitcnt lgkmcnt(0)
; #define PG8_LAS __attribute__((address_space(3)))
; __device__ __forceinline__ unsigned cvtpk(float lo, float hi) { f32x2 v = {lo, hi}; bf16x2_t b = __builtin_convertvector(v, bf16x2_t); return __builtin_bit_cast(unsigned, b); }
; __device__ __forceinline__ void moe_down_stream(PG8_LAS unsigned char* lds, int e, int cb0, int slot0, int nv, const bf16_t* HIDp, const float* Wd, bf16_t* Y, const float* slot_w, const int* slot_dst) {
;     ...
;         if (((t + 1) & 7) == 7) {
;             const int cb = cb0 + ((t + 1) >> 3);
; #pragma unroll
;             for (int m = 0; m < DNM; ++m) {
;                 const float w_ = lw[4 * (16 * m + fr) + wr];
; #pragma unroll
;                 for (int p = 0; p < 2; ++p) { const f32x4 v0 = acc[m][2 * p] * w_, v1 = acc[m][2 * p + 1] * w_; u32x4 w; w.x = cvtpk(v0[0], v0[1]); w.y = cvtpk(v0[2], v0[3]); w.z = cvtpk(v1[0], v1[1]); w.w = cvtpk(v1[2], v1[3]);
;                     *(PG8_LAS u32x4*)(stg + fr * 128 + (((4 * p + fq) ^ (fr & 7)) * 16)) = w; }
; #pragma unroll
;                 for (int hh = 0; hh < 2; ++hh) { const int r = (lane >> 3) + 8 * hh, cc = lane & 7; const u32x4 d = *(const PG8_LAS u32x4*)(stg + r * 128 + ((cc ^ (r & 7)) * 16)); const int dst_ = ldst[4 * (16 * m + r) + wr];
;                     if (dst_ >= 0) *(u32x4*)(Y + (size_t)dst_ * D + 128 * cb + 64 * wc + 8 * cc) = d; }
; #pragma unroll
;                 for (int n = 0; n < 4; ++n) acc[m][n] = (f32x4){0.f, 0.f, 0.f, 0.f}; } }
	global_store_dwordx4 v[148:149], v[182:185], off
	ds_read_b128 v[182:185], v165 offset:8192
	v_cmp_lt_i32_e32 vcc, -1, v166
	v_lshlrev_b32_e32 v148, 13, v166
	v_mov_b32_e32 v149, 0
	v_lshl_add_u64 v[148:149], v[148:149], 0, v[86:87]
	v_cndmask_b32_e32 v148, v168, v148, vcc
	v_cndmask_b32_e32 v149, v169, v149, vcc
	s_waitcnt lgkmcnt(0)
	global_store_dwordx4 v[148:149], v[182:185], off
	ds_read_b32 v150, v82 offset:768
	ds_read_b32 v151, v83 offset:768
	ds_read_b32 v166, v83 offset:896
	s_waitcnt lgkmcnt(2)
	v_mul_f32_e32 v18, v150, v18
	v_mul_f32_e32 v19, v150, v19
	v_mul_f32_e32 v20, v150, v20
	v_mul_f32_e32 v21, v150, v21
	v_mul_f32_e32 v22, v150, v22
	v_mul_f32_e32 v23, v150, v23
	v_mul_f32_e32 v24, v150, v24
	v_mul_f32_e32 v25, v150, v25
	v_cvt_pk_bf16_f32 v182, v18, v19
	v_cvt_pk_bf16_f32 v183, v20, v21
	v_cvt_pk_bf16_f32 v184, v22, v23
	v_cvt_pk_bf16_f32 v185, v24, v25
	ds_write_b128 v164, v[182:185]
	v_mul_f32_e32 v26, v150, v26
	v_mul_f32_e32 v27, v150, v27
	v_mul_f32_e32 v28, v150, v28
	v_mul_f32_e32 v29, v150, v29
	v_mul_f32_e32 v30, v150, v30
	v_mul_f32_e32 v31, v150, v31
	v_mul_f32_e32 v32, v150, v32
	v_mul_f32_e32 v33, v150, v33
	v_cvt_pk_bf16_f32 v182, v26, v27
	v_cvt_pk_bf16_f32 v183, v28, v29
	v_cvt_pk_bf16_f32 v184, v30, v31
	v_cvt_pk_bf16_f32 v185, v32, v33
	v_xor_b32_e32 v167, 64, v164
	ds_write_b128 v167, v[182:185]
	v_mov_b32_e32 v18, 0
	v_mov_b32_e32 v22, 0
	v_mov_b32_e32 v26, 0
	v_mov_b32_e32 v30, 0
	v_mov_b32_e32 v19, 0
	v_mov_b32_e32 v23, 0
	v_mov_b32_e32 v27, 0
	v_mov_b32_e32 v31, 0
	v_mov_b32_e32 v20, 0
	v_mov_b32_e32 v24, 0
	v_mov_b32_e32 v28, 0
	v_mov_b32_e32 v32, 0
	v_mov_b32_e32 v21, 0
	v_mov_b32_e32 v25, 0
	v_mov_b32_e32 v29, 0
	v_mov_b32_e32 v33, 0
	ds_read_b128 v[182:185], v165 offset:0
	v_cmp_lt_i32_e32 vcc, -1, v151
	v_lshlrev_b32_e32 v148, 13, v151
	v_mov_b32_e32 v149, 0
	v_lshl_add_u64 v[148:149], v[148:149], 0, v[86:87]
	v_cndmask_b32_e32 v148, v168, v148, vcc
	v_cndmask_b32_e32 v149, v169, v149, vcc
	s_waitcnt lgkmcnt(0)
	global_store_dwordx4 v[148:149], v[182:185], off
	ds_read_b128 v[182:185], v165 offset:8192
	v_cmp_lt_i32_e32 vcc, -1, v166
	v_lshlrev_b32_e32 v148, 13, v166
	v_mov_b32_e32 v149, 0
	v_lshl_add_u64 v[148:149], v[148:149], 0, v[86:87]
	v_cndmask_b32_e32 v148, v168, v148, vcc
	v_cndmask_b32_e32 v149, v169, v149, vcc
	s_waitcnt lgkmcnt(0)
	global_store_dwordx4 v[148:149], v[182:185], off
	ds_read_b32 v150, v82 offset:1024
	ds_read_b32 v151, v83 offset:1024
	ds_read_b32 v166, v83 offset:1152
	s_waitcnt lgkmcnt(2)
	v_mul_f32_e32 v2, v150, v2
	v_mul_f32_e32 v3, v150, v3
	v_mul_f32_e32 v4, v150, v4
	v_mul_f32_e32 v5, v150, v5
	v_mul_f32_e32 v6, v150, v6
	v_mul_f32_e32 v7, v150, v7
	v_mul_f32_e32 v8, v150, v8
	v_mul_f32_e32 v9, v150, v9
	v_cvt_pk_bf16_f32 v182, v2, v3
	v_cvt_pk_bf16_f32 v183, v4, v5
	v_cvt_pk_bf16_f32 v184, v6, v7
	v_cvt_pk_bf16_f32 v185, v8, v9
	ds_write_b128 v164, v[182:185]
	v_mul_f32_e32 v10, v150, v10
	v_mul_f32_e32 v11, v150, v11
	v_mul_f32_e32 v12, v150, v12
	v_mul_f32_e32 v13, v150, v13
	v_mul_f32_e32 v14, v150, v14
	v_mul_f32_e32 v15, v150, v15
	v_mul_f32_e32 v16, v150, v16
	v_mul_f32_e32 v17, v150, v17
	v_cvt_pk_bf16_f32 v182, v10, v11
	v_cvt_pk_bf16_f32 v183, v12, v13
	v_cvt_pk_bf16_f32 v184, v14, v15
	v_cvt_pk_bf16_f32 v185, v16, v17
	v_xor_b32_e32 v167, 64, v164
	ds_write_b128 v167, v[182:185]
	v_mov_b32_e32 v2, 0
	v_mov_b32_e32 v6, 0
	v_mov_b32_e32 v10, 0
	v_mov_b32_e32 v14, 0
	v_mov_b32_e32 v3, 0
	v_mov_b32_e32 v7, 0
	v_mov_b32_e32 v11, 0
	v_mov_b32_e32 v15, 0
	v_mov_b32_e32 v4, 0
	v_mov_b32_e32 v8, 0
	v_mov_b32_e32 v12, 0
	v_mov_b32_e32 v16, 0
	v_mov_b32_e32 v5, 0
	v_mov_b32_e32 v9, 0
	v_mov_b32_e32 v13, 0
	v_mov_b32_e32 v17, 0
	ds_read_b128 v[182:185], v165 offset:0
	v_cmp_lt_i32_e32 vcc, -1, v151
	v_lshlrev_b32_e32 v148, 13, v151
	v_mov_b32_e32 v149, 0
	v_lshl_add_u64 v[148:149], v[148:149], 0, v[86:87]
	v_cndmask_b32_e32 v148, v168, v148, vcc
	v_cndmask_b32_e32 v149, v169, v149, vcc
	s_waitcnt lgkmcnt(0)
	global_store_dwordx4 v[148:149], v[182:185], off
	ds_read_b128 v[182:185], v165 offset:8192
	v_cmp_lt_i32_e32 vcc, -1, v166
	v_lshlrev_b32_e32 v148, 13, v166
	v_mov_b32_e32 v149, 0
	v_lshl_add_u64 v[148:149], v[148:149], 0, v[86:87]
	v_cndmask_b32_e32 v148, v168, v148, vcc
	v_cndmask_b32_e32 v149, v169, v149, vcc
	s_waitcnt lgkmcnt(0)
	global_store_dwordx4 v[148:149], v[182:185], off
	v_add_co_u32_e32 v86, vcc, 0x400, v86
	s_nop 1
	v_addc_co_u32_e32 v87, vcc, 0, v87, vcc
	s_waitcnt lgkmcnt(0)
; #define MD_GLDS_A(buf, tau) do { _Pragma("unroll") for (int i = 0; i < 5; ++i) if (amask & (1u << i)) \
;         __builtin_amdgcn_global_load_lds((const unsigned*)((const char*)HIDp + aoff[i] + (size_t)((tau) & 7) * 128), (PG8_LAS unsigned*)(MD_SA(buf) + wid * 1024 + i * 8192), 16, 0, 0); } while (0)
; #define MD_B_ISSUE(sb, tau) do { const char* kb_ = Bb + (size_t)((tau) >> 3) * 512 + (size_t)((tau) & 7) * (64 * (size_t)RB); _Pragma("unroll") for (int j = 0; j < 8; ++j) { const char* p_ = kb_ + (size_t)j * RB; \
;         asm volatile("global_load_dwordx2 %0, %1, off" : "=&v"(sb[j]) : "v"(p_) : "memory"); } } while (0)
; #define MD_B_WAIT(sb, N) asm volatile("s_waitcnt vmcnt(%8)" : "+v"(sb[0]), "+v"(sb[1]), "+v"(sb[2]), "+v"(sb[3]), "+v"(sb[4]), "+v"(sb[5]), "+v"(sb[6]), "+v"(sb[7]) : "n"(N) : "memory")
; #define MD_END(last) do { if (last) asm volatile("s_waitcnt vmcnt(0)" ::: "memory"); else asm volatile("s_waitcnt vmcnt(8)" ::: "memory"); \
;         asm volatile("s_waitcnt lgkmcnt(0)" ::: "memory"); __builtin_amdgcn_s_barrier(); asm volatile("" ::: "memory"); } while (0)
; __device__ __forceinline__ void moe_down_stream(PG8_LAS unsigned char* lds, int e, int cb0, int slot0, int nv, const bf16_t* HIDp, const float* Wd, bf16_t* Y, const float* slot_w, const int* slot_dst) {
;     ...
;     for (int t = 0; t < NT; t += 2) {
;         if (t + 2 < NT) MD_B_WAIT(s1, 8); else MD_B_WAIT(s1, 0);
;         MD_B_WRITE(s1, 1); __builtin_amdgcn_sched_barrier(0); MD_GLDS_A(1, t + 1); __builtin_amdgcn_sched_barrier(0);
;         if (t + 3 < NT) MD_B_ISSUE(s1, t + 3);
;         MD_COMPUTE(0);
;         MD_END(t + 3 >= NT);
;         if (t + 2 < NT) { MD_B_WAIT(s0, 8); MD_B_WRITE(s0, 0); __builtin_amdgcn_sched_barrier(0); MD_GLDS_A(0, t + 2); __builtin_amdgcn_sched_barrier(0); }
;         if (t + 4 < NT) MD_B_ISSUE(s0, t + 4);
;         MD_COMPUTE(1);
;         MD_END(t + 4 >= NT);
.Lmd_noepi_X:
	s_sub_u32 s56, s56, 1
	s_cmp_lg_u32 s56, 0
	s_cbranch_scc1 .Lmd_loop_X
	v_cvt_pk_bf16_f32 v172, v114, v116
	v_cvt_pk_bf16_f32 v173, v118, v120
	v_cvt_pk_bf16_f32 v174, v122, v124
	v_cvt_pk_bf16_f32 v175, v126, v128
	v_cvt_pk_bf16_f32 v176, v115, v117
	v_cvt_pk_bf16_f32 v177, v119, v121
	v_cvt_pk_bf16_f32 v178, v123, v125
	v_cvt_pk_bf16_f32 v179, v127, v129
	ds_write_b128 v95, v[172:175] offset:19456
	ds_write_b128 v95, v[176:179] offset:19584
	v_add_u32_e32 v91, s46, v135
	v_add_u32_e32 v93, s46, v137
	ds_read_b128 v[238:241], v139 offset:0
	ds_read_b128 v[242:245], v139 offset:2048
	ds_read_b128 v[246:249], v139 offset:4096
	ds_read_b128 v[250:253], v139 offset:6144
	ds_read_b128 v[218:221], v91 offset:0
	ds_read_b128 v[222:225], v91 offset:2048
	ds_read_b128 v[226:229], v91 offset:4096
	ds_read_b128 v[230:233], v91 offset:6144
	ds_read_b128 v[234:237], v91 offset:8192
	s_add_i32 s49, s48, s74
	s_add_i32 s52, s52, 1
	s_and_b32 s54, s52, 7
	s_cmp_eq_u32 s54, 0
	s_cselect_b32 s54, s53, s32
	s_cselect_b32 s55, -1, 0
	s_add_u32 s30, s30, s54
	s_addc_u32 s31, s31, s55
	s_waitcnt lgkmcnt(0)
	v_mfma_f32_16x16x32_bf16 v[78:81], v[238:241], v[218:221], v[78:81]
	v_mfma_f32_16x16x32_bf16 v[74:77], v[242:245], v[218:221], v[74:77]
	v_mfma_f32_16x16x32_bf16 v[70:73], v[246:249], v[218:221], v[70:73]
	v_mfma_f32_16x16x32_bf16 v[66:69], v[250:253], v[218:221], v[66:69]
	ds_read_b128 v[218:221], v93 offset:0
	ds_read_b128 v[142:145], v141 offset:0
	s_mov_b32 m0, s49
	s_nop 0
	global_load_lds_dwordx4 v88, s[30:31]
	v_mfma_f32_16x16x32_bf16 v[62:65], v[238:241], v[222:225], v[62:65]
	v_mfma_f32_16x16x32_bf16 v[58:61], v[242:245], v[222:225], v[58:61]
	v_mfma_f32_16x16x32_bf16 v[54:57], v[246:249], v[222:225], v[54:57]
	v_mfma_f32_16x16x32_bf16 v[50:53], v[250:253], v[222:225], v[50:53]
	ds_read_b128 v[222:225], v93 offset:2048
	ds_read_b128 v[146:149], v141 offset:2048
	s_add_i32 m0, s49, 0x2000
	s_nop 0
	global_load_lds_dwordx4 v90, s[30:31]
	v_mfma_f32_16x16x32_bf16 v[46:49], v[238:241], v[226:229], v[46:49]
	v_mfma_f32_16x16x32_bf16 v[42:45], v[242:245], v[226:229], v[42:45]
	v_mfma_f32_16x16x32_bf16 v[38:41], v[246:249], v[226:229], v[38:41]
	v_mfma_f32_16x16x32_bf16 v[34:37], v[250:253], v[226:229], v[34:37]
	ds_read_b128 v[226:229], v93 offset:4096
	ds_read_b128 v[156:159], v141 offset:4096
	s_add_i32 m0, s49, 0x4000
	s_nop 0
	global_load_lds_dwordx4 v92, s[30:31]
	v_mfma_f32_16x16x32_bf16 v[18:21], v[238:241], v[230:233], v[18:21]
	v_mfma_f32_16x16x32_bf16 v[22:25], v[242:245], v[230:233], v[22:25]
	v_mfma_f32_16x16x32_bf16 v[26:29], v[246:249], v[230:233], v[26:29]
	v_mfma_f32_16x16x32_bf16 v[30:33], v[250:253], v[230:233], v[30:33]
	ds_read_b128 v[230:233], v93 offset:6144
	ds_read_b128 v[160:163], v141 offset:6144
	s_add_i32 m0, s49, 0x6000
	s_nop 0
	global_load_lds_dwordx4 v94, s[30:31]
	v_mfma_f32_16x16x32_bf16 v[2:5], v[238:241], v[234:237], v[2:5]
	v_mfma_f32_16x16x32_bf16 v[6:9], v[242:245], v[234:237], v[6:9]
	v_mfma_f32_16x16x32_bf16 v[10:13], v[246:249], v[234:237], v[10:13]
	v_mfma_f32_16x16x32_bf16 v[14:17], v[250:253], v[234:237], v[14:17]
	ds_read_b128 v[234:237], v93 offset:8192
	s_add_i32 m0, s49, 0x8000
	s_nop 0
	global_load_lds_dwordx4 v96, s[30:31]
	s_waitcnt lgkmcnt(0)
	v_mfma_f32_16x16x32_bf16 v[78:81], v[142:145], v[218:221], v[78:81]
	v_mfma_f32_16x16x32_bf16 v[74:77], v[146:149], v[218:221], v[74:77]
	v_mfma_f32_16x16x32_bf16 v[70:73], v[156:159], v[218:221], v[70:73]
	v_mfma_f32_16x16x32_bf16 v[66:69], v[160:163], v[218:221], v[66:69]
	s_add_i32 s51, s51, 1
	s_and_b32 s54, s51, 7
	s_cmp_eq_u32 s54, 0
	s_cselect_b32 s44, s34, s35
	s_cselect_b32 s45, -1, 0
	v_lshl_add_u64 v[132:133], v[132:133], 0, s[44:45]
	global_load_dwordx2 v[114:115], v[132:133], off
	v_lshl_add_u64 v[180:181], v[132:133], 0, s[24:25]
	global_load_dwordx2 v[116:117], v[180:181], off
	v_mfma_f32_16x16x32_bf16 v[62:65], v[142:145], v[222:225], v[62:65]
	v_mfma_f32_16x16x32_bf16 v[58:61], v[146:149], v[222:225], v[58:61]
	v_mfma_f32_16x16x32_bf16 v[54:57], v[156:159], v[222:225], v[54:57]
	v_mfma_f32_16x16x32_bf16 v[50:53], v[160:163], v[222:225], v[50:53]
	v_lshl_add_u64 v[180:181], v[132:133], 0, s[26:27]
	global_load_dwordx2 v[118:119], v[180:181], off
	v_lshl_add_u64 v[180:181], v[132:133], 0, s[28:29]
	global_load_dwordx2 v[120:121], v[180:181], off
	v_mfma_f32_16x16x32_bf16 v[46:49], v[142:145], v[226:229], v[46:49]
	v_mfma_f32_16x16x32_bf16 v[42:45], v[146:149], v[226:229], v[42:45]
	v_mfma_f32_16x16x32_bf16 v[38:41], v[156:159], v[226:229], v[38:41]
	v_mfma_f32_16x16x32_bf16 v[34:37], v[160:163], v[226:229], v[34:37]
	v_lshl_add_u64 v[180:181], v[132:133], 0, s[36:37]
	global_load_dwordx2 v[122:123], v[180:181], off
	v_lshl_add_u64 v[180:181], v[132:133], 0, s[38:39]
	global_load_dwordx2 v[124:125], v[180:181], off
	v_mfma_f32_16x16x32_bf16 v[18:21], v[142:145], v[230:233], v[18:21]
	v_mfma_f32_16x16x32_bf16 v[22:25], v[146:149], v[230:233], v[22:25]
	v_mfma_f32_16x16x32_bf16 v[26:29], v[156:159], v[230:233], v[26:29]
	v_mfma_f32_16x16x32_bf16 v[30:33], v[160:163], v[230:233], v[30:33]
	v_lshl_add_u64 v[180:181], v[132:133], 0, s[40:41]
	global_load_dwordx2 v[126:127], v[180:181], off
	v_lshl_add_u64 v[180:181], v[132:133], 0, s[42:43]
	global_load_dwordx2 v[128:129], v[180:181], off
	v_mfma_f32_16x16x32_bf16 v[2:5], v[142:145], v[234:237], v[2:5]
	v_mfma_f32_16x16x32_bf16 v[6:9], v[146:149], v[234:237], v[6:9]
	v_mfma_f32_16x16x32_bf16 v[10:13], v[156:159], v[234:237], v[10:13]
	v_mfma_f32_16x16x32_bf16 v[14:17], v[160:163], v[234:237], v[14:17]
	s_waitcnt vmcnt(21)
	s_mov_b32 s49, s46
	s_mov_b32 s46, s47
	s_mov_b32 s47, s48
	s_mov_b32 s48, s49
	s_add_i32 s50, s50, 1
	s_waitcnt lgkmcnt(0)
	s_barrier
; #define MD_GLDS_A(buf, tau) do { _Pragma("unroll") for (int i = 0; i < 5; ++i) if (amask & (1u << i)) \
;         __builtin_amdgcn_global_load_lds((const unsigned*)((const char*)HIDp + aoff[i] + (size_t)((tau) & 7) * 128), (PG8_LAS unsigned*)(MD_SA(buf) + wid * 1024 + i * 8192), 16, 0, 0); } while (0)
; #define MD_B_ISSUE(sb, tau) do { const char* kb_ = Bb + (size_t)((tau) >> 3) * 512 + (size_t)((tau) & 7) * (64 * (size_t)RB); _Pragma("unroll") for (int j = 0; j < 8; ++j) { const char* p_ = kb_ + (size_t)j * RB; \
;         asm volatile("global_load_dwordx2 %0, %1, off" : "=&v"(sb[j]) : "v"(p_) : "memory"); } } while (0)
; #define MD_B_WAIT(sb, N) asm volatile("s_waitcnt vmcnt(%8)" : "+v"(sb[0]), "+v"(sb[1]), "+v"(sb[2]), "+v"(sb[3]), "+v"(sb[4]), "+v"(sb[5]), "+v"(sb[6]), "+v"(sb[7]) : "n"(N) : "memory")
; #define MD_END(last) do { if (last) asm volatile("s_waitcnt vmcnt(0)" ::: "memory"); else asm volatile("s_waitcnt vmcnt(8)" ::: "memory"); \
;         asm volatile("s_waitcnt lgkmcnt(0)" ::: "memory"); __builtin_amdgcn_s_barrier(); asm volatile("" ::: "memory"); } while (0)
; __device__ __forceinline__ void moe_down_stream(PG8_LAS unsigned char* lds, int e, int cb0, int slot0, int nv, const bf16_t* HIDp, const float* Wd, bf16_t* Y, const float* slot_w, const int* slot_dst) {
;     ...
;     for (int t = 0; t < NT; t += 2) {
;         if (t + 2 < NT) MD_B_WAIT(s1, 8); else MD_B_WAIT(s1, 0);
;         MD_B_WRITE(s1, 1); __builtin_amdgcn_sched_barrier(0); MD_GLDS_A(1, t + 1); __builtin_amdgcn_sched_barrier(0);
;         if (t + 3 < NT) MD_B_ISSUE(s1, t + 3);
;         MD_COMPUTE(0);
;         MD_END(t + 3 >= NT);
;         if (t + 2 < NT) { MD_B_WAIT(s0, 8); MD_B_WRITE(s0, 0); __builtin_amdgcn_sched_barrier(0); MD_GLDS_A(0, t + 2); __builtin_amdgcn_sched_barrier(0); }
;         if (t + 4 < NT) MD_B_ISSUE(s0, t + 4);
;         MD_COMPUTE(1);
;         MD_END(t + 4 >= NT);
	v_cvt_pk_bf16_f32 v172, v186, v188
	v_cvt_pk_bf16_f32 v173, v190, v192
	v_cvt_pk_bf16_f32 v174, v194, v196
	v_cvt_pk_bf16_f32 v175, v198, v200
	v_cvt_pk_bf16_f32 v176, v187, v189
	v_cvt_pk_bf16_f32 v177, v191, v193
	v_cvt_pk_bf16_f32 v178, v195, v197
	v_cvt_pk_bf16_f32 v179, v199, v201
	ds_write_b128 v95, v[172:175] offset:0
	ds_write_b128 v95, v[176:179] offset:128
	v_add_u32_e32 v91, s46, v135
	v_add_u32_e32 v93, s46, v137
	ds_read_b128 v[238:241], v139 offset:19456
	ds_read_b128 v[242:245], v139 offset:21504
	ds_read_b128 v[246:249], v139 offset:23552
	ds_read_b128 v[250:253], v139 offset:25600
	ds_read_b128 v[218:221], v91 offset:0
	ds_read_b128 v[222:225], v91 offset:2048
	ds_read_b128 v[226:229], v91 offset:4096
	ds_read_b128 v[230:233], v91 offset:6144
	ds_read_b128 v[234:237], v91 offset:8192
	s_add_i32 s49, s48, s74
	s_add_i32 s52, s52, 1
	s_and_b32 s54, s52, 7
	s_cmp_eq_u32 s54, 0
	s_cselect_b32 s54, s53, s32
	s_cselect_b32 s55, -1, 0
	s_add_u32 s30, s30, s54
	s_addc_u32 s31, s31, s55
	s_waitcnt lgkmcnt(0)
	v_mfma_f32_16x16x32_bf16 v[78:81], v[238:241], v[218:221], v[78:81]
	v_mfma_f32_16x16x32_bf16 v[74:77], v[242:245], v[218:221], v[74:77]
	v_mfma_f32_16x16x32_bf16 v[70:73], v[246:249], v[218:221], v[70:73]
	v_mfma_f32_16x16x32_bf16 v[66:69], v[250:253], v[218:221], v[66:69]
	ds_read_b128 v[218:221], v93 offset:0
	ds_read_b128 v[142:145], v141 offset:19456
	s_mov_b32 m0, s49
	s_nop 0
	global_load_lds_dwordx4 v88, s[30:31]
	v_mfma_f32_16x16x32_bf16 v[62:65], v[238:241], v[222:225], v[62:65]
	v_mfma_f32_16x16x32_bf16 v[58:61], v[242:245], v[222:225], v[58:61]
	v_mfma_f32_16x16x32_bf16 v[54:57], v[246:249], v[222:225], v[54:57]
	v_mfma_f32_16x16x32_bf16 v[50:53], v[250:253], v[222:225], v[50:53]
	ds_read_b128 v[222:225], v93 offset:2048
	ds_read_b128 v[146:149], v141 offset:21504
	s_add_i32 m0, s49, 0x2000
	s_nop 0
	global_load_lds_dwordx4 v90, s[30:31]
	v_mfma_f32_16x16x32_bf16 v[46:49], v[238:241], v[226:229], v[46:49]
	v_mfma_f32_16x16x32_bf16 v[42:45], v[242:245], v[226:229], v[42:45]
	v_mfma_f32_16x16x32_bf16 v[38:41], v[246:249], v[226:229], v[38:41]
	v_mfma_f32_16x16x32_bf16 v[34:37], v[250:253], v[226:229], v[34:37]
	ds_read_b128 v[226:229], v93 offset:4096
	ds_read_b128 v[156:159], v141 offset:23552
	s_add_i32 m0, s49, 0x4000
	s_nop 0
	global_load_lds_dwordx4 v92, s[30:31]
	v_mfma_f32_16x16x32_bf16 v[18:21], v[238:241], v[230:233], v[18:21]
	v_mfma_f32_16x16x32_bf16 v[22:25], v[242:245], v[230:233], v[22:25]
	v_mfma_f32_16x16x32_bf16 v[26:29], v[246:249], v[230:233], v[26:29]
	v_mfma_f32_16x16x32_bf16 v[30:33], v[250:253], v[230:233], v[30:33]
	ds_read_b128 v[230:233], v93 offset:6144
	ds_read_b128 v[160:163], v141 offset:25600
	s_add_i32 m0, s49, 0x6000
	s_nop 0
	global_load_lds_dwordx4 v94, s[30:31]
	v_mfma_f32_16x16x32_bf16 v[2:5], v[238:241], v[234:237], v[2:5]
	v_mfma_f32_16x16x32_bf16 v[6:9], v[242:245], v[234:237], v[6:9]
	v_mfma_f32_16x16x32_bf16 v[10:13], v[246:249], v[234:237], v[10:13]
	v_mfma_f32_16x16x32_bf16 v[14:17], v[250:253], v[234:237], v[14:17]
	ds_read_b128 v[234:237], v93 offset:8192
	s_add_i32 m0, s49, 0x8000
	s_nop 0
	global_load_lds_dwordx4 v96, s[30:31]
	s_waitcnt lgkmcnt(0)
	v_mfma_f32_16x16x32_bf16 v[78:81], v[142:145], v[218:221], v[78:81]
	v_mfma_f32_16x16x32_bf16 v[74:77], v[146:149], v[218:221], v[74:77]
	v_mfma_f32_16x16x32_bf16 v[70:73], v[156:159], v[218:221], v[70:73]
	v_mfma_f32_16x16x32_bf16 v[66:69], v[160:163], v[218:221], v[66:69]
	s_add_i32 s51, s51, 1
	s_and_b32 s54, s51, 7
	s_cmp_eq_u32 s54, 0
	s_cselect_b32 s44, s34, s35
	s_cselect_b32 s45, -1, 0
	v_lshl_add_u64 v[132:133], v[132:133], 0, s[44:45]
	global_load_dwordx2 v[186:187], v[132:133], off
	v_lshl_add_u64 v[180:181], v[132:133], 0, s[24:25]
	global_load_dwordx2 v[188:189], v[180:181], off
	v_mfma_f32_16x16x32_bf16 v[62:65], v[142:145], v[222:225], v[62:65]
	v_mfma_f32_16x16x32_bf16 v[58:61], v[146:149], v[222:225], v[58:61]
	v_mfma_f32_16x16x32_bf16 v[54:57], v[156:159], v[222:225], v[54:57]
	v_mfma_f32_16x16x32_bf16 v[50:53], v[160:163], v[222:225], v[50:53]
	v_lshl_add_u64 v[180:181], v[132:133], 0, s[26:27]
	global_load_dwordx2 v[190:191], v[180:181], off
	v_lshl_add_u64 v[180:181], v[132:133], 0, s[28:29]
	global_load_dwordx2 v[192:193], v[180:181], off
	v_mfma_f32_16x16x32_bf16 v[46:49], v[142:145], v[226:229], v[46:49]
	v_mfma_f32_16x16x32_bf16 v[42:45], v[146:149], v[226:229], v[42:45]
	v_mfma_f32_16x16x32_bf16 v[38:41], v[156:159], v[226:229], v[38:41]
	v_mfma_f32_16x16x32_bf16 v[34:37], v[160:163], v[226:229], v[34:37]
	v_lshl_add_u64 v[180:181], v[132:133], 0, s[36:37]
	global_load_dwordx2 v[194:195], v[180:181], off
	v_lshl_add_u64 v[180:181], v[132:133], 0, s[38:39]
	global_load_dwordx2 v[196:197], v[180:181], off
	v_mfma_f32_16x16x32_bf16 v[18:21], v[142:145], v[230:233], v[18:21]
	v_mfma_f32_16x16x32_bf16 v[22:25], v[146:149], v[230:233], v[22:25]
	v_mfma_f32_16x16x32_bf16 v[26:29], v[156:159], v[230:233], v[26:29]
	v_mfma_f32_16x16x32_bf16 v[30:33], v[160:163], v[230:233], v[30:33]
	v_lshl_add_u64 v[180:181], v[132:133], 0, s[40:41]
	global_load_dwordx2 v[198:199], v[180:181], off
	v_lshl_add_u64 v[180:181], v[132:133], 0, s[42:43]
	global_load_dwordx2 v[200:201], v[180:181], off
	v_mfma_f32_16x16x32_bf16 v[2:5], v[142:145], v[234:237], v[2:5]
	v_mfma_f32_16x16x32_bf16 v[6:9], v[146:149], v[234:237], v[6:9]
	v_mfma_f32_16x16x32_bf16 v[10:13], v[156:159], v[234:237], v[10:13]
	v_mfma_f32_16x16x32_bf16 v[14:17], v[160:163], v[234:237], v[14:17]
	s_waitcnt vmcnt(21)
	s_mov_b32 s49, s46
	s_mov_b32 s46, s47
	s_mov_b32 s47, s48
	s_mov_b32 s48, s49
	s_add_i32 s50, s50, 1
	s_waitcnt lgkmcnt(0)
	s_barrier
; #define MD_GLDS_A(buf, tau) do { _Pragma("unroll") for (int i = 0; i < 5; ++i) if (amask & (1u << i)) \
;         __builtin_amdgcn_global_load_lds((const unsigned*)((const char*)HIDp + aoff[i] + (size_t)((tau) & 7) * 128), (PG8_LAS unsigned*)(MD_SA(buf) + wid * 1024 + i * 8192), 16, 0, 0); } while (0)
; #define MD_B_ISSUE(sb, tau) do { const char* kb_ = Bb + (size_t)((tau) >> 3) * 512 + (size_t)((tau) & 7) * (64 * (size_t)RB); _Pragma("unroll") for (int j = 0; j < 8; ++j) { const char* p_ = kb_ + (size_t)j * RB; \
;         asm volatile("global_load_dwordx2 %0, %1, off" : "=&v"(sb[j]) : "v"(p_) : "memory"); } } while (0)
; #define MD_B_WAIT(sb, N) asm volatile("s_waitcnt vmcnt(%8)" : "+v"(sb[0]), "+v"(sb[1]), "+v"(sb[2]), "+v"(sb[3]), "+v"(sb[4]), "+v"(sb[5]), "+v"(sb[6]), "+v"(sb[7]) : "n"(N) : "memory")
; #define MD_END(last) do { if (last) asm volatile("s_waitcnt vmcnt(0)" ::: "memory"); else asm volatile("s_waitcnt vmcnt(8)" ::: "memory"); \
;         asm volatile("s_waitcnt lgkmcnt(0)" ::: "memory"); __builtin_amdgcn_s_barrier(); asm volatile("" ::: "memory"); } while (0)
; __device__ __forceinline__ void moe_down_stream(PG8_LAS unsigned char* lds, int e, int cb0, int slot0, int nv, const bf16_t* HIDp, const float* Wd, bf16_t* Y, const float* slot_w, const int* slot_dst) {
;     ...
;     for (int t = 0; t < NT; t += 2) {
;         if (t + 2 < NT) MD_B_WAIT(s1, 8); else MD_B_WAIT(s1, 0);
;         MD_B_WRITE(s1, 1); __builtin_amdgcn_sched_barrier(0); MD_GLDS_A(1, t + 1); __builtin_amdgcn_sched_barrier(0);
;         if (t + 3 < NT) MD_B_ISSUE(s1, t + 3);
;         MD_COMPUTE(0);
;         MD_END(t + 3 >= NT);
;         if (t + 2 < NT) { MD_B_WAIT(s0, 8); MD_B_WRITE(s0, 0); __builtin_amdgcn_sched_barrier(0); MD_GLDS_A(0, t + 2); __builtin_amdgcn_sched_barrier(0); }
;         if (t + 4 < NT) MD_B_ISSUE(s0, t + 4);
;         MD_COMPUTE(1);
;         MD_END(t + 4 >= NT);
	v_cvt_pk_bf16_f32 v172, v202, v204
	v_cvt_pk_bf16_f32 v173, v206, v208
	v_cvt_pk_bf16_f32 v174, v210, v212
	v_cvt_pk_bf16_f32 v175, v214, v216
	v_cvt_pk_bf16_f32 v176, v203, v205
	v_cvt_pk_bf16_f32 v177, v207, v209
	v_cvt_pk_bf16_f32 v178, v211, v213
	v_cvt_pk_bf16_f32 v179, v215, v217
	ds_write_b128 v95, v[172:175] offset:19456
	ds_write_b128 v95, v[176:179] offset:19584
	v_add_u32_e32 v91, s46, v135
	v_add_u32_e32 v93, s46, v137
	ds_read_b128 v[238:241], v139 offset:0
	ds_read_b128 v[242:245], v139 offset:2048
	ds_read_b128 v[246:249], v139 offset:4096
	ds_read_b128 v[250:253], v139 offset:6144
	ds_read_b128 v[218:221], v91 offset:0
	ds_read_b128 v[222:225], v91 offset:2048
	ds_read_b128 v[226:229], v91 offset:4096
	ds_read_b128 v[230:233], v91 offset:6144
	ds_read_b128 v[234:237], v91 offset:8192
	s_add_i32 s49, s48, s74
	s_add_i32 s52, s52, 1
	s_and_b32 s54, s52, 7
	s_cmp_eq_u32 s54, 0
	s_cselect_b32 s54, s53, s32
	s_cselect_b32 s55, -1, 0
	s_add_u32 s30, s30, s54
	s_addc_u32 s31, s31, s55
	s_waitcnt lgkmcnt(0)
	v_mfma_f32_16x16x32_bf16 v[78:81], v[238:241], v[218:221], v[78:81]
	v_mfma_f32_16x16x32_bf16 v[74:77], v[242:245], v[218:221], v[74:77]
	v_mfma_f32_16x16x32_bf16 v[70:73], v[246:249], v[218:221], v[70:73]
	v_mfma_f32_16x16x32_bf16 v[66:69], v[250:253], v[218:221], v[66:69]
	ds_read_b128 v[218:221], v93 offset:0
	ds_read_b128 v[142:145], v141 offset:0
	s_mov_b32 m0, s49
	s_nop 0
	global_load_lds_dwordx4 v88, s[30:31]
	v_mfma_f32_16x16x32_bf16 v[62:65], v[238:241], v[222:225], v[62:65]
	v_mfma_f32_16x16x32_bf16 v[58:61], v[242:245], v[222:225], v[58:61]
	v_mfma_f32_16x16x32_bf16 v[54:57], v[246:249], v[222:225], v[54:57]
	v_mfma_f32_16x16x32_bf16 v[50:53], v[250:253], v[222:225], v[50:53]
	ds_read_b128 v[222:225], v93 offset:2048
	ds_read_b128 v[146:149], v141 offset:2048
	s_add_i32 m0, s49, 0x2000
	s_nop 0
	global_load_lds_dwordx4 v90, s[30:31]
	v_mfma_f32_16x16x32_bf16 v[46:49], v[238:241], v[226:229], v[46:49]
	v_mfma_f32_16x16x32_bf16 v[42:45], v[242:245], v[226:229], v[42:45]
	v_mfma_f32_16x16x32_bf16 v[38:41], v[246:249], v[226:229], v[38:41]
	v_mfma_f32_16x16x32_bf16 v[34:37], v[250:253], v[226:229], v[34:37]
	ds_read_b128 v[226:229], v93 offset:4096
	ds_read_b128 v[156:159], v141 offset:4096
	s_add_i32 m0, s49, 0x4000
	s_nop 0
	global_load_lds_dwordx4 v92, s[30:31]
	v_mfma_f32_16x16x32_bf16 v[18:21], v[238:241], v[230:233], v[18:21]
	v_mfma_f32_16x16x32_bf16 v[22:25], v[242:245], v[230:233], v[22:25]
	v_mfma_f32_16x16x32_bf16 v[26:29], v[246:249], v[230:233], v[26:29]
	v_mfma_f32_16x16x32_bf16 v[30:33], v[250:253], v[230:233], v[30:33]
	ds_read_b128 v[230:233], v93 offset:6144
	ds_read_b128 v[160:163], v141 offset:6144
	s_add_i32 m0, s49, 0x6000
	s_nop 0
	global_load_lds_dwordx4 v94, s[30:31]
	v_mfma_f32_16x16x32_bf16 v[2:5], v[238:241], v[234:237], v[2:5]
	v_mfma_f32_16x16x32_bf16 v[6:9], v[242:245], v[234:237], v[6:9]
	v_mfma_f32_16x16x32_bf16 v[10:13], v[246:249], v[234:237], v[10:13]
	v_mfma_f32_16x16x32_bf16 v[14:17], v[250:253], v[234:237], v[14:17]
	ds_read_b128 v[234:237], v93 offset:8192
	s_add_i32 m0, s49, 0x8000
	s_nop 0
	global_load_lds_dwordx4 v96, s[30:31]
	s_waitcnt lgkmcnt(0)
	v_mfma_f32_16x16x32_bf16 v[78:81], v[142:145], v[218:221], v[78:81]
	v_mfma_f32_16x16x32_bf16 v[74:77], v[146:149], v[218:221], v[74:77]
	v_mfma_f32_16x16x32_bf16 v[70:73], v[156:159], v[218:221], v[70:73]
	v_mfma_f32_16x16x32_bf16 v[66:69], v[160:163], v[218:221], v[66:69]
	s_add_i32 s51, s51, 1
	s_and_b32 s54, s51, 7
	s_cmp_eq_u32 s54, 0
	s_cselect_b32 s44, s34, s35
	s_cselect_b32 s45, -1, 0
	v_lshl_add_u64 v[132:133], v[132:133], 0, s[44:45]
	global_load_dwordx2 v[202:203], v[132:133], off
	v_lshl_add_u64 v[180:181], v[132:133], 0, s[24:25]
	global_load_dwordx2 v[204:205], v[180:181], off
	v_mfma_f32_16x16x32_bf16 v[62:65], v[142:145], v[222:225], v[62:65]
	v_mfma_f32_16x16x32_bf16 v[58:61], v[146:149], v[222:225], v[58:61]
	v_mfma_f32_16x16x32_bf16 v[54:57], v[156:159], v[222:225], v[54:57]
	v_mfma_f32_16x16x32_bf16 v[50:53], v[160:163], v[222:225], v[50:53]
	v_lshl_add_u64 v[180:181], v[132:133], 0, s[26:27]
	global_load_dwordx2 v[206:207], v[180:181], off
	v_lshl_add_u64 v[180:181], v[132:133], 0, s[28:29]
	global_load_dwordx2 v[208:209], v[180:181], off
	v_mfma_f32_16x16x32_bf16 v[46:49], v[142:145], v[226:229], v[46:49]
	v_mfma_f32_16x16x32_bf16 v[42:45], v[146:149], v[226:229], v[42:45]
	v_mfma_f32_16x16x32_bf16 v[38:41], v[156:159], v[226:229], v[38:41]
	v_mfma_f32_16x16x32_bf16 v[34:37], v[160:163], v[226:229], v[34:37]
	v_lshl_add_u64 v[180:181], v[132:133], 0, s[36:37]
	global_load_dwordx2 v[210:211], v[180:181], off
	v_lshl_add_u64 v[180:181], v[132:133], 0, s[38:39]
	global_load_dwordx2 v[212:213], v[180:181], off
	v_mfma_f32_16x16x32_bf16 v[18:21], v[142:145], v[230:233], v[18:21]
	v_mfma_f32_16x16x32_bf16 v[22:25], v[146:149], v[230:233], v[22:25]
	v_mfma_f32_16x16x32_bf16 v[26:29], v[156:159], v[230:233], v[26:29]
	v_mfma_f32_16x16x32_bf16 v[30:33], v[160:163], v[230:233], v[30:33]
	v_lshl_add_u64 v[180:181], v[132:133], 0, s[40:41]
	global_load_dwordx2 v[214:215], v[180:181], off
	v_lshl_add_u64 v[180:181], v[132:133], 0, s[42:43]
	global_load_dwordx2 v[216:217], v[180:181], off
	v_mfma_f32_16x16x32_bf16 v[2:5], v[142:145], v[234:237], v[2:5]
	v_mfma_f32_16x16x32_bf16 v[6:9], v[146:149], v[234:237], v[6:9]
	v_mfma_f32_16x16x32_bf16 v[10:13], v[156:159], v[234:237], v[10:13]
	v_mfma_f32_16x16x32_bf16 v[14:17], v[160:163], v[234:237], v[14:17]
	s_waitcnt vmcnt(21)
	s_mov_b32 s49, s46
	s_mov_b32 s46, s47
	s_mov_b32 s47, s48
	s_mov_b32 s48, s49
	s_add_i32 s50, s50, 1
	s_waitcnt lgkmcnt(0)
	s_barrier
; #define MD_GLDS_A(buf, tau) do { _Pragma("unroll") for (int i = 0; i < 5; ++i) if (amask & (1u << i)) \
;         __builtin_amdgcn_global_load_lds((const unsigned*)((const char*)HIDp + aoff[i] + (size_t)((tau) & 7) * 128), (PG8_LAS unsigned*)(MD_SA(buf) + wid * 1024 + i * 8192), 16, 0, 0); } while (0)
; #define MD_B_ISSUE(sb, tau) do { const char* kb_ = Bb + (size_t)((tau) >> 3) * 512 + (size_t)((tau) & 7) * (64 * (size_t)RB); _Pragma("unroll") for (int j = 0; j < 8; ++j) { const char* p_ = kb_ + (size_t)j * RB; \
;         asm volatile("global_load_dwordx2 %0, %1, off" : "=&v"(sb[j]) : "v"(p_) : "memory"); } } while (0)
; #define MD_B_WAIT(sb, N) asm volatile("s_waitcnt vmcnt(%8)" : "+v"(sb[0]), "+v"(sb[1]), "+v"(sb[2]), "+v"(sb[3]), "+v"(sb[4]), "+v"(sb[5]), "+v"(sb[6]), "+v"(sb[7]) : "n"(N) : "memory")
; #define MD_END(last) do { if (last) asm volatile("s_waitcnt vmcnt(0)" ::: "memory"); else asm volatile("s_waitcnt vmcnt(8)" ::: "memory"); \
;         asm volatile("s_waitcnt lgkmcnt(0)" ::: "memory"); __builtin_amdgcn_s_barrier(); asm volatile("" ::: "memory"); } while (0)
; __device__ __forceinline__ void moe_down_stream(PG8_LAS unsigned char* lds, int e, int cb0, int slot0, int nv, const bf16_t* HIDp, const float* Wd, bf16_t* Y, const float* slot_w, const int* slot_dst) {
;     ...
;     for (int t = 0; t < NT; t += 2) {
;         if (t + 2 < NT) MD_B_WAIT(s1, 8); else MD_B_WAIT(s1, 0);
;         MD_B_WRITE(s1, 1); __builtin_amdgcn_sched_barrier(0); MD_GLDS_A(1, t + 1); __builtin_amdgcn_sched_barrier(0);
;         if (t + 3 < NT) MD_B_ISSUE(s1, t + 3);
;         MD_COMPUTE(0);
;         MD_END(t + 3 >= NT);
;         if (t + 2 < NT) { MD_B_WAIT(s0, 8); MD_B_WRITE(s0, 0); __builtin_amdgcn_sched_barrier(0); MD_GLDS_A(0, t + 2); __builtin_amdgcn_sched_barrier(0); }
;         if (t + 4 < NT) MD_B_ISSUE(s0, t + 4);
;         MD_COMPUTE(1);
;         MD_END(t + 4 >= NT);
	v_cvt_pk_bf16_f32 v172, v98, v100
	v_cvt_pk_bf16_f32 v173, v102, v104
	v_cvt_pk_bf16_f32 v174, v106, v108
	v_cvt_pk_bf16_f32 v175, v110, v112
	v_cvt_pk_bf16_f32 v176, v99, v101
	v_cvt_pk_bf16_f32 v177, v103, v105
	v_cvt_pk_bf16_f32 v178, v107, v109
	v_cvt_pk_bf16_f32 v179, v111, v113
	ds_write_b128 v95, v[172:175] offset:0
	ds_write_b128 v95, v[176:179] offset:128
	v_add_u32_e32 v91, s46, v135
	v_add_u32_e32 v93, s46, v137
	ds_read_b128 v[238:241], v139 offset:19456
	ds_read_b128 v[242:245], v139 offset:21504
	ds_read_b128 v[246:249], v139 offset:23552
	ds_read_b128 v[250:253], v139 offset:25600
	ds_read_b128 v[218:221], v91 offset:0
	ds_read_b128 v[222:225], v91 offset:2048
	ds_read_b128 v[226:229], v91 offset:4096
	ds_read_b128 v[230:233], v91 offset:6144
	ds_read_b128 v[234:237], v91 offset:8192
	s_add_i32 s49, s48, s74
	s_add_i32 s52, s52, 1
	s_and_b32 s54, s52, 7
	s_cmp_eq_u32 s54, 0
	s_cselect_b32 s54, s53, s32
	s_cselect_b32 s55, -1, 0
	s_add_u32 s30, s30, s54
	s_addc_u32 s31, s31, s55
	s_waitcnt lgkmcnt(0)
	v_mfma_f32_16x16x32_bf16 v[78:81], v[238:241], v[218:221], v[78:81]
	v_mfma_f32_16x16x32_bf16 v[74:77], v[242:245], v[218:221], v[74:77]
	v_mfma_f32_16x16x32_bf16 v[70:73], v[246:249], v[218:221], v[70:73]
	v_mfma_f32_16x16x32_bf16 v[66:69], v[250:253], v[218:221], v[66:69]
	ds_read_b128 v[218:221], v93 offset:0
	ds_read_b128 v[142:145], v141 offset:19456
	s_mov_b32 m0, s49
	s_nop 0
	global_load_lds_dwordx4 v88, s[30:31]
	v_mfma_f32_16x16x32_bf16 v[62:65], v[238:241], v[222:225], v[62:65]
	v_mfma_f32_16x16x32_bf16 v[58:61], v[242:245], v[222:225], v[58:61]
	v_mfma_f32_16x16x32_bf16 v[54:57], v[246:249], v[222:225], v[54:57]
	v_mfma_f32_16x16x32_bf16 v[50:53], v[250:253], v[222:225], v[50:53]
	ds_read_b128 v[222:225], v93 offset:2048
	ds_read_b128 v[146:149], v141 offset:21504
	s_add_i32 m0, s49, 0x2000
	s_nop 0
	global_load_lds_dwordx4 v90, s[30:31]
	v_mfma_f32_16x16x32_bf16 v[46:49], v[238:241], v[226:229], v[46:49]
	v_mfma_f32_16x16x32_bf16 v[42:45], v[242:245], v[226:229], v[42:45]
	v_mfma_f32_16x16x32_bf16 v[38:41], v[246:249], v[226:229], v[38:41]
	v_mfma_f32_16x16x32_bf16 v[34:37], v[250:253], v[226:229], v[34:37]
	ds_read_b128 v[226:229], v93 offset:4096
	ds_read_b128 v[156:159], v141 offset:23552
	s_add_i32 m0, s49, 0x4000
	s_nop 0
	global_load_lds_dwordx4 v92, s[30:31]
	v_mfma_f32_16x16x32_bf16 v[18:21], v[238:241], v[230:233], v[18:21]
	v_mfma_f32_16x16x32_bf16 v[22:25], v[242:245], v[230:233], v[22:25]
	v_mfma_f32_16x16x32_bf16 v[26:29], v[246:249], v[230:233], v[26:29]
	v_mfma_f32_16x16x32_bf16 v[30:33], v[250:253], v[230:233], v[30:33]
	ds_read_b128 v[230:233], v93 offset:6144
	ds_read_b128 v[160:163], v141 offset:25600
	s_add_i32 m0, s49, 0x6000
	s_nop 0
	global_load_lds_dwordx4 v94, s[30:31]
	v_mfma_f32_16x16x32_bf16 v[2:5], v[238:241], v[234:237], v[2:5]
	v_mfma_f32_16x16x32_bf16 v[6:9], v[242:245], v[234:237], v[6:9]
	v_mfma_f32_16x16x32_bf16 v[10:13], v[246:249], v[234:237], v[10:13]
	v_mfma_f32_16x16x32_bf16 v[14:17], v[250:253], v[234:237], v[14:17]
	ds_read_b128 v[234:237], v93 offset:8192
	s_add_i32 m0, s49, 0x8000
	s_nop 0
	global_load_lds_dwordx4 v96, s[30:31]
	s_waitcnt lgkmcnt(0)
	v_mfma_f32_16x16x32_bf16 v[78:81], v[142:145], v[218:221], v[78:81]
	v_mfma_f32_16x16x32_bf16 v[74:77], v[146:149], v[218:221], v[74:77]
	v_mfma_f32_16x16x32_bf16 v[70:73], v[156:159], v[218:221], v[70:73]
	v_mfma_f32_16x16x32_bf16 v[66:69], v[160:163], v[218:221], v[66:69]
	v_mfma_f32_16x16x32_bf16 v[62:65], v[142:145], v[222:225], v[62:65]
	v_mfma_f32_16x16x32_bf16 v[58:61], v[146:149], v[222:225], v[58:61]
	v_mfma_f32_16x16x32_bf16 v[54:57], v[156:159], v[222:225], v[54:57]
	v_mfma_f32_16x16x32_bf16 v[50:53], v[160:163], v[222:225], v[50:53]
	v_mfma_f32_16x16x32_bf16 v[46:49], v[142:145], v[226:229], v[46:49]
	v_mfma_f32_16x16x32_bf16 v[42:45], v[146:149], v[226:229], v[42:45]
	v_mfma_f32_16x16x32_bf16 v[38:41], v[156:159], v[226:229], v[38:41]
	v_mfma_f32_16x16x32_bf16 v[34:37], v[160:163], v[226:229], v[34:37]
	v_mfma_f32_16x16x32_bf16 v[18:21], v[142:145], v[230:233], v[18:21]
	v_mfma_f32_16x16x32_bf16 v[22:25], v[146:149], v[230:233], v[22:25]
	v_mfma_f32_16x16x32_bf16 v[26:29], v[156:159], v[230:233], v[26:29]
	v_mfma_f32_16x16x32_bf16 v[30:33], v[160:163], v[230:233], v[30:33]
	v_mfma_f32_16x16x32_bf16 v[2:5], v[142:145], v[234:237], v[2:5]
	v_mfma_f32_16x16x32_bf16 v[6:9], v[146:149], v[234:237], v[6:9]
	v_mfma_f32_16x16x32_bf16 v[10:13], v[156:159], v[234:237], v[10:13]
	v_mfma_f32_16x16x32_bf16 v[14:17], v[160:163], v[234:237], v[14:17]
	s_waitcnt vmcnt(13)
	s_mov_b32 s49, s46
	s_mov_b32 s46, s47
	s_mov_b32 s47, s48
	s_mov_b32 s48, s49
	s_add_i32 s50, s50, 1
	s_waitcnt lgkmcnt(0)
	s_barrier
; #define MD_GLDS_A(buf, tau) do { _Pragma("unroll") for (int i = 0; i < 5; ++i) if (amask & (1u << i)) \
;         __builtin_amdgcn_global_load_lds((const unsigned*)((const char*)HIDp + aoff[i] + (size_t)((tau) & 7) * 128), (PG8_LAS unsigned*)(MD_SA(buf) + wid * 1024 + i * 8192), 16, 0, 0); } while (0)
; #define MD_B_ISSUE(sb, tau) do { const char* kb_ = Bb + (size_t)((tau) >> 3) * 512 + (size_t)((tau) & 7) * (64 * (size_t)RB); _Pragma("unroll") for (int j = 0; j < 8; ++j) { const char* p_ = kb_ + (size_t)j * RB; \
;         asm volatile("global_load_dwordx2 %0, %1, off" : "=&v"(sb[j]) : "v"(p_) : "memory"); } } while (0)
; #define MD_B_WAIT(sb, N) asm volatile("s_waitcnt vmcnt(%8)" : "+v"(sb[0]), "+v"(sb[1]), "+v"(sb[2]), "+v"(sb[3]), "+v"(sb[4]), "+v"(sb[5]), "+v"(sb[6]), "+v"(sb[7]) : "n"(N) : "memory")
; #define MD_END(last) do { if (last) asm volatile("s_waitcnt vmcnt(0)" ::: "memory"); else asm volatile("s_waitcnt vmcnt(8)" ::: "memory"); \
;         asm volatile("s_waitcnt lgkmcnt(0)" ::: "memory"); __builtin_amdgcn_s_barrier(); asm volatile("" ::: "memory"); } while (0)
; __device__ __forceinline__ void moe_down_stream(PG8_LAS unsigned char* lds, int e, int cb0, int slot0, int nv, const bf16_t* HIDp, const float* Wd, bf16_t* Y, const float* slot_w, const int* slot_dst) {
;     ...
;     for (int t = 0; t < NT; t += 2) {
;         if (t + 2 < NT) MD_B_WAIT(s1, 8); else MD_B_WAIT(s1, 0);
;         MD_B_WRITE(s1, 1); __builtin_amdgcn_sched_barrier(0); MD_GLDS_A(1, t + 1); __builtin_amdgcn_sched_barrier(0);
;         if (t + 3 < NT) MD_B_ISSUE(s1, t + 3);
;         MD_COMPUTE(0);
;         MD_END(t + 3 >= NT);
;         if (t + 2 < NT) { MD_B_WAIT(s0, 8); MD_B_WRITE(s0, 0); __builtin_amdgcn_sched_barrier(0); MD_GLDS_A(0, t + 2); __builtin_amdgcn_sched_barrier(0); }
;         if (t + 4 < NT) MD_B_ISSUE(s0, t + 4);
;         MD_COMPUTE(1);
;         MD_END(t + 4 >= NT);
	v_cvt_pk_bf16_f32 v172, v114, v116
	v_cvt_pk_bf16_f32 v173, v118, v120
	v_cvt_pk_bf16_f32 v174, v122, v124
	v_cvt_pk_bf16_f32 v175, v126, v128
	v_cvt_pk_bf16_f32 v176, v115, v117
	v_cvt_pk_bf16_f32 v177, v119, v121
	v_cvt_pk_bf16_f32 v178, v123, v125
	v_cvt_pk_bf16_f32 v179, v127, v129
	ds_write_b128 v95, v[172:175] offset:19456
	ds_write_b128 v95, v[176:179] offset:19584
	v_add_u32_e32 v91, s46, v135
	v_add_u32_e32 v93, s46, v137
	ds_read_b128 v[238:241], v139 offset:0
	ds_read_b128 v[242:245], v139 offset:2048
	ds_read_b128 v[246:249], v139 offset:4096
	ds_read_b128 v[250:253], v139 offset:6144
	ds_read_b128 v[218:221], v91 offset:0
	ds_read_b128 v[222:225], v91 offset:2048
	ds_read_b128 v[226:229], v91 offset:4096
	ds_read_b128 v[230:233], v91 offset:6144
	ds_read_b128 v[234:237], v91 offset:8192
	s_add_i32 s49, s48, s74
	s_add_i32 s52, s52, 1
	s_and_b32 s54, s52, 7
	s_cmp_eq_u32 s54, 0
	s_cselect_b32 s54, s53, s32
	s_cselect_b32 s55, -1, 0
	s_add_u32 s30, s30, s54
	s_addc_u32 s31, s31, s55
	s_waitcnt lgkmcnt(0)
	v_mfma_f32_16x16x32_bf16 v[78:81], v[238:241], v[218:221], v[78:81]
	v_mfma_f32_16x16x32_bf16 v[74:77], v[242:245], v[218:221], v[74:77]
	v_mfma_f32_16x16x32_bf16 v[70:73], v[246:249], v[218:221], v[70:73]
	v_mfma_f32_16x16x32_bf16 v[66:69], v[250:253], v[218:221], v[66:69]
	ds_read_b128 v[218:221], v93 offset:0
	ds_read_b128 v[142:145], v141 offset:0
	s_mov_b32 m0, s49
	s_nop 0
	global_load_lds_dwordx4 v88, s[30:31]
	v_mfma_f32_16x16x32_bf16 v[62:65], v[238:241], v[222:225], v[62:65]
	v_mfma_f32_16x16x32_bf16 v[58:61], v[242:245], v[222:225], v[58:61]
	v_mfma_f32_16x16x32_bf16 v[54:57], v[246:249], v[222:225], v[54:57]
	v_mfma_f32_16x16x32_bf16 v[50:53], v[250:253], v[222:225], v[50:53]
	ds_read_b128 v[222:225], v93 offset:2048
	ds_read_b128 v[146:149], v141 offset:2048
	s_add_i32 m0, s49, 0x2000
	s_nop 0
	global_load_lds_dwordx4 v90, s[30:31]
	v_mfma_f32_16x16x32_bf16 v[46:49], v[238:241], v[226:229], v[46:49]
	v_mfma_f32_16x16x32_bf16 v[42:45], v[242:245], v[226:229], v[42:45]
	v_mfma_f32_16x16x32_bf16 v[38:41], v[246:249], v[226:229], v[38:41]
	v_mfma_f32_16x16x32_bf16 v[34:37], v[250:253], v[226:229], v[34:37]
	ds_read_b128 v[226:229], v93 offset:4096
	ds_read_b128 v[156:159], v141 offset:4096
	s_add_i32 m0, s49, 0x4000
	s_nop 0
	global_load_lds_dwordx4 v92, s[30:31]
	v_mfma_f32_16x16x32_bf16 v[18:21], v[238:241], v[230:233], v[18:21]
	v_mfma_f32_16x16x32_bf16 v[22:25], v[242:245], v[230:233], v[22:25]
	v_mfma_f32_16x16x32_bf16 v[26:29], v[246:249], v[230:233], v[26:29]
	v_mfma_f32_16x16x32_bf16 v[30:33], v[250:253], v[230:233], v[30:33]
	ds_read_b128 v[230:233], v93 offset:6144
	ds_read_b128 v[160:163], v141 offset:6144
	s_add_i32 m0, s49, 0x6000
	s_nop 0
	global_load_lds_dwordx4 v94, s[30:31]
	v_mfma_f32_16x16x32_bf16 v[2:5], v[238:241], v[234:237], v[2:5]
	v_mfma_f32_16x16x32_bf16 v[6:9], v[242:245], v[234:237], v[6:9]
	v_mfma_f32_16x16x32_bf16 v[10:13], v[246:249], v[234:237], v[10:13]
	v_mfma_f32_16x16x32_bf16 v[14:17], v[250:253], v[234:237], v[14:17]
	ds_read_b128 v[234:237], v93 offset:8192
	s_add_i32 m0, s49, 0x8000
	s_nop 0
	global_load_lds_dwordx4 v96, s[30:31]
	s_waitcnt lgkmcnt(0)
	v_mfma_f32_16x16x32_bf16 v[78:81], v[142:145], v[218:221], v[78:81]
	v_mfma_f32_16x16x32_bf16 v[74:77], v[146:149], v[218:221], v[74:77]
	v_mfma_f32_16x16x32_bf16 v[70:73], v[156:159], v[218:221], v[70:73]
	v_mfma_f32_16x16x32_bf16 v[66:69], v[160:163], v[218:221], v[66:69]
	v_mfma_f32_16x16x32_bf16 v[62:65], v[142:145], v[222:225], v[62:65]
	v_mfma_f32_16x16x32_bf16 v[58:61], v[146:149], v[222:225], v[58:61]
	v_mfma_f32_16x16x32_bf16 v[54:57], v[156:159], v[222:225], v[54:57]
	v_mfma_f32_16x16x32_bf16 v[50:53], v[160:163], v[222:225], v[50:53]
	v_mfma_f32_16x16x32_bf16 v[46:49], v[142:145], v[226:229], v[46:49]
	v_mfma_f32_16x16x32_bf16 v[42:45], v[146:149], v[226:229], v[42:45]
	v_mfma_f32_16x16x32_bf16 v[38:41], v[156:159], v[226:229], v[38:41]
	v_mfma_f32_16x16x32_bf16 v[34:37], v[160:163], v[226:229], v[34:37]
	v_mfma_f32_16x16x32_bf16 v[18:21], v[142:145], v[230:233], v[18:21]
	v_mfma_f32_16x16x32_bf16 v[22:25], v[146:149], v[230:233], v[22:25]
	v_mfma_f32_16x16x32_bf16 v[26:29], v[156:159], v[230:233], v[26:29]
	v_mfma_f32_16x16x32_bf16 v[30:33], v[160:163], v[230:233], v[30:33]
	v_mfma_f32_16x16x32_bf16 v[2:5], v[142:145], v[234:237], v[2:5]
	v_mfma_f32_16x16x32_bf16 v[6:9], v[146:149], v[234:237], v[6:9]
	v_mfma_f32_16x16x32_bf16 v[10:13], v[156:159], v[234:237], v[10:13]
	v_mfma_f32_16x16x32_bf16 v[14:17], v[160:163], v[234:237], v[14:17]
	s_waitcnt vmcnt(5)
	s_mov_b32 s49, s46
	s_mov_b32 s46, s47
	s_mov_b32 s47, s48
	s_mov_b32 s48, s49
	s_add_i32 s50, s50, 1
	s_waitcnt lgkmcnt(0)
	s_barrier
; #define MD_GLDS_A(buf, tau) do { _Pragma("unroll") for (int i = 0; i < 5; ++i) if (amask & (1u << i)) \
;         __builtin_amdgcn_global_load_lds((const unsigned*)((const char*)HIDp + aoff[i] + (size_t)((tau) & 7) * 128), (PG8_LAS unsigned*)(MD_SA(buf) + wid * 1024 + i * 8192), 16, 0, 0); } while (0)
; #define MD_B_ISSUE(sb, tau) do { const char* kb_ = Bb + (size_t)((tau) >> 3) * 512 + (size_t)((tau) & 7) * (64 * (size_t)RB); _Pragma("unroll") for (int j = 0; j < 8; ++j) { const char* p_ = kb_ + (size_t)j * RB; \
;         asm volatile("global_load_dwordx2 %0, %1, off" : "=&v"(sb[j]) : "v"(p_) : "memory"); } } while (0)
; #define MD_B_WAIT(sb, N) asm volatile("s_waitcnt vmcnt(%8)" : "+v"(sb[0]), "+v"(sb[1]), "+v"(sb[2]), "+v"(sb[3]), "+v"(sb[4]), "+v"(sb[5]), "+v"(sb[6]), "+v"(sb[7]) : "n"(N) : "memory")
; #define MD_END(last) do { if (last) asm volatile("s_waitcnt vmcnt(0)" ::: "memory"); else asm volatile("s_waitcnt vmcnt(8)" ::: "memory"); \
;         asm volatile("s_waitcnt lgkmcnt(0)" ::: "memory"); __builtin_amdgcn_s_barrier(); asm volatile("" ::: "memory"); } while (0)
; __device__ __forceinline__ void moe_down_stream(PG8_LAS unsigned char* lds, int e, int cb0, int slot0, int nv, const bf16_t* HIDp, const float* Wd, bf16_t* Y, const float* slot_w, const int* slot_dst) {
;     ...
;     for (int t = 0; t < NT; t += 2) {
;         if (t + 2 < NT) MD_B_WAIT(s1, 8); else MD_B_WAIT(s1, 0);
;         MD_B_WRITE(s1, 1); __builtin_amdgcn_sched_barrier(0); MD_GLDS_A(1, t + 1); __builtin_amdgcn_sched_barrier(0);
;         if (t + 3 < NT) MD_B_ISSUE(s1, t + 3);
;         MD_COMPUTE(0);
;         MD_END(t + 3 >= NT);
;         if (t + 2 < NT) { MD_B_WAIT(s0, 8); MD_B_WRITE(s0, 0); __builtin_amdgcn_sched_barrier(0); MD_GLDS_A(0, t + 2); __builtin_amdgcn_sched_barrier(0); }
;         if (t + 4 < NT) MD_B_ISSUE(s0, t + 4);
;         MD_COMPUTE(1);
;         MD_END(t + 4 >= NT);
	v_cvt_pk_bf16_f32 v172, v186, v188
	v_cvt_pk_bf16_f32 v173, v190, v192
	v_cvt_pk_bf16_f32 v174, v194, v196
	v_cvt_pk_bf16_f32 v175, v198, v200
	v_cvt_pk_bf16_f32 v176, v187, v189
	v_cvt_pk_bf16_f32 v177, v191, v193
	v_cvt_pk_bf16_f32 v178, v195, v197
	v_cvt_pk_bf16_f32 v179, v199, v201
	ds_write_b128 v95, v[172:175] offset:0
	ds_write_b128 v95, v[176:179] offset:128
	v_add_u32_e32 v91, s46, v135
	v_add_u32_e32 v93, s46, v137
	ds_read_b128 v[238:241], v139 offset:19456
	ds_read_b128 v[242:245], v139 offset:21504
	ds_read_b128 v[246:249], v139 offset:23552
	ds_read_b128 v[250:253], v139 offset:25600
	ds_read_b128 v[218:221], v91 offset:0
	ds_read_b128 v[222:225], v91 offset:2048
	ds_read_b128 v[226:229], v91 offset:4096
	ds_read_b128 v[230:233], v91 offset:6144
	ds_read_b128 v[234:237], v91 offset:8192
	s_add_i32 s49, s48, s74
	s_add_i32 s52, s52, 1
	s_and_b32 s54, s52, 7
	s_cmp_eq_u32 s54, 0
	s_cselect_b32 s54, s53, s32
	s_cselect_b32 s55, -1, 0
	s_add_u32 s30, s30, s54
	s_addc_u32 s31, s31, s55
	s_waitcnt lgkmcnt(0)
	v_mfma_f32_16x16x32_bf16 v[78:81], v[238:241], v[218:221], v[78:81]
	v_mfma_f32_16x16x32_bf16 v[74:77], v[242:245], v[218:221], v[74:77]
	v_mfma_f32_16x16x32_bf16 v[70:73], v[246:249], v[218:221], v[70:73]
	v_mfma_f32_16x16x32_bf16 v[66:69], v[250:253], v[218:221], v[66:69]
	ds_read_b128 v[218:221], v93 offset:0
	ds_read_b128 v[142:145], v141 offset:19456
	s_mov_b32 m0, s49
	s_nop 0
	global_load_lds_dwordx4 v88, s[30:31]
	v_mfma_f32_16x16x32_bf16 v[62:65], v[238:241], v[222:225], v[62:65]
	v_mfma_f32_16x16x32_bf16 v[58:61], v[242:245], v[222:225], v[58:61]
	v_mfma_f32_16x16x32_bf16 v[54:57], v[246:249], v[222:225], v[54:57]
	v_mfma_f32_16x16x32_bf16 v[50:53], v[250:253], v[222:225], v[50:53]
	ds_read_b128 v[222:225], v93 offset:2048
	ds_read_b128 v[146:149], v141 offset:21504
	s_add_i32 m0, s49, 0x2000
	s_nop 0
	global_load_lds_dwordx4 v90, s[30:31]
	v_mfma_f32_16x16x32_bf16 v[46:49], v[238:241], v[226:229], v[46:49]
	v_mfma_f32_16x16x32_bf16 v[42:45], v[242:245], v[226:229], v[42:45]
	v_mfma_f32_16x16x32_bf16 v[38:41], v[246:249], v[226:229], v[38:41]
	v_mfma_f32_16x16x32_bf16 v[34:37], v[250:253], v[226:229], v[34:37]
	ds_read_b128 v[226:229], v93 offset:4096
	ds_read_b128 v[156:159], v141 offset:23552
	s_add_i32 m0, s49, 0x4000
	s_nop 0
	global_load_lds_dwordx4 v92, s[30:31]
	v_mfma_f32_16x16x32_bf16 v[18:21], v[238:241], v[230:233], v[18:21]
	v_mfma_f32_16x16x32_bf16 v[22:25], v[242:245], v[230:233], v[22:25]
	v_mfma_f32_16x16x32_bf16 v[26:29], v[246:249], v[230:233], v[26:29]
	v_mfma_f32_16x16x32_bf16 v[30:33], v[250:253], v[230:233], v[30:33]
	ds_read_b128 v[230:233], v93 offset:6144
	ds_read_b128 v[160:163], v141 offset:25600
	s_add_i32 m0, s49, 0x6000
	s_nop 0
	global_load_lds_dwordx4 v94, s[30:31]
	v_mfma_f32_16x16x32_bf16 v[2:5], v[238:241], v[234:237], v[2:5]
	v_mfma_f32_16x16x32_bf16 v[6:9], v[242:245], v[234:237], v[6:9]
	v_mfma_f32_16x16x32_bf16 v[10:13], v[246:249], v[234:237], v[10:13]
	v_mfma_f32_16x16x32_bf16 v[14:17], v[250:253], v[234:237], v[14:17]
	ds_read_b128 v[234:237], v93 offset:8192
	s_add_i32 m0, s49, 0x8000
	s_nop 0
	global_load_lds_dwordx4 v96, s[30:31]
	s_waitcnt lgkmcnt(0)
	v_mfma_f32_16x16x32_bf16 v[78:81], v[142:145], v[218:221], v[78:81]
	v_mfma_f32_16x16x32_bf16 v[74:77], v[146:149], v[218:221], v[74:77]
	v_mfma_f32_16x16x32_bf16 v[70:73], v[156:159], v[218:221], v[70:73]
	v_mfma_f32_16x16x32_bf16 v[66:69], v[160:163], v[218:221], v[66:69]
	v_mfma_f32_16x16x32_bf16 v[62:65], v[142:145], v[222:225], v[62:65]
	v_mfma_f32_16x16x32_bf16 v[58:61], v[146:149], v[222:225], v[58:61]
	v_mfma_f32_16x16x32_bf16 v[54:57], v[156:159], v[222:225], v[54:57]
	v_mfma_f32_16x16x32_bf16 v[50:53], v[160:163], v[222:225], v[50:53]
	v_mfma_f32_16x16x32_bf16 v[46:49], v[142:145], v[226:229], v[46:49]
	v_mfma_f32_16x16x32_bf16 v[42:45], v[146:149], v[226:229], v[42:45]
	v_mfma_f32_16x16x32_bf16 v[38:41], v[156:159], v[226:229], v[38:41]
	v_mfma_f32_16x16x32_bf16 v[34:37], v[160:163], v[226:229], v[34:37]
	v_mfma_f32_16x16x32_bf16 v[18:21], v[142:145], v[230:233], v[18:21]
	v_mfma_f32_16x16x32_bf16 v[22:25], v[146:149], v[230:233], v[22:25]
	v_mfma_f32_16x16x32_bf16 v[26:29], v[156:159], v[230:233], v[26:29]
	v_mfma_f32_16x16x32_bf16 v[30:33], v[160:163], v[230:233], v[30:33]
	v_mfma_f32_16x16x32_bf16 v[2:5], v[142:145], v[234:237], v[2:5]
	v_mfma_f32_16x16x32_bf16 v[6:9], v[146:149], v[234:237], v[6:9]
	v_mfma_f32_16x16x32_bf16 v[10:13], v[156:159], v[234:237], v[10:13]
	v_mfma_f32_16x16x32_bf16 v[14:17], v[160:163], v[234:237], v[14:17]
	s_waitcnt vmcnt(5)
	s_mov_b32 s49, s46
	s_mov_b32 s46, s47
	s_mov_b32 s47, s48
	s_mov_b32 s48, s49
	s_add_i32 s50, s50, 1
	s_waitcnt lgkmcnt(0)
	s_barrier
; #define MD_GLDS_A(buf, tau) do { _Pragma("unroll") for (int i = 0; i < 5; ++i) if (amask & (1u << i)) \
;         __builtin_amdgcn_global_load_lds((const unsigned*)((const char*)HIDp + aoff[i] + (size_t)((tau) & 7) * 128), (PG8_LAS unsigned*)(MD_SA(buf) + wid * 1024 + i * 8192), 16, 0, 0); } while (0)
; #define MD_B_ISSUE(sb, tau) do { const char* kb_ = Bb + (size_t)((tau) >> 3) * 512 + (size_t)((tau) & 7) * (64 * (size_t)RB); _Pragma("unroll") for (int j = 0; j < 8; ++j) { const char* p_ = kb_ + (size_t)j * RB; \
;         asm volatile("global_load_dwordx2 %0, %1, off" : "=&v"(sb[j]) : "v"(p_) : "memory"); } } while (0)
; #define MD_B_WAIT(sb, N) asm volatile("s_waitcnt vmcnt(%8)" : "+v"(sb[0]), "+v"(sb[1]), "+v"(sb[2]), "+v"(sb[3]), "+v"(sb[4]), "+v"(sb[5]), "+v"(sb[6]), "+v"(sb[7]) : "n"(N) : "memory")
; #define MD_END(last) do { if (last) asm volatile("s_waitcnt vmcnt(0)" ::: "memory"); else asm volatile("s_waitcnt vmcnt(8)" ::: "memory"); \
;         asm volatile("s_waitcnt lgkmcnt(0)" ::: "memory"); __builtin_amdgcn_s_barrier(); asm volatile("" ::: "memory"); } while (0)
; __device__ __forceinline__ void moe_down_stream(PG8_LAS unsigned char* lds, int e, int cb0, int slot0, int nv, const bf16_t* HIDp, const float* Wd, bf16_t* Y, const float* slot_w, const int* slot_dst) {
;     ...
;     for (int t = 0; t < NT; t += 2) {
;         if (t + 2 < NT) MD_B_WAIT(s1, 8); else MD_B_WAIT(s1, 0);
;         MD_B_WRITE(s1, 1); __builtin_amdgcn_sched_barrier(0); MD_GLDS_A(1, t + 1); __builtin_amdgcn_sched_barrier(0);
;         if (t + 3 < NT) MD_B_ISSUE(s1, t + 3);
;         MD_COMPUTE(0);
;         MD_END(t + 3 >= NT);
;         if (t + 2 < NT) { MD_B_WAIT(s0, 8); MD_B_WRITE(s0, 0); __builtin_amdgcn_sched_barrier(0); MD_GLDS_A(0, t + 2); __builtin_amdgcn_sched_barrier(0); }
;         if (t + 4 < NT) MD_B_ISSUE(s0, t + 4);
;         MD_COMPUTE(1);
;         MD_END(t + 4 >= NT);
	v_cvt_pk_bf16_f32 v172, v202, v204
	v_cvt_pk_bf16_f32 v173, v206, v208
	v_cvt_pk_bf16_f32 v174, v210, v212
	v_cvt_pk_bf16_f32 v175, v214, v216
	v_cvt_pk_bf16_f32 v176, v203, v205
	v_cvt_pk_bf16_f32 v177, v207, v209
	v_cvt_pk_bf16_f32 v178, v211, v213
	v_cvt_pk_bf16_f32 v179, v215, v217
	ds_write_b128 v95, v[172:175] offset:19456
	ds_write_b128 v95, v[176:179] offset:19584
	v_add_u32_e32 v91, s46, v135
	v_add_u32_e32 v93, s46, v137
	ds_read_b128 v[238:241], v139 offset:0
	ds_read_b128 v[242:245], v139 offset:2048
	ds_read_b128 v[246:249], v139 offset:4096
	ds_read_b128 v[250:253], v139 offset:6144
	ds_read_b128 v[218:221], v91 offset:0
	ds_read_b128 v[222:225], v91 offset:2048
	ds_read_b128 v[226:229], v91 offset:4096
	ds_read_b128 v[230:233], v91 offset:6144
	ds_read_b128 v[234:237], v91 offset:8192
	s_waitcnt lgkmcnt(0)
	v_mfma_f32_16x16x32_bf16 v[78:81], v[238:241], v[218:221], v[78:81]
	v_mfma_f32_16x16x32_bf16 v[74:77], v[242:245], v[218:221], v[74:77]
	v_mfma_f32_16x16x32_bf16 v[70:73], v[246:249], v[218:221], v[70:73]
	v_mfma_f32_16x16x32_bf16 v[66:69], v[250:253], v[218:221], v[66:69]
	ds_read_b128 v[218:221], v93 offset:0
	ds_read_b128 v[142:145], v141 offset:0
	v_mfma_f32_16x16x32_bf16 v[62:65], v[238:241], v[222:225], v[62:65]
	v_mfma_f32_16x16x32_bf16 v[58:61], v[242:245], v[222:225], v[58:61]
	v_mfma_f32_16x16x32_bf16 v[54:57], v[246:249], v[222:225], v[54:57]
	v_mfma_f32_16x16x32_bf16 v[50:53], v[250:253], v[222:225], v[50:53]
	ds_read_b128 v[222:225], v93 offset:2048
	ds_read_b128 v[146:149], v141 offset:2048
	v_mfma_f32_16x16x32_bf16 v[46:49], v[238:241], v[226:229], v[46:49]
	v_mfma_f32_16x16x32_bf16 v[42:45], v[242:245], v[226:229], v[42:45]
	v_mfma_f32_16x16x32_bf16 v[38:41], v[246:249], v[226:229], v[38:41]
	v_mfma_f32_16x16x32_bf16 v[34:37], v[250:253], v[226:229], v[34:37]
	ds_read_b128 v[226:229], v93 offset:4096
	ds_read_b128 v[156:159], v141 offset:4096
	v_mfma_f32_16x16x32_bf16 v[18:21], v[238:241], v[230:233], v[18:21]
	v_mfma_f32_16x16x32_bf16 v[22:25], v[242:245], v[230:233], v[22:25]
	v_mfma_f32_16x16x32_bf16 v[26:29], v[246:249], v[230:233], v[26:29]
	v_mfma_f32_16x16x32_bf16 v[30:33], v[250:253], v[230:233], v[30:33]
	ds_read_b128 v[230:233], v93 offset:6144
	ds_read_b128 v[160:163], v141 offset:6144
	v_mfma_f32_16x16x32_bf16 v[2:5], v[238:241], v[234:237], v[2:5]
	v_mfma_f32_16x16x32_bf16 v[6:9], v[242:245], v[234:237], v[6:9]
	v_mfma_f32_16x16x32_bf16 v[10:13], v[246:249], v[234:237], v[10:13]
	v_mfma_f32_16x16x32_bf16 v[14:17], v[250:253], v[234:237], v[14:17]
	ds_read_b128 v[234:237], v93 offset:8192
	s_waitcnt lgkmcnt(0)
	v_mfma_f32_16x16x32_bf16 v[78:81], v[142:145], v[218:221], v[78:81]
	v_mfma_f32_16x16x32_bf16 v[74:77], v[146:149], v[218:221], v[74:77]
	v_mfma_f32_16x16x32_bf16 v[70:73], v[156:159], v[218:221], v[70:73]
	v_mfma_f32_16x16x32_bf16 v[66:69], v[160:163], v[218:221], v[66:69]
	v_mfma_f32_16x16x32_bf16 v[62:65], v[142:145], v[222:225], v[62:65]
	v_mfma_f32_16x16x32_bf16 v[58:61], v[146:149], v[222:225], v[58:61]
	v_mfma_f32_16x16x32_bf16 v[54:57], v[156:159], v[222:225], v[54:57]
	v_mfma_f32_16x16x32_bf16 v[50:53], v[160:163], v[222:225], v[50:53]
	v_mfma_f32_16x16x32_bf16 v[46:49], v[142:145], v[226:229], v[46:49]
	v_mfma_f32_16x16x32_bf16 v[42:45], v[146:149], v[226:229], v[42:45]
	v_mfma_f32_16x16x32_bf16 v[38:41], v[156:159], v[226:229], v[38:41]
	v_mfma_f32_16x16x32_bf16 v[34:37], v[160:163], v[226:229], v[34:37]
	v_mfma_f32_16x16x32_bf16 v[18:21], v[142:145], v[230:233], v[18:21]
	v_mfma_f32_16x16x32_bf16 v[22:25], v[146:149], v[230:233], v[22:25]
	v_mfma_f32_16x16x32_bf16 v[26:29], v[156:159], v[230:233], v[26:29]
	v_mfma_f32_16x16x32_bf16 v[30:33], v[160:163], v[230:233], v[30:33]
	v_mfma_f32_16x16x32_bf16 v[2:5], v[142:145], v[234:237], v[2:5]
	v_mfma_f32_16x16x32_bf16 v[6:9], v[146:149], v[234:237], v[6:9]
	v_mfma_f32_16x16x32_bf16 v[10:13], v[156:159], v[234:237], v[10:13]
	v_mfma_f32_16x16x32_bf16 v[14:17], v[160:163], v[234:237], v[14:17]
	s_waitcnt vmcnt(0)
	s_mov_b32 s49, s46
	s_mov_b32 s46, s47
	s_mov_b32 s47, s48
	s_mov_b32 s48, s49
	s_add_i32 s50, s50, 1
	s_waitcnt lgkmcnt(0)
	s_barrier
	v_add_u32_e32 v91, s46, v135
	v_add_u32_e32 v93, s46, v137
	ds_read_b128 v[238:241], v139 offset:19456
	ds_read_b128 v[242:245], v139 offset:21504
	ds_read_b128 v[246:249], v139 offset:23552
	ds_read_b128 v[250:253], v139 offset:25600
	ds_read_b128 v[218:221], v91 offset:0
	ds_read_b128 v[222:225], v91 offset:2048
	ds_read_b128 v[226:229], v91 offset:4096
	ds_read_b128 v[230:233], v91 offset:6144
	ds_read_b128 v[234:237], v91 offset:8192
	s_waitcnt lgkmcnt(0)
	v_mfma_f32_16x16x32_bf16 v[78:81], v[238:241], v[218:221], v[78:81]
	v_mfma_f32_16x16x32_bf16 v[74:77], v[242:245], v[218:221], v[74:77]
	v_mfma_f32_16x16x32_bf16 v[70:73], v[246:249], v[218:221], v[70:73]
	v_mfma_f32_16x16x32_bf16 v[66:69], v[250:253], v[218:221], v[66:69]
	ds_read_b128 v[218:221], v93 offset:0
	ds_read_b128 v[142:145], v141 offset:19456
	v_mfma_f32_16x16x32_bf16 v[62:65], v[238:241], v[222:225], v[62:65]
	v_mfma_f32_16x16x32_bf16 v[58:61], v[242:245], v[222:225], v[58:61]
	v_mfma_f32_16x16x32_bf16 v[54:57], v[246:249], v[222:225], v[54:57]
	v_mfma_f32_16x16x32_bf16 v[50:53], v[250:253], v[222:225], v[50:53]
	ds_read_b128 v[222:225], v93 offset:2048
	ds_read_b128 v[146:149], v141 offset:21504
	v_mfma_f32_16x16x32_bf16 v[46:49], v[238:241], v[226:229], v[46:49]
	v_mfma_f32_16x16x32_bf16 v[42:45], v[242:245], v[226:229], v[42:45]
	v_mfma_f32_16x16x32_bf16 v[38:41], v[246:249], v[226:229], v[38:41]
	v_mfma_f32_16x16x32_bf16 v[34:37], v[250:253], v[226:229], v[34:37]
	ds_read_b128 v[226:229], v93 offset:4096
	ds_read_b128 v[156:159], v141 offset:23552
	v_mfma_f32_16x16x32_bf16 v[18:21], v[238:241], v[230:233], v[18:21]
	v_mfma_f32_16x16x32_bf16 v[22:25], v[242:245], v[230:233], v[22:25]
	v_mfma_f32_16x16x32_bf16 v[26:29], v[246:249], v[230:233], v[26:29]
	v_mfma_f32_16x16x32_bf16 v[30:33], v[250:253], v[230:233], v[30:33]
	ds_read_b128 v[230:233], v93 offset:6144
	ds_read_b128 v[160:163], v141 offset:25600
	v_mfma_f32_16x16x32_bf16 v[2:5], v[238:241], v[234:237], v[2:5]
	v_mfma_f32_16x16x32_bf16 v[6:9], v[242:245], v[234:237], v[6:9]
	v_mfma_f32_16x16x32_bf16 v[10:13], v[246:249], v[234:237], v[10:13]
	v_mfma_f32_16x16x32_bf16 v[14:17], v[250:253], v[234:237], v[14:17]
	ds_read_b128 v[234:237], v93 offset:8192
	s_waitcnt lgkmcnt(0)
; #define PG8_LAS __attribute__((address_space(3)))
; __device__ __forceinline__ unsigned cvtpk(float lo, float hi) { f32x2 v = {lo, hi}; bf16x2_t b = __builtin_convertvector(v, bf16x2_t); return __builtin_bit_cast(unsigned, b); }
; __device__ __forceinline__ void moe_down_stream(PG8_LAS unsigned char* lds, int e, int cb0, int slot0, int nv, const bf16_t* HIDp, const float* Wd, bf16_t* Y, const float* slot_w, const int* slot_dst) {
;     ...
;         if (((t + 1) & 7) == 7) {
;             const int cb = cb0 + ((t + 1) >> 3);
; #pragma unroll
;             for (int m = 0; m < DNM; ++m) {
;                 const float w_ = lw[4 * (16 * m + fr) + wr];
; #pragma unroll
;                 for (int p = 0; p < 2; ++p) { const f32x4 v0 = acc[m][2 * p] * w_, v1 = acc[m][2 * p + 1] * w_; u32x4 w; w.x = cvtpk(v0[0], v0[1]); w.y = cvtpk(v0[2], v0[3]); w.z = cvtpk(v1[0], v1[1]); w.w = cvtpk(v1[2], v1[3]);
;                     *(PG8_LAS u32x4*)(stg + fr * 128 + (((4 * p + fq) ^ (fr & 7)) * 16)) = w; }
; #pragma unroll
;                 for (int hh = 0; hh < 2; ++hh) { const int r = (lane >> 3) + 8 * hh, cc = lane & 7; const u32x4 d = *(const PG8_LAS u32x4*)(stg + r * 128 + ((cc ^ (r & 7)) * 16)); const int dst_ = ldst[4 * (16 * m + r) + wr];
;                     if (dst_ >= 0) *(u32x4*)(Y + (size_t)dst_ * D + 128 * cb + 64 * wc + 8 * cc) = d; }
; #pragma unroll
;                 for (int n = 0; n < 4; ++n) acc[m][n] = (f32x4){0.f, 0.f, 0.f, 0.f}; } }
	v_mfma_f32_16x16x32_bf16 v[78:81], v[142:145], v[218:221], v[78:81]
	v_mfma_f32_16x16x32_bf16 v[74:77], v[146:149], v[218:221], v[74:77]
	v_mfma_f32_16x16x32_bf16 v[70:73], v[156:159], v[218:221], v[70:73]
	v_mfma_f32_16x16x32_bf16 v[66:69], v[160:163], v[218:221], v[66:69]
	v_mfma_f32_16x16x32_bf16 v[62:65], v[142:145], v[222:225], v[62:65]
	v_mfma_f32_16x16x32_bf16 v[58:61], v[146:149], v[222:225], v[58:61]
	v_mfma_f32_16x16x32_bf16 v[54:57], v[156:159], v[222:225], v[54:57]
	v_mfma_f32_16x16x32_bf16 v[50:53], v[160:163], v[222:225], v[50:53]
	v_mfma_f32_16x16x32_bf16 v[46:49], v[142:145], v[226:229], v[46:49]
	v_mfma_f32_16x16x32_bf16 v[42:45], v[146:149], v[226:229], v[42:45]
	v_mfma_f32_16x16x32_bf16 v[38:41], v[156:159], v[226:229], v[38:41]
	v_mfma_f32_16x16x32_bf16 v[34:37], v[160:163], v[226:229], v[34:37]
	v_mfma_f32_16x16x32_bf16 v[18:21], v[142:145], v[230:233], v[18:21]
	v_mfma_f32_16x16x32_bf16 v[22:25], v[146:149], v[230:233], v[22:25]
	v_mfma_f32_16x16x32_bf16 v[26:29], v[156:159], v[230:233], v[26:29]
	v_mfma_f32_16x16x32_bf16 v[30:33], v[160:163], v[230:233], v[30:33]
	v_mfma_f32_16x16x32_bf16 v[2:5], v[142:145], v[234:237], v[2:5]
	v_mfma_f32_16x16x32_bf16 v[6:9], v[146:149], v[234:237], v[6:9]
	v_mfma_f32_16x16x32_bf16 v[10:13], v[156:159], v[234:237], v[10:13]
	v_mfma_f32_16x16x32_bf16 v[14:17], v[160:163], v[234:237], v[14:17]
	s_mov_b32 s49, s46
	s_mov_b32 s46, s47
	s_mov_b32 s47, s48
	s_mov_b32 s48, s49
	s_add_i32 s50, s50, 1
	s_waitcnt lgkmcnt(0)
	s_barrier
	s_add_i32 s54, s48, s74
	v_add_u32_e32 v164, s54, v84
	v_add_u32_e32 v165, s54, v85
	ds_read_b32 v150, v82 offset:0
	ds_read_b32 v151, v83 offset:0
	ds_read_b32 v166, v83 offset:128
	s_waitcnt lgkmcnt(2)
	v_mul_f32_e32 v78, v150, v78
	v_mul_f32_e32 v79, v150, v79
	v_mul_f32_e32 v80, v150, v80
	v_mul_f32_e32 v81, v150, v81
	v_mul_f32_e32 v74, v150, v74
	v_mul_f32_e32 v75, v150, v75
	v_mul_f32_e32 v76, v150, v76
	v_mul_f32_e32 v77, v150, v77
	v_cvt_pk_bf16_f32 v182, v78, v79
	v_cvt_pk_bf16_f32 v183, v80, v81
	v_cvt_pk_bf16_f32 v184, v74, v75
	v_cvt_pk_bf16_f32 v185, v76, v77
	ds_write_b128 v164, v[182:185]
	v_mul_f32_e32 v70, v150, v70
	v_mul_f32_e32 v71, v150, v71
	v_mul_f32_e32 v72, v150, v72
	v_mul_f32_e32 v73, v150, v73
	v_mul_f32_e32 v66, v150, v66
	v_mul_f32_e32 v67, v150, v67
	v_mul_f32_e32 v68, v150, v68
	v_mul_f32_e32 v69, v150, v69
	v_cvt_pk_bf16_f32 v182, v70, v71
	v_cvt_pk_bf16_f32 v183, v72, v73
	v_cvt_pk_bf16_f32 v184, v66, v67
	v_cvt_pk_bf16_f32 v185, v68, v69
	v_xor_b32_e32 v167, 64, v164
	ds_write_b128 v167, v[182:185]
	v_mov_b32_e32 v78, 0
	v_mov_b32_e32 v74, 0
	v_mov_b32_e32 v70, 0
	v_mov_b32_e32 v66, 0
	v_mov_b32_e32 v79, 0
	v_mov_b32_e32 v75, 0
	v_mov_b32_e32 v71, 0
	v_mov_b32_e32 v67, 0
	v_mov_b32_e32 v80, 0
	v_mov_b32_e32 v76, 0
	v_mov_b32_e32 v72, 0
	v_mov_b32_e32 v68, 0
	v_mov_b32_e32 v81, 0
	v_mov_b32_e32 v77, 0
	v_mov_b32_e32 v73, 0
	v_mov_b32_e32 v69, 0
	ds_read_b128 v[182:185], v165 offset:0
	v_cmp_lt_i32_e32 vcc, -1, v151
	v_lshlrev_b32_e32 v148, 13, v151
	v_mov_b32_e32 v149, 0
	v_lshl_add_u64 v[148:149], v[148:149], 0, v[86:87]
	v_cndmask_b32_e32 v148, v168, v148, vcc
	v_cndmask_b32_e32 v149, v169, v149, vcc
	s_waitcnt lgkmcnt(0)
	global_store_dwordx4 v[148:149], v[182:185], off
	ds_read_b128 v[182:185], v165 offset:8192
	v_cmp_lt_i32_e32 vcc, -1, v166
	v_lshlrev_b32_e32 v148, 13, v166
	v_mov_b32_e32 v149, 0
	v_lshl_add_u64 v[148:149], v[148:149], 0, v[86:87]
	v_cndmask_b32_e32 v148, v168, v148, vcc
	v_cndmask_b32_e32 v149, v169, v149, vcc
	s_waitcnt lgkmcnt(0)
	global_store_dwordx4 v[148:149], v[182:185], off
	ds_read_b32 v150, v82 offset:256
	ds_read_b32 v151, v83 offset:256
	ds_read_b32 v166, v83 offset:384
	s_waitcnt lgkmcnt(2)
	v_mul_f32_e32 v62, v150, v62
	v_mul_f32_e32 v63, v150, v63
	v_mul_f32_e32 v64, v150, v64
	v_mul_f32_e32 v65, v150, v65
	v_mul_f32_e32 v58, v150, v58
	v_mul_f32_e32 v59, v150, v59
	v_mul_f32_e32 v60, v150, v60
	v_mul_f32_e32 v61, v150, v61
	v_cvt_pk_bf16_f32 v182, v62, v63
	v_cvt_pk_bf16_f32 v183, v64, v65
	v_cvt_pk_bf16_f32 v184, v58, v59
	v_cvt_pk_bf16_f32 v185, v60, v61
	ds_write_b128 v164, v[182:185]
	v_mul_f32_e32 v54, v150, v54
	v_mul_f32_e32 v55, v150, v55
	v_mul_f32_e32 v56, v150, v56
	v_mul_f32_e32 v57, v150, v57
	v_mul_f32_e32 v50, v150, v50
	v_mul_f32_e32 v51, v150, v51
	v_mul_f32_e32 v52, v150, v52
	v_mul_f32_e32 v53, v150, v53
	v_cvt_pk_bf16_f32 v182, v54, v55
	v_cvt_pk_bf16_f32 v183, v56, v57
	v_cvt_pk_bf16_f32 v184, v50, v51
	v_cvt_pk_bf16_f32 v185, v52, v53
	v_xor_b32_e32 v167, 64, v164
	ds_write_b128 v167, v[182:185]
	v_mov_b32_e32 v62, 0
	v_mov_b32_e32 v58, 0
	v_mov_b32_e32 v54, 0
	v_mov_b32_e32 v50, 0
	v_mov_b32_e32 v63, 0
	v_mov_b32_e32 v59, 0
	v_mov_b32_e32 v55, 0
	v_mov_b32_e32 v51, 0
	v_mov_b32_e32 v64, 0
	v_mov_b32_e32 v60, 0
	v_mov_b32_e32 v56, 0
	v_mov_b32_e32 v52, 0
	v_mov_b32_e32 v65, 0
	v_mov_b32_e32 v61, 0
	v_mov_b32_e32 v57, 0
	v_mov_b32_e32 v53, 0
	ds_read_b128 v[182:185], v165 offset:0
	v_cmp_lt_i32_e32 vcc, -1, v151
	v_lshlrev_b32_e32 v148, 13, v151
	v_mov_b32_e32 v149, 0
	v_lshl_add_u64 v[148:149], v[148:149], 0, v[86:87]
	v_cndmask_b32_e32 v148, v168, v148, vcc
	v_cndmask_b32_e32 v149, v169, v149, vcc
	s_waitcnt lgkmcnt(0)
	global_store_dwordx4 v[148:149], v[182:185], off
	ds_read_b128 v[182:185], v165 offset:8192
	v_cmp_lt_i32_e32 vcc, -1, v166
	v_lshlrev_b32_e32 v148, 13, v166
	v_mov_b32_e32 v149, 0
	v_lshl_add_u64 v[148:149], v[148:149], 0, v[86:87]
	v_cndmask_b32_e32 v148, v168, v148, vcc
	v_cndmask_b32_e32 v149, v169, v149, vcc
	s_waitcnt lgkmcnt(0)
	global_store_dwordx4 v[148:149], v[182:185], off
	ds_read_b32 v150, v82 offset:512
	ds_read_b32 v151, v83 offset:512
	ds_read_b32 v166, v83 offset:640
	s_waitcnt lgkmcnt(2)
; #define PG8_LAS __attribute__((address_space(3)))
; __device__ __forceinline__ unsigned cvtpk(float lo, float hi) { f32x2 v = {lo, hi}; bf16x2_t b = __builtin_convertvector(v, bf16x2_t); return __builtin_bit_cast(unsigned, b); }
; __device__ __forceinline__ void moe_down_stream(PG8_LAS unsigned char* lds, int e, int cb0, int slot0, int nv, const bf16_t* HIDp, const float* Wd, bf16_t* Y, const float* slot_w, const int* slot_dst) {
;     ...
;         if (((t + 1) & 7) == 7) {
;             const int cb = cb0 + ((t + 1) >> 3);
; #pragma unroll
;             for (int m = 0; m < DNM; ++m) {
;                 const float w_ = lw[4 * (16 * m + fr) + wr];
; #pragma unroll
;                 for (int p = 0; p < 2; ++p) { const f32x4 v0 = acc[m][2 * p] * w_, v1 = acc[m][2 * p + 1] * w_; u32x4 w; w.x = cvtpk(v0[0], v0[1]); w.y = cvtpk(v0[2], v0[3]); w.z = cvtpk(v1[0], v1[1]); w.w = cvtpk(v1[2], v1[3]);
;                     *(PG8_LAS u32x4*)(stg + fr * 128 + (((4 * p + fq) ^ (fr & 7)) * 16)) = w; }
; #pragma unroll
;                 for (int hh = 0; hh < 2; ++hh) { const int r = (lane >> 3) + 8 * hh, cc = lane & 7; const u32x4 d = *(const PG8_LAS u32x4*)(stg + r * 128 + ((cc ^ (r & 7)) * 16)); const int dst_ = ldst[4 * (16 * m + r) + wr];
;                     if (dst_ >= 0) *(u32x4*)(Y + (size_t)dst_ * D + 128 * cb + 64 * wc + 8 * cc) = d; }
; #pragma unroll
;                 for (int n = 0; n < 4; ++n) acc[m][n] = (f32x4){0.f, 0.f, 0.f, 0.f}; } }
	v_mul_f32_e32 v46, v150, v46
	v_mul_f32_e32 v47, v150, v47
	v_mul_f32_e32 v48, v150, v48
	v_mul_f32_e32 v49, v150, v49
	v_mul_f32_e32 v42, v150, v42
	v_mul_f32_e32 v43, v150, v43
	v_mul_f32_e32 v44, v150, v44
	v_mul_f32_e32 v45, v150, v45
	v_cvt_pk_bf16_f32 v182, v46, v47
	v_cvt_pk_bf16_f32 v183, v48, v49
	v_cvt_pk_bf16_f32 v184, v42, v43
	v_cvt_pk_bf16_f32 v185, v44, v45
	ds_write_b128 v164, v[182:185]
	v_mul_f32_e32 v38, v150, v38
	v_mul_f32_e32 v39, v150, v39
	v_mul_f32_e32 v40, v150, v40
	v_mul_f32_e32 v41, v150, v41
	v_mul_f32_e32 v34, v150, v34
	v_mul_f32_e32 v35, v150, v35
	v_mul_f32_e32 v36, v150, v36
	v_mul_f32_e32 v37, v150, v37
	v_cvt_pk_bf16_f32 v182, v38, v39
	v_cvt_pk_bf16_f32 v183, v40, v41
	v_cvt_pk_bf16_f32 v184, v34, v35
	v_cvt_pk_bf16_f32 v185, v36, v37
	v_xor_b32_e32 v167, 64, v164
	ds_write_b128 v167, v[182:185]
	v_mov_b32_e32 v46, 0
	v_mov_b32_e32 v42, 0
	v_mov_b32_e32 v38, 0
	v_mov_b32_e32 v34, 0
	v_mov_b32_e32 v47, 0
	v_mov_b32_e32 v43, 0
	v_mov_b32_e32 v39, 0
	v_mov_b32_e32 v35, 0
	v_mov_b32_e32 v48, 0
	v_mov_b32_e32 v44, 0
	v_mov_b32_e32 v40, 0
	v_mov_b32_e32 v36, 0
	v_mov_b32_e32 v49, 0
	v_mov_b32_e32 v45, 0
	v_mov_b32_e32 v41, 0
	v_mov_b32_e32 v37, 0
	ds_read_b128 v[182:185], v165 offset:0
	v_cmp_lt_i32_e32 vcc, -1, v151
	v_lshlrev_b32_e32 v148, 13, v151
	v_mov_b32_e32 v149, 0
	v_lshl_add_u64 v[148:149], v[148:149], 0, v[86:87]
	v_cndmask_b32_e32 v148, v168, v148, vcc
	v_cndmask_b32_e32 v149, v169, v149, vcc
	s_waitcnt lgkmcnt(0)
	global_store_dwordx4 v[148:149], v[182:185], off
	ds_read_b128 v[182:185], v165 offset:8192
	v_cmp_lt_i32_e32 vcc, -1, v166
	v_lshlrev_b32_e32 v148, 13, v166
	v_mov_b32_e32 v149, 0
	v_lshl_add_u64 v[148:149], v[148:149], 0, v[86:87]
	v_cndmask_b32_e32 v148, v168, v148, vcc
	v_cndmask_b32_e32 v149, v169, v149, vcc
	s_waitcnt lgkmcnt(0)
	global_store_dwordx4 v[148:149], v[182:185], off
	ds_read_b32 v150, v82 offset:768
	ds_read_b32 v151, v83 offset:768
	ds_read_b32 v166, v83 offset:896
	s_waitcnt lgkmcnt(2)
	v_mul_f32_e32 v18, v150, v18
	v_mul_f32_e32 v19, v150, v19
	v_mul_f32_e32 v20, v150, v20
	v_mul_f32_e32 v21, v150, v21
	v_mul_f32_e32 v22, v150, v22
	v_mul_f32_e32 v23, v150, v23
	v_mul_f32_e32 v24, v150, v24
	v_mul_f32_e32 v25, v150, v25
	v_cvt_pk_bf16_f32 v182, v18, v19
	v_cvt_pk_bf16_f32 v183, v20, v21
	v_cvt_pk_bf16_f32 v184, v22, v23
	v_cvt_pk_bf16_f32 v185, v24, v25
	ds_write_b128 v164, v[182:185]
	v_mul_f32_e32 v26, v150, v26
	v_mul_f32_e32 v27, v150, v27
	v_mul_f32_e32 v28, v150, v28
	v_mul_f32_e32 v29, v150, v29
	v_mul_f32_e32 v30, v150, v30
	v_mul_f32_e32 v31, v150, v31
	v_mul_f32_e32 v32, v150, v32
	v_mul_f32_e32 v33, v150, v33
	v_cvt_pk_bf16_f32 v182, v26, v27
	v_cvt_pk_bf16_f32 v183, v28, v29
	v_cvt_pk_bf16_f32 v184, v30, v31
	v_cvt_pk_bf16_f32 v185, v32, v33
	v_xor_b32_e32 v167, 64, v164
	ds_write_b128 v167, v[182:185]
	v_mov_b32_e32 v18, 0
	v_mov_b32_e32 v22, 0
	v_mov_b32_e32 v26, 0
	v_mov_b32_e32 v30, 0
	v_mov_b32_e32 v19, 0
	v_mov_b32_e32 v23, 0
	v_mov_b32_e32 v27, 0
	v_mov_b32_e32 v31, 0
	v_mov_b32_e32 v20, 0
	v_mov_b32_e32 v24, 0
	v_mov_b32_e32 v28, 0
	v_mov_b32_e32 v32, 0
	v_mov_b32_e32 v21, 0
	v_mov_b32_e32 v25, 0
	v_mov_b32_e32 v29, 0
	v_mov_b32_e32 v33, 0
	ds_read_b128 v[182:185], v165 offset:0
	v_cmp_lt_i32_e32 vcc, -1, v151
	v_lshlrev_b32_e32 v148, 13, v151
	v_mov_b32_e32 v149, 0
	v_lshl_add_u64 v[148:149], v[148:149], 0, v[86:87]
	v_cndmask_b32_e32 v148, v168, v148, vcc
	v_cndmask_b32_e32 v149, v169, v149, vcc
	s_waitcnt lgkmcnt(0)
	global_store_dwordx4 v[148:149], v[182:185], off
	ds_read_b128 v[182:185], v165 offset:8192
	v_cmp_lt_i32_e32 vcc, -1, v166
	v_lshlrev_b32_e32 v148, 13, v166
	v_mov_b32_e32 v149, 0
	v_lshl_add_u64 v[148:149], v[148:149], 0, v[86:87]
	v_cndmask_b32_e32 v148, v168, v148, vcc
	v_cndmask_b32_e32 v149, v169, v149, vcc
	s_waitcnt lgkmcnt(0)
	global_store_dwordx4 v[148:149], v[182:185], off
	ds_read_b32 v150, v82 offset:1024
	ds_read_b32 v151, v83 offset:1024
	ds_read_b32 v166, v83 offset:1152
	s_waitcnt lgkmcnt(2)
	v_mul_f32_e32 v2, v150, v2
	v_mul_f32_e32 v3, v150, v3
	v_mul_f32_e32 v4, v150, v4
	v_mul_f32_e32 v5, v150, v5
	v_mul_f32_e32 v6, v150, v6
	v_mul_f32_e32 v7, v150, v7
	v_mul_f32_e32 v8, v150, v8
	v_mul_f32_e32 v9, v150, v9
	v_cvt_pk_bf16_f32 v182, v2, v3
	v_cvt_pk_bf16_f32 v183, v4, v5
	v_cvt_pk_bf16_f32 v184, v6, v7
	v_cvt_pk_bf16_f32 v185, v8, v9
	ds_write_b128 v164, v[182:185]
	v_mul_f32_e32 v10, v150, v10
	v_mul_f32_e32 v11, v150, v11
	v_mul_f32_e32 v12, v150, v12
	v_mul_f32_e32 v13, v150, v13
	v_mul_f32_e32 v14, v150, v14
	v_mul_f32_e32 v15, v150, v15
	v_mul_f32_e32 v16, v150, v16
	v_mul_f32_e32 v17, v150, v17
	v_cvt_pk_bf16_f32 v182, v10, v11
	v_cvt_pk_bf16_f32 v183, v12, v13
	v_cvt_pk_bf16_f32 v184, v14, v15
	v_cvt_pk_bf16_f32 v185, v16, v17
	v_xor_b32_e32 v167, 64, v164
	ds_write_b128 v167, v[182:185]
	v_mov_b32_e32 v2, 0
	v_mov_b32_e32 v6, 0
	v_mov_b32_e32 v10, 0
	v_mov_b32_e32 v14, 0
	v_mov_b32_e32 v3, 0
	v_mov_b32_e32 v7, 0
	v_mov_b32_e32 v11, 0
	v_mov_b32_e32 v15, 0
	v_mov_b32_e32 v4, 0
	v_mov_b32_e32 v8, 0
	v_mov_b32_e32 v12, 0
	v_mov_b32_e32 v16, 0
	v_mov_b32_e32 v5, 0
	v_mov_b32_e32 v9, 0
	v_mov_b32_e32 v13, 0
	v_mov_b32_e32 v17, 0
	ds_read_b128 v[182:185], v165 offset:0
	v_cmp_lt_i32_e32 vcc, -1, v151
	v_lshlrev_b32_e32 v148, 13, v151
	v_mov_b32_e32 v149, 0
	v_lshl_add_u64 v[148:149], v[148:149], 0, v[86:87]
	v_cndmask_b32_e32 v148, v168, v148, vcc
	v_cndmask_b32_e32 v149, v169, v149, vcc
	s_waitcnt lgkmcnt(0)
	global_store_dwordx4 v[148:149], v[182:185], off
	ds_read_b128 v[182:185], v165 offset:8192
	v_cmp_lt_i32_e32 vcc, -1, v166
	v_lshlrev_b32_e32 v148, 13, v166
	v_mov_b32_e32 v149, 0
	v_lshl_add_u64 v[148:149], v[148:149], 0, v[86:87]
	v_cndmask_b32_e32 v148, v168, v148, vcc
	v_cndmask_b32_e32 v149, v169, v149, vcc
	s_waitcnt lgkmcnt(0)
	global_store_dwordx4 v[148:149], v[182:185], off
	v_add_co_u32_e32 v86, vcc, 0x400, v86
	s_nop 1
	v_addc_co_u32_e32 v87, vcc, 0, v87, vcc
	s_waitcnt lgkmcnt(0)
	s_branch .Lmd_done
; #define MD_GLDS_A(buf, tau) do { _Pragma("unroll") for (int i = 0; i < 5; ++i) if (amask & (1u << i)) \
;         __builtin_amdgcn_global_load_lds((const unsigned*)((const char*)HIDp + aoff[i] + (size_t)((tau) & 7) * 128), (PG8_LAS unsigned*)(MD_SA(buf) + wid * 1024 + i * 8192), 16, 0, 0); } while (0)
; #define MD_B_ISSUE(sb, tau) do { const char* kb_ = Bb + (size_t)((tau) >> 3) * 512 + (size_t)((tau) & 7) * (64 * (size_t)RB); _Pragma("unroll") for (int j = 0; j < 8; ++j) { const char* p_ = kb_ + (size_t)j * RB; \
;         asm volatile("global_load_dwordx2 %0, %1, off" : "=&v"(sb[j]) : "v"(p_) : "memory"); } } while (0)
; #define MD_B_WAIT(sb, N) asm volatile("s_waitcnt vmcnt(%8)" : "+v"(sb[0]), "+v"(sb[1]), "+v"(sb[2]), "+v"(sb[3]), "+v"(sb[4]), "+v"(sb[5]), "+v"(sb[6]), "+v"(sb[7]) : "n"(N) : "memory")
; #define MD_END(last) do { if (last) asm volatile("s_waitcnt vmcnt(0)" ::: "memory"); else asm volatile("s_waitcnt vmcnt(8)" ::: "memory"); \
;         asm volatile("s_waitcnt lgkmcnt(0)" ::: "memory"); __builtin_amdgcn_s_barrier(); asm volatile("" ::: "memory"); } while (0)
; __device__ __forceinline__ void moe_down_stream(PG8_LAS unsigned char* lds, int e, int cb0, int slot0, int nv, const bf16_t* HIDp, const float* Wd, bf16_t* Y, const float* slot_w, const int* slot_dst) {
;     ...
;     for (int t = 0; t < NT; t += 2) {
;         if (t + 2 < NT) MD_B_WAIT(s1, 8); else MD_B_WAIT(s1, 0);
;         MD_B_WRITE(s1, 1); __builtin_amdgcn_sched_barrier(0); MD_GLDS_A(1, t + 1); __builtin_amdgcn_sched_barrier(0);
;         if (t + 3 < NT) MD_B_ISSUE(s1, t + 3);
;         MD_COMPUTE(0);
;         MD_END(t + 3 >= NT);
;         if (t + 2 < NT) { MD_B_WAIT(s0, 8); MD_B_WRITE(s0, 0); __builtin_amdgcn_sched_barrier(0); MD_GLDS_A(0, t + 2); __builtin_amdgcn_sched_barrier(0); }
;         if (t + 4 < NT) MD_B_ISSUE(s0, t + 4);
;         MD_COMPUTE(1);
;         MD_END(t + 4 >= NT);
.Lmd_grpY:
	s_add_i32 s49, s48, s74
	s_add_i32 s52, s52, 1
	s_and_b32 s54, s52, 7
	s_cmp_eq_u32 s54, 0
	s_cselect_b32 s54, s53, s32
	s_cselect_b32 s55, -1, 0
	s_add_u32 s30, s30, s54
	s_addc_u32 s31, s31, s55
	s_mov_b32 m0, s49
	s_nop 0
	global_load_lds_dwordx4 v88, s[30:31]
	s_add_i32 m0, s49, 0x2000
	s_nop 0
	global_load_lds_dwordx4 v90, s[30:31]
	s_add_i32 m0, s49, 0x4000
	s_nop 0
	global_load_lds_dwordx4 v92, s[30:31]
	s_add_i32 m0, s49, 0x6000
	s_nop 0
	global_load_lds_dwordx4 v94, s[30:31]
	s_add_i32 m0, s49, 0x8000
	s_nop 0
	global_load_lds_dwordx4 v96, s[30:31]
	s_waitcnt vmcnt(29)
	v_cvt_pk_bf16_f32 v172, v114, v116
	v_cvt_pk_bf16_f32 v173, v118, v120
	v_cvt_pk_bf16_f32 v174, v122, v124
	v_cvt_pk_bf16_f32 v175, v126, v128
	v_cvt_pk_bf16_f32 v176, v115, v117
	v_cvt_pk_bf16_f32 v177, v119, v121
	v_cvt_pk_bf16_f32 v178, v123, v125
	v_cvt_pk_bf16_f32 v179, v127, v129
	ds_write_b128 v95, v[172:175] offset:19456
	ds_write_b128 v95, v[176:179] offset:19584
	v_add_u32_e32 v91, s46, v135
	v_add_u32_e32 v93, s46, v137
	ds_read_b128 v[238:241], v139 offset:0
	ds_read_b128 v[242:245], v139 offset:2048
	ds_read_b128 v[246:249], v139 offset:4096
	ds_read_b128 v[250:253], v139 offset:6144
	ds_read_b128 v[218:221], v91 offset:0
	ds_read_b128 v[222:225], v91 offset:2048
	ds_read_b128 v[226:229], v91 offset:4096
	ds_read_b128 v[230:233], v91 offset:6144
	ds_read_b128 v[234:237], v91 offset:8192
	s_waitcnt lgkmcnt(0)
	v_mfma_f32_16x16x32_bf16 v[78:81], v[238:241], v[218:221], v[78:81]
	v_mfma_f32_16x16x32_bf16 v[74:77], v[242:245], v[218:221], v[74:77]
	v_mfma_f32_16x16x32_bf16 v[70:73], v[246:249], v[218:221], v[70:73]
	v_mfma_f32_16x16x32_bf16 v[66:69], v[250:253], v[218:221], v[66:69]
	ds_read_b128 v[218:221], v93 offset:0
	ds_read_b128 v[142:145], v141 offset:0
	s_add_i32 s51, s51, 1
	s_and_b32 s54, s51, 7
	s_cmp_eq_u32 s54, 0
	s_cselect_b32 s44, s34, s35
	s_cselect_b32 s45, -1, 0
	v_lshl_add_u64 v[132:133], v[132:133], 0, s[44:45]
	global_load_dwordx2 v[114:115], v[132:133], off
	v_lshl_add_u64 v[180:181], v[132:133], 0, s[24:25]
	global_load_dwordx2 v[116:117], v[180:181], off
	v_mfma_f32_16x16x32_bf16 v[62:65], v[238:241], v[222:225], v[62:65]
	v_mfma_f32_16x16x32_bf16 v[58:61], v[242:245], v[222:225], v[58:61]
	v_mfma_f32_16x16x32_bf16 v[54:57], v[246:249], v[222:225], v[54:57]
	v_mfma_f32_16x16x32_bf16 v[50:53], v[250:253], v[222:225], v[50:53]
	ds_read_b128 v[222:225], v93 offset:2048
	ds_read_b128 v[146:149], v141 offset:2048
	v_lshl_add_u64 v[180:181], v[132:133], 0, s[26:27]
	global_load_dwordx2 v[118:119], v[180:181], off
	v_lshl_add_u64 v[180:181], v[132:133], 0, s[28:29]
	global_load_dwordx2 v[120:121], v[180:181], off
	v_mfma_f32_16x16x32_bf16 v[46:49], v[238:241], v[226:229], v[46:49]
	v_mfma_f32_16x16x32_bf16 v[42:45], v[242:245], v[226:229], v[42:45]
	v_mfma_f32_16x16x32_bf16 v[38:41], v[246:249], v[226:229], v[38:41]
	v_mfma_f32_16x16x32_bf16 v[34:37], v[250:253], v[226:229], v[34:37]
	ds_read_b128 v[226:229], v93 offset:4096
	ds_read_b128 v[156:159], v141 offset:4096
	v_lshl_add_u64 v[180:181], v[132:133], 0, s[36:37]
	global_load_dwordx2 v[122:123], v[180:181], off
	v_lshl_add_u64 v[180:181], v[132:133], 0, s[38:39]
	global_load_dwordx2 v[124:125], v[180:181], off
	v_mfma_f32_16x16x32_bf16 v[18:21], v[238:241], v[230:233], v[18:21]
	v_mfma_f32_16x16x32_bf16 v[22:25], v[242:245], v[230:233], v[22:25]
	v_mfma_f32_16x16x32_bf16 v[26:29], v[246:249], v[230:233], v[26:29]
	v_mfma_f32_16x16x32_bf16 v[30:33], v[250:253], v[230:233], v[30:33]
	ds_read_b128 v[230:233], v93 offset:6144
	ds_read_b128 v[160:163], v141 offset:6144
	v_lshl_add_u64 v[180:181], v[132:133], 0, s[40:41]
	global_load_dwordx2 v[126:127], v[180:181], off
	v_lshl_add_u64 v[180:181], v[132:133], 0, s[42:43]
	global_load_dwordx2 v[128:129], v[180:181], off
	v_mfma_f32_16x16x32_bf16 v[2:5], v[238:241], v[234:237], v[2:5]
	v_mfma_f32_16x16x32_bf16 v[6:9], v[242:245], v[234:237], v[6:9]
	v_mfma_f32_16x16x32_bf16 v[10:13], v[246:249], v[234:237], v[10:13]
	v_mfma_f32_16x16x32_bf16 v[14:17], v[250:253], v[234:237], v[14:17]
	ds_read_b128 v[234:237], v93 offset:8192
	s_mov_b32 s49, s46
	s_mov_b32 s46, s47
	s_mov_b32 s47, s48
	s_mov_b32 s48, s49
	s_add_i32 s50, s50, 1
	s_waitcnt lgkmcnt(0)
	s_barrier
; #define MD_GLDS_A(buf, tau) do { _Pragma("unroll") for (int i = 0; i < 5; ++i) if (amask & (1u << i)) \
;         __builtin_amdgcn_global_load_lds((const unsigned*)((const char*)HIDp + aoff[i] + (size_t)((tau) & 7) * 128), (PG8_LAS unsigned*)(MD_SA(buf) + wid * 1024 + i * 8192), 16, 0, 0); } while (0)
; #define MD_B_ISSUE(sb, tau) do { const char* kb_ = Bb + (size_t)((tau) >> 3) * 512 + (size_t)((tau) & 7) * (64 * (size_t)RB); _Pragma("unroll") for (int j = 0; j < 8; ++j) { const char* p_ = kb_ + (size_t)j * RB; \
;         asm volatile("global_load_dwordx2 %0, %1, off" : "=&v"(sb[j]) : "v"(p_) : "memory"); } } while (0)
; #define MD_B_WAIT(sb, N) asm volatile("s_waitcnt vmcnt(%8)" : "+v"(sb[0]), "+v"(sb[1]), "+v"(sb[2]), "+v"(sb[3]), "+v"(sb[4]), "+v"(sb[5]), "+v"(sb[6]), "+v"(sb[7]) : "n"(N) : "memory")
; #define MD_END(last) do { if (last) asm volatile("s_waitcnt vmcnt(0)" ::: "memory"); else asm volatile("s_waitcnt vmcnt(8)" ::: "memory"); \
;         asm volatile("s_waitcnt lgkmcnt(0)" ::: "memory"); __builtin_amdgcn_s_barrier(); asm volatile("" ::: "memory"); } while (0)
; __device__ __forceinline__ void moe_down_stream(PG8_LAS unsigned char* lds, int e, int cb0, int slot0, int nv, const bf16_t* HIDp, const float* Wd, bf16_t* Y, const float* slot_w, const int* slot_dst) {
;     ...
;     for (int t = 0; t < NT; t += 2) {
;         if (t + 2 < NT) MD_B_WAIT(s1, 8); else MD_B_WAIT(s1, 0);
;         MD_B_WRITE(s1, 1); __builtin_amdgcn_sched_barrier(0); MD_GLDS_A(1, t + 1); __builtin_amdgcn_sched_barrier(0);
;         if (t + 3 < NT) MD_B_ISSUE(s1, t + 3);
;         MD_COMPUTE(0);
;         MD_END(t + 3 >= NT);
;         if (t + 2 < NT) { MD_B_WAIT(s0, 8); MD_B_WRITE(s0, 0); __builtin_amdgcn_sched_barrier(0); MD_GLDS_A(0, t + 2); __builtin_amdgcn_sched_barrier(0); }
;         if (t + 4 < NT) MD_B_ISSUE(s0, t + 4);
;         MD_COMPUTE(1);
;         MD_END(t + 4 >= NT);
	s_add_i32 s49, s48, s74
	s_add_i32 s52, s52, 1
	s_and_b32 s54, s52, 7
	s_cmp_eq_u32 s54, 0
	s_cselect_b32 s54, s53, s32
	s_cselect_b32 s55, -1, 0
	s_add_u32 s30, s30, s54
	s_addc_u32 s31, s31, s55
	v_mfma_f32_16x16x32_bf16 v[78:81], v[142:145], v[218:221], v[78:81]
	v_mfma_f32_16x16x32_bf16 v[74:77], v[146:149], v[218:221], v[74:77]
	v_mfma_f32_16x16x32_bf16 v[70:73], v[156:159], v[218:221], v[70:73]
	v_mfma_f32_16x16x32_bf16 v[66:69], v[160:163], v[218:221], v[66:69]
	s_mov_b32 m0, s49
	s_nop 0
	global_load_lds_dwordx4 v88, s[30:31]
	v_mfma_f32_16x16x32_bf16 v[62:65], v[142:145], v[222:225], v[62:65]
	v_mfma_f32_16x16x32_bf16 v[58:61], v[146:149], v[222:225], v[58:61]
	v_mfma_f32_16x16x32_bf16 v[54:57], v[156:159], v[222:225], v[54:57]
	v_mfma_f32_16x16x32_bf16 v[50:53], v[160:163], v[222:225], v[50:53]
	s_add_i32 m0, s49, 0x2000
	s_nop 0
	global_load_lds_dwordx4 v90, s[30:31]
	v_mfma_f32_16x16x32_bf16 v[46:49], v[142:145], v[226:229], v[46:49]
	v_mfma_f32_16x16x32_bf16 v[42:45], v[146:149], v[226:229], v[42:45]
	v_mfma_f32_16x16x32_bf16 v[38:41], v[156:159], v[226:229], v[38:41]
	v_mfma_f32_16x16x32_bf16 v[34:37], v[160:163], v[226:229], v[34:37]
	s_add_i32 m0, s49, 0x4000
	s_nop 0
	global_load_lds_dwordx4 v92, s[30:31]
	v_mfma_f32_16x16x32_bf16 v[18:21], v[142:145], v[230:233], v[18:21]
	v_mfma_f32_16x16x32_bf16 v[22:25], v[146:149], v[230:233], v[22:25]
	v_mfma_f32_16x16x32_bf16 v[26:29], v[156:159], v[230:233], v[26:29]
	v_mfma_f32_16x16x32_bf16 v[30:33], v[160:163], v[230:233], v[30:33]
	s_add_i32 m0, s49, 0x6000
	s_nop 0
	global_load_lds_dwordx4 v94, s[30:31]
	v_mfma_f32_16x16x32_bf16 v[2:5], v[142:145], v[234:237], v[2:5]
	v_mfma_f32_16x16x32_bf16 v[6:9], v[146:149], v[234:237], v[6:9]
	v_mfma_f32_16x16x32_bf16 v[10:13], v[156:159], v[234:237], v[10:13]
	v_mfma_f32_16x16x32_bf16 v[14:17], v[160:163], v[234:237], v[14:17]
	s_add_i32 m0, s49, 0x8000
	s_nop 0
	global_load_lds_dwordx4 v96, s[30:31]
	s_waitcnt vmcnt(34)
	v_cvt_pk_bf16_f32 v172, v186, v188
	v_cvt_pk_bf16_f32 v173, v190, v192
	v_cvt_pk_bf16_f32 v174, v194, v196
	v_cvt_pk_bf16_f32 v175, v198, v200
	v_cvt_pk_bf16_f32 v176, v187, v189
	v_cvt_pk_bf16_f32 v177, v191, v193
	v_cvt_pk_bf16_f32 v178, v195, v197
	v_cvt_pk_bf16_f32 v179, v199, v201
	ds_write_b128 v95, v[172:175] offset:0
	ds_write_b128 v95, v[176:179] offset:128
	v_add_u32_e32 v91, s46, v135
	v_add_u32_e32 v93, s46, v137
	ds_read_b128 v[238:241], v139 offset:19456
	ds_read_b128 v[242:245], v139 offset:21504
	ds_read_b128 v[246:249], v139 offset:23552
	ds_read_b128 v[250:253], v139 offset:25600
	ds_read_b128 v[218:221], v91 offset:0
	ds_read_b128 v[222:225], v91 offset:2048
	ds_read_b128 v[226:229], v91 offset:4096
	ds_read_b128 v[230:233], v91 offset:6144
	ds_read_b128 v[234:237], v91 offset:8192
	s_waitcnt lgkmcnt(0)
	v_mfma_f32_16x16x32_bf16 v[78:81], v[238:241], v[218:221], v[78:81]
	v_mfma_f32_16x16x32_bf16 v[74:77], v[242:245], v[218:221], v[74:77]
	v_mfma_f32_16x16x32_bf16 v[70:73], v[246:249], v[218:221], v[70:73]
	v_mfma_f32_16x16x32_bf16 v[66:69], v[250:253], v[218:221], v[66:69]
	ds_read_b128 v[218:221], v93 offset:0
	ds_read_b128 v[142:145], v141 offset:19456
	s_add_i32 s51, s51, 1
	s_and_b32 s54, s51, 7
	s_cmp_eq_u32 s54, 0
	s_cselect_b32 s44, s34, s35
	s_cselect_b32 s45, -1, 0
	v_lshl_add_u64 v[132:133], v[132:133], 0, s[44:45]
	global_load_dwordx2 v[186:187], v[132:133], off
	v_lshl_add_u64 v[180:181], v[132:133], 0, s[24:25]
	global_load_dwordx2 v[188:189], v[180:181], off
	v_mfma_f32_16x16x32_bf16 v[62:65], v[238:241], v[222:225], v[62:65]
	v_mfma_f32_16x16x32_bf16 v[58:61], v[242:245], v[222:225], v[58:61]
	v_mfma_f32_16x16x32_bf16 v[54:57], v[246:249], v[222:225], v[54:57]
	v_mfma_f32_16x16x32_bf16 v[50:53], v[250:253], v[222:225], v[50:53]
	ds_read_b128 v[222:225], v93 offset:2048
	ds_read_b128 v[146:149], v141 offset:21504
	v_lshl_add_u64 v[180:181], v[132:133], 0, s[26:27]
	global_load_dwordx2 v[190:191], v[180:181], off
	v_lshl_add_u64 v[180:181], v[132:133], 0, s[28:29]
	global_load_dwordx2 v[192:193], v[180:181], off
	v_mfma_f32_16x16x32_bf16 v[46:49], v[238:241], v[226:229], v[46:49]
	v_mfma_f32_16x16x32_bf16 v[42:45], v[242:245], v[226:229], v[42:45]
	v_mfma_f32_16x16x32_bf16 v[38:41], v[246:249], v[226:229], v[38:41]
	v_mfma_f32_16x16x32_bf16 v[34:37], v[250:253], v[226:229], v[34:37]
	ds_read_b128 v[226:229], v93 offset:4096
	ds_read_b128 v[156:159], v141 offset:23552
	v_lshl_add_u64 v[180:181], v[132:133], 0, s[36:37]
	global_load_dwordx2 v[194:195], v[180:181], off
	v_lshl_add_u64 v[180:181], v[132:133], 0, s[38:39]
	global_load_dwordx2 v[196:197], v[180:181], off
	v_mfma_f32_16x16x32_bf16 v[18:21], v[238:241], v[230:233], v[18:21]
	v_mfma_f32_16x16x32_bf16 v[22:25], v[242:245], v[230:233], v[22:25]
	v_mfma_f32_16x16x32_bf16 v[26:29], v[246:249], v[230:233], v[26:29]
	v_mfma_f32_16x16x32_bf16 v[30:33], v[250:253], v[230:233], v[30:33]
	ds_read_b128 v[230:233], v93 offset:6144
	ds_read_b128 v[160:163], v141 offset:25600
	v_lshl_add_u64 v[180:181], v[132:133], 0, s[40:41]
	global_load_dwordx2 v[198:199], v[180:181], off
	v_lshl_add_u64 v[180:181], v[132:133], 0, s[42:43]
	global_load_dwordx2 v[200:201], v[180:181], off
	v_mfma_f32_16x16x32_bf16 v[2:5], v[238:241], v[234:237], v[2:5]
	v_mfma_f32_16x16x32_bf16 v[6:9], v[242:245], v[234:237], v[6:9]
	v_mfma_f32_16x16x32_bf16 v[10:13], v[246:249], v[234:237], v[10:13]
	v_mfma_f32_16x16x32_bf16 v[14:17], v[250:253], v[234:237], v[14:17]
	ds_read_b128 v[234:237], v93 offset:8192
	s_waitcnt vmcnt(21)
	s_mov_b32 s49, s46
	s_mov_b32 s46, s47
	s_mov_b32 s47, s48
	s_mov_b32 s48, s49
	s_add_i32 s50, s50, 1
	s_waitcnt lgkmcnt(0)
	s_barrier
; #define MD_GLDS_A(buf, tau) do { _Pragma("unroll") for (int i = 0; i < 5; ++i) if (amask & (1u << i)) \
;         __builtin_amdgcn_global_load_lds((const unsigned*)((const char*)HIDp + aoff[i] + (size_t)((tau) & 7) * 128), (PG8_LAS unsigned*)(MD_SA(buf) + wid * 1024 + i * 8192), 16, 0, 0); } while (0)
; #define MD_B_ISSUE(sb, tau) do { const char* kb_ = Bb + (size_t)((tau) >> 3) * 512 + (size_t)((tau) & 7) * (64 * (size_t)RB); _Pragma("unroll") for (int j = 0; j < 8; ++j) { const char* p_ = kb_ + (size_t)j * RB; \
;         asm volatile("global_load_dwordx2 %0, %1, off" : "=&v"(sb[j]) : "v"(p_) : "memory"); } } while (0)
; #define MD_B_WAIT(sb, N) asm volatile("s_waitcnt vmcnt(%8)" : "+v"(sb[0]), "+v"(sb[1]), "+v"(sb[2]), "+v"(sb[3]), "+v"(sb[4]), "+v"(sb[5]), "+v"(sb[6]), "+v"(sb[7]) : "n"(N) : "memory")
; #define MD_END(last) do { if (last) asm volatile("s_waitcnt vmcnt(0)" ::: "memory"); else asm volatile("s_waitcnt vmcnt(8)" ::: "memory"); \
;         asm volatile("s_waitcnt lgkmcnt(0)" ::: "memory"); __builtin_amdgcn_s_barrier(); asm volatile("" ::: "memory"); } while (0)
; __device__ __forceinline__ void moe_down_stream(PG8_LAS unsigned char* lds, int e, int cb0, int slot0, int nv, const bf16_t* HIDp, const float* Wd, bf16_t* Y, const float* slot_w, const int* slot_dst) {
;     ...
;     for (int t = 0; t < NT; t += 2) {
;         if (t + 2 < NT) MD_B_WAIT(s1, 8); else MD_B_WAIT(s1, 0);
;         MD_B_WRITE(s1, 1); __builtin_amdgcn_sched_barrier(0); MD_GLDS_A(1, t + 1); __builtin_amdgcn_sched_barrier(0);
;         if (t + 3 < NT) MD_B_ISSUE(s1, t + 3);
;         MD_COMPUTE(0);
;         MD_END(t + 3 >= NT);
;         if (t + 2 < NT) { MD_B_WAIT(s0, 8); MD_B_WRITE(s0, 0); __builtin_amdgcn_sched_barrier(0); MD_GLDS_A(0, t + 2); __builtin_amdgcn_sched_barrier(0); }
;         if (t + 4 < NT) MD_B_ISSUE(s0, t + 4);
;         MD_COMPUTE(1);
;         MD_END(t + 4 >= NT);
	s_add_i32 s49, s48, s74
	s_add_i32 s52, s52, 1
	s_and_b32 s54, s52, 7
	s_cmp_eq_u32 s54, 0
	s_cselect_b32 s54, s53, s32
	s_cselect_b32 s55, -1, 0
	s_add_u32 s30, s30, s54
	s_addc_u32 s31, s31, s55
	v_mfma_f32_16x16x32_bf16 v[78:81], v[142:145], v[218:221], v[78:81]
	v_mfma_f32_16x16x32_bf16 v[74:77], v[146:149], v[218:221], v[74:77]
	v_mfma_f32_16x16x32_bf16 v[70:73], v[156:159], v[218:221], v[70:73]
	v_mfma_f32_16x16x32_bf16 v[66:69], v[160:163], v[218:221], v[66:69]
	s_mov_b32 m0, s49
	s_nop 0
	global_load_lds_dwordx4 v88, s[30:31]
	v_mfma_f32_16x16x32_bf16 v[62:65], v[142:145], v[222:225], v[62:65]
	v_mfma_f32_16x16x32_bf16 v[58:61], v[146:149], v[222:225], v[58:61]
	v_mfma_f32_16x16x32_bf16 v[54:57], v[156:159], v[222:225], v[54:57]
	v_mfma_f32_16x16x32_bf16 v[50:53], v[160:163], v[222:225], v[50:53]
	s_add_i32 m0, s49, 0x2000
	s_nop 0
	global_load_lds_dwordx4 v90, s[30:31]
	v_mfma_f32_16x16x32_bf16 v[46:49], v[142:145], v[226:229], v[46:49]
	v_mfma_f32_16x16x32_bf16 v[42:45], v[146:149], v[226:229], v[42:45]
	v_mfma_f32_16x16x32_bf16 v[38:41], v[156:159], v[226:229], v[38:41]
	v_mfma_f32_16x16x32_bf16 v[34:37], v[160:163], v[226:229], v[34:37]
	s_add_i32 m0, s49, 0x4000
	s_nop 0
	global_load_lds_dwordx4 v92, s[30:31]
	v_mfma_f32_16x16x32_bf16 v[18:21], v[142:145], v[230:233], v[18:21]
	v_mfma_f32_16x16x32_bf16 v[22:25], v[146:149], v[230:233], v[22:25]
	v_mfma_f32_16x16x32_bf16 v[26:29], v[156:159], v[230:233], v[26:29]
	v_mfma_f32_16x16x32_bf16 v[30:33], v[160:163], v[230:233], v[30:33]
	s_add_i32 m0, s49, 0x6000
	s_nop 0
	global_load_lds_dwordx4 v94, s[30:31]
	v_mfma_f32_16x16x32_bf16 v[2:5], v[142:145], v[234:237], v[2:5]
	v_mfma_f32_16x16x32_bf16 v[6:9], v[146:149], v[234:237], v[6:9]
	v_mfma_f32_16x16x32_bf16 v[10:13], v[156:159], v[234:237], v[10:13]
	v_mfma_f32_16x16x32_bf16 v[14:17], v[160:163], v[234:237], v[14:17]
	s_add_i32 m0, s49, 0x8000
	s_nop 0
	global_load_lds_dwordx4 v96, s[30:31]
	v_cvt_pk_bf16_f32 v172, v202, v204
	v_cvt_pk_bf16_f32 v173, v206, v208
	v_cvt_pk_bf16_f32 v174, v210, v212
	v_cvt_pk_bf16_f32 v175, v214, v216
	v_cvt_pk_bf16_f32 v176, v203, v205
	v_cvt_pk_bf16_f32 v177, v207, v209
	v_cvt_pk_bf16_f32 v178, v211, v213
	v_cvt_pk_bf16_f32 v179, v215, v217
	ds_write_b128 v95, v[172:175] offset:19456
	ds_write_b128 v95, v[176:179] offset:19584
	v_add_u32_e32 v91, s46, v135
	v_add_u32_e32 v93, s46, v137
	ds_read_b128 v[238:241], v139 offset:0
	ds_read_b128 v[242:245], v139 offset:2048
	ds_read_b128 v[246:249], v139 offset:4096
	ds_read_b128 v[250:253], v139 offset:6144
	ds_read_b128 v[218:221], v91 offset:0
	ds_read_b128 v[222:225], v91 offset:2048
	ds_read_b128 v[226:229], v91 offset:4096
	ds_read_b128 v[230:233], v91 offset:6144
	ds_read_b128 v[234:237], v91 offset:8192
	s_waitcnt lgkmcnt(0)
	v_mfma_f32_16x16x32_bf16 v[78:81], v[238:241], v[218:221], v[78:81]
	v_mfma_f32_16x16x32_bf16 v[74:77], v[242:245], v[218:221], v[74:77]
	v_mfma_f32_16x16x32_bf16 v[70:73], v[246:249], v[218:221], v[70:73]
	v_mfma_f32_16x16x32_bf16 v[66:69], v[250:253], v[218:221], v[66:69]
	ds_read_b128 v[218:221], v93 offset:0
	ds_read_b128 v[142:145], v141 offset:0
	s_add_i32 s51, s51, 1
	s_and_b32 s54, s51, 7
	s_cmp_eq_u32 s54, 0
	s_cselect_b32 s44, s34, s35
	s_cselect_b32 s45, -1, 0
	v_lshl_add_u64 v[132:133], v[132:133], 0, s[44:45]
	global_load_dwordx2 v[202:203], v[132:133], off
	v_lshl_add_u64 v[180:181], v[132:133], 0, s[24:25]
	global_load_dwordx2 v[204:205], v[180:181], off
	v_mfma_f32_16x16x32_bf16 v[62:65], v[238:241], v[222:225], v[62:65]
	v_mfma_f32_16x16x32_bf16 v[58:61], v[242:245], v[222:225], v[58:61]
	v_mfma_f32_16x16x32_bf16 v[54:57], v[246:249], v[222:225], v[54:57]
	v_mfma_f32_16x16x32_bf16 v[50:53], v[250:253], v[222:225], v[50:53]
	ds_read_b128 v[222:225], v93 offset:2048
	ds_read_b128 v[146:149], v141 offset:2048
	v_lshl_add_u64 v[180:181], v[132:133], 0, s[26:27]
	global_load_dwordx2 v[206:207], v[180:181], off
	v_lshl_add_u64 v[180:181], v[132:133], 0, s[28:29]
	global_load_dwordx2 v[208:209], v[180:181], off
	v_mfma_f32_16x16x32_bf16 v[46:49], v[238:241], v[226:229], v[46:49]
	v_mfma_f32_16x16x32_bf16 v[42:45], v[242:245], v[226:229], v[42:45]
	v_mfma_f32_16x16x32_bf16 v[38:41], v[246:249], v[226:229], v[38:41]
	v_mfma_f32_16x16x32_bf16 v[34:37], v[250:253], v[226:229], v[34:37]
	ds_read_b128 v[226:229], v93 offset:4096
	ds_read_b128 v[156:159], v141 offset:4096
	v_lshl_add_u64 v[180:181], v[132:133], 0, s[36:37]
	global_load_dwordx2 v[210:211], v[180:181], off
	v_lshl_add_u64 v[180:181], v[132:133], 0, s[38:39]
	global_load_dwordx2 v[212:213], v[180:181], off
	v_mfma_f32_16x16x32_bf16 v[18:21], v[238:241], v[230:233], v[18:21]
	v_mfma_f32_16x16x32_bf16 v[22:25], v[242:245], v[230:233], v[22:25]
	v_mfma_f32_16x16x32_bf16 v[26:29], v[246:249], v[230:233], v[26:29]
	v_mfma_f32_16x16x32_bf16 v[30:33], v[250:253], v[230:233], v[30:33]
	ds_read_b128 v[230:233], v93 offset:6144
	ds_read_b128 v[160:163], v141 offset:6144
	v_lshl_add_u64 v[180:181], v[132:133], 0, s[40:41]
	global_load_dwordx2 v[214:215], v[180:181], off
	v_lshl_add_u64 v[180:181], v[132:133], 0, s[42:43]
	global_load_dwordx2 v[216:217], v[180:181], off
	v_mfma_f32_16x16x32_bf16 v[2:5], v[238:241], v[234:237], v[2:5]
	v_mfma_f32_16x16x32_bf16 v[6:9], v[242:245], v[234:237], v[6:9]
	v_mfma_f32_16x16x32_bf16 v[10:13], v[246:249], v[234:237], v[10:13]
	v_mfma_f32_16x16x32_bf16 v[14:17], v[250:253], v[234:237], v[14:17]
	ds_read_b128 v[234:237], v93 offset:8192
	s_waitcnt vmcnt(21)
	s_mov_b32 s49, s46
	s_mov_b32 s46, s47
	s_mov_b32 s47, s48
	s_mov_b32 s48, s49
	s_add_i32 s50, s50, 1
	s_waitcnt lgkmcnt(0)
	s_barrier
; #define MD_GLDS_A(buf, tau) do { _Pragma("unroll") for (int i = 0; i < 5; ++i) if (amask & (1u << i)) \
;         __builtin_amdgcn_global_load_lds((const unsigned*)((const char*)HIDp + aoff[i] + (size_t)((tau) & 7) * 128), (PG8_LAS unsigned*)(MD_SA(buf) + wid * 1024 + i * 8192), 16, 0, 0); } while (0)
; #define MD_B_ISSUE(sb, tau) do { const char* kb_ = Bb + (size_t)((tau) >> 3) * 512 + (size_t)((tau) & 7) * (64 * (size_t)RB); _Pragma("unroll") for (int j = 0; j < 8; ++j) { const char* p_ = kb_ + (size_t)j * RB; \
;         asm volatile("global_load_dwordx2 %0, %1, off" : "=&v"(sb[j]) : "v"(p_) : "memory"); } } while (0)
; #define MD_B_WAIT(sb, N) asm volatile("s_waitcnt vmcnt(%8)" : "+v"(sb[0]), "+v"(sb[1]), "+v"(sb[2]), "+v"(sb[3]), "+v"(sb[4]), "+v"(sb[5]), "+v"(sb[6]), "+v"(sb[7]) : "n"(N) : "memory")
; #define MD_END(last) do { if (last) asm volatile("s_waitcnt vmcnt(0)" ::: "memory"); else asm volatile("s_waitcnt vmcnt(8)" ::: "memory"); \
;         asm volatile("s_waitcnt lgkmcnt(0)" ::: "memory"); __builtin_amdgcn_s_barrier(); asm volatile("" ::: "memory"); } while (0)
; __device__ __forceinline__ void moe_down_stream(PG8_LAS unsigned char* lds, int e, int cb0, int slot0, int nv, const bf16_t* HIDp, const float* Wd, bf16_t* Y, const float* slot_w, const int* slot_dst) {
;     ...
;     for (int t = 0; t < NT; t += 2) {
;         if (t + 2 < NT) MD_B_WAIT(s1, 8); else MD_B_WAIT(s1, 0);
;         MD_B_WRITE(s1, 1); __builtin_amdgcn_sched_barrier(0); MD_GLDS_A(1, t + 1); __builtin_amdgcn_sched_barrier(0);
;         if (t + 3 < NT) MD_B_ISSUE(s1, t + 3);
;         MD_COMPUTE(0);
;         MD_END(t + 3 >= NT);
;         if (t + 2 < NT) { MD_B_WAIT(s0, 8); MD_B_WRITE(s0, 0); __builtin_amdgcn_sched_barrier(0); MD_GLDS_A(0, t + 2); __builtin_amdgcn_sched_barrier(0); }
;         if (t + 4 < NT) MD_B_ISSUE(s0, t + 4);
;         MD_COMPUTE(1);
;         MD_END(t + 4 >= NT);
	s_add_i32 s49, s48, s74
	s_add_i32 s52, s52, 1
	s_and_b32 s54, s52, 7
	s_cmp_eq_u32 s54, 0
	s_cselect_b32 s54, s53, s32
	s_cselect_b32 s55, -1, 0
	s_add_u32 s30, s30, s54
	s_addc_u32 s31, s31, s55
	v_mfma_f32_16x16x32_bf16 v[78:81], v[142:145], v[218:221], v[78:81]
	v_mfma_f32_16x16x32_bf16 v[74:77], v[146:149], v[218:221], v[74:77]
	v_mfma_f32_16x16x32_bf16 v[70:73], v[156:159], v[218:221], v[70:73]
	v_mfma_f32_16x16x32_bf16 v[66:69], v[160:163], v[218:221], v[66:69]
	s_mov_b32 m0, s49
	s_nop 0
	global_load_lds_dwordx4 v88, s[30:31]
	v_mfma_f32_16x16x32_bf16 v[62:65], v[142:145], v[222:225], v[62:65]
	v_mfma_f32_16x16x32_bf16 v[58:61], v[146:149], v[222:225], v[58:61]
	v_mfma_f32_16x16x32_bf16 v[54:57], v[156:159], v[222:225], v[54:57]
	v_mfma_f32_16x16x32_bf16 v[50:53], v[160:163], v[222:225], v[50:53]
	s_add_i32 m0, s49, 0x2000
	s_nop 0
	global_load_lds_dwordx4 v90, s[30:31]
	v_mfma_f32_16x16x32_bf16 v[46:49], v[142:145], v[226:229], v[46:49]
	v_mfma_f32_16x16x32_bf16 v[42:45], v[146:149], v[226:229], v[42:45]
	v_mfma_f32_16x16x32_bf16 v[38:41], v[156:159], v[226:229], v[38:41]
	v_mfma_f32_16x16x32_bf16 v[34:37], v[160:163], v[226:229], v[34:37]
	s_add_i32 m0, s49, 0x4000
	s_nop 0
	global_load_lds_dwordx4 v92, s[30:31]
	v_mfma_f32_16x16x32_bf16 v[18:21], v[142:145], v[230:233], v[18:21]
	v_mfma_f32_16x16x32_bf16 v[22:25], v[146:149], v[230:233], v[22:25]
	v_mfma_f32_16x16x32_bf16 v[26:29], v[156:159], v[230:233], v[26:29]
	v_mfma_f32_16x16x32_bf16 v[30:33], v[160:163], v[230:233], v[30:33]
	s_add_i32 m0, s49, 0x6000
	s_nop 0
	global_load_lds_dwordx4 v94, s[30:31]
	v_mfma_f32_16x16x32_bf16 v[2:5], v[142:145], v[234:237], v[2:5]
	v_mfma_f32_16x16x32_bf16 v[6:9], v[146:149], v[234:237], v[6:9]
	v_mfma_f32_16x16x32_bf16 v[10:13], v[156:159], v[234:237], v[10:13]
	v_mfma_f32_16x16x32_bf16 v[14:17], v[160:163], v[234:237], v[14:17]
	s_add_i32 m0, s49, 0x8000
	s_nop 0
	global_load_lds_dwordx4 v96, s[30:31]
	v_cvt_pk_bf16_f32 v172, v98, v100
	v_cvt_pk_bf16_f32 v173, v102, v104
	v_cvt_pk_bf16_f32 v174, v106, v108
	v_cvt_pk_bf16_f32 v175, v110, v112
	v_cvt_pk_bf16_f32 v176, v99, v101
	v_cvt_pk_bf16_f32 v177, v103, v105
	v_cvt_pk_bf16_f32 v178, v107, v109
	v_cvt_pk_bf16_f32 v179, v111, v113
	ds_write_b128 v95, v[172:175] offset:0
	ds_write_b128 v95, v[176:179] offset:128
	v_add_u32_e32 v91, s46, v135
	v_add_u32_e32 v93, s46, v137
	ds_read_b128 v[238:241], v139 offset:19456
	ds_read_b128 v[242:245], v139 offset:21504
	ds_read_b128 v[246:249], v139 offset:23552
	ds_read_b128 v[250:253], v139 offset:25600
	ds_read_b128 v[218:221], v91 offset:0
	ds_read_b128 v[222:225], v91 offset:2048
	ds_read_b128 v[226:229], v91 offset:4096
	ds_read_b128 v[230:233], v91 offset:6144
	ds_read_b128 v[234:237], v91 offset:8192
	s_waitcnt lgkmcnt(0)
	v_mfma_f32_16x16x32_bf16 v[78:81], v[238:241], v[218:221], v[78:81]
	v_mfma_f32_16x16x32_bf16 v[74:77], v[242:245], v[218:221], v[74:77]
	v_mfma_f32_16x16x32_bf16 v[70:73], v[246:249], v[218:221], v[70:73]
	v_mfma_f32_16x16x32_bf16 v[66:69], v[250:253], v[218:221], v[66:69]
	ds_read_b128 v[218:221], v93 offset:0
	ds_read_b128 v[142:145], v141 offset:19456
	s_add_i32 s51, s51, 1
	s_and_b32 s54, s51, 7
	s_cmp_eq_u32 s54, 0
	s_cselect_b32 s44, s34, s35
	s_cselect_b32 s45, -1, 0
	v_lshl_add_u64 v[132:133], v[132:133], 0, s[44:45]
	global_load_dwordx2 v[98:99], v[132:133], off
	v_lshl_add_u64 v[180:181], v[132:133], 0, s[24:25]
	global_load_dwordx2 v[100:101], v[180:181], off
	v_mfma_f32_16x16x32_bf16 v[62:65], v[238:241], v[222:225], v[62:65]
	v_mfma_f32_16x16x32_bf16 v[58:61], v[242:245], v[222:225], v[58:61]
	v_mfma_f32_16x16x32_bf16 v[54:57], v[246:249], v[222:225], v[54:57]
	v_mfma_f32_16x16x32_bf16 v[50:53], v[250:253], v[222:225], v[50:53]
	ds_read_b128 v[222:225], v93 offset:2048
	ds_read_b128 v[146:149], v141 offset:21504
	v_lshl_add_u64 v[180:181], v[132:133], 0, s[26:27]
	global_load_dwordx2 v[102:103], v[180:181], off
	v_lshl_add_u64 v[180:181], v[132:133], 0, s[28:29]
	global_load_dwordx2 v[104:105], v[180:181], off
	v_mfma_f32_16x16x32_bf16 v[46:49], v[238:241], v[226:229], v[46:49]
	v_mfma_f32_16x16x32_bf16 v[42:45], v[242:245], v[226:229], v[42:45]
	v_mfma_f32_16x16x32_bf16 v[38:41], v[246:249], v[226:229], v[38:41]
	v_mfma_f32_16x16x32_bf16 v[34:37], v[250:253], v[226:229], v[34:37]
	ds_read_b128 v[226:229], v93 offset:4096
	ds_read_b128 v[156:159], v141 offset:23552
	v_lshl_add_u64 v[180:181], v[132:133], 0, s[36:37]
	global_load_dwordx2 v[106:107], v[180:181], off
	v_lshl_add_u64 v[180:181], v[132:133], 0, s[38:39]
	global_load_dwordx2 v[108:109], v[180:181], off
	v_mfma_f32_16x16x32_bf16 v[18:21], v[238:241], v[230:233], v[18:21]
	v_mfma_f32_16x16x32_bf16 v[22:25], v[242:245], v[230:233], v[22:25]
	v_mfma_f32_16x16x32_bf16 v[26:29], v[246:249], v[230:233], v[26:29]
	v_mfma_f32_16x16x32_bf16 v[30:33], v[250:253], v[230:233], v[30:33]
	ds_read_b128 v[230:233], v93 offset:6144
	ds_read_b128 v[160:163], v141 offset:25600
	v_lshl_add_u64 v[180:181], v[132:133], 0, s[40:41]
	global_load_dwordx2 v[110:111], v[180:181], off
	v_lshl_add_u64 v[180:181], v[132:133], 0, s[42:43]
	global_load_dwordx2 v[112:113], v[180:181], off
	v_mfma_f32_16x16x32_bf16 v[2:5], v[238:241], v[234:237], v[2:5]
	v_mfma_f32_16x16x32_bf16 v[6:9], v[242:245], v[234:237], v[6:9]
	v_mfma_f32_16x16x32_bf16 v[10:13], v[246:249], v[234:237], v[10:13]
	v_mfma_f32_16x16x32_bf16 v[14:17], v[250:253], v[234:237], v[14:17]
	ds_read_b128 v[234:237], v93 offset:8192
	s_waitcnt vmcnt(21)
	s_mov_b32 s49, s46
	s_mov_b32 s46, s47
	s_mov_b32 s47, s48
	s_mov_b32 s48, s49
	s_add_i32 s50, s50, 1
	s_waitcnt lgkmcnt(0)
	s_barrier
	s_mov_b32 s56, 13

; #define MD_GLDS_A(buf, tau) do { _Pragma("unroll") for (int i = 0; i < 5; ++i) if (amask & (1u << i)) \
;         __builtin_amdgcn_global_load_lds((const unsigned*)((const char*)HIDp + aoff[i] + (size_t)((tau) & 7) * 128), (PG8_LAS unsigned*)(MD_SA(buf) + wid * 1024 + i * 8192), 16, 0, 0); } while (0)
; #define MD_B_ISSUE(sb, tau) do { const char* kb_ = Bb + (size_t)((tau) >> 3) * 512 + (size_t)((tau) & 7) * (64 * (size_t)RB); _Pragma("unroll") for (int j = 0; j < 8; ++j) { const char* p_ = kb_ + (size_t)j * RB; \
;         asm volatile("global_load_dwordx2 %0, %1, off" : "=&v"(sb[j]) : "v"(p_) : "memory"); } } while (0)
; #define MD_B_WAIT(sb, N) asm volatile("s_waitcnt vmcnt(%8)" : "+v"(sb[0]), "+v"(sb[1]), "+v"(sb[2]), "+v"(sb[3]), "+v"(sb[4]), "+v"(sb[5]), "+v"(sb[6]), "+v"(sb[7]) : "n"(N) : "memory")
; #define MD_END(last) do { if (last) asm volatile("s_waitcnt vmcnt(0)" ::: "memory"); else asm volatile("s_waitcnt vmcnt(8)" ::: "memory"); \
;         asm volatile("s_waitcnt lgkmcnt(0)" ::: "memory"); __builtin_amdgcn_s_barrier(); asm volatile("" ::: "memory"); } while (0)
; __device__ __forceinline__ void moe_down_stream(PG8_LAS unsigned char* lds, int e, int cb0, int slot0, int nv, const bf16_t* HIDp, const float* Wd, bf16_t* Y, const float* slot_w, const int* slot_dst) {
;     ...
;     for (int t = 0; t < NT; t += 2) {
;         if (t + 2 < NT) MD_B_WAIT(s1, 8); else MD_B_WAIT(s1, 0);
;         MD_B_WRITE(s1, 1); __builtin_amdgcn_sched_barrier(0); MD_GLDS_A(1, t + 1); __builtin_amdgcn_sched_barrier(0);
;         if (t + 3 < NT) MD_B_ISSUE(s1, t + 3);
;         MD_COMPUTE(0);
;         MD_END(t + 3 >= NT);
;         if (t + 2 < NT) { MD_B_WAIT(s0, 8); MD_B_WRITE(s0, 0); __builtin_amdgcn_sched_barrier(0); MD_GLDS_A(0, t + 2); __builtin_amdgcn_sched_barrier(0); }
;         if (t + 4 < NT) MD_B_ISSUE(s0, t + 4);
;         MD_COMPUTE(1);
;         MD_END(t + 4 >= NT);
.Lmd_noepi_Y:
	s_add_i32 s49, s48, s74
	s_add_i32 s52, s52, 1
	s_and_b32 s54, s52, 7
	s_cmp_eq_u32 s54, 0
	s_cselect_b32 s54, s53, s32
	s_cselect_b32 s55, -1, 0
	s_add_u32 s30, s30, s54
	s_addc_u32 s31, s31, s55
	s_mov_b32 m0, s49
	s_nop 0
	global_load_lds_dwordx4 v88, s[30:31]
	s_add_i32 m0, s49, 0x2000
	s_nop 0
	global_load_lds_dwordx4 v90, s[30:31]
	s_add_i32 m0, s49, 0x4000
	s_nop 0
	global_load_lds_dwordx4 v92, s[30:31]
	s_add_i32 m0, s49, 0x6000
	s_nop 0
	global_load_lds_dwordx4 v94, s[30:31]
	s_add_i32 m0, s49, 0x8000
	s_nop 0
	global_load_lds_dwordx4 v96, s[30:31]
	v_cvt_pk_bf16_f32 v172, v114, v116
	v_cvt_pk_bf16_f32 v173, v118, v120
	v_cvt_pk_bf16_f32 v174, v122, v124
	v_cvt_pk_bf16_f32 v175, v126, v128
	v_cvt_pk_bf16_f32 v176, v115, v117
	v_cvt_pk_bf16_f32 v177, v119, v121
	v_cvt_pk_bf16_f32 v178, v123, v125
	v_cvt_pk_bf16_f32 v179, v127, v129
	ds_write_b128 v95, v[172:175] offset:19456
	ds_write_b128 v95, v[176:179] offset:19584
	v_add_u32_e32 v91, s46, v135
	v_add_u32_e32 v93, s46, v137
	ds_read_b128 v[238:241], v139 offset:0
	ds_read_b128 v[242:245], v139 offset:2048
	ds_read_b128 v[246:249], v139 offset:4096
	ds_read_b128 v[250:253], v139 offset:6144
	ds_read_b128 v[218:221], v91 offset:0
	ds_read_b128 v[222:225], v91 offset:2048
	ds_read_b128 v[226:229], v91 offset:4096
	ds_read_b128 v[230:233], v91 offset:6144
	ds_read_b128 v[234:237], v91 offset:8192
	s_waitcnt lgkmcnt(0)
	v_mfma_f32_16x16x32_bf16 v[78:81], v[238:241], v[218:221], v[78:81]
	v_mfma_f32_16x16x32_bf16 v[74:77], v[242:245], v[218:221], v[74:77]
	v_mfma_f32_16x16x32_bf16 v[70:73], v[246:249], v[218:221], v[70:73]
	v_mfma_f32_16x16x32_bf16 v[66:69], v[250:253], v[218:221], v[66:69]
	ds_read_b128 v[218:221], v93 offset:0
	ds_read_b128 v[142:145], v141 offset:0
	s_add_i32 s51, s51, 1
	s_and_b32 s54, s51, 7
	s_cmp_eq_u32 s54, 0
	s_cselect_b32 s44, s34, s35
	s_cselect_b32 s45, -1, 0
	v_lshl_add_u64 v[132:133], v[132:133], 0, s[44:45]
	global_load_dwordx2 v[114:115], v[132:133], off
	v_lshl_add_u64 v[180:181], v[132:133], 0, s[24:25]
	global_load_dwordx2 v[116:117], v[180:181], off
	v_mfma_f32_16x16x32_bf16 v[62:65], v[238:241], v[222:225], v[62:65]
	v_mfma_f32_16x16x32_bf16 v[58:61], v[242:245], v[222:225], v[58:61]
	v_mfma_f32_16x16x32_bf16 v[54:57], v[246:249], v[222:225], v[54:57]
	v_mfma_f32_16x16x32_bf16 v[50:53], v[250:253], v[222:225], v[50:53]
	ds_read_b128 v[222:225], v93 offset:2048
	ds_read_b128 v[146:149], v141 offset:2048
	v_lshl_add_u64 v[180:181], v[132:133], 0, s[26:27]
	global_load_dwordx2 v[118:119], v[180:181], off
	v_lshl_add_u64 v[180:181], v[132:133], 0, s[28:29]
	global_load_dwordx2 v[120:121], v[180:181], off
	v_mfma_f32_16x16x32_bf16 v[46:49], v[238:241], v[226:229], v[46:49]
	v_mfma_f32_16x16x32_bf16 v[42:45], v[242:245], v[226:229], v[42:45]
	v_mfma_f32_16x16x32_bf16 v[38:41], v[246:249], v[226:229], v[38:41]
	v_mfma_f32_16x16x32_bf16 v[34:37], v[250:253], v[226:229], v[34:37]
	ds_read_b128 v[226:229], v93 offset:4096
	ds_read_b128 v[156:159], v141 offset:4096
	v_lshl_add_u64 v[180:181], v[132:133], 0, s[36:37]
	global_load_dwordx2 v[122:123], v[180:181], off
	v_lshl_add_u64 v[180:181], v[132:133], 0, s[38:39]
	global_load_dwordx2 v[124:125], v[180:181], off
	v_mfma_f32_16x16x32_bf16 v[18:21], v[238:241], v[230:233], v[18:21]
	v_mfma_f32_16x16x32_bf16 v[22:25], v[242:245], v[230:233], v[22:25]
	v_mfma_f32_16x16x32_bf16 v[26:29], v[246:249], v[230:233], v[26:29]
	v_mfma_f32_16x16x32_bf16 v[30:33], v[250:253], v[230:233], v[30:33]
	ds_read_b128 v[230:233], v93 offset:6144
	ds_read_b128 v[160:163], v141 offset:6144
	v_lshl_add_u64 v[180:181], v[132:133], 0, s[40:41]
	global_load_dwordx2 v[126:127], v[180:181], off
	v_lshl_add_u64 v[180:181], v[132:133], 0, s[42:43]
	global_load_dwordx2 v[128:129], v[180:181], off
	v_mfma_f32_16x16x32_bf16 v[2:5], v[238:241], v[234:237], v[2:5]
	v_mfma_f32_16x16x32_bf16 v[6:9], v[242:245], v[234:237], v[6:9]
	v_mfma_f32_16x16x32_bf16 v[10:13], v[246:249], v[234:237], v[10:13]
	v_mfma_f32_16x16x32_bf16 v[14:17], v[250:253], v[234:237], v[14:17]
	ds_read_b128 v[234:237], v93 offset:8192
	s_waitcnt vmcnt(21)
	s_mov_b32 s49, s46
	s_mov_b32 s46, s47
	s_mov_b32 s47, s48
	s_mov_b32 s48, s49
	s_add_i32 s50, s50, 1
	s_waitcnt lgkmcnt(0)
	s_barrier
; #define MD_GLDS_A(buf, tau) do { _Pragma("unroll") for (int i = 0; i < 5; ++i) if (amask & (1u << i)) \
;         __builtin_amdgcn_global_load_lds((const unsigned*)((const char*)HIDp + aoff[i] + (size_t)((tau) & 7) * 128), (PG8_LAS unsigned*)(MD_SA(buf) + wid * 1024 + i * 8192), 16, 0, 0); } while (0)
; #define MD_B_ISSUE(sb, tau) do { const char* kb_ = Bb + (size_t)((tau) >> 3) * 512 + (size_t)((tau) & 7) * (64 * (size_t)RB); _Pragma("unroll") for (int j = 0; j < 8; ++j) { const char* p_ = kb_ + (size_t)j * RB; \
;         asm volatile("global_load_dwordx2 %0, %1, off" : "=&v"(sb[j]) : "v"(p_) : "memory"); } } while (0)
; #define MD_B_WAIT(sb, N) asm volatile("s_waitcnt vmcnt(%8)" : "+v"(sb[0]), "+v"(sb[1]), "+v"(sb[2]), "+v"(sb[3]), "+v"(sb[4]), "+v"(sb[5]), "+v"(sb[6]), "+v"(sb[7]) : "n"(N) : "memory")
; #define MD_END(last) do { if (last) asm volatile("s_waitcnt vmcnt(0)" ::: "memory"); else asm volatile("s_waitcnt vmcnt(8)" ::: "memory"); \
;         asm volatile("s_waitcnt lgkmcnt(0)" ::: "memory"); __builtin_amdgcn_s_barrier(); asm volatile("" ::: "memory"); } while (0)
; __device__ __forceinline__ void moe_down_stream(PG8_LAS unsigned char* lds, int e, int cb0, int slot0, int nv, const bf16_t* HIDp, const float* Wd, bf16_t* Y, const float* slot_w, const int* slot_dst) {
;     ...
;     for (int t = 0; t < NT; t += 2) {
;         if (t + 2 < NT) MD_B_WAIT(s1, 8); else MD_B_WAIT(s1, 0);
;         MD_B_WRITE(s1, 1); __builtin_amdgcn_sched_barrier(0); MD_GLDS_A(1, t + 1); __builtin_amdgcn_sched_barrier(0);
;         if (t + 3 < NT) MD_B_ISSUE(s1, t + 3);
;         MD_COMPUTE(0);
;         MD_END(t + 3 >= NT);
;         if (t + 2 < NT) { MD_B_WAIT(s0, 8); MD_B_WRITE(s0, 0); __builtin_amdgcn_sched_barrier(0); MD_GLDS_A(0, t + 2); __builtin_amdgcn_sched_barrier(0); }
;         if (t + 4 < NT) MD_B_ISSUE(s0, t + 4);
;         MD_COMPUTE(1);
;         MD_END(t + 4 >= NT);
	s_add_i32 s49, s48, s74
	s_add_i32 s52, s52, 1
	s_and_b32 s54, s52, 7
	s_cmp_eq_u32 s54, 0
	s_cselect_b32 s54, s53, s32
	s_cselect_b32 s55, -1, 0
	s_add_u32 s30, s30, s54
	s_addc_u32 s31, s31, s55
	v_mfma_f32_16x16x32_bf16 v[78:81], v[142:145], v[218:221], v[78:81]
	v_mfma_f32_16x16x32_bf16 v[74:77], v[146:149], v[218:221], v[74:77]
	v_mfma_f32_16x16x32_bf16 v[70:73], v[156:159], v[218:221], v[70:73]
	v_mfma_f32_16x16x32_bf16 v[66:69], v[160:163], v[218:221], v[66:69]
	s_mov_b32 m0, s49
	s_nop 0
	global_load_lds_dwordx4 v88, s[30:31]
	v_mfma_f32_16x16x32_bf16 v[62:65], v[142:145], v[222:225], v[62:65]
	v_mfma_f32_16x16x32_bf16 v[58:61], v[146:149], v[222:225], v[58:61]
	v_mfma_f32_16x16x32_bf16 v[54:57], v[156:159], v[222:225], v[54:57]
	v_mfma_f32_16x16x32_bf16 v[50:53], v[160:163], v[222:225], v[50:53]
	s_add_i32 m0, s49, 0x2000
	s_nop 0
	global_load_lds_dwordx4 v90, s[30:31]
	v_mfma_f32_16x16x32_bf16 v[46:49], v[142:145], v[226:229], v[46:49]
	v_mfma_f32_16x16x32_bf16 v[42:45], v[146:149], v[226:229], v[42:45]
	v_mfma_f32_16x16x32_bf16 v[38:41], v[156:159], v[226:229], v[38:41]
	v_mfma_f32_16x16x32_bf16 v[34:37], v[160:163], v[226:229], v[34:37]
	s_add_i32 m0, s49, 0x4000
	s_nop 0
	global_load_lds_dwordx4 v92, s[30:31]
	v_mfma_f32_16x16x32_bf16 v[18:21], v[142:145], v[230:233], v[18:21]
	v_mfma_f32_16x16x32_bf16 v[22:25], v[146:149], v[230:233], v[22:25]
	v_mfma_f32_16x16x32_bf16 v[26:29], v[156:159], v[230:233], v[26:29]
	v_mfma_f32_16x16x32_bf16 v[30:33], v[160:163], v[230:233], v[30:33]
	s_add_i32 m0, s49, 0x6000
	s_nop 0
	global_load_lds_dwordx4 v94, s[30:31]
	v_mfma_f32_16x16x32_bf16 v[2:5], v[142:145], v[234:237], v[2:5]
	v_mfma_f32_16x16x32_bf16 v[6:9], v[146:149], v[234:237], v[6:9]
	v_mfma_f32_16x16x32_bf16 v[10:13], v[156:159], v[234:237], v[10:13]
	v_mfma_f32_16x16x32_bf16 v[14:17], v[160:163], v[234:237], v[14:17]
	s_add_i32 m0, s49, 0x8000
	s_nop 0
	global_load_lds_dwordx4 v96, s[30:31]
	v_cvt_pk_bf16_f32 v172, v186, v188
	v_cvt_pk_bf16_f32 v173, v190, v192
	v_cvt_pk_bf16_f32 v174, v194, v196
	v_cvt_pk_bf16_f32 v175, v198, v200
	v_cvt_pk_bf16_f32 v176, v187, v189
	v_cvt_pk_bf16_f32 v177, v191, v193
	v_cvt_pk_bf16_f32 v178, v195, v197
	v_cvt_pk_bf16_f32 v179, v199, v201
	ds_write_b128 v95, v[172:175] offset:0
	ds_write_b128 v95, v[176:179] offset:128
	v_add_u32_e32 v91, s46, v135
	v_add_u32_e32 v93, s46, v137
	ds_read_b128 v[238:241], v139 offset:19456
	ds_read_b128 v[242:245], v139 offset:21504
	ds_read_b128 v[246:249], v139 offset:23552
	ds_read_b128 v[250:253], v139 offset:25600
	ds_read_b128 v[218:221], v91 offset:0
	ds_read_b128 v[222:225], v91 offset:2048
	ds_read_b128 v[226:229], v91 offset:4096
	ds_read_b128 v[230:233], v91 offset:6144
	ds_read_b128 v[234:237], v91 offset:8192
	s_waitcnt lgkmcnt(0)
	v_mfma_f32_16x16x32_bf16 v[78:81], v[238:241], v[218:221], v[78:81]
	v_mfma_f32_16x16x32_bf16 v[74:77], v[242:245], v[218:221], v[74:77]
	v_mfma_f32_16x16x32_bf16 v[70:73], v[246:249], v[218:221], v[70:73]
	v_mfma_f32_16x16x32_bf16 v[66:69], v[250:253], v[218:221], v[66:69]
	ds_read_b128 v[218:221], v93 offset:0
	ds_read_b128 v[142:145], v141 offset:19456
	s_add_i32 s51, s51, 1
	s_and_b32 s54, s51, 7
	s_cmp_eq_u32 s54, 0
	s_cselect_b32 s44, s34, s35
	s_cselect_b32 s45, -1, 0
	v_lshl_add_u64 v[132:133], v[132:133], 0, s[44:45]
	global_load_dwordx2 v[186:187], v[132:133], off
	v_lshl_add_u64 v[180:181], v[132:133], 0, s[24:25]
	global_load_dwordx2 v[188:189], v[180:181], off
	v_mfma_f32_16x16x32_bf16 v[62:65], v[238:241], v[222:225], v[62:65]
	v_mfma_f32_16x16x32_bf16 v[58:61], v[242:245], v[222:225], v[58:61]
	v_mfma_f32_16x16x32_bf16 v[54:57], v[246:249], v[222:225], v[54:57]
	v_mfma_f32_16x16x32_bf16 v[50:53], v[250:253], v[222:225], v[50:53]
	ds_read_b128 v[222:225], v93 offset:2048
	ds_read_b128 v[146:149], v141 offset:21504
	v_lshl_add_u64 v[180:181], v[132:133], 0, s[26:27]
	global_load_dwordx2 v[190:191], v[180:181], off
	v_lshl_add_u64 v[180:181], v[132:133], 0, s[28:29]
	global_load_dwordx2 v[192:193], v[180:181], off
	v_mfma_f32_16x16x32_bf16 v[46:49], v[238:241], v[226:229], v[46:49]
	v_mfma_f32_16x16x32_bf16 v[42:45], v[242:245], v[226:229], v[42:45]
	v_mfma_f32_16x16x32_bf16 v[38:41], v[246:249], v[226:229], v[38:41]
	v_mfma_f32_16x16x32_bf16 v[34:37], v[250:253], v[226:229], v[34:37]
	ds_read_b128 v[226:229], v93 offset:4096
	ds_read_b128 v[156:159], v141 offset:23552
	v_lshl_add_u64 v[180:181], v[132:133], 0, s[36:37]
	global_load_dwordx2 v[194:195], v[180:181], off
	v_lshl_add_u64 v[180:181], v[132:133], 0, s[38:39]
	global_load_dwordx2 v[196:197], v[180:181], off
	v_mfma_f32_16x16x32_bf16 v[18:21], v[238:241], v[230:233], v[18:21]
	v_mfma_f32_16x16x32_bf16 v[22:25], v[242:245], v[230:233], v[22:25]
	v_mfma_f32_16x16x32_bf16 v[26:29], v[246:249], v[230:233], v[26:29]
	v_mfma_f32_16x16x32_bf16 v[30:33], v[250:253], v[230:233], v[30:33]
	ds_read_b128 v[230:233], v93 offset:6144
	ds_read_b128 v[160:163], v141 offset:25600
	v_lshl_add_u64 v[180:181], v[132:133], 0, s[40:41]
	global_load_dwordx2 v[198:199], v[180:181], off
	v_lshl_add_u64 v[180:181], v[132:133], 0, s[42:43]
	global_load_dwordx2 v[200:201], v[180:181], off
	v_mfma_f32_16x16x32_bf16 v[2:5], v[238:241], v[234:237], v[2:5]
	v_mfma_f32_16x16x32_bf16 v[6:9], v[242:245], v[234:237], v[6:9]
	v_mfma_f32_16x16x32_bf16 v[10:13], v[246:249], v[234:237], v[10:13]
	v_mfma_f32_16x16x32_bf16 v[14:17], v[250:253], v[234:237], v[14:17]
	ds_read_b128 v[234:237], v93 offset:8192
	s_waitcnt vmcnt(21)
	s_mov_b32 s49, s46
	s_mov_b32 s46, s47
	s_mov_b32 s47, s48
	s_mov_b32 s48, s49
	s_add_i32 s50, s50, 1
	s_waitcnt lgkmcnt(0)
	s_barrier
; #define MD_GLDS_A(buf, tau) do { _Pragma("unroll") for (int i = 0; i < 5; ++i) if (amask & (1u << i)) \
;         __builtin_amdgcn_global_load_lds((const unsigned*)((const char*)HIDp + aoff[i] + (size_t)((tau) & 7) * 128), (PG8_LAS unsigned*)(MD_SA(buf) + wid * 1024 + i * 8192), 16, 0, 0); } while (0)
; #define MD_B_ISSUE(sb, tau) do { const char* kb_ = Bb + (size_t)((tau) >> 3) * 512 + (size_t)((tau) & 7) * (64 * (size_t)RB); _Pragma("unroll") for (int j = 0; j < 8; ++j) { const char* p_ = kb_ + (size_t)j * RB; \
;         asm volatile("global_load_dwordx2 %0, %1, off" : "=&v"(sb[j]) : "v"(p_) : "memory"); } } while (0)
; #define MD_B_WAIT(sb, N) asm volatile("s_waitcnt vmcnt(%8)" : "+v"(sb[0]), "+v"(sb[1]), "+v"(sb[2]), "+v"(sb[3]), "+v"(sb[4]), "+v"(sb[5]), "+v"(sb[6]), "+v"(sb[7]) : "n"(N) : "memory")
; #define MD_END(last) do { if (last) asm volatile("s_waitcnt vmcnt(0)" ::: "memory"); else asm volatile("s_waitcnt vmcnt(8)" ::: "memory"); \
;         asm volatile("s_waitcnt lgkmcnt(0)" ::: "memory"); __builtin_amdgcn_s_barrier(); asm volatile("" ::: "memory"); } while (0)
; __device__ __forceinline__ void moe_down_stream(PG8_LAS unsigned char* lds, int e, int cb0, int slot0, int nv, const bf16_t* HIDp, const float* Wd, bf16_t* Y, const float* slot_w, const int* slot_dst) {
;     ...
;     for (int t = 0; t < NT; t += 2) {
;         if (t + 2 < NT) MD_B_WAIT(s1, 8); else MD_B_WAIT(s1, 0);
;         MD_B_WRITE(s1, 1); __builtin_amdgcn_sched_barrier(0); MD_GLDS_A(1, t + 1); __builtin_amdgcn_sched_barrier(0);
;         if (t + 3 < NT) MD_B_ISSUE(s1, t + 3);
;         MD_COMPUTE(0);
;         MD_END(t + 3 >= NT);
;         if (t + 2 < NT) { MD_B_WAIT(s0, 8); MD_B_WRITE(s0, 0); __builtin_amdgcn_sched_barrier(0); MD_GLDS_A(0, t + 2); __builtin_amdgcn_sched_barrier(0); }
;         if (t + 4 < NT) MD_B_ISSUE(s0, t + 4);
;         MD_COMPUTE(1);
;         MD_END(t + 4 >= NT);
	s_add_i32 s49, s48, s74
	s_add_i32 s52, s52, 1
	s_and_b32 s54, s52, 7
	s_cmp_eq_u32 s54, 0
	s_cselect_b32 s54, s53, s32
	s_cselect_b32 s55, -1, 0
	s_add_u32 s30, s30, s54
	s_addc_u32 s31, s31, s55
	v_mfma_f32_16x16x32_bf16 v[78:81], v[142:145], v[218:221], v[78:81]
	v_mfma_f32_16x16x32_bf16 v[74:77], v[146:149], v[218:221], v[74:77]
	v_mfma_f32_16x16x32_bf16 v[70:73], v[156:159], v[218:221], v[70:73]
	v_mfma_f32_16x16x32_bf16 v[66:69], v[160:163], v[218:221], v[66:69]
	s_mov_b32 m0, s49
	s_nop 0
	global_load_lds_dwordx4 v88, s[30:31]
	v_mfma_f32_16x16x32_bf16 v[62:65], v[142:145], v[222:225], v[62:65]
	v_mfma_f32_16x16x32_bf16 v[58:61], v[146:149], v[222:225], v[58:61]
	v_mfma_f32_16x16x32_bf16 v[54:57], v[156:159], v[222:225], v[54:57]
	v_mfma_f32_16x16x32_bf16 v[50:53], v[160:163], v[222:225], v[50:53]
	s_add_i32 m0, s49, 0x2000
	s_nop 0
	global_load_lds_dwordx4 v90, s[30:31]
	v_mfma_f32_16x16x32_bf16 v[46:49], v[142:145], v[226:229], v[46:49]
	v_mfma_f32_16x16x32_bf16 v[42:45], v[146:149], v[226:229], v[42:45]
	v_mfma_f32_16x16x32_bf16 v[38:41], v[156:159], v[226:229], v[38:41]
	v_mfma_f32_16x16x32_bf16 v[34:37], v[160:163], v[226:229], v[34:37]
	s_add_i32 m0, s49, 0x4000
	s_nop 0
	global_load_lds_dwordx4 v92, s[30:31]
	v_mfma_f32_16x16x32_bf16 v[18:21], v[142:145], v[230:233], v[18:21]
	v_mfma_f32_16x16x32_bf16 v[22:25], v[146:149], v[230:233], v[22:25]
	v_mfma_f32_16x16x32_bf16 v[26:29], v[156:159], v[230:233], v[26:29]
	v_mfma_f32_16x16x32_bf16 v[30:33], v[160:163], v[230:233], v[30:33]
	s_add_i32 m0, s49, 0x6000
	s_nop 0
	global_load_lds_dwordx4 v94, s[30:31]
	v_mfma_f32_16x16x32_bf16 v[2:5], v[142:145], v[234:237], v[2:5]
	v_mfma_f32_16x16x32_bf16 v[6:9], v[146:149], v[234:237], v[6:9]
	v_mfma_f32_16x16x32_bf16 v[10:13], v[156:159], v[234:237], v[10:13]
	v_mfma_f32_16x16x32_bf16 v[14:17], v[160:163], v[234:237], v[14:17]
	s_add_i32 m0, s49, 0x8000
	s_nop 0
	global_load_lds_dwordx4 v96, s[30:31]
	v_cvt_pk_bf16_f32 v172, v202, v204
	v_cvt_pk_bf16_f32 v173, v206, v208
	v_cvt_pk_bf16_f32 v174, v210, v212
	v_cvt_pk_bf16_f32 v175, v214, v216
	v_cvt_pk_bf16_f32 v176, v203, v205
	v_cvt_pk_bf16_f32 v177, v207, v209
	v_cvt_pk_bf16_f32 v178, v211, v213
	v_cvt_pk_bf16_f32 v179, v215, v217
	ds_write_b128 v95, v[172:175] offset:19456
	ds_write_b128 v95, v[176:179] offset:19584
	v_add_u32_e32 v91, s46, v135
	v_add_u32_e32 v93, s46, v137
	ds_read_b128 v[238:241], v139 offset:0
	ds_read_b128 v[242:245], v139 offset:2048
	ds_read_b128 v[246:249], v139 offset:4096
	ds_read_b128 v[250:253], v139 offset:6144
	ds_read_b128 v[218:221], v91 offset:0
	ds_read_b128 v[222:225], v91 offset:2048
	ds_read_b128 v[226:229], v91 offset:4096
	ds_read_b128 v[230:233], v91 offset:6144
	ds_read_b128 v[234:237], v91 offset:8192
	s_waitcnt lgkmcnt(0)
	v_mfma_f32_16x16x32_bf16 v[78:81], v[238:241], v[218:221], v[78:81]
	v_mfma_f32_16x16x32_bf16 v[74:77], v[242:245], v[218:221], v[74:77]
	v_mfma_f32_16x16x32_bf16 v[70:73], v[246:249], v[218:221], v[70:73]
	v_mfma_f32_16x16x32_bf16 v[66:69], v[250:253], v[218:221], v[66:69]
	ds_read_b128 v[218:221], v93 offset:0
	ds_read_b128 v[142:145], v141 offset:0
	s_add_i32 s51, s51, 1
	s_and_b32 s54, s51, 7
	s_cmp_eq_u32 s54, 0
	s_cselect_b32 s44, s34, s35
	s_cselect_b32 s45, -1, 0
	v_lshl_add_u64 v[132:133], v[132:133], 0, s[44:45]
	global_load_dwordx2 v[202:203], v[132:133], off
	v_lshl_add_u64 v[180:181], v[132:133], 0, s[24:25]
	global_load_dwordx2 v[204:205], v[180:181], off
	v_mfma_f32_16x16x32_bf16 v[62:65], v[238:241], v[222:225], v[62:65]
	v_mfma_f32_16x16x32_bf16 v[58:61], v[242:245], v[222:225], v[58:61]
	v_mfma_f32_16x16x32_bf16 v[54:57], v[246:249], v[222:225], v[54:57]
	v_mfma_f32_16x16x32_bf16 v[50:53], v[250:253], v[222:225], v[50:53]
	ds_read_b128 v[222:225], v93 offset:2048
	ds_read_b128 v[146:149], v141 offset:2048
	v_lshl_add_u64 v[180:181], v[132:133], 0, s[26:27]
	global_load_dwordx2 v[206:207], v[180:181], off
	v_lshl_add_u64 v[180:181], v[132:133], 0, s[28:29]
	global_load_dwordx2 v[208:209], v[180:181], off
	v_mfma_f32_16x16x32_bf16 v[46:49], v[238:241], v[226:229], v[46:49]
	v_mfma_f32_16x16x32_bf16 v[42:45], v[242:245], v[226:229], v[42:45]
	v_mfma_f32_16x16x32_bf16 v[38:41], v[246:249], v[226:229], v[38:41]
	v_mfma_f32_16x16x32_bf16 v[34:37], v[250:253], v[226:229], v[34:37]
	ds_read_b128 v[226:229], v93 offset:4096
	ds_read_b128 v[156:159], v141 offset:4096
	v_lshl_add_u64 v[180:181], v[132:133], 0, s[36:37]
	global_load_dwordx2 v[210:211], v[180:181], off
	v_lshl_add_u64 v[180:181], v[132:133], 0, s[38:39]
	global_load_dwordx2 v[212:213], v[180:181], off
	v_mfma_f32_16x16x32_bf16 v[18:21], v[238:241], v[230:233], v[18:21]
	v_mfma_f32_16x16x32_bf16 v[22:25], v[242:245], v[230:233], v[22:25]
	v_mfma_f32_16x16x32_bf16 v[26:29], v[246:249], v[230:233], v[26:29]
	v_mfma_f32_16x16x32_bf16 v[30:33], v[250:253], v[230:233], v[30:33]
	ds_read_b128 v[230:233], v93 offset:6144
	ds_read_b128 v[160:163], v141 offset:6144
	v_lshl_add_u64 v[180:181], v[132:133], 0, s[40:41]
	global_load_dwordx2 v[214:215], v[180:181], off
	v_lshl_add_u64 v[180:181], v[132:133], 0, s[42:43]
	global_load_dwordx2 v[216:217], v[180:181], off
	v_mfma_f32_16x16x32_bf16 v[2:5], v[238:241], v[234:237], v[2:5]
	v_mfma_f32_16x16x32_bf16 v[6:9], v[242:245], v[234:237], v[6:9]
	v_mfma_f32_16x16x32_bf16 v[10:13], v[246:249], v[234:237], v[10:13]
	v_mfma_f32_16x16x32_bf16 v[14:17], v[250:253], v[234:237], v[14:17]
	ds_read_b128 v[234:237], v93 offset:8192
	s_waitcnt vmcnt(21)
	s_mov_b32 s49, s46
	s_mov_b32 s46, s47
	s_mov_b32 s47, s48
	s_mov_b32 s48, s49
	s_add_i32 s50, s50, 1
	s_waitcnt lgkmcnt(0)
	s_barrier
; #define MD_GLDS_A(buf, tau) do { _Pragma("unroll") for (int i = 0; i < 5; ++i) if (amask & (1u << i)) \
;         __builtin_amdgcn_global_load_lds((const unsigned*)((const char*)HIDp + aoff[i] + (size_t)((tau) & 7) * 128), (PG8_LAS unsigned*)(MD_SA(buf) + wid * 1024 + i * 8192), 16, 0, 0); } while (0)
; #define MD_B_ISSUE(sb, tau) do { const char* kb_ = Bb + (size_t)((tau) >> 3) * 512 + (size_t)((tau) & 7) * (64 * (size_t)RB); _Pragma("unroll") for (int j = 0; j < 8; ++j) { const char* p_ = kb_ + (size_t)j * RB; \
;         asm volatile("global_load_dwordx2 %0, %1, off" : "=&v"(sb[j]) : "v"(p_) : "memory"); } } while (0)
; #define MD_B_WAIT(sb, N) asm volatile("s_waitcnt vmcnt(%8)" : "+v"(sb[0]), "+v"(sb[1]), "+v"(sb[2]), "+v"(sb[3]), "+v"(sb[4]), "+v"(sb[5]), "+v"(sb[6]), "+v"(sb[7]) : "n"(N) : "memory")
; #define MD_END(last) do { if (last) asm volatile("s_waitcnt vmcnt(0)" ::: "memory"); else asm volatile("s_waitcnt vmcnt(8)" ::: "memory"); \
;         asm volatile("s_waitcnt lgkmcnt(0)" ::: "memory"); __builtin_amdgcn_s_barrier(); asm volatile("" ::: "memory"); } while (0)
; __device__ __forceinline__ void moe_down_stream(PG8_LAS unsigned char* lds, int e, int cb0, int slot0, int nv, const bf16_t* HIDp, const float* Wd, bf16_t* Y, const float* slot_w, const int* slot_dst) {
;     ...
;     for (int t = 0; t < NT; t += 2) {
;         if (t + 2 < NT) MD_B_WAIT(s1, 8); else MD_B_WAIT(s1, 0);
;         MD_B_WRITE(s1, 1); __builtin_amdgcn_sched_barrier(0); MD_GLDS_A(1, t + 1); __builtin_amdgcn_sched_barrier(0);
;         if (t + 3 < NT) MD_B_ISSUE(s1, t + 3);
;         MD_COMPUTE(0);
;         MD_END(t + 3 >= NT);
;         if (t + 2 < NT) { MD_B_WAIT(s0, 8); MD_B_WRITE(s0, 0); __builtin_amdgcn_sched_barrier(0); MD_GLDS_A(0, t + 2); __builtin_amdgcn_sched_barrier(0); }
;         if (t + 4 < NT) MD_B_ISSUE(s0, t + 4);
;         MD_COMPUTE(1);
;         MD_END(t + 4 >= NT);
	s_add_i32 s49, s48, s74
	s_add_i32 s52, s52, 1
	s_and_b32 s54, s52, 7
	s_cmp_eq_u32 s54, 0
	s_cselect_b32 s54, s53, s32
	s_cselect_b32 s55, -1, 0
	s_add_u32 s30, s30, s54
	s_addc_u32 s31, s31, s55
	v_mfma_f32_16x16x32_bf16 v[78:81], v[142:145], v[218:221], v[78:81]
	v_mfma_f32_16x16x32_bf16 v[74:77], v[146:149], v[218:221], v[74:77]
	v_mfma_f32_16x16x32_bf16 v[70:73], v[156:159], v[218:221], v[70:73]
	v_mfma_f32_16x16x32_bf16 v[66:69], v[160:163], v[218:221], v[66:69]
	s_mov_b32 m0, s49
	s_nop 0
	global_load_lds_dwordx4 v88, s[30:31]
	v_mfma_f32_16x16x32_bf16 v[62:65], v[142:145], v[222:225], v[62:65]
	v_mfma_f32_16x16x32_bf16 v[58:61], v[146:149], v[222:225], v[58:61]
	v_mfma_f32_16x16x32_bf16 v[54:57], v[156:159], v[222:225], v[54:57]
	v_mfma_f32_16x16x32_bf16 v[50:53], v[160:163], v[222:225], v[50:53]
	s_add_i32 m0, s49, 0x2000
	s_nop 0
	global_load_lds_dwordx4 v90, s[30:31]
	v_mfma_f32_16x16x32_bf16 v[46:49], v[142:145], v[226:229], v[46:49]
	v_mfma_f32_16x16x32_bf16 v[42:45], v[146:149], v[226:229], v[42:45]
	v_mfma_f32_16x16x32_bf16 v[38:41], v[156:159], v[226:229], v[38:41]
	v_mfma_f32_16x16x32_bf16 v[34:37], v[160:163], v[226:229], v[34:37]
	s_add_i32 m0, s49, 0x4000
	s_nop 0
	global_load_lds_dwordx4 v92, s[30:31]
	v_mfma_f32_16x16x32_bf16 v[18:21], v[142:145], v[230:233], v[18:21]
	v_mfma_f32_16x16x32_bf16 v[22:25], v[146:149], v[230:233], v[22:25]
	v_mfma_f32_16x16x32_bf16 v[26:29], v[156:159], v[230:233], v[26:29]
	v_mfma_f32_16x16x32_bf16 v[30:33], v[160:163], v[230:233], v[30:33]
	s_add_i32 m0, s49, 0x6000
	s_nop 0
	global_load_lds_dwordx4 v94, s[30:31]
	v_mfma_f32_16x16x32_bf16 v[2:5], v[142:145], v[234:237], v[2:5]
	v_mfma_f32_16x16x32_bf16 v[6:9], v[146:149], v[234:237], v[6:9]
	v_mfma_f32_16x16x32_bf16 v[10:13], v[156:159], v[234:237], v[10:13]
	v_mfma_f32_16x16x32_bf16 v[14:17], v[160:163], v[234:237], v[14:17]
	s_add_i32 m0, s49, 0x8000
	s_nop 0
	global_load_lds_dwordx4 v96, s[30:31]
	v_cvt_pk_bf16_f32 v172, v98, v100
	v_cvt_pk_bf16_f32 v173, v102, v104
	v_cvt_pk_bf16_f32 v174, v106, v108
	v_cvt_pk_bf16_f32 v175, v110, v112
	v_cvt_pk_bf16_f32 v176, v99, v101
	v_cvt_pk_bf16_f32 v177, v103, v105
	v_cvt_pk_bf16_f32 v178, v107, v109
	v_cvt_pk_bf16_f32 v179, v111, v113
	ds_write_b128 v95, v[172:175] offset:0
	ds_write_b128 v95, v[176:179] offset:128
	v_add_u32_e32 v91, s46, v135
	v_add_u32_e32 v93, s46, v137
	ds_read_b128 v[238:241], v139 offset:19456
	ds_read_b128 v[242:245], v139 offset:21504
	ds_read_b128 v[246:249], v139 offset:23552
	ds_read_b128 v[250:253], v139 offset:25600
	ds_read_b128 v[218:221], v91 offset:0
	ds_read_b128 v[222:225], v91 offset:2048
	ds_read_b128 v[226:229], v91 offset:4096
	ds_read_b128 v[230:233], v91 offset:6144
	ds_read_b128 v[234:237], v91 offset:8192
	s_waitcnt lgkmcnt(0)
	v_mfma_f32_16x16x32_bf16 v[78:81], v[238:241], v[218:221], v[78:81]
	v_mfma_f32_16x16x32_bf16 v[74:77], v[242:245], v[218:221], v[74:77]
	v_mfma_f32_16x16x32_bf16 v[70:73], v[246:249], v[218:221], v[70:73]
	v_mfma_f32_16x16x32_bf16 v[66:69], v[250:253], v[218:221], v[66:69]
	ds_read_b128 v[218:221], v93 offset:0
	ds_read_b128 v[142:145], v141 offset:19456
	s_add_i32 s51, s51, 1
	s_and_b32 s54, s51, 7
	s_cmp_eq_u32 s54, 0
	s_cselect_b32 s44, s34, s35
	s_cselect_b32 s45, -1, 0
	v_lshl_add_u64 v[132:133], v[132:133], 0, s[44:45]
	global_load_dwordx2 v[98:99], v[132:133], off
	v_lshl_add_u64 v[180:181], v[132:133], 0, s[24:25]
	global_load_dwordx2 v[100:101], v[180:181], off
	v_mfma_f32_16x16x32_bf16 v[62:65], v[238:241], v[222:225], v[62:65]
	v_mfma_f32_16x16x32_bf16 v[58:61], v[242:245], v[222:225], v[58:61]
	v_mfma_f32_16x16x32_bf16 v[54:57], v[246:249], v[222:225], v[54:57]
	v_mfma_f32_16x16x32_bf16 v[50:53], v[250:253], v[222:225], v[50:53]
	ds_read_b128 v[222:225], v93 offset:2048
	ds_read_b128 v[146:149], v141 offset:21504
	v_lshl_add_u64 v[180:181], v[132:133], 0, s[26:27]
	global_load_dwordx2 v[102:103], v[180:181], off
	v_lshl_add_u64 v[180:181], v[132:133], 0, s[28:29]
	global_load_dwordx2 v[104:105], v[180:181], off
	v_mfma_f32_16x16x32_bf16 v[46:49], v[238:241], v[226:229], v[46:49]
	v_mfma_f32_16x16x32_bf16 v[42:45], v[242:245], v[226:229], v[42:45]
	v_mfma_f32_16x16x32_bf16 v[38:41], v[246:249], v[226:229], v[38:41]
	v_mfma_f32_16x16x32_bf16 v[34:37], v[250:253], v[226:229], v[34:37]
	ds_read_b128 v[226:229], v93 offset:4096
	ds_read_b128 v[156:159], v141 offset:23552
	v_lshl_add_u64 v[180:181], v[132:133], 0, s[36:37]
	global_load_dwordx2 v[106:107], v[180:181], off
	v_lshl_add_u64 v[180:181], v[132:133], 0, s[38:39]
	global_load_dwordx2 v[108:109], v[180:181], off
	v_mfma_f32_16x16x32_bf16 v[18:21], v[238:241], v[230:233], v[18:21]
	v_mfma_f32_16x16x32_bf16 v[22:25], v[242:245], v[230:233], v[22:25]
	v_mfma_f32_16x16x32_bf16 v[26:29], v[246:249], v[230:233], v[26:29]
	v_mfma_f32_16x16x32_bf16 v[30:33], v[250:253], v[230:233], v[30:33]
	ds_read_b128 v[230:233], v93 offset:6144
	ds_read_b128 v[160:163], v141 offset:25600
	v_lshl_add_u64 v[180:181], v[132:133], 0, s[40:41]
	global_load_dwordx2 v[110:111], v[180:181], off
	v_lshl_add_u64 v[180:181], v[132:133], 0, s[42:43]
	global_load_dwordx2 v[112:113], v[180:181], off
	v_mfma_f32_16x16x32_bf16 v[2:5], v[238:241], v[234:237], v[2:5]
	v_mfma_f32_16x16x32_bf16 v[6:9], v[242:245], v[234:237], v[6:9]
	v_mfma_f32_16x16x32_bf16 v[10:13], v[246:249], v[234:237], v[10:13]
	v_mfma_f32_16x16x32_bf16 v[14:17], v[250:253], v[234:237], v[14:17]
	ds_read_b128 v[234:237], v93 offset:8192
	s_waitcnt vmcnt(21)
	s_mov_b32 s49, s46
	s_mov_b32 s46, s47
	s_mov_b32 s47, s48
	s_mov_b32 s48, s49
	s_add_i32 s50, s50, 1
	s_waitcnt lgkmcnt(0)
	s_barrier
; #define PG8_LAS __attribute__((address_space(3)))
; __device__ __forceinline__ unsigned cvtpk(float lo, float hi) { f32x2 v = {lo, hi}; bf16x2_t b = __builtin_convertvector(v, bf16x2_t); return __builtin_bit_cast(unsigned, b); }
; __device__ __forceinline__ void moe_down_stream(PG8_LAS unsigned char* lds, int e, int cb0, int slot0, int nv, const bf16_t* HIDp, const float* Wd, bf16_t* Y, const float* slot_w, const int* slot_dst) {
;     ...
;         if (((t + 1) & 7) == 7) {
;             const int cb = cb0 + ((t + 1) >> 3);
; #pragma unroll
;             for (int m = 0; m < DNM; ++m) {
;                 const float w_ = lw[4 * (16 * m + fr) + wr];
; #pragma unroll
;                 for (int p = 0; p < 2; ++p) { const f32x4 v0 = acc[m][2 * p] * w_, v1 = acc[m][2 * p + 1] * w_; u32x4 w; w.x = cvtpk(v0[0], v0[1]); w.y = cvtpk(v0[2], v0[3]); w.z = cvtpk(v1[0], v1[1]); w.w = cvtpk(v1[2], v1[3]);
;                     *(PG8_LAS u32x4*)(stg + fr * 128 + (((4 * p + fq) ^ (fr & 7)) * 16)) = w; }
; #pragma unroll
;                 for (int hh = 0; hh < 2; ++hh) { const int r = (lane >> 3) + 8 * hh, cc = lane & 7; const u32x4 d = *(const PG8_LAS u32x4*)(stg + r * 128 + ((cc ^ (r & 7)) * 16)); const int dst_ = ldst[4 * (16 * m + r) + wr];
;                     if (dst_ >= 0) *(u32x4*)(Y + (size_t)dst_ * D + 128 * cb + 64 * wc + 8 * cc) = d; }
; #pragma unroll
;                 for (int n = 0; n < 4; ++n) acc[m][n] = (f32x4){0.f, 0.f, 0.f, 0.f}; } }
	s_sub_u32 s56, s56, 1
	s_cmp_lg_u32 s56, 0
	s_cbranch_scc1 .Lmd_loop_Y
	v_mfma_f32_16x16x32_bf16 v[78:81], v[142:145], v[218:221], v[78:81]
	v_mfma_f32_16x16x32_bf16 v[74:77], v[146:149], v[218:221], v[74:77]
	v_mfma_f32_16x16x32_bf16 v[70:73], v[156:159], v[218:221], v[70:73]
	v_mfma_f32_16x16x32_bf16 v[66:69], v[160:163], v[218:221], v[66:69]
	v_mfma_f32_16x16x32_bf16 v[62:65], v[142:145], v[222:225], v[62:65]
	v_mfma_f32_16x16x32_bf16 v[58:61], v[146:149], v[222:225], v[58:61]
	v_mfma_f32_16x16x32_bf16 v[54:57], v[156:159], v[222:225], v[54:57]
	v_mfma_f32_16x16x32_bf16 v[50:53], v[160:163], v[222:225], v[50:53]
	v_mfma_f32_16x16x32_bf16 v[46:49], v[142:145], v[226:229], v[46:49]
	v_mfma_f32_16x16x32_bf16 v[42:45], v[146:149], v[226:229], v[42:45]
	v_mfma_f32_16x16x32_bf16 v[38:41], v[156:159], v[226:229], v[38:41]
	v_mfma_f32_16x16x32_bf16 v[34:37], v[160:163], v[226:229], v[34:37]
	v_mfma_f32_16x16x32_bf16 v[18:21], v[142:145], v[230:233], v[18:21]
	v_mfma_f32_16x16x32_bf16 v[22:25], v[146:149], v[230:233], v[22:25]
	v_mfma_f32_16x16x32_bf16 v[26:29], v[156:159], v[230:233], v[26:29]
	v_mfma_f32_16x16x32_bf16 v[30:33], v[160:163], v[230:233], v[30:33]
	v_mfma_f32_16x16x32_bf16 v[2:5], v[142:145], v[234:237], v[2:5]
	v_mfma_f32_16x16x32_bf16 v[6:9], v[146:149], v[234:237], v[6:9]
	v_mfma_f32_16x16x32_bf16 v[10:13], v[156:159], v[234:237], v[10:13]
	v_mfma_f32_16x16x32_bf16 v[14:17], v[160:163], v[234:237], v[14:17]
	s_add_i32 s54, s48, s74
	v_add_u32_e32 v164, s54, v84
	v_add_u32_e32 v165, s54, v85
	ds_read_b32 v150, v82 offset:0
	ds_read_b32 v151, v83 offset:0
	ds_read_b32 v166, v83 offset:128
	s_waitcnt lgkmcnt(2)
	v_mul_f32_e32 v78, v150, v78
	v_mul_f32_e32 v79, v150, v79
	v_mul_f32_e32 v80, v150, v80
	v_mul_f32_e32 v81, v150, v81
	v_mul_f32_e32 v74, v150, v74
	v_mul_f32_e32 v75, v150, v75
	v_mul_f32_e32 v76, v150, v76
	v_mul_f32_e32 v77, v150, v77
	v_cvt_pk_bf16_f32 v182, v78, v79
	v_cvt_pk_bf16_f32 v183, v80, v81
	v_cvt_pk_bf16_f32 v184, v74, v75
	v_cvt_pk_bf16_f32 v185, v76, v77
	ds_write_b128 v164, v[182:185]
	v_mul_f32_e32 v70, v150, v70
	v_mul_f32_e32 v71, v150, v71
	v_mul_f32_e32 v72, v150, v72
	v_mul_f32_e32 v73, v150, v73
	v_mul_f32_e32 v66, v150, v66
	v_mul_f32_e32 v67, v150, v67
	v_mul_f32_e32 v68, v150, v68
	v_mul_f32_e32 v69, v150, v69
	v_cvt_pk_bf16_f32 v182, v70, v71
	v_cvt_pk_bf16_f32 v183, v72, v73
	v_cvt_pk_bf16_f32 v184, v66, v67
	v_cvt_pk_bf16_f32 v185, v68, v69
	v_xor_b32_e32 v167, 64, v164
	ds_write_b128 v167, v[182:185]
	v_mov_b32_e32 v78, 0
	v_mov_b32_e32 v74, 0
	v_mov_b32_e32 v70, 0
	v_mov_b32_e32 v66, 0
	v_mov_b32_e32 v79, 0
	v_mov_b32_e32 v75, 0
	v_mov_b32_e32 v71, 0
	v_mov_b32_e32 v67, 0
	v_mov_b32_e32 v80, 0
	v_mov_b32_e32 v76, 0
	v_mov_b32_e32 v72, 0
	v_mov_b32_e32 v68, 0
	v_mov_b32_e32 v81, 0
	v_mov_b32_e32 v77, 0
	v_mov_b32_e32 v73, 0
	v_mov_b32_e32 v69, 0
	ds_read_b128 v[182:185], v165 offset:0
	v_cmp_lt_i32_e32 vcc, -1, v151
	v_lshlrev_b32_e32 v148, 13, v151
	v_mov_b32_e32 v149, 0
	v_lshl_add_u64 v[148:149], v[148:149], 0, v[86:87]
	v_cndmask_b32_e32 v148, v168, v148, vcc
	v_cndmask_b32_e32 v149, v169, v149, vcc
	s_waitcnt lgkmcnt(0)
	global_store_dwordx4 v[148:149], v[182:185], off
	ds_read_b128 v[182:185], v165 offset:8192
	v_cmp_lt_i32_e32 vcc, -1, v166
	v_lshlrev_b32_e32 v148, 13, v166
	v_mov_b32_e32 v149, 0
	v_lshl_add_u64 v[148:149], v[148:149], 0, v[86:87]
	v_cndmask_b32_e32 v148, v168, v148, vcc
	v_cndmask_b32_e32 v149, v169, v149, vcc
	s_waitcnt lgkmcnt(0)
	global_store_dwordx4 v[148:149], v[182:185], off
	ds_read_b32 v150, v82 offset:256
	ds_read_b32 v151, v83 offset:256
	ds_read_b32 v166, v83 offset:384
	s_waitcnt lgkmcnt(2)
	v_mul_f32_e32 v62, v150, v62
	v_mul_f32_e32 v63, v150, v63
	v_mul_f32_e32 v64, v150, v64
	v_mul_f32_e32 v65, v150, v65
	v_mul_f32_e32 v58, v150, v58
	v_mul_f32_e32 v59, v150, v59
	v_mul_f32_e32 v60, v150, v60
	v_mul_f32_e32 v61, v150, v61
	v_cvt_pk_bf16_f32 v182, v62, v63
	v_cvt_pk_bf16_f32 v183, v64, v65
	v_cvt_pk_bf16_f32 v184, v58, v59
	v_cvt_pk_bf16_f32 v185, v60, v61
	ds_write_b128 v164, v[182:185]
	v_mul_f32_e32 v54, v150, v54
	v_mul_f32_e32 v55, v150, v55
	v_mul_f32_e32 v56, v150, v56
	v_mul_f32_e32 v57, v150, v57
	v_mul_f32_e32 v50, v150, v50
	v_mul_f32_e32 v51, v150, v51
	v_mul_f32_e32 v52, v150, v52
	v_mul_f32_e32 v53, v150, v53
	v_cvt_pk_bf16_f32 v182, v54, v55
	v_cvt_pk_bf16_f32 v183, v56, v57
	v_cvt_pk_bf16_f32 v184, v50, v51
	v_cvt_pk_bf16_f32 v185, v52, v53
	v_xor_b32_e32 v167, 64, v164
	ds_write_b128 v167, v[182:185]
	v_mov_b32_e32 v62, 0
	v_mov_b32_e32 v58, 0
	v_mov_b32_e32 v54, 0
	v_mov_b32_e32 v50, 0
	v_mov_b32_e32 v63, 0
	v_mov_b32_e32 v59, 0
	v_mov_b32_e32 v55, 0
	v_mov_b32_e32 v51, 0
	v_mov_b32_e32 v64, 0
	v_mov_b32_e32 v60, 0
	v_mov_b32_e32 v56, 0
	v_mov_b32_e32 v52, 0
	v_mov_b32_e32 v65, 0
	v_mov_b32_e32 v61, 0
	v_mov_b32_e32 v57, 0
	v_mov_b32_e32 v53, 0
	ds_read_b128 v[182:185], v165 offset:0
	v_cmp_lt_i32_e32 vcc, -1, v151
	v_lshlrev_b32_e32 v148, 13, v151
	v_mov_b32_e32 v149, 0
	v_lshl_add_u64 v[148:149], v[148:149], 0, v[86:87]
	v_cndmask_b32_e32 v148, v168, v148, vcc
	v_cndmask_b32_e32 v149, v169, v149, vcc
	s_waitcnt lgkmcnt(0)
	global_store_dwordx4 v[148:149], v[182:185], off
	ds_read_b128 v[182:185], v165 offset:8192
	v_cmp_lt_i32_e32 vcc, -1, v166
	v_lshlrev_b32_e32 v148, 13, v166
	v_mov_b32_e32 v149, 0
	v_lshl_add_u64 v[148:149], v[148:149], 0, v[86:87]
	v_cndmask_b32_e32 v148, v168, v148, vcc
	v_cndmask_b32_e32 v149, v169, v149, vcc
	s_waitcnt lgkmcnt(0)
	global_store_dwordx4 v[148:149], v[182:185], off
	ds_read_b32 v150, v82 offset:512
	ds_read_b32 v151, v83 offset:512
	ds_read_b32 v166, v83 offset:640
	s_waitcnt lgkmcnt(2)
; #define PG8_LAS __attribute__((address_space(3)))
; __device__ __forceinline__ unsigned cvtpk(float lo, float hi) { f32x2 v = {lo, hi}; bf16x2_t b = __builtin_convertvector(v, bf16x2_t); return __builtin_bit_cast(unsigned, b); }
; __device__ __forceinline__ void moe_down_stream(PG8_LAS unsigned char* lds, int e, int cb0, int slot0, int nv, const bf16_t* HIDp, const float* Wd, bf16_t* Y, const float* slot_w, const int* slot_dst) {
;     ...
;         if (((t + 1) & 7) == 7) {
;             const int cb = cb0 + ((t + 1) >> 3);
; #pragma unroll
;             for (int m = 0; m < DNM; ++m) {
;                 const float w_ = lw[4 * (16 * m + fr) + wr];
; #pragma unroll
;                 for (int p = 0; p < 2; ++p) { const f32x4 v0 = acc[m][2 * p] * w_, v1 = acc[m][2 * p + 1] * w_; u32x4 w; w.x = cvtpk(v0[0], v0[1]); w.y = cvtpk(v0[2], v0[3]); w.z = cvtpk(v1[0], v1[1]); w.w = cvtpk(v1[2], v1[3]);
;                     *(PG8_LAS u32x4*)(stg + fr * 128 + (((4 * p + fq) ^ (fr & 7)) * 16)) = w; }
; #pragma unroll
;                 for (int hh = 0; hh < 2; ++hh) { const int r = (lane >> 3) + 8 * hh, cc = lane & 7; const u32x4 d = *(const PG8_LAS u32x4*)(stg + r * 128 + ((cc ^ (r & 7)) * 16)); const int dst_ = ldst[4 * (16 * m + r) + wr];
;                     if (dst_ >= 0) *(u32x4*)(Y + (size_t)dst_ * D + 128 * cb + 64 * wc + 8 * cc) = d; }
; #pragma unroll
;                 for (int n = 0; n < 4; ++n) acc[m][n] = (f32x4){0.f, 0.f, 0.f, 0.f}; } }
	v_mul_f32_e32 v46, v150, v46
	v_mul_f32_e32 v47, v150, v47
	v_mul_f32_e32 v48, v150, v48
	v_mul_f32_e32 v49, v150, v49
	v_mul_f32_e32 v42, v150, v42
	v_mul_f32_e32 v43, v150, v43
	v_mul_f32_e32 v44, v150, v44
	v_mul_f32_e32 v45, v150, v45
	v_cvt_pk_bf16_f32 v182, v46, v47
	v_cvt_pk_bf16_f32 v183, v48, v49
	v_cvt_pk_bf16_f32 v184, v42, v43
	v_cvt_pk_bf16_f32 v185, v44, v45
	ds_write_b128 v164, v[182:185]
	v_mul_f32_e32 v38, v150, v38
	v_mul_f32_e32 v39, v150, v39
	v_mul_f32_e32 v40, v150, v40
	v_mul_f32_e32 v41, v150, v41
	v_mul_f32_e32 v34, v150, v34
	v_mul_f32_e32 v35, v150, v35
	v_mul_f32_e32 v36, v150, v36
	v_mul_f32_e32 v37, v150, v37
	v_cvt_pk_bf16_f32 v182, v38, v39
	v_cvt_pk_bf16_f32 v183, v40, v41
	v_cvt_pk_bf16_f32 v184, v34, v35
	v_cvt_pk_bf16_f32 v185, v36, v37
	v_xor_b32_e32 v167, 64, v164
	ds_write_b128 v167, v[182:185]
	v_mov_b32_e32 v46, 0
	v_mov_b32_e32 v42, 0
	v_mov_b32_e32 v38, 0
	v_mov_b32_e32 v34, 0
	v_mov_b32_e32 v47, 0
	v_mov_b32_e32 v43, 0
	v_mov_b32_e32 v39, 0
	v_mov_b32_e32 v35, 0
	v_mov_b32_e32 v48, 0
	v_mov_b32_e32 v44, 0
	v_mov_b32_e32 v40, 0
	v_mov_b32_e32 v36, 0
	v_mov_b32_e32 v49, 0
	v_mov_b32_e32 v45, 0
	v_mov_b32_e32 v41, 0
	v_mov_b32_e32 v37, 0
	ds_read_b128 v[182:185], v165 offset:0
	v_cmp_lt_i32_e32 vcc, -1, v151
	v_lshlrev_b32_e32 v148, 13, v151
	v_mov_b32_e32 v149, 0
	v_lshl_add_u64 v[148:149], v[148:149], 0, v[86:87]
	v_cndmask_b32_e32 v148, v168, v148, vcc
	v_cndmask_b32_e32 v149, v169, v149, vcc
	s_waitcnt lgkmcnt(0)
	global_store_dwordx4 v[148:149], v[182:185], off
	ds_read_b128 v[182:185], v165 offset:8192
	v_cmp_lt_i32_e32 vcc, -1, v166
	v_lshlrev_b32_e32 v148, 13, v166
	v_mov_b32_e32 v149, 0
	v_lshl_add_u64 v[148:149], v[148:149], 0, v[86:87]
	v_cndmask_b32_e32 v148, v168, v148, vcc
	v_cndmask_b32_e32 v149, v169, v149, vcc
	s_waitcnt lgkmcnt(0)
	global_store_dwordx4 v[148:149], v[182:185], off
	ds_read_b32 v150, v82 offset:768
	ds_read_b32 v151, v83 offset:768
	ds_read_b32 v166, v83 offset:896
	s_waitcnt lgkmcnt(2)
	v_mul_f32_e32 v18, v150, v18
	v_mul_f32_e32 v19, v150, v19
	v_mul_f32_e32 v20, v150, v20
	v_mul_f32_e32 v21, v150, v21
	v_mul_f32_e32 v22, v150, v22
	v_mul_f32_e32 v23, v150, v23
	v_mul_f32_e32 v24, v150, v24
	v_mul_f32_e32 v25, v150, v25
	v_cvt_pk_bf16_f32 v182, v18, v19
	v_cvt_pk_bf16_f32 v183, v20, v21
	v_cvt_pk_bf16_f32 v184, v22, v23
	v_cvt_pk_bf16_f32 v185, v24, v25
	ds_write_b128 v164, v[182:185]
	v_mul_f32_e32 v26, v150, v26
	v_mul_f32_e32 v27, v150, v27
	v_mul_f32_e32 v28, v150, v28
	v_mul_f32_e32 v29, v150, v29
	v_mul_f32_e32 v30, v150, v30
	v_mul_f32_e32 v31, v150, v31
	v_mul_f32_e32 v32, v150, v32
	v_mul_f32_e32 v33, v150, v33
	v_cvt_pk_bf16_f32 v182, v26, v27
	v_cvt_pk_bf16_f32 v183, v28, v29
	v_cvt_pk_bf16_f32 v184, v30, v31
	v_cvt_pk_bf16_f32 v185, v32, v33
	v_xor_b32_e32 v167, 64, v164
	ds_write_b128 v167, v[182:185]
	v_mov_b32_e32 v18, 0
	v_mov_b32_e32 v22, 0
	v_mov_b32_e32 v26, 0
	v_mov_b32_e32 v30, 0
	v_mov_b32_e32 v19, 0
	v_mov_b32_e32 v23, 0
	v_mov_b32_e32 v27, 0
	v_mov_b32_e32 v31, 0
	v_mov_b32_e32 v20, 0
	v_mov_b32_e32 v24, 0
	v_mov_b32_e32 v28, 0
	v_mov_b32_e32 v32, 0
	v_mov_b32_e32 v21, 0
	v_mov_b32_e32 v25, 0
	v_mov_b32_e32 v29, 0
	v_mov_b32_e32 v33, 0
	ds_read_b128 v[182:185], v165 offset:0
	v_cmp_lt_i32_e32 vcc, -1, v151
	v_lshlrev_b32_e32 v148, 13, v151
	v_mov_b32_e32 v149, 0
	v_lshl_add_u64 v[148:149], v[148:149], 0, v[86:87]
	v_cndmask_b32_e32 v148, v168, v148, vcc
	v_cndmask_b32_e32 v149, v169, v149, vcc
	s_waitcnt lgkmcnt(0)
	global_store_dwordx4 v[148:149], v[182:185], off
	ds_read_b128 v[182:185], v165 offset:8192
	v_cmp_lt_i32_e32 vcc, -1, v166
	v_lshlrev_b32_e32 v148, 13, v166
	v_mov_b32_e32 v149, 0
	v_lshl_add_u64 v[148:149], v[148:149], 0, v[86:87]
	v_cndmask_b32_e32 v148, v168, v148, vcc
	v_cndmask_b32_e32 v149, v169, v149, vcc
	s_waitcnt lgkmcnt(0)
	global_store_dwordx4 v[148:149], v[182:185], off
	ds_read_b32 v150, v82 offset:1024
	ds_read_b32 v151, v83 offset:1024
	ds_read_b32 v166, v83 offset:1152
	s_waitcnt lgkmcnt(2)
	v_mul_f32_e32 v2, v150, v2
	v_mul_f32_e32 v3, v150, v3
	v_mul_f32_e32 v4, v150, v4
	v_mul_f32_e32 v5, v150, v5
	v_mul_f32_e32 v6, v150, v6
	v_mul_f32_e32 v7, v150, v7
	v_mul_f32_e32 v8, v150, v8
	v_mul_f32_e32 v9, v150, v9
	v_cvt_pk_bf16_f32 v182, v2, v3
	v_cvt_pk_bf16_f32 v183, v4, v5
	v_cvt_pk_bf16_f32 v184, v6, v7
	v_cvt_pk_bf16_f32 v185, v8, v9
	ds_write_b128 v164, v[182:185]
	v_mul_f32_e32 v10, v150, v10
	v_mul_f32_e32 v11, v150, v11
	v_mul_f32_e32 v12, v150, v12
	v_mul_f32_e32 v13, v150, v13
	v_mul_f32_e32 v14, v150, v14
	v_mul_f32_e32 v15, v150, v15
	v_mul_f32_e32 v16, v150, v16
	v_mul_f32_e32 v17, v150, v17
	v_cvt_pk_bf16_f32 v182, v10, v11
	v_cvt_pk_bf16_f32 v183, v12, v13
	v_cvt_pk_bf16_f32 v184, v14, v15
	v_cvt_pk_bf16_f32 v185, v16, v17
	v_xor_b32_e32 v167, 64, v164
	ds_write_b128 v167, v[182:185]
	v_mov_b32_e32 v2, 0
	v_mov_b32_e32 v6, 0
	v_mov_b32_e32 v10, 0
	v_mov_b32_e32 v14, 0
	v_mov_b32_e32 v3, 0
	v_mov_b32_e32 v7, 0
	v_mov_b32_e32 v11, 0
	v_mov_b32_e32 v15, 0
	v_mov_b32_e32 v4, 0
	v_mov_b32_e32 v8, 0
	v_mov_b32_e32 v12, 0
	v_mov_b32_e32 v16, 0
	v_mov_b32_e32 v5, 0
	v_mov_b32_e32 v9, 0
	v_mov_b32_e32 v13, 0
	v_mov_b32_e32 v17, 0
	ds_read_b128 v[182:185], v165 offset:0
	v_cmp_lt_i32_e32 vcc, -1, v151
	v_lshlrev_b32_e32 v148, 13, v151
	v_mov_b32_e32 v149, 0
	v_lshl_add_u64 v[148:149], v[148:149], 0, v[86:87]
	v_cndmask_b32_e32 v148, v168, v148, vcc
	v_cndmask_b32_e32 v149, v169, v149, vcc
	s_waitcnt lgkmcnt(0)
	global_store_dwordx4 v[148:149], v[182:185], off
	ds_read_b128 v[182:185], v165 offset:8192
	v_cmp_lt_i32_e32 vcc, -1, v166
	v_lshlrev_b32_e32 v148, 13, v166
	v_mov_b32_e32 v149, 0
	v_lshl_add_u64 v[148:149], v[148:149], 0, v[86:87]
	v_cndmask_b32_e32 v148, v168, v148, vcc
	v_cndmask_b32_e32 v149, v169, v149, vcc
	s_waitcnt lgkmcnt(0)
; #define PG8_LAS __attribute__((address_space(3)))
; __device__ __forceinline__ unsigned cvtpk(float lo, float hi) { f32x2 v = {lo, hi}; bf16x2_t b = __builtin_convertvector(v, bf16x2_t); return __builtin_bit_cast(unsigned, b); }
; __device__ __forceinline__ void moe_down_stream(PG8_LAS unsigned char* lds, int e, int cb0, int slot0, int nv, const bf16_t* HIDp, const float* Wd, bf16_t* Y, const float* slot_w, const int* slot_dst) {
;     ...
;                 for (int p = 0; p < 2; ++p) { const f32x4 v0 = acc[m][2 * p] * w_, v1 = acc[m][2 * p + 1] * w_; u32x4 w; w.x = cvtpk(v0[0], v0[1]); w.y = cvtpk(v0[2], v0[3]); w.z = cvtpk(v1[0], v1[1]); w.w = cvtpk(v1[2], v1[3]);
;                     *(PG8_LAS u32x4*)(stg + fr * 128 + (((4 * p + fq) ^ (fr & 7)) * 16)) = w; }
; #pragma unroll
;                 for (int hh = 0; hh < 2; ++hh) { const int r = (lane >> 3) + 8 * hh, cc = lane & 7; const u32x4 d = *(const PG8_LAS u32x4*)(stg + r * 128 + ((cc ^ (r & 7)) * 16)); const int dst_ = ldst[4 * (16 * m + r) + wr];
;                     if (dst_ >= 0) *(u32x4*)(Y + (size_t)dst_ * D + 128 * cb + 64 * wc + 8 * cc) = d; }
; #pragma unroll
;                 for (int n = 0; n < 4; ++n) acc[m][n] = (f32x4){0.f, 0.f, 0.f, 0.f}; } }
	global_store_dwordx4 v[148:149], v[182:185], off
	v_add_co_u32_e32 v86, vcc, 0x400, v86
	s_nop 1
	v_addc_co_u32_e32 v87, vcc, 0, v87, vcc
	s_waitcnt lgkmcnt(0)
	s_add_i32 s49, s48, s74
	s_add_i32 s52, s52, 1
	s_and_b32 s54, s52, 7
	s_cmp_eq_u32 s54, 0
	s_cselect_b32 s54, s53, s32
	s_cselect_b32 s55, -1, 0
	s_add_u32 s30, s30, s54
	s_addc_u32 s31, s31, s55
	s_mov_b32 m0, s49
	s_nop 0
	global_load_lds_dwordx4 v88, s[30:31]
	s_add_i32 m0, s49, 0x2000
	s_nop 0
	global_load_lds_dwordx4 v90, s[30:31]
	s_add_i32 m0, s49, 0x4000
	s_nop 0
	global_load_lds_dwordx4 v92, s[30:31]
	s_add_i32 m0, s49, 0x6000
	s_nop 0
	global_load_lds_dwordx4 v94, s[30:31]
	s_add_i32 m0, s49, 0x8000
	s_nop 0
	global_load_lds_dwordx4 v96, s[30:31]
	v_cvt_pk_bf16_f32 v172, v114, v116
	v_cvt_pk_bf16_f32 v173, v118, v120
	v_cvt_pk_bf16_f32 v174, v122, v124
	v_cvt_pk_bf16_f32 v175, v126, v128
	v_cvt_pk_bf16_f32 v176, v115, v117
	v_cvt_pk_bf16_f32 v177, v119, v121
	v_cvt_pk_bf16_f32 v178, v123, v125
	v_cvt_pk_bf16_f32 v179, v127, v129
	ds_write_b128 v95, v[172:175] offset:19456
	ds_write_b128 v95, v[176:179] offset:19584
	v_add_u32_e32 v91, s46, v135
	v_add_u32_e32 v93, s46, v137
	ds_read_b128 v[238:241], v139 offset:0
	ds_read_b128 v[242:245], v139 offset:2048
	ds_read_b128 v[246:249], v139 offset:4096
	ds_read_b128 v[250:253], v139 offset:6144
	ds_read_b128 v[218:221], v91 offset:0
	ds_read_b128 v[222:225], v91 offset:2048
	ds_read_b128 v[226:229], v91 offset:4096
	ds_read_b128 v[230:233], v91 offset:6144
	ds_read_b128 v[234:237], v91 offset:8192
	s_waitcnt lgkmcnt(0)
	v_mfma_f32_16x16x32_bf16 v[78:81], v[238:241], v[218:221], v[78:81]
	v_mfma_f32_16x16x32_bf16 v[74:77], v[242:245], v[218:221], v[74:77]
	v_mfma_f32_16x16x32_bf16 v[70:73], v[246:249], v[218:221], v[70:73]
	v_mfma_f32_16x16x32_bf16 v[66:69], v[250:253], v[218:221], v[66:69]
	ds_read_b128 v[218:221], v93 offset:0
	ds_read_b128 v[142:145], v141 offset:0
	s_add_i32 s51, s51, 1
	s_and_b32 s54, s51, 7
	s_cmp_eq_u32 s54, 0
	s_cselect_b32 s44, s34, s35
	s_cselect_b32 s45, -1, 0
	v_lshl_add_u64 v[132:133], v[132:133], 0, s[44:45]
	global_load_dwordx2 v[114:115], v[132:133], off
	v_lshl_add_u64 v[180:181], v[132:133], 0, s[24:25]
	global_load_dwordx2 v[116:117], v[180:181], off
	v_mfma_f32_16x16x32_bf16 v[62:65], v[238:241], v[222:225], v[62:65]
	v_mfma_f32_16x16x32_bf16 v[58:61], v[242:245], v[222:225], v[58:61]
	v_mfma_f32_16x16x32_bf16 v[54:57], v[246:249], v[222:225], v[54:57]
	v_mfma_f32_16x16x32_bf16 v[50:53], v[250:253], v[222:225], v[50:53]
	ds_read_b128 v[222:225], v93 offset:2048
	ds_read_b128 v[146:149], v141 offset:2048
	v_lshl_add_u64 v[180:181], v[132:133], 0, s[26:27]
	global_load_dwordx2 v[118:119], v[180:181], off
	v_lshl_add_u64 v[180:181], v[132:133], 0, s[28:29]
	global_load_dwordx2 v[120:121], v[180:181], off
	v_mfma_f32_16x16x32_bf16 v[46:49], v[238:241], v[226:229], v[46:49]
	v_mfma_f32_16x16x32_bf16 v[42:45], v[242:245], v[226:229], v[42:45]
	v_mfma_f32_16x16x32_bf16 v[38:41], v[246:249], v[226:229], v[38:41]
	v_mfma_f32_16x16x32_bf16 v[34:37], v[250:253], v[226:229], v[34:37]
	ds_read_b128 v[226:229], v93 offset:4096
	ds_read_b128 v[156:159], v141 offset:4096
	v_lshl_add_u64 v[180:181], v[132:133], 0, s[36:37]
	global_load_dwordx2 v[122:123], v[180:181], off
	v_lshl_add_u64 v[180:181], v[132:133], 0, s[38:39]
	global_load_dwordx2 v[124:125], v[180:181], off
	v_mfma_f32_16x16x32_bf16 v[18:21], v[238:241], v[230:233], v[18:21]
	v_mfma_f32_16x16x32_bf16 v[22:25], v[242:245], v[230:233], v[22:25]
	v_mfma_f32_16x16x32_bf16 v[26:29], v[246:249], v[230:233], v[26:29]
	v_mfma_f32_16x16x32_bf16 v[30:33], v[250:253], v[230:233], v[30:33]
	ds_read_b128 v[230:233], v93 offset:6144
	ds_read_b128 v[160:163], v141 offset:6144
	v_lshl_add_u64 v[180:181], v[132:133], 0, s[40:41]
	global_load_dwordx2 v[126:127], v[180:181], off
	v_lshl_add_u64 v[180:181], v[132:133], 0, s[42:43]
	global_load_dwordx2 v[128:129], v[180:181], off
	v_mfma_f32_16x16x32_bf16 v[2:5], v[238:241], v[234:237], v[2:5]
	v_mfma_f32_16x16x32_bf16 v[6:9], v[242:245], v[234:237], v[6:9]
	v_mfma_f32_16x16x32_bf16 v[10:13], v[246:249], v[234:237], v[10:13]
	v_mfma_f32_16x16x32_bf16 v[14:17], v[250:253], v[234:237], v[14:17]
	ds_read_b128 v[234:237], v93 offset:8192
	s_waitcnt vmcnt(31)
	s_mov_b32 s49, s46
	s_mov_b32 s46, s47
	s_mov_b32 s47, s48
	s_mov_b32 s48, s49
	s_add_i32 s50, s50, 1
	s_waitcnt lgkmcnt(0)
	s_barrier
; #define MD_GLDS_A(buf, tau) do { _Pragma("unroll") for (int i = 0; i < 5; ++i) if (amask & (1u << i)) \
;         __builtin_amdgcn_global_load_lds((const unsigned*)((const char*)HIDp + aoff[i] + (size_t)((tau) & 7) * 128), (PG8_LAS unsigned*)(MD_SA(buf) + wid * 1024 + i * 8192), 16, 0, 0); } while (0)
; #define MD_B_ISSUE(sb, tau) do { const char* kb_ = Bb + (size_t)((tau) >> 3) * 512 + (size_t)((tau) & 7) * (64 * (size_t)RB); _Pragma("unroll") for (int j = 0; j < 8; ++j) { const char* p_ = kb_ + (size_t)j * RB; \
;         asm volatile("global_load_dwordx2 %0, %1, off" : "=&v"(sb[j]) : "v"(p_) : "memory"); } } while (0)
; #define MD_B_WAIT(sb, N) asm volatile("s_waitcnt vmcnt(%8)" : "+v"(sb[0]), "+v"(sb[1]), "+v"(sb[2]), "+v"(sb[3]), "+v"(sb[4]), "+v"(sb[5]), "+v"(sb[6]), "+v"(sb[7]) : "n"(N) : "memory")
; #define MD_END(last) do { if (last) asm volatile("s_waitcnt vmcnt(0)" ::: "memory"); else asm volatile("s_waitcnt vmcnt(8)" ::: "memory"); \
;         asm volatile("s_waitcnt lgkmcnt(0)" ::: "memory"); __builtin_amdgcn_s_barrier(); asm volatile("" ::: "memory"); } while (0)
; __device__ __forceinline__ void moe_down_stream(PG8_LAS unsigned char* lds, int e, int cb0, int slot0, int nv, const bf16_t* HIDp, const float* Wd, bf16_t* Y, const float* slot_w, const int* slot_dst) {
;     ...
;     for (int t = 0; t < NT; t += 2) {
;         if (t + 2 < NT) MD_B_WAIT(s1, 8); else MD_B_WAIT(s1, 0);
;         MD_B_WRITE(s1, 1); __builtin_amdgcn_sched_barrier(0); MD_GLDS_A(1, t + 1); __builtin_amdgcn_sched_barrier(0);
;         if (t + 3 < NT) MD_B_ISSUE(s1, t + 3);
;         MD_COMPUTE(0);
;         MD_END(t + 3 >= NT);
;         if (t + 2 < NT) { MD_B_WAIT(s0, 8); MD_B_WRITE(s0, 0); __builtin_amdgcn_sched_barrier(0); MD_GLDS_A(0, t + 2); __builtin_amdgcn_sched_barrier(0); }
;         if (t + 4 < NT) MD_B_ISSUE(s0, t + 4);
;         MD_COMPUTE(1);
;         MD_END(t + 4 >= NT);
	s_add_i32 s49, s48, s74
	s_add_i32 s52, s52, 1
	s_and_b32 s54, s52, 7
	s_cmp_eq_u32 s54, 0
	s_cselect_b32 s54, s53, s32
	s_cselect_b32 s55, -1, 0
	s_add_u32 s30, s30, s54
	s_addc_u32 s31, s31, s55
	v_mfma_f32_16x16x32_bf16 v[78:81], v[142:145], v[218:221], v[78:81]
	v_mfma_f32_16x16x32_bf16 v[74:77], v[146:149], v[218:221], v[74:77]
	v_mfma_f32_16x16x32_bf16 v[70:73], v[156:159], v[218:221], v[70:73]
	v_mfma_f32_16x16x32_bf16 v[66:69], v[160:163], v[218:221], v[66:69]
	s_mov_b32 m0, s49
	s_nop 0
	global_load_lds_dwordx4 v88, s[30:31]
	v_mfma_f32_16x16x32_bf16 v[62:65], v[142:145], v[222:225], v[62:65]
	v_mfma_f32_16x16x32_bf16 v[58:61], v[146:149], v[222:225], v[58:61]
	v_mfma_f32_16x16x32_bf16 v[54:57], v[156:159], v[222:225], v[54:57]
	v_mfma_f32_16x16x32_bf16 v[50:53], v[160:163], v[222:225], v[50:53]
	s_add_i32 m0, s49, 0x2000
	s_nop 0
	global_load_lds_dwordx4 v90, s[30:31]
	v_mfma_f32_16x16x32_bf16 v[46:49], v[142:145], v[226:229], v[46:49]
	v_mfma_f32_16x16x32_bf16 v[42:45], v[146:149], v[226:229], v[42:45]
	v_mfma_f32_16x16x32_bf16 v[38:41], v[156:159], v[226:229], v[38:41]
	v_mfma_f32_16x16x32_bf16 v[34:37], v[160:163], v[226:229], v[34:37]
	s_add_i32 m0, s49, 0x4000
	s_nop 0
	global_load_lds_dwordx4 v92, s[30:31]
	v_mfma_f32_16x16x32_bf16 v[18:21], v[142:145], v[230:233], v[18:21]
	v_mfma_f32_16x16x32_bf16 v[22:25], v[146:149], v[230:233], v[22:25]
	v_mfma_f32_16x16x32_bf16 v[26:29], v[156:159], v[230:233], v[26:29]
	v_mfma_f32_16x16x32_bf16 v[30:33], v[160:163], v[230:233], v[30:33]
	s_add_i32 m0, s49, 0x6000
	s_nop 0
	global_load_lds_dwordx4 v94, s[30:31]
	v_mfma_f32_16x16x32_bf16 v[2:5], v[142:145], v[234:237], v[2:5]
	v_mfma_f32_16x16x32_bf16 v[6:9], v[146:149], v[234:237], v[6:9]
	v_mfma_f32_16x16x32_bf16 v[10:13], v[156:159], v[234:237], v[10:13]
	v_mfma_f32_16x16x32_bf16 v[14:17], v[160:163], v[234:237], v[14:17]
	s_add_i32 m0, s49, 0x8000
	s_nop 0
	global_load_lds_dwordx4 v96, s[30:31]
	v_cvt_pk_bf16_f32 v172, v186, v188
	v_cvt_pk_bf16_f32 v173, v190, v192
	v_cvt_pk_bf16_f32 v174, v194, v196
	v_cvt_pk_bf16_f32 v175, v198, v200
	v_cvt_pk_bf16_f32 v176, v187, v189
	v_cvt_pk_bf16_f32 v177, v191, v193
	v_cvt_pk_bf16_f32 v178, v195, v197
	v_cvt_pk_bf16_f32 v179, v199, v201
	ds_write_b128 v95, v[172:175] offset:0
	ds_write_b128 v95, v[176:179] offset:128
	v_add_u32_e32 v91, s46, v135
	v_add_u32_e32 v93, s46, v137
	ds_read_b128 v[238:241], v139 offset:19456
	ds_read_b128 v[242:245], v139 offset:21504
	ds_read_b128 v[246:249], v139 offset:23552
	ds_read_b128 v[250:253], v139 offset:25600
	ds_read_b128 v[218:221], v91 offset:0
	ds_read_b128 v[222:225], v91 offset:2048
	ds_read_b128 v[226:229], v91 offset:4096
	ds_read_b128 v[230:233], v91 offset:6144
	ds_read_b128 v[234:237], v91 offset:8192
	s_waitcnt lgkmcnt(0)
	v_mfma_f32_16x16x32_bf16 v[78:81], v[238:241], v[218:221], v[78:81]
	v_mfma_f32_16x16x32_bf16 v[74:77], v[242:245], v[218:221], v[74:77]
	v_mfma_f32_16x16x32_bf16 v[70:73], v[246:249], v[218:221], v[70:73]
	v_mfma_f32_16x16x32_bf16 v[66:69], v[250:253], v[218:221], v[66:69]
	ds_read_b128 v[218:221], v93 offset:0
	ds_read_b128 v[142:145], v141 offset:19456
	s_add_i32 s51, s51, 1
	s_and_b32 s54, s51, 7
	s_cmp_eq_u32 s54, 0
	s_cselect_b32 s44, s34, s35
	s_cselect_b32 s45, -1, 0
	v_lshl_add_u64 v[132:133], v[132:133], 0, s[44:45]
	global_load_dwordx2 v[186:187], v[132:133], off
	v_lshl_add_u64 v[180:181], v[132:133], 0, s[24:25]
	global_load_dwordx2 v[188:189], v[180:181], off
	v_mfma_f32_16x16x32_bf16 v[62:65], v[238:241], v[222:225], v[62:65]
	v_mfma_f32_16x16x32_bf16 v[58:61], v[242:245], v[222:225], v[58:61]
	v_mfma_f32_16x16x32_bf16 v[54:57], v[246:249], v[222:225], v[54:57]
	v_mfma_f32_16x16x32_bf16 v[50:53], v[250:253], v[222:225], v[50:53]
	ds_read_b128 v[222:225], v93 offset:2048
	ds_read_b128 v[146:149], v141 offset:21504
	v_lshl_add_u64 v[180:181], v[132:133], 0, s[26:27]
	global_load_dwordx2 v[190:191], v[180:181], off
	v_lshl_add_u64 v[180:181], v[132:133], 0, s[28:29]
	global_load_dwordx2 v[192:193], v[180:181], off
	v_mfma_f32_16x16x32_bf16 v[46:49], v[238:241], v[226:229], v[46:49]
	v_mfma_f32_16x16x32_bf16 v[42:45], v[242:245], v[226:229], v[42:45]
	v_mfma_f32_16x16x32_bf16 v[38:41], v[246:249], v[226:229], v[38:41]
	v_mfma_f32_16x16x32_bf16 v[34:37], v[250:253], v[226:229], v[34:37]
	ds_read_b128 v[226:229], v93 offset:4096
	ds_read_b128 v[156:159], v141 offset:23552
	v_lshl_add_u64 v[180:181], v[132:133], 0, s[36:37]
	global_load_dwordx2 v[194:195], v[180:181], off
	v_lshl_add_u64 v[180:181], v[132:133], 0, s[38:39]
	global_load_dwordx2 v[196:197], v[180:181], off
	v_mfma_f32_16x16x32_bf16 v[18:21], v[238:241], v[230:233], v[18:21]
	v_mfma_f32_16x16x32_bf16 v[22:25], v[242:245], v[230:233], v[22:25]
	v_mfma_f32_16x16x32_bf16 v[26:29], v[246:249], v[230:233], v[26:29]
	v_mfma_f32_16x16x32_bf16 v[30:33], v[250:253], v[230:233], v[30:33]
	ds_read_b128 v[230:233], v93 offset:6144
	ds_read_b128 v[160:163], v141 offset:25600
	v_lshl_add_u64 v[180:181], v[132:133], 0, s[40:41]
	global_load_dwordx2 v[198:199], v[180:181], off
	v_lshl_add_u64 v[180:181], v[132:133], 0, s[42:43]
	global_load_dwordx2 v[200:201], v[180:181], off
	v_mfma_f32_16x16x32_bf16 v[2:5], v[238:241], v[234:237], v[2:5]
	v_mfma_f32_16x16x32_bf16 v[6:9], v[242:245], v[234:237], v[6:9]
	v_mfma_f32_16x16x32_bf16 v[10:13], v[246:249], v[234:237], v[10:13]
	v_mfma_f32_16x16x32_bf16 v[14:17], v[250:253], v[234:237], v[14:17]
	ds_read_b128 v[234:237], v93 offset:8192
	s_waitcnt vmcnt(21)
	s_mov_b32 s49, s46
	s_mov_b32 s46, s47
	s_mov_b32 s47, s48
	s_mov_b32 s48, s49
	s_add_i32 s50, s50, 1
	s_waitcnt lgkmcnt(0)
	s_barrier
; #define MD_GLDS_A(buf, tau) do { _Pragma("unroll") for (int i = 0; i < 5; ++i) if (amask & (1u << i)) \
;         __builtin_amdgcn_global_load_lds((const unsigned*)((const char*)HIDp + aoff[i] + (size_t)((tau) & 7) * 128), (PG8_LAS unsigned*)(MD_SA(buf) + wid * 1024 + i * 8192), 16, 0, 0); } while (0)
; #define MD_B_ISSUE(sb, tau) do { const char* kb_ = Bb + (size_t)((tau) >> 3) * 512 + (size_t)((tau) & 7) * (64 * (size_t)RB); _Pragma("unroll") for (int j = 0; j < 8; ++j) { const char* p_ = kb_ + (size_t)j * RB; \
;         asm volatile("global_load_dwordx2 %0, %1, off" : "=&v"(sb[j]) : "v"(p_) : "memory"); } } while (0)
; #define MD_B_WAIT(sb, N) asm volatile("s_waitcnt vmcnt(%8)" : "+v"(sb[0]), "+v"(sb[1]), "+v"(sb[2]), "+v"(sb[3]), "+v"(sb[4]), "+v"(sb[5]), "+v"(sb[6]), "+v"(sb[7]) : "n"(N) : "memory")
; #define MD_END(last) do { if (last) asm volatile("s_waitcnt vmcnt(0)" ::: "memory"); else asm volatile("s_waitcnt vmcnt(8)" ::: "memory"); \
;         asm volatile("s_waitcnt lgkmcnt(0)" ::: "memory"); __builtin_amdgcn_s_barrier(); asm volatile("" ::: "memory"); } while (0)
; __device__ __forceinline__ void moe_down_stream(PG8_LAS unsigned char* lds, int e, int cb0, int slot0, int nv, const bf16_t* HIDp, const float* Wd, bf16_t* Y, const float* slot_w, const int* slot_dst) {
;     ...
;     for (int t = 0; t < NT; t += 2) {
;         if (t + 2 < NT) MD_B_WAIT(s1, 8); else MD_B_WAIT(s1, 0);
;         MD_B_WRITE(s1, 1); __builtin_amdgcn_sched_barrier(0); MD_GLDS_A(1, t + 1); __builtin_amdgcn_sched_barrier(0);
;         if (t + 3 < NT) MD_B_ISSUE(s1, t + 3);
;         MD_COMPUTE(0);
;         MD_END(t + 3 >= NT);
;         if (t + 2 < NT) { MD_B_WAIT(s0, 8); MD_B_WRITE(s0, 0); __builtin_amdgcn_sched_barrier(0); MD_GLDS_A(0, t + 2); __builtin_amdgcn_sched_barrier(0); }
;         if (t + 4 < NT) MD_B_ISSUE(s0, t + 4);
;         MD_COMPUTE(1);
;         MD_END(t + 4 >= NT);
	s_add_i32 s49, s48, s74
	s_add_i32 s52, s52, 1
	s_and_b32 s54, s52, 7
	s_cmp_eq_u32 s54, 0
	s_cselect_b32 s54, s53, s32
	s_cselect_b32 s55, -1, 0
	s_add_u32 s30, s30, s54
	s_addc_u32 s31, s31, s55
	v_mfma_f32_16x16x32_bf16 v[78:81], v[142:145], v[218:221], v[78:81]
	v_mfma_f32_16x16x32_bf16 v[74:77], v[146:149], v[218:221], v[74:77]
	v_mfma_f32_16x16x32_bf16 v[70:73], v[156:159], v[218:221], v[70:73]
	v_mfma_f32_16x16x32_bf16 v[66:69], v[160:163], v[218:221], v[66:69]
	s_mov_b32 m0, s49
	s_nop 0
	global_load_lds_dwordx4 v88, s[30:31]
	v_mfma_f32_16x16x32_bf16 v[62:65], v[142:145], v[222:225], v[62:65]
	v_mfma_f32_16x16x32_bf16 v[58:61], v[146:149], v[222:225], v[58:61]
	v_mfma_f32_16x16x32_bf16 v[54:57], v[156:159], v[222:225], v[54:57]
	v_mfma_f32_16x16x32_bf16 v[50:53], v[160:163], v[222:225], v[50:53]
	s_add_i32 m0, s49, 0x2000
	s_nop 0
	global_load_lds_dwordx4 v90, s[30:31]
	v_mfma_f32_16x16x32_bf16 v[46:49], v[142:145], v[226:229], v[46:49]
	v_mfma_f32_16x16x32_bf16 v[42:45], v[146:149], v[226:229], v[42:45]
	v_mfma_f32_16x16x32_bf16 v[38:41], v[156:159], v[226:229], v[38:41]
	v_mfma_f32_16x16x32_bf16 v[34:37], v[160:163], v[226:229], v[34:37]
	s_add_i32 m0, s49, 0x4000
	s_nop 0
	global_load_lds_dwordx4 v92, s[30:31]
	v_mfma_f32_16x16x32_bf16 v[18:21], v[142:145], v[230:233], v[18:21]
	v_mfma_f32_16x16x32_bf16 v[22:25], v[146:149], v[230:233], v[22:25]
	v_mfma_f32_16x16x32_bf16 v[26:29], v[156:159], v[230:233], v[26:29]
	v_mfma_f32_16x16x32_bf16 v[30:33], v[160:163], v[230:233], v[30:33]
	s_add_i32 m0, s49, 0x6000
	s_nop 0
	global_load_lds_dwordx4 v94, s[30:31]
	v_mfma_f32_16x16x32_bf16 v[2:5], v[142:145], v[234:237], v[2:5]
	v_mfma_f32_16x16x32_bf16 v[6:9], v[146:149], v[234:237], v[6:9]
	v_mfma_f32_16x16x32_bf16 v[10:13], v[156:159], v[234:237], v[10:13]
	v_mfma_f32_16x16x32_bf16 v[14:17], v[160:163], v[234:237], v[14:17]
	s_add_i32 m0, s49, 0x8000
	s_nop 0
	global_load_lds_dwordx4 v96, s[30:31]
	v_cvt_pk_bf16_f32 v172, v202, v204
	v_cvt_pk_bf16_f32 v173, v206, v208
	v_cvt_pk_bf16_f32 v174, v210, v212
	v_cvt_pk_bf16_f32 v175, v214, v216
	v_cvt_pk_bf16_f32 v176, v203, v205
	v_cvt_pk_bf16_f32 v177, v207, v209
	v_cvt_pk_bf16_f32 v178, v211, v213
	v_cvt_pk_bf16_f32 v179, v215, v217
	ds_write_b128 v95, v[172:175] offset:19456
	ds_write_b128 v95, v[176:179] offset:19584
	v_add_u32_e32 v91, s46, v135
	v_add_u32_e32 v93, s46, v137
	ds_read_b128 v[238:241], v139 offset:0
	ds_read_b128 v[242:245], v139 offset:2048
	ds_read_b128 v[246:249], v139 offset:4096
	ds_read_b128 v[250:253], v139 offset:6144
	ds_read_b128 v[218:221], v91 offset:0
	ds_read_b128 v[222:225], v91 offset:2048
	ds_read_b128 v[226:229], v91 offset:4096
	ds_read_b128 v[230:233], v91 offset:6144
	ds_read_b128 v[234:237], v91 offset:8192
	s_waitcnt lgkmcnt(0)
	v_mfma_f32_16x16x32_bf16 v[78:81], v[238:241], v[218:221], v[78:81]
	v_mfma_f32_16x16x32_bf16 v[74:77], v[242:245], v[218:221], v[74:77]
	v_mfma_f32_16x16x32_bf16 v[70:73], v[246:249], v[218:221], v[70:73]
	v_mfma_f32_16x16x32_bf16 v[66:69], v[250:253], v[218:221], v[66:69]
	ds_read_b128 v[218:221], v93 offset:0
	ds_read_b128 v[142:145], v141 offset:0
	s_add_i32 s51, s51, 1
	s_and_b32 s54, s51, 7
	s_cmp_eq_u32 s54, 0
	s_cselect_b32 s44, s34, s35
	s_cselect_b32 s45, -1, 0
	v_lshl_add_u64 v[132:133], v[132:133], 0, s[44:45]
	global_load_dwordx2 v[202:203], v[132:133], off
	v_lshl_add_u64 v[180:181], v[132:133], 0, s[24:25]
	global_load_dwordx2 v[204:205], v[180:181], off
	v_mfma_f32_16x16x32_bf16 v[62:65], v[238:241], v[222:225], v[62:65]
	v_mfma_f32_16x16x32_bf16 v[58:61], v[242:245], v[222:225], v[58:61]
	v_mfma_f32_16x16x32_bf16 v[54:57], v[246:249], v[222:225], v[54:57]
	v_mfma_f32_16x16x32_bf16 v[50:53], v[250:253], v[222:225], v[50:53]
	ds_read_b128 v[222:225], v93 offset:2048
	ds_read_b128 v[146:149], v141 offset:2048
	v_lshl_add_u64 v[180:181], v[132:133], 0, s[26:27]
	global_load_dwordx2 v[206:207], v[180:181], off
	v_lshl_add_u64 v[180:181], v[132:133], 0, s[28:29]
	global_load_dwordx2 v[208:209], v[180:181], off
	v_mfma_f32_16x16x32_bf16 v[46:49], v[238:241], v[226:229], v[46:49]
	v_mfma_f32_16x16x32_bf16 v[42:45], v[242:245], v[226:229], v[42:45]
	v_mfma_f32_16x16x32_bf16 v[38:41], v[246:249], v[226:229], v[38:41]
	v_mfma_f32_16x16x32_bf16 v[34:37], v[250:253], v[226:229], v[34:37]
	ds_read_b128 v[226:229], v93 offset:4096
	ds_read_b128 v[156:159], v141 offset:4096
	v_lshl_add_u64 v[180:181], v[132:133], 0, s[36:37]
	global_load_dwordx2 v[210:211], v[180:181], off
	v_lshl_add_u64 v[180:181], v[132:133], 0, s[38:39]
	global_load_dwordx2 v[212:213], v[180:181], off
	v_mfma_f32_16x16x32_bf16 v[18:21], v[238:241], v[230:233], v[18:21]
	v_mfma_f32_16x16x32_bf16 v[22:25], v[242:245], v[230:233], v[22:25]
	v_mfma_f32_16x16x32_bf16 v[26:29], v[246:249], v[230:233], v[26:29]
	v_mfma_f32_16x16x32_bf16 v[30:33], v[250:253], v[230:233], v[30:33]
	ds_read_b128 v[230:233], v93 offset:6144
	ds_read_b128 v[160:163], v141 offset:6144
	v_lshl_add_u64 v[180:181], v[132:133], 0, s[40:41]
	global_load_dwordx2 v[214:215], v[180:181], off
	v_lshl_add_u64 v[180:181], v[132:133], 0, s[42:43]
	global_load_dwordx2 v[216:217], v[180:181], off
	v_mfma_f32_16x16x32_bf16 v[2:5], v[238:241], v[234:237], v[2:5]
	v_mfma_f32_16x16x32_bf16 v[6:9], v[242:245], v[234:237], v[6:9]
	v_mfma_f32_16x16x32_bf16 v[10:13], v[246:249], v[234:237], v[10:13]
	v_mfma_f32_16x16x32_bf16 v[14:17], v[250:253], v[234:237], v[14:17]
	ds_read_b128 v[234:237], v93 offset:8192
	s_waitcnt vmcnt(21)
	s_mov_b32 s49, s46
	s_mov_b32 s46, s47
	s_mov_b32 s47, s48
	s_mov_b32 s48, s49
	s_add_i32 s50, s50, 1
	s_waitcnt lgkmcnt(0)
	s_barrier
; #define MD_GLDS_A(buf, tau) do { _Pragma("unroll") for (int i = 0; i < 5; ++i) if (amask & (1u << i)) \
;         __builtin_amdgcn_global_load_lds((const unsigned*)((const char*)HIDp + aoff[i] + (size_t)((tau) & 7) * 128), (PG8_LAS unsigned*)(MD_SA(buf) + wid * 1024 + i * 8192), 16, 0, 0); } while (0)
; #define MD_B_ISSUE(sb, tau) do { const char* kb_ = Bb + (size_t)((tau) >> 3) * 512 + (size_t)((tau) & 7) * (64 * (size_t)RB); _Pragma("unroll") for (int j = 0; j < 8; ++j) { const char* p_ = kb_ + (size_t)j * RB; \
;         asm volatile("global_load_dwordx2 %0, %1, off" : "=&v"(sb[j]) : "v"(p_) : "memory"); } } while (0)
; #define MD_B_WAIT(sb, N) asm volatile("s_waitcnt vmcnt(%8)" : "+v"(sb[0]), "+v"(sb[1]), "+v"(sb[2]), "+v"(sb[3]), "+v"(sb[4]), "+v"(sb[5]), "+v"(sb[6]), "+v"(sb[7]) : "n"(N) : "memory")
; __device__ __forceinline__ void moe_down_stream(PG8_LAS unsigned char* lds, int e, int cb0, int slot0, int nv, const bf16_t* HIDp, const float* Wd, bf16_t* Y, const float* slot_w, const int* slot_dst) {
;     ...
;     f32x4 acc[DNM][4];
; #pragma unroll
;     for (int m = 0; m < DNM; ++m)
; #pragma unroll
;         for (int n = 0; n < 4; ++n) acc[m][n] = (f32x4){0.f, 0.f, 0.f, 0.f};
;     f32x2 s0[8], s1[8];
;     MD_GLDS_A(0, 0); MD_B_ISSUE(s0, 0); MD_B_ISSUE(s1, 1);
;     MD_B_WAIT(s0, 8); MD_B_WRITE(s0, 0); __builtin_amdgcn_sched_barrier(0); MD_B_ISSUE(s0, 2);
;     asm volatile("s_waitcnt vmcnt(16)" ::: "memory");
;     asm volatile("s_waitcnt lgkmcnt(0)" ::: "memory"); __builtin_amdgcn_s_barrier(); asm volatile("" ::: "memory");
; #pragma unroll 1
;     for (int t = 0; t < NT; t += 2) {
;         if (t + 2 < NT) MD_B_WAIT(s1, 8); else MD_B_WAIT(s1, 0);
;         MD_B_WRITE(s1, 1); __builtin_amdgcn_sched_barrier(0); MD_GLDS_A(1, t + 1); __builtin_amdgcn_sched_barrier(0);
;         if (t + 3 < NT) MD_B_ISSUE(s1, t + 3);
;         MD_COMPUTE(0);
;         MD_END(t + 3 >= NT);
;         if (t + 2 < NT) { MD_B_WAIT(s0, 8); MD_B_WRITE(s0, 0); __builtin_amdgcn_sched_barrier(0); MD_GLDS_A(0, t + 2); __builtin_amdgcn_sched_barrier(0); }
;         if (t + 4 < NT) MD_B_ISSUE(s0, t + 4);
;         MD_COMPUTE(1);
;         MD_END(t + 4 >= NT);
	s_add_i32 s49, s48, s74
	s_add_i32 s52, s52, 1
	s_and_b32 s54, s52, 7
	s_cmp_eq_u32 s54, 0
	s_cselect_b32 s54, s53, s32
	s_cselect_b32 s55, -1, 0
	s_add_u32 s30, s30, s54
	s_addc_u32 s31, s31, s55
	v_mfma_f32_16x16x32_bf16 v[78:81], v[142:145], v[218:221], v[78:81]
	v_mfma_f32_16x16x32_bf16 v[74:77], v[146:149], v[218:221], v[74:77]
	v_mfma_f32_16x16x32_bf16 v[70:73], v[156:159], v[218:221], v[70:73]
	v_mfma_f32_16x16x32_bf16 v[66:69], v[160:163], v[218:221], v[66:69]
	s_mov_b32 m0, s49
	s_nop 0
	global_load_lds_dwordx4 v88, s[30:31]
	v_mfma_f32_16x16x32_bf16 v[62:65], v[142:145], v[222:225], v[62:65]
	v_mfma_f32_16x16x32_bf16 v[58:61], v[146:149], v[222:225], v[58:61]
	v_mfma_f32_16x16x32_bf16 v[54:57], v[156:159], v[222:225], v[54:57]
	v_mfma_f32_16x16x32_bf16 v[50:53], v[160:163], v[222:225], v[50:53]
	s_add_i32 m0, s49, 0x2000
	s_nop 0
	global_load_lds_dwordx4 v90, s[30:31]
	v_mfma_f32_16x16x32_bf16 v[46:49], v[142:145], v[226:229], v[46:49]
	v_mfma_f32_16x16x32_bf16 v[42:45], v[146:149], v[226:229], v[42:45]
	v_mfma_f32_16x16x32_bf16 v[38:41], v[156:159], v[226:229], v[38:41]
	v_mfma_f32_16x16x32_bf16 v[34:37], v[160:163], v[226:229], v[34:37]
	s_add_i32 m0, s49, 0x4000
	s_nop 0
	global_load_lds_dwordx4 v92, s[30:31]
	v_mfma_f32_16x16x32_bf16 v[18:21], v[142:145], v[230:233], v[18:21]
	v_mfma_f32_16x16x32_bf16 v[22:25], v[146:149], v[230:233], v[22:25]
	v_mfma_f32_16x16x32_bf16 v[26:29], v[156:159], v[230:233], v[26:29]
	v_mfma_f32_16x16x32_bf16 v[30:33], v[160:163], v[230:233], v[30:33]
	s_add_i32 m0, s49, 0x6000
	s_nop 0
	global_load_lds_dwordx4 v94, s[30:31]
	v_mfma_f32_16x16x32_bf16 v[2:5], v[142:145], v[234:237], v[2:5]
	v_mfma_f32_16x16x32_bf16 v[6:9], v[146:149], v[234:237], v[6:9]
	v_mfma_f32_16x16x32_bf16 v[10:13], v[156:159], v[234:237], v[10:13]
	v_mfma_f32_16x16x32_bf16 v[14:17], v[160:163], v[234:237], v[14:17]
	s_add_i32 m0, s49, 0x8000
	s_nop 0
	global_load_lds_dwordx4 v96, s[30:31]
	v_cvt_pk_bf16_f32 v172, v98, v100
	v_cvt_pk_bf16_f32 v173, v102, v104
	v_cvt_pk_bf16_f32 v174, v106, v108
	v_cvt_pk_bf16_f32 v175, v110, v112
	v_cvt_pk_bf16_f32 v176, v99, v101
	v_cvt_pk_bf16_f32 v177, v103, v105
	v_cvt_pk_bf16_f32 v178, v107, v109
	v_cvt_pk_bf16_f32 v179, v111, v113
	ds_write_b128 v95, v[172:175] offset:0
	ds_write_b128 v95, v[176:179] offset:128
	v_add_u32_e32 v91, s46, v135
	v_add_u32_e32 v93, s46, v137
	ds_read_b128 v[238:241], v139 offset:19456
	ds_read_b128 v[242:245], v139 offset:21504
	ds_read_b128 v[246:249], v139 offset:23552
	ds_read_b128 v[250:253], v139 offset:25600
	ds_read_b128 v[218:221], v91 offset:0
	ds_read_b128 v[222:225], v91 offset:2048
	ds_read_b128 v[226:229], v91 offset:4096
	ds_read_b128 v[230:233], v91 offset:6144
	ds_read_b128 v[234:237], v91 offset:8192
	s_waitcnt lgkmcnt(0)
	v_mfma_f32_16x16x32_bf16 v[78:81], v[238:241], v[218:221], v[78:81]
	v_mfma_f32_16x16x32_bf16 v[74:77], v[242:245], v[218:221], v[74:77]
	v_mfma_f32_16x16x32_bf16 v[70:73], v[246:249], v[218:221], v[70:73]
	v_mfma_f32_16x16x32_bf16 v[66:69], v[250:253], v[218:221], v[66:69]
	ds_read_b128 v[218:221], v93 offset:0
	ds_read_b128 v[142:145], v141 offset:19456
	v_mfma_f32_16x16x32_bf16 v[62:65], v[238:241], v[222:225], v[62:65]
	v_mfma_f32_16x16x32_bf16 v[58:61], v[242:245], v[222:225], v[58:61]
	v_mfma_f32_16x16x32_bf16 v[54:57], v[246:249], v[222:225], v[54:57]
	v_mfma_f32_16x16x32_bf16 v[50:53], v[250:253], v[222:225], v[50:53]
	ds_read_b128 v[222:225], v93 offset:2048
	ds_read_b128 v[146:149], v141 offset:21504
	v_mfma_f32_16x16x32_bf16 v[46:49], v[238:241], v[226:229], v[46:49]
	v_mfma_f32_16x16x32_bf16 v[42:45], v[242:245], v[226:229], v[42:45]
	v_mfma_f32_16x16x32_bf16 v[38:41], v[246:249], v[226:229], v[38:41]
	v_mfma_f32_16x16x32_bf16 v[34:37], v[250:253], v[226:229], v[34:37]
	ds_read_b128 v[226:229], v93 offset:4096
	ds_read_b128 v[156:159], v141 offset:23552
	v_mfma_f32_16x16x32_bf16 v[18:21], v[238:241], v[230:233], v[18:21]
	v_mfma_f32_16x16x32_bf16 v[22:25], v[242:245], v[230:233], v[22:25]
	v_mfma_f32_16x16x32_bf16 v[26:29], v[246:249], v[230:233], v[26:29]
	v_mfma_f32_16x16x32_bf16 v[30:33], v[250:253], v[230:233], v[30:33]
	ds_read_b128 v[230:233], v93 offset:6144
	ds_read_b128 v[160:163], v141 offset:25600
	v_mfma_f32_16x16x32_bf16 v[2:5], v[238:241], v[234:237], v[2:5]
	v_mfma_f32_16x16x32_bf16 v[6:9], v[242:245], v[234:237], v[6:9]
	v_mfma_f32_16x16x32_bf16 v[10:13], v[246:249], v[234:237], v[10:13]
	v_mfma_f32_16x16x32_bf16 v[14:17], v[250:253], v[234:237], v[14:17]
	ds_read_b128 v[234:237], v93 offset:8192
	s_waitcnt vmcnt(13)
	s_mov_b32 s49, s46
	s_mov_b32 s46, s47
	s_mov_b32 s47, s48
	s_mov_b32 s48, s49
	s_add_i32 s50, s50, 1
	s_waitcnt lgkmcnt(0)
	s_barrier
; #define MD_GLDS_A(buf, tau) do { _Pragma("unroll") for (int i = 0; i < 5; ++i) if (amask & (1u << i)) \
;         __builtin_amdgcn_global_load_lds((const unsigned*)((const char*)HIDp + aoff[i] + (size_t)((tau) & 7) * 128), (PG8_LAS unsigned*)(MD_SA(buf) + wid * 1024 + i * 8192), 16, 0, 0); } while (0)
; #define MD_B_ISSUE(sb, tau) do { const char* kb_ = Bb + (size_t)((tau) >> 3) * 512 + (size_t)((tau) & 7) * (64 * (size_t)RB); _Pragma("unroll") for (int j = 0; j < 8; ++j) { const char* p_ = kb_ + (size_t)j * RB; \
;         asm volatile("global_load_dwordx2 %0, %1, off" : "=&v"(sb[j]) : "v"(p_) : "memory"); } } while (0)
; #define MD_B_WAIT(sb, N) asm volatile("s_waitcnt vmcnt(%8)" : "+v"(sb[0]), "+v"(sb[1]), "+v"(sb[2]), "+v"(sb[3]), "+v"(sb[4]), "+v"(sb[5]), "+v"(sb[6]), "+v"(sb[7]) : "n"(N) : "memory")
; __device__ __forceinline__ void moe_down_stream(PG8_LAS unsigned char* lds, int e, int cb0, int slot0, int nv, const bf16_t* HIDp, const float* Wd, bf16_t* Y, const float* slot_w, const int* slot_dst) {
;     ...
;     f32x4 acc[DNM][4];
; #pragma unroll
;     for (int m = 0; m < DNM; ++m)
; #pragma unroll
;         for (int n = 0; n < 4; ++n) acc[m][n] = (f32x4){0.f, 0.f, 0.f, 0.f};
;     f32x2 s0[8], s1[8];
;     MD_GLDS_A(0, 0); MD_B_ISSUE(s0, 0); MD_B_ISSUE(s1, 1);
;     MD_B_WAIT(s0, 8); MD_B_WRITE(s0, 0); __builtin_amdgcn_sched_barrier(0); MD_B_ISSUE(s0, 2);
;     asm volatile("s_waitcnt vmcnt(16)" ::: "memory");
;     asm volatile("s_waitcnt lgkmcnt(0)" ::: "memory"); __builtin_amdgcn_s_barrier(); asm volatile("" ::: "memory");
; #pragma unroll 1
;     for (int t = 0; t < NT; t += 2) {
;         if (t + 2 < NT) MD_B_WAIT(s1, 8); else MD_B_WAIT(s1, 0);
;         MD_B_WRITE(s1, 1); __builtin_amdgcn_sched_barrier(0); MD_GLDS_A(1, t + 1); __builtin_amdgcn_sched_barrier(0);
;         if (t + 3 < NT) MD_B_ISSUE(s1, t + 3);
;         MD_COMPUTE(0);
;         MD_END(t + 3 >= NT);
;         if (t + 2 < NT) { MD_B_WAIT(s0, 8); MD_B_WRITE(s0, 0); __builtin_amdgcn_sched_barrier(0); MD_GLDS_A(0, t + 2); __builtin_amdgcn_sched_barrier(0); }
;         if (t + 4 < NT) MD_B_ISSUE(s0, t + 4);
;         MD_COMPUTE(1);
;         MD_END(t + 4 >= NT);
	s_add_i32 s49, s48, s74
	s_add_i32 s52, s52, 1
	s_and_b32 s54, s52, 7
	s_cmp_eq_u32 s54, 0
	s_cselect_b32 s54, s53, s32
	s_cselect_b32 s55, -1, 0
	s_add_u32 s30, s30, s54
	s_addc_u32 s31, s31, s55
	v_mfma_f32_16x16x32_bf16 v[78:81], v[142:145], v[218:221], v[78:81]
	v_mfma_f32_16x16x32_bf16 v[74:77], v[146:149], v[218:221], v[74:77]
	v_mfma_f32_16x16x32_bf16 v[70:73], v[156:159], v[218:221], v[70:73]
	v_mfma_f32_16x16x32_bf16 v[66:69], v[160:163], v[218:221], v[66:69]
	s_mov_b32 m0, s49
	s_nop 0
	global_load_lds_dwordx4 v88, s[30:31]
	v_mfma_f32_16x16x32_bf16 v[62:65], v[142:145], v[222:225], v[62:65]
	v_mfma_f32_16x16x32_bf16 v[58:61], v[146:149], v[222:225], v[58:61]
	v_mfma_f32_16x16x32_bf16 v[54:57], v[156:159], v[222:225], v[54:57]
	v_mfma_f32_16x16x32_bf16 v[50:53], v[160:163], v[222:225], v[50:53]
	s_add_i32 m0, s49, 0x2000
	s_nop 0
	global_load_lds_dwordx4 v90, s[30:31]
	v_mfma_f32_16x16x32_bf16 v[46:49], v[142:145], v[226:229], v[46:49]
	v_mfma_f32_16x16x32_bf16 v[42:45], v[146:149], v[226:229], v[42:45]
	v_mfma_f32_16x16x32_bf16 v[38:41], v[156:159], v[226:229], v[38:41]
	v_mfma_f32_16x16x32_bf16 v[34:37], v[160:163], v[226:229], v[34:37]
	s_add_i32 m0, s49, 0x4000
	s_nop 0
	global_load_lds_dwordx4 v92, s[30:31]
	v_mfma_f32_16x16x32_bf16 v[18:21], v[142:145], v[230:233], v[18:21]
	v_mfma_f32_16x16x32_bf16 v[22:25], v[146:149], v[230:233], v[22:25]
	v_mfma_f32_16x16x32_bf16 v[26:29], v[156:159], v[230:233], v[26:29]
	v_mfma_f32_16x16x32_bf16 v[30:33], v[160:163], v[230:233], v[30:33]
	s_add_i32 m0, s49, 0x6000
	s_nop 0
	global_load_lds_dwordx4 v94, s[30:31]
	v_mfma_f32_16x16x32_bf16 v[2:5], v[142:145], v[234:237], v[2:5]
	v_mfma_f32_16x16x32_bf16 v[6:9], v[146:149], v[234:237], v[6:9]
	v_mfma_f32_16x16x32_bf16 v[10:13], v[156:159], v[234:237], v[10:13]
	v_mfma_f32_16x16x32_bf16 v[14:17], v[160:163], v[234:237], v[14:17]
	s_add_i32 m0, s49, 0x8000
	s_nop 0
	global_load_lds_dwordx4 v96, s[30:31]
	v_cvt_pk_bf16_f32 v172, v114, v116
	v_cvt_pk_bf16_f32 v173, v118, v120
	v_cvt_pk_bf16_f32 v174, v122, v124
	v_cvt_pk_bf16_f32 v175, v126, v128
	v_cvt_pk_bf16_f32 v176, v115, v117
	v_cvt_pk_bf16_f32 v177, v119, v121
	v_cvt_pk_bf16_f32 v178, v123, v125
	v_cvt_pk_bf16_f32 v179, v127, v129
	ds_write_b128 v95, v[172:175] offset:19456
	ds_write_b128 v95, v[176:179] offset:19584
	v_add_u32_e32 v91, s46, v135
	v_add_u32_e32 v93, s46, v137
	ds_read_b128 v[238:241], v139 offset:0
	ds_read_b128 v[242:245], v139 offset:2048
	ds_read_b128 v[246:249], v139 offset:4096
	ds_read_b128 v[250:253], v139 offset:6144
	ds_read_b128 v[218:221], v91 offset:0
	ds_read_b128 v[222:225], v91 offset:2048
	ds_read_b128 v[226:229], v91 offset:4096
	ds_read_b128 v[230:233], v91 offset:6144
	ds_read_b128 v[234:237], v91 offset:8192
	s_waitcnt lgkmcnt(0)
	v_mfma_f32_16x16x32_bf16 v[78:81], v[238:241], v[218:221], v[78:81]
	v_mfma_f32_16x16x32_bf16 v[74:77], v[242:245], v[218:221], v[74:77]
	v_mfma_f32_16x16x32_bf16 v[70:73], v[246:249], v[218:221], v[70:73]
	v_mfma_f32_16x16x32_bf16 v[66:69], v[250:253], v[218:221], v[66:69]
	ds_read_b128 v[218:221], v93 offset:0
	ds_read_b128 v[142:145], v141 offset:0
	v_mfma_f32_16x16x32_bf16 v[62:65], v[238:241], v[222:225], v[62:65]
	v_mfma_f32_16x16x32_bf16 v[58:61], v[242:245], v[222:225], v[58:61]
	v_mfma_f32_16x16x32_bf16 v[54:57], v[246:249], v[222:225], v[54:57]
	v_mfma_f32_16x16x32_bf16 v[50:53], v[250:253], v[222:225], v[50:53]
	ds_read_b128 v[222:225], v93 offset:2048
	ds_read_b128 v[146:149], v141 offset:2048
	v_mfma_f32_16x16x32_bf16 v[46:49], v[238:241], v[226:229], v[46:49]
	v_mfma_f32_16x16x32_bf16 v[42:45], v[242:245], v[226:229], v[42:45]
	v_mfma_f32_16x16x32_bf16 v[38:41], v[246:249], v[226:229], v[38:41]
	v_mfma_f32_16x16x32_bf16 v[34:37], v[250:253], v[226:229], v[34:37]
	ds_read_b128 v[226:229], v93 offset:4096
	ds_read_b128 v[156:159], v141 offset:4096
	v_mfma_f32_16x16x32_bf16 v[18:21], v[238:241], v[230:233], v[18:21]
	v_mfma_f32_16x16x32_bf16 v[22:25], v[242:245], v[230:233], v[22:25]
	v_mfma_f32_16x16x32_bf16 v[26:29], v[246:249], v[230:233], v[26:29]
	v_mfma_f32_16x16x32_bf16 v[30:33], v[250:253], v[230:233], v[30:33]
	ds_read_b128 v[230:233], v93 offset:6144
	ds_read_b128 v[160:163], v141 offset:6144
	v_mfma_f32_16x16x32_bf16 v[2:5], v[238:241], v[234:237], v[2:5]
	v_mfma_f32_16x16x32_bf16 v[6:9], v[242:245], v[234:237], v[6:9]
	v_mfma_f32_16x16x32_bf16 v[10:13], v[246:249], v[234:237], v[10:13]
	v_mfma_f32_16x16x32_bf16 v[14:17], v[250:253], v[234:237], v[14:17]
	ds_read_b128 v[234:237], v93 offset:8192
	s_waitcnt vmcnt(5)
	s_mov_b32 s49, s46
	s_mov_b32 s46, s47
	s_mov_b32 s47, s48
	s_mov_b32 s48, s49
	s_add_i32 s50, s50, 1
	s_waitcnt lgkmcnt(0)
	s_barrier
; #define MD_GLDS_A(buf, tau) do { _Pragma("unroll") for (int i = 0; i < 5; ++i) if (amask & (1u << i)) \
;         __builtin_amdgcn_global_load_lds((const unsigned*)((const char*)HIDp + aoff[i] + (size_t)((tau) & 7) * 128), (PG8_LAS unsigned*)(MD_SA(buf) + wid * 1024 + i * 8192), 16, 0, 0); } while (0)
; #define MD_B_ISSUE(sb, tau) do { const char* kb_ = Bb + (size_t)((tau) >> 3) * 512 + (size_t)((tau) & 7) * (64 * (size_t)RB); _Pragma("unroll") for (int j = 0; j < 8; ++j) { const char* p_ = kb_ + (size_t)j * RB; \
;         asm volatile("global_load_dwordx2 %0, %1, off" : "=&v"(sb[j]) : "v"(p_) : "memory"); } } while (0)
; #define MD_B_WAIT(sb, N) asm volatile("s_waitcnt vmcnt(%8)" : "+v"(sb[0]), "+v"(sb[1]), "+v"(sb[2]), "+v"(sb[3]), "+v"(sb[4]), "+v"(sb[5]), "+v"(sb[6]), "+v"(sb[7]) : "n"(N) : "memory")
; __device__ __forceinline__ void moe_down_stream(PG8_LAS unsigned char* lds, int e, int cb0, int slot0, int nv, const bf16_t* HIDp, const float* Wd, bf16_t* Y, const float* slot_w, const int* slot_dst) {
;     ...
;     f32x4 acc[DNM][4];
; #pragma unroll
;     for (int m = 0; m < DNM; ++m)
; #pragma unroll
;         for (int n = 0; n < 4; ++n) acc[m][n] = (f32x4){0.f, 0.f, 0.f, 0.f};
;     f32x2 s0[8], s1[8];
;     MD_GLDS_A(0, 0); MD_B_ISSUE(s0, 0); MD_B_ISSUE(s1, 1);
;     MD_B_WAIT(s0, 8); MD_B_WRITE(s0, 0); __builtin_amdgcn_sched_barrier(0); MD_B_ISSUE(s0, 2);
;     asm volatile("s_waitcnt vmcnt(16)" ::: "memory");
;     asm volatile("s_waitcnt lgkmcnt(0)" ::: "memory"); __builtin_amdgcn_s_barrier(); asm volatile("" ::: "memory");
; #pragma unroll 1
;     for (int t = 0; t < NT; t += 2) {
;         if (t + 2 < NT) MD_B_WAIT(s1, 8); else MD_B_WAIT(s1, 0);
;         MD_B_WRITE(s1, 1); __builtin_amdgcn_sched_barrier(0); MD_GLDS_A(1, t + 1); __builtin_amdgcn_sched_barrier(0);
;         if (t + 3 < NT) MD_B_ISSUE(s1, t + 3);
;         MD_COMPUTE(0);
;         MD_END(t + 3 >= NT);
;         if (t + 2 < NT) { MD_B_WAIT(s0, 8); MD_B_WRITE(s0, 0); __builtin_amdgcn_sched_barrier(0); MD_GLDS_A(0, t + 2); __builtin_amdgcn_sched_barrier(0); }
;         if (t + 4 < NT) MD_B_ISSUE(s0, t + 4);
;         MD_COMPUTE(1);
;         MD_END(t + 4 >= NT);
	s_add_i32 s49, s48, s74
	s_add_i32 s52, s52, 1
	s_and_b32 s54, s52, 7
	s_cmp_eq_u32 s54, 0
	s_cselect_b32 s54, s53, s32
	s_cselect_b32 s55, -1, 0
	s_add_u32 s30, s30, s54
	s_addc_u32 s31, s31, s55
	v_mfma_f32_16x16x32_bf16 v[78:81], v[142:145], v[218:221], v[78:81]
	v_mfma_f32_16x16x32_bf16 v[74:77], v[146:149], v[218:221], v[74:77]
	v_mfma_f32_16x16x32_bf16 v[70:73], v[156:159], v[218:221], v[70:73]
	v_mfma_f32_16x16x32_bf16 v[66:69], v[160:163], v[218:221], v[66:69]
	s_mov_b32 m0, s49
	s_nop 0
	global_load_lds_dwordx4 v88, s[30:31]
	v_mfma_f32_16x16x32_bf16 v[62:65], v[142:145], v[222:225], v[62:65]
	v_mfma_f32_16x16x32_bf16 v[58:61], v[146:149], v[222:225], v[58:61]
	v_mfma_f32_16x16x32_bf16 v[54:57], v[156:159], v[222:225], v[54:57]
	v_mfma_f32_16x16x32_bf16 v[50:53], v[160:163], v[222:225], v[50:53]
	s_add_i32 m0, s49, 0x2000
	s_nop 0
	global_load_lds_dwordx4 v90, s[30:31]
	v_mfma_f32_16x16x32_bf16 v[46:49], v[142:145], v[226:229], v[46:49]
	v_mfma_f32_16x16x32_bf16 v[42:45], v[146:149], v[226:229], v[42:45]
	v_mfma_f32_16x16x32_bf16 v[38:41], v[156:159], v[226:229], v[38:41]
	v_mfma_f32_16x16x32_bf16 v[34:37], v[160:163], v[226:229], v[34:37]
	s_add_i32 m0, s49, 0x4000
	s_nop 0
	global_load_lds_dwordx4 v92, s[30:31]
	v_mfma_f32_16x16x32_bf16 v[18:21], v[142:145], v[230:233], v[18:21]
	v_mfma_f32_16x16x32_bf16 v[22:25], v[146:149], v[230:233], v[22:25]
	v_mfma_f32_16x16x32_bf16 v[26:29], v[156:159], v[230:233], v[26:29]
	v_mfma_f32_16x16x32_bf16 v[30:33], v[160:163], v[230:233], v[30:33]
	s_add_i32 m0, s49, 0x6000
	s_nop 0
	global_load_lds_dwordx4 v94, s[30:31]
	v_mfma_f32_16x16x32_bf16 v[2:5], v[142:145], v[234:237], v[2:5]
	v_mfma_f32_16x16x32_bf16 v[6:9], v[146:149], v[234:237], v[6:9]
	v_mfma_f32_16x16x32_bf16 v[10:13], v[156:159], v[234:237], v[10:13]
	v_mfma_f32_16x16x32_bf16 v[14:17], v[160:163], v[234:237], v[14:17]
	s_add_i32 m0, s49, 0x8000
	s_nop 0
	global_load_lds_dwordx4 v96, s[30:31]
	v_cvt_pk_bf16_f32 v172, v186, v188
	v_cvt_pk_bf16_f32 v173, v190, v192
	v_cvt_pk_bf16_f32 v174, v194, v196
	v_cvt_pk_bf16_f32 v175, v198, v200
	v_cvt_pk_bf16_f32 v176, v187, v189
	v_cvt_pk_bf16_f32 v177, v191, v193
	v_cvt_pk_bf16_f32 v178, v195, v197
	v_cvt_pk_bf16_f32 v179, v199, v201
	ds_write_b128 v95, v[172:175] offset:0
	ds_write_b128 v95, v[176:179] offset:128
	v_add_u32_e32 v91, s46, v135
	v_add_u32_e32 v93, s46, v137
	ds_read_b128 v[238:241], v139 offset:19456
	ds_read_b128 v[242:245], v139 offset:21504
	ds_read_b128 v[246:249], v139 offset:23552
	ds_read_b128 v[250:253], v139 offset:25600
	ds_read_b128 v[218:221], v91 offset:0
	ds_read_b128 v[222:225], v91 offset:2048
	ds_read_b128 v[226:229], v91 offset:4096
	ds_read_b128 v[230:233], v91 offset:6144
	ds_read_b128 v[234:237], v91 offset:8192
	s_waitcnt lgkmcnt(0)
	v_mfma_f32_16x16x32_bf16 v[78:81], v[238:241], v[218:221], v[78:81]
	v_mfma_f32_16x16x32_bf16 v[74:77], v[242:245], v[218:221], v[74:77]
	v_mfma_f32_16x16x32_bf16 v[70:73], v[246:249], v[218:221], v[70:73]
	v_mfma_f32_16x16x32_bf16 v[66:69], v[250:253], v[218:221], v[66:69]
	ds_read_b128 v[218:221], v93 offset:0
	ds_read_b128 v[142:145], v141 offset:19456
	v_mfma_f32_16x16x32_bf16 v[62:65], v[238:241], v[222:225], v[62:65]
	v_mfma_f32_16x16x32_bf16 v[58:61], v[242:245], v[222:225], v[58:61]
	v_mfma_f32_16x16x32_bf16 v[54:57], v[246:249], v[222:225], v[54:57]
	v_mfma_f32_16x16x32_bf16 v[50:53], v[250:253], v[222:225], v[50:53]
	ds_read_b128 v[222:225], v93 offset:2048
	ds_read_b128 v[146:149], v141 offset:21504
	v_mfma_f32_16x16x32_bf16 v[46:49], v[238:241], v[226:229], v[46:49]
	v_mfma_f32_16x16x32_bf16 v[42:45], v[242:245], v[226:229], v[42:45]
	v_mfma_f32_16x16x32_bf16 v[38:41], v[246:249], v[226:229], v[38:41]
	v_mfma_f32_16x16x32_bf16 v[34:37], v[250:253], v[226:229], v[34:37]
	ds_read_b128 v[226:229], v93 offset:4096
	ds_read_b128 v[156:159], v141 offset:23552
	v_mfma_f32_16x16x32_bf16 v[18:21], v[238:241], v[230:233], v[18:21]
	v_mfma_f32_16x16x32_bf16 v[22:25], v[242:245], v[230:233], v[22:25]
	v_mfma_f32_16x16x32_bf16 v[26:29], v[246:249], v[230:233], v[26:29]
	v_mfma_f32_16x16x32_bf16 v[30:33], v[250:253], v[230:233], v[30:33]
	ds_read_b128 v[230:233], v93 offset:6144
	ds_read_b128 v[160:163], v141 offset:25600
	v_mfma_f32_16x16x32_bf16 v[2:5], v[238:241], v[234:237], v[2:5]
	v_mfma_f32_16x16x32_bf16 v[6:9], v[242:245], v[234:237], v[6:9]
	v_mfma_f32_16x16x32_bf16 v[10:13], v[246:249], v[234:237], v[10:13]
	v_mfma_f32_16x16x32_bf16 v[14:17], v[250:253], v[234:237], v[14:17]
	ds_read_b128 v[234:237], v93 offset:8192
	s_waitcnt vmcnt(5)
	s_mov_b32 s49, s46
	s_mov_b32 s46, s47
	s_mov_b32 s47, s48
	s_mov_b32 s48, s49
	s_add_i32 s50, s50, 1
	s_waitcnt lgkmcnt(0)
	s_barrier
; #define MD_GLDS_A(buf, tau) do { _Pragma("unroll") for (int i = 0; i < 5; ++i) if (amask & (1u << i)) \
;         __builtin_amdgcn_global_load_lds((const unsigned*)((const char*)HIDp + aoff[i] + (size_t)((tau) & 7) * 128), (PG8_LAS unsigned*)(MD_SA(buf) + wid * 1024 + i * 8192), 16, 0, 0); } while (0)
; #define MD_B_ISSUE(sb, tau) do { const char* kb_ = Bb + (size_t)((tau) >> 3) * 512 + (size_t)((tau) & 7) * (64 * (size_t)RB); _Pragma("unroll") for (int j = 0; j < 8; ++j) { const char* p_ = kb_ + (size_t)j * RB; \
;         asm volatile("global_load_dwordx2 %0, %1, off" : "=&v"(sb[j]) : "v"(p_) : "memory"); } } while (0)
; #define MD_B_WAIT(sb, N) asm volatile("s_waitcnt vmcnt(%8)" : "+v"(sb[0]), "+v"(sb[1]), "+v"(sb[2]), "+v"(sb[3]), "+v"(sb[4]), "+v"(sb[5]), "+v"(sb[6]), "+v"(sb[7]) : "n"(N) : "memory")
; __device__ __forceinline__ void moe_down_stream(PG8_LAS unsigned char* lds, int e, int cb0, int slot0, int nv, const bf16_t* HIDp, const float* Wd, bf16_t* Y, const float* slot_w, const int* slot_dst) {
;     ...
;     f32x4 acc[DNM][4];
; #pragma unroll
;     for (int m = 0; m < DNM; ++m)
; #pragma unroll
;         for (int n = 0; n < 4; ++n) acc[m][n] = (f32x4){0.f, 0.f, 0.f, 0.f};
;     f32x2 s0[8], s1[8];
;     MD_GLDS_A(0, 0); MD_B_ISSUE(s0, 0); MD_B_ISSUE(s1, 1);
;     MD_B_WAIT(s0, 8); MD_B_WRITE(s0, 0); __builtin_amdgcn_sched_barrier(0); MD_B_ISSUE(s0, 2);
;     asm volatile("s_waitcnt vmcnt(16)" ::: "memory");
;     asm volatile("s_waitcnt lgkmcnt(0)" ::: "memory"); __builtin_amdgcn_s_barrier(); asm volatile("" ::: "memory");
; #pragma unroll 1
;     for (int t = 0; t < NT; t += 2) {
;         if (t + 2 < NT) MD_B_WAIT(s1, 8); else MD_B_WAIT(s1, 0);
;         MD_B_WRITE(s1, 1); __builtin_amdgcn_sched_barrier(0); MD_GLDS_A(1, t + 1); __builtin_amdgcn_sched_barrier(0);
;         if (t + 3 < NT) MD_B_ISSUE(s1, t + 3);
;         MD_COMPUTE(0);
;         MD_END(t + 3 >= NT);
;         if (t + 2 < NT) { MD_B_WAIT(s0, 8); MD_B_WRITE(s0, 0); __builtin_amdgcn_sched_barrier(0); MD_GLDS_A(0, t + 2); __builtin_amdgcn_sched_barrier(0); }
;         if (t + 4 < NT) MD_B_ISSUE(s0, t + 4);
;         MD_COMPUTE(1);
;         MD_END(t + 4 >= NT);
	v_mfma_f32_16x16x32_bf16 v[78:81], v[142:145], v[218:221], v[78:81]
	v_mfma_f32_16x16x32_bf16 v[74:77], v[146:149], v[218:221], v[74:77]
	v_mfma_f32_16x16x32_bf16 v[70:73], v[156:159], v[218:221], v[70:73]
	v_mfma_f32_16x16x32_bf16 v[66:69], v[160:163], v[218:221], v[66:69]
	v_mfma_f32_16x16x32_bf16 v[62:65], v[142:145], v[222:225], v[62:65]
	v_mfma_f32_16x16x32_bf16 v[58:61], v[146:149], v[222:225], v[58:61]
	v_mfma_f32_16x16x32_bf16 v[54:57], v[156:159], v[222:225], v[54:57]
	v_mfma_f32_16x16x32_bf16 v[50:53], v[160:163], v[222:225], v[50:53]
	v_mfma_f32_16x16x32_bf16 v[46:49], v[142:145], v[226:229], v[46:49]
	v_mfma_f32_16x16x32_bf16 v[42:45], v[146:149], v[226:229], v[42:45]
	v_mfma_f32_16x16x32_bf16 v[38:41], v[156:159], v[226:229], v[38:41]
	v_mfma_f32_16x16x32_bf16 v[34:37], v[160:163], v[226:229], v[34:37]
	v_mfma_f32_16x16x32_bf16 v[18:21], v[142:145], v[230:233], v[18:21]
	v_mfma_f32_16x16x32_bf16 v[22:25], v[146:149], v[230:233], v[22:25]
	v_mfma_f32_16x16x32_bf16 v[26:29], v[156:159], v[230:233], v[26:29]
	v_mfma_f32_16x16x32_bf16 v[30:33], v[160:163], v[230:233], v[30:33]
	v_mfma_f32_16x16x32_bf16 v[2:5], v[142:145], v[234:237], v[2:5]
	v_mfma_f32_16x16x32_bf16 v[6:9], v[146:149], v[234:237], v[6:9]
	v_mfma_f32_16x16x32_bf16 v[10:13], v[156:159], v[234:237], v[10:13]
	v_mfma_f32_16x16x32_bf16 v[14:17], v[160:163], v[234:237], v[14:17]
	v_cvt_pk_bf16_f32 v172, v202, v204
	v_cvt_pk_bf16_f32 v173, v206, v208
	v_cvt_pk_bf16_f32 v174, v210, v212
	v_cvt_pk_bf16_f32 v175, v214, v216
	v_cvt_pk_bf16_f32 v176, v203, v205
	v_cvt_pk_bf16_f32 v177, v207, v209
	v_cvt_pk_bf16_f32 v178, v211, v213
	v_cvt_pk_bf16_f32 v179, v215, v217
	ds_write_b128 v95, v[172:175] offset:19456
	ds_write_b128 v95, v[176:179] offset:19584
	v_add_u32_e32 v91, s46, v135
	v_add_u32_e32 v93, s46, v137
	ds_read_b128 v[238:241], v139 offset:0
	ds_read_b128 v[242:245], v139 offset:2048
	ds_read_b128 v[246:249], v139 offset:4096
	ds_read_b128 v[250:253], v139 offset:6144
	ds_read_b128 v[218:221], v91 offset:0
	ds_read_b128 v[222:225], v91 offset:2048
	ds_read_b128 v[226:229], v91 offset:4096
	ds_read_b128 v[230:233], v91 offset:6144
	ds_read_b128 v[234:237], v91 offset:8192
	s_waitcnt lgkmcnt(0)
	v_mfma_f32_16x16x32_bf16 v[78:81], v[238:241], v[218:221], v[78:81]
	v_mfma_f32_16x16x32_bf16 v[74:77], v[242:245], v[218:221], v[74:77]
	v_mfma_f32_16x16x32_bf16 v[70:73], v[246:249], v[218:221], v[70:73]
	v_mfma_f32_16x16x32_bf16 v[66:69], v[250:253], v[218:221], v[66:69]
	ds_read_b128 v[218:221], v93 offset:0
	ds_read_b128 v[142:145], v141 offset:0
	v_mfma_f32_16x16x32_bf16 v[62:65], v[238:241], v[222:225], v[62:65]
	v_mfma_f32_16x16x32_bf16 v[58:61], v[242:245], v[222:225], v[58:61]
	v_mfma_f32_16x16x32_bf16 v[54:57], v[246:249], v[222:225], v[54:57]
	v_mfma_f32_16x16x32_bf16 v[50:53], v[250:253], v[222:225], v[50:53]
	ds_read_b128 v[222:225], v93 offset:2048
	ds_read_b128 v[146:149], v141 offset:2048
	v_mfma_f32_16x16x32_bf16 v[46:49], v[238:241], v[226:229], v[46:49]
	v_mfma_f32_16x16x32_bf16 v[42:45], v[242:245], v[226:229], v[42:45]
	v_mfma_f32_16x16x32_bf16 v[38:41], v[246:249], v[226:229], v[38:41]
	v_mfma_f32_16x16x32_bf16 v[34:37], v[250:253], v[226:229], v[34:37]
	ds_read_b128 v[226:229], v93 offset:4096
	ds_read_b128 v[156:159], v141 offset:4096
	v_mfma_f32_16x16x32_bf16 v[18:21], v[238:241], v[230:233], v[18:21]
	v_mfma_f32_16x16x32_bf16 v[22:25], v[242:245], v[230:233], v[22:25]
	v_mfma_f32_16x16x32_bf16 v[26:29], v[246:249], v[230:233], v[26:29]
	v_mfma_f32_16x16x32_bf16 v[30:33], v[250:253], v[230:233], v[30:33]
	ds_read_b128 v[230:233], v93 offset:6144
	ds_read_b128 v[160:163], v141 offset:6144
	v_mfma_f32_16x16x32_bf16 v[2:5], v[238:241], v[234:237], v[2:5]
	v_mfma_f32_16x16x32_bf16 v[6:9], v[242:245], v[234:237], v[6:9]
	v_mfma_f32_16x16x32_bf16 v[10:13], v[246:249], v[234:237], v[10:13]
	v_mfma_f32_16x16x32_bf16 v[14:17], v[250:253], v[234:237], v[14:17]
	ds_read_b128 v[234:237], v93 offset:8192
	s_waitcnt vmcnt(0)
	s_mov_b32 s49, s46
	s_mov_b32 s46, s47
	s_mov_b32 s47, s48
	s_mov_b32 s48, s49
	s_add_i32 s50, s50, 1
	s_waitcnt lgkmcnt(0)
	s_barrier
	v_mfma_f32_16x16x32_bf16 v[78:81], v[142:145], v[218:221], v[78:81]
	v_mfma_f32_16x16x32_bf16 v[74:77], v[146:149], v[218:221], v[74:77]
	v_mfma_f32_16x16x32_bf16 v[70:73], v[156:159], v[218:221], v[70:73]
	v_mfma_f32_16x16x32_bf16 v[66:69], v[160:163], v[218:221], v[66:69]
	v_mfma_f32_16x16x32_bf16 v[62:65], v[142:145], v[222:225], v[62:65]
	v_mfma_f32_16x16x32_bf16 v[58:61], v[146:149], v[222:225], v[58:61]
	v_mfma_f32_16x16x32_bf16 v[54:57], v[156:159], v[222:225], v[54:57]
	v_mfma_f32_16x16x32_bf16 v[50:53], v[160:163], v[222:225], v[50:53]
	v_mfma_f32_16x16x32_bf16 v[46:49], v[142:145], v[226:229], v[46:49]
	v_mfma_f32_16x16x32_bf16 v[42:45], v[146:149], v[226:229], v[42:45]
	v_mfma_f32_16x16x32_bf16 v[38:41], v[156:159], v[226:229], v[38:41]
	v_mfma_f32_16x16x32_bf16 v[34:37], v[160:163], v[226:229], v[34:37]
	v_mfma_f32_16x16x32_bf16 v[18:21], v[142:145], v[230:233], v[18:21]
	v_mfma_f32_16x16x32_bf16 v[22:25], v[146:149], v[230:233], v[22:25]
	v_mfma_f32_16x16x32_bf16 v[26:29], v[156:159], v[230:233], v[26:29]
	v_mfma_f32_16x16x32_bf16 v[30:33], v[160:163], v[230:233], v[30:33]
	v_mfma_f32_16x16x32_bf16 v[2:5], v[142:145], v[234:237], v[2:5]
	v_mfma_f32_16x16x32_bf16 v[6:9], v[146:149], v[234:237], v[6:9]
	v_mfma_f32_16x16x32_bf16 v[10:13], v[156:159], v[234:237], v[10:13]
	v_mfma_f32_16x16x32_bf16 v[14:17], v[160:163], v[234:237], v[14:17]
	v_add_u32_e32 v91, s46, v135
	v_add_u32_e32 v93, s46, v137
	ds_read_b128 v[238:241], v139 offset:19456
	ds_read_b128 v[242:245], v139 offset:21504
	ds_read_b128 v[246:249], v139 offset:23552
	ds_read_b128 v[250:253], v139 offset:25600
	ds_read_b128 v[218:221], v91 offset:0
	ds_read_b128 v[222:225], v91 offset:2048
	ds_read_b128 v[226:229], v91 offset:4096
	ds_read_b128 v[230:233], v91 offset:6144
	ds_read_b128 v[234:237], v91 offset:8192
	s_waitcnt lgkmcnt(0)
; #define PG8_LAS __attribute__((address_space(3)))
; __device__ __forceinline__ unsigned cvtpk(float lo, float hi) { f32x2 v = {lo, hi}; bf16x2_t b = __builtin_convertvector(v, bf16x2_t); return __builtin_bit_cast(unsigned, b); }
; __device__ __forceinline__ void moe_down_stream(PG8_LAS unsigned char* lds, int e, int cb0, int slot0, int nv, const bf16_t* HIDp, const float* Wd, bf16_t* Y, const float* slot_w, const int* slot_dst) {
;     ...
;         if (((t + 1) & 7) == 7) {
;             const int cb = cb0 + ((t + 1) >> 3);
; #pragma unroll
;             for (int m = 0; m < DNM; ++m) {
;                 const float w_ = lw[4 * (16 * m + fr) + wr];
; #pragma unroll
;                 for (int p = 0; p < 2; ++p) { const f32x4 v0 = acc[m][2 * p] * w_, v1 = acc[m][2 * p + 1] * w_; u32x4 w; w.x = cvtpk(v0[0], v0[1]); w.y = cvtpk(v0[2], v0[3]); w.z = cvtpk(v1[0], v1[1]); w.w = cvtpk(v1[2], v1[3]);
;                     *(PG8_LAS u32x4*)(stg + fr * 128 + (((4 * p + fq) ^ (fr & 7)) * 16)) = w; }
; #pragma unroll
;                 for (int hh = 0; hh < 2; ++hh) { const int r = (lane >> 3) + 8 * hh, cc = lane & 7; const u32x4 d = *(const PG8_LAS u32x4*)(stg + r * 128 + ((cc ^ (r & 7)) * 16)); const int dst_ = ldst[4 * (16 * m + r) + wr];
;                     if (dst_ >= 0) *(u32x4*)(Y + (size_t)dst_ * D + 128 * cb + 64 * wc + 8 * cc) = d; }
; #pragma unroll
;                 for (int n = 0; n < 4; ++n) acc[m][n] = (f32x4){0.f, 0.f, 0.f, 0.f}; } }
	v_mfma_f32_16x16x32_bf16 v[78:81], v[238:241], v[218:221], v[78:81]
	v_mfma_f32_16x16x32_bf16 v[74:77], v[242:245], v[218:221], v[74:77]
	v_mfma_f32_16x16x32_bf16 v[70:73], v[246:249], v[218:221], v[70:73]
	v_mfma_f32_16x16x32_bf16 v[66:69], v[250:253], v[218:221], v[66:69]
	ds_read_b128 v[218:221], v93 offset:0
	ds_read_b128 v[142:145], v141 offset:19456
	v_mfma_f32_16x16x32_bf16 v[62:65], v[238:241], v[222:225], v[62:65]
	v_mfma_f32_16x16x32_bf16 v[58:61], v[242:245], v[222:225], v[58:61]
	v_mfma_f32_16x16x32_bf16 v[54:57], v[246:249], v[222:225], v[54:57]
	v_mfma_f32_16x16x32_bf16 v[50:53], v[250:253], v[222:225], v[50:53]
	ds_read_b128 v[222:225], v93 offset:2048
	ds_read_b128 v[146:149], v141 offset:21504
	v_mfma_f32_16x16x32_bf16 v[46:49], v[238:241], v[226:229], v[46:49]
	v_mfma_f32_16x16x32_bf16 v[42:45], v[242:245], v[226:229], v[42:45]
	v_mfma_f32_16x16x32_bf16 v[38:41], v[246:249], v[226:229], v[38:41]
	v_mfma_f32_16x16x32_bf16 v[34:37], v[250:253], v[226:229], v[34:37]
	ds_read_b128 v[226:229], v93 offset:4096
	ds_read_b128 v[156:159], v141 offset:23552
	v_mfma_f32_16x16x32_bf16 v[18:21], v[238:241], v[230:233], v[18:21]
	v_mfma_f32_16x16x32_bf16 v[22:25], v[242:245], v[230:233], v[22:25]
	v_mfma_f32_16x16x32_bf16 v[26:29], v[246:249], v[230:233], v[26:29]
	v_mfma_f32_16x16x32_bf16 v[30:33], v[250:253], v[230:233], v[30:33]
	ds_read_b128 v[230:233], v93 offset:6144
	ds_read_b128 v[160:163], v141 offset:25600
	v_mfma_f32_16x16x32_bf16 v[2:5], v[238:241], v[234:237], v[2:5]
	v_mfma_f32_16x16x32_bf16 v[6:9], v[242:245], v[234:237], v[6:9]
	v_mfma_f32_16x16x32_bf16 v[10:13], v[246:249], v[234:237], v[10:13]
	v_mfma_f32_16x16x32_bf16 v[14:17], v[250:253], v[234:237], v[14:17]
	ds_read_b128 v[234:237], v93 offset:8192
	s_mov_b32 s49, s46
	s_mov_b32 s46, s47
	s_mov_b32 s47, s48
	s_mov_b32 s48, s49
	s_add_i32 s50, s50, 1
	s_waitcnt lgkmcnt(0)
	s_barrier
	v_mfma_f32_16x16x32_bf16 v[78:81], v[142:145], v[218:221], v[78:81]
	v_mfma_f32_16x16x32_bf16 v[74:77], v[146:149], v[218:221], v[74:77]
	v_mfma_f32_16x16x32_bf16 v[70:73], v[156:159], v[218:221], v[70:73]
	v_mfma_f32_16x16x32_bf16 v[66:69], v[160:163], v[218:221], v[66:69]
	v_mfma_f32_16x16x32_bf16 v[62:65], v[142:145], v[222:225], v[62:65]
	v_mfma_f32_16x16x32_bf16 v[58:61], v[146:149], v[222:225], v[58:61]
	v_mfma_f32_16x16x32_bf16 v[54:57], v[156:159], v[222:225], v[54:57]
	v_mfma_f32_16x16x32_bf16 v[50:53], v[160:163], v[222:225], v[50:53]
	v_mfma_f32_16x16x32_bf16 v[46:49], v[142:145], v[226:229], v[46:49]
	v_mfma_f32_16x16x32_bf16 v[42:45], v[146:149], v[226:229], v[42:45]
	v_mfma_f32_16x16x32_bf16 v[38:41], v[156:159], v[226:229], v[38:41]
	v_mfma_f32_16x16x32_bf16 v[34:37], v[160:163], v[226:229], v[34:37]
	v_mfma_f32_16x16x32_bf16 v[18:21], v[142:145], v[230:233], v[18:21]
	v_mfma_f32_16x16x32_bf16 v[22:25], v[146:149], v[230:233], v[22:25]
	v_mfma_f32_16x16x32_bf16 v[26:29], v[156:159], v[230:233], v[26:29]
	v_mfma_f32_16x16x32_bf16 v[30:33], v[160:163], v[230:233], v[30:33]
	v_mfma_f32_16x16x32_bf16 v[2:5], v[142:145], v[234:237], v[2:5]
	v_mfma_f32_16x16x32_bf16 v[6:9], v[146:149], v[234:237], v[6:9]
	v_mfma_f32_16x16x32_bf16 v[10:13], v[156:159], v[234:237], v[10:13]
	v_mfma_f32_16x16x32_bf16 v[14:17], v[160:163], v[234:237], v[14:17]
	s_add_i32 s54, s48, s74
	v_add_u32_e32 v164, s54, v84
	v_add_u32_e32 v165, s54, v85
	ds_read_b32 v150, v82 offset:0
	ds_read_b32 v151, v83 offset:0
	ds_read_b32 v166, v83 offset:128
	s_waitcnt lgkmcnt(2)
	v_mul_f32_e32 v78, v150, v78
	v_mul_f32_e32 v79, v150, v79
	v_mul_f32_e32 v80, v150, v80
	v_mul_f32_e32 v81, v150, v81
	v_mul_f32_e32 v74, v150, v74
	v_mul_f32_e32 v75, v150, v75
	v_mul_f32_e32 v76, v150, v76
	v_mul_f32_e32 v77, v150, v77
	v_cvt_pk_bf16_f32 v182, v78, v79
	v_cvt_pk_bf16_f32 v183, v80, v81
	v_cvt_pk_bf16_f32 v184, v74, v75
	v_cvt_pk_bf16_f32 v185, v76, v77
	ds_write_b128 v164, v[182:185]
	v_mul_f32_e32 v70, v150, v70
	v_mul_f32_e32 v71, v150, v71
	v_mul_f32_e32 v72, v150, v72
	v_mul_f32_e32 v73, v150, v73
	v_mul_f32_e32 v66, v150, v66
	v_mul_f32_e32 v67, v150, v67
	v_mul_f32_e32 v68, v150, v68
	v_mul_f32_e32 v69, v150, v69
	v_cvt_pk_bf16_f32 v182, v70, v71
	v_cvt_pk_bf16_f32 v183, v72, v73
	v_cvt_pk_bf16_f32 v184, v66, v67
	v_cvt_pk_bf16_f32 v185, v68, v69
	v_xor_b32_e32 v167, 64, v164
	ds_write_b128 v167, v[182:185]
	v_mov_b32_e32 v78, 0
	v_mov_b32_e32 v74, 0
	v_mov_b32_e32 v70, 0
	v_mov_b32_e32 v66, 0
	v_mov_b32_e32 v79, 0
	v_mov_b32_e32 v75, 0
	v_mov_b32_e32 v71, 0
	v_mov_b32_e32 v67, 0
	v_mov_b32_e32 v80, 0
	v_mov_b32_e32 v76, 0
	v_mov_b32_e32 v72, 0
	v_mov_b32_e32 v68, 0
	v_mov_b32_e32 v81, 0
	v_mov_b32_e32 v77, 0
	v_mov_b32_e32 v73, 0
	v_mov_b32_e32 v69, 0
	ds_read_b128 v[182:185], v165 offset:0
	v_cmp_lt_i32_e32 vcc, -1, v151
	v_lshlrev_b32_e32 v148, 13, v151
	v_mov_b32_e32 v149, 0
	v_lshl_add_u64 v[148:149], v[148:149], 0, v[86:87]
	v_cndmask_b32_e32 v148, v168, v148, vcc
	v_cndmask_b32_e32 v149, v169, v149, vcc
	s_waitcnt lgkmcnt(0)
	global_store_dwordx4 v[148:149], v[182:185], off
	ds_read_b128 v[182:185], v165 offset:8192
	v_cmp_lt_i32_e32 vcc, -1, v166
	v_lshlrev_b32_e32 v148, 13, v166
	v_mov_b32_e32 v149, 0
	v_lshl_add_u64 v[148:149], v[148:149], 0, v[86:87]
	v_cndmask_b32_e32 v148, v168, v148, vcc
	v_cndmask_b32_e32 v149, v169, v149, vcc
	s_waitcnt lgkmcnt(0)
	global_store_dwordx4 v[148:149], v[182:185], off
	ds_read_b32 v150, v82 offset:256
	ds_read_b32 v151, v83 offset:256
	ds_read_b32 v166, v83 offset:384
	s_waitcnt lgkmcnt(2)
; #define PG8_LAS __attribute__((address_space(3)))
; __device__ __forceinline__ unsigned cvtpk(float lo, float hi) { f32x2 v = {lo, hi}; bf16x2_t b = __builtin_convertvector(v, bf16x2_t); return __builtin_bit_cast(unsigned, b); }
; __device__ __forceinline__ void moe_down_stream(PG8_LAS unsigned char* lds, int e, int cb0, int slot0, int nv, const bf16_t* HIDp, const float* Wd, bf16_t* Y, const float* slot_w, const int* slot_dst) {
;     ...
;         if (((t + 1) & 7) == 7) {
;             const int cb = cb0 + ((t + 1) >> 3);
; #pragma unroll
;             for (int m = 0; m < DNM; ++m) {
;                 const float w_ = lw[4 * (16 * m + fr) + wr];
; #pragma unroll
;                 for (int p = 0; p < 2; ++p) { const f32x4 v0 = acc[m][2 * p] * w_, v1 = acc[m][2 * p + 1] * w_; u32x4 w; w.x = cvtpk(v0[0], v0[1]); w.y = cvtpk(v0[2], v0[3]); w.z = cvtpk(v1[0], v1[1]); w.w = cvtpk(v1[2], v1[3]);
;                     *(PG8_LAS u32x4*)(stg + fr * 128 + (((4 * p + fq) ^ (fr & 7)) * 16)) = w; }
; #pragma unroll
;                 for (int hh = 0; hh < 2; ++hh) { const int r = (lane >> 3) + 8 * hh, cc = lane & 7; const u32x4 d = *(const PG8_LAS u32x4*)(stg + r * 128 + ((cc ^ (r & 7)) * 16)); const int dst_ = ldst[4 * (16 * m + r) + wr];
;                     if (dst_ >= 0) *(u32x4*)(Y + (size_t)dst_ * D + 128 * cb + 64 * wc + 8 * cc) = d; }
; #pragma unroll
;                 for (int n = 0; n < 4; ++n) acc[m][n] = (f32x4){0.f, 0.f, 0.f, 0.f}; } }
	v_mul_f32_e32 v62, v150, v62
	v_mul_f32_e32 v63, v150, v63
	v_mul_f32_e32 v64, v150, v64
	v_mul_f32_e32 v65, v150, v65
	v_mul_f32_e32 v58, v150, v58
	v_mul_f32_e32 v59, v150, v59
	v_mul_f32_e32 v60, v150, v60
	v_mul_f32_e32 v61, v150, v61
	v_cvt_pk_bf16_f32 v182, v62, v63
	v_cvt_pk_bf16_f32 v183, v64, v65
	v_cvt_pk_bf16_f32 v184, v58, v59
	v_cvt_pk_bf16_f32 v185, v60, v61
	ds_write_b128 v164, v[182:185]
	v_mul_f32_e32 v54, v150, v54
	v_mul_f32_e32 v55, v150, v55
	v_mul_f32_e32 v56, v150, v56
	v_mul_f32_e32 v57, v150, v57
	v_mul_f32_e32 v50, v150, v50
	v_mul_f32_e32 v51, v150, v51
	v_mul_f32_e32 v52, v150, v52
	v_mul_f32_e32 v53, v150, v53
	v_cvt_pk_bf16_f32 v182, v54, v55
	v_cvt_pk_bf16_f32 v183, v56, v57
	v_cvt_pk_bf16_f32 v184, v50, v51
	v_cvt_pk_bf16_f32 v185, v52, v53
	v_xor_b32_e32 v167, 64, v164
	ds_write_b128 v167, v[182:185]
	v_mov_b32_e32 v62, 0
	v_mov_b32_e32 v58, 0
	v_mov_b32_e32 v54, 0
	v_mov_b32_e32 v50, 0
	v_mov_b32_e32 v63, 0
	v_mov_b32_e32 v59, 0
	v_mov_b32_e32 v55, 0
	v_mov_b32_e32 v51, 0
	v_mov_b32_e32 v64, 0
	v_mov_b32_e32 v60, 0
	v_mov_b32_e32 v56, 0
	v_mov_b32_e32 v52, 0
	v_mov_b32_e32 v65, 0
	v_mov_b32_e32 v61, 0
	v_mov_b32_e32 v57, 0
	v_mov_b32_e32 v53, 0
	ds_read_b128 v[182:185], v165 offset:0
	v_cmp_lt_i32_e32 vcc, -1, v151
	v_lshlrev_b32_e32 v148, 13, v151
	v_mov_b32_e32 v149, 0
	v_lshl_add_u64 v[148:149], v[148:149], 0, v[86:87]
	v_cndmask_b32_e32 v148, v168, v148, vcc
	v_cndmask_b32_e32 v149, v169, v149, vcc
	s_waitcnt lgkmcnt(0)
	global_store_dwordx4 v[148:149], v[182:185], off
	ds_read_b128 v[182:185], v165 offset:8192
	v_cmp_lt_i32_e32 vcc, -1, v166
	v_lshlrev_b32_e32 v148, 13, v166
	v_mov_b32_e32 v149, 0
	v_lshl_add_u64 v[148:149], v[148:149], 0, v[86:87]
	v_cndmask_b32_e32 v148, v168, v148, vcc
	v_cndmask_b32_e32 v149, v169, v149, vcc
	s_waitcnt lgkmcnt(0)
	global_store_dwordx4 v[148:149], v[182:185], off
	ds_read_b32 v150, v82 offset:512
	ds_read_b32 v151, v83 offset:512
	ds_read_b32 v166, v83 offset:640
	s_waitcnt lgkmcnt(2)
	v_mul_f32_e32 v46, v150, v46
	v_mul_f32_e32 v47, v150, v47
	v_mul_f32_e32 v48, v150, v48
	v_mul_f32_e32 v49, v150, v49
	v_mul_f32_e32 v42, v150, v42
	v_mul_f32_e32 v43, v150, v43
	v_mul_f32_e32 v44, v150, v44
	v_mul_f32_e32 v45, v150, v45
	v_cvt_pk_bf16_f32 v182, v46, v47
	v_cvt_pk_bf16_f32 v183, v48, v49
	v_cvt_pk_bf16_f32 v184, v42, v43
	v_cvt_pk_bf16_f32 v185, v44, v45
	ds_write_b128 v164, v[182:185]
	v_mul_f32_e32 v38, v150, v38
	v_mul_f32_e32 v39, v150, v39
	v_mul_f32_e32 v40, v150, v40
	v_mul_f32_e32 v41, v150, v41
	v_mul_f32_e32 v34, v150, v34
	v_mul_f32_e32 v35, v150, v35
	v_mul_f32_e32 v36, v150, v36
	v_mul_f32_e32 v37, v150, v37
	v_cvt_pk_bf16_f32 v182, v38, v39
	v_cvt_pk_bf16_f32 v183, v40, v41
	v_cvt_pk_bf16_f32 v184, v34, v35
	v_cvt_pk_bf16_f32 v185, v36, v37
	v_xor_b32_e32 v167, 64, v164
	ds_write_b128 v167, v[182:185]
	v_mov_b32_e32 v46, 0
	v_mov_b32_e32 v42, 0
	v_mov_b32_e32 v38, 0
	v_mov_b32_e32 v34, 0
	v_mov_b32_e32 v47, 0
	v_mov_b32_e32 v43, 0
	v_mov_b32_e32 v39, 0
	v_mov_b32_e32 v35, 0
	v_mov_b32_e32 v48, 0
	v_mov_b32_e32 v44, 0
	v_mov_b32_e32 v40, 0
	v_mov_b32_e32 v36, 0
	v_mov_b32_e32 v49, 0
	v_mov_b32_e32 v45, 0
	v_mov_b32_e32 v41, 0
	v_mov_b32_e32 v37, 0
	ds_read_b128 v[182:185], v165 offset:0
	v_cmp_lt_i32_e32 vcc, -1, v151
	v_lshlrev_b32_e32 v148, 13, v151
	v_mov_b32_e32 v149, 0
	v_lshl_add_u64 v[148:149], v[148:149], 0, v[86:87]
	v_cndmask_b32_e32 v148, v168, v148, vcc
	v_cndmask_b32_e32 v149, v169, v149, vcc
	s_waitcnt lgkmcnt(0)
	global_store_dwordx4 v[148:149], v[182:185], off
	ds_read_b128 v[182:185], v165 offset:8192
	v_cmp_lt_i32_e32 vcc, -1, v166
	v_lshlrev_b32_e32 v148, 13, v166
	v_mov_b32_e32 v149, 0
	v_lshl_add_u64 v[148:149], v[148:149], 0, v[86:87]
	v_cndmask_b32_e32 v148, v168, v148, vcc
	v_cndmask_b32_e32 v149, v169, v149, vcc
	s_waitcnt lgkmcnt(0)
	global_store_dwordx4 v[148:149], v[182:185], off
	ds_read_b32 v150, v82 offset:768
	ds_read_b32 v151, v83 offset:768
	ds_read_b32 v166, v83 offset:896
	s_waitcnt lgkmcnt(2)
; #define PG8_LAS __attribute__((address_space(3)))
; __device__ __forceinline__ unsigned cvtpk(float lo, float hi) { f32x2 v = {lo, hi}; bf16x2_t b = __builtin_convertvector(v, bf16x2_t); return __builtin_bit_cast(unsigned, b); }
; __device__ __forceinline__ void moe_down_stream(PG8_LAS unsigned char* lds, int e, int cb0, int slot0, int nv, const bf16_t* HIDp, const float* Wd, bf16_t* Y, const float* slot_w, const int* slot_dst) {
;     ...
;         if (((t + 1) & 7) == 7) {
;             const int cb = cb0 + ((t + 1) >> 3);
; #pragma unroll
;             for (int m = 0; m < DNM; ++m) {
;                 const float w_ = lw[4 * (16 * m + fr) + wr];
; #pragma unroll
;                 for (int p = 0; p < 2; ++p) { const f32x4 v0 = acc[m][2 * p] * w_, v1 = acc[m][2 * p + 1] * w_; u32x4 w; w.x = cvtpk(v0[0], v0[1]); w.y = cvtpk(v0[2], v0[3]); w.z = cvtpk(v1[0], v1[1]); w.w = cvtpk(v1[2], v1[3]);
;                     *(PG8_LAS u32x4*)(stg + fr * 128 + (((4 * p + fq) ^ (fr & 7)) * 16)) = w; }
; #pragma unroll
;                 for (int hh = 0; hh < 2; ++hh) { const int r = (lane >> 3) + 8 * hh, cc = lane & 7; const u32x4 d = *(const PG8_LAS u32x4*)(stg + r * 128 + ((cc ^ (r & 7)) * 16)); const int dst_ = ldst[4 * (16 * m + r) + wr];
;                     if (dst_ >= 0) *(u32x4*)(Y + (size_t)dst_ * D + 128 * cb + 64 * wc + 8 * cc) = d; }
; #pragma unroll
;                 for (int n = 0; n < 4; ++n) acc[m][n] = (f32x4){0.f, 0.f, 0.f, 0.f}; } }
	v_mul_f32_e32 v18, v150, v18
	v_mul_f32_e32 v19, v150, v19
	v_mul_f32_e32 v20, v150, v20
	v_mul_f32_e32 v21, v150, v21
	v_mul_f32_e32 v22, v150, v22
	v_mul_f32_e32 v23, v150, v23
	v_mul_f32_e32 v24, v150, v24
	v_mul_f32_e32 v25, v150, v25
	v_cvt_pk_bf16_f32 v182, v18, v19
	v_cvt_pk_bf16_f32 v183, v20, v21
	v_cvt_pk_bf16_f32 v184, v22, v23
	v_cvt_pk_bf16_f32 v185, v24, v25
	ds_write_b128 v164, v[182:185]
	v_mul_f32_e32 v26, v150, v26
	v_mul_f32_e32 v27, v150, v27
	v_mul_f32_e32 v28, v150, v28
	v_mul_f32_e32 v29, v150, v29
	v_mul_f32_e32 v30, v150, v30
	v_mul_f32_e32 v31, v150, v31
	v_mul_f32_e32 v32, v150, v32
	v_mul_f32_e32 v33, v150, v33
	v_cvt_pk_bf16_f32 v182, v26, v27
	v_cvt_pk_bf16_f32 v183, v28, v29
	v_cvt_pk_bf16_f32 v184, v30, v31
	v_cvt_pk_bf16_f32 v185, v32, v33
	v_xor_b32_e32 v167, 64, v164
	ds_write_b128 v167, v[182:185]
	v_mov_b32_e32 v18, 0
	v_mov_b32_e32 v22, 0
	v_mov_b32_e32 v26, 0
	v_mov_b32_e32 v30, 0
	v_mov_b32_e32 v19, 0
	v_mov_b32_e32 v23, 0
	v_mov_b32_e32 v27, 0
	v_mov_b32_e32 v31, 0
	v_mov_b32_e32 v20, 0
	v_mov_b32_e32 v24, 0
	v_mov_b32_e32 v28, 0
	v_mov_b32_e32 v32, 0
	v_mov_b32_e32 v21, 0
	v_mov_b32_e32 v25, 0
	v_mov_b32_e32 v29, 0
	v_mov_b32_e32 v33, 0
	ds_read_b128 v[182:185], v165 offset:0
	v_cmp_lt_i32_e32 vcc, -1, v151
	v_lshlrev_b32_e32 v148, 13, v151
	v_mov_b32_e32 v149, 0
	v_lshl_add_u64 v[148:149], v[148:149], 0, v[86:87]
	v_cndmask_b32_e32 v148, v168, v148, vcc
	v_cndmask_b32_e32 v149, v169, v149, vcc
	s_waitcnt lgkmcnt(0)
	global_store_dwordx4 v[148:149], v[182:185], off
	ds_read_b128 v[182:185], v165 offset:8192
	v_cmp_lt_i32_e32 vcc, -1, v166
	v_lshlrev_b32_e32 v148, 13, v166
	v_mov_b32_e32 v149, 0
	v_lshl_add_u64 v[148:149], v[148:149], 0, v[86:87]
	v_cndmask_b32_e32 v148, v168, v148, vcc
	v_cndmask_b32_e32 v149, v169, v149, vcc
	s_waitcnt lgkmcnt(0)
	global_store_dwordx4 v[148:149], v[182:185], off
	ds_read_b32 v150, v82 offset:1024
	ds_read_b32 v151, v83 offset:1024
	ds_read_b32 v166, v83 offset:1152
	s_waitcnt lgkmcnt(2)
	v_mul_f32_e32 v2, v150, v2
	v_mul_f32_e32 v3, v150, v3
	v_mul_f32_e32 v4, v150, v4
	v_mul_f32_e32 v5, v150, v5
	v_mul_f32_e32 v6, v150, v6
	v_mul_f32_e32 v7, v150, v7
	v_mul_f32_e32 v8, v150, v8
	v_mul_f32_e32 v9, v150, v9
	v_cvt_pk_bf16_f32 v182, v2, v3
	v_cvt_pk_bf16_f32 v183, v4, v5
	v_cvt_pk_bf16_f32 v184, v6, v7
	v_cvt_pk_bf16_f32 v185, v8, v9
	ds_write_b128 v164, v[182:185]
	v_mul_f32_e32 v10, v150, v10
	v_mul_f32_e32 v11, v150, v11
	v_mul_f32_e32 v12, v150, v12
	v_mul_f32_e32 v13, v150, v13
	v_mul_f32_e32 v14, v150, v14
	v_mul_f32_e32 v15, v150, v15
	v_mul_f32_e32 v16, v150, v16
	v_mul_f32_e32 v17, v150, v17
	v_cvt_pk_bf16_f32 v182, v10, v11
	v_cvt_pk_bf16_f32 v183, v12, v13
	v_cvt_pk_bf16_f32 v184, v14, v15
	v_cvt_pk_bf16_f32 v185, v16, v17
	v_xor_b32_e32 v167, 64, v164
	ds_write_b128 v167, v[182:185]
	v_mov_b32_e32 v2, 0
	v_mov_b32_e32 v6, 0
	v_mov_b32_e32 v10, 0
	v_mov_b32_e32 v14, 0
	v_mov_b32_e32 v3, 0
	v_mov_b32_e32 v7, 0
	v_mov_b32_e32 v11, 0
	v_mov_b32_e32 v15, 0
	v_mov_b32_e32 v4, 0
	v_mov_b32_e32 v8, 0
	v_mov_b32_e32 v12, 0
	v_mov_b32_e32 v16, 0
	v_mov_b32_e32 v5, 0
	v_mov_b32_e32 v9, 0
	v_mov_b32_e32 v13, 0
	v_mov_b32_e32 v17, 0
	ds_read_b128 v[182:185], v165 offset:0
	v_cmp_lt_i32_e32 vcc, -1, v151
	v_lshlrev_b32_e32 v148, 13, v151
	v_mov_b32_e32 v149, 0
	v_lshl_add_u64 v[148:149], v[148:149], 0, v[86:87]
	v_cndmask_b32_e32 v148, v168, v148, vcc
	v_cndmask_b32_e32 v149, v169, v149, vcc
	s_waitcnt lgkmcnt(0)
	global_store_dwordx4 v[148:149], v[182:185], off
	ds_read_b128 v[182:185], v165 offset:8192
	v_cmp_lt_i32_e32 vcc, -1, v166
	v_lshlrev_b32_e32 v148, 13, v166
	v_mov_b32_e32 v149, 0
	v_lshl_add_u64 v[148:149], v[148:149], 0, v[86:87]
	v_cndmask_b32_e32 v148, v168, v148, vcc
	v_cndmask_b32_e32 v149, v169, v149, vcc
	s_waitcnt lgkmcnt(0)
	global_store_dwordx4 v[148:149], v[182:185], off
	v_add_co_u32_e32 v86, vcc, 0x400, v86
	s_nop 1
	v_addc_co_u32_e32 v87, vcc, 0, v87, vcc
	s_waitcnt lgkmcnt(0)
